# P0: one continuous cooperative transposer pipeline over w_up, w_down, w_in, w_out of both layers (no pipeline restart between matrices; all RMSNorm gains preloaded)
# baseline (speedup 1.0000x reference)
; #define LDS_WAIT() asm volatile("s_waitcnt lgkmcnt(0)" ::: "memory")
;     const int pr = item >> 1, kb = 2 * (pr / nblk) + (item & 1), nb = pr % nblk, k0 = 64 * kb, n0 = 32 * nb;
;     const int nr = n0 + (lane & 31); const int sc = MAP == 1 ? src_col_in(nr) : nr;
;     float v[32];
; #pragma unroll
;     for (int i = 0; i < 32; ++i) v[i] = sc >= 0 ? W[(size_t)(k0 + 2 * i + (lane >> 5)) * Nsrc + sc] : 0.f;
; #pragma unroll
;     for (int i = 0; i < 32; ++i) { const int k = k0 + 2 * i + (lane >> 5); float x = v[i] * wscale; if (KS) x *= (k < ksplit ? ksA[k] : ksB[k - ksplit]); scr[(2 * i + (lane >> 5)) * 33 + (lane & 31)] = x; }
;     LDS_WAIT(); asm volatile("" ::: "memory");
;     const int c = lane & 7;
; #pragma unroll
; __global__ void __launch_bounds__(NWAVES * 64, 2) hybrid_fwd(Args args) {
;     ...
;         for (int rep = 0; rep < REP_PRO; ++rep)
;         for (int it = gw; it < DEPTH * I_L; it += NGW) {
;             const int l = it / I_L; int r = it % I_L;
;             if (r < I_IN) { if (l >= PROJ_F8_FROM) p0_transpose_item_f8<true, 1>(args.in[2] + (size_t)l * DM * NSRC, DM, NSRC, NPROJ / 32, (unsigned char*)(ws + WS_WIN + l * SZ_WIN), WUP8_SCALE, args.in[1] + l * DM, args.in[1] + l * DM, DM, scr, r, lane);
;                 else p0_transpose_item<1, true>(args.in[2] + (size_t)l * DM * NSRC, DM, NSRC, NPROJ / 32, (bf16*)(ws + WS_WIN + l * SZ_WIN), args.in[1] + l * DM, args.in[1] + l * DM, DM, scr, r, lane); continue; } r -= I_IN;
;             if (r < I_O) { if (l >= WO_F8_FROM) p0_transpose_item_f8<true>(args.in[13] + (size_t)l * DM * DM, DM, DM, DM / 32, (unsigned char*)(ws + WS_WO + l * SZ_WO), 64.f, args.in[6] + l * 2048, args.in[12] + l * 2048, 2048, scr, r, lane);
;                 else p0_transpose_item<0, true>(args.in[13] + (size_t)l * DM * DM, DM, DM, DM / 32, (bf16*)(ws + WS_WO + l * SZ_WO), args.in[6] + l * 2048, args.in[12] + l * 2048, 2048, scr, r, lane); continue; } r -= I_O;
;             if (r < I_UP) { p0_transpose_item_f8<true>(args.in[15] + (size_t)l * DM * FF, DM, FF, FF / 32, (unsigned char*)(ws + WS_WUP + l * SZ_WUP), WUP8_SCALE, args.in[14] + l * DM, args.in[14] + l * DM, DM, scr, r, lane); continue; } r -= I_UP;
;             p0_transpose_item_f8<false>(args.in[16] + (size_t)l * FF * DM, FF, DM, DM / 32, (unsigned char*)(ws + WS_WDN + l * SZ_WDN), 128.f, args.in[16], args.in[16], 0, scr, r, lane);
.LBB0_11:
	s_or_b64 exec, exec, s[0:1]
	v_mov_b32_e32 v1, v0
	v_readlane_b32 s1, v253, 2
	v_readfirstlane_b32 s0, v1
	s_ashr_i32 s0, s0, 6
	s_lshl_b32 s1, s1, 3
	s_add_i32 s80, s0, s1
	s_lshl_b32 s0, s0, 14
	v_lshlrev_b32_e32 v2, 3, v1
	v_writelane_b32 v253, s1, 46
	s_add_i32 s1, s0, 0
	v_and_b32_e32 v18, 31, v1
	v_bfe_u32 v20, v1, 3, 3
	v_and_b32_e32 v8, 56, v2
	s_lshl_b32 s96, s83, 3
	s_lshl_b32 s76, s83, 9
	v_bfe_u32 v6, v1, 5, 1
	v_lshl_add_u32 v25, v18, 2, s1
	s_movk_i32 s0, 0x84
	v_mul_u32_u24_e32 v2, 0x84, v8
	v_lshlrev_b32_e32 v3, 2, v20
	s_cmp_gt_i32 s80, 0x2f3ff
	v_mad_u32_u24 v19, v6, s0, v25
	v_mov_b32_e32 v11, 0
	v_add3_u32 v21, s1, v2, v3
	v_or_b32_e32 v22, 8, v20
	v_or_b32_e32 v23, 16, v20
	v_or_b32_e32 v24, 24, v20
	s_cbranch_scc1 .Lco3_hop_192
	v_and_b32_e32 v249, 63, v0
	v_lshrrev_b32_e32 v250, 6, v0
	v_readlane_b32 s15, v253, 2
	s_lshr_b32 s22, s15, 3
	s_and_b32 s23, s15, 7
	v_lshrrev_b32_e32 v246, 5, v249
	v_lshl_add_u32 v247, v250, 4, v246
	v_and_b32_e32 v248, 31, v249
	v_xor_b32_e32 v248, v248, v250
	v_lshlrev_b32_e32 v248, 4, v248
	v_lshl_add_u32 v209, v247, 9, v248
	v_add_u32_e32 v210, 0x10000, v209
	v_lshlrev_b32_e32 v96, 2, v247
	v_and_b32_e32 v248, 31, v249
	v_lshlrev_b32_e32 v248, 4, v248
	s_mov_b32 s20, 0x10000
	v_mad_u32_u24 v74, v247, s20, v248
	s_mov_b32 s20, 0x4000
	v_mad_u32_u24 v75, v247, s20, v248
	s_mov_b32 s20, 0xb140
	v_mad_u32_u24 v76, v247, s20, v248
	v_and_b32_e32 v246, 7, v249
	v_lshrrev_b32_e32 v247, 5, v249
	v_lshl_add_u32 v247, v250, 2, v247
	v_xor_b32_e32 v247, v247, v246
	v_lshlrev_b32_e32 v247, 4, v247
	v_lshl_add_u32 v247, v246, 13, v247
	v_bfe_u32 v248, v249, 3, 2
	v_lshl_add_u32 v211, v248, 2, v247
	v_add_u32_e32 v212, 0x10000, v211
	v_and_b32_e32 v246, 7, v249
	v_lshrrev_b32_e32 v247, 5, v249
	v_lshl_add_u32 v247, v250, 2, v247
	v_add_u32_e32 v247, 2, v247
	v_xor_b32_e32 v247, v247, v246
	v_lshlrev_b32_e32 v247, 4, v247
	v_lshl_add_u32 v247, v246, 13, v247
	v_bfe_u32 v248, v249, 3, 2
	v_lshl_add_u32 v213, v248, 2, v247
	v_add_u32_e32 v214, 0x10000, v213
	v_and_b32_e32 v246, 15, v249
	v_lshrrev_b32_e32 v247, 1, v246
	v_lshlrev_b32_e32 v248, 2, v250
	v_xor_b32_e32 v248, v248, v247
	v_lshlrev_b32_e32 v248, 4, v248
	v_lshl_add_u32 v248, v246, 12, v248
	v_lshrrev_b32_e32 v247, 4, v249
	v_lshl_add_u32 v112, v247, 2, v248
	v_add_u32_e32 v113, 0x10000, v112
	v_and_b32_e32 v246, 15, v249
	v_lshrrev_b32_e32 v247, 1, v246
	v_lshlrev_b32_e32 v248, 2, v250
	v_add_u32_e32 v248, 1, v248
	v_xor_b32_e32 v248, v248, v247
	v_lshlrev_b32_e32 v248, 4, v248
	v_lshl_add_u32 v248, v246, 12, v248
	v_lshrrev_b32_e32 v247, 4, v249
	v_lshl_add_u32 v114, v247, 2, v248
	v_add_u32_e32 v115, 0x10000, v114
	v_and_b32_e32 v246, 15, v249
	v_lshrrev_b32_e32 v247, 1, v246
	v_lshlrev_b32_e32 v248, 2, v250
	v_add_u32_e32 v248, 2, v248
	v_xor_b32_e32 v248, v248, v247
	v_lshlrev_b32_e32 v248, 4, v248
	v_lshl_add_u32 v248, v246, 12, v248
	v_lshrrev_b32_e32 v247, 4, v249
	v_lshl_add_u32 v116, v247, 2, v248
	v_add_u32_e32 v117, 0x10000, v116
	v_and_b32_e32 v246, 15, v249
	v_lshrrev_b32_e32 v247, 1, v246
	v_lshlrev_b32_e32 v248, 2, v250
	v_add_u32_e32 v248, 3, v248
	v_xor_b32_e32 v248, v248, v247
	v_lshlrev_b32_e32 v248, 4, v248
	v_lshl_add_u32 v248, v246, 12, v248
	v_lshrrev_b32_e32 v247, 4, v249
	v_lshl_add_u32 v118, v247, 2, v248
	v_add_u32_e32 v119, 0x10000, v118
	v_lshrrev_b32_e32 v246, 3, v249
	v_lshl_add_u32 v246, v250, 4, v246
	v_and_b32_e32 v247, 7, v249
	v_lshlrev_b32_e32 v247, 4, v247
	v_lshl_add_u32 v77, v246, 12, v247
	v_lshl_add_u32 v79, v246, 14, v247
	v_and_b32_e32 v248, 63, v246
	v_lshlrev_b32_e32 v248, 1, v248
	v_lshrrev_b32_e32 v246, 6, v246
	v_or_b32_e32 v248, v248, v246
	v_lshl_add_u32 v81, v248, 12, v247
	v_lshrrev_b32_e32 v246, 3, v249
	v_lshl_add_u32 v246, v250, 4, v246
	v_add_u32_e32 v246, 8, v246
	v_and_b32_e32 v247, 7, v249
	v_lshlrev_b32_e32 v247, 4, v247
	v_lshl_add_u32 v78, v246, 12, v247
	v_lshl_add_u32 v80, v246, 14, v247
	v_and_b32_e32 v248, 63, v246
	v_lshlrev_b32_e32 v248, 1, v248
	v_lshrrev_b32_e32 v246, 6, v246
	v_or_b32_e32 v248, v248, v246
	v_lshl_add_u32 v82, v248, 12, v247
	v_lshrrev_b32_e32 v246, 4, v249
	v_lshl_add_u32 v246, v250, 4, v246
	v_and_b32_e32 v247, 15, v249
	v_lshlrev_b32_e32 v247, 4, v247
	v_lshl_add_u32 v83, v246, 13, v247
	v_and_b32_e32 v248, 63, v246
	v_lshlrev_b32_e32 v248, 1, v248
	v_lshrrev_b32_e32 v246, 6, v246
	v_or_b32_e32 v248, v248, v246
	v_lshl_add_u32 v87, v248, 13, v247
	v_lshrrev_b32_e32 v246, 4, v249
	v_lshl_add_u32 v246, v250, 4, v246
	v_add_u32_e32 v246, 4, v246
	v_and_b32_e32 v247, 15, v249
	v_lshlrev_b32_e32 v247, 4, v247
	v_lshl_add_u32 v84, v246, 13, v247
	v_and_b32_e32 v248, 63, v246
	v_lshlrev_b32_e32 v248, 1, v248
	v_lshrrev_b32_e32 v246, 6, v246
	v_or_b32_e32 v248, v248, v246
	v_lshl_add_u32 v88, v248, 13, v247
	v_lshrrev_b32_e32 v246, 4, v249
	v_lshl_add_u32 v246, v250, 4, v246
	v_add_u32_e32 v246, 8, v246
	v_and_b32_e32 v247, 15, v249
	v_lshlrev_b32_e32 v247, 4, v247
	v_lshl_add_u32 v85, v246, 13, v247
	v_and_b32_e32 v248, 63, v246
	v_lshlrev_b32_e32 v248, 1, v248
	v_lshrrev_b32_e32 v246, 6, v246
	v_or_b32_e32 v248, v248, v246
	v_lshl_add_u32 v89, v248, 13, v247
	v_lshrrev_b32_e32 v246, 4, v249
	v_lshl_add_u32 v246, v250, 4, v246
	v_add_u32_e32 v246, 12, v246
	v_and_b32_e32 v247, 15, v249
	v_lshlrev_b32_e32 v247, 4, v247
	v_lshl_add_u32 v86, v246, 13, v247
	v_and_b32_e32 v248, 63, v246
	v_lshlrev_b32_e32 v248, 1, v248
	v_lshrrev_b32_e32 v246, 6, v246
	v_or_b32_e32 v248, v248, v246
	v_lshl_add_u32 v90, v248, 13, v247
	v_mov_b32_e32 v95, 0x43e00000
	s_mov_b32 s62, 0xc3e00000
	s_mov_b32 s63, 0x7fff
	s_mov_b32 s64, 0x07060302
	v_readlane_b32 s10, v253, 5
;     ...
;     for (int i = 0; i < 32; ++i) { const int k = k0 + 2 * i + (lane >> 5); float x = v[i] * wscale; if (KS) x *= (k < ksplit ? ksA[k] : ksB[k - ksplit]); scr[(2 * i + (lane >> 5)) * 33 + (lane & 31)] = x; }
; __global__ void __launch_bounds__(NWAVES * 64, 2) hybrid_fwd(Args args) {
;     ...
;             const int l = it / I_L; int r = it % I_L;
;             if (r < I_IN) { if (l >= PROJ_F8_FROM) p0_transpose_item_f8<true, 1>(args.in[2] + (size_t)l * DM * NSRC, DM, NSRC, NPROJ / 32, (unsigned char*)(ws + WS_WIN + l * SZ_WIN), WUP8_SCALE, args.in[1] + l * DM, args.in[1] + l * DM, DM, scr, r, lane);
;                 else p0_transpose_item<1, true>(args.in[2] + (size_t)l * DM * NSRC, DM, NSRC, NPROJ / 32, (bf16*)(ws + WS_WIN + l * SZ_WIN), args.in[1] + l * DM, args.in[1] + l * DM, DM, scr, r, lane); continue; } r -= I_IN;
;             if (r < I_O) { if (l >= WO_F8_FROM) p0_transpose_item_f8<true>(args.in[13] + (size_t)l * DM * DM, DM, DM, DM / 32, (unsigned char*)(ws + WS_WO + l * SZ_WO), 64.f, args.in[6] + l * 2048, args.in[12] + l * 2048, 2048, scr, r, lane);
;                 else p0_transpose_item<0, true>(args.in[13] + (size_t)l * DM * DM, DM, DM, DM / 32, (bf16*)(ws + WS_WO + l * SZ_WO), args.in[6] + l * 2048, args.in[12] + l * 2048, 2048, scr, r, lane); continue; } r -= I_O;
;             if (r < I_UP) { p0_transpose_item_f8<true>(args.in[15] + (size_t)l * DM * FF, DM, FF, FF / 32, (unsigned char*)(ws + WS_WUP + l * SZ_WUP), WUP8_SCALE, args.in[14] + l * DM, args.in[14] + l * DM, DM, scr, r, lane); continue; } r -= I_UP;
	v_readlane_b32 s11, v253, 6
	s_lshl_b32 s20, s22, 9
	s_add_u32 s10, s10, s20
	s_addc_u32 s11, s11, 0
	global_load_dword v42, v96, s[10:11] offset:0
	global_load_dword v43, v96, s[10:11] offset:8
	global_load_dword v44, v96, s[10:11] offset:16
	global_load_dword v45, v96, s[10:11] offset:24
	global_load_dword v46, v96, s[10:11] offset:32
	global_load_dword v47, v96, s[10:11] offset:40
	global_load_dword v48, v96, s[10:11] offset:48
	global_load_dword v49, v96, s[10:11] offset:56
	v_readlane_b32 s10, v253, 5
	v_readlane_b32 s11, v253, 6
	s_lshl_b32 s20, s22, 9
	s_add_i32 s20, s20, 0x4000
	s_add_u32 s10, s10, s20
	s_addc_u32 s11, s11, 0
	global_load_dword v50, v96, s[10:11] offset:0
	global_load_dword v51, v96, s[10:11] offset:8
	global_load_dword v52, v96, s[10:11] offset:16
	global_load_dword v53, v96, s[10:11] offset:24
	global_load_dword v54, v96, s[10:11] offset:32
	global_load_dword v55, v96, s[10:11] offset:40
	global_load_dword v56, v96, s[10:11] offset:48
	global_load_dword v57, v96, s[10:11] offset:56
	v_readlane_b32 s10, v253, 15
	v_readlane_b32 s11, v253, 16
	v_readlane_b32 s20, v253, 27
	v_readlane_b32 s21, v253, 28
	s_sub_i32 s26, s22, 16
	s_cmp_lt_u32 s22, 16
	s_cselect_b32 s10, s10, s20
	s_cselect_b32 s11, s11, s21
	s_cselect_b32 s26, s22, s26
	s_lshl_b32 s20, s26, 9
	s_add_u32 s10, s10, s20
	s_addc_u32 s11, s11, 0
	global_load_dword v58, v96, s[10:11] offset:0
	global_load_dword v59, v96, s[10:11] offset:8
	global_load_dword v60, v96, s[10:11] offset:16
	global_load_dword v61, v96, s[10:11] offset:24
	global_load_dword v62, v96, s[10:11] offset:32
	global_load_dword v63, v96, s[10:11] offset:40
	global_load_dword v64, v96, s[10:11] offset:48
	global_load_dword v65, v96, s[10:11] offset:56
	v_readlane_b32 s10, v253, 15
	v_readlane_b32 s11, v253, 16
	v_readlane_b32 s20, v253, 27
	v_readlane_b32 s21, v253, 28
	s_sub_i32 s26, s22, 16
	s_cmp_lt_u32 s22, 16
	s_cselect_b32 s10, s10, s20
	s_cselect_b32 s11, s11, s21
	s_cselect_b32 s26, s22, s26
	s_lshl_b32 s20, s26, 9
	s_add_i32 s20, s20, 0x2000
	s_add_u32 s10, s10, s20
	s_addc_u32 s11, s11, 0
	global_load_dword v66, v96, s[10:11] offset:0
	global_load_dword v67, v96, s[10:11] offset:8
	global_load_dword v68, v96, s[10:11] offset:16
	global_load_dword v69, v96, s[10:11] offset:24
	global_load_dword v70, v96, s[10:11] offset:32
	global_load_dword v71, v96, s[10:11] offset:40
	global_load_dword v72, v96, s[10:11] offset:48
	global_load_dword v73, v96, s[10:11] offset:56
	v_readlane_b32 s10, v253, 31
	v_readlane_b32 s11, v253, 32
	s_lshl_b32 s20, s22, 9
	s_add_u32 s10, s10, s20
	s_addc_u32 s11, s11, 0
	global_load_dword v26, v96, s[10:11] offset:0
	global_load_dword v27, v96, s[10:11] offset:8
	global_load_dword v28, v96, s[10:11] offset:16
	global_load_dword v29, v96, s[10:11] offset:24
	global_load_dword v30, v96, s[10:11] offset:32
	global_load_dword v31, v96, s[10:11] offset:40
	global_load_dword v32, v96, s[10:11] offset:48
	global_load_dword v33, v96, s[10:11] offset:56
	v_readlane_b32 s10, v253, 31
	v_readlane_b32 s11, v253, 32
	s_lshl_b32 s20, s22, 9
	s_add_i32 s20, s20, 0x4000
	s_add_u32 s10, s10, s20
	s_addc_u32 s11, s11, 0
	global_load_dword v34, v96, s[10:11] offset:0
	global_load_dword v35, v96, s[10:11] offset:8
	global_load_dword v36, v96, s[10:11] offset:16
	global_load_dword v37, v96, s[10:11] offset:24
	global_load_dword v38, v96, s[10:11] offset:32
	global_load_dword v39, v96, s[10:11] offset:40
	global_load_dword v40, v96, s[10:11] offset:48
	global_load_dword v41, v96, s[10:11] offset:56
	s_waitcnt vmcnt(0)
	v_mul_f32_e32 v50, 0x42800000, v50
	v_mul_f32_e32 v51, 0x42800000, v51
	v_mul_f32_e32 v52, 0x42800000, v52
	v_mul_f32_e32 v53, 0x42800000, v53
	v_mul_f32_e32 v54, 0x42800000, v54
	v_mul_f32_e32 v55, 0x42800000, v55
	v_mul_f32_e32 v56, 0x42800000, v56
	v_mul_f32_e32 v57, 0x42800000, v57
	v_mul_f32_e32 v66, 0x42800000, v66
	v_mul_f32_e32 v67, 0x42800000, v67
	v_mul_f32_e32 v68, 0x42800000, v68
	v_mul_f32_e32 v69, 0x42800000, v69
	v_mul_f32_e32 v70, 0x42800000, v70
	v_mul_f32_e32 v71, 0x42800000, v71
	v_mul_f32_e32 v72, 0x42800000, v72
	v_mul_f32_e32 v73, 0x42800000, v73
	v_mul_f32_e32 v26, 0x42800000, v26
	v_mul_f32_e32 v27, 0x42800000, v27
	v_mul_f32_e32 v28, 0x42800000, v28
	v_mul_f32_e32 v29, 0x42800000, v29
	v_mul_f32_e32 v30, 0x42800000, v30
	v_mul_f32_e32 v31, 0x42800000, v31
	v_mul_f32_e32 v32, 0x42800000, v32
	v_mul_f32_e32 v33, 0x42800000, v33
	v_mul_f32_e32 v34, 0x42800000, v34
	v_mul_f32_e32 v35, 0x42800000, v35
	v_mul_f32_e32 v36, 0x42800000, v36
	v_mul_f32_e32 v37, 0x42800000, v37
	v_mul_f32_e32 v38, 0x42800000, v38
	v_mul_f32_e32 v39, 0x42800000, v39
	v_mul_f32_e32 v40, 0x42800000, v40
	v_mul_f32_e32 v41, 0x42800000, v41
	v_readlane_b32 s30, v253, 33
	v_readlane_b32 s31, v253, 34
	v_readlane_b32 s32, v253, 41
	v_readlane_b32 s33, v253, 42
	s_mul_i32 s20, s22, 0x800000
	s_lshl_b32 s21, s23, 9
	s_add_u32 s20, s20, s21
	s_add_u32 s30, s30, s20
	s_addc_u32 s31, s31, 0
	s_add_u32 s32, s32, 0xf600000
	s_addc_u32 s33, s33, 0
	s_lshl_b32 s20, s22, 7
	s_mul_i32 s21, s23, 0x80000
	s_add_u32 s20, s20, s21
	s_add_u32 s32, s32, s20
	s_addc_u32 s33, s33, 0
	v_readlane_b32 s34, v253, 33
	v_readlane_b32 s35, v253, 34
	v_readlane_b32 s36, v253, 41
	v_readlane_b32 s37, v253, 42
	s_add_u32 s34, s34, 0x10000000
	s_addc_u32 s35, s35, 0
	s_mul_i32 s20, s22, 0x800000
	s_lshl_b32 s21, s23, 9
	s_add_u32 s20, s20, s21
	s_add_u32 s34, s34, s20
	s_addc_u32 s35, s35, 0
	s_add_u32 s36, s36, 0x17600000
	s_addc_u32 s37, s37, 0
	s_lshl_b32 s20, s22, 7
	s_mul_i32 s21, s23, 0x80000
	s_add_u32 s20, s20, s21
	s_add_u32 s36, s36, s20
	s_addc_u32 s37, s37, 0
	v_readlane_b32 s38, v253, 35
;     const int pr = item >> 1, kb = 2 * (pr / nblk) + (item & 1), nb = pr % nblk, k0 = 64 * kb, n0 = 32 * nb;
;     const int nr = n0 + (lane & 31); const int sc = MAP == 1 ? src_col_in(nr) : nr;
;     float v[32];
; #pragma unroll
;     for (int i = 0; i < 32; ++i) v[i] = sc >= 0 ? W[(size_t)(k0 + 2 * i + (lane >> 5)) * Nsrc + sc] : 0.f;
; #pragma unroll
;     for (int i = 0; i < 32; ++i) { const int k = k0 + 2 * i + (lane >> 5); float x = v[i] * wscale; if (KS) x *= (k < ksplit ? ksA[k] : ksB[k - ksplit]); scr[(2 * i + (lane >> 5)) * 33 + (lane & 31)] = x; }
; __global__ void __launch_bounds__(NWAVES * 64, 2) hybrid_fwd(Args args) {
;     ...
;             if (r < I_IN) { if (l >= PROJ_F8_FROM) p0_transpose_item_f8<true, 1>(args.in[2] + (size_t)l * DM * NSRC, DM, NSRC, NPROJ / 32, (unsigned char*)(ws + WS_WIN + l * SZ_WIN), WUP8_SCALE, args.in[1] + l * DM, args.in[1] + l * DM, DM, scr, r, lane);
;                 else p0_transpose_item<1, true>(args.in[2] + (size_t)l * DM * NSRC, DM, NSRC, NPROJ / 32, (bf16*)(ws + WS_WIN + l * SZ_WIN), args.in[1] + l * DM, args.in[1] + l * DM, DM, scr, r, lane); continue; } r -= I_IN;
;             if (r < I_O) { if (l >= WO_F8_FROM) p0_transpose_item_f8<true>(args.in[13] + (size_t)l * DM * DM, DM, DM, DM / 32, (unsigned char*)(ws + WS_WO + l * SZ_WO), 64.f, args.in[6] + l * 2048, args.in[12] + l * 2048, 2048, scr, r, lane);
;                 else p0_transpose_item<0, true>(args.in[13] + (size_t)l * DM * DM, DM, DM, DM / 32, (bf16*)(ws + WS_WO + l * SZ_WO), args.in[6] + l * 2048, args.in[12] + l * 2048, 2048, scr, r, lane); continue; } r -= I_O;
;             if (r < I_UP) { p0_transpose_item_f8<true>(args.in[15] + (size_t)l * DM * FF, DM, FF, FF / 32, (unsigned char*)(ws + WS_WUP + l * SZ_WUP), WUP8_SCALE, args.in[14] + l * DM, args.in[14] + l * DM, DM, scr, r, lane); continue; } r -= I_UP;
;             p0_transpose_item_f8<false>(args.in[16] + (size_t)l * FF * DM, FF, DM, DM / 32, (unsigned char*)(ws + WS_WDN + l * SZ_WDN), 128.f, args.in[16], args.in[16], 0, scr, r, lane);
	v_readlane_b32 s39, v253, 36
	v_readlane_b32 s40, v253, 41
	v_readlane_b32 s41, v253, 42
	s_mul_i32 s20, s22, 0x200000
	s_lshl_b32 s21, s23, 9
	s_add_u32 s20, s20, s21
	s_add_u32 s38, s38, s20
	s_addc_u32 s39, s39, 0
	s_add_u32 s40, s40, 0x1f600000
	s_addc_u32 s41, s41, 0
	s_lshl_b32 s20, s22, 7
	s_mul_i32 s21, s23, 0x200000
	s_add_u32 s20, s20, s21
	s_add_u32 s40, s40, s20
	s_addc_u32 s41, s41, 0
	v_readlane_b32 s42, v253, 35
	v_readlane_b32 s43, v253, 36
	v_readlane_b32 s44, v253, 41
	v_readlane_b32 s45, v253, 42
	s_add_u32 s42, s42, 0x10000000
	s_addc_u32 s43, s43, 0
	s_mul_i32 s20, s22, 0x200000
	s_lshl_b32 s21, s23, 9
	s_add_u32 s20, s20, s21
	s_add_u32 s42, s42, s20
	s_addc_u32 s43, s43, 0
	s_add_u32 s44, s44, 0x27600000
	s_addc_u32 s45, s45, 0
	s_lshl_b32 s20, s22, 7
	s_mul_i32 s21, s23, 0x200000
	s_add_u32 s20, s20, s21
	s_add_u32 s44, s44, s20
	s_addc_u32 s45, s45, 0
	v_readlane_b32 s46, v253, 7
	v_readlane_b32 s47, v253, 8
	v_readlane_b32 s48, v253, 41
	v_readlane_b32 s49, v253, 42
	s_mul_i32 s20, s22, 0x58a000
	s_add_u32 s46, s46, s20
	s_addc_u32 s47, s47, 0
	s_add_u32 s48, s48, 0x200000
	s_addc_u32 s49, s49, 0
	s_lshl_b32 s20, s22, 8
	s_add_u32 s48, s48, s20
	s_addc_u32 s49, s49, 0
	v_readlane_b32 s50, v253, 7
	v_readlane_b32 s51, v253, 8
	v_readlane_b32 s52, v253, 41
	v_readlane_b32 s53, v253, 42
	s_add_u32 s50, s50, 0xb140000
	s_addc_u32 s51, s51, 0
	s_mul_i32 s20, s22, 0x58a000
	s_add_u32 s50, s50, s20
	s_addc_u32 s51, s51, 0
	s_add_u32 s52, s52, 0x5c00000
	s_addc_u32 s53, s53, 0
	s_lshl_b32 s20, s22, 7
	s_add_u32 s52, s52, s20
	s_addc_u32 s53, s53, 0
	v_readlane_b32 s54, v253, 29
	v_readlane_b32 s55, v253, 30
	v_readlane_b32 s56, v253, 41
	v_readlane_b32 s57, v253, 42
	s_mul_i32 s20, s22, 0x200000
	s_lshl_b32 s21, s23, 9
	s_add_u32 s20, s20, s21
	s_add_u32 s54, s54, s20
	s_addc_u32 s55, s55, 0
	s_add_u32 s56, s56, 0xb600000
	s_addc_u32 s57, s57, 0
	s_lshl_b32 s20, s22, 8
	s_mul_i32 s21, s23, 0x100000
	s_add_u32 s20, s20, s21
	s_add_u32 s56, s56, s20
	s_addc_u32 s57, s57, 0
	v_readlane_b32 s58, v253, 29
	v_readlane_b32 s59, v253, 30
	v_readlane_b32 s60, v253, 41
	v_readlane_b32 s61, v253, 42
	s_add_u32 s58, s58, 0x4000000
	s_addc_u32 s59, s59, 0
	s_mul_i32 s20, s22, 0x200000
	s_lshl_b32 s21, s23, 9
	s_add_u32 s20, s20, s21
	s_add_u32 s58, s58, s20
	s_addc_u32 s59, s59, 0
	s_add_u32 s60, s60, 0xd600000
	s_addc_u32 s61, s61, 0
	s_lshl_b32 s20, s22, 7
	s_mul_i32 s21, s23, 0x80000
	s_add_u32 s20, s20, s21
	s_add_u32 s60, s60, s20
	s_addc_u32 s61, s61, 0
	s_mov_b64 s[8:9], s[30:31]
	global_load_dwordx4 v[144:147], v74, s[8:9]
	s_add_u32 s8, s8, 0x20000
	s_addc_u32 s9, s9, 0
	global_load_dwordx4 v[148:151], v74, s[8:9]
	s_add_u32 s8, s8, 0x20000
	s_addc_u32 s9, s9, 0
	global_load_dwordx4 v[152:155], v74, s[8:9]
	s_add_u32 s8, s8, 0x20000
	s_addc_u32 s9, s9, 0
	global_load_dwordx4 v[156:159], v74, s[8:9]
	s_add_u32 s8, s8, 0x20000
	s_addc_u32 s9, s9, 0
	global_load_dwordx4 v[160:163], v74, s[8:9]
	s_add_u32 s8, s8, 0x20000
	s_addc_u32 s9, s9, 0
	global_load_dwordx4 v[164:167], v74, s[8:9]
	s_add_u32 s8, s8, 0x20000
	s_addc_u32 s9, s9, 0
	global_load_dwordx4 v[168:171], v74, s[8:9]
	s_add_u32 s8, s8, 0x20000
	s_addc_u32 s9, s9, 0
	global_load_dwordx4 v[172:175], v74, s[8:9]
	s_add_u32 s8, s30, 0x1000
	s_addc_u32 s9, s31, 0
	global_load_dwordx4 v[176:179], v74, s[8:9]
	s_add_u32 s8, s8, 0x20000
	s_addc_u32 s9, s9, 0
	global_load_dwordx4 v[180:183], v74, s[8:9]
	s_add_u32 s8, s8, 0x20000
	s_addc_u32 s9, s9, 0
	global_load_dwordx4 v[184:187], v74, s[8:9]
	s_add_u32 s8, s8, 0x20000
	s_addc_u32 s9, s9, 0
	global_load_dwordx4 v[188:191], v74, s[8:9]
	s_add_u32 s8, s8, 0x20000
	s_addc_u32 s9, s9, 0
	global_load_dwordx4 v[192:195], v74, s[8:9]
	s_add_u32 s8, s8, 0x20000
	s_addc_u32 s9, s9, 0
	global_load_dwordx4 v[196:199], v74, s[8:9]
	s_add_u32 s8, s8, 0x20000
	s_addc_u32 s9, s9, 0
	global_load_dwordx4 v[200:203], v74, s[8:9]
	s_add_u32 s8, s8, 0x20000
	s_addc_u32 s9, s9, 0
	global_load_dwordx4 v[204:207], v74, s[8:9]
	s_waitcnt vmcnt(8)
	v_mul_f32_e32 v144, v26, v144
	v_mul_f32_e32 v145, v26, v145
	v_mul_f32_e32 v146, v26, v146
	v_mul_f32_e32 v147, v26, v147
	ds_write_b128 v209, v[144:147]
	v_mul_f32_e32 v148, v27, v148
	v_mul_f32_e32 v149, v27, v149
	v_mul_f32_e32 v150, v27, v150
	v_mul_f32_e32 v151, v27, v151
	ds_write_b128 v209, v[148:151] offset:1024
	v_mul_f32_e32 v152, v28, v152
	v_mul_f32_e32 v153, v28, v153
	v_mul_f32_e32 v154, v28, v154
	v_mul_f32_e32 v155, v28, v155
	ds_write_b128 v209, v[152:155] offset:2048
	v_mul_f32_e32 v156, v29, v156
	v_mul_f32_e32 v157, v29, v157
	v_mul_f32_e32 v158, v29, v158
	v_mul_f32_e32 v159, v29, v159
	ds_write_b128 v209, v[156:159] offset:3072
	v_mul_f32_e32 v160, v30, v160
	v_mul_f32_e32 v161, v30, v161
	v_mul_f32_e32 v162, v30, v162
	v_mul_f32_e32 v163, v30, v163
	ds_write_b128 v209, v[160:163] offset:4096
	v_mul_f32_e32 v164, v31, v164
	v_mul_f32_e32 v165, v31, v165
	v_mul_f32_e32 v166, v31, v166
	v_mul_f32_e32 v167, v31, v167
	ds_write_b128 v209, v[164:167] offset:5120
	v_mul_f32_e32 v168, v32, v168
	v_mul_f32_e32 v169, v32, v169
	v_mul_f32_e32 v170, v32, v170
	v_mul_f32_e32 v171, v32, v171
	ds_write_b128 v209, v[168:171] offset:6144
	v_mul_f32_e32 v172, v33, v172
	v_mul_f32_e32 v173, v33, v173
	v_mul_f32_e32 v174, v33, v174
	v_mul_f32_e32 v175, v33, v175
	ds_write_b128 v209, v[172:175] offset:7168
	s_waitcnt lgkmcnt(0)
	s_barrier
; #define GAS __attribute__((address_space(1)))
; #define LAS __attribute__((address_space(3)))
; #define LDS_WAIT() asm volatile("s_waitcnt lgkmcnt(0)" ::: "memory")
;     const int pr = item >> 1, kb = 2 * (pr / nblk) + (item & 1), nb = pr % nblk, k0 = 64 * kb, n0 = 32 * nb;
;     const int nr = n0 + (lane & 31); const int sc = MAP == 1 ? src_col_in(nr) : nr;
;     float v[32];
; #pragma unroll
;     for (int i = 0; i < 32; ++i) v[i] = sc >= 0 ? W[(size_t)(k0 + 2 * i + (lane >> 5)) * Nsrc + sc] : 0.f;
; #pragma unroll
;     for (int i = 0; i < 32; ++i) { const int k = k0 + 2 * i + (lane >> 5); float x = v[i] * wscale; if (KS) x *= (k < ksplit ? ksA[k] : ksB[k - ksplit]); scr[(2 * i + (lane >> 5)) * 33 + (lane & 31)] = x; }
;     LDS_WAIT(); asm volatile("" ::: "memory");
;     const int c = lane & 7;
; #pragma unroll
;     for (int j = 0; j < 4; ++j) { const int n = (lane >> 3) + 8 * j; const LAS float* s = scr + (8 * c) * 33 + n;
;         const unsigned long long o = (unsigned long long)pg8::pk4_fp8(s[0 * 33], s[1 * 33], s[2 * 33], s[3 * 33]) | ((unsigned long long)pg8::pk4_fp8(s[4 * 33], s[5 * 33], s[6 * 33], s[7 * 33]) << 32);
;         *(GAS unsigned long long*)(WT + (size_t)(n0 + n) * K + k0 + 8 * c) = o; }
;     LDS_WAIT(); asm volatile("" ::: "memory");
	s_add_u32 s8, s30, 0x2000
	s_addc_u32 s9, s31, 0
	global_load_dwordx4 v[144:147], v74, s[8:9]
	s_add_u32 s8, s8, 0x20000
	s_addc_u32 s9, s9, 0
	global_load_dwordx4 v[148:151], v74, s[8:9]
	s_add_u32 s8, s8, 0x20000
	s_addc_u32 s9, s9, 0
	global_load_dwordx4 v[152:155], v74, s[8:9]
	s_add_u32 s8, s8, 0x20000
	s_addc_u32 s9, s9, 0
	global_load_dwordx4 v[156:159], v74, s[8:9]
	s_add_u32 s8, s8, 0x20000
	s_addc_u32 s9, s9, 0
	global_load_dwordx4 v[160:163], v74, s[8:9]
	s_add_u32 s8, s8, 0x20000
	s_addc_u32 s9, s9, 0
	global_load_dwordx4 v[164:167], v74, s[8:9]
	s_add_u32 s8, s8, 0x20000
	s_addc_u32 s9, s9, 0
	global_load_dwordx4 v[168:171], v74, s[8:9]
	s_add_u32 s8, s8, 0x20000
	s_addc_u32 s9, s9, 0
	global_load_dwordx4 v[172:175], v74, s[8:9]
	s_mov_b64 s[6:7], s[32:33]
	ds_read_b32 v226, v211
	ds_read_b32 v227, v211 offset:512
	ds_read_b32 v228, v211 offset:1024
	ds_read_b32 v229, v211 offset:1536
	ds_read_b32 v230, v211 offset:2048
	ds_read_b32 v231, v211 offset:2560
	ds_read_b32 v232, v211 offset:3072
	ds_read_b32 v233, v211 offset:3584
	ds_read_b32 v234, v211 offset:4096
	ds_read_b32 v235, v211 offset:4608
	ds_read_b32 v236, v211 offset:5120
	ds_read_b32 v237, v211 offset:5632
	ds_read_b32 v238, v211 offset:6144
	ds_read_b32 v239, v211 offset:6656
	ds_read_b32 v240, v211 offset:7168
	ds_read_b32 v241, v211 offset:7680
	s_waitcnt lgkmcnt(0)
	v_max_f32_e32 v226, v226, v226
	v_max_f32_e32 v227, v227, v227
	v_max_f32_e32 v228, v228, v228
	v_max_f32_e32 v229, v229, v229
	v_max_f32_e32 v230, v230, v230
	v_max_f32_e32 v231, v231, v231
	v_max_f32_e32 v232, v232, v232
	v_max_f32_e32 v233, v233, v233
	v_max_f32_e32 v234, v234, v234
	v_max_f32_e32 v235, v235, v235
	v_max_f32_e32 v236, v236, v236
	v_max_f32_e32 v237, v237, v237
	v_max_f32_e32 v238, v238, v238
	v_max_f32_e32 v239, v239, v239
	v_max_f32_e32 v240, v240, v240
	v_max_f32_e32 v241, v241, v241
	v_med3_f32 v226, v226, s62, v95
	v_med3_f32 v227, v227, s62, v95
	v_med3_f32 v228, v228, s62, v95
	v_med3_f32 v229, v229, s62, v95
	v_med3_f32 v230, v230, s62, v95
	v_med3_f32 v231, v231, s62, v95
	v_med3_f32 v232, v232, s62, v95
	v_med3_f32 v233, v233, s62, v95
	v_med3_f32 v234, v234, s62, v95
	v_med3_f32 v235, v235, s62, v95
	v_med3_f32 v236, v236, s62, v95
	v_med3_f32 v237, v237, s62, v95
	v_med3_f32 v238, v238, s62, v95
	v_med3_f32 v239, v239, s62, v95
	v_med3_f32 v240, v240, s62, v95
	v_med3_f32 v241, v241, s62, v95
	v_mov_b32_e32 v242, 0
	v_mov_b32_e32 v243, 0
	v_mov_b32_e32 v244, 0
	v_mov_b32_e32 v245, 0
	v_cvt_pk_fp8_f32 v242, v226, v227
	v_cvt_pk_fp8_f32 v243, v230, v231
	v_cvt_pk_fp8_f32 v244, v234, v235
	v_cvt_pk_fp8_f32 v245, v238, v239
	v_cvt_pk_fp8_f32 v242, v228, v229 op_sel:[0,0,1]
	v_cvt_pk_fp8_f32 v243, v232, v233 op_sel:[0,0,1]
	v_cvt_pk_fp8_f32 v244, v236, v237 op_sel:[0,0,1]
	v_cvt_pk_fp8_f32 v245, v240, v241 op_sel:[0,0,1]
	s_nop 0
	global_store_dwordx4 v77, v[242:245], s[6:7]
	ds_read_b32 v226, v213
	ds_read_b32 v227, v213 offset:512
	ds_read_b32 v228, v213 offset:1024
	ds_read_b32 v229, v213 offset:1536
	ds_read_b32 v230, v213 offset:2048
	ds_read_b32 v231, v213 offset:2560
	ds_read_b32 v232, v213 offset:3072
	ds_read_b32 v233, v213 offset:3584
	ds_read_b32 v234, v213 offset:4096
	ds_read_b32 v235, v213 offset:4608
	ds_read_b32 v236, v213 offset:5120
	ds_read_b32 v237, v213 offset:5632
	ds_read_b32 v238, v213 offset:6144
	ds_read_b32 v239, v213 offset:6656
	ds_read_b32 v240, v213 offset:7168
	ds_read_b32 v241, v213 offset:7680
	s_waitcnt lgkmcnt(0)
	v_max_f32_e32 v226, v226, v226
	v_max_f32_e32 v227, v227, v227
	v_max_f32_e32 v228, v228, v228
	v_max_f32_e32 v229, v229, v229
	v_max_f32_e32 v230, v230, v230
	v_max_f32_e32 v231, v231, v231
	v_max_f32_e32 v232, v232, v232
	v_max_f32_e32 v233, v233, v233
	v_max_f32_e32 v234, v234, v234
	v_max_f32_e32 v235, v235, v235
	v_max_f32_e32 v236, v236, v236
	v_max_f32_e32 v237, v237, v237
	v_max_f32_e32 v238, v238, v238
	v_max_f32_e32 v239, v239, v239
	v_max_f32_e32 v240, v240, v240
	v_max_f32_e32 v241, v241, v241
	v_med3_f32 v226, v226, s62, v95
	v_med3_f32 v227, v227, s62, v95
	v_med3_f32 v228, v228, s62, v95
	v_med3_f32 v229, v229, s62, v95
	v_med3_f32 v230, v230, s62, v95
	v_med3_f32 v231, v231, s62, v95
	v_med3_f32 v232, v232, s62, v95
	v_med3_f32 v233, v233, s62, v95
	v_med3_f32 v234, v234, s62, v95
	v_med3_f32 v235, v235, s62, v95
	v_med3_f32 v236, v236, s62, v95
	v_med3_f32 v237, v237, s62, v95
	v_med3_f32 v238, v238, s62, v95
	v_med3_f32 v239, v239, s62, v95
	v_med3_f32 v240, v240, s62, v95
	v_med3_f32 v241, v241, s62, v95
	v_mov_b32_e32 v242, 0
	v_mov_b32_e32 v243, 0
	v_mov_b32_e32 v244, 0
	v_mov_b32_e32 v245, 0
	v_cvt_pk_fp8_f32 v242, v226, v227
	v_cvt_pk_fp8_f32 v243, v230, v231
	v_cvt_pk_fp8_f32 v244, v234, v235
	v_cvt_pk_fp8_f32 v245, v238, v239
	v_cvt_pk_fp8_f32 v242, v228, v229 op_sel:[0,0,1]
	v_cvt_pk_fp8_f32 v243, v232, v233 op_sel:[0,0,1]
	v_cvt_pk_fp8_f32 v244, v236, v237 op_sel:[0,0,1]
	v_cvt_pk_fp8_f32 v245, v240, v241 op_sel:[0,0,1]
	s_nop 0
	global_store_dwordx4 v78, v[242:245], s[6:7]
	s_waitcnt vmcnt(10)
	v_mul_f32_e32 v176, v26, v176
	v_mul_f32_e32 v177, v26, v177
	v_mul_f32_e32 v178, v26, v178
	v_mul_f32_e32 v179, v26, v179
	ds_write_b128 v210, v[176:179]
	v_mul_f32_e32 v180, v27, v180
	v_mul_f32_e32 v181, v27, v181
	v_mul_f32_e32 v182, v27, v182
	v_mul_f32_e32 v183, v27, v183
	ds_write_b128 v210, v[180:183] offset:1024
	v_mul_f32_e32 v184, v28, v184
	v_mul_f32_e32 v185, v28, v185
	v_mul_f32_e32 v186, v28, v186
	v_mul_f32_e32 v187, v28, v187
	ds_write_b128 v210, v[184:187] offset:2048
	v_mul_f32_e32 v188, v29, v188
	v_mul_f32_e32 v189, v29, v189
	v_mul_f32_e32 v190, v29, v190
	v_mul_f32_e32 v191, v29, v191
	ds_write_b128 v210, v[188:191] offset:3072
	v_mul_f32_e32 v192, v30, v192
	v_mul_f32_e32 v193, v30, v193
	v_mul_f32_e32 v194, v30, v194
	v_mul_f32_e32 v195, v30, v195
	ds_write_b128 v210, v[192:195] offset:4096
	v_mul_f32_e32 v196, v31, v196
	v_mul_f32_e32 v197, v31, v197
	v_mul_f32_e32 v198, v31, v198
	v_mul_f32_e32 v199, v31, v199
	ds_write_b128 v210, v[196:199] offset:5120
	v_mul_f32_e32 v200, v32, v200
	v_mul_f32_e32 v201, v32, v201
	v_mul_f32_e32 v202, v32, v202
	v_mul_f32_e32 v203, v32, v203
	ds_write_b128 v210, v[200:203] offset:6144
	v_mul_f32_e32 v204, v33, v204
	v_mul_f32_e32 v205, v33, v205
	v_mul_f32_e32 v206, v33, v206
	v_mul_f32_e32 v207, v33, v207
	ds_write_b128 v210, v[204:207] offset:7168
	s_waitcnt lgkmcnt(0)
	s_barrier
; #define GAS __attribute__((address_space(1)))
; #define LAS __attribute__((address_space(3)))
; #define LDS_WAIT() asm volatile("s_waitcnt lgkmcnt(0)" ::: "memory")
;     const int pr = item >> 1, kb = 2 * (pr / nblk) + (item & 1), nb = pr % nblk, k0 = 64 * kb, n0 = 32 * nb;
;     const int nr = n0 + (lane & 31); const int sc = MAP == 1 ? src_col_in(nr) : nr;
;     float v[32];
; #pragma unroll
;     for (int i = 0; i < 32; ++i) v[i] = sc >= 0 ? W[(size_t)(k0 + 2 * i + (lane >> 5)) * Nsrc + sc] : 0.f;
; #pragma unroll
;     for (int i = 0; i < 32; ++i) { const int k = k0 + 2 * i + (lane >> 5); float x = v[i] * wscale; if (KS) x *= (k < ksplit ? ksA[k] : ksB[k - ksplit]); scr[(2 * i + (lane >> 5)) * 33 + (lane & 31)] = x; }
;     LDS_WAIT(); asm volatile("" ::: "memory");
;     const int c = lane & 7;
; #pragma unroll
;     for (int j = 0; j < 4; ++j) { const int n = (lane >> 3) + 8 * j; const LAS float* s = scr + (8 * c) * 33 + n;
;         const unsigned long long o = (unsigned long long)pg8::pk4_fp8(s[0 * 33], s[1 * 33], s[2 * 33], s[3 * 33]) | ((unsigned long long)pg8::pk4_fp8(s[4 * 33], s[5 * 33], s[6 * 33], s[7 * 33]) << 32);
;         *(GAS unsigned long long*)(WT + (size_t)(n0 + n) * K + k0 + 8 * c) = o; }
;     LDS_WAIT(); asm volatile("" ::: "memory");
	s_add_u32 s8, s30, 0x3000
	s_addc_u32 s9, s31, 0
	global_load_dwordx4 v[176:179], v74, s[8:9]
	s_add_u32 s8, s8, 0x20000
	s_addc_u32 s9, s9, 0
	global_load_dwordx4 v[180:183], v74, s[8:9]
	s_add_u32 s8, s8, 0x20000
	s_addc_u32 s9, s9, 0
	global_load_dwordx4 v[184:187], v74, s[8:9]
	s_add_u32 s8, s8, 0x20000
	s_addc_u32 s9, s9, 0
	global_load_dwordx4 v[188:191], v74, s[8:9]
	s_add_u32 s8, s8, 0x20000
	s_addc_u32 s9, s9, 0
	global_load_dwordx4 v[192:195], v74, s[8:9]
	s_add_u32 s8, s8, 0x20000
	s_addc_u32 s9, s9, 0
	global_load_dwordx4 v[196:199], v74, s[8:9]
	s_add_u32 s8, s8, 0x20000
	s_addc_u32 s9, s9, 0
	global_load_dwordx4 v[200:203], v74, s[8:9]
	s_add_u32 s8, s8, 0x20000
	s_addc_u32 s9, s9, 0
	global_load_dwordx4 v[204:207], v74, s[8:9]
	s_add_u32 s6, s32, 0x400000
	s_addc_u32 s7, s33, 0
	ds_read_b32 v226, v212
	ds_read_b32 v227, v212 offset:512
	ds_read_b32 v228, v212 offset:1024
	ds_read_b32 v229, v212 offset:1536
	ds_read_b32 v230, v212 offset:2048
	ds_read_b32 v231, v212 offset:2560
	ds_read_b32 v232, v212 offset:3072
	ds_read_b32 v233, v212 offset:3584
	ds_read_b32 v234, v212 offset:4096
	ds_read_b32 v235, v212 offset:4608
	ds_read_b32 v236, v212 offset:5120
	ds_read_b32 v237, v212 offset:5632
	ds_read_b32 v238, v212 offset:6144
	ds_read_b32 v239, v212 offset:6656
	ds_read_b32 v240, v212 offset:7168
	ds_read_b32 v241, v212 offset:7680
	s_waitcnt lgkmcnt(0)
	v_max_f32_e32 v226, v226, v226
	v_max_f32_e32 v227, v227, v227
	v_max_f32_e32 v228, v228, v228
	v_max_f32_e32 v229, v229, v229
	v_max_f32_e32 v230, v230, v230
	v_max_f32_e32 v231, v231, v231
	v_max_f32_e32 v232, v232, v232
	v_max_f32_e32 v233, v233, v233
	v_max_f32_e32 v234, v234, v234
	v_max_f32_e32 v235, v235, v235
	v_max_f32_e32 v236, v236, v236
	v_max_f32_e32 v237, v237, v237
	v_max_f32_e32 v238, v238, v238
	v_max_f32_e32 v239, v239, v239
	v_max_f32_e32 v240, v240, v240
	v_max_f32_e32 v241, v241, v241
	v_med3_f32 v226, v226, s62, v95
	v_med3_f32 v227, v227, s62, v95
	v_med3_f32 v228, v228, s62, v95
	v_med3_f32 v229, v229, s62, v95
	v_med3_f32 v230, v230, s62, v95
	v_med3_f32 v231, v231, s62, v95
	v_med3_f32 v232, v232, s62, v95
	v_med3_f32 v233, v233, s62, v95
	v_med3_f32 v234, v234, s62, v95
	v_med3_f32 v235, v235, s62, v95
	v_med3_f32 v236, v236, s62, v95
	v_med3_f32 v237, v237, s62, v95
	v_med3_f32 v238, v238, s62, v95
	v_med3_f32 v239, v239, s62, v95
	v_med3_f32 v240, v240, s62, v95
	v_med3_f32 v241, v241, s62, v95
	v_mov_b32_e32 v242, 0
	v_mov_b32_e32 v243, 0
	v_mov_b32_e32 v244, 0
	v_mov_b32_e32 v245, 0
	v_cvt_pk_fp8_f32 v242, v226, v227
	v_cvt_pk_fp8_f32 v243, v230, v231
	v_cvt_pk_fp8_f32 v244, v234, v235
	v_cvt_pk_fp8_f32 v245, v238, v239
	v_cvt_pk_fp8_f32 v242, v228, v229 op_sel:[0,0,1]
	v_cvt_pk_fp8_f32 v243, v232, v233 op_sel:[0,0,1]
	v_cvt_pk_fp8_f32 v244, v236, v237 op_sel:[0,0,1]
	v_cvt_pk_fp8_f32 v245, v240, v241 op_sel:[0,0,1]
	s_nop 0
	global_store_dwordx4 v77, v[242:245], s[6:7]
	ds_read_b32 v226, v214
	ds_read_b32 v227, v214 offset:512
	ds_read_b32 v228, v214 offset:1024
	ds_read_b32 v229, v214 offset:1536
	ds_read_b32 v230, v214 offset:2048
	ds_read_b32 v231, v214 offset:2560
	ds_read_b32 v232, v214 offset:3072
	ds_read_b32 v233, v214 offset:3584
	ds_read_b32 v234, v214 offset:4096
	ds_read_b32 v235, v214 offset:4608
	ds_read_b32 v236, v214 offset:5120
	ds_read_b32 v237, v214 offset:5632
	ds_read_b32 v238, v214 offset:6144
	ds_read_b32 v239, v214 offset:6656
	ds_read_b32 v240, v214 offset:7168
	ds_read_b32 v241, v214 offset:7680
	s_waitcnt lgkmcnt(0)
	v_max_f32_e32 v226, v226, v226
	v_max_f32_e32 v227, v227, v227
	v_max_f32_e32 v228, v228, v228
	v_max_f32_e32 v229, v229, v229
	v_max_f32_e32 v230, v230, v230
	v_max_f32_e32 v231, v231, v231
	v_max_f32_e32 v232, v232, v232
	v_max_f32_e32 v233, v233, v233
	v_max_f32_e32 v234, v234, v234
	v_max_f32_e32 v235, v235, v235
	v_max_f32_e32 v236, v236, v236
	v_max_f32_e32 v237, v237, v237
	v_max_f32_e32 v238, v238, v238
	v_max_f32_e32 v239, v239, v239
	v_max_f32_e32 v240, v240, v240
	v_max_f32_e32 v241, v241, v241
	v_med3_f32 v226, v226, s62, v95
	v_med3_f32 v227, v227, s62, v95
	v_med3_f32 v228, v228, s62, v95
	v_med3_f32 v229, v229, s62, v95
	v_med3_f32 v230, v230, s62, v95
	v_med3_f32 v231, v231, s62, v95
	v_med3_f32 v232, v232, s62, v95
	v_med3_f32 v233, v233, s62, v95
	v_med3_f32 v234, v234, s62, v95
	v_med3_f32 v235, v235, s62, v95
	v_med3_f32 v236, v236, s62, v95
	v_med3_f32 v237, v237, s62, v95
	v_med3_f32 v238, v238, s62, v95
	v_med3_f32 v239, v239, s62, v95
	v_med3_f32 v240, v240, s62, v95
	v_med3_f32 v241, v241, s62, v95
	v_mov_b32_e32 v242, 0
	v_mov_b32_e32 v243, 0
	v_mov_b32_e32 v244, 0
	v_mov_b32_e32 v245, 0
	v_cvt_pk_fp8_f32 v242, v226, v227
	v_cvt_pk_fp8_f32 v243, v230, v231
	v_cvt_pk_fp8_f32 v244, v234, v235
	v_cvt_pk_fp8_f32 v245, v238, v239
	v_cvt_pk_fp8_f32 v242, v228, v229 op_sel:[0,0,1]
	v_cvt_pk_fp8_f32 v243, v232, v233 op_sel:[0,0,1]
	v_cvt_pk_fp8_f32 v244, v236, v237 op_sel:[0,0,1]
	v_cvt_pk_fp8_f32 v245, v240, v241 op_sel:[0,0,1]
	s_nop 0
	global_store_dwordx4 v78, v[242:245], s[6:7]
	s_waitcnt vmcnt(12)
	v_mul_f32_e32 v144, v26, v144
	v_mul_f32_e32 v145, v26, v145
	v_mul_f32_e32 v146, v26, v146
	v_mul_f32_e32 v147, v26, v147
	ds_write_b128 v209, v[144:147]
	v_mul_f32_e32 v148, v27, v148
	v_mul_f32_e32 v149, v27, v149
	v_mul_f32_e32 v150, v27, v150
	v_mul_f32_e32 v151, v27, v151
	ds_write_b128 v209, v[148:151] offset:1024
	v_mul_f32_e32 v152, v28, v152
	v_mul_f32_e32 v153, v28, v153
	v_mul_f32_e32 v154, v28, v154
	v_mul_f32_e32 v155, v28, v155
	ds_write_b128 v209, v[152:155] offset:2048
	v_mul_f32_e32 v156, v29, v156
	v_mul_f32_e32 v157, v29, v157
	v_mul_f32_e32 v158, v29, v158
	v_mul_f32_e32 v159, v29, v159
	ds_write_b128 v209, v[156:159] offset:3072
	v_mul_f32_e32 v160, v30, v160
	v_mul_f32_e32 v161, v30, v161
	v_mul_f32_e32 v162, v30, v162
	v_mul_f32_e32 v163, v30, v163
	ds_write_b128 v209, v[160:163] offset:4096
	v_mul_f32_e32 v164, v31, v164
	v_mul_f32_e32 v165, v31, v165
	v_mul_f32_e32 v166, v31, v166
	v_mul_f32_e32 v167, v31, v167
	ds_write_b128 v209, v[164:167] offset:5120
	v_mul_f32_e32 v168, v32, v168
	v_mul_f32_e32 v169, v32, v169
	v_mul_f32_e32 v170, v32, v170
	v_mul_f32_e32 v171, v32, v171
	ds_write_b128 v209, v[168:171] offset:6144
	v_mul_f32_e32 v172, v33, v172
	v_mul_f32_e32 v173, v33, v173
	v_mul_f32_e32 v174, v33, v174
	v_mul_f32_e32 v175, v33, v175
	ds_write_b128 v209, v[172:175] offset:7168
	s_waitcnt lgkmcnt(0)
	s_barrier
; #define GAS __attribute__((address_space(1)))
; #define LAS __attribute__((address_space(3)))
; #define LDS_WAIT() asm volatile("s_waitcnt lgkmcnt(0)" ::: "memory")
;     const int pr = item >> 1, kb = 2 * (pr / nblk) + (item & 1), nb = pr % nblk, k0 = 64 * kb, n0 = 32 * nb;
;     const int nr = n0 + (lane & 31); const int sc = MAP == 1 ? src_col_in(nr) : nr;
;     float v[32];
; #pragma unroll
;     for (int i = 0; i < 32; ++i) v[i] = sc >= 0 ? W[(size_t)(k0 + 2 * i + (lane >> 5)) * Nsrc + sc] : 0.f;
; #pragma unroll
;     for (int i = 0; i < 32; ++i) { const int k = k0 + 2 * i + (lane >> 5); float x = v[i] * wscale; if (KS) x *= (k < ksplit ? ksA[k] : ksB[k - ksplit]); scr[(2 * i + (lane >> 5)) * 33 + (lane & 31)] = x; }
;     LDS_WAIT(); asm volatile("" ::: "memory");
;     const int c = lane & 7;
; #pragma unroll
;     for (int j = 0; j < 4; ++j) { const int n = (lane >> 3) + 8 * j; const LAS float* s = scr + (8 * c) * 33 + n;
;         const unsigned long long o = (unsigned long long)pg8::pk4_fp8(s[0 * 33], s[1 * 33], s[2 * 33], s[3 * 33]) | ((unsigned long long)pg8::pk4_fp8(s[4 * 33], s[5 * 33], s[6 * 33], s[7 * 33]) << 32);
;         *(GAS unsigned long long*)(WT + (size_t)(n0 + n) * K + k0 + 8 * c) = o; }
;     LDS_WAIT(); asm volatile("" ::: "memory");
	s_add_u32 s8, s30, 0x4000
	s_addc_u32 s9, s31, 0
	global_load_dwordx4 v[144:147], v74, s[8:9]
	s_add_u32 s8, s8, 0x20000
	s_addc_u32 s9, s9, 0
	global_load_dwordx4 v[148:151], v74, s[8:9]
	s_add_u32 s8, s8, 0x20000
	s_addc_u32 s9, s9, 0
	global_load_dwordx4 v[152:155], v74, s[8:9]
	s_add_u32 s8, s8, 0x20000
	s_addc_u32 s9, s9, 0
	global_load_dwordx4 v[156:159], v74, s[8:9]
	s_add_u32 s8, s8, 0x20000
	s_addc_u32 s9, s9, 0
	global_load_dwordx4 v[160:163], v74, s[8:9]
	s_add_u32 s8, s8, 0x20000
	s_addc_u32 s9, s9, 0
	global_load_dwordx4 v[164:167], v74, s[8:9]
	s_add_u32 s8, s8, 0x20000
	s_addc_u32 s9, s9, 0
	global_load_dwordx4 v[168:171], v74, s[8:9]
	s_add_u32 s8, s8, 0x20000
	s_addc_u32 s9, s9, 0
	global_load_dwordx4 v[172:175], v74, s[8:9]
	s_add_u32 s6, s32, 0x800000
	s_addc_u32 s7, s33, 0
	ds_read_b32 v226, v211
	ds_read_b32 v227, v211 offset:512
	ds_read_b32 v228, v211 offset:1024
	ds_read_b32 v229, v211 offset:1536
	ds_read_b32 v230, v211 offset:2048
	ds_read_b32 v231, v211 offset:2560
	ds_read_b32 v232, v211 offset:3072
	ds_read_b32 v233, v211 offset:3584
	ds_read_b32 v234, v211 offset:4096
	ds_read_b32 v235, v211 offset:4608
	ds_read_b32 v236, v211 offset:5120
	ds_read_b32 v237, v211 offset:5632
	ds_read_b32 v238, v211 offset:6144
	ds_read_b32 v239, v211 offset:6656
	ds_read_b32 v240, v211 offset:7168
	ds_read_b32 v241, v211 offset:7680
	s_waitcnt lgkmcnt(0)
	v_max_f32_e32 v226, v226, v226
	v_max_f32_e32 v227, v227, v227
	v_max_f32_e32 v228, v228, v228
	v_max_f32_e32 v229, v229, v229
	v_max_f32_e32 v230, v230, v230
	v_max_f32_e32 v231, v231, v231
	v_max_f32_e32 v232, v232, v232
	v_max_f32_e32 v233, v233, v233
	v_max_f32_e32 v234, v234, v234
	v_max_f32_e32 v235, v235, v235
	v_max_f32_e32 v236, v236, v236
	v_max_f32_e32 v237, v237, v237
	v_max_f32_e32 v238, v238, v238
	v_max_f32_e32 v239, v239, v239
	v_max_f32_e32 v240, v240, v240
	v_max_f32_e32 v241, v241, v241
	v_med3_f32 v226, v226, s62, v95
	v_med3_f32 v227, v227, s62, v95
	v_med3_f32 v228, v228, s62, v95
	v_med3_f32 v229, v229, s62, v95
	v_med3_f32 v230, v230, s62, v95
	v_med3_f32 v231, v231, s62, v95
	v_med3_f32 v232, v232, s62, v95
	v_med3_f32 v233, v233, s62, v95
	v_med3_f32 v234, v234, s62, v95
	v_med3_f32 v235, v235, s62, v95
	v_med3_f32 v236, v236, s62, v95
	v_med3_f32 v237, v237, s62, v95
	v_med3_f32 v238, v238, s62, v95
	v_med3_f32 v239, v239, s62, v95
	v_med3_f32 v240, v240, s62, v95
	v_med3_f32 v241, v241, s62, v95
	v_mov_b32_e32 v242, 0
	v_mov_b32_e32 v243, 0
	v_mov_b32_e32 v244, 0
	v_mov_b32_e32 v245, 0
	v_cvt_pk_fp8_f32 v242, v226, v227
	v_cvt_pk_fp8_f32 v243, v230, v231
	v_cvt_pk_fp8_f32 v244, v234, v235
	v_cvt_pk_fp8_f32 v245, v238, v239
	v_cvt_pk_fp8_f32 v242, v228, v229 op_sel:[0,0,1]
	v_cvt_pk_fp8_f32 v243, v232, v233 op_sel:[0,0,1]
	v_cvt_pk_fp8_f32 v244, v236, v237 op_sel:[0,0,1]
	v_cvt_pk_fp8_f32 v245, v240, v241 op_sel:[0,0,1]
	s_nop 0
	global_store_dwordx4 v77, v[242:245], s[6:7]
	ds_read_b32 v226, v213
	ds_read_b32 v227, v213 offset:512
	ds_read_b32 v228, v213 offset:1024
	ds_read_b32 v229, v213 offset:1536
	ds_read_b32 v230, v213 offset:2048
	ds_read_b32 v231, v213 offset:2560
	ds_read_b32 v232, v213 offset:3072
	ds_read_b32 v233, v213 offset:3584
	ds_read_b32 v234, v213 offset:4096
	ds_read_b32 v235, v213 offset:4608
	ds_read_b32 v236, v213 offset:5120
	ds_read_b32 v237, v213 offset:5632
	ds_read_b32 v238, v213 offset:6144
	ds_read_b32 v239, v213 offset:6656
	ds_read_b32 v240, v213 offset:7168
	ds_read_b32 v241, v213 offset:7680
	s_waitcnt lgkmcnt(0)
	v_max_f32_e32 v226, v226, v226
	v_max_f32_e32 v227, v227, v227
	v_max_f32_e32 v228, v228, v228
	v_max_f32_e32 v229, v229, v229
	v_max_f32_e32 v230, v230, v230
	v_max_f32_e32 v231, v231, v231
	v_max_f32_e32 v232, v232, v232
	v_max_f32_e32 v233, v233, v233
	v_max_f32_e32 v234, v234, v234
	v_max_f32_e32 v235, v235, v235
	v_max_f32_e32 v236, v236, v236
	v_max_f32_e32 v237, v237, v237
	v_max_f32_e32 v238, v238, v238
	v_max_f32_e32 v239, v239, v239
	v_max_f32_e32 v240, v240, v240
	v_max_f32_e32 v241, v241, v241
	v_med3_f32 v226, v226, s62, v95
	v_med3_f32 v227, v227, s62, v95
	v_med3_f32 v228, v228, s62, v95
	v_med3_f32 v229, v229, s62, v95
	v_med3_f32 v230, v230, s62, v95
	v_med3_f32 v231, v231, s62, v95
	v_med3_f32 v232, v232, s62, v95
	v_med3_f32 v233, v233, s62, v95
	v_med3_f32 v234, v234, s62, v95
	v_med3_f32 v235, v235, s62, v95
	v_med3_f32 v236, v236, s62, v95
	v_med3_f32 v237, v237, s62, v95
	v_med3_f32 v238, v238, s62, v95
	v_med3_f32 v239, v239, s62, v95
	v_med3_f32 v240, v240, s62, v95
	v_med3_f32 v241, v241, s62, v95
	v_mov_b32_e32 v242, 0
	v_mov_b32_e32 v243, 0
	v_mov_b32_e32 v244, 0
	v_mov_b32_e32 v245, 0
	v_cvt_pk_fp8_f32 v242, v226, v227
	v_cvt_pk_fp8_f32 v243, v230, v231
	v_cvt_pk_fp8_f32 v244, v234, v235
	v_cvt_pk_fp8_f32 v245, v238, v239
	v_cvt_pk_fp8_f32 v242, v228, v229 op_sel:[0,0,1]
	v_cvt_pk_fp8_f32 v243, v232, v233 op_sel:[0,0,1]
	v_cvt_pk_fp8_f32 v244, v236, v237 op_sel:[0,0,1]
	v_cvt_pk_fp8_f32 v245, v240, v241 op_sel:[0,0,1]
	s_nop 0
	global_store_dwordx4 v78, v[242:245], s[6:7]
	s_waitcnt vmcnt(12)
	v_mul_f32_e32 v176, v26, v176
	v_mul_f32_e32 v177, v26, v177
	v_mul_f32_e32 v178, v26, v178
	v_mul_f32_e32 v179, v26, v179
	ds_write_b128 v210, v[176:179]
	v_mul_f32_e32 v180, v27, v180
	v_mul_f32_e32 v181, v27, v181
	v_mul_f32_e32 v182, v27, v182
	v_mul_f32_e32 v183, v27, v183
	ds_write_b128 v210, v[180:183] offset:1024
	v_mul_f32_e32 v184, v28, v184
	v_mul_f32_e32 v185, v28, v185
	v_mul_f32_e32 v186, v28, v186
	v_mul_f32_e32 v187, v28, v187
	ds_write_b128 v210, v[184:187] offset:2048
	v_mul_f32_e32 v188, v29, v188
	v_mul_f32_e32 v189, v29, v189
	v_mul_f32_e32 v190, v29, v190
	v_mul_f32_e32 v191, v29, v191
	ds_write_b128 v210, v[188:191] offset:3072
	v_mul_f32_e32 v192, v30, v192
	v_mul_f32_e32 v193, v30, v193
	v_mul_f32_e32 v194, v30, v194
	v_mul_f32_e32 v195, v30, v195
	ds_write_b128 v210, v[192:195] offset:4096
	v_mul_f32_e32 v196, v31, v196
	v_mul_f32_e32 v197, v31, v197
	v_mul_f32_e32 v198, v31, v198
	v_mul_f32_e32 v199, v31, v199
	ds_write_b128 v210, v[196:199] offset:5120
	v_mul_f32_e32 v200, v32, v200
	v_mul_f32_e32 v201, v32, v201
	v_mul_f32_e32 v202, v32, v202
	v_mul_f32_e32 v203, v32, v203
	ds_write_b128 v210, v[200:203] offset:6144
	v_mul_f32_e32 v204, v33, v204
	v_mul_f32_e32 v205, v33, v205
	v_mul_f32_e32 v206, v33, v206
	v_mul_f32_e32 v207, v33, v207
	ds_write_b128 v210, v[204:207] offset:7168
	s_waitcnt lgkmcnt(0)
	s_barrier
; #define GAS __attribute__((address_space(1)))
; #define LAS __attribute__((address_space(3)))
; #define LDS_WAIT() asm volatile("s_waitcnt lgkmcnt(0)" ::: "memory")
;     const int pr = item >> 1, kb = 2 * (pr / nblk) + (item & 1), nb = pr % nblk, k0 = 64 * kb, n0 = 32 * nb;
;     const int nr = n0 + (lane & 31); const int sc = MAP == 1 ? src_col_in(nr) : nr;
;     float v[32];
; #pragma unroll
;     for (int i = 0; i < 32; ++i) v[i] = sc >= 0 ? W[(size_t)(k0 + 2 * i + (lane >> 5)) * Nsrc + sc] : 0.f;
; #pragma unroll
;     for (int i = 0; i < 32; ++i) { const int k = k0 + 2 * i + (lane >> 5); float x = v[i] * wscale; if (KS) x *= (k < ksplit ? ksA[k] : ksB[k - ksplit]); scr[(2 * i + (lane >> 5)) * 33 + (lane & 31)] = x; }
;     LDS_WAIT(); asm volatile("" ::: "memory");
;     const int c = lane & 7;
; #pragma unroll
;     for (int j = 0; j < 4; ++j) { const int n = (lane >> 3) + 8 * j; const LAS float* s = scr + (8 * c) * 33 + n;
;         const unsigned long long o = (unsigned long long)pg8::pk4_fp8(s[0 * 33], s[1 * 33], s[2 * 33], s[3 * 33]) | ((unsigned long long)pg8::pk4_fp8(s[4 * 33], s[5 * 33], s[6 * 33], s[7 * 33]) << 32);
;         *(GAS unsigned long long*)(WT + (size_t)(n0 + n) * K + k0 + 8 * c) = o; }
;     LDS_WAIT(); asm volatile("" ::: "memory");
	s_add_u32 s8, s30, 0x5000
	s_addc_u32 s9, s31, 0
	global_load_dwordx4 v[176:179], v74, s[8:9]
	s_add_u32 s8, s8, 0x20000
	s_addc_u32 s9, s9, 0
	global_load_dwordx4 v[180:183], v74, s[8:9]
	s_add_u32 s8, s8, 0x20000
	s_addc_u32 s9, s9, 0
	global_load_dwordx4 v[184:187], v74, s[8:9]
	s_add_u32 s8, s8, 0x20000
	s_addc_u32 s9, s9, 0
	global_load_dwordx4 v[188:191], v74, s[8:9]
	s_add_u32 s8, s8, 0x20000
	s_addc_u32 s9, s9, 0
	global_load_dwordx4 v[192:195], v74, s[8:9]
	s_add_u32 s8, s8, 0x20000
	s_addc_u32 s9, s9, 0
	global_load_dwordx4 v[196:199], v74, s[8:9]
	s_add_u32 s8, s8, 0x20000
	s_addc_u32 s9, s9, 0
	global_load_dwordx4 v[200:203], v74, s[8:9]
	s_add_u32 s8, s8, 0x20000
	s_addc_u32 s9, s9, 0
	global_load_dwordx4 v[204:207], v74, s[8:9]
	s_add_u32 s6, s32, 0xc00000
	s_addc_u32 s7, s33, 0
	ds_read_b32 v226, v212
	ds_read_b32 v227, v212 offset:512
	ds_read_b32 v228, v212 offset:1024
	ds_read_b32 v229, v212 offset:1536
	ds_read_b32 v230, v212 offset:2048
	ds_read_b32 v231, v212 offset:2560
	ds_read_b32 v232, v212 offset:3072
	ds_read_b32 v233, v212 offset:3584
	ds_read_b32 v234, v212 offset:4096
	ds_read_b32 v235, v212 offset:4608
	ds_read_b32 v236, v212 offset:5120
	ds_read_b32 v237, v212 offset:5632
	ds_read_b32 v238, v212 offset:6144
	ds_read_b32 v239, v212 offset:6656
	ds_read_b32 v240, v212 offset:7168
	ds_read_b32 v241, v212 offset:7680
	s_waitcnt lgkmcnt(0)
	v_max_f32_e32 v226, v226, v226
	v_max_f32_e32 v227, v227, v227
	v_max_f32_e32 v228, v228, v228
	v_max_f32_e32 v229, v229, v229
	v_max_f32_e32 v230, v230, v230
	v_max_f32_e32 v231, v231, v231
	v_max_f32_e32 v232, v232, v232
	v_max_f32_e32 v233, v233, v233
	v_max_f32_e32 v234, v234, v234
	v_max_f32_e32 v235, v235, v235
	v_max_f32_e32 v236, v236, v236
	v_max_f32_e32 v237, v237, v237
	v_max_f32_e32 v238, v238, v238
	v_max_f32_e32 v239, v239, v239
	v_max_f32_e32 v240, v240, v240
	v_max_f32_e32 v241, v241, v241
	v_med3_f32 v226, v226, s62, v95
	v_med3_f32 v227, v227, s62, v95
	v_med3_f32 v228, v228, s62, v95
	v_med3_f32 v229, v229, s62, v95
	v_med3_f32 v230, v230, s62, v95
	v_med3_f32 v231, v231, s62, v95
	v_med3_f32 v232, v232, s62, v95
	v_med3_f32 v233, v233, s62, v95
	v_med3_f32 v234, v234, s62, v95
	v_med3_f32 v235, v235, s62, v95
	v_med3_f32 v236, v236, s62, v95
	v_med3_f32 v237, v237, s62, v95
	v_med3_f32 v238, v238, s62, v95
	v_med3_f32 v239, v239, s62, v95
	v_med3_f32 v240, v240, s62, v95
	v_med3_f32 v241, v241, s62, v95
	v_mov_b32_e32 v242, 0
	v_mov_b32_e32 v243, 0
	v_mov_b32_e32 v244, 0
	v_mov_b32_e32 v245, 0
	v_cvt_pk_fp8_f32 v242, v226, v227
	v_cvt_pk_fp8_f32 v243, v230, v231
	v_cvt_pk_fp8_f32 v244, v234, v235
	v_cvt_pk_fp8_f32 v245, v238, v239
	v_cvt_pk_fp8_f32 v242, v228, v229 op_sel:[0,0,1]
	v_cvt_pk_fp8_f32 v243, v232, v233 op_sel:[0,0,1]
	v_cvt_pk_fp8_f32 v244, v236, v237 op_sel:[0,0,1]
	v_cvt_pk_fp8_f32 v245, v240, v241 op_sel:[0,0,1]
	s_nop 0
	global_store_dwordx4 v77, v[242:245], s[6:7]
	ds_read_b32 v226, v214
	ds_read_b32 v227, v214 offset:512
	ds_read_b32 v228, v214 offset:1024
	ds_read_b32 v229, v214 offset:1536
	ds_read_b32 v230, v214 offset:2048
	ds_read_b32 v231, v214 offset:2560
	ds_read_b32 v232, v214 offset:3072
	ds_read_b32 v233, v214 offset:3584
	ds_read_b32 v234, v214 offset:4096
	ds_read_b32 v235, v214 offset:4608
	ds_read_b32 v236, v214 offset:5120
	ds_read_b32 v237, v214 offset:5632
	ds_read_b32 v238, v214 offset:6144
	ds_read_b32 v239, v214 offset:6656
	ds_read_b32 v240, v214 offset:7168
	ds_read_b32 v241, v214 offset:7680
	s_waitcnt lgkmcnt(0)
	v_max_f32_e32 v226, v226, v226
	v_max_f32_e32 v227, v227, v227
	v_max_f32_e32 v228, v228, v228
	v_max_f32_e32 v229, v229, v229
	v_max_f32_e32 v230, v230, v230
	v_max_f32_e32 v231, v231, v231
	v_max_f32_e32 v232, v232, v232
	v_max_f32_e32 v233, v233, v233
	v_max_f32_e32 v234, v234, v234
	v_max_f32_e32 v235, v235, v235
	v_max_f32_e32 v236, v236, v236
	v_max_f32_e32 v237, v237, v237
	v_max_f32_e32 v238, v238, v238
	v_max_f32_e32 v239, v239, v239
	v_max_f32_e32 v240, v240, v240
	v_max_f32_e32 v241, v241, v241
	v_med3_f32 v226, v226, s62, v95
	v_med3_f32 v227, v227, s62, v95
	v_med3_f32 v228, v228, s62, v95
	v_med3_f32 v229, v229, s62, v95
	v_med3_f32 v230, v230, s62, v95
	v_med3_f32 v231, v231, s62, v95
	v_med3_f32 v232, v232, s62, v95
	v_med3_f32 v233, v233, s62, v95
	v_med3_f32 v234, v234, s62, v95
	v_med3_f32 v235, v235, s62, v95
	v_med3_f32 v236, v236, s62, v95
	v_med3_f32 v237, v237, s62, v95
	v_med3_f32 v238, v238, s62, v95
	v_med3_f32 v239, v239, s62, v95
	v_med3_f32 v240, v240, s62, v95
	v_med3_f32 v241, v241, s62, v95
	v_mov_b32_e32 v242, 0
	v_mov_b32_e32 v243, 0
	v_mov_b32_e32 v244, 0
	v_mov_b32_e32 v245, 0
	v_cvt_pk_fp8_f32 v242, v226, v227
	v_cvt_pk_fp8_f32 v243, v230, v231
	v_cvt_pk_fp8_f32 v244, v234, v235
	v_cvt_pk_fp8_f32 v245, v238, v239
	v_cvt_pk_fp8_f32 v242, v228, v229 op_sel:[0,0,1]
	v_cvt_pk_fp8_f32 v243, v232, v233 op_sel:[0,0,1]
	v_cvt_pk_fp8_f32 v244, v236, v237 op_sel:[0,0,1]
	v_cvt_pk_fp8_f32 v245, v240, v241 op_sel:[0,0,1]
	s_nop 0
	global_store_dwordx4 v78, v[242:245], s[6:7]
	s_waitcnt vmcnt(12)
	v_mul_f32_e32 v144, v26, v144
	v_mul_f32_e32 v145, v26, v145
	v_mul_f32_e32 v146, v26, v146
	v_mul_f32_e32 v147, v26, v147
	ds_write_b128 v209, v[144:147]
	v_mul_f32_e32 v148, v27, v148
	v_mul_f32_e32 v149, v27, v149
	v_mul_f32_e32 v150, v27, v150
	v_mul_f32_e32 v151, v27, v151
	ds_write_b128 v209, v[148:151] offset:1024
	v_mul_f32_e32 v152, v28, v152
	v_mul_f32_e32 v153, v28, v153
	v_mul_f32_e32 v154, v28, v154
	v_mul_f32_e32 v155, v28, v155
	ds_write_b128 v209, v[152:155] offset:2048
	v_mul_f32_e32 v156, v29, v156
	v_mul_f32_e32 v157, v29, v157
	v_mul_f32_e32 v158, v29, v158
	v_mul_f32_e32 v159, v29, v159
	ds_write_b128 v209, v[156:159] offset:3072
	v_mul_f32_e32 v160, v30, v160
	v_mul_f32_e32 v161, v30, v161
	v_mul_f32_e32 v162, v30, v162
	v_mul_f32_e32 v163, v30, v163
	ds_write_b128 v209, v[160:163] offset:4096
	v_mul_f32_e32 v164, v31, v164
	v_mul_f32_e32 v165, v31, v165
	v_mul_f32_e32 v166, v31, v166
	v_mul_f32_e32 v167, v31, v167
	ds_write_b128 v209, v[164:167] offset:5120
	v_mul_f32_e32 v168, v32, v168
	v_mul_f32_e32 v169, v32, v169
	v_mul_f32_e32 v170, v32, v170
	v_mul_f32_e32 v171, v32, v171
	ds_write_b128 v209, v[168:171] offset:6144
	v_mul_f32_e32 v172, v33, v172
	v_mul_f32_e32 v173, v33, v173
	v_mul_f32_e32 v174, v33, v174
	v_mul_f32_e32 v175, v33, v175
	ds_write_b128 v209, v[172:175] offset:7168
	s_waitcnt lgkmcnt(0)
	s_barrier
; #define GAS __attribute__((address_space(1)))
; #define LAS __attribute__((address_space(3)))
; #define LDS_WAIT() asm volatile("s_waitcnt lgkmcnt(0)" ::: "memory")
;     const int pr = item >> 1, kb = 2 * (pr / nblk) + (item & 1), nb = pr % nblk, k0 = 64 * kb, n0 = 32 * nb;
;     const int nr = n0 + (lane & 31); const int sc = MAP == 1 ? src_col_in(nr) : nr;
;     float v[32];
; #pragma unroll
;     for (int i = 0; i < 32; ++i) v[i] = sc >= 0 ? W[(size_t)(k0 + 2 * i + (lane >> 5)) * Nsrc + sc] : 0.f;
; #pragma unroll
;     for (int i = 0; i < 32; ++i) { const int k = k0 + 2 * i + (lane >> 5); float x = v[i] * wscale; if (KS) x *= (k < ksplit ? ksA[k] : ksB[k - ksplit]); scr[(2 * i + (lane >> 5)) * 33 + (lane & 31)] = x; }
;     LDS_WAIT(); asm volatile("" ::: "memory");
;     const int c = lane & 7;
; #pragma unroll
;     for (int j = 0; j < 4; ++j) { const int n = (lane >> 3) + 8 * j; const LAS float* s = scr + (8 * c) * 33 + n;
;         const unsigned long long o = (unsigned long long)pg8::pk4_fp8(s[0 * 33], s[1 * 33], s[2 * 33], s[3 * 33]) | ((unsigned long long)pg8::pk4_fp8(s[4 * 33], s[5 * 33], s[6 * 33], s[7 * 33]) << 32);
;         *(GAS unsigned long long*)(WT + (size_t)(n0 + n) * K + k0 + 8 * c) = o; }
;     LDS_WAIT(); asm volatile("" ::: "memory");
	s_add_u32 s8, s30, 0x6000
	s_addc_u32 s9, s31, 0
	global_load_dwordx4 v[144:147], v74, s[8:9]
	s_add_u32 s8, s8, 0x20000
	s_addc_u32 s9, s9, 0
	global_load_dwordx4 v[148:151], v74, s[8:9]
	s_add_u32 s8, s8, 0x20000
	s_addc_u32 s9, s9, 0
	global_load_dwordx4 v[152:155], v74, s[8:9]
	s_add_u32 s8, s8, 0x20000
	s_addc_u32 s9, s9, 0
	global_load_dwordx4 v[156:159], v74, s[8:9]
	s_add_u32 s8, s8, 0x20000
	s_addc_u32 s9, s9, 0
	global_load_dwordx4 v[160:163], v74, s[8:9]
	s_add_u32 s8, s8, 0x20000
	s_addc_u32 s9, s9, 0
	global_load_dwordx4 v[164:167], v74, s[8:9]
	s_add_u32 s8, s8, 0x20000
	s_addc_u32 s9, s9, 0
	global_load_dwordx4 v[168:171], v74, s[8:9]
	s_add_u32 s8, s8, 0x20000
	s_addc_u32 s9, s9, 0
	global_load_dwordx4 v[172:175], v74, s[8:9]
	s_add_u32 s6, s32, 0x1000000
	s_addc_u32 s7, s33, 0
	ds_read_b32 v226, v211
	ds_read_b32 v227, v211 offset:512
	ds_read_b32 v228, v211 offset:1024
	ds_read_b32 v229, v211 offset:1536
	ds_read_b32 v230, v211 offset:2048
	ds_read_b32 v231, v211 offset:2560
	ds_read_b32 v232, v211 offset:3072
	ds_read_b32 v233, v211 offset:3584
	ds_read_b32 v234, v211 offset:4096
	ds_read_b32 v235, v211 offset:4608
	ds_read_b32 v236, v211 offset:5120
	ds_read_b32 v237, v211 offset:5632
	ds_read_b32 v238, v211 offset:6144
	ds_read_b32 v239, v211 offset:6656
	ds_read_b32 v240, v211 offset:7168
	ds_read_b32 v241, v211 offset:7680
	s_waitcnt lgkmcnt(0)
	v_max_f32_e32 v226, v226, v226
	v_max_f32_e32 v227, v227, v227
	v_max_f32_e32 v228, v228, v228
	v_max_f32_e32 v229, v229, v229
	v_max_f32_e32 v230, v230, v230
	v_max_f32_e32 v231, v231, v231
	v_max_f32_e32 v232, v232, v232
	v_max_f32_e32 v233, v233, v233
	v_max_f32_e32 v234, v234, v234
	v_max_f32_e32 v235, v235, v235
	v_max_f32_e32 v236, v236, v236
	v_max_f32_e32 v237, v237, v237
	v_max_f32_e32 v238, v238, v238
	v_max_f32_e32 v239, v239, v239
	v_max_f32_e32 v240, v240, v240
	v_max_f32_e32 v241, v241, v241
	v_med3_f32 v226, v226, s62, v95
	v_med3_f32 v227, v227, s62, v95
	v_med3_f32 v228, v228, s62, v95
	v_med3_f32 v229, v229, s62, v95
	v_med3_f32 v230, v230, s62, v95
	v_med3_f32 v231, v231, s62, v95
	v_med3_f32 v232, v232, s62, v95
	v_med3_f32 v233, v233, s62, v95
	v_med3_f32 v234, v234, s62, v95
	v_med3_f32 v235, v235, s62, v95
	v_med3_f32 v236, v236, s62, v95
	v_med3_f32 v237, v237, s62, v95
	v_med3_f32 v238, v238, s62, v95
	v_med3_f32 v239, v239, s62, v95
	v_med3_f32 v240, v240, s62, v95
	v_med3_f32 v241, v241, s62, v95
	v_mov_b32_e32 v242, 0
	v_mov_b32_e32 v243, 0
	v_mov_b32_e32 v244, 0
	v_mov_b32_e32 v245, 0
	v_cvt_pk_fp8_f32 v242, v226, v227
	v_cvt_pk_fp8_f32 v243, v230, v231
	v_cvt_pk_fp8_f32 v244, v234, v235
	v_cvt_pk_fp8_f32 v245, v238, v239
	v_cvt_pk_fp8_f32 v242, v228, v229 op_sel:[0,0,1]
	v_cvt_pk_fp8_f32 v243, v232, v233 op_sel:[0,0,1]
	v_cvt_pk_fp8_f32 v244, v236, v237 op_sel:[0,0,1]
	v_cvt_pk_fp8_f32 v245, v240, v241 op_sel:[0,0,1]
	s_nop 0
	global_store_dwordx4 v77, v[242:245], s[6:7]
	ds_read_b32 v226, v213
	ds_read_b32 v227, v213 offset:512
	ds_read_b32 v228, v213 offset:1024
	ds_read_b32 v229, v213 offset:1536
	ds_read_b32 v230, v213 offset:2048
	ds_read_b32 v231, v213 offset:2560
	ds_read_b32 v232, v213 offset:3072
	ds_read_b32 v233, v213 offset:3584
	ds_read_b32 v234, v213 offset:4096
	ds_read_b32 v235, v213 offset:4608
	ds_read_b32 v236, v213 offset:5120
	ds_read_b32 v237, v213 offset:5632
	ds_read_b32 v238, v213 offset:6144
	ds_read_b32 v239, v213 offset:6656
	ds_read_b32 v240, v213 offset:7168
	ds_read_b32 v241, v213 offset:7680
	s_waitcnt lgkmcnt(0)
	v_max_f32_e32 v226, v226, v226
	v_max_f32_e32 v227, v227, v227
	v_max_f32_e32 v228, v228, v228
	v_max_f32_e32 v229, v229, v229
	v_max_f32_e32 v230, v230, v230
	v_max_f32_e32 v231, v231, v231
	v_max_f32_e32 v232, v232, v232
	v_max_f32_e32 v233, v233, v233
	v_max_f32_e32 v234, v234, v234
	v_max_f32_e32 v235, v235, v235
	v_max_f32_e32 v236, v236, v236
	v_max_f32_e32 v237, v237, v237
	v_max_f32_e32 v238, v238, v238
	v_max_f32_e32 v239, v239, v239
	v_max_f32_e32 v240, v240, v240
	v_max_f32_e32 v241, v241, v241
	v_med3_f32 v226, v226, s62, v95
	v_med3_f32 v227, v227, s62, v95
	v_med3_f32 v228, v228, s62, v95
	v_med3_f32 v229, v229, s62, v95
	v_med3_f32 v230, v230, s62, v95
	v_med3_f32 v231, v231, s62, v95
	v_med3_f32 v232, v232, s62, v95
	v_med3_f32 v233, v233, s62, v95
	v_med3_f32 v234, v234, s62, v95
	v_med3_f32 v235, v235, s62, v95
	v_med3_f32 v236, v236, s62, v95
	v_med3_f32 v237, v237, s62, v95
	v_med3_f32 v238, v238, s62, v95
	v_med3_f32 v239, v239, s62, v95
	v_med3_f32 v240, v240, s62, v95
	v_med3_f32 v241, v241, s62, v95
	v_mov_b32_e32 v242, 0
	v_mov_b32_e32 v243, 0
	v_mov_b32_e32 v244, 0
	v_mov_b32_e32 v245, 0
	v_cvt_pk_fp8_f32 v242, v226, v227
	v_cvt_pk_fp8_f32 v243, v230, v231
	v_cvt_pk_fp8_f32 v244, v234, v235
	v_cvt_pk_fp8_f32 v245, v238, v239
	v_cvt_pk_fp8_f32 v242, v228, v229 op_sel:[0,0,1]
	v_cvt_pk_fp8_f32 v243, v232, v233 op_sel:[0,0,1]
	v_cvt_pk_fp8_f32 v244, v236, v237 op_sel:[0,0,1]
	v_cvt_pk_fp8_f32 v245, v240, v241 op_sel:[0,0,1]
	s_nop 0
	global_store_dwordx4 v78, v[242:245], s[6:7]
	s_waitcnt vmcnt(12)
	v_mul_f32_e32 v176, v26, v176
	v_mul_f32_e32 v177, v26, v177
	v_mul_f32_e32 v178, v26, v178
	v_mul_f32_e32 v179, v26, v179
	ds_write_b128 v210, v[176:179]
	v_mul_f32_e32 v180, v27, v180
	v_mul_f32_e32 v181, v27, v181
	v_mul_f32_e32 v182, v27, v182
	v_mul_f32_e32 v183, v27, v183
	ds_write_b128 v210, v[180:183] offset:1024
	v_mul_f32_e32 v184, v28, v184
	v_mul_f32_e32 v185, v28, v185
	v_mul_f32_e32 v186, v28, v186
	v_mul_f32_e32 v187, v28, v187
	ds_write_b128 v210, v[184:187] offset:2048
	v_mul_f32_e32 v188, v29, v188
	v_mul_f32_e32 v189, v29, v189
	v_mul_f32_e32 v190, v29, v190
	v_mul_f32_e32 v191, v29, v191
	ds_write_b128 v210, v[188:191] offset:3072
	v_mul_f32_e32 v192, v30, v192
	v_mul_f32_e32 v193, v30, v193
	v_mul_f32_e32 v194, v30, v194
	v_mul_f32_e32 v195, v30, v195
	ds_write_b128 v210, v[192:195] offset:4096
	v_mul_f32_e32 v196, v31, v196
	v_mul_f32_e32 v197, v31, v197
	v_mul_f32_e32 v198, v31, v198
	v_mul_f32_e32 v199, v31, v199
	ds_write_b128 v210, v[196:199] offset:5120
	v_mul_f32_e32 v200, v32, v200
	v_mul_f32_e32 v201, v32, v201
	v_mul_f32_e32 v202, v32, v202
	v_mul_f32_e32 v203, v32, v203
	ds_write_b128 v210, v[200:203] offset:6144
	v_mul_f32_e32 v204, v33, v204
	v_mul_f32_e32 v205, v33, v205
	v_mul_f32_e32 v206, v33, v206
	v_mul_f32_e32 v207, v33, v207
	ds_write_b128 v210, v[204:207] offset:7168
	s_waitcnt lgkmcnt(0)
	s_barrier
; #define GAS __attribute__((address_space(1)))
; #define LAS __attribute__((address_space(3)))
; #define LDS_WAIT() asm volatile("s_waitcnt lgkmcnt(0)" ::: "memory")
;     const int pr = item >> 1, kb = 2 * (pr / nblk) + (item & 1), nb = pr % nblk, k0 = 64 * kb, n0 = 32 * nb;
;     const int nr = n0 + (lane & 31); const int sc = MAP == 1 ? src_col_in(nr) : nr;
;     float v[32];
; #pragma unroll
;     for (int i = 0; i < 32; ++i) v[i] = sc >= 0 ? W[(size_t)(k0 + 2 * i + (lane >> 5)) * Nsrc + sc] : 0.f;
; #pragma unroll
;     for (int i = 0; i < 32; ++i) { const int k = k0 + 2 * i + (lane >> 5); float x = v[i] * wscale; if (KS) x *= (k < ksplit ? ksA[k] : ksB[k - ksplit]); scr[(2 * i + (lane >> 5)) * 33 + (lane & 31)] = x; }
;     LDS_WAIT(); asm volatile("" ::: "memory");
;     const int c = lane & 7;
; #pragma unroll
;     for (int j = 0; j < 4; ++j) { const int n = (lane >> 3) + 8 * j; const LAS float* s = scr + (8 * c) * 33 + n;
;         const unsigned long long o = (unsigned long long)pg8::pk4_fp8(s[0 * 33], s[1 * 33], s[2 * 33], s[3 * 33]) | ((unsigned long long)pg8::pk4_fp8(s[4 * 33], s[5 * 33], s[6 * 33], s[7 * 33]) << 32);
;         *(GAS unsigned long long*)(WT + (size_t)(n0 + n) * K + k0 + 8 * c) = o; }
;     LDS_WAIT(); asm volatile("" ::: "memory");
	s_add_u32 s8, s30, 0x7000
	s_addc_u32 s9, s31, 0
	global_load_dwordx4 v[176:179], v74, s[8:9]
	s_add_u32 s8, s8, 0x20000
	s_addc_u32 s9, s9, 0
	global_load_dwordx4 v[180:183], v74, s[8:9]
	s_add_u32 s8, s8, 0x20000
	s_addc_u32 s9, s9, 0
	global_load_dwordx4 v[184:187], v74, s[8:9]
	s_add_u32 s8, s8, 0x20000
	s_addc_u32 s9, s9, 0
	global_load_dwordx4 v[188:191], v74, s[8:9]
	s_add_u32 s8, s8, 0x20000
	s_addc_u32 s9, s9, 0
	global_load_dwordx4 v[192:195], v74, s[8:9]
	s_add_u32 s8, s8, 0x20000
	s_addc_u32 s9, s9, 0
	global_load_dwordx4 v[196:199], v74, s[8:9]
	s_add_u32 s8, s8, 0x20000
	s_addc_u32 s9, s9, 0
	global_load_dwordx4 v[200:203], v74, s[8:9]
	s_add_u32 s8, s8, 0x20000
	s_addc_u32 s9, s9, 0
	global_load_dwordx4 v[204:207], v74, s[8:9]
	s_add_u32 s6, s32, 0x1400000
	s_addc_u32 s7, s33, 0
	ds_read_b32 v226, v212
	ds_read_b32 v227, v212 offset:512
	ds_read_b32 v228, v212 offset:1024
	ds_read_b32 v229, v212 offset:1536
	ds_read_b32 v230, v212 offset:2048
	ds_read_b32 v231, v212 offset:2560
	ds_read_b32 v232, v212 offset:3072
	ds_read_b32 v233, v212 offset:3584
	ds_read_b32 v234, v212 offset:4096
	ds_read_b32 v235, v212 offset:4608
	ds_read_b32 v236, v212 offset:5120
	ds_read_b32 v237, v212 offset:5632
	ds_read_b32 v238, v212 offset:6144
	ds_read_b32 v239, v212 offset:6656
	ds_read_b32 v240, v212 offset:7168
	ds_read_b32 v241, v212 offset:7680
	s_waitcnt lgkmcnt(0)
	v_max_f32_e32 v226, v226, v226
	v_max_f32_e32 v227, v227, v227
	v_max_f32_e32 v228, v228, v228
	v_max_f32_e32 v229, v229, v229
	v_max_f32_e32 v230, v230, v230
	v_max_f32_e32 v231, v231, v231
	v_max_f32_e32 v232, v232, v232
	v_max_f32_e32 v233, v233, v233
	v_max_f32_e32 v234, v234, v234
	v_max_f32_e32 v235, v235, v235
	v_max_f32_e32 v236, v236, v236
	v_max_f32_e32 v237, v237, v237
	v_max_f32_e32 v238, v238, v238
	v_max_f32_e32 v239, v239, v239
	v_max_f32_e32 v240, v240, v240
	v_max_f32_e32 v241, v241, v241
	v_med3_f32 v226, v226, s62, v95
	v_med3_f32 v227, v227, s62, v95
	v_med3_f32 v228, v228, s62, v95
	v_med3_f32 v229, v229, s62, v95
	v_med3_f32 v230, v230, s62, v95
	v_med3_f32 v231, v231, s62, v95
	v_med3_f32 v232, v232, s62, v95
	v_med3_f32 v233, v233, s62, v95
	v_med3_f32 v234, v234, s62, v95
	v_med3_f32 v235, v235, s62, v95
	v_med3_f32 v236, v236, s62, v95
	v_med3_f32 v237, v237, s62, v95
	v_med3_f32 v238, v238, s62, v95
	v_med3_f32 v239, v239, s62, v95
	v_med3_f32 v240, v240, s62, v95
	v_med3_f32 v241, v241, s62, v95
	v_mov_b32_e32 v242, 0
	v_mov_b32_e32 v243, 0
	v_mov_b32_e32 v244, 0
	v_mov_b32_e32 v245, 0
	v_cvt_pk_fp8_f32 v242, v226, v227
	v_cvt_pk_fp8_f32 v243, v230, v231
	v_cvt_pk_fp8_f32 v244, v234, v235
	v_cvt_pk_fp8_f32 v245, v238, v239
	v_cvt_pk_fp8_f32 v242, v228, v229 op_sel:[0,0,1]
	v_cvt_pk_fp8_f32 v243, v232, v233 op_sel:[0,0,1]
	v_cvt_pk_fp8_f32 v244, v236, v237 op_sel:[0,0,1]
	v_cvt_pk_fp8_f32 v245, v240, v241 op_sel:[0,0,1]
	s_nop 0
	global_store_dwordx4 v77, v[242:245], s[6:7]
	ds_read_b32 v226, v214
	ds_read_b32 v227, v214 offset:512
	ds_read_b32 v228, v214 offset:1024
	ds_read_b32 v229, v214 offset:1536
	ds_read_b32 v230, v214 offset:2048
	ds_read_b32 v231, v214 offset:2560
	ds_read_b32 v232, v214 offset:3072
	ds_read_b32 v233, v214 offset:3584
	ds_read_b32 v234, v214 offset:4096
	ds_read_b32 v235, v214 offset:4608
	ds_read_b32 v236, v214 offset:5120
	ds_read_b32 v237, v214 offset:5632
	ds_read_b32 v238, v214 offset:6144
	ds_read_b32 v239, v214 offset:6656
	ds_read_b32 v240, v214 offset:7168
	ds_read_b32 v241, v214 offset:7680
	s_waitcnt lgkmcnt(0)
	v_max_f32_e32 v226, v226, v226
	v_max_f32_e32 v227, v227, v227
	v_max_f32_e32 v228, v228, v228
	v_max_f32_e32 v229, v229, v229
	v_max_f32_e32 v230, v230, v230
	v_max_f32_e32 v231, v231, v231
	v_max_f32_e32 v232, v232, v232
	v_max_f32_e32 v233, v233, v233
	v_max_f32_e32 v234, v234, v234
	v_max_f32_e32 v235, v235, v235
	v_max_f32_e32 v236, v236, v236
	v_max_f32_e32 v237, v237, v237
	v_max_f32_e32 v238, v238, v238
	v_max_f32_e32 v239, v239, v239
	v_max_f32_e32 v240, v240, v240
	v_max_f32_e32 v241, v241, v241
	v_med3_f32 v226, v226, s62, v95
	v_med3_f32 v227, v227, s62, v95
	v_med3_f32 v228, v228, s62, v95
	v_med3_f32 v229, v229, s62, v95
	v_med3_f32 v230, v230, s62, v95
	v_med3_f32 v231, v231, s62, v95
	v_med3_f32 v232, v232, s62, v95
	v_med3_f32 v233, v233, s62, v95
	v_med3_f32 v234, v234, s62, v95
	v_med3_f32 v235, v235, s62, v95
	v_med3_f32 v236, v236, s62, v95
	v_med3_f32 v237, v237, s62, v95
	v_med3_f32 v238, v238, s62, v95
	v_med3_f32 v239, v239, s62, v95
	v_med3_f32 v240, v240, s62, v95
	v_med3_f32 v241, v241, s62, v95
	v_mov_b32_e32 v242, 0
	v_mov_b32_e32 v243, 0
	v_mov_b32_e32 v244, 0
	v_mov_b32_e32 v245, 0
	v_cvt_pk_fp8_f32 v242, v226, v227
	v_cvt_pk_fp8_f32 v243, v230, v231
	v_cvt_pk_fp8_f32 v244, v234, v235
	v_cvt_pk_fp8_f32 v245, v238, v239
	v_cvt_pk_fp8_f32 v242, v228, v229 op_sel:[0,0,1]
	v_cvt_pk_fp8_f32 v243, v232, v233 op_sel:[0,0,1]
	v_cvt_pk_fp8_f32 v244, v236, v237 op_sel:[0,0,1]
	v_cvt_pk_fp8_f32 v245, v240, v241 op_sel:[0,0,1]
	s_nop 0
	global_store_dwordx4 v78, v[242:245], s[6:7]
	s_waitcnt vmcnt(12)
	v_mul_f32_e32 v144, v26, v144
	v_mul_f32_e32 v145, v26, v145
	v_mul_f32_e32 v146, v26, v146
	v_mul_f32_e32 v147, v26, v147
	ds_write_b128 v209, v[144:147]
	v_mul_f32_e32 v148, v27, v148
	v_mul_f32_e32 v149, v27, v149
	v_mul_f32_e32 v150, v27, v150
	v_mul_f32_e32 v151, v27, v151
	ds_write_b128 v209, v[148:151] offset:1024
	v_mul_f32_e32 v152, v28, v152
	v_mul_f32_e32 v153, v28, v153
	v_mul_f32_e32 v154, v28, v154
	v_mul_f32_e32 v155, v28, v155
	ds_write_b128 v209, v[152:155] offset:2048
	v_mul_f32_e32 v156, v29, v156
	v_mul_f32_e32 v157, v29, v157
	v_mul_f32_e32 v158, v29, v158
	v_mul_f32_e32 v159, v29, v159
	ds_write_b128 v209, v[156:159] offset:3072
	v_mul_f32_e32 v160, v30, v160
	v_mul_f32_e32 v161, v30, v161
	v_mul_f32_e32 v162, v30, v162
	v_mul_f32_e32 v163, v30, v163
	ds_write_b128 v209, v[160:163] offset:4096
	v_mul_f32_e32 v164, v31, v164
	v_mul_f32_e32 v165, v31, v165
	v_mul_f32_e32 v166, v31, v166
	v_mul_f32_e32 v167, v31, v167
	ds_write_b128 v209, v[164:167] offset:5120
	v_mul_f32_e32 v168, v32, v168
	v_mul_f32_e32 v169, v32, v169
	v_mul_f32_e32 v170, v32, v170
	v_mul_f32_e32 v171, v32, v171
	ds_write_b128 v209, v[168:171] offset:6144
	v_mul_f32_e32 v172, v33, v172
	v_mul_f32_e32 v173, v33, v173
	v_mul_f32_e32 v174, v33, v174
	v_mul_f32_e32 v175, v33, v175
	ds_write_b128 v209, v[172:175] offset:7168
	s_waitcnt lgkmcnt(0)
	s_barrier
; #define GAS __attribute__((address_space(1)))
; #define LAS __attribute__((address_space(3)))
; #define LDS_WAIT() asm volatile("s_waitcnt lgkmcnt(0)" ::: "memory")
;     const int pr = item >> 1, kb = 2 * (pr / nblk) + (item & 1), nb = pr % nblk, k0 = 64 * kb, n0 = 32 * nb;
;     const int nr = n0 + (lane & 31); const int sc = MAP == 1 ? src_col_in(nr) : nr;
;     float v[32];
; #pragma unroll
;     for (int i = 0; i < 32; ++i) v[i] = sc >= 0 ? W[(size_t)(k0 + 2 * i + (lane >> 5)) * Nsrc + sc] : 0.f;
; #pragma unroll
;     for (int i = 0; i < 32; ++i) { const int k = k0 + 2 * i + (lane >> 5); float x = v[i] * wscale; if (KS) x *= (k < ksplit ? ksA[k] : ksB[k - ksplit]); scr[(2 * i + (lane >> 5)) * 33 + (lane & 31)] = x; }
;     LDS_WAIT(); asm volatile("" ::: "memory");
;     const int c = lane & 7;
; #pragma unroll
;     for (int j = 0; j < 4; ++j) { const int n = (lane >> 3) + 8 * j; const LAS float* s = scr + (8 * c) * 33 + n;
;         const unsigned long long o = (unsigned long long)pg8::pk4_fp8(s[0 * 33], s[1 * 33], s[2 * 33], s[3 * 33]) | ((unsigned long long)pg8::pk4_fp8(s[4 * 33], s[5 * 33], s[6 * 33], s[7 * 33]) << 32);
;         *(GAS unsigned long long*)(WT + (size_t)(n0 + n) * K + k0 + 8 * c) = o; }
;     LDS_WAIT(); asm volatile("" ::: "memory");
	s_add_u32 s8, s30, 0x8000
	s_addc_u32 s9, s31, 0
	global_load_dwordx4 v[144:147], v74, s[8:9]
	s_add_u32 s8, s8, 0x20000
	s_addc_u32 s9, s9, 0
	global_load_dwordx4 v[148:151], v74, s[8:9]
	s_add_u32 s8, s8, 0x20000
	s_addc_u32 s9, s9, 0
	global_load_dwordx4 v[152:155], v74, s[8:9]
	s_add_u32 s8, s8, 0x20000
	s_addc_u32 s9, s9, 0
	global_load_dwordx4 v[156:159], v74, s[8:9]
	s_add_u32 s8, s8, 0x20000
	s_addc_u32 s9, s9, 0
	global_load_dwordx4 v[160:163], v74, s[8:9]
	s_add_u32 s8, s8, 0x20000
	s_addc_u32 s9, s9, 0
	global_load_dwordx4 v[164:167], v74, s[8:9]
	s_add_u32 s8, s8, 0x20000
	s_addc_u32 s9, s9, 0
	global_load_dwordx4 v[168:171], v74, s[8:9]
	s_add_u32 s8, s8, 0x20000
	s_addc_u32 s9, s9, 0
	global_load_dwordx4 v[172:175], v74, s[8:9]
	s_add_u32 s6, s32, 0x1800000
	s_addc_u32 s7, s33, 0
	ds_read_b32 v226, v211
	ds_read_b32 v227, v211 offset:512
	ds_read_b32 v228, v211 offset:1024
	ds_read_b32 v229, v211 offset:1536
	ds_read_b32 v230, v211 offset:2048
	ds_read_b32 v231, v211 offset:2560
	ds_read_b32 v232, v211 offset:3072
	ds_read_b32 v233, v211 offset:3584
	ds_read_b32 v234, v211 offset:4096
	ds_read_b32 v235, v211 offset:4608
	ds_read_b32 v236, v211 offset:5120
	ds_read_b32 v237, v211 offset:5632
	ds_read_b32 v238, v211 offset:6144
	ds_read_b32 v239, v211 offset:6656
	ds_read_b32 v240, v211 offset:7168
	ds_read_b32 v241, v211 offset:7680
	s_waitcnt lgkmcnt(0)
	v_max_f32_e32 v226, v226, v226
	v_max_f32_e32 v227, v227, v227
	v_max_f32_e32 v228, v228, v228
	v_max_f32_e32 v229, v229, v229
	v_max_f32_e32 v230, v230, v230
	v_max_f32_e32 v231, v231, v231
	v_max_f32_e32 v232, v232, v232
	v_max_f32_e32 v233, v233, v233
	v_max_f32_e32 v234, v234, v234
	v_max_f32_e32 v235, v235, v235
	v_max_f32_e32 v236, v236, v236
	v_max_f32_e32 v237, v237, v237
	v_max_f32_e32 v238, v238, v238
	v_max_f32_e32 v239, v239, v239
	v_max_f32_e32 v240, v240, v240
	v_max_f32_e32 v241, v241, v241
	v_med3_f32 v226, v226, s62, v95
	v_med3_f32 v227, v227, s62, v95
	v_med3_f32 v228, v228, s62, v95
	v_med3_f32 v229, v229, s62, v95
	v_med3_f32 v230, v230, s62, v95
	v_med3_f32 v231, v231, s62, v95
	v_med3_f32 v232, v232, s62, v95
	v_med3_f32 v233, v233, s62, v95
	v_med3_f32 v234, v234, s62, v95
	v_med3_f32 v235, v235, s62, v95
	v_med3_f32 v236, v236, s62, v95
	v_med3_f32 v237, v237, s62, v95
	v_med3_f32 v238, v238, s62, v95
	v_med3_f32 v239, v239, s62, v95
	v_med3_f32 v240, v240, s62, v95
	v_med3_f32 v241, v241, s62, v95
	v_mov_b32_e32 v242, 0
	v_mov_b32_e32 v243, 0
	v_mov_b32_e32 v244, 0
	v_mov_b32_e32 v245, 0
	v_cvt_pk_fp8_f32 v242, v226, v227
	v_cvt_pk_fp8_f32 v243, v230, v231
	v_cvt_pk_fp8_f32 v244, v234, v235
	v_cvt_pk_fp8_f32 v245, v238, v239
	v_cvt_pk_fp8_f32 v242, v228, v229 op_sel:[0,0,1]
	v_cvt_pk_fp8_f32 v243, v232, v233 op_sel:[0,0,1]
	v_cvt_pk_fp8_f32 v244, v236, v237 op_sel:[0,0,1]
	v_cvt_pk_fp8_f32 v245, v240, v241 op_sel:[0,0,1]
	s_nop 0
	global_store_dwordx4 v77, v[242:245], s[6:7]
	ds_read_b32 v226, v213
	ds_read_b32 v227, v213 offset:512
	ds_read_b32 v228, v213 offset:1024
	ds_read_b32 v229, v213 offset:1536
	ds_read_b32 v230, v213 offset:2048
	ds_read_b32 v231, v213 offset:2560
	ds_read_b32 v232, v213 offset:3072
	ds_read_b32 v233, v213 offset:3584
	ds_read_b32 v234, v213 offset:4096
	ds_read_b32 v235, v213 offset:4608
	ds_read_b32 v236, v213 offset:5120
	ds_read_b32 v237, v213 offset:5632
	ds_read_b32 v238, v213 offset:6144
	ds_read_b32 v239, v213 offset:6656
	ds_read_b32 v240, v213 offset:7168
	ds_read_b32 v241, v213 offset:7680
	s_waitcnt lgkmcnt(0)
	v_max_f32_e32 v226, v226, v226
	v_max_f32_e32 v227, v227, v227
	v_max_f32_e32 v228, v228, v228
	v_max_f32_e32 v229, v229, v229
	v_max_f32_e32 v230, v230, v230
	v_max_f32_e32 v231, v231, v231
	v_max_f32_e32 v232, v232, v232
	v_max_f32_e32 v233, v233, v233
	v_max_f32_e32 v234, v234, v234
	v_max_f32_e32 v235, v235, v235
	v_max_f32_e32 v236, v236, v236
	v_max_f32_e32 v237, v237, v237
	v_max_f32_e32 v238, v238, v238
	v_max_f32_e32 v239, v239, v239
	v_max_f32_e32 v240, v240, v240
	v_max_f32_e32 v241, v241, v241
	v_med3_f32 v226, v226, s62, v95
	v_med3_f32 v227, v227, s62, v95
	v_med3_f32 v228, v228, s62, v95
	v_med3_f32 v229, v229, s62, v95
	v_med3_f32 v230, v230, s62, v95
	v_med3_f32 v231, v231, s62, v95
	v_med3_f32 v232, v232, s62, v95
	v_med3_f32 v233, v233, s62, v95
	v_med3_f32 v234, v234, s62, v95
	v_med3_f32 v235, v235, s62, v95
	v_med3_f32 v236, v236, s62, v95
	v_med3_f32 v237, v237, s62, v95
	v_med3_f32 v238, v238, s62, v95
	v_med3_f32 v239, v239, s62, v95
	v_med3_f32 v240, v240, s62, v95
	v_med3_f32 v241, v241, s62, v95
	v_mov_b32_e32 v242, 0
	v_mov_b32_e32 v243, 0
	v_mov_b32_e32 v244, 0
	v_mov_b32_e32 v245, 0
	v_cvt_pk_fp8_f32 v242, v226, v227
	v_cvt_pk_fp8_f32 v243, v230, v231
	v_cvt_pk_fp8_f32 v244, v234, v235
	v_cvt_pk_fp8_f32 v245, v238, v239
	v_cvt_pk_fp8_f32 v242, v228, v229 op_sel:[0,0,1]
	v_cvt_pk_fp8_f32 v243, v232, v233 op_sel:[0,0,1]
	v_cvt_pk_fp8_f32 v244, v236, v237 op_sel:[0,0,1]
	v_cvt_pk_fp8_f32 v245, v240, v241 op_sel:[0,0,1]
	s_nop 0
	global_store_dwordx4 v78, v[242:245], s[6:7]
	s_waitcnt vmcnt(12)
	v_mul_f32_e32 v176, v26, v176
	v_mul_f32_e32 v177, v26, v177
	v_mul_f32_e32 v178, v26, v178
	v_mul_f32_e32 v179, v26, v179
	ds_write_b128 v210, v[176:179]
	v_mul_f32_e32 v180, v27, v180
	v_mul_f32_e32 v181, v27, v181
	v_mul_f32_e32 v182, v27, v182
	v_mul_f32_e32 v183, v27, v183
	ds_write_b128 v210, v[180:183] offset:1024
	v_mul_f32_e32 v184, v28, v184
	v_mul_f32_e32 v185, v28, v185
	v_mul_f32_e32 v186, v28, v186
	v_mul_f32_e32 v187, v28, v187
	ds_write_b128 v210, v[184:187] offset:2048
	v_mul_f32_e32 v188, v29, v188
	v_mul_f32_e32 v189, v29, v189
	v_mul_f32_e32 v190, v29, v190
	v_mul_f32_e32 v191, v29, v191
	ds_write_b128 v210, v[188:191] offset:3072
	v_mul_f32_e32 v192, v30, v192
	v_mul_f32_e32 v193, v30, v193
	v_mul_f32_e32 v194, v30, v194
	v_mul_f32_e32 v195, v30, v195
	ds_write_b128 v210, v[192:195] offset:4096
	v_mul_f32_e32 v196, v31, v196
	v_mul_f32_e32 v197, v31, v197
	v_mul_f32_e32 v198, v31, v198
	v_mul_f32_e32 v199, v31, v199
	ds_write_b128 v210, v[196:199] offset:5120
	v_mul_f32_e32 v200, v32, v200
	v_mul_f32_e32 v201, v32, v201
	v_mul_f32_e32 v202, v32, v202
	v_mul_f32_e32 v203, v32, v203
	ds_write_b128 v210, v[200:203] offset:6144
	v_mul_f32_e32 v204, v33, v204
	v_mul_f32_e32 v205, v33, v205
	v_mul_f32_e32 v206, v33, v206
	v_mul_f32_e32 v207, v33, v207
	ds_write_b128 v210, v[204:207] offset:7168
	s_waitcnt lgkmcnt(0)
	s_barrier
; #define GAS __attribute__((address_space(1)))
; #define LAS __attribute__((address_space(3)))
; #define LDS_WAIT() asm volatile("s_waitcnt lgkmcnt(0)" ::: "memory")
;     const int pr = item >> 1, kb = 2 * (pr / nblk) + (item & 1), nb = pr % nblk, k0 = 64 * kb, n0 = 32 * nb;
;     const int nr = n0 + (lane & 31); const int sc = MAP == 1 ? src_col_in(nr) : nr;
;     float v[32];
; #pragma unroll
;     for (int i = 0; i < 32; ++i) v[i] = sc >= 0 ? W[(size_t)(k0 + 2 * i + (lane >> 5)) * Nsrc + sc] : 0.f;
; #pragma unroll
;     for (int i = 0; i < 32; ++i) { const int k = k0 + 2 * i + (lane >> 5); float x = v[i] * wscale; if (KS) x *= (k < ksplit ? ksA[k] : ksB[k - ksplit]); scr[(2 * i + (lane >> 5)) * 33 + (lane & 31)] = x; }
;     LDS_WAIT(); asm volatile("" ::: "memory");
;     const int c = lane & 7;
; #pragma unroll
;     for (int j = 0; j < 4; ++j) { const int n = (lane >> 3) + 8 * j; const LAS float* s = scr + (8 * c) * 33 + n;
;         const unsigned long long o = (unsigned long long)pg8::pk4_fp8(s[0 * 33], s[1 * 33], s[2 * 33], s[3 * 33]) | ((unsigned long long)pg8::pk4_fp8(s[4 * 33], s[5 * 33], s[6 * 33], s[7 * 33]) << 32);
;         *(GAS unsigned long long*)(WT + (size_t)(n0 + n) * K + k0 + 8 * c) = o; }
;     LDS_WAIT(); asm volatile("" ::: "memory");
	s_add_u32 s8, s30, 0x9000
	s_addc_u32 s9, s31, 0
	global_load_dwordx4 v[176:179], v74, s[8:9]
	s_add_u32 s8, s8, 0x20000
	s_addc_u32 s9, s9, 0
	global_load_dwordx4 v[180:183], v74, s[8:9]
	s_add_u32 s8, s8, 0x20000
	s_addc_u32 s9, s9, 0
	global_load_dwordx4 v[184:187], v74, s[8:9]
	s_add_u32 s8, s8, 0x20000
	s_addc_u32 s9, s9, 0
	global_load_dwordx4 v[188:191], v74, s[8:9]
	s_add_u32 s8, s8, 0x20000
	s_addc_u32 s9, s9, 0
	global_load_dwordx4 v[192:195], v74, s[8:9]
	s_add_u32 s8, s8, 0x20000
	s_addc_u32 s9, s9, 0
	global_load_dwordx4 v[196:199], v74, s[8:9]
	s_add_u32 s8, s8, 0x20000
	s_addc_u32 s9, s9, 0
	global_load_dwordx4 v[200:203], v74, s[8:9]
	s_add_u32 s8, s8, 0x20000
	s_addc_u32 s9, s9, 0
	global_load_dwordx4 v[204:207], v74, s[8:9]
	s_add_u32 s6, s32, 0x1c00000
	s_addc_u32 s7, s33, 0
	ds_read_b32 v226, v212
	ds_read_b32 v227, v212 offset:512
	ds_read_b32 v228, v212 offset:1024
	ds_read_b32 v229, v212 offset:1536
	ds_read_b32 v230, v212 offset:2048
	ds_read_b32 v231, v212 offset:2560
	ds_read_b32 v232, v212 offset:3072
	ds_read_b32 v233, v212 offset:3584
	ds_read_b32 v234, v212 offset:4096
	ds_read_b32 v235, v212 offset:4608
	ds_read_b32 v236, v212 offset:5120
	ds_read_b32 v237, v212 offset:5632
	ds_read_b32 v238, v212 offset:6144
	ds_read_b32 v239, v212 offset:6656
	ds_read_b32 v240, v212 offset:7168
	ds_read_b32 v241, v212 offset:7680
	s_waitcnt lgkmcnt(0)
	v_max_f32_e32 v226, v226, v226
	v_max_f32_e32 v227, v227, v227
	v_max_f32_e32 v228, v228, v228
	v_max_f32_e32 v229, v229, v229
	v_max_f32_e32 v230, v230, v230
	v_max_f32_e32 v231, v231, v231
	v_max_f32_e32 v232, v232, v232
	v_max_f32_e32 v233, v233, v233
	v_max_f32_e32 v234, v234, v234
	v_max_f32_e32 v235, v235, v235
	v_max_f32_e32 v236, v236, v236
	v_max_f32_e32 v237, v237, v237
	v_max_f32_e32 v238, v238, v238
	v_max_f32_e32 v239, v239, v239
	v_max_f32_e32 v240, v240, v240
	v_max_f32_e32 v241, v241, v241
	v_med3_f32 v226, v226, s62, v95
	v_med3_f32 v227, v227, s62, v95
	v_med3_f32 v228, v228, s62, v95
	v_med3_f32 v229, v229, s62, v95
	v_med3_f32 v230, v230, s62, v95
	v_med3_f32 v231, v231, s62, v95
	v_med3_f32 v232, v232, s62, v95
	v_med3_f32 v233, v233, s62, v95
	v_med3_f32 v234, v234, s62, v95
	v_med3_f32 v235, v235, s62, v95
	v_med3_f32 v236, v236, s62, v95
	v_med3_f32 v237, v237, s62, v95
	v_med3_f32 v238, v238, s62, v95
	v_med3_f32 v239, v239, s62, v95
	v_med3_f32 v240, v240, s62, v95
	v_med3_f32 v241, v241, s62, v95
	v_mov_b32_e32 v242, 0
	v_mov_b32_e32 v243, 0
	v_mov_b32_e32 v244, 0
	v_mov_b32_e32 v245, 0
	v_cvt_pk_fp8_f32 v242, v226, v227
	v_cvt_pk_fp8_f32 v243, v230, v231
	v_cvt_pk_fp8_f32 v244, v234, v235
	v_cvt_pk_fp8_f32 v245, v238, v239
	v_cvt_pk_fp8_f32 v242, v228, v229 op_sel:[0,0,1]
	v_cvt_pk_fp8_f32 v243, v232, v233 op_sel:[0,0,1]
	v_cvt_pk_fp8_f32 v244, v236, v237 op_sel:[0,0,1]
	v_cvt_pk_fp8_f32 v245, v240, v241 op_sel:[0,0,1]
	s_nop 0
	global_store_dwordx4 v77, v[242:245], s[6:7]
	ds_read_b32 v226, v214
	ds_read_b32 v227, v214 offset:512
	ds_read_b32 v228, v214 offset:1024
	ds_read_b32 v229, v214 offset:1536
	ds_read_b32 v230, v214 offset:2048
	ds_read_b32 v231, v214 offset:2560
	ds_read_b32 v232, v214 offset:3072
	ds_read_b32 v233, v214 offset:3584
	ds_read_b32 v234, v214 offset:4096
	ds_read_b32 v235, v214 offset:4608
	ds_read_b32 v236, v214 offset:5120
	ds_read_b32 v237, v214 offset:5632
	ds_read_b32 v238, v214 offset:6144
	ds_read_b32 v239, v214 offset:6656
	ds_read_b32 v240, v214 offset:7168
	ds_read_b32 v241, v214 offset:7680
	s_waitcnt lgkmcnt(0)
	v_max_f32_e32 v226, v226, v226
	v_max_f32_e32 v227, v227, v227
	v_max_f32_e32 v228, v228, v228
	v_max_f32_e32 v229, v229, v229
	v_max_f32_e32 v230, v230, v230
	v_max_f32_e32 v231, v231, v231
	v_max_f32_e32 v232, v232, v232
	v_max_f32_e32 v233, v233, v233
	v_max_f32_e32 v234, v234, v234
	v_max_f32_e32 v235, v235, v235
	v_max_f32_e32 v236, v236, v236
	v_max_f32_e32 v237, v237, v237
	v_max_f32_e32 v238, v238, v238
	v_max_f32_e32 v239, v239, v239
	v_max_f32_e32 v240, v240, v240
	v_max_f32_e32 v241, v241, v241
	v_med3_f32 v226, v226, s62, v95
	v_med3_f32 v227, v227, s62, v95
	v_med3_f32 v228, v228, s62, v95
	v_med3_f32 v229, v229, s62, v95
	v_med3_f32 v230, v230, s62, v95
	v_med3_f32 v231, v231, s62, v95
	v_med3_f32 v232, v232, s62, v95
	v_med3_f32 v233, v233, s62, v95
	v_med3_f32 v234, v234, s62, v95
	v_med3_f32 v235, v235, s62, v95
	v_med3_f32 v236, v236, s62, v95
	v_med3_f32 v237, v237, s62, v95
	v_med3_f32 v238, v238, s62, v95
	v_med3_f32 v239, v239, s62, v95
	v_med3_f32 v240, v240, s62, v95
	v_med3_f32 v241, v241, s62, v95
	v_mov_b32_e32 v242, 0
	v_mov_b32_e32 v243, 0
	v_mov_b32_e32 v244, 0
	v_mov_b32_e32 v245, 0
	v_cvt_pk_fp8_f32 v242, v226, v227
	v_cvt_pk_fp8_f32 v243, v230, v231
	v_cvt_pk_fp8_f32 v244, v234, v235
	v_cvt_pk_fp8_f32 v245, v238, v239
	v_cvt_pk_fp8_f32 v242, v228, v229 op_sel:[0,0,1]
	v_cvt_pk_fp8_f32 v243, v232, v233 op_sel:[0,0,1]
	v_cvt_pk_fp8_f32 v244, v236, v237 op_sel:[0,0,1]
	v_cvt_pk_fp8_f32 v245, v240, v241 op_sel:[0,0,1]
	s_nop 0
	global_store_dwordx4 v78, v[242:245], s[6:7]
	s_waitcnt vmcnt(12)
	v_mul_f32_e32 v144, v26, v144
	v_mul_f32_e32 v145, v26, v145
	v_mul_f32_e32 v146, v26, v146
	v_mul_f32_e32 v147, v26, v147
	ds_write_b128 v209, v[144:147]
	v_mul_f32_e32 v148, v27, v148
	v_mul_f32_e32 v149, v27, v149
	v_mul_f32_e32 v150, v27, v150
	v_mul_f32_e32 v151, v27, v151
	ds_write_b128 v209, v[148:151] offset:1024
	v_mul_f32_e32 v152, v28, v152
	v_mul_f32_e32 v153, v28, v153
	v_mul_f32_e32 v154, v28, v154
	v_mul_f32_e32 v155, v28, v155
	ds_write_b128 v209, v[152:155] offset:2048
	v_mul_f32_e32 v156, v29, v156
	v_mul_f32_e32 v157, v29, v157
	v_mul_f32_e32 v158, v29, v158
	v_mul_f32_e32 v159, v29, v159
	ds_write_b128 v209, v[156:159] offset:3072
	v_mul_f32_e32 v160, v30, v160
	v_mul_f32_e32 v161, v30, v161
	v_mul_f32_e32 v162, v30, v162
	v_mul_f32_e32 v163, v30, v163
	ds_write_b128 v209, v[160:163] offset:4096
	v_mul_f32_e32 v164, v31, v164
	v_mul_f32_e32 v165, v31, v165
	v_mul_f32_e32 v166, v31, v166
	v_mul_f32_e32 v167, v31, v167
	ds_write_b128 v209, v[164:167] offset:5120
	v_mul_f32_e32 v168, v32, v168
	v_mul_f32_e32 v169, v32, v169
	v_mul_f32_e32 v170, v32, v170
	v_mul_f32_e32 v171, v32, v171
	ds_write_b128 v209, v[168:171] offset:6144
	v_mul_f32_e32 v172, v33, v172
	v_mul_f32_e32 v173, v33, v173
	v_mul_f32_e32 v174, v33, v174
	v_mul_f32_e32 v175, v33, v175
	ds_write_b128 v209, v[172:175] offset:7168
	s_waitcnt lgkmcnt(0)
	s_barrier
; #define GAS __attribute__((address_space(1)))
; #define LAS __attribute__((address_space(3)))
; #define LDS_WAIT() asm volatile("s_waitcnt lgkmcnt(0)" ::: "memory")
;     const int pr = item >> 1, kb = 2 * (pr / nblk) + (item & 1), nb = pr % nblk, k0 = 64 * kb, n0 = 32 * nb;
;     const int nr = n0 + (lane & 31); const int sc = MAP == 1 ? src_col_in(nr) : nr;
;     float v[32];
; #pragma unroll
;     for (int i = 0; i < 32; ++i) v[i] = sc >= 0 ? W[(size_t)(k0 + 2 * i + (lane >> 5)) * Nsrc + sc] : 0.f;
; #pragma unroll
;     for (int i = 0; i < 32; ++i) { const int k = k0 + 2 * i + (lane >> 5); float x = v[i] * wscale; if (KS) x *= (k < ksplit ? ksA[k] : ksB[k - ksplit]); scr[(2 * i + (lane >> 5)) * 33 + (lane & 31)] = x; }
;     LDS_WAIT(); asm volatile("" ::: "memory");
;     const int c = lane & 7;
; #pragma unroll
;     for (int j = 0; j < 4; ++j) { const int n = (lane >> 3) + 8 * j; const LAS float* s = scr + (8 * c) * 33 + n;
;         const unsigned long long o = (unsigned long long)pg8::pk4_fp8(s[0 * 33], s[1 * 33], s[2 * 33], s[3 * 33]) | ((unsigned long long)pg8::pk4_fp8(s[4 * 33], s[5 * 33], s[6 * 33], s[7 * 33]) << 32);
;         *(GAS unsigned long long*)(WT + (size_t)(n0 + n) * K + k0 + 8 * c) = o; }
;     LDS_WAIT(); asm volatile("" ::: "memory");
	s_add_u32 s8, s30, 0xa000
	s_addc_u32 s9, s31, 0
	global_load_dwordx4 v[144:147], v74, s[8:9]
	s_add_u32 s8, s8, 0x20000
	s_addc_u32 s9, s9, 0
	global_load_dwordx4 v[148:151], v74, s[8:9]
	s_add_u32 s8, s8, 0x20000
	s_addc_u32 s9, s9, 0
	global_load_dwordx4 v[152:155], v74, s[8:9]
	s_add_u32 s8, s8, 0x20000
	s_addc_u32 s9, s9, 0
	global_load_dwordx4 v[156:159], v74, s[8:9]
	s_add_u32 s8, s8, 0x20000
	s_addc_u32 s9, s9, 0
	global_load_dwordx4 v[160:163], v74, s[8:9]
	s_add_u32 s8, s8, 0x20000
	s_addc_u32 s9, s9, 0
	global_load_dwordx4 v[164:167], v74, s[8:9]
	s_add_u32 s8, s8, 0x20000
	s_addc_u32 s9, s9, 0
	global_load_dwordx4 v[168:171], v74, s[8:9]
	s_add_u32 s8, s8, 0x20000
	s_addc_u32 s9, s9, 0
	global_load_dwordx4 v[172:175], v74, s[8:9]
	s_add_u32 s6, s32, 0x2000000
	s_addc_u32 s7, s33, 0
	ds_read_b32 v226, v211
	ds_read_b32 v227, v211 offset:512
	ds_read_b32 v228, v211 offset:1024
	ds_read_b32 v229, v211 offset:1536
	ds_read_b32 v230, v211 offset:2048
	ds_read_b32 v231, v211 offset:2560
	ds_read_b32 v232, v211 offset:3072
	ds_read_b32 v233, v211 offset:3584
	ds_read_b32 v234, v211 offset:4096
	ds_read_b32 v235, v211 offset:4608
	ds_read_b32 v236, v211 offset:5120
	ds_read_b32 v237, v211 offset:5632
	ds_read_b32 v238, v211 offset:6144
	ds_read_b32 v239, v211 offset:6656
	ds_read_b32 v240, v211 offset:7168
	ds_read_b32 v241, v211 offset:7680
	s_waitcnt lgkmcnt(0)
	v_max_f32_e32 v226, v226, v226
	v_max_f32_e32 v227, v227, v227
	v_max_f32_e32 v228, v228, v228
	v_max_f32_e32 v229, v229, v229
	v_max_f32_e32 v230, v230, v230
	v_max_f32_e32 v231, v231, v231
	v_max_f32_e32 v232, v232, v232
	v_max_f32_e32 v233, v233, v233
	v_max_f32_e32 v234, v234, v234
	v_max_f32_e32 v235, v235, v235
	v_max_f32_e32 v236, v236, v236
	v_max_f32_e32 v237, v237, v237
	v_max_f32_e32 v238, v238, v238
	v_max_f32_e32 v239, v239, v239
	v_max_f32_e32 v240, v240, v240
	v_max_f32_e32 v241, v241, v241
	v_med3_f32 v226, v226, s62, v95
	v_med3_f32 v227, v227, s62, v95
	v_med3_f32 v228, v228, s62, v95
	v_med3_f32 v229, v229, s62, v95
	v_med3_f32 v230, v230, s62, v95
	v_med3_f32 v231, v231, s62, v95
	v_med3_f32 v232, v232, s62, v95
	v_med3_f32 v233, v233, s62, v95
	v_med3_f32 v234, v234, s62, v95
	v_med3_f32 v235, v235, s62, v95
	v_med3_f32 v236, v236, s62, v95
	v_med3_f32 v237, v237, s62, v95
	v_med3_f32 v238, v238, s62, v95
	v_med3_f32 v239, v239, s62, v95
	v_med3_f32 v240, v240, s62, v95
	v_med3_f32 v241, v241, s62, v95
	v_mov_b32_e32 v242, 0
	v_mov_b32_e32 v243, 0
	v_mov_b32_e32 v244, 0
	v_mov_b32_e32 v245, 0
	v_cvt_pk_fp8_f32 v242, v226, v227
	v_cvt_pk_fp8_f32 v243, v230, v231
	v_cvt_pk_fp8_f32 v244, v234, v235
	v_cvt_pk_fp8_f32 v245, v238, v239
	v_cvt_pk_fp8_f32 v242, v228, v229 op_sel:[0,0,1]
	v_cvt_pk_fp8_f32 v243, v232, v233 op_sel:[0,0,1]
	v_cvt_pk_fp8_f32 v244, v236, v237 op_sel:[0,0,1]
	v_cvt_pk_fp8_f32 v245, v240, v241 op_sel:[0,0,1]
	s_nop 0
	global_store_dwordx4 v77, v[242:245], s[6:7]
	ds_read_b32 v226, v213
	ds_read_b32 v227, v213 offset:512
	ds_read_b32 v228, v213 offset:1024
	ds_read_b32 v229, v213 offset:1536
	ds_read_b32 v230, v213 offset:2048
	ds_read_b32 v231, v213 offset:2560
	ds_read_b32 v232, v213 offset:3072
	ds_read_b32 v233, v213 offset:3584
	ds_read_b32 v234, v213 offset:4096
	ds_read_b32 v235, v213 offset:4608
	ds_read_b32 v236, v213 offset:5120
	ds_read_b32 v237, v213 offset:5632
	ds_read_b32 v238, v213 offset:6144
	ds_read_b32 v239, v213 offset:6656
	ds_read_b32 v240, v213 offset:7168
	ds_read_b32 v241, v213 offset:7680
	s_waitcnt lgkmcnt(0)
	v_max_f32_e32 v226, v226, v226
	v_max_f32_e32 v227, v227, v227
	v_max_f32_e32 v228, v228, v228
	v_max_f32_e32 v229, v229, v229
	v_max_f32_e32 v230, v230, v230
	v_max_f32_e32 v231, v231, v231
	v_max_f32_e32 v232, v232, v232
	v_max_f32_e32 v233, v233, v233
	v_max_f32_e32 v234, v234, v234
	v_max_f32_e32 v235, v235, v235
	v_max_f32_e32 v236, v236, v236
	v_max_f32_e32 v237, v237, v237
	v_max_f32_e32 v238, v238, v238
	v_max_f32_e32 v239, v239, v239
	v_max_f32_e32 v240, v240, v240
	v_max_f32_e32 v241, v241, v241
	v_med3_f32 v226, v226, s62, v95
	v_med3_f32 v227, v227, s62, v95
	v_med3_f32 v228, v228, s62, v95
	v_med3_f32 v229, v229, s62, v95
	v_med3_f32 v230, v230, s62, v95
	v_med3_f32 v231, v231, s62, v95
	v_med3_f32 v232, v232, s62, v95
	v_med3_f32 v233, v233, s62, v95
	v_med3_f32 v234, v234, s62, v95
	v_med3_f32 v235, v235, s62, v95
	v_med3_f32 v236, v236, s62, v95
	v_med3_f32 v237, v237, s62, v95
	v_med3_f32 v238, v238, s62, v95
	v_med3_f32 v239, v239, s62, v95
	v_med3_f32 v240, v240, s62, v95
	v_med3_f32 v241, v241, s62, v95
	v_mov_b32_e32 v242, 0
	v_mov_b32_e32 v243, 0
	v_mov_b32_e32 v244, 0
	v_mov_b32_e32 v245, 0
	v_cvt_pk_fp8_f32 v242, v226, v227
	v_cvt_pk_fp8_f32 v243, v230, v231
	v_cvt_pk_fp8_f32 v244, v234, v235
	v_cvt_pk_fp8_f32 v245, v238, v239
	v_cvt_pk_fp8_f32 v242, v228, v229 op_sel:[0,0,1]
	v_cvt_pk_fp8_f32 v243, v232, v233 op_sel:[0,0,1]
	v_cvt_pk_fp8_f32 v244, v236, v237 op_sel:[0,0,1]
	v_cvt_pk_fp8_f32 v245, v240, v241 op_sel:[0,0,1]
	s_nop 0
	global_store_dwordx4 v78, v[242:245], s[6:7]
	s_waitcnt vmcnt(12)
	v_mul_f32_e32 v176, v26, v176
	v_mul_f32_e32 v177, v26, v177
	v_mul_f32_e32 v178, v26, v178
	v_mul_f32_e32 v179, v26, v179
	ds_write_b128 v210, v[176:179]
	v_mul_f32_e32 v180, v27, v180
	v_mul_f32_e32 v181, v27, v181
	v_mul_f32_e32 v182, v27, v182
	v_mul_f32_e32 v183, v27, v183
	ds_write_b128 v210, v[180:183] offset:1024
	v_mul_f32_e32 v184, v28, v184
	v_mul_f32_e32 v185, v28, v185
	v_mul_f32_e32 v186, v28, v186
	v_mul_f32_e32 v187, v28, v187
	ds_write_b128 v210, v[184:187] offset:2048
	v_mul_f32_e32 v188, v29, v188
	v_mul_f32_e32 v189, v29, v189
	v_mul_f32_e32 v190, v29, v190
	v_mul_f32_e32 v191, v29, v191
	ds_write_b128 v210, v[188:191] offset:3072
	v_mul_f32_e32 v192, v30, v192
	v_mul_f32_e32 v193, v30, v193
	v_mul_f32_e32 v194, v30, v194
	v_mul_f32_e32 v195, v30, v195
	ds_write_b128 v210, v[192:195] offset:4096
	v_mul_f32_e32 v196, v31, v196
	v_mul_f32_e32 v197, v31, v197
	v_mul_f32_e32 v198, v31, v198
	v_mul_f32_e32 v199, v31, v199
	ds_write_b128 v210, v[196:199] offset:5120
	v_mul_f32_e32 v200, v32, v200
	v_mul_f32_e32 v201, v32, v201
	v_mul_f32_e32 v202, v32, v202
	v_mul_f32_e32 v203, v32, v203
	ds_write_b128 v210, v[200:203] offset:6144
	v_mul_f32_e32 v204, v33, v204
	v_mul_f32_e32 v205, v33, v205
	v_mul_f32_e32 v206, v33, v206
	v_mul_f32_e32 v207, v33, v207
	ds_write_b128 v210, v[204:207] offset:7168
	s_waitcnt lgkmcnt(0)
	s_barrier
; #define GAS __attribute__((address_space(1)))
; #define LAS __attribute__((address_space(3)))
; #define LDS_WAIT() asm volatile("s_waitcnt lgkmcnt(0)" ::: "memory")
; __device__ __forceinline__ unsigned pk4_fp8(float a, float b, float c, float d) {
;     a = fminf(fmaxf(a, -448.f), 448.f); b = fminf(fmaxf(b, -448.f), 448.f); c = fminf(fmaxf(c, -448.f), 448.f); d = fminf(fmaxf(d, -448.f), 448.f);
;     int w = __builtin_amdgcn_cvt_pk_fp8_f32(a, b, 0, false); w = __builtin_amdgcn_cvt_pk_fp8_f32(c, d, w, true); return (unsigned)w; }
;     const int pr = item >> 1, kb = 2 * (pr / nblk) + (item & 1), nb = pr % nblk, k0 = 64 * kb, n0 = 32 * nb;
;     const int nr = n0 + (lane & 31); const int sc = MAP == 1 ? src_col_in(nr) : nr;
;     float v[32];
; #pragma unroll
;     for (int i = 0; i < 32; ++i) v[i] = sc >= 0 ? W[(size_t)(k0 + 2 * i + (lane >> 5)) * Nsrc + sc] : 0.f;
; #pragma unroll
;     for (int i = 0; i < 32; ++i) { const int k = k0 + 2 * i + (lane >> 5); float x = v[i] * wscale; if (KS) x *= (k < ksplit ? ksA[k] : ksB[k - ksplit]); scr[(2 * i + (lane >> 5)) * 33 + (lane & 31)] = x; }
;     LDS_WAIT(); asm volatile("" ::: "memory");
;     const int c = lane & 7;
; #pragma unroll
;     for (int j = 0; j < 4; ++j) { const int n = (lane >> 3) + 8 * j; const LAS float* s = scr + (8 * c) * 33 + n;
;         const unsigned long long o = (unsigned long long)pg8::pk4_fp8(s[0 * 33], s[1 * 33], s[2 * 33], s[3 * 33]) | ((unsigned long long)pg8::pk4_fp8(s[4 * 33], s[5 * 33], s[6 * 33], s[7 * 33]) << 32);
;         *(GAS unsigned long long*)(WT + (size_t)(n0 + n) * K + k0 + 8 * c) = o; }
;     LDS_WAIT(); asm volatile("" ::: "memory");
; }
	s_add_u32 s8, s30, 0xb000
	s_addc_u32 s9, s31, 0
	global_load_dwordx4 v[176:179], v74, s[8:9]
	s_add_u32 s8, s8, 0x20000
	s_addc_u32 s9, s9, 0
	global_load_dwordx4 v[180:183], v74, s[8:9]
	s_add_u32 s8, s8, 0x20000
	s_addc_u32 s9, s9, 0
	global_load_dwordx4 v[184:187], v74, s[8:9]
	s_add_u32 s8, s8, 0x20000
	s_addc_u32 s9, s9, 0
	global_load_dwordx4 v[188:191], v74, s[8:9]
	s_add_u32 s8, s8, 0x20000
	s_addc_u32 s9, s9, 0
	global_load_dwordx4 v[192:195], v74, s[8:9]
	s_add_u32 s8, s8, 0x20000
	s_addc_u32 s9, s9, 0
	global_load_dwordx4 v[196:199], v74, s[8:9]
	s_add_u32 s8, s8, 0x20000
	s_addc_u32 s9, s9, 0
	global_load_dwordx4 v[200:203], v74, s[8:9]
	s_add_u32 s8, s8, 0x20000
	s_addc_u32 s9, s9, 0
	global_load_dwordx4 v[204:207], v74, s[8:9]
	s_add_u32 s6, s32, 0x2400000
	s_addc_u32 s7, s33, 0
	ds_read_b32 v226, v212
	ds_read_b32 v227, v212 offset:512
	ds_read_b32 v228, v212 offset:1024
	ds_read_b32 v229, v212 offset:1536
	ds_read_b32 v230, v212 offset:2048
	ds_read_b32 v231, v212 offset:2560
	ds_read_b32 v232, v212 offset:3072
	ds_read_b32 v233, v212 offset:3584
	ds_read_b32 v234, v212 offset:4096
	ds_read_b32 v235, v212 offset:4608
	ds_read_b32 v236, v212 offset:5120
	ds_read_b32 v237, v212 offset:5632
	ds_read_b32 v238, v212 offset:6144
	ds_read_b32 v239, v212 offset:6656
	ds_read_b32 v240, v212 offset:7168
	ds_read_b32 v241, v212 offset:7680
	s_waitcnt lgkmcnt(0)
	v_max_f32_e32 v226, v226, v226
	v_max_f32_e32 v227, v227, v227
	v_max_f32_e32 v228, v228, v228
	v_max_f32_e32 v229, v229, v229
	v_max_f32_e32 v230, v230, v230
	v_max_f32_e32 v231, v231, v231
	v_max_f32_e32 v232, v232, v232
	v_max_f32_e32 v233, v233, v233
	v_max_f32_e32 v234, v234, v234
	v_max_f32_e32 v235, v235, v235
	v_max_f32_e32 v236, v236, v236
	v_max_f32_e32 v237, v237, v237
	v_max_f32_e32 v238, v238, v238
	v_max_f32_e32 v239, v239, v239
	v_max_f32_e32 v240, v240, v240
	v_max_f32_e32 v241, v241, v241
	v_med3_f32 v226, v226, s62, v95
	v_med3_f32 v227, v227, s62, v95
	v_med3_f32 v228, v228, s62, v95
	v_med3_f32 v229, v229, s62, v95
	v_med3_f32 v230, v230, s62, v95
	v_med3_f32 v231, v231, s62, v95
	v_med3_f32 v232, v232, s62, v95
	v_med3_f32 v233, v233, s62, v95
	v_med3_f32 v234, v234, s62, v95
	v_med3_f32 v235, v235, s62, v95
	v_med3_f32 v236, v236, s62, v95
	v_med3_f32 v237, v237, s62, v95
	v_med3_f32 v238, v238, s62, v95
	v_med3_f32 v239, v239, s62, v95
	v_med3_f32 v240, v240, s62, v95
	v_med3_f32 v241, v241, s62, v95
	v_mov_b32_e32 v242, 0
	v_mov_b32_e32 v243, 0
	v_mov_b32_e32 v244, 0
	v_mov_b32_e32 v245, 0
	v_cvt_pk_fp8_f32 v242, v226, v227
	v_cvt_pk_fp8_f32 v243, v230, v231
	v_cvt_pk_fp8_f32 v244, v234, v235
	v_cvt_pk_fp8_f32 v245, v238, v239
	v_cvt_pk_fp8_f32 v242, v228, v229 op_sel:[0,0,1]
	v_cvt_pk_fp8_f32 v243, v232, v233 op_sel:[0,0,1]
	v_cvt_pk_fp8_f32 v244, v236, v237 op_sel:[0,0,1]
	v_cvt_pk_fp8_f32 v245, v240, v241 op_sel:[0,0,1]
	s_nop 0
	global_store_dwordx4 v77, v[242:245], s[6:7]
	ds_read_b32 v226, v214
	ds_read_b32 v227, v214 offset:512
	ds_read_b32 v228, v214 offset:1024
	ds_read_b32 v229, v214 offset:1536
	ds_read_b32 v230, v214 offset:2048
	ds_read_b32 v231, v214 offset:2560
	ds_read_b32 v232, v214 offset:3072
	ds_read_b32 v233, v214 offset:3584
	ds_read_b32 v234, v214 offset:4096
	ds_read_b32 v235, v214 offset:4608
	ds_read_b32 v236, v214 offset:5120
	ds_read_b32 v237, v214 offset:5632
	ds_read_b32 v238, v214 offset:6144
	ds_read_b32 v239, v214 offset:6656
	ds_read_b32 v240, v214 offset:7168
	ds_read_b32 v241, v214 offset:7680
	s_waitcnt lgkmcnt(0)
	v_max_f32_e32 v226, v226, v226
	v_max_f32_e32 v227, v227, v227
	v_max_f32_e32 v228, v228, v228
	v_max_f32_e32 v229, v229, v229
	v_max_f32_e32 v230, v230, v230
	v_max_f32_e32 v231, v231, v231
	v_max_f32_e32 v232, v232, v232
	v_max_f32_e32 v233, v233, v233
	v_max_f32_e32 v234, v234, v234
	v_max_f32_e32 v235, v235, v235
	v_max_f32_e32 v236, v236, v236
	v_max_f32_e32 v237, v237, v237
	v_max_f32_e32 v238, v238, v238
	v_max_f32_e32 v239, v239, v239
	v_max_f32_e32 v240, v240, v240
	v_max_f32_e32 v241, v241, v241
	v_med3_f32 v226, v226, s62, v95
	v_med3_f32 v227, v227, s62, v95
	v_med3_f32 v228, v228, s62, v95
	v_med3_f32 v229, v229, s62, v95
	v_med3_f32 v230, v230, s62, v95
	v_med3_f32 v231, v231, s62, v95
	v_med3_f32 v232, v232, s62, v95
	v_med3_f32 v233, v233, s62, v95
	v_med3_f32 v234, v234, s62, v95
	v_med3_f32 v235, v235, s62, v95
	v_med3_f32 v236, v236, s62, v95
	v_med3_f32 v237, v237, s62, v95
	v_med3_f32 v238, v238, s62, v95
	v_med3_f32 v239, v239, s62, v95
	v_med3_f32 v240, v240, s62, v95
	v_med3_f32 v241, v241, s62, v95
	v_mov_b32_e32 v242, 0
	v_mov_b32_e32 v243, 0
	v_mov_b32_e32 v244, 0
	v_mov_b32_e32 v245, 0
	v_cvt_pk_fp8_f32 v242, v226, v227
	v_cvt_pk_fp8_f32 v243, v230, v231
	v_cvt_pk_fp8_f32 v244, v234, v235
	v_cvt_pk_fp8_f32 v245, v238, v239
	v_cvt_pk_fp8_f32 v242, v228, v229 op_sel:[0,0,1]
	v_cvt_pk_fp8_f32 v243, v232, v233 op_sel:[0,0,1]
	v_cvt_pk_fp8_f32 v244, v236, v237 op_sel:[0,0,1]
	v_cvt_pk_fp8_f32 v245, v240, v241 op_sel:[0,0,1]
	s_nop 0
	global_store_dwordx4 v78, v[242:245], s[6:7]
	s_waitcnt vmcnt(12)
	v_mul_f32_e32 v144, v26, v144
	v_mul_f32_e32 v145, v26, v145
	v_mul_f32_e32 v146, v26, v146
	v_mul_f32_e32 v147, v26, v147
	ds_write_b128 v209, v[144:147]
	v_mul_f32_e32 v148, v27, v148
	v_mul_f32_e32 v149, v27, v149
	v_mul_f32_e32 v150, v27, v150
	v_mul_f32_e32 v151, v27, v151
	ds_write_b128 v209, v[148:151] offset:1024
	v_mul_f32_e32 v152, v28, v152
	v_mul_f32_e32 v153, v28, v153
	v_mul_f32_e32 v154, v28, v154
	v_mul_f32_e32 v155, v28, v155
	ds_write_b128 v209, v[152:155] offset:2048
	v_mul_f32_e32 v156, v29, v156
	v_mul_f32_e32 v157, v29, v157
	v_mul_f32_e32 v158, v29, v158
	v_mul_f32_e32 v159, v29, v159
	ds_write_b128 v209, v[156:159] offset:3072
	v_mul_f32_e32 v160, v30, v160
	v_mul_f32_e32 v161, v30, v161
	v_mul_f32_e32 v162, v30, v162
	v_mul_f32_e32 v163, v30, v163
	ds_write_b128 v209, v[160:163] offset:4096
	v_mul_f32_e32 v164, v31, v164
	v_mul_f32_e32 v165, v31, v165
	v_mul_f32_e32 v166, v31, v166
	v_mul_f32_e32 v167, v31, v167
	ds_write_b128 v209, v[164:167] offset:5120
	v_mul_f32_e32 v168, v32, v168
	v_mul_f32_e32 v169, v32, v169
	v_mul_f32_e32 v170, v32, v170
	v_mul_f32_e32 v171, v32, v171
	ds_write_b128 v209, v[168:171] offset:6144
	v_mul_f32_e32 v172, v33, v172
	v_mul_f32_e32 v173, v33, v173
	v_mul_f32_e32 v174, v33, v174
	v_mul_f32_e32 v175, v33, v175
	ds_write_b128 v209, v[172:175] offset:7168
	s_waitcnt lgkmcnt(0)
	s_barrier
; #define GAS __attribute__((address_space(1)))
; #define LAS __attribute__((address_space(3)))
; #define LDS_WAIT() asm volatile("s_waitcnt lgkmcnt(0)" ::: "memory")
; __device__ __forceinline__ unsigned pk4_fp8(float a, float b, float c, float d) {
;     a = fminf(fmaxf(a, -448.f), 448.f); b = fminf(fmaxf(b, -448.f), 448.f); c = fminf(fmaxf(c, -448.f), 448.f); d = fminf(fmaxf(d, -448.f), 448.f);
;     int w = __builtin_amdgcn_cvt_pk_fp8_f32(a, b, 0, false); w = __builtin_amdgcn_cvt_pk_fp8_f32(c, d, w, true); return (unsigned)w; }
;     const int pr = item >> 1, kb = 2 * (pr / nblk) + (item & 1), nb = pr % nblk, k0 = 64 * kb, n0 = 32 * nb;
;     const int nr = n0 + (lane & 31); const int sc = MAP == 1 ? src_col_in(nr) : nr;
;     float v[32];
; #pragma unroll
;     for (int i = 0; i < 32; ++i) v[i] = sc >= 0 ? W[(size_t)(k0 + 2 * i + (lane >> 5)) * Nsrc + sc] : 0.f;
; #pragma unroll
;     for (int i = 0; i < 32; ++i) { const int k = k0 + 2 * i + (lane >> 5); float x = v[i] * wscale; if (KS) x *= (k < ksplit ? ksA[k] : ksB[k - ksplit]); scr[(2 * i + (lane >> 5)) * 33 + (lane & 31)] = x; }
;     LDS_WAIT(); asm volatile("" ::: "memory");
;     const int c = lane & 7;
; #pragma unroll
;     for (int j = 0; j < 4; ++j) { const int n = (lane >> 3) + 8 * j; const LAS float* s = scr + (8 * c) * 33 + n;
;         const unsigned long long o = (unsigned long long)pg8::pk4_fp8(s[0 * 33], s[1 * 33], s[2 * 33], s[3 * 33]) | ((unsigned long long)pg8::pk4_fp8(s[4 * 33], s[5 * 33], s[6 * 33], s[7 * 33]) << 32);
;         *(GAS unsigned long long*)(WT + (size_t)(n0 + n) * K + k0 + 8 * c) = o; }
;     LDS_WAIT(); asm volatile("" ::: "memory");
; }
	s_add_u32 s8, s30, 0xc000
	s_addc_u32 s9, s31, 0
	global_load_dwordx4 v[144:147], v74, s[8:9]
	s_add_u32 s8, s8, 0x20000
	s_addc_u32 s9, s9, 0
	global_load_dwordx4 v[148:151], v74, s[8:9]
	s_add_u32 s8, s8, 0x20000
	s_addc_u32 s9, s9, 0
	global_load_dwordx4 v[152:155], v74, s[8:9]
	s_add_u32 s8, s8, 0x20000
	s_addc_u32 s9, s9, 0
	global_load_dwordx4 v[156:159], v74, s[8:9]
	s_add_u32 s8, s8, 0x20000
	s_addc_u32 s9, s9, 0
	global_load_dwordx4 v[160:163], v74, s[8:9]
	s_add_u32 s8, s8, 0x20000
	s_addc_u32 s9, s9, 0
	global_load_dwordx4 v[164:167], v74, s[8:9]
	s_add_u32 s8, s8, 0x20000
	s_addc_u32 s9, s9, 0
	global_load_dwordx4 v[168:171], v74, s[8:9]
	s_add_u32 s8, s8, 0x20000
	s_addc_u32 s9, s9, 0
	global_load_dwordx4 v[172:175], v74, s[8:9]
	s_add_u32 s6, s32, 0x2800000
	s_addc_u32 s7, s33, 0
	ds_read_b32 v226, v211
	ds_read_b32 v227, v211 offset:512
	ds_read_b32 v228, v211 offset:1024
	ds_read_b32 v229, v211 offset:1536
	ds_read_b32 v230, v211 offset:2048
	ds_read_b32 v231, v211 offset:2560
	ds_read_b32 v232, v211 offset:3072
	ds_read_b32 v233, v211 offset:3584
	ds_read_b32 v234, v211 offset:4096
	ds_read_b32 v235, v211 offset:4608
	ds_read_b32 v236, v211 offset:5120
	ds_read_b32 v237, v211 offset:5632
	ds_read_b32 v238, v211 offset:6144
	ds_read_b32 v239, v211 offset:6656
	ds_read_b32 v240, v211 offset:7168
	ds_read_b32 v241, v211 offset:7680
	s_waitcnt lgkmcnt(0)
	v_max_f32_e32 v226, v226, v226
	v_max_f32_e32 v227, v227, v227
	v_max_f32_e32 v228, v228, v228
	v_max_f32_e32 v229, v229, v229
	v_max_f32_e32 v230, v230, v230
	v_max_f32_e32 v231, v231, v231
	v_max_f32_e32 v232, v232, v232
	v_max_f32_e32 v233, v233, v233
	v_max_f32_e32 v234, v234, v234
	v_max_f32_e32 v235, v235, v235
	v_max_f32_e32 v236, v236, v236
	v_max_f32_e32 v237, v237, v237
	v_max_f32_e32 v238, v238, v238
	v_max_f32_e32 v239, v239, v239
	v_max_f32_e32 v240, v240, v240
	v_max_f32_e32 v241, v241, v241
	v_med3_f32 v226, v226, s62, v95
	v_med3_f32 v227, v227, s62, v95
	v_med3_f32 v228, v228, s62, v95
	v_med3_f32 v229, v229, s62, v95
	v_med3_f32 v230, v230, s62, v95
	v_med3_f32 v231, v231, s62, v95
	v_med3_f32 v232, v232, s62, v95
	v_med3_f32 v233, v233, s62, v95
	v_med3_f32 v234, v234, s62, v95
	v_med3_f32 v235, v235, s62, v95
	v_med3_f32 v236, v236, s62, v95
	v_med3_f32 v237, v237, s62, v95
	v_med3_f32 v238, v238, s62, v95
	v_med3_f32 v239, v239, s62, v95
	v_med3_f32 v240, v240, s62, v95
	v_med3_f32 v241, v241, s62, v95
	v_mov_b32_e32 v242, 0
	v_mov_b32_e32 v243, 0
	v_mov_b32_e32 v244, 0
	v_mov_b32_e32 v245, 0
	v_cvt_pk_fp8_f32 v242, v226, v227
	v_cvt_pk_fp8_f32 v243, v230, v231
	v_cvt_pk_fp8_f32 v244, v234, v235
	v_cvt_pk_fp8_f32 v245, v238, v239
	v_cvt_pk_fp8_f32 v242, v228, v229 op_sel:[0,0,1]
	v_cvt_pk_fp8_f32 v243, v232, v233 op_sel:[0,0,1]
	v_cvt_pk_fp8_f32 v244, v236, v237 op_sel:[0,0,1]
	v_cvt_pk_fp8_f32 v245, v240, v241 op_sel:[0,0,1]
	s_nop 0
	global_store_dwordx4 v77, v[242:245], s[6:7]
	ds_read_b32 v226, v213
	ds_read_b32 v227, v213 offset:512
	ds_read_b32 v228, v213 offset:1024
	ds_read_b32 v229, v213 offset:1536
	ds_read_b32 v230, v213 offset:2048
	ds_read_b32 v231, v213 offset:2560
	ds_read_b32 v232, v213 offset:3072
	ds_read_b32 v233, v213 offset:3584
	ds_read_b32 v234, v213 offset:4096
	ds_read_b32 v235, v213 offset:4608
	ds_read_b32 v236, v213 offset:5120
	ds_read_b32 v237, v213 offset:5632
	ds_read_b32 v238, v213 offset:6144
	ds_read_b32 v239, v213 offset:6656
	ds_read_b32 v240, v213 offset:7168
	ds_read_b32 v241, v213 offset:7680
	s_waitcnt lgkmcnt(0)
	v_max_f32_e32 v226, v226, v226
	v_max_f32_e32 v227, v227, v227
	v_max_f32_e32 v228, v228, v228
	v_max_f32_e32 v229, v229, v229
	v_max_f32_e32 v230, v230, v230
	v_max_f32_e32 v231, v231, v231
	v_max_f32_e32 v232, v232, v232
	v_max_f32_e32 v233, v233, v233
	v_max_f32_e32 v234, v234, v234
	v_max_f32_e32 v235, v235, v235
	v_max_f32_e32 v236, v236, v236
	v_max_f32_e32 v237, v237, v237
	v_max_f32_e32 v238, v238, v238
	v_max_f32_e32 v239, v239, v239
	v_max_f32_e32 v240, v240, v240
	v_max_f32_e32 v241, v241, v241
	v_med3_f32 v226, v226, s62, v95
	v_med3_f32 v227, v227, s62, v95
	v_med3_f32 v228, v228, s62, v95
	v_med3_f32 v229, v229, s62, v95
	v_med3_f32 v230, v230, s62, v95
	v_med3_f32 v231, v231, s62, v95
	v_med3_f32 v232, v232, s62, v95
	v_med3_f32 v233, v233, s62, v95
	v_med3_f32 v234, v234, s62, v95
	v_med3_f32 v235, v235, s62, v95
	v_med3_f32 v236, v236, s62, v95
	v_med3_f32 v237, v237, s62, v95
	v_med3_f32 v238, v238, s62, v95
	v_med3_f32 v239, v239, s62, v95
	v_med3_f32 v240, v240, s62, v95
	v_med3_f32 v241, v241, s62, v95
	v_mov_b32_e32 v242, 0
	v_mov_b32_e32 v243, 0
	v_mov_b32_e32 v244, 0
	v_mov_b32_e32 v245, 0
	v_cvt_pk_fp8_f32 v242, v226, v227
	v_cvt_pk_fp8_f32 v243, v230, v231
	v_cvt_pk_fp8_f32 v244, v234, v235
	v_cvt_pk_fp8_f32 v245, v238, v239
	v_cvt_pk_fp8_f32 v242, v228, v229 op_sel:[0,0,1]
	v_cvt_pk_fp8_f32 v243, v232, v233 op_sel:[0,0,1]
	v_cvt_pk_fp8_f32 v244, v236, v237 op_sel:[0,0,1]
	v_cvt_pk_fp8_f32 v245, v240, v241 op_sel:[0,0,1]
	s_nop 0
	global_store_dwordx4 v78, v[242:245], s[6:7]
	s_waitcnt vmcnt(12)
	v_mul_f32_e32 v176, v26, v176
	v_mul_f32_e32 v177, v26, v177
	v_mul_f32_e32 v178, v26, v178
	v_mul_f32_e32 v179, v26, v179
	ds_write_b128 v210, v[176:179]
	v_mul_f32_e32 v180, v27, v180
	v_mul_f32_e32 v181, v27, v181
	v_mul_f32_e32 v182, v27, v182
	v_mul_f32_e32 v183, v27, v183
	ds_write_b128 v210, v[180:183] offset:1024
	v_mul_f32_e32 v184, v28, v184
	v_mul_f32_e32 v185, v28, v185
	v_mul_f32_e32 v186, v28, v186
	v_mul_f32_e32 v187, v28, v187
	ds_write_b128 v210, v[184:187] offset:2048
	v_mul_f32_e32 v188, v29, v188
	v_mul_f32_e32 v189, v29, v189
	v_mul_f32_e32 v190, v29, v190
	v_mul_f32_e32 v191, v29, v191
	ds_write_b128 v210, v[188:191] offset:3072
	v_mul_f32_e32 v192, v30, v192
	v_mul_f32_e32 v193, v30, v193
	v_mul_f32_e32 v194, v30, v194
	v_mul_f32_e32 v195, v30, v195
	ds_write_b128 v210, v[192:195] offset:4096
	v_mul_f32_e32 v196, v31, v196
	v_mul_f32_e32 v197, v31, v197
	v_mul_f32_e32 v198, v31, v198
	v_mul_f32_e32 v199, v31, v199
	ds_write_b128 v210, v[196:199] offset:5120
	v_mul_f32_e32 v200, v32, v200
	v_mul_f32_e32 v201, v32, v201
	v_mul_f32_e32 v202, v32, v202
	v_mul_f32_e32 v203, v32, v203
	ds_write_b128 v210, v[200:203] offset:6144
	v_mul_f32_e32 v204, v33, v204
	v_mul_f32_e32 v205, v33, v205
	v_mul_f32_e32 v206, v33, v206
	v_mul_f32_e32 v207, v33, v207
	ds_write_b128 v210, v[204:207] offset:7168
	s_waitcnt lgkmcnt(0)
	s_barrier
; #define GAS __attribute__((address_space(1)))
; #define LAS __attribute__((address_space(3)))
; #define LDS_WAIT() asm volatile("s_waitcnt lgkmcnt(0)" ::: "memory")
; __device__ __forceinline__ unsigned pk4_fp8(float a, float b, float c, float d) {
;     a = fminf(fmaxf(a, -448.f), 448.f); b = fminf(fmaxf(b, -448.f), 448.f); c = fminf(fmaxf(c, -448.f), 448.f); d = fminf(fmaxf(d, -448.f), 448.f);
;     int w = __builtin_amdgcn_cvt_pk_fp8_f32(a, b, 0, false); w = __builtin_amdgcn_cvt_pk_fp8_f32(c, d, w, true); return (unsigned)w; }
;     const int pr = item >> 1, kb = 2 * (pr / nblk) + (item & 1), nb = pr % nblk, k0 = 64 * kb, n0 = 32 * nb;
;     const int nr = n0 + (lane & 31); const int sc = MAP == 1 ? src_col_in(nr) : nr;
;     float v[32];
; #pragma unroll
;     for (int i = 0; i < 32; ++i) v[i] = sc >= 0 ? W[(size_t)(k0 + 2 * i + (lane >> 5)) * Nsrc + sc] : 0.f;
; #pragma unroll
;     for (int i = 0; i < 32; ++i) { const int k = k0 + 2 * i + (lane >> 5); float x = v[i] * wscale; if (KS) x *= (k < ksplit ? ksA[k] : ksB[k - ksplit]); scr[(2 * i + (lane >> 5)) * 33 + (lane & 31)] = x; }
;     LDS_WAIT(); asm volatile("" ::: "memory");
;     const int c = lane & 7;
; #pragma unroll
;     for (int j = 0; j < 4; ++j) { const int n = (lane >> 3) + 8 * j; const LAS float* s = scr + (8 * c) * 33 + n;
;         const unsigned long long o = (unsigned long long)pg8::pk4_fp8(s[0 * 33], s[1 * 33], s[2 * 33], s[3 * 33]) | ((unsigned long long)pg8::pk4_fp8(s[4 * 33], s[5 * 33], s[6 * 33], s[7 * 33]) << 32);
;         *(GAS unsigned long long*)(WT + (size_t)(n0 + n) * K + k0 + 8 * c) = o; }
;     LDS_WAIT(); asm volatile("" ::: "memory");
; }
	s_add_u32 s8, s30, 0xd000
	s_addc_u32 s9, s31, 0
	global_load_dwordx4 v[176:179], v74, s[8:9]
	s_add_u32 s8, s8, 0x20000
	s_addc_u32 s9, s9, 0
	global_load_dwordx4 v[180:183], v74, s[8:9]
	s_add_u32 s8, s8, 0x20000
	s_addc_u32 s9, s9, 0
	global_load_dwordx4 v[184:187], v74, s[8:9]
	s_add_u32 s8, s8, 0x20000
	s_addc_u32 s9, s9, 0
	global_load_dwordx4 v[188:191], v74, s[8:9]
	s_add_u32 s8, s8, 0x20000
	s_addc_u32 s9, s9, 0
	global_load_dwordx4 v[192:195], v74, s[8:9]
	s_add_u32 s8, s8, 0x20000
	s_addc_u32 s9, s9, 0
	global_load_dwordx4 v[196:199], v74, s[8:9]
	s_add_u32 s8, s8, 0x20000
	s_addc_u32 s9, s9, 0
	global_load_dwordx4 v[200:203], v74, s[8:9]
	s_add_u32 s8, s8, 0x20000
	s_addc_u32 s9, s9, 0
	global_load_dwordx4 v[204:207], v74, s[8:9]
	s_add_u32 s6, s32, 0x2c00000
	s_addc_u32 s7, s33, 0
	ds_read_b32 v226, v212
	ds_read_b32 v227, v212 offset:512
	ds_read_b32 v228, v212 offset:1024
	ds_read_b32 v229, v212 offset:1536
	ds_read_b32 v230, v212 offset:2048
	ds_read_b32 v231, v212 offset:2560
	ds_read_b32 v232, v212 offset:3072
	ds_read_b32 v233, v212 offset:3584
	ds_read_b32 v234, v212 offset:4096
	ds_read_b32 v235, v212 offset:4608
	ds_read_b32 v236, v212 offset:5120
	ds_read_b32 v237, v212 offset:5632
	ds_read_b32 v238, v212 offset:6144
	ds_read_b32 v239, v212 offset:6656
	ds_read_b32 v240, v212 offset:7168
	ds_read_b32 v241, v212 offset:7680
	s_waitcnt lgkmcnt(0)
	v_max_f32_e32 v226, v226, v226
	v_max_f32_e32 v227, v227, v227
	v_max_f32_e32 v228, v228, v228
	v_max_f32_e32 v229, v229, v229
	v_max_f32_e32 v230, v230, v230
	v_max_f32_e32 v231, v231, v231
	v_max_f32_e32 v232, v232, v232
	v_max_f32_e32 v233, v233, v233
	v_max_f32_e32 v234, v234, v234
	v_max_f32_e32 v235, v235, v235
	v_max_f32_e32 v236, v236, v236
	v_max_f32_e32 v237, v237, v237
	v_max_f32_e32 v238, v238, v238
	v_max_f32_e32 v239, v239, v239
	v_max_f32_e32 v240, v240, v240
	v_max_f32_e32 v241, v241, v241
	v_med3_f32 v226, v226, s62, v95
	v_med3_f32 v227, v227, s62, v95
	v_med3_f32 v228, v228, s62, v95
	v_med3_f32 v229, v229, s62, v95
	v_med3_f32 v230, v230, s62, v95
	v_med3_f32 v231, v231, s62, v95
	v_med3_f32 v232, v232, s62, v95
	v_med3_f32 v233, v233, s62, v95
	v_med3_f32 v234, v234, s62, v95
	v_med3_f32 v235, v235, s62, v95
	v_med3_f32 v236, v236, s62, v95
	v_med3_f32 v237, v237, s62, v95
	v_med3_f32 v238, v238, s62, v95
	v_med3_f32 v239, v239, s62, v95
	v_med3_f32 v240, v240, s62, v95
	v_med3_f32 v241, v241, s62, v95
	v_mov_b32_e32 v242, 0
	v_mov_b32_e32 v243, 0
	v_mov_b32_e32 v244, 0
	v_mov_b32_e32 v245, 0
	v_cvt_pk_fp8_f32 v242, v226, v227
	v_cvt_pk_fp8_f32 v243, v230, v231
	v_cvt_pk_fp8_f32 v244, v234, v235
	v_cvt_pk_fp8_f32 v245, v238, v239
	v_cvt_pk_fp8_f32 v242, v228, v229 op_sel:[0,0,1]
	v_cvt_pk_fp8_f32 v243, v232, v233 op_sel:[0,0,1]
	v_cvt_pk_fp8_f32 v244, v236, v237 op_sel:[0,0,1]
	v_cvt_pk_fp8_f32 v245, v240, v241 op_sel:[0,0,1]
	s_nop 0
	global_store_dwordx4 v77, v[242:245], s[6:7]
	ds_read_b32 v226, v214
	ds_read_b32 v227, v214 offset:512
	ds_read_b32 v228, v214 offset:1024
	ds_read_b32 v229, v214 offset:1536
	ds_read_b32 v230, v214 offset:2048
	ds_read_b32 v231, v214 offset:2560
	ds_read_b32 v232, v214 offset:3072
	ds_read_b32 v233, v214 offset:3584
	ds_read_b32 v234, v214 offset:4096
	ds_read_b32 v235, v214 offset:4608
	ds_read_b32 v236, v214 offset:5120
	ds_read_b32 v237, v214 offset:5632
	ds_read_b32 v238, v214 offset:6144
	ds_read_b32 v239, v214 offset:6656
	ds_read_b32 v240, v214 offset:7168
	ds_read_b32 v241, v214 offset:7680
	s_waitcnt lgkmcnt(0)
	v_max_f32_e32 v226, v226, v226
	v_max_f32_e32 v227, v227, v227
	v_max_f32_e32 v228, v228, v228
	v_max_f32_e32 v229, v229, v229
	v_max_f32_e32 v230, v230, v230
	v_max_f32_e32 v231, v231, v231
	v_max_f32_e32 v232, v232, v232
	v_max_f32_e32 v233, v233, v233
	v_max_f32_e32 v234, v234, v234
	v_max_f32_e32 v235, v235, v235
	v_max_f32_e32 v236, v236, v236
	v_max_f32_e32 v237, v237, v237
	v_max_f32_e32 v238, v238, v238
	v_max_f32_e32 v239, v239, v239
	v_max_f32_e32 v240, v240, v240
	v_max_f32_e32 v241, v241, v241
	v_med3_f32 v226, v226, s62, v95
	v_med3_f32 v227, v227, s62, v95
	v_med3_f32 v228, v228, s62, v95
	v_med3_f32 v229, v229, s62, v95
	v_med3_f32 v230, v230, s62, v95
	v_med3_f32 v231, v231, s62, v95
	v_med3_f32 v232, v232, s62, v95
	v_med3_f32 v233, v233, s62, v95
	v_med3_f32 v234, v234, s62, v95
	v_med3_f32 v235, v235, s62, v95
	v_med3_f32 v236, v236, s62, v95
	v_med3_f32 v237, v237, s62, v95
	v_med3_f32 v238, v238, s62, v95
	v_med3_f32 v239, v239, s62, v95
	v_med3_f32 v240, v240, s62, v95
	v_med3_f32 v241, v241, s62, v95
	v_mov_b32_e32 v242, 0
	v_mov_b32_e32 v243, 0
	v_mov_b32_e32 v244, 0
	v_mov_b32_e32 v245, 0
	v_cvt_pk_fp8_f32 v242, v226, v227
	v_cvt_pk_fp8_f32 v243, v230, v231
	v_cvt_pk_fp8_f32 v244, v234, v235
	v_cvt_pk_fp8_f32 v245, v238, v239
	v_cvt_pk_fp8_f32 v242, v228, v229 op_sel:[0,0,1]
	v_cvt_pk_fp8_f32 v243, v232, v233 op_sel:[0,0,1]
	v_cvt_pk_fp8_f32 v244, v236, v237 op_sel:[0,0,1]
	v_cvt_pk_fp8_f32 v245, v240, v241 op_sel:[0,0,1]
	s_nop 0
	global_store_dwordx4 v78, v[242:245], s[6:7]
	s_waitcnt vmcnt(12)
	v_mul_f32_e32 v144, v26, v144
	v_mul_f32_e32 v145, v26, v145
	v_mul_f32_e32 v146, v26, v146
	v_mul_f32_e32 v147, v26, v147
	ds_write_b128 v209, v[144:147]
	v_mul_f32_e32 v148, v27, v148
	v_mul_f32_e32 v149, v27, v149
	v_mul_f32_e32 v150, v27, v150
	v_mul_f32_e32 v151, v27, v151
	ds_write_b128 v209, v[148:151] offset:1024
	v_mul_f32_e32 v152, v28, v152
	v_mul_f32_e32 v153, v28, v153
	v_mul_f32_e32 v154, v28, v154
	v_mul_f32_e32 v155, v28, v155
	ds_write_b128 v209, v[152:155] offset:2048
	v_mul_f32_e32 v156, v29, v156
	v_mul_f32_e32 v157, v29, v157
	v_mul_f32_e32 v158, v29, v158
	v_mul_f32_e32 v159, v29, v159
	ds_write_b128 v209, v[156:159] offset:3072
	v_mul_f32_e32 v160, v30, v160
	v_mul_f32_e32 v161, v30, v161
	v_mul_f32_e32 v162, v30, v162
	v_mul_f32_e32 v163, v30, v163
	ds_write_b128 v209, v[160:163] offset:4096
	v_mul_f32_e32 v164, v31, v164
	v_mul_f32_e32 v165, v31, v165
	v_mul_f32_e32 v166, v31, v166
	v_mul_f32_e32 v167, v31, v167
	ds_write_b128 v209, v[164:167] offset:5120
	v_mul_f32_e32 v168, v32, v168
	v_mul_f32_e32 v169, v32, v169
	v_mul_f32_e32 v170, v32, v170
	v_mul_f32_e32 v171, v32, v171
	ds_write_b128 v209, v[168:171] offset:6144
	v_mul_f32_e32 v172, v33, v172
	v_mul_f32_e32 v173, v33, v173
	v_mul_f32_e32 v174, v33, v174
	v_mul_f32_e32 v175, v33, v175
	ds_write_b128 v209, v[172:175] offset:7168
	s_waitcnt lgkmcnt(0)
	s_barrier
; #define GAS __attribute__((address_space(1)))
; #define LAS __attribute__((address_space(3)))
; #define LDS_WAIT() asm volatile("s_waitcnt lgkmcnt(0)" ::: "memory")
; __device__ __forceinline__ unsigned pk4_fp8(float a, float b, float c, float d) {
;     a = fminf(fmaxf(a, -448.f), 448.f); b = fminf(fmaxf(b, -448.f), 448.f); c = fminf(fmaxf(c, -448.f), 448.f); d = fminf(fmaxf(d, -448.f), 448.f);
;     int w = __builtin_amdgcn_cvt_pk_fp8_f32(a, b, 0, false); w = __builtin_amdgcn_cvt_pk_fp8_f32(c, d, w, true); return (unsigned)w; }
;     const int pr = item >> 1, kb = 2 * (pr / nblk) + (item & 1), nb = pr % nblk, k0 = 64 * kb, n0 = 32 * nb;
;     const int nr = n0 + (lane & 31); const int sc = MAP == 1 ? src_col_in(nr) : nr;
;     float v[32];
; #pragma unroll
;     for (int i = 0; i < 32; ++i) v[i] = sc >= 0 ? W[(size_t)(k0 + 2 * i + (lane >> 5)) * Nsrc + sc] : 0.f;
; #pragma unroll
;     for (int i = 0; i < 32; ++i) { const int k = k0 + 2 * i + (lane >> 5); float x = v[i] * wscale; if (KS) x *= (k < ksplit ? ksA[k] : ksB[k - ksplit]); scr[(2 * i + (lane >> 5)) * 33 + (lane & 31)] = x; }
;     LDS_WAIT(); asm volatile("" ::: "memory");
;     const int c = lane & 7;
; #pragma unroll
;     for (int j = 0; j < 4; ++j) { const int n = (lane >> 3) + 8 * j; const LAS float* s = scr + (8 * c) * 33 + n;
;         const unsigned long long o = (unsigned long long)pg8::pk4_fp8(s[0 * 33], s[1 * 33], s[2 * 33], s[3 * 33]) | ((unsigned long long)pg8::pk4_fp8(s[4 * 33], s[5 * 33], s[6 * 33], s[7 * 33]) << 32);
;         *(GAS unsigned long long*)(WT + (size_t)(n0 + n) * K + k0 + 8 * c) = o; }
;     LDS_WAIT(); asm volatile("" ::: "memory");
; }
	s_add_u32 s8, s30, 0xe000
	s_addc_u32 s9, s31, 0
	global_load_dwordx4 v[144:147], v74, s[8:9]
	s_add_u32 s8, s8, 0x20000
	s_addc_u32 s9, s9, 0
	global_load_dwordx4 v[148:151], v74, s[8:9]
	s_add_u32 s8, s8, 0x20000
	s_addc_u32 s9, s9, 0
	global_load_dwordx4 v[152:155], v74, s[8:9]
	s_add_u32 s8, s8, 0x20000
	s_addc_u32 s9, s9, 0
	global_load_dwordx4 v[156:159], v74, s[8:9]
	s_add_u32 s8, s8, 0x20000
	s_addc_u32 s9, s9, 0
	global_load_dwordx4 v[160:163], v74, s[8:9]
	s_add_u32 s8, s8, 0x20000
	s_addc_u32 s9, s9, 0
	global_load_dwordx4 v[164:167], v74, s[8:9]
	s_add_u32 s8, s8, 0x20000
	s_addc_u32 s9, s9, 0
	global_load_dwordx4 v[168:171], v74, s[8:9]
	s_add_u32 s8, s8, 0x20000
	s_addc_u32 s9, s9, 0
	global_load_dwordx4 v[172:175], v74, s[8:9]
	s_add_u32 s6, s32, 0x3000000
	s_addc_u32 s7, s33, 0
	ds_read_b32 v226, v211
	ds_read_b32 v227, v211 offset:512
	ds_read_b32 v228, v211 offset:1024
	ds_read_b32 v229, v211 offset:1536
	ds_read_b32 v230, v211 offset:2048
	ds_read_b32 v231, v211 offset:2560
	ds_read_b32 v232, v211 offset:3072
	ds_read_b32 v233, v211 offset:3584
	ds_read_b32 v234, v211 offset:4096
	ds_read_b32 v235, v211 offset:4608
	ds_read_b32 v236, v211 offset:5120
	ds_read_b32 v237, v211 offset:5632
	ds_read_b32 v238, v211 offset:6144
	ds_read_b32 v239, v211 offset:6656
	ds_read_b32 v240, v211 offset:7168
	ds_read_b32 v241, v211 offset:7680
	s_waitcnt lgkmcnt(0)
	v_max_f32_e32 v226, v226, v226
	v_max_f32_e32 v227, v227, v227
	v_max_f32_e32 v228, v228, v228
	v_max_f32_e32 v229, v229, v229
	v_max_f32_e32 v230, v230, v230
	v_max_f32_e32 v231, v231, v231
	v_max_f32_e32 v232, v232, v232
	v_max_f32_e32 v233, v233, v233
	v_max_f32_e32 v234, v234, v234
	v_max_f32_e32 v235, v235, v235
	v_max_f32_e32 v236, v236, v236
	v_max_f32_e32 v237, v237, v237
	v_max_f32_e32 v238, v238, v238
	v_max_f32_e32 v239, v239, v239
	v_max_f32_e32 v240, v240, v240
	v_max_f32_e32 v241, v241, v241
	v_med3_f32 v226, v226, s62, v95
	v_med3_f32 v227, v227, s62, v95
	v_med3_f32 v228, v228, s62, v95
	v_med3_f32 v229, v229, s62, v95
	v_med3_f32 v230, v230, s62, v95
	v_med3_f32 v231, v231, s62, v95
	v_med3_f32 v232, v232, s62, v95
	v_med3_f32 v233, v233, s62, v95
	v_med3_f32 v234, v234, s62, v95
	v_med3_f32 v235, v235, s62, v95
	v_med3_f32 v236, v236, s62, v95
	v_med3_f32 v237, v237, s62, v95
	v_med3_f32 v238, v238, s62, v95
	v_med3_f32 v239, v239, s62, v95
	v_med3_f32 v240, v240, s62, v95
	v_med3_f32 v241, v241, s62, v95
	v_mov_b32_e32 v242, 0
	v_mov_b32_e32 v243, 0
	v_mov_b32_e32 v244, 0
	v_mov_b32_e32 v245, 0
	v_cvt_pk_fp8_f32 v242, v226, v227
	v_cvt_pk_fp8_f32 v243, v230, v231
	v_cvt_pk_fp8_f32 v244, v234, v235
	v_cvt_pk_fp8_f32 v245, v238, v239
	v_cvt_pk_fp8_f32 v242, v228, v229 op_sel:[0,0,1]
	v_cvt_pk_fp8_f32 v243, v232, v233 op_sel:[0,0,1]
	v_cvt_pk_fp8_f32 v244, v236, v237 op_sel:[0,0,1]
	v_cvt_pk_fp8_f32 v245, v240, v241 op_sel:[0,0,1]
	s_nop 0
	global_store_dwordx4 v77, v[242:245], s[6:7]
	ds_read_b32 v226, v213
	ds_read_b32 v227, v213 offset:512
	ds_read_b32 v228, v213 offset:1024
	ds_read_b32 v229, v213 offset:1536
	ds_read_b32 v230, v213 offset:2048
	ds_read_b32 v231, v213 offset:2560
	ds_read_b32 v232, v213 offset:3072
	ds_read_b32 v233, v213 offset:3584
	ds_read_b32 v234, v213 offset:4096
	ds_read_b32 v235, v213 offset:4608
	ds_read_b32 v236, v213 offset:5120
	ds_read_b32 v237, v213 offset:5632
	ds_read_b32 v238, v213 offset:6144
	ds_read_b32 v239, v213 offset:6656
	ds_read_b32 v240, v213 offset:7168
	ds_read_b32 v241, v213 offset:7680
	s_waitcnt lgkmcnt(0)
	v_max_f32_e32 v226, v226, v226
	v_max_f32_e32 v227, v227, v227
	v_max_f32_e32 v228, v228, v228
	v_max_f32_e32 v229, v229, v229
	v_max_f32_e32 v230, v230, v230
	v_max_f32_e32 v231, v231, v231
	v_max_f32_e32 v232, v232, v232
	v_max_f32_e32 v233, v233, v233
	v_max_f32_e32 v234, v234, v234
	v_max_f32_e32 v235, v235, v235
	v_max_f32_e32 v236, v236, v236
	v_max_f32_e32 v237, v237, v237
	v_max_f32_e32 v238, v238, v238
	v_max_f32_e32 v239, v239, v239
	v_max_f32_e32 v240, v240, v240
	v_max_f32_e32 v241, v241, v241
	v_med3_f32 v226, v226, s62, v95
	v_med3_f32 v227, v227, s62, v95
	v_med3_f32 v228, v228, s62, v95
	v_med3_f32 v229, v229, s62, v95
	v_med3_f32 v230, v230, s62, v95
	v_med3_f32 v231, v231, s62, v95
	v_med3_f32 v232, v232, s62, v95
	v_med3_f32 v233, v233, s62, v95
	v_med3_f32 v234, v234, s62, v95
	v_med3_f32 v235, v235, s62, v95
	v_med3_f32 v236, v236, s62, v95
	v_med3_f32 v237, v237, s62, v95
	v_med3_f32 v238, v238, s62, v95
	v_med3_f32 v239, v239, s62, v95
	v_med3_f32 v240, v240, s62, v95
	v_med3_f32 v241, v241, s62, v95
	v_mov_b32_e32 v242, 0
	v_mov_b32_e32 v243, 0
	v_mov_b32_e32 v244, 0
	v_mov_b32_e32 v245, 0
	v_cvt_pk_fp8_f32 v242, v226, v227
	v_cvt_pk_fp8_f32 v243, v230, v231
	v_cvt_pk_fp8_f32 v244, v234, v235
	v_cvt_pk_fp8_f32 v245, v238, v239
	v_cvt_pk_fp8_f32 v242, v228, v229 op_sel:[0,0,1]
	v_cvt_pk_fp8_f32 v243, v232, v233 op_sel:[0,0,1]
	v_cvt_pk_fp8_f32 v244, v236, v237 op_sel:[0,0,1]
	v_cvt_pk_fp8_f32 v245, v240, v241 op_sel:[0,0,1]
	s_nop 0
	global_store_dwordx4 v78, v[242:245], s[6:7]
	s_waitcnt vmcnt(12)
	v_mul_f32_e32 v176, v26, v176
	v_mul_f32_e32 v177, v26, v177
	v_mul_f32_e32 v178, v26, v178
	v_mul_f32_e32 v179, v26, v179
	ds_write_b128 v210, v[176:179]
	v_mul_f32_e32 v180, v27, v180
	v_mul_f32_e32 v181, v27, v181
	v_mul_f32_e32 v182, v27, v182
	v_mul_f32_e32 v183, v27, v183
	ds_write_b128 v210, v[180:183] offset:1024
	v_mul_f32_e32 v184, v28, v184
	v_mul_f32_e32 v185, v28, v185
	v_mul_f32_e32 v186, v28, v186
	v_mul_f32_e32 v187, v28, v187
	ds_write_b128 v210, v[184:187] offset:2048
	v_mul_f32_e32 v188, v29, v188
	v_mul_f32_e32 v189, v29, v189
	v_mul_f32_e32 v190, v29, v190
	v_mul_f32_e32 v191, v29, v191
	ds_write_b128 v210, v[188:191] offset:3072
	v_mul_f32_e32 v192, v30, v192
	v_mul_f32_e32 v193, v30, v193
	v_mul_f32_e32 v194, v30, v194
	v_mul_f32_e32 v195, v30, v195
	ds_write_b128 v210, v[192:195] offset:4096
	v_mul_f32_e32 v196, v31, v196
	v_mul_f32_e32 v197, v31, v197
	v_mul_f32_e32 v198, v31, v198
	v_mul_f32_e32 v199, v31, v199
	ds_write_b128 v210, v[196:199] offset:5120
	v_mul_f32_e32 v200, v32, v200
	v_mul_f32_e32 v201, v32, v201
	v_mul_f32_e32 v202, v32, v202
	v_mul_f32_e32 v203, v32, v203
	ds_write_b128 v210, v[200:203] offset:6144
	v_mul_f32_e32 v204, v33, v204
	v_mul_f32_e32 v205, v33, v205
	v_mul_f32_e32 v206, v33, v206
	v_mul_f32_e32 v207, v33, v207
	ds_write_b128 v210, v[204:207] offset:7168
	s_waitcnt lgkmcnt(0)
	s_barrier
; #define GAS __attribute__((address_space(1)))
; #define LAS __attribute__((address_space(3)))
; #define LDS_WAIT() asm volatile("s_waitcnt lgkmcnt(0)" ::: "memory")
; __device__ __forceinline__ unsigned pk4_fp8(float a, float b, float c, float d) {
;     a = fminf(fmaxf(a, -448.f), 448.f); b = fminf(fmaxf(b, -448.f), 448.f); c = fminf(fmaxf(c, -448.f), 448.f); d = fminf(fmaxf(d, -448.f), 448.f);
;     int w = __builtin_amdgcn_cvt_pk_fp8_f32(a, b, 0, false); w = __builtin_amdgcn_cvt_pk_fp8_f32(c, d, w, true); return (unsigned)w; }
;     const int pr = item >> 1, kb = 2 * (pr / nblk) + (item & 1), nb = pr % nblk, k0 = 64 * kb, n0 = 32 * nb;
;     const int nr = n0 + (lane & 31); const int sc = MAP == 1 ? src_col_in(nr) : nr;
;     float v[32];
; #pragma unroll
;     for (int i = 0; i < 32; ++i) v[i] = sc >= 0 ? W[(size_t)(k0 + 2 * i + (lane >> 5)) * Nsrc + sc] : 0.f;
; #pragma unroll
;     for (int i = 0; i < 32; ++i) { const int k = k0 + 2 * i + (lane >> 5); float x = v[i] * wscale; if (KS) x *= (k < ksplit ? ksA[k] : ksB[k - ksplit]); scr[(2 * i + (lane >> 5)) * 33 + (lane & 31)] = x; }
;     LDS_WAIT(); asm volatile("" ::: "memory");
;     const int c = lane & 7;
; #pragma unroll
;     for (int j = 0; j < 4; ++j) { const int n = (lane >> 3) + 8 * j; const LAS float* s = scr + (8 * c) * 33 + n;
;         const unsigned long long o = (unsigned long long)pg8::pk4_fp8(s[0 * 33], s[1 * 33], s[2 * 33], s[3 * 33]) | ((unsigned long long)pg8::pk4_fp8(s[4 * 33], s[5 * 33], s[6 * 33], s[7 * 33]) << 32);
;         *(GAS unsigned long long*)(WT + (size_t)(n0 + n) * K + k0 + 8 * c) = o; }
;     LDS_WAIT(); asm volatile("" ::: "memory");
; }
	s_add_u32 s8, s30, 0xf000
	s_addc_u32 s9, s31, 0
	global_load_dwordx4 v[176:179], v74, s[8:9]
	s_add_u32 s8, s8, 0x20000
	s_addc_u32 s9, s9, 0
	global_load_dwordx4 v[180:183], v74, s[8:9]
	s_add_u32 s8, s8, 0x20000
	s_addc_u32 s9, s9, 0
	global_load_dwordx4 v[184:187], v74, s[8:9]
	s_add_u32 s8, s8, 0x20000
	s_addc_u32 s9, s9, 0
	global_load_dwordx4 v[188:191], v74, s[8:9]
	s_add_u32 s8, s8, 0x20000
	s_addc_u32 s9, s9, 0
	global_load_dwordx4 v[192:195], v74, s[8:9]
	s_add_u32 s8, s8, 0x20000
	s_addc_u32 s9, s9, 0
	global_load_dwordx4 v[196:199], v74, s[8:9]
	s_add_u32 s8, s8, 0x20000
	s_addc_u32 s9, s9, 0
	global_load_dwordx4 v[200:203], v74, s[8:9]
	s_add_u32 s8, s8, 0x20000
	s_addc_u32 s9, s9, 0
	global_load_dwordx4 v[204:207], v74, s[8:9]
	s_add_u32 s6, s32, 0x3400000
	s_addc_u32 s7, s33, 0
	ds_read_b32 v226, v212
	ds_read_b32 v227, v212 offset:512
	ds_read_b32 v228, v212 offset:1024
	ds_read_b32 v229, v212 offset:1536
	ds_read_b32 v230, v212 offset:2048
	ds_read_b32 v231, v212 offset:2560
	ds_read_b32 v232, v212 offset:3072
	ds_read_b32 v233, v212 offset:3584
	ds_read_b32 v234, v212 offset:4096
	ds_read_b32 v235, v212 offset:4608
	ds_read_b32 v236, v212 offset:5120
	ds_read_b32 v237, v212 offset:5632
	ds_read_b32 v238, v212 offset:6144
	ds_read_b32 v239, v212 offset:6656
	ds_read_b32 v240, v212 offset:7168
	ds_read_b32 v241, v212 offset:7680
	s_waitcnt lgkmcnt(0)
	v_max_f32_e32 v226, v226, v226
	v_max_f32_e32 v227, v227, v227
	v_max_f32_e32 v228, v228, v228
	v_max_f32_e32 v229, v229, v229
	v_max_f32_e32 v230, v230, v230
	v_max_f32_e32 v231, v231, v231
	v_max_f32_e32 v232, v232, v232
	v_max_f32_e32 v233, v233, v233
	v_max_f32_e32 v234, v234, v234
	v_max_f32_e32 v235, v235, v235
	v_max_f32_e32 v236, v236, v236
	v_max_f32_e32 v237, v237, v237
	v_max_f32_e32 v238, v238, v238
	v_max_f32_e32 v239, v239, v239
	v_max_f32_e32 v240, v240, v240
	v_max_f32_e32 v241, v241, v241
	v_med3_f32 v226, v226, s62, v95
	v_med3_f32 v227, v227, s62, v95
	v_med3_f32 v228, v228, s62, v95
	v_med3_f32 v229, v229, s62, v95
	v_med3_f32 v230, v230, s62, v95
	v_med3_f32 v231, v231, s62, v95
	v_med3_f32 v232, v232, s62, v95
	v_med3_f32 v233, v233, s62, v95
	v_med3_f32 v234, v234, s62, v95
	v_med3_f32 v235, v235, s62, v95
	v_med3_f32 v236, v236, s62, v95
	v_med3_f32 v237, v237, s62, v95
	v_med3_f32 v238, v238, s62, v95
	v_med3_f32 v239, v239, s62, v95
	v_med3_f32 v240, v240, s62, v95
	v_med3_f32 v241, v241, s62, v95
	v_mov_b32_e32 v242, 0
	v_mov_b32_e32 v243, 0
	v_mov_b32_e32 v244, 0
	v_mov_b32_e32 v245, 0
	v_cvt_pk_fp8_f32 v242, v226, v227
	v_cvt_pk_fp8_f32 v243, v230, v231
	v_cvt_pk_fp8_f32 v244, v234, v235
	v_cvt_pk_fp8_f32 v245, v238, v239
	v_cvt_pk_fp8_f32 v242, v228, v229 op_sel:[0,0,1]
	v_cvt_pk_fp8_f32 v243, v232, v233 op_sel:[0,0,1]
	v_cvt_pk_fp8_f32 v244, v236, v237 op_sel:[0,0,1]
	v_cvt_pk_fp8_f32 v245, v240, v241 op_sel:[0,0,1]
	s_nop 0
	global_store_dwordx4 v77, v[242:245], s[6:7]
	ds_read_b32 v226, v214
	ds_read_b32 v227, v214 offset:512
	ds_read_b32 v228, v214 offset:1024
	ds_read_b32 v229, v214 offset:1536
	ds_read_b32 v230, v214 offset:2048
	ds_read_b32 v231, v214 offset:2560
	ds_read_b32 v232, v214 offset:3072
	ds_read_b32 v233, v214 offset:3584
	ds_read_b32 v234, v214 offset:4096
	ds_read_b32 v235, v214 offset:4608
	ds_read_b32 v236, v214 offset:5120
	ds_read_b32 v237, v214 offset:5632
	ds_read_b32 v238, v214 offset:6144
	ds_read_b32 v239, v214 offset:6656
	ds_read_b32 v240, v214 offset:7168
	ds_read_b32 v241, v214 offset:7680
	s_waitcnt lgkmcnt(0)
	v_max_f32_e32 v226, v226, v226
	v_max_f32_e32 v227, v227, v227
	v_max_f32_e32 v228, v228, v228
	v_max_f32_e32 v229, v229, v229
	v_max_f32_e32 v230, v230, v230
	v_max_f32_e32 v231, v231, v231
	v_max_f32_e32 v232, v232, v232
	v_max_f32_e32 v233, v233, v233
	v_max_f32_e32 v234, v234, v234
	v_max_f32_e32 v235, v235, v235
	v_max_f32_e32 v236, v236, v236
	v_max_f32_e32 v237, v237, v237
	v_max_f32_e32 v238, v238, v238
	v_max_f32_e32 v239, v239, v239
	v_max_f32_e32 v240, v240, v240
	v_max_f32_e32 v241, v241, v241
	v_med3_f32 v226, v226, s62, v95
	v_med3_f32 v227, v227, s62, v95
	v_med3_f32 v228, v228, s62, v95
	v_med3_f32 v229, v229, s62, v95
	v_med3_f32 v230, v230, s62, v95
	v_med3_f32 v231, v231, s62, v95
	v_med3_f32 v232, v232, s62, v95
	v_med3_f32 v233, v233, s62, v95
	v_med3_f32 v234, v234, s62, v95
	v_med3_f32 v235, v235, s62, v95
	v_med3_f32 v236, v236, s62, v95
	v_med3_f32 v237, v237, s62, v95
	v_med3_f32 v238, v238, s62, v95
	v_med3_f32 v239, v239, s62, v95
	v_med3_f32 v240, v240, s62, v95
	v_med3_f32 v241, v241, s62, v95
	v_mov_b32_e32 v242, 0
	v_mov_b32_e32 v243, 0
	v_mov_b32_e32 v244, 0
	v_mov_b32_e32 v245, 0
	v_cvt_pk_fp8_f32 v242, v226, v227
	v_cvt_pk_fp8_f32 v243, v230, v231
	v_cvt_pk_fp8_f32 v244, v234, v235
	v_cvt_pk_fp8_f32 v245, v238, v239
	v_cvt_pk_fp8_f32 v242, v228, v229 op_sel:[0,0,1]
	v_cvt_pk_fp8_f32 v243, v232, v233 op_sel:[0,0,1]
	v_cvt_pk_fp8_f32 v244, v236, v237 op_sel:[0,0,1]
	v_cvt_pk_fp8_f32 v245, v240, v241 op_sel:[0,0,1]
	s_nop 0
	global_store_dwordx4 v78, v[242:245], s[6:7]
	s_waitcnt vmcnt(12)
	v_mul_f32_e32 v144, v26, v144
	v_mul_f32_e32 v145, v26, v145
	v_mul_f32_e32 v146, v26, v146
	v_mul_f32_e32 v147, v26, v147
	ds_write_b128 v209, v[144:147]
	v_mul_f32_e32 v148, v27, v148
	v_mul_f32_e32 v149, v27, v149
	v_mul_f32_e32 v150, v27, v150
	v_mul_f32_e32 v151, v27, v151
	ds_write_b128 v209, v[148:151] offset:1024
	v_mul_f32_e32 v152, v28, v152
	v_mul_f32_e32 v153, v28, v153
	v_mul_f32_e32 v154, v28, v154
	v_mul_f32_e32 v155, v28, v155
	ds_write_b128 v209, v[152:155] offset:2048
	v_mul_f32_e32 v156, v29, v156
	v_mul_f32_e32 v157, v29, v157
	v_mul_f32_e32 v158, v29, v158
	v_mul_f32_e32 v159, v29, v159
	ds_write_b128 v209, v[156:159] offset:3072
	v_mul_f32_e32 v160, v30, v160
	v_mul_f32_e32 v161, v30, v161
	v_mul_f32_e32 v162, v30, v162
	v_mul_f32_e32 v163, v30, v163
	ds_write_b128 v209, v[160:163] offset:4096
	v_mul_f32_e32 v164, v31, v164
	v_mul_f32_e32 v165, v31, v165
	v_mul_f32_e32 v166, v31, v166
	v_mul_f32_e32 v167, v31, v167
	ds_write_b128 v209, v[164:167] offset:5120
	v_mul_f32_e32 v168, v32, v168
	v_mul_f32_e32 v169, v32, v169
	v_mul_f32_e32 v170, v32, v170
	v_mul_f32_e32 v171, v32, v171
	ds_write_b128 v209, v[168:171] offset:6144
	v_mul_f32_e32 v172, v33, v172
	v_mul_f32_e32 v173, v33, v173
	v_mul_f32_e32 v174, v33, v174
	v_mul_f32_e32 v175, v33, v175
	ds_write_b128 v209, v[172:175] offset:7168
	s_waitcnt lgkmcnt(0)
	s_barrier
; #define GAS __attribute__((address_space(1)))
; #define LAS __attribute__((address_space(3)))
; #define LDS_WAIT() asm volatile("s_waitcnt lgkmcnt(0)" ::: "memory")
; __device__ __forceinline__ unsigned pk4_fp8(float a, float b, float c, float d) {
;     a = fminf(fmaxf(a, -448.f), 448.f); b = fminf(fmaxf(b, -448.f), 448.f); c = fminf(fmaxf(c, -448.f), 448.f); d = fminf(fmaxf(d, -448.f), 448.f);
;     int w = __builtin_amdgcn_cvt_pk_fp8_f32(a, b, 0, false); w = __builtin_amdgcn_cvt_pk_fp8_f32(c, d, w, true); return (unsigned)w; }
;     const int pr = item >> 1, kb = 2 * (pr / nblk) + (item & 1), nb = pr % nblk, k0 = 64 * kb, n0 = 32 * nb;
;     const int nr = n0 + (lane & 31); const int sc = MAP == 1 ? src_col_in(nr) : nr;
;     float v[32];
; #pragma unroll
;     for (int i = 0; i < 32; ++i) v[i] = sc >= 0 ? W[(size_t)(k0 + 2 * i + (lane >> 5)) * Nsrc + sc] : 0.f;
; #pragma unroll
;     for (int i = 0; i < 32; ++i) { const int k = k0 + 2 * i + (lane >> 5); float x = v[i] * wscale; if (KS) x *= (k < ksplit ? ksA[k] : ksB[k - ksplit]); scr[(2 * i + (lane >> 5)) * 33 + (lane & 31)] = x; }
;     LDS_WAIT(); asm volatile("" ::: "memory");
;     const int c = lane & 7;
; #pragma unroll
;     for (int j = 0; j < 4; ++j) { const int n = (lane >> 3) + 8 * j; const LAS float* s = scr + (8 * c) * 33 + n;
;         const unsigned long long o = (unsigned long long)pg8::pk4_fp8(s[0 * 33], s[1 * 33], s[2 * 33], s[3 * 33]) | ((unsigned long long)pg8::pk4_fp8(s[4 * 33], s[5 * 33], s[6 * 33], s[7 * 33]) << 32);
;         *(GAS unsigned long long*)(WT + (size_t)(n0 + n) * K + k0 + 8 * c) = o; }
;     LDS_WAIT(); asm volatile("" ::: "memory");
; }
	s_mov_b64 s[8:9], s[34:35]
	global_load_dwordx4 v[144:147], v74, s[8:9]
	s_add_u32 s8, s8, 0x20000
	s_addc_u32 s9, s9, 0
	global_load_dwordx4 v[148:151], v74, s[8:9]
	s_add_u32 s8, s8, 0x20000
	s_addc_u32 s9, s9, 0
	global_load_dwordx4 v[152:155], v74, s[8:9]
	s_add_u32 s8, s8, 0x20000
	s_addc_u32 s9, s9, 0
	global_load_dwordx4 v[156:159], v74, s[8:9]
	s_add_u32 s8, s8, 0x20000
	s_addc_u32 s9, s9, 0
	global_load_dwordx4 v[160:163], v74, s[8:9]
	s_add_u32 s8, s8, 0x20000
	s_addc_u32 s9, s9, 0
	global_load_dwordx4 v[164:167], v74, s[8:9]
	s_add_u32 s8, s8, 0x20000
	s_addc_u32 s9, s9, 0
	global_load_dwordx4 v[168:171], v74, s[8:9]
	s_add_u32 s8, s8, 0x20000
	s_addc_u32 s9, s9, 0
	global_load_dwordx4 v[172:175], v74, s[8:9]
	s_add_u32 s6, s32, 0x3800000
	s_addc_u32 s7, s33, 0
	ds_read_b32 v226, v211
	ds_read_b32 v227, v211 offset:512
	ds_read_b32 v228, v211 offset:1024
	ds_read_b32 v229, v211 offset:1536
	ds_read_b32 v230, v211 offset:2048
	ds_read_b32 v231, v211 offset:2560
	ds_read_b32 v232, v211 offset:3072
	ds_read_b32 v233, v211 offset:3584
	ds_read_b32 v234, v211 offset:4096
	ds_read_b32 v235, v211 offset:4608
	ds_read_b32 v236, v211 offset:5120
	ds_read_b32 v237, v211 offset:5632
	ds_read_b32 v238, v211 offset:6144
	ds_read_b32 v239, v211 offset:6656
	ds_read_b32 v240, v211 offset:7168
	ds_read_b32 v241, v211 offset:7680
	s_waitcnt lgkmcnt(0)
	v_max_f32_e32 v226, v226, v226
	v_max_f32_e32 v227, v227, v227
	v_max_f32_e32 v228, v228, v228
	v_max_f32_e32 v229, v229, v229
	v_max_f32_e32 v230, v230, v230
	v_max_f32_e32 v231, v231, v231
	v_max_f32_e32 v232, v232, v232
	v_max_f32_e32 v233, v233, v233
	v_max_f32_e32 v234, v234, v234
	v_max_f32_e32 v235, v235, v235
	v_max_f32_e32 v236, v236, v236
	v_max_f32_e32 v237, v237, v237
	v_max_f32_e32 v238, v238, v238
	v_max_f32_e32 v239, v239, v239
	v_max_f32_e32 v240, v240, v240
	v_max_f32_e32 v241, v241, v241
	v_med3_f32 v226, v226, s62, v95
	v_med3_f32 v227, v227, s62, v95
	v_med3_f32 v228, v228, s62, v95
	v_med3_f32 v229, v229, s62, v95
	v_med3_f32 v230, v230, s62, v95
	v_med3_f32 v231, v231, s62, v95
	v_med3_f32 v232, v232, s62, v95
	v_med3_f32 v233, v233, s62, v95
	v_med3_f32 v234, v234, s62, v95
	v_med3_f32 v235, v235, s62, v95
	v_med3_f32 v236, v236, s62, v95
	v_med3_f32 v237, v237, s62, v95
	v_med3_f32 v238, v238, s62, v95
	v_med3_f32 v239, v239, s62, v95
	v_med3_f32 v240, v240, s62, v95
	v_med3_f32 v241, v241, s62, v95
	v_mov_b32_e32 v242, 0
	v_mov_b32_e32 v243, 0
	v_mov_b32_e32 v244, 0
	v_mov_b32_e32 v245, 0
	v_cvt_pk_fp8_f32 v242, v226, v227
	v_cvt_pk_fp8_f32 v243, v230, v231
	v_cvt_pk_fp8_f32 v244, v234, v235
	v_cvt_pk_fp8_f32 v245, v238, v239
	v_cvt_pk_fp8_f32 v242, v228, v229 op_sel:[0,0,1]
	v_cvt_pk_fp8_f32 v243, v232, v233 op_sel:[0,0,1]
	v_cvt_pk_fp8_f32 v244, v236, v237 op_sel:[0,0,1]
	v_cvt_pk_fp8_f32 v245, v240, v241 op_sel:[0,0,1]
	s_nop 0
	global_store_dwordx4 v77, v[242:245], s[6:7]
	ds_read_b32 v226, v213
	ds_read_b32 v227, v213 offset:512
	ds_read_b32 v228, v213 offset:1024
	ds_read_b32 v229, v213 offset:1536
	ds_read_b32 v230, v213 offset:2048
	ds_read_b32 v231, v213 offset:2560
	ds_read_b32 v232, v213 offset:3072
	ds_read_b32 v233, v213 offset:3584
	ds_read_b32 v234, v213 offset:4096
	ds_read_b32 v235, v213 offset:4608
	ds_read_b32 v236, v213 offset:5120
	ds_read_b32 v237, v213 offset:5632
	ds_read_b32 v238, v213 offset:6144
	ds_read_b32 v239, v213 offset:6656
	ds_read_b32 v240, v213 offset:7168
	ds_read_b32 v241, v213 offset:7680
	s_waitcnt lgkmcnt(0)
	v_max_f32_e32 v226, v226, v226
	v_max_f32_e32 v227, v227, v227
	v_max_f32_e32 v228, v228, v228
	v_max_f32_e32 v229, v229, v229
	v_max_f32_e32 v230, v230, v230
	v_max_f32_e32 v231, v231, v231
	v_max_f32_e32 v232, v232, v232
	v_max_f32_e32 v233, v233, v233
	v_max_f32_e32 v234, v234, v234
	v_max_f32_e32 v235, v235, v235
	v_max_f32_e32 v236, v236, v236
	v_max_f32_e32 v237, v237, v237
	v_max_f32_e32 v238, v238, v238
	v_max_f32_e32 v239, v239, v239
	v_max_f32_e32 v240, v240, v240
	v_max_f32_e32 v241, v241, v241
	v_med3_f32 v226, v226, s62, v95
	v_med3_f32 v227, v227, s62, v95
	v_med3_f32 v228, v228, s62, v95
	v_med3_f32 v229, v229, s62, v95
	v_med3_f32 v230, v230, s62, v95
	v_med3_f32 v231, v231, s62, v95
	v_med3_f32 v232, v232, s62, v95
	v_med3_f32 v233, v233, s62, v95
	v_med3_f32 v234, v234, s62, v95
	v_med3_f32 v235, v235, s62, v95
	v_med3_f32 v236, v236, s62, v95
	v_med3_f32 v237, v237, s62, v95
	v_med3_f32 v238, v238, s62, v95
	v_med3_f32 v239, v239, s62, v95
	v_med3_f32 v240, v240, s62, v95
	v_med3_f32 v241, v241, s62, v95
	v_mov_b32_e32 v242, 0
	v_mov_b32_e32 v243, 0
	v_mov_b32_e32 v244, 0
	v_mov_b32_e32 v245, 0
	v_cvt_pk_fp8_f32 v242, v226, v227
	v_cvt_pk_fp8_f32 v243, v230, v231
	v_cvt_pk_fp8_f32 v244, v234, v235
	v_cvt_pk_fp8_f32 v245, v238, v239
	v_cvt_pk_fp8_f32 v242, v228, v229 op_sel:[0,0,1]
	v_cvt_pk_fp8_f32 v243, v232, v233 op_sel:[0,0,1]
	v_cvt_pk_fp8_f32 v244, v236, v237 op_sel:[0,0,1]
	v_cvt_pk_fp8_f32 v245, v240, v241 op_sel:[0,0,1]
	s_nop 0
	global_store_dwordx4 v78, v[242:245], s[6:7]
	s_waitcnt vmcnt(12)
	v_mul_f32_e32 v176, v26, v176
	v_mul_f32_e32 v177, v26, v177
	v_mul_f32_e32 v178, v26, v178
	v_mul_f32_e32 v179, v26, v179
	ds_write_b128 v210, v[176:179]
	v_mul_f32_e32 v180, v27, v180
	v_mul_f32_e32 v181, v27, v181
	v_mul_f32_e32 v182, v27, v182
	v_mul_f32_e32 v183, v27, v183
	ds_write_b128 v210, v[180:183] offset:1024
	v_mul_f32_e32 v184, v28, v184
	v_mul_f32_e32 v185, v28, v185
	v_mul_f32_e32 v186, v28, v186
	v_mul_f32_e32 v187, v28, v187
	ds_write_b128 v210, v[184:187] offset:2048
	v_mul_f32_e32 v188, v29, v188
	v_mul_f32_e32 v189, v29, v189
	v_mul_f32_e32 v190, v29, v190
	v_mul_f32_e32 v191, v29, v191
	ds_write_b128 v210, v[188:191] offset:3072
	v_mul_f32_e32 v192, v30, v192
	v_mul_f32_e32 v193, v30, v193
	v_mul_f32_e32 v194, v30, v194
	v_mul_f32_e32 v195, v30, v195
	ds_write_b128 v210, v[192:195] offset:4096
	v_mul_f32_e32 v196, v31, v196
	v_mul_f32_e32 v197, v31, v197
	v_mul_f32_e32 v198, v31, v198
	v_mul_f32_e32 v199, v31, v199
	ds_write_b128 v210, v[196:199] offset:5120
	v_mul_f32_e32 v200, v32, v200
	v_mul_f32_e32 v201, v32, v201
	v_mul_f32_e32 v202, v32, v202
	v_mul_f32_e32 v203, v32, v203
	ds_write_b128 v210, v[200:203] offset:6144
	v_mul_f32_e32 v204, v33, v204
	v_mul_f32_e32 v205, v33, v205
	v_mul_f32_e32 v206, v33, v206
	v_mul_f32_e32 v207, v33, v207
	ds_write_b128 v210, v[204:207] offset:7168
	s_waitcnt lgkmcnt(0)
	s_barrier
; #define GAS __attribute__((address_space(1)))
; #define LAS __attribute__((address_space(3)))
; #define LDS_WAIT() asm volatile("s_waitcnt lgkmcnt(0)" ::: "memory")
; __device__ __forceinline__ unsigned pk4_fp8(float a, float b, float c, float d) {
;     a = fminf(fmaxf(a, -448.f), 448.f); b = fminf(fmaxf(b, -448.f), 448.f); c = fminf(fmaxf(c, -448.f), 448.f); d = fminf(fmaxf(d, -448.f), 448.f);
;     int w = __builtin_amdgcn_cvt_pk_fp8_f32(a, b, 0, false); w = __builtin_amdgcn_cvt_pk_fp8_f32(c, d, w, true); return (unsigned)w; }
;     const int pr = item >> 1, kb = 2 * (pr / nblk) + (item & 1), nb = pr % nblk, k0 = 64 * kb, n0 = 32 * nb;
;     const int nr = n0 + (lane & 31); const int sc = MAP == 1 ? src_col_in(nr) : nr;
;     float v[32];
; #pragma unroll
;     for (int i = 0; i < 32; ++i) v[i] = sc >= 0 ? W[(size_t)(k0 + 2 * i + (lane >> 5)) * Nsrc + sc] : 0.f;
; #pragma unroll
;     for (int i = 0; i < 32; ++i) { const int k = k0 + 2 * i + (lane >> 5); float x = v[i] * wscale; if (KS) x *= (k < ksplit ? ksA[k] : ksB[k - ksplit]); scr[(2 * i + (lane >> 5)) * 33 + (lane & 31)] = x; }
;     LDS_WAIT(); asm volatile("" ::: "memory");
;     const int c = lane & 7;
; #pragma unroll
;     for (int j = 0; j < 4; ++j) { const int n = (lane >> 3) + 8 * j; const LAS float* s = scr + (8 * c) * 33 + n;
;         const unsigned long long o = (unsigned long long)pg8::pk4_fp8(s[0 * 33], s[1 * 33], s[2 * 33], s[3 * 33]) | ((unsigned long long)pg8::pk4_fp8(s[4 * 33], s[5 * 33], s[6 * 33], s[7 * 33]) << 32);
;         *(GAS unsigned long long*)(WT + (size_t)(n0 + n) * K + k0 + 8 * c) = o; }
;     LDS_WAIT(); asm volatile("" ::: "memory");
; }
	s_add_u32 s8, s34, 0x1000
	s_addc_u32 s9, s35, 0
	global_load_dwordx4 v[176:179], v74, s[8:9]
	s_add_u32 s8, s8, 0x20000
	s_addc_u32 s9, s9, 0
	global_load_dwordx4 v[180:183], v74, s[8:9]
	s_add_u32 s8, s8, 0x20000
	s_addc_u32 s9, s9, 0
	global_load_dwordx4 v[184:187], v74, s[8:9]
	s_add_u32 s8, s8, 0x20000
	s_addc_u32 s9, s9, 0
	global_load_dwordx4 v[188:191], v74, s[8:9]
	s_add_u32 s8, s8, 0x20000
	s_addc_u32 s9, s9, 0
	global_load_dwordx4 v[192:195], v74, s[8:9]
	s_add_u32 s8, s8, 0x20000
	s_addc_u32 s9, s9, 0
	global_load_dwordx4 v[196:199], v74, s[8:9]
	s_add_u32 s8, s8, 0x20000
	s_addc_u32 s9, s9, 0
	global_load_dwordx4 v[200:203], v74, s[8:9]
	s_add_u32 s8, s8, 0x20000
	s_addc_u32 s9, s9, 0
	global_load_dwordx4 v[204:207], v74, s[8:9]
	s_add_u32 s6, s32, 0x3c00000
	s_addc_u32 s7, s33, 0
	ds_read_b32 v226, v212
	ds_read_b32 v227, v212 offset:512
	ds_read_b32 v228, v212 offset:1024
	ds_read_b32 v229, v212 offset:1536
	ds_read_b32 v230, v212 offset:2048
	ds_read_b32 v231, v212 offset:2560
	ds_read_b32 v232, v212 offset:3072
	ds_read_b32 v233, v212 offset:3584
	ds_read_b32 v234, v212 offset:4096
	ds_read_b32 v235, v212 offset:4608
	ds_read_b32 v236, v212 offset:5120
	ds_read_b32 v237, v212 offset:5632
	ds_read_b32 v238, v212 offset:6144
	ds_read_b32 v239, v212 offset:6656
	ds_read_b32 v240, v212 offset:7168
	ds_read_b32 v241, v212 offset:7680
	s_waitcnt lgkmcnt(0)
	v_max_f32_e32 v226, v226, v226
	v_max_f32_e32 v227, v227, v227
	v_max_f32_e32 v228, v228, v228
	v_max_f32_e32 v229, v229, v229
	v_max_f32_e32 v230, v230, v230
	v_max_f32_e32 v231, v231, v231
	v_max_f32_e32 v232, v232, v232
	v_max_f32_e32 v233, v233, v233
	v_max_f32_e32 v234, v234, v234
	v_max_f32_e32 v235, v235, v235
	v_max_f32_e32 v236, v236, v236
	v_max_f32_e32 v237, v237, v237
	v_max_f32_e32 v238, v238, v238
	v_max_f32_e32 v239, v239, v239
	v_max_f32_e32 v240, v240, v240
	v_max_f32_e32 v241, v241, v241
	v_med3_f32 v226, v226, s62, v95
	v_med3_f32 v227, v227, s62, v95
	v_med3_f32 v228, v228, s62, v95
	v_med3_f32 v229, v229, s62, v95
	v_med3_f32 v230, v230, s62, v95
	v_med3_f32 v231, v231, s62, v95
	v_med3_f32 v232, v232, s62, v95
	v_med3_f32 v233, v233, s62, v95
	v_med3_f32 v234, v234, s62, v95
	v_med3_f32 v235, v235, s62, v95
	v_med3_f32 v236, v236, s62, v95
	v_med3_f32 v237, v237, s62, v95
	v_med3_f32 v238, v238, s62, v95
	v_med3_f32 v239, v239, s62, v95
	v_med3_f32 v240, v240, s62, v95
	v_med3_f32 v241, v241, s62, v95
	v_mov_b32_e32 v242, 0
	v_mov_b32_e32 v243, 0
	v_mov_b32_e32 v244, 0
	v_mov_b32_e32 v245, 0
	v_cvt_pk_fp8_f32 v242, v226, v227
	v_cvt_pk_fp8_f32 v243, v230, v231
	v_cvt_pk_fp8_f32 v244, v234, v235
	v_cvt_pk_fp8_f32 v245, v238, v239
	v_cvt_pk_fp8_f32 v242, v228, v229 op_sel:[0,0,1]
	v_cvt_pk_fp8_f32 v243, v232, v233 op_sel:[0,0,1]
	v_cvt_pk_fp8_f32 v244, v236, v237 op_sel:[0,0,1]
	v_cvt_pk_fp8_f32 v245, v240, v241 op_sel:[0,0,1]
	s_nop 0
	global_store_dwordx4 v77, v[242:245], s[6:7]
	ds_read_b32 v226, v214
	ds_read_b32 v227, v214 offset:512
	ds_read_b32 v228, v214 offset:1024
	ds_read_b32 v229, v214 offset:1536
	ds_read_b32 v230, v214 offset:2048
	ds_read_b32 v231, v214 offset:2560
	ds_read_b32 v232, v214 offset:3072
	ds_read_b32 v233, v214 offset:3584
	ds_read_b32 v234, v214 offset:4096
	ds_read_b32 v235, v214 offset:4608
	ds_read_b32 v236, v214 offset:5120
	ds_read_b32 v237, v214 offset:5632
	ds_read_b32 v238, v214 offset:6144
	ds_read_b32 v239, v214 offset:6656
	ds_read_b32 v240, v214 offset:7168
	ds_read_b32 v241, v214 offset:7680
	s_waitcnt lgkmcnt(0)
	v_max_f32_e32 v226, v226, v226
	v_max_f32_e32 v227, v227, v227
	v_max_f32_e32 v228, v228, v228
	v_max_f32_e32 v229, v229, v229
	v_max_f32_e32 v230, v230, v230
	v_max_f32_e32 v231, v231, v231
	v_max_f32_e32 v232, v232, v232
	v_max_f32_e32 v233, v233, v233
	v_max_f32_e32 v234, v234, v234
	v_max_f32_e32 v235, v235, v235
	v_max_f32_e32 v236, v236, v236
	v_max_f32_e32 v237, v237, v237
	v_max_f32_e32 v238, v238, v238
	v_max_f32_e32 v239, v239, v239
	v_max_f32_e32 v240, v240, v240
	v_max_f32_e32 v241, v241, v241
	v_med3_f32 v226, v226, s62, v95
	v_med3_f32 v227, v227, s62, v95
	v_med3_f32 v228, v228, s62, v95
	v_med3_f32 v229, v229, s62, v95
	v_med3_f32 v230, v230, s62, v95
	v_med3_f32 v231, v231, s62, v95
	v_med3_f32 v232, v232, s62, v95
	v_med3_f32 v233, v233, s62, v95
	v_med3_f32 v234, v234, s62, v95
	v_med3_f32 v235, v235, s62, v95
	v_med3_f32 v236, v236, s62, v95
	v_med3_f32 v237, v237, s62, v95
	v_med3_f32 v238, v238, s62, v95
	v_med3_f32 v239, v239, s62, v95
	v_med3_f32 v240, v240, s62, v95
	v_med3_f32 v241, v241, s62, v95
	v_mov_b32_e32 v242, 0
	v_mov_b32_e32 v243, 0
	v_mov_b32_e32 v244, 0
	v_mov_b32_e32 v245, 0
	v_cvt_pk_fp8_f32 v242, v226, v227
	v_cvt_pk_fp8_f32 v243, v230, v231
	v_cvt_pk_fp8_f32 v244, v234, v235
	v_cvt_pk_fp8_f32 v245, v238, v239
	v_cvt_pk_fp8_f32 v242, v228, v229 op_sel:[0,0,1]
	v_cvt_pk_fp8_f32 v243, v232, v233 op_sel:[0,0,1]
	v_cvt_pk_fp8_f32 v244, v236, v237 op_sel:[0,0,1]
	v_cvt_pk_fp8_f32 v245, v240, v241 op_sel:[0,0,1]
	s_nop 0
	global_store_dwordx4 v78, v[242:245], s[6:7]
	s_waitcnt vmcnt(12)
	v_mul_f32_e32 v144, v34, v144
	v_mul_f32_e32 v145, v34, v145
	v_mul_f32_e32 v146, v34, v146
	v_mul_f32_e32 v147, v34, v147
	ds_write_b128 v209, v[144:147]
	v_mul_f32_e32 v148, v35, v148
	v_mul_f32_e32 v149, v35, v149
	v_mul_f32_e32 v150, v35, v150
	v_mul_f32_e32 v151, v35, v151
	ds_write_b128 v209, v[148:151] offset:1024
	v_mul_f32_e32 v152, v36, v152
	v_mul_f32_e32 v153, v36, v153
	v_mul_f32_e32 v154, v36, v154
	v_mul_f32_e32 v155, v36, v155
	ds_write_b128 v209, v[152:155] offset:2048
	v_mul_f32_e32 v156, v37, v156
	v_mul_f32_e32 v157, v37, v157
	v_mul_f32_e32 v158, v37, v158
	v_mul_f32_e32 v159, v37, v159
	ds_write_b128 v209, v[156:159] offset:3072
	v_mul_f32_e32 v160, v38, v160
	v_mul_f32_e32 v161, v38, v161
	v_mul_f32_e32 v162, v38, v162
	v_mul_f32_e32 v163, v38, v163
	ds_write_b128 v209, v[160:163] offset:4096
	v_mul_f32_e32 v164, v39, v164
	v_mul_f32_e32 v165, v39, v165
	v_mul_f32_e32 v166, v39, v166
	v_mul_f32_e32 v167, v39, v167
	ds_write_b128 v209, v[164:167] offset:5120
	v_mul_f32_e32 v168, v40, v168
	v_mul_f32_e32 v169, v40, v169
	v_mul_f32_e32 v170, v40, v170
	v_mul_f32_e32 v171, v40, v171
	ds_write_b128 v209, v[168:171] offset:6144
	v_mul_f32_e32 v172, v41, v172
	v_mul_f32_e32 v173, v41, v173
	v_mul_f32_e32 v174, v41, v174
	v_mul_f32_e32 v175, v41, v175
	ds_write_b128 v209, v[172:175] offset:7168
	s_waitcnt lgkmcnt(0)
	s_barrier
; #define GAS __attribute__((address_space(1)))
; #define LAS __attribute__((address_space(3)))
; #define LDS_WAIT() asm volatile("s_waitcnt lgkmcnt(0)" ::: "memory")
; __device__ __forceinline__ unsigned pk4_fp8(float a, float b, float c, float d) {
;     a = fminf(fmaxf(a, -448.f), 448.f); b = fminf(fmaxf(b, -448.f), 448.f); c = fminf(fmaxf(c, -448.f), 448.f); d = fminf(fmaxf(d, -448.f), 448.f);
;     int w = __builtin_amdgcn_cvt_pk_fp8_f32(a, b, 0, false); w = __builtin_amdgcn_cvt_pk_fp8_f32(c, d, w, true); return (unsigned)w; }
;     const int pr = item >> 1, kb = 2 * (pr / nblk) + (item & 1), nb = pr % nblk, k0 = 64 * kb, n0 = 32 * nb;
;     const int nr = n0 + (lane & 31); const int sc = MAP == 1 ? src_col_in(nr) : nr;
;     float v[32];
; #pragma unroll
;     for (int i = 0; i < 32; ++i) v[i] = sc >= 0 ? W[(size_t)(k0 + 2 * i + (lane >> 5)) * Nsrc + sc] : 0.f;
; #pragma unroll
;     for (int i = 0; i < 32; ++i) { const int k = k0 + 2 * i + (lane >> 5); float x = v[i] * wscale; if (KS) x *= (k < ksplit ? ksA[k] : ksB[k - ksplit]); scr[(2 * i + (lane >> 5)) * 33 + (lane & 31)] = x; }
;     LDS_WAIT(); asm volatile("" ::: "memory");
;     const int c = lane & 7;
; #pragma unroll
;     for (int j = 0; j < 4; ++j) { const int n = (lane >> 3) + 8 * j; const LAS float* s = scr + (8 * c) * 33 + n;
;         const unsigned long long o = (unsigned long long)pg8::pk4_fp8(s[0 * 33], s[1 * 33], s[2 * 33], s[3 * 33]) | ((unsigned long long)pg8::pk4_fp8(s[4 * 33], s[5 * 33], s[6 * 33], s[7 * 33]) << 32);
;         *(GAS unsigned long long*)(WT + (size_t)(n0 + n) * K + k0 + 8 * c) = o; }
;     LDS_WAIT(); asm volatile("" ::: "memory");
; }
	s_add_u32 s8, s34, 0x2000
	s_addc_u32 s9, s35, 0
	global_load_dwordx4 v[144:147], v74, s[8:9]
	s_add_u32 s8, s8, 0x20000
	s_addc_u32 s9, s9, 0
	global_load_dwordx4 v[148:151], v74, s[8:9]
	s_add_u32 s8, s8, 0x20000
	s_addc_u32 s9, s9, 0
	global_load_dwordx4 v[152:155], v74, s[8:9]
	s_add_u32 s8, s8, 0x20000
	s_addc_u32 s9, s9, 0
	global_load_dwordx4 v[156:159], v74, s[8:9]
	s_add_u32 s8, s8, 0x20000
	s_addc_u32 s9, s9, 0
	global_load_dwordx4 v[160:163], v74, s[8:9]
	s_add_u32 s8, s8, 0x20000
	s_addc_u32 s9, s9, 0
	global_load_dwordx4 v[164:167], v74, s[8:9]
	s_add_u32 s8, s8, 0x20000
	s_addc_u32 s9, s9, 0
	global_load_dwordx4 v[168:171], v74, s[8:9]
	s_add_u32 s8, s8, 0x20000
	s_addc_u32 s9, s9, 0
	global_load_dwordx4 v[172:175], v74, s[8:9]
	s_mov_b64 s[6:7], s[36:37]
	ds_read_b32 v226, v211
	ds_read_b32 v227, v211 offset:512
	ds_read_b32 v228, v211 offset:1024
	ds_read_b32 v229, v211 offset:1536
	ds_read_b32 v230, v211 offset:2048
	ds_read_b32 v231, v211 offset:2560
	ds_read_b32 v232, v211 offset:3072
	ds_read_b32 v233, v211 offset:3584
	ds_read_b32 v234, v211 offset:4096
	ds_read_b32 v235, v211 offset:4608
	ds_read_b32 v236, v211 offset:5120
	ds_read_b32 v237, v211 offset:5632
	ds_read_b32 v238, v211 offset:6144
	ds_read_b32 v239, v211 offset:6656
	ds_read_b32 v240, v211 offset:7168
	ds_read_b32 v241, v211 offset:7680
	s_waitcnt lgkmcnt(0)
	v_max_f32_e32 v226, v226, v226
	v_max_f32_e32 v227, v227, v227
	v_max_f32_e32 v228, v228, v228
	v_max_f32_e32 v229, v229, v229
	v_max_f32_e32 v230, v230, v230
	v_max_f32_e32 v231, v231, v231
	v_max_f32_e32 v232, v232, v232
	v_max_f32_e32 v233, v233, v233
	v_max_f32_e32 v234, v234, v234
	v_max_f32_e32 v235, v235, v235
	v_max_f32_e32 v236, v236, v236
	v_max_f32_e32 v237, v237, v237
	v_max_f32_e32 v238, v238, v238
	v_max_f32_e32 v239, v239, v239
	v_max_f32_e32 v240, v240, v240
	v_max_f32_e32 v241, v241, v241
	v_med3_f32 v226, v226, s62, v95
	v_med3_f32 v227, v227, s62, v95
	v_med3_f32 v228, v228, s62, v95
	v_med3_f32 v229, v229, s62, v95
	v_med3_f32 v230, v230, s62, v95
	v_med3_f32 v231, v231, s62, v95
	v_med3_f32 v232, v232, s62, v95
	v_med3_f32 v233, v233, s62, v95
	v_med3_f32 v234, v234, s62, v95
	v_med3_f32 v235, v235, s62, v95
	v_med3_f32 v236, v236, s62, v95
	v_med3_f32 v237, v237, s62, v95
	v_med3_f32 v238, v238, s62, v95
	v_med3_f32 v239, v239, s62, v95
	v_med3_f32 v240, v240, s62, v95
	v_med3_f32 v241, v241, s62, v95
	v_mov_b32_e32 v242, 0
	v_mov_b32_e32 v243, 0
	v_mov_b32_e32 v244, 0
	v_mov_b32_e32 v245, 0
	v_cvt_pk_fp8_f32 v242, v226, v227
	v_cvt_pk_fp8_f32 v243, v230, v231
	v_cvt_pk_fp8_f32 v244, v234, v235
	v_cvt_pk_fp8_f32 v245, v238, v239
	v_cvt_pk_fp8_f32 v242, v228, v229 op_sel:[0,0,1]
	v_cvt_pk_fp8_f32 v243, v232, v233 op_sel:[0,0,1]
	v_cvt_pk_fp8_f32 v244, v236, v237 op_sel:[0,0,1]
	v_cvt_pk_fp8_f32 v245, v240, v241 op_sel:[0,0,1]
	s_nop 0
	global_store_dwordx4 v77, v[242:245], s[6:7]
	ds_read_b32 v226, v213
	ds_read_b32 v227, v213 offset:512
	ds_read_b32 v228, v213 offset:1024
	ds_read_b32 v229, v213 offset:1536
	ds_read_b32 v230, v213 offset:2048
	ds_read_b32 v231, v213 offset:2560
	ds_read_b32 v232, v213 offset:3072
	ds_read_b32 v233, v213 offset:3584
	ds_read_b32 v234, v213 offset:4096
	ds_read_b32 v235, v213 offset:4608
	ds_read_b32 v236, v213 offset:5120
	ds_read_b32 v237, v213 offset:5632
	ds_read_b32 v238, v213 offset:6144
	ds_read_b32 v239, v213 offset:6656
	ds_read_b32 v240, v213 offset:7168
	ds_read_b32 v241, v213 offset:7680
	s_waitcnt lgkmcnt(0)
	v_max_f32_e32 v226, v226, v226
	v_max_f32_e32 v227, v227, v227
	v_max_f32_e32 v228, v228, v228
	v_max_f32_e32 v229, v229, v229
	v_max_f32_e32 v230, v230, v230
	v_max_f32_e32 v231, v231, v231
	v_max_f32_e32 v232, v232, v232
	v_max_f32_e32 v233, v233, v233
	v_max_f32_e32 v234, v234, v234
	v_max_f32_e32 v235, v235, v235
	v_max_f32_e32 v236, v236, v236
	v_max_f32_e32 v237, v237, v237
	v_max_f32_e32 v238, v238, v238
	v_max_f32_e32 v239, v239, v239
	v_max_f32_e32 v240, v240, v240
	v_max_f32_e32 v241, v241, v241
	v_med3_f32 v226, v226, s62, v95
	v_med3_f32 v227, v227, s62, v95
	v_med3_f32 v228, v228, s62, v95
	v_med3_f32 v229, v229, s62, v95
	v_med3_f32 v230, v230, s62, v95
	v_med3_f32 v231, v231, s62, v95
	v_med3_f32 v232, v232, s62, v95
	v_med3_f32 v233, v233, s62, v95
	v_med3_f32 v234, v234, s62, v95
	v_med3_f32 v235, v235, s62, v95
	v_med3_f32 v236, v236, s62, v95
	v_med3_f32 v237, v237, s62, v95
	v_med3_f32 v238, v238, s62, v95
	v_med3_f32 v239, v239, s62, v95
	v_med3_f32 v240, v240, s62, v95
	v_med3_f32 v241, v241, s62, v95
	v_mov_b32_e32 v242, 0
	v_mov_b32_e32 v243, 0
	v_mov_b32_e32 v244, 0
	v_mov_b32_e32 v245, 0
	v_cvt_pk_fp8_f32 v242, v226, v227
	v_cvt_pk_fp8_f32 v243, v230, v231
	v_cvt_pk_fp8_f32 v244, v234, v235
	v_cvt_pk_fp8_f32 v245, v238, v239
	v_cvt_pk_fp8_f32 v242, v228, v229 op_sel:[0,0,1]
	v_cvt_pk_fp8_f32 v243, v232, v233 op_sel:[0,0,1]
	v_cvt_pk_fp8_f32 v244, v236, v237 op_sel:[0,0,1]
	v_cvt_pk_fp8_f32 v245, v240, v241 op_sel:[0,0,1]
	s_nop 0
	global_store_dwordx4 v78, v[242:245], s[6:7]
	s_waitcnt vmcnt(12)
	v_mul_f32_e32 v176, v34, v176
	v_mul_f32_e32 v177, v34, v177
	v_mul_f32_e32 v178, v34, v178
	v_mul_f32_e32 v179, v34, v179
	ds_write_b128 v210, v[176:179]
	v_mul_f32_e32 v180, v35, v180
	v_mul_f32_e32 v181, v35, v181
	v_mul_f32_e32 v182, v35, v182
	v_mul_f32_e32 v183, v35, v183
	ds_write_b128 v210, v[180:183] offset:1024
	v_mul_f32_e32 v184, v36, v184
	v_mul_f32_e32 v185, v36, v185
	v_mul_f32_e32 v186, v36, v186
	v_mul_f32_e32 v187, v36, v187
	ds_write_b128 v210, v[184:187] offset:2048
	v_mul_f32_e32 v188, v37, v188
	v_mul_f32_e32 v189, v37, v189
	v_mul_f32_e32 v190, v37, v190
	v_mul_f32_e32 v191, v37, v191
	ds_write_b128 v210, v[188:191] offset:3072
	v_mul_f32_e32 v192, v38, v192
	v_mul_f32_e32 v193, v38, v193
	v_mul_f32_e32 v194, v38, v194
	v_mul_f32_e32 v195, v38, v195
	ds_write_b128 v210, v[192:195] offset:4096
	v_mul_f32_e32 v196, v39, v196
	v_mul_f32_e32 v197, v39, v197
	v_mul_f32_e32 v198, v39, v198
	v_mul_f32_e32 v199, v39, v199
	ds_write_b128 v210, v[196:199] offset:5120
	v_mul_f32_e32 v200, v40, v200
	v_mul_f32_e32 v201, v40, v201
	v_mul_f32_e32 v202, v40, v202
	v_mul_f32_e32 v203, v40, v203
	ds_write_b128 v210, v[200:203] offset:6144
	v_mul_f32_e32 v204, v41, v204
	v_mul_f32_e32 v205, v41, v205
	v_mul_f32_e32 v206, v41, v206
	v_mul_f32_e32 v207, v41, v207
	ds_write_b128 v210, v[204:207] offset:7168
	s_waitcnt lgkmcnt(0)
	s_barrier
; #define GAS __attribute__((address_space(1)))
; #define LAS __attribute__((address_space(3)))
; #define LDS_WAIT() asm volatile("s_waitcnt lgkmcnt(0)" ::: "memory")
; __device__ __forceinline__ unsigned pk4_fp8(float a, float b, float c, float d) {
;     a = fminf(fmaxf(a, -448.f), 448.f); b = fminf(fmaxf(b, -448.f), 448.f); c = fminf(fmaxf(c, -448.f), 448.f); d = fminf(fmaxf(d, -448.f), 448.f);
;     int w = __builtin_amdgcn_cvt_pk_fp8_f32(a, b, 0, false); w = __builtin_amdgcn_cvt_pk_fp8_f32(c, d, w, true); return (unsigned)w; }
;     const int pr = item >> 1, kb = 2 * (pr / nblk) + (item & 1), nb = pr % nblk, k0 = 64 * kb, n0 = 32 * nb;
;     const int nr = n0 + (lane & 31); const int sc = MAP == 1 ? src_col_in(nr) : nr;
;     float v[32];
; #pragma unroll
;     for (int i = 0; i < 32; ++i) v[i] = sc >= 0 ? W[(size_t)(k0 + 2 * i + (lane >> 5)) * Nsrc + sc] : 0.f;
; #pragma unroll
;     for (int i = 0; i < 32; ++i) { const int k = k0 + 2 * i + (lane >> 5); float x = v[i] * wscale; if (KS) x *= (k < ksplit ? ksA[k] : ksB[k - ksplit]); scr[(2 * i + (lane >> 5)) * 33 + (lane & 31)] = x; }
;     LDS_WAIT(); asm volatile("" ::: "memory");
;     const int c = lane & 7;
; #pragma unroll
;     for (int j = 0; j < 4; ++j) { const int n = (lane >> 3) + 8 * j; const LAS float* s = scr + (8 * c) * 33 + n;
;         const unsigned long long o = (unsigned long long)pg8::pk4_fp8(s[0 * 33], s[1 * 33], s[2 * 33], s[3 * 33]) | ((unsigned long long)pg8::pk4_fp8(s[4 * 33], s[5 * 33], s[6 * 33], s[7 * 33]) << 32);
;         *(GAS unsigned long long*)(WT + (size_t)(n0 + n) * K + k0 + 8 * c) = o; }
;     LDS_WAIT(); asm volatile("" ::: "memory");
; }
	s_add_u32 s8, s34, 0x3000
	s_addc_u32 s9, s35, 0
	global_load_dwordx4 v[176:179], v74, s[8:9]
	s_add_u32 s8, s8, 0x20000
	s_addc_u32 s9, s9, 0
	global_load_dwordx4 v[180:183], v74, s[8:9]
	s_add_u32 s8, s8, 0x20000
	s_addc_u32 s9, s9, 0
	global_load_dwordx4 v[184:187], v74, s[8:9]
	s_add_u32 s8, s8, 0x20000
	s_addc_u32 s9, s9, 0
	global_load_dwordx4 v[188:191], v74, s[8:9]
	s_add_u32 s8, s8, 0x20000
	s_addc_u32 s9, s9, 0
	global_load_dwordx4 v[192:195], v74, s[8:9]
	s_add_u32 s8, s8, 0x20000
	s_addc_u32 s9, s9, 0
	global_load_dwordx4 v[196:199], v74, s[8:9]
	s_add_u32 s8, s8, 0x20000
	s_addc_u32 s9, s9, 0
	global_load_dwordx4 v[200:203], v74, s[8:9]
	s_add_u32 s8, s8, 0x20000
	s_addc_u32 s9, s9, 0
	global_load_dwordx4 v[204:207], v74, s[8:9]
	s_add_u32 s6, s36, 0x400000
	s_addc_u32 s7, s37, 0
	ds_read_b32 v226, v212
	ds_read_b32 v227, v212 offset:512
	ds_read_b32 v228, v212 offset:1024
	ds_read_b32 v229, v212 offset:1536
	ds_read_b32 v230, v212 offset:2048
	ds_read_b32 v231, v212 offset:2560
	ds_read_b32 v232, v212 offset:3072
	ds_read_b32 v233, v212 offset:3584
	ds_read_b32 v234, v212 offset:4096
	ds_read_b32 v235, v212 offset:4608
	ds_read_b32 v236, v212 offset:5120
	ds_read_b32 v237, v212 offset:5632
	ds_read_b32 v238, v212 offset:6144
	ds_read_b32 v239, v212 offset:6656
	ds_read_b32 v240, v212 offset:7168
	ds_read_b32 v241, v212 offset:7680
	s_waitcnt lgkmcnt(0)
	v_max_f32_e32 v226, v226, v226
	v_max_f32_e32 v227, v227, v227
	v_max_f32_e32 v228, v228, v228
	v_max_f32_e32 v229, v229, v229
	v_max_f32_e32 v230, v230, v230
	v_max_f32_e32 v231, v231, v231
	v_max_f32_e32 v232, v232, v232
	v_max_f32_e32 v233, v233, v233
	v_max_f32_e32 v234, v234, v234
	v_max_f32_e32 v235, v235, v235
	v_max_f32_e32 v236, v236, v236
	v_max_f32_e32 v237, v237, v237
	v_max_f32_e32 v238, v238, v238
	v_max_f32_e32 v239, v239, v239
	v_max_f32_e32 v240, v240, v240
	v_max_f32_e32 v241, v241, v241
	v_med3_f32 v226, v226, s62, v95
	v_med3_f32 v227, v227, s62, v95
	v_med3_f32 v228, v228, s62, v95
	v_med3_f32 v229, v229, s62, v95
	v_med3_f32 v230, v230, s62, v95
	v_med3_f32 v231, v231, s62, v95
	v_med3_f32 v232, v232, s62, v95
	v_med3_f32 v233, v233, s62, v95
	v_med3_f32 v234, v234, s62, v95
	v_med3_f32 v235, v235, s62, v95
	v_med3_f32 v236, v236, s62, v95
	v_med3_f32 v237, v237, s62, v95
	v_med3_f32 v238, v238, s62, v95
	v_med3_f32 v239, v239, s62, v95
	v_med3_f32 v240, v240, s62, v95
	v_med3_f32 v241, v241, s62, v95
	v_mov_b32_e32 v242, 0
	v_mov_b32_e32 v243, 0
	v_mov_b32_e32 v244, 0
	v_mov_b32_e32 v245, 0
	v_cvt_pk_fp8_f32 v242, v226, v227
	v_cvt_pk_fp8_f32 v243, v230, v231
	v_cvt_pk_fp8_f32 v244, v234, v235
	v_cvt_pk_fp8_f32 v245, v238, v239
	v_cvt_pk_fp8_f32 v242, v228, v229 op_sel:[0,0,1]
	v_cvt_pk_fp8_f32 v243, v232, v233 op_sel:[0,0,1]
	v_cvt_pk_fp8_f32 v244, v236, v237 op_sel:[0,0,1]
	v_cvt_pk_fp8_f32 v245, v240, v241 op_sel:[0,0,1]
	s_nop 0
	global_store_dwordx4 v77, v[242:245], s[6:7]
	ds_read_b32 v226, v214
	ds_read_b32 v227, v214 offset:512
	ds_read_b32 v228, v214 offset:1024
	ds_read_b32 v229, v214 offset:1536
	ds_read_b32 v230, v214 offset:2048
	ds_read_b32 v231, v214 offset:2560
	ds_read_b32 v232, v214 offset:3072
	ds_read_b32 v233, v214 offset:3584
	ds_read_b32 v234, v214 offset:4096
	ds_read_b32 v235, v214 offset:4608
	ds_read_b32 v236, v214 offset:5120
	ds_read_b32 v237, v214 offset:5632
	ds_read_b32 v238, v214 offset:6144
	ds_read_b32 v239, v214 offset:6656
	ds_read_b32 v240, v214 offset:7168
	ds_read_b32 v241, v214 offset:7680
	s_waitcnt lgkmcnt(0)
	v_max_f32_e32 v226, v226, v226
	v_max_f32_e32 v227, v227, v227
	v_max_f32_e32 v228, v228, v228
	v_max_f32_e32 v229, v229, v229
	v_max_f32_e32 v230, v230, v230
	v_max_f32_e32 v231, v231, v231
	v_max_f32_e32 v232, v232, v232
	v_max_f32_e32 v233, v233, v233
	v_max_f32_e32 v234, v234, v234
	v_max_f32_e32 v235, v235, v235
	v_max_f32_e32 v236, v236, v236
	v_max_f32_e32 v237, v237, v237
	v_max_f32_e32 v238, v238, v238
	v_max_f32_e32 v239, v239, v239
	v_max_f32_e32 v240, v240, v240
	v_max_f32_e32 v241, v241, v241
	v_med3_f32 v226, v226, s62, v95
	v_med3_f32 v227, v227, s62, v95
	v_med3_f32 v228, v228, s62, v95
	v_med3_f32 v229, v229, s62, v95
	v_med3_f32 v230, v230, s62, v95
	v_med3_f32 v231, v231, s62, v95
	v_med3_f32 v232, v232, s62, v95
	v_med3_f32 v233, v233, s62, v95
	v_med3_f32 v234, v234, s62, v95
	v_med3_f32 v235, v235, s62, v95
	v_med3_f32 v236, v236, s62, v95
	v_med3_f32 v237, v237, s62, v95
	v_med3_f32 v238, v238, s62, v95
	v_med3_f32 v239, v239, s62, v95
	v_med3_f32 v240, v240, s62, v95
	v_med3_f32 v241, v241, s62, v95
	v_mov_b32_e32 v242, 0
	v_mov_b32_e32 v243, 0
	v_mov_b32_e32 v244, 0
	v_mov_b32_e32 v245, 0
	v_cvt_pk_fp8_f32 v242, v226, v227
	v_cvt_pk_fp8_f32 v243, v230, v231
	v_cvt_pk_fp8_f32 v244, v234, v235
	v_cvt_pk_fp8_f32 v245, v238, v239
	v_cvt_pk_fp8_f32 v242, v228, v229 op_sel:[0,0,1]
	v_cvt_pk_fp8_f32 v243, v232, v233 op_sel:[0,0,1]
	v_cvt_pk_fp8_f32 v244, v236, v237 op_sel:[0,0,1]
	v_cvt_pk_fp8_f32 v245, v240, v241 op_sel:[0,0,1]
	s_nop 0
	global_store_dwordx4 v78, v[242:245], s[6:7]
	s_waitcnt vmcnt(12)
	v_mul_f32_e32 v144, v34, v144
	v_mul_f32_e32 v145, v34, v145
	v_mul_f32_e32 v146, v34, v146
	v_mul_f32_e32 v147, v34, v147
	ds_write_b128 v209, v[144:147]
	v_mul_f32_e32 v148, v35, v148
	v_mul_f32_e32 v149, v35, v149
	v_mul_f32_e32 v150, v35, v150
	v_mul_f32_e32 v151, v35, v151
	ds_write_b128 v209, v[148:151] offset:1024
	v_mul_f32_e32 v152, v36, v152
	v_mul_f32_e32 v153, v36, v153
	v_mul_f32_e32 v154, v36, v154
	v_mul_f32_e32 v155, v36, v155
	ds_write_b128 v209, v[152:155] offset:2048
	v_mul_f32_e32 v156, v37, v156
	v_mul_f32_e32 v157, v37, v157
	v_mul_f32_e32 v158, v37, v158
	v_mul_f32_e32 v159, v37, v159
	ds_write_b128 v209, v[156:159] offset:3072
	v_mul_f32_e32 v160, v38, v160
	v_mul_f32_e32 v161, v38, v161
	v_mul_f32_e32 v162, v38, v162
	v_mul_f32_e32 v163, v38, v163
	ds_write_b128 v209, v[160:163] offset:4096
	v_mul_f32_e32 v164, v39, v164
	v_mul_f32_e32 v165, v39, v165
	v_mul_f32_e32 v166, v39, v166
	v_mul_f32_e32 v167, v39, v167
	ds_write_b128 v209, v[164:167] offset:5120
	v_mul_f32_e32 v168, v40, v168
	v_mul_f32_e32 v169, v40, v169
	v_mul_f32_e32 v170, v40, v170
	v_mul_f32_e32 v171, v40, v171
	ds_write_b128 v209, v[168:171] offset:6144
	v_mul_f32_e32 v172, v41, v172
	v_mul_f32_e32 v173, v41, v173
	v_mul_f32_e32 v174, v41, v174
	v_mul_f32_e32 v175, v41, v175
	ds_write_b128 v209, v[172:175] offset:7168
	s_waitcnt lgkmcnt(0)
	s_barrier
; #define GAS __attribute__((address_space(1)))
; #define LAS __attribute__((address_space(3)))
; #define LDS_WAIT() asm volatile("s_waitcnt lgkmcnt(0)" ::: "memory")
; __device__ __forceinline__ unsigned pk4_fp8(float a, float b, float c, float d) {
;     a = fminf(fmaxf(a, -448.f), 448.f); b = fminf(fmaxf(b, -448.f), 448.f); c = fminf(fmaxf(c, -448.f), 448.f); d = fminf(fmaxf(d, -448.f), 448.f);
;     int w = __builtin_amdgcn_cvt_pk_fp8_f32(a, b, 0, false); w = __builtin_amdgcn_cvt_pk_fp8_f32(c, d, w, true); return (unsigned)w; }
;     const int pr = item >> 1, kb = 2 * (pr / nblk) + (item & 1), nb = pr % nblk, k0 = 64 * kb, n0 = 32 * nb;
;     const int nr = n0 + (lane & 31); const int sc = MAP == 1 ? src_col_in(nr) : nr;
;     float v[32];
; #pragma unroll
;     for (int i = 0; i < 32; ++i) v[i] = sc >= 0 ? W[(size_t)(k0 + 2 * i + (lane >> 5)) * Nsrc + sc] : 0.f;
; #pragma unroll
;     for (int i = 0; i < 32; ++i) { const int k = k0 + 2 * i + (lane >> 5); float x = v[i] * wscale; if (KS) x *= (k < ksplit ? ksA[k] : ksB[k - ksplit]); scr[(2 * i + (lane >> 5)) * 33 + (lane & 31)] = x; }
;     LDS_WAIT(); asm volatile("" ::: "memory");
;     const int c = lane & 7;
; #pragma unroll
;     for (int j = 0; j < 4; ++j) { const int n = (lane >> 3) + 8 * j; const LAS float* s = scr + (8 * c) * 33 + n;
;         const unsigned long long o = (unsigned long long)pg8::pk4_fp8(s[0 * 33], s[1 * 33], s[2 * 33], s[3 * 33]) | ((unsigned long long)pg8::pk4_fp8(s[4 * 33], s[5 * 33], s[6 * 33], s[7 * 33]) << 32);
;         *(GAS unsigned long long*)(WT + (size_t)(n0 + n) * K + k0 + 8 * c) = o; }
;     LDS_WAIT(); asm volatile("" ::: "memory");
; }
	s_add_u32 s8, s34, 0x4000
	s_addc_u32 s9, s35, 0
	global_load_dwordx4 v[144:147], v74, s[8:9]
	s_add_u32 s8, s8, 0x20000
	s_addc_u32 s9, s9, 0
	global_load_dwordx4 v[148:151], v74, s[8:9]
	s_add_u32 s8, s8, 0x20000
	s_addc_u32 s9, s9, 0
	global_load_dwordx4 v[152:155], v74, s[8:9]
	s_add_u32 s8, s8, 0x20000
	s_addc_u32 s9, s9, 0
	global_load_dwordx4 v[156:159], v74, s[8:9]
	s_add_u32 s8, s8, 0x20000
	s_addc_u32 s9, s9, 0
	global_load_dwordx4 v[160:163], v74, s[8:9]
	s_add_u32 s8, s8, 0x20000
	s_addc_u32 s9, s9, 0
	global_load_dwordx4 v[164:167], v74, s[8:9]
	s_add_u32 s8, s8, 0x20000
	s_addc_u32 s9, s9, 0
	global_load_dwordx4 v[168:171], v74, s[8:9]
	s_add_u32 s8, s8, 0x20000
	s_addc_u32 s9, s9, 0
	global_load_dwordx4 v[172:175], v74, s[8:9]
	s_add_u32 s6, s36, 0x800000
	s_addc_u32 s7, s37, 0
	ds_read_b32 v226, v211
	ds_read_b32 v227, v211 offset:512
	ds_read_b32 v228, v211 offset:1024
	ds_read_b32 v229, v211 offset:1536
	ds_read_b32 v230, v211 offset:2048
	ds_read_b32 v231, v211 offset:2560
	ds_read_b32 v232, v211 offset:3072
	ds_read_b32 v233, v211 offset:3584
	ds_read_b32 v234, v211 offset:4096
	ds_read_b32 v235, v211 offset:4608
	ds_read_b32 v236, v211 offset:5120
	ds_read_b32 v237, v211 offset:5632
	ds_read_b32 v238, v211 offset:6144
	ds_read_b32 v239, v211 offset:6656
	ds_read_b32 v240, v211 offset:7168
	ds_read_b32 v241, v211 offset:7680
	s_waitcnt lgkmcnt(0)
	v_max_f32_e32 v226, v226, v226
	v_max_f32_e32 v227, v227, v227
	v_max_f32_e32 v228, v228, v228
	v_max_f32_e32 v229, v229, v229
	v_max_f32_e32 v230, v230, v230
	v_max_f32_e32 v231, v231, v231
	v_max_f32_e32 v232, v232, v232
	v_max_f32_e32 v233, v233, v233
	v_max_f32_e32 v234, v234, v234
	v_max_f32_e32 v235, v235, v235
	v_max_f32_e32 v236, v236, v236
	v_max_f32_e32 v237, v237, v237
	v_max_f32_e32 v238, v238, v238
	v_max_f32_e32 v239, v239, v239
	v_max_f32_e32 v240, v240, v240
	v_max_f32_e32 v241, v241, v241
	v_med3_f32 v226, v226, s62, v95
	v_med3_f32 v227, v227, s62, v95
	v_med3_f32 v228, v228, s62, v95
	v_med3_f32 v229, v229, s62, v95
	v_med3_f32 v230, v230, s62, v95
	v_med3_f32 v231, v231, s62, v95
	v_med3_f32 v232, v232, s62, v95
	v_med3_f32 v233, v233, s62, v95
	v_med3_f32 v234, v234, s62, v95
	v_med3_f32 v235, v235, s62, v95
	v_med3_f32 v236, v236, s62, v95
	v_med3_f32 v237, v237, s62, v95
	v_med3_f32 v238, v238, s62, v95
	v_med3_f32 v239, v239, s62, v95
	v_med3_f32 v240, v240, s62, v95
	v_med3_f32 v241, v241, s62, v95
	v_mov_b32_e32 v242, 0
	v_mov_b32_e32 v243, 0
	v_mov_b32_e32 v244, 0
	v_mov_b32_e32 v245, 0
	v_cvt_pk_fp8_f32 v242, v226, v227
	v_cvt_pk_fp8_f32 v243, v230, v231
	v_cvt_pk_fp8_f32 v244, v234, v235
	v_cvt_pk_fp8_f32 v245, v238, v239
	v_cvt_pk_fp8_f32 v242, v228, v229 op_sel:[0,0,1]
	v_cvt_pk_fp8_f32 v243, v232, v233 op_sel:[0,0,1]
	v_cvt_pk_fp8_f32 v244, v236, v237 op_sel:[0,0,1]
	v_cvt_pk_fp8_f32 v245, v240, v241 op_sel:[0,0,1]
	s_nop 0
	global_store_dwordx4 v77, v[242:245], s[6:7]
	ds_read_b32 v226, v213
	ds_read_b32 v227, v213 offset:512
	ds_read_b32 v228, v213 offset:1024
	ds_read_b32 v229, v213 offset:1536
	ds_read_b32 v230, v213 offset:2048
	ds_read_b32 v231, v213 offset:2560
	ds_read_b32 v232, v213 offset:3072
	ds_read_b32 v233, v213 offset:3584
	ds_read_b32 v234, v213 offset:4096
	ds_read_b32 v235, v213 offset:4608
	ds_read_b32 v236, v213 offset:5120
	ds_read_b32 v237, v213 offset:5632
	ds_read_b32 v238, v213 offset:6144
	ds_read_b32 v239, v213 offset:6656
	ds_read_b32 v240, v213 offset:7168
	ds_read_b32 v241, v213 offset:7680
	s_waitcnt lgkmcnt(0)
	v_max_f32_e32 v226, v226, v226
	v_max_f32_e32 v227, v227, v227
	v_max_f32_e32 v228, v228, v228
	v_max_f32_e32 v229, v229, v229
	v_max_f32_e32 v230, v230, v230
	v_max_f32_e32 v231, v231, v231
	v_max_f32_e32 v232, v232, v232
	v_max_f32_e32 v233, v233, v233
	v_max_f32_e32 v234, v234, v234
	v_max_f32_e32 v235, v235, v235
	v_max_f32_e32 v236, v236, v236
	v_max_f32_e32 v237, v237, v237
	v_max_f32_e32 v238, v238, v238
	v_max_f32_e32 v239, v239, v239
	v_max_f32_e32 v240, v240, v240
	v_max_f32_e32 v241, v241, v241
	v_med3_f32 v226, v226, s62, v95
	v_med3_f32 v227, v227, s62, v95
	v_med3_f32 v228, v228, s62, v95
	v_med3_f32 v229, v229, s62, v95
	v_med3_f32 v230, v230, s62, v95
	v_med3_f32 v231, v231, s62, v95
	v_med3_f32 v232, v232, s62, v95
	v_med3_f32 v233, v233, s62, v95
	v_med3_f32 v234, v234, s62, v95
	v_med3_f32 v235, v235, s62, v95
	v_med3_f32 v236, v236, s62, v95
	v_med3_f32 v237, v237, s62, v95
	v_med3_f32 v238, v238, s62, v95
	v_med3_f32 v239, v239, s62, v95
	v_med3_f32 v240, v240, s62, v95
	v_med3_f32 v241, v241, s62, v95
	v_mov_b32_e32 v242, 0
	v_mov_b32_e32 v243, 0
	v_mov_b32_e32 v244, 0
	v_mov_b32_e32 v245, 0
	v_cvt_pk_fp8_f32 v242, v226, v227
	v_cvt_pk_fp8_f32 v243, v230, v231
	v_cvt_pk_fp8_f32 v244, v234, v235
	v_cvt_pk_fp8_f32 v245, v238, v239
	v_cvt_pk_fp8_f32 v242, v228, v229 op_sel:[0,0,1]
	v_cvt_pk_fp8_f32 v243, v232, v233 op_sel:[0,0,1]
	v_cvt_pk_fp8_f32 v244, v236, v237 op_sel:[0,0,1]
	v_cvt_pk_fp8_f32 v245, v240, v241 op_sel:[0,0,1]
	s_nop 0
	global_store_dwordx4 v78, v[242:245], s[6:7]
	s_waitcnt vmcnt(12)
	v_mul_f32_e32 v176, v34, v176
	v_mul_f32_e32 v177, v34, v177
	v_mul_f32_e32 v178, v34, v178
	v_mul_f32_e32 v179, v34, v179
	ds_write_b128 v210, v[176:179]
	v_mul_f32_e32 v180, v35, v180
	v_mul_f32_e32 v181, v35, v181
	v_mul_f32_e32 v182, v35, v182
	v_mul_f32_e32 v183, v35, v183
	ds_write_b128 v210, v[180:183] offset:1024
	v_mul_f32_e32 v184, v36, v184
	v_mul_f32_e32 v185, v36, v185
	v_mul_f32_e32 v186, v36, v186
	v_mul_f32_e32 v187, v36, v187
	ds_write_b128 v210, v[184:187] offset:2048
	v_mul_f32_e32 v188, v37, v188
	v_mul_f32_e32 v189, v37, v189
	v_mul_f32_e32 v190, v37, v190
	v_mul_f32_e32 v191, v37, v191
	ds_write_b128 v210, v[188:191] offset:3072
	v_mul_f32_e32 v192, v38, v192
	v_mul_f32_e32 v193, v38, v193
	v_mul_f32_e32 v194, v38, v194
	v_mul_f32_e32 v195, v38, v195
	ds_write_b128 v210, v[192:195] offset:4096
	v_mul_f32_e32 v196, v39, v196
	v_mul_f32_e32 v197, v39, v197
	v_mul_f32_e32 v198, v39, v198
	v_mul_f32_e32 v199, v39, v199
	ds_write_b128 v210, v[196:199] offset:5120
	v_mul_f32_e32 v200, v40, v200
	v_mul_f32_e32 v201, v40, v201
	v_mul_f32_e32 v202, v40, v202
	v_mul_f32_e32 v203, v40, v203
	ds_write_b128 v210, v[200:203] offset:6144
	v_mul_f32_e32 v204, v41, v204
	v_mul_f32_e32 v205, v41, v205
	v_mul_f32_e32 v206, v41, v206
	v_mul_f32_e32 v207, v41, v207
	ds_write_b128 v210, v[204:207] offset:7168
	s_waitcnt lgkmcnt(0)
	s_barrier
; #define GAS __attribute__((address_space(1)))
; #define LAS __attribute__((address_space(3)))
; #define LDS_WAIT() asm volatile("s_waitcnt lgkmcnt(0)" ::: "memory")
; __device__ __forceinline__ unsigned pk4_fp8(float a, float b, float c, float d) {
;     a = fminf(fmaxf(a, -448.f), 448.f); b = fminf(fmaxf(b, -448.f), 448.f); c = fminf(fmaxf(c, -448.f), 448.f); d = fminf(fmaxf(d, -448.f), 448.f);
;     int w = __builtin_amdgcn_cvt_pk_fp8_f32(a, b, 0, false); w = __builtin_amdgcn_cvt_pk_fp8_f32(c, d, w, true); return (unsigned)w; }
;     const int pr = item >> 1, kb = 2 * (pr / nblk) + (item & 1), nb = pr % nblk, k0 = 64 * kb, n0 = 32 * nb;
;     const int nr = n0 + (lane & 31); const int sc = MAP == 1 ? src_col_in(nr) : nr;
;     float v[32];
; #pragma unroll
;     for (int i = 0; i < 32; ++i) v[i] = sc >= 0 ? W[(size_t)(k0 + 2 * i + (lane >> 5)) * Nsrc + sc] : 0.f;
; #pragma unroll
;     for (int i = 0; i < 32; ++i) { const int k = k0 + 2 * i + (lane >> 5); float x = v[i] * wscale; if (KS) x *= (k < ksplit ? ksA[k] : ksB[k - ksplit]); scr[(2 * i + (lane >> 5)) * 33 + (lane & 31)] = x; }
;     LDS_WAIT(); asm volatile("" ::: "memory");
;     const int c = lane & 7;
; #pragma unroll
;     for (int j = 0; j < 4; ++j) { const int n = (lane >> 3) + 8 * j; const LAS float* s = scr + (8 * c) * 33 + n;
;         const unsigned long long o = (unsigned long long)pg8::pk4_fp8(s[0 * 33], s[1 * 33], s[2 * 33], s[3 * 33]) | ((unsigned long long)pg8::pk4_fp8(s[4 * 33], s[5 * 33], s[6 * 33], s[7 * 33]) << 32);
;         *(GAS unsigned long long*)(WT + (size_t)(n0 + n) * K + k0 + 8 * c) = o; }
;     LDS_WAIT(); asm volatile("" ::: "memory");
; }
	s_add_u32 s8, s34, 0x5000
	s_addc_u32 s9, s35, 0
	global_load_dwordx4 v[176:179], v74, s[8:9]
	s_add_u32 s8, s8, 0x20000
	s_addc_u32 s9, s9, 0
	global_load_dwordx4 v[180:183], v74, s[8:9]
	s_add_u32 s8, s8, 0x20000
	s_addc_u32 s9, s9, 0
	global_load_dwordx4 v[184:187], v74, s[8:9]
	s_add_u32 s8, s8, 0x20000
	s_addc_u32 s9, s9, 0
	global_load_dwordx4 v[188:191], v74, s[8:9]
	s_add_u32 s8, s8, 0x20000
	s_addc_u32 s9, s9, 0
	global_load_dwordx4 v[192:195], v74, s[8:9]
	s_add_u32 s8, s8, 0x20000
	s_addc_u32 s9, s9, 0
	global_load_dwordx4 v[196:199], v74, s[8:9]
	s_add_u32 s8, s8, 0x20000
	s_addc_u32 s9, s9, 0
	global_load_dwordx4 v[200:203], v74, s[8:9]
	s_add_u32 s8, s8, 0x20000
	s_addc_u32 s9, s9, 0
	global_load_dwordx4 v[204:207], v74, s[8:9]
	s_add_u32 s6, s36, 0xc00000
	s_addc_u32 s7, s37, 0
	ds_read_b32 v226, v212
	ds_read_b32 v227, v212 offset:512
	ds_read_b32 v228, v212 offset:1024
	ds_read_b32 v229, v212 offset:1536
	ds_read_b32 v230, v212 offset:2048
	ds_read_b32 v231, v212 offset:2560
	ds_read_b32 v232, v212 offset:3072
	ds_read_b32 v233, v212 offset:3584
	ds_read_b32 v234, v212 offset:4096
	ds_read_b32 v235, v212 offset:4608
	ds_read_b32 v236, v212 offset:5120
	ds_read_b32 v237, v212 offset:5632
	ds_read_b32 v238, v212 offset:6144
	ds_read_b32 v239, v212 offset:6656
	ds_read_b32 v240, v212 offset:7168
	ds_read_b32 v241, v212 offset:7680
	s_waitcnt lgkmcnt(0)
	v_max_f32_e32 v226, v226, v226
	v_max_f32_e32 v227, v227, v227
	v_max_f32_e32 v228, v228, v228
	v_max_f32_e32 v229, v229, v229
	v_max_f32_e32 v230, v230, v230
	v_max_f32_e32 v231, v231, v231
	v_max_f32_e32 v232, v232, v232
	v_max_f32_e32 v233, v233, v233
	v_max_f32_e32 v234, v234, v234
	v_max_f32_e32 v235, v235, v235
	v_max_f32_e32 v236, v236, v236
	v_max_f32_e32 v237, v237, v237
	v_max_f32_e32 v238, v238, v238
	v_max_f32_e32 v239, v239, v239
	v_max_f32_e32 v240, v240, v240
	v_max_f32_e32 v241, v241, v241
	v_med3_f32 v226, v226, s62, v95
	v_med3_f32 v227, v227, s62, v95
	v_med3_f32 v228, v228, s62, v95
	v_med3_f32 v229, v229, s62, v95
	v_med3_f32 v230, v230, s62, v95
	v_med3_f32 v231, v231, s62, v95
	v_med3_f32 v232, v232, s62, v95
	v_med3_f32 v233, v233, s62, v95
	v_med3_f32 v234, v234, s62, v95
	v_med3_f32 v235, v235, s62, v95
	v_med3_f32 v236, v236, s62, v95
	v_med3_f32 v237, v237, s62, v95
	v_med3_f32 v238, v238, s62, v95
	v_med3_f32 v239, v239, s62, v95
	v_med3_f32 v240, v240, s62, v95
	v_med3_f32 v241, v241, s62, v95
	v_mov_b32_e32 v242, 0
	v_mov_b32_e32 v243, 0
	v_mov_b32_e32 v244, 0
	v_mov_b32_e32 v245, 0
	v_cvt_pk_fp8_f32 v242, v226, v227
	v_cvt_pk_fp8_f32 v243, v230, v231
	v_cvt_pk_fp8_f32 v244, v234, v235
	v_cvt_pk_fp8_f32 v245, v238, v239
	v_cvt_pk_fp8_f32 v242, v228, v229 op_sel:[0,0,1]
	v_cvt_pk_fp8_f32 v243, v232, v233 op_sel:[0,0,1]
	v_cvt_pk_fp8_f32 v244, v236, v237 op_sel:[0,0,1]
	v_cvt_pk_fp8_f32 v245, v240, v241 op_sel:[0,0,1]
	s_nop 0
	global_store_dwordx4 v77, v[242:245], s[6:7]
	ds_read_b32 v226, v214
	ds_read_b32 v227, v214 offset:512
	ds_read_b32 v228, v214 offset:1024
	ds_read_b32 v229, v214 offset:1536
	ds_read_b32 v230, v214 offset:2048
	ds_read_b32 v231, v214 offset:2560
	ds_read_b32 v232, v214 offset:3072
	ds_read_b32 v233, v214 offset:3584
	ds_read_b32 v234, v214 offset:4096
	ds_read_b32 v235, v214 offset:4608
	ds_read_b32 v236, v214 offset:5120
	ds_read_b32 v237, v214 offset:5632
	ds_read_b32 v238, v214 offset:6144
	ds_read_b32 v239, v214 offset:6656
	ds_read_b32 v240, v214 offset:7168
	ds_read_b32 v241, v214 offset:7680
	s_waitcnt lgkmcnt(0)
	v_max_f32_e32 v226, v226, v226
	v_max_f32_e32 v227, v227, v227
	v_max_f32_e32 v228, v228, v228
	v_max_f32_e32 v229, v229, v229
	v_max_f32_e32 v230, v230, v230
	v_max_f32_e32 v231, v231, v231
	v_max_f32_e32 v232, v232, v232
	v_max_f32_e32 v233, v233, v233
	v_max_f32_e32 v234, v234, v234
	v_max_f32_e32 v235, v235, v235
	v_max_f32_e32 v236, v236, v236
	v_max_f32_e32 v237, v237, v237
	v_max_f32_e32 v238, v238, v238
	v_max_f32_e32 v239, v239, v239
	v_max_f32_e32 v240, v240, v240
	v_max_f32_e32 v241, v241, v241
	v_med3_f32 v226, v226, s62, v95
	v_med3_f32 v227, v227, s62, v95
	v_med3_f32 v228, v228, s62, v95
	v_med3_f32 v229, v229, s62, v95
	v_med3_f32 v230, v230, s62, v95
	v_med3_f32 v231, v231, s62, v95
	v_med3_f32 v232, v232, s62, v95
	v_med3_f32 v233, v233, s62, v95
	v_med3_f32 v234, v234, s62, v95
	v_med3_f32 v235, v235, s62, v95
	v_med3_f32 v236, v236, s62, v95
	v_med3_f32 v237, v237, s62, v95
	v_med3_f32 v238, v238, s62, v95
	v_med3_f32 v239, v239, s62, v95
	v_med3_f32 v240, v240, s62, v95
	v_med3_f32 v241, v241, s62, v95
	v_mov_b32_e32 v242, 0
	v_mov_b32_e32 v243, 0
	v_mov_b32_e32 v244, 0
	v_mov_b32_e32 v245, 0
	v_cvt_pk_fp8_f32 v242, v226, v227
	v_cvt_pk_fp8_f32 v243, v230, v231
	v_cvt_pk_fp8_f32 v244, v234, v235
	v_cvt_pk_fp8_f32 v245, v238, v239
	v_cvt_pk_fp8_f32 v242, v228, v229 op_sel:[0,0,1]
	v_cvt_pk_fp8_f32 v243, v232, v233 op_sel:[0,0,1]
	v_cvt_pk_fp8_f32 v244, v236, v237 op_sel:[0,0,1]
	v_cvt_pk_fp8_f32 v245, v240, v241 op_sel:[0,0,1]
	s_nop 0
	global_store_dwordx4 v78, v[242:245], s[6:7]
	s_waitcnt vmcnt(12)
	v_mul_f32_e32 v144, v34, v144
	v_mul_f32_e32 v145, v34, v145
	v_mul_f32_e32 v146, v34, v146
	v_mul_f32_e32 v147, v34, v147
	ds_write_b128 v209, v[144:147]
	v_mul_f32_e32 v148, v35, v148
	v_mul_f32_e32 v149, v35, v149
	v_mul_f32_e32 v150, v35, v150
	v_mul_f32_e32 v151, v35, v151
	ds_write_b128 v209, v[148:151] offset:1024
	v_mul_f32_e32 v152, v36, v152
	v_mul_f32_e32 v153, v36, v153
	v_mul_f32_e32 v154, v36, v154
	v_mul_f32_e32 v155, v36, v155
	ds_write_b128 v209, v[152:155] offset:2048
	v_mul_f32_e32 v156, v37, v156
	v_mul_f32_e32 v157, v37, v157
	v_mul_f32_e32 v158, v37, v158
	v_mul_f32_e32 v159, v37, v159
	ds_write_b128 v209, v[156:159] offset:3072
	v_mul_f32_e32 v160, v38, v160
	v_mul_f32_e32 v161, v38, v161
	v_mul_f32_e32 v162, v38, v162
	v_mul_f32_e32 v163, v38, v163
	ds_write_b128 v209, v[160:163] offset:4096
	v_mul_f32_e32 v164, v39, v164
	v_mul_f32_e32 v165, v39, v165
	v_mul_f32_e32 v166, v39, v166
	v_mul_f32_e32 v167, v39, v167
	ds_write_b128 v209, v[164:167] offset:5120
	v_mul_f32_e32 v168, v40, v168
	v_mul_f32_e32 v169, v40, v169
	v_mul_f32_e32 v170, v40, v170
	v_mul_f32_e32 v171, v40, v171
	ds_write_b128 v209, v[168:171] offset:6144
	v_mul_f32_e32 v172, v41, v172
	v_mul_f32_e32 v173, v41, v173
	v_mul_f32_e32 v174, v41, v174
	v_mul_f32_e32 v175, v41, v175
	ds_write_b128 v209, v[172:175] offset:7168
	s_waitcnt lgkmcnt(0)
	s_barrier
; #define GAS __attribute__((address_space(1)))
; #define LAS __attribute__((address_space(3)))
; #define LDS_WAIT() asm volatile("s_waitcnt lgkmcnt(0)" ::: "memory")
; __device__ __forceinline__ unsigned pk4_fp8(float a, float b, float c, float d) {
;     a = fminf(fmaxf(a, -448.f), 448.f); b = fminf(fmaxf(b, -448.f), 448.f); c = fminf(fmaxf(c, -448.f), 448.f); d = fminf(fmaxf(d, -448.f), 448.f);
;     int w = __builtin_amdgcn_cvt_pk_fp8_f32(a, b, 0, false); w = __builtin_amdgcn_cvt_pk_fp8_f32(c, d, w, true); return (unsigned)w; }
;     const int pr = item >> 1, kb = 2 * (pr / nblk) + (item & 1), nb = pr % nblk, k0 = 64 * kb, n0 = 32 * nb;
;     const int nr = n0 + (lane & 31); const int sc = MAP == 1 ? src_col_in(nr) : nr;
;     float v[32];
; #pragma unroll
;     for (int i = 0; i < 32; ++i) v[i] = sc >= 0 ? W[(size_t)(k0 + 2 * i + (lane >> 5)) * Nsrc + sc] : 0.f;
; #pragma unroll
;     for (int i = 0; i < 32; ++i) { const int k = k0 + 2 * i + (lane >> 5); float x = v[i] * wscale; if (KS) x *= (k < ksplit ? ksA[k] : ksB[k - ksplit]); scr[(2 * i + (lane >> 5)) * 33 + (lane & 31)] = x; }
;     LDS_WAIT(); asm volatile("" ::: "memory");
;     const int c = lane & 7;
; #pragma unroll
;     for (int j = 0; j < 4; ++j) { const int n = (lane >> 3) + 8 * j; const LAS float* s = scr + (8 * c) * 33 + n;
;         const unsigned long long o = (unsigned long long)pg8::pk4_fp8(s[0 * 33], s[1 * 33], s[2 * 33], s[3 * 33]) | ((unsigned long long)pg8::pk4_fp8(s[4 * 33], s[5 * 33], s[6 * 33], s[7 * 33]) << 32);
;         *(GAS unsigned long long*)(WT + (size_t)(n0 + n) * K + k0 + 8 * c) = o; }
;     LDS_WAIT(); asm volatile("" ::: "memory");
; }
	s_add_u32 s8, s34, 0x6000
	s_addc_u32 s9, s35, 0
	global_load_dwordx4 v[144:147], v74, s[8:9]
	s_add_u32 s8, s8, 0x20000
	s_addc_u32 s9, s9, 0
	global_load_dwordx4 v[148:151], v74, s[8:9]
	s_add_u32 s8, s8, 0x20000
	s_addc_u32 s9, s9, 0
	global_load_dwordx4 v[152:155], v74, s[8:9]
	s_add_u32 s8, s8, 0x20000
	s_addc_u32 s9, s9, 0
	global_load_dwordx4 v[156:159], v74, s[8:9]
	s_add_u32 s8, s8, 0x20000
	s_addc_u32 s9, s9, 0
	global_load_dwordx4 v[160:163], v74, s[8:9]
	s_add_u32 s8, s8, 0x20000
	s_addc_u32 s9, s9, 0
	global_load_dwordx4 v[164:167], v74, s[8:9]
	s_add_u32 s8, s8, 0x20000
	s_addc_u32 s9, s9, 0
	global_load_dwordx4 v[168:171], v74, s[8:9]
	s_add_u32 s8, s8, 0x20000
	s_addc_u32 s9, s9, 0
	global_load_dwordx4 v[172:175], v74, s[8:9]
	s_add_u32 s6, s36, 0x1000000
	s_addc_u32 s7, s37, 0
	ds_read_b32 v226, v211
	ds_read_b32 v227, v211 offset:512
	ds_read_b32 v228, v211 offset:1024
	ds_read_b32 v229, v211 offset:1536
	ds_read_b32 v230, v211 offset:2048
	ds_read_b32 v231, v211 offset:2560
	ds_read_b32 v232, v211 offset:3072
	ds_read_b32 v233, v211 offset:3584
	ds_read_b32 v234, v211 offset:4096
	ds_read_b32 v235, v211 offset:4608
	ds_read_b32 v236, v211 offset:5120
	ds_read_b32 v237, v211 offset:5632
	ds_read_b32 v238, v211 offset:6144
	ds_read_b32 v239, v211 offset:6656
	ds_read_b32 v240, v211 offset:7168
	ds_read_b32 v241, v211 offset:7680
	s_waitcnt lgkmcnt(0)
	v_max_f32_e32 v226, v226, v226
	v_max_f32_e32 v227, v227, v227
	v_max_f32_e32 v228, v228, v228
	v_max_f32_e32 v229, v229, v229
	v_max_f32_e32 v230, v230, v230
	v_max_f32_e32 v231, v231, v231
	v_max_f32_e32 v232, v232, v232
	v_max_f32_e32 v233, v233, v233
	v_max_f32_e32 v234, v234, v234
	v_max_f32_e32 v235, v235, v235
	v_max_f32_e32 v236, v236, v236
	v_max_f32_e32 v237, v237, v237
	v_max_f32_e32 v238, v238, v238
	v_max_f32_e32 v239, v239, v239
	v_max_f32_e32 v240, v240, v240
	v_max_f32_e32 v241, v241, v241
	v_med3_f32 v226, v226, s62, v95
	v_med3_f32 v227, v227, s62, v95
	v_med3_f32 v228, v228, s62, v95
	v_med3_f32 v229, v229, s62, v95
	v_med3_f32 v230, v230, s62, v95
	v_med3_f32 v231, v231, s62, v95
	v_med3_f32 v232, v232, s62, v95
	v_med3_f32 v233, v233, s62, v95
	v_med3_f32 v234, v234, s62, v95
	v_med3_f32 v235, v235, s62, v95
	v_med3_f32 v236, v236, s62, v95
	v_med3_f32 v237, v237, s62, v95
	v_med3_f32 v238, v238, s62, v95
	v_med3_f32 v239, v239, s62, v95
	v_med3_f32 v240, v240, s62, v95
	v_med3_f32 v241, v241, s62, v95
	v_mov_b32_e32 v242, 0
	v_mov_b32_e32 v243, 0
	v_mov_b32_e32 v244, 0
	v_mov_b32_e32 v245, 0
	v_cvt_pk_fp8_f32 v242, v226, v227
	v_cvt_pk_fp8_f32 v243, v230, v231
	v_cvt_pk_fp8_f32 v244, v234, v235
	v_cvt_pk_fp8_f32 v245, v238, v239
	v_cvt_pk_fp8_f32 v242, v228, v229 op_sel:[0,0,1]
	v_cvt_pk_fp8_f32 v243, v232, v233 op_sel:[0,0,1]
	v_cvt_pk_fp8_f32 v244, v236, v237 op_sel:[0,0,1]
	v_cvt_pk_fp8_f32 v245, v240, v241 op_sel:[0,0,1]
	s_nop 0
	global_store_dwordx4 v77, v[242:245], s[6:7]
	ds_read_b32 v226, v213
	ds_read_b32 v227, v213 offset:512
	ds_read_b32 v228, v213 offset:1024
	ds_read_b32 v229, v213 offset:1536
	ds_read_b32 v230, v213 offset:2048
	ds_read_b32 v231, v213 offset:2560
	ds_read_b32 v232, v213 offset:3072
	ds_read_b32 v233, v213 offset:3584
	ds_read_b32 v234, v213 offset:4096
	ds_read_b32 v235, v213 offset:4608
	ds_read_b32 v236, v213 offset:5120
	ds_read_b32 v237, v213 offset:5632
	ds_read_b32 v238, v213 offset:6144
	ds_read_b32 v239, v213 offset:6656
	ds_read_b32 v240, v213 offset:7168
	ds_read_b32 v241, v213 offset:7680
	s_waitcnt lgkmcnt(0)
	v_max_f32_e32 v226, v226, v226
	v_max_f32_e32 v227, v227, v227
	v_max_f32_e32 v228, v228, v228
	v_max_f32_e32 v229, v229, v229
	v_max_f32_e32 v230, v230, v230
	v_max_f32_e32 v231, v231, v231
	v_max_f32_e32 v232, v232, v232
	v_max_f32_e32 v233, v233, v233
	v_max_f32_e32 v234, v234, v234
	v_max_f32_e32 v235, v235, v235
	v_max_f32_e32 v236, v236, v236
	v_max_f32_e32 v237, v237, v237
	v_max_f32_e32 v238, v238, v238
	v_max_f32_e32 v239, v239, v239
	v_max_f32_e32 v240, v240, v240
	v_max_f32_e32 v241, v241, v241
	v_med3_f32 v226, v226, s62, v95
	v_med3_f32 v227, v227, s62, v95
	v_med3_f32 v228, v228, s62, v95
	v_med3_f32 v229, v229, s62, v95
	v_med3_f32 v230, v230, s62, v95
	v_med3_f32 v231, v231, s62, v95
	v_med3_f32 v232, v232, s62, v95
	v_med3_f32 v233, v233, s62, v95
	v_med3_f32 v234, v234, s62, v95
	v_med3_f32 v235, v235, s62, v95
	v_med3_f32 v236, v236, s62, v95
	v_med3_f32 v237, v237, s62, v95
	v_med3_f32 v238, v238, s62, v95
	v_med3_f32 v239, v239, s62, v95
	v_med3_f32 v240, v240, s62, v95
	v_med3_f32 v241, v241, s62, v95
	v_mov_b32_e32 v242, 0
	v_mov_b32_e32 v243, 0
	v_mov_b32_e32 v244, 0
	v_mov_b32_e32 v245, 0
	v_cvt_pk_fp8_f32 v242, v226, v227
	v_cvt_pk_fp8_f32 v243, v230, v231
	v_cvt_pk_fp8_f32 v244, v234, v235
	v_cvt_pk_fp8_f32 v245, v238, v239
	v_cvt_pk_fp8_f32 v242, v228, v229 op_sel:[0,0,1]
	v_cvt_pk_fp8_f32 v243, v232, v233 op_sel:[0,0,1]
	v_cvt_pk_fp8_f32 v244, v236, v237 op_sel:[0,0,1]
	v_cvt_pk_fp8_f32 v245, v240, v241 op_sel:[0,0,1]
	s_nop 0
	global_store_dwordx4 v78, v[242:245], s[6:7]
	s_waitcnt vmcnt(12)
	v_mul_f32_e32 v176, v34, v176
	v_mul_f32_e32 v177, v34, v177
	v_mul_f32_e32 v178, v34, v178
	v_mul_f32_e32 v179, v34, v179
	ds_write_b128 v210, v[176:179]
	v_mul_f32_e32 v180, v35, v180
	v_mul_f32_e32 v181, v35, v181
	v_mul_f32_e32 v182, v35, v182
	v_mul_f32_e32 v183, v35, v183
	ds_write_b128 v210, v[180:183] offset:1024
	v_mul_f32_e32 v184, v36, v184
	v_mul_f32_e32 v185, v36, v185
	v_mul_f32_e32 v186, v36, v186
	v_mul_f32_e32 v187, v36, v187
	ds_write_b128 v210, v[184:187] offset:2048
	v_mul_f32_e32 v188, v37, v188
	v_mul_f32_e32 v189, v37, v189
	v_mul_f32_e32 v190, v37, v190
	v_mul_f32_e32 v191, v37, v191
	ds_write_b128 v210, v[188:191] offset:3072
	v_mul_f32_e32 v192, v38, v192
	v_mul_f32_e32 v193, v38, v193
	v_mul_f32_e32 v194, v38, v194
	v_mul_f32_e32 v195, v38, v195
	ds_write_b128 v210, v[192:195] offset:4096
	v_mul_f32_e32 v196, v39, v196
	v_mul_f32_e32 v197, v39, v197
	v_mul_f32_e32 v198, v39, v198
	v_mul_f32_e32 v199, v39, v199
	ds_write_b128 v210, v[196:199] offset:5120
	v_mul_f32_e32 v200, v40, v200
	v_mul_f32_e32 v201, v40, v201
	v_mul_f32_e32 v202, v40, v202
	v_mul_f32_e32 v203, v40, v203
	ds_write_b128 v210, v[200:203] offset:6144
	v_mul_f32_e32 v204, v41, v204
	v_mul_f32_e32 v205, v41, v205
	v_mul_f32_e32 v206, v41, v206
	v_mul_f32_e32 v207, v41, v207
	ds_write_b128 v210, v[204:207] offset:7168
	s_waitcnt lgkmcnt(0)
	s_barrier
; #define GAS __attribute__((address_space(1)))
; #define LAS __attribute__((address_space(3)))
; #define LDS_WAIT() asm volatile("s_waitcnt lgkmcnt(0)" ::: "memory")
; __device__ __forceinline__ unsigned pk4_fp8(float a, float b, float c, float d) {
;     a = fminf(fmaxf(a, -448.f), 448.f); b = fminf(fmaxf(b, -448.f), 448.f); c = fminf(fmaxf(c, -448.f), 448.f); d = fminf(fmaxf(d, -448.f), 448.f);
;     int w = __builtin_amdgcn_cvt_pk_fp8_f32(a, b, 0, false); w = __builtin_amdgcn_cvt_pk_fp8_f32(c, d, w, true); return (unsigned)w; }
;     const int pr = item >> 1, kb = 2 * (pr / nblk) + (item & 1), nb = pr % nblk, k0 = 64 * kb, n0 = 32 * nb;
;     const int nr = n0 + (lane & 31); const int sc = MAP == 1 ? src_col_in(nr) : nr;
;     float v[32];
; #pragma unroll
;     for (int i = 0; i < 32; ++i) v[i] = sc >= 0 ? W[(size_t)(k0 + 2 * i + (lane >> 5)) * Nsrc + sc] : 0.f;
; #pragma unroll
;     for (int i = 0; i < 32; ++i) { const int k = k0 + 2 * i + (lane >> 5); float x = v[i] * wscale; if (KS) x *= (k < ksplit ? ksA[k] : ksB[k - ksplit]); scr[(2 * i + (lane >> 5)) * 33 + (lane & 31)] = x; }
;     LDS_WAIT(); asm volatile("" ::: "memory");
;     const int c = lane & 7;
; #pragma unroll
;     for (int j = 0; j < 4; ++j) { const int n = (lane >> 3) + 8 * j; const LAS float* s = scr + (8 * c) * 33 + n;
;         const unsigned long long o = (unsigned long long)pg8::pk4_fp8(s[0 * 33], s[1 * 33], s[2 * 33], s[3 * 33]) | ((unsigned long long)pg8::pk4_fp8(s[4 * 33], s[5 * 33], s[6 * 33], s[7 * 33]) << 32);
;         *(GAS unsigned long long*)(WT + (size_t)(n0 + n) * K + k0 + 8 * c) = o; }
;     LDS_WAIT(); asm volatile("" ::: "memory");
; }
	s_add_u32 s8, s34, 0x7000
	s_addc_u32 s9, s35, 0
	global_load_dwordx4 v[176:179], v74, s[8:9]
	s_add_u32 s8, s8, 0x20000
	s_addc_u32 s9, s9, 0
	global_load_dwordx4 v[180:183], v74, s[8:9]
	s_add_u32 s8, s8, 0x20000
	s_addc_u32 s9, s9, 0
	global_load_dwordx4 v[184:187], v74, s[8:9]
	s_add_u32 s8, s8, 0x20000
	s_addc_u32 s9, s9, 0
	global_load_dwordx4 v[188:191], v74, s[8:9]
	s_add_u32 s8, s8, 0x20000
	s_addc_u32 s9, s9, 0
	global_load_dwordx4 v[192:195], v74, s[8:9]
	s_add_u32 s8, s8, 0x20000
	s_addc_u32 s9, s9, 0
	global_load_dwordx4 v[196:199], v74, s[8:9]
	s_add_u32 s8, s8, 0x20000
	s_addc_u32 s9, s9, 0
	global_load_dwordx4 v[200:203], v74, s[8:9]
	s_add_u32 s8, s8, 0x20000
	s_addc_u32 s9, s9, 0
	global_load_dwordx4 v[204:207], v74, s[8:9]
	s_add_u32 s6, s36, 0x1400000
	s_addc_u32 s7, s37, 0
	ds_read_b32 v226, v212
	ds_read_b32 v227, v212 offset:512
	ds_read_b32 v228, v212 offset:1024
	ds_read_b32 v229, v212 offset:1536
	ds_read_b32 v230, v212 offset:2048
	ds_read_b32 v231, v212 offset:2560
	ds_read_b32 v232, v212 offset:3072
	ds_read_b32 v233, v212 offset:3584
	ds_read_b32 v234, v212 offset:4096
	ds_read_b32 v235, v212 offset:4608
	ds_read_b32 v236, v212 offset:5120
	ds_read_b32 v237, v212 offset:5632
	ds_read_b32 v238, v212 offset:6144
	ds_read_b32 v239, v212 offset:6656
	ds_read_b32 v240, v212 offset:7168
	ds_read_b32 v241, v212 offset:7680
	s_waitcnt lgkmcnt(0)
	v_max_f32_e32 v226, v226, v226
	v_max_f32_e32 v227, v227, v227
	v_max_f32_e32 v228, v228, v228
	v_max_f32_e32 v229, v229, v229
	v_max_f32_e32 v230, v230, v230
	v_max_f32_e32 v231, v231, v231
	v_max_f32_e32 v232, v232, v232
	v_max_f32_e32 v233, v233, v233
	v_max_f32_e32 v234, v234, v234
	v_max_f32_e32 v235, v235, v235
	v_max_f32_e32 v236, v236, v236
	v_max_f32_e32 v237, v237, v237
	v_max_f32_e32 v238, v238, v238
	v_max_f32_e32 v239, v239, v239
	v_max_f32_e32 v240, v240, v240
	v_max_f32_e32 v241, v241, v241
	v_med3_f32 v226, v226, s62, v95
	v_med3_f32 v227, v227, s62, v95
	v_med3_f32 v228, v228, s62, v95
	v_med3_f32 v229, v229, s62, v95
	v_med3_f32 v230, v230, s62, v95
	v_med3_f32 v231, v231, s62, v95
	v_med3_f32 v232, v232, s62, v95
	v_med3_f32 v233, v233, s62, v95
	v_med3_f32 v234, v234, s62, v95
	v_med3_f32 v235, v235, s62, v95
	v_med3_f32 v236, v236, s62, v95
	v_med3_f32 v237, v237, s62, v95
	v_med3_f32 v238, v238, s62, v95
	v_med3_f32 v239, v239, s62, v95
	v_med3_f32 v240, v240, s62, v95
	v_med3_f32 v241, v241, s62, v95
	v_mov_b32_e32 v242, 0
	v_mov_b32_e32 v243, 0
	v_mov_b32_e32 v244, 0
	v_mov_b32_e32 v245, 0
	v_cvt_pk_fp8_f32 v242, v226, v227
	v_cvt_pk_fp8_f32 v243, v230, v231
	v_cvt_pk_fp8_f32 v244, v234, v235
	v_cvt_pk_fp8_f32 v245, v238, v239
	v_cvt_pk_fp8_f32 v242, v228, v229 op_sel:[0,0,1]
	v_cvt_pk_fp8_f32 v243, v232, v233 op_sel:[0,0,1]
	v_cvt_pk_fp8_f32 v244, v236, v237 op_sel:[0,0,1]
	v_cvt_pk_fp8_f32 v245, v240, v241 op_sel:[0,0,1]
	s_nop 0
	global_store_dwordx4 v77, v[242:245], s[6:7]
	ds_read_b32 v226, v214
	ds_read_b32 v227, v214 offset:512
	ds_read_b32 v228, v214 offset:1024
	ds_read_b32 v229, v214 offset:1536
	ds_read_b32 v230, v214 offset:2048
	ds_read_b32 v231, v214 offset:2560
	ds_read_b32 v232, v214 offset:3072
	ds_read_b32 v233, v214 offset:3584
	ds_read_b32 v234, v214 offset:4096
	ds_read_b32 v235, v214 offset:4608
	ds_read_b32 v236, v214 offset:5120
	ds_read_b32 v237, v214 offset:5632
	ds_read_b32 v238, v214 offset:6144
	ds_read_b32 v239, v214 offset:6656
	ds_read_b32 v240, v214 offset:7168
	ds_read_b32 v241, v214 offset:7680
	s_waitcnt lgkmcnt(0)
	v_max_f32_e32 v226, v226, v226
	v_max_f32_e32 v227, v227, v227
	v_max_f32_e32 v228, v228, v228
	v_max_f32_e32 v229, v229, v229
	v_max_f32_e32 v230, v230, v230
	v_max_f32_e32 v231, v231, v231
	v_max_f32_e32 v232, v232, v232
	v_max_f32_e32 v233, v233, v233
	v_max_f32_e32 v234, v234, v234
	v_max_f32_e32 v235, v235, v235
	v_max_f32_e32 v236, v236, v236
	v_max_f32_e32 v237, v237, v237
	v_max_f32_e32 v238, v238, v238
	v_max_f32_e32 v239, v239, v239
	v_max_f32_e32 v240, v240, v240
	v_max_f32_e32 v241, v241, v241
	v_med3_f32 v226, v226, s62, v95
	v_med3_f32 v227, v227, s62, v95
	v_med3_f32 v228, v228, s62, v95
	v_med3_f32 v229, v229, s62, v95
	v_med3_f32 v230, v230, s62, v95
	v_med3_f32 v231, v231, s62, v95
	v_med3_f32 v232, v232, s62, v95
	v_med3_f32 v233, v233, s62, v95
	v_med3_f32 v234, v234, s62, v95
	v_med3_f32 v235, v235, s62, v95
	v_med3_f32 v236, v236, s62, v95
	v_med3_f32 v237, v237, s62, v95
	v_med3_f32 v238, v238, s62, v95
	v_med3_f32 v239, v239, s62, v95
	v_med3_f32 v240, v240, s62, v95
	v_med3_f32 v241, v241, s62, v95
	v_mov_b32_e32 v242, 0
	v_mov_b32_e32 v243, 0
	v_mov_b32_e32 v244, 0
	v_mov_b32_e32 v245, 0
	v_cvt_pk_fp8_f32 v242, v226, v227
	v_cvt_pk_fp8_f32 v243, v230, v231
	v_cvt_pk_fp8_f32 v244, v234, v235
	v_cvt_pk_fp8_f32 v245, v238, v239
	v_cvt_pk_fp8_f32 v242, v228, v229 op_sel:[0,0,1]
	v_cvt_pk_fp8_f32 v243, v232, v233 op_sel:[0,0,1]
	v_cvt_pk_fp8_f32 v244, v236, v237 op_sel:[0,0,1]
	v_cvt_pk_fp8_f32 v245, v240, v241 op_sel:[0,0,1]
	s_nop 0
	global_store_dwordx4 v78, v[242:245], s[6:7]
	s_waitcnt vmcnt(12)
	v_mul_f32_e32 v144, v34, v144
	v_mul_f32_e32 v145, v34, v145
	v_mul_f32_e32 v146, v34, v146
	v_mul_f32_e32 v147, v34, v147
	ds_write_b128 v209, v[144:147]
	v_mul_f32_e32 v148, v35, v148
	v_mul_f32_e32 v149, v35, v149
	v_mul_f32_e32 v150, v35, v150
	v_mul_f32_e32 v151, v35, v151
	ds_write_b128 v209, v[148:151] offset:1024
	v_mul_f32_e32 v152, v36, v152
	v_mul_f32_e32 v153, v36, v153
	v_mul_f32_e32 v154, v36, v154
	v_mul_f32_e32 v155, v36, v155
	ds_write_b128 v209, v[152:155] offset:2048
	v_mul_f32_e32 v156, v37, v156
	v_mul_f32_e32 v157, v37, v157
	v_mul_f32_e32 v158, v37, v158
	v_mul_f32_e32 v159, v37, v159
	ds_write_b128 v209, v[156:159] offset:3072
	v_mul_f32_e32 v160, v38, v160
	v_mul_f32_e32 v161, v38, v161
	v_mul_f32_e32 v162, v38, v162
	v_mul_f32_e32 v163, v38, v163
	ds_write_b128 v209, v[160:163] offset:4096
	v_mul_f32_e32 v164, v39, v164
	v_mul_f32_e32 v165, v39, v165
	v_mul_f32_e32 v166, v39, v166
	v_mul_f32_e32 v167, v39, v167
	ds_write_b128 v209, v[164:167] offset:5120
	v_mul_f32_e32 v168, v40, v168
	v_mul_f32_e32 v169, v40, v169
	v_mul_f32_e32 v170, v40, v170
	v_mul_f32_e32 v171, v40, v171
	ds_write_b128 v209, v[168:171] offset:6144
	v_mul_f32_e32 v172, v41, v172
	v_mul_f32_e32 v173, v41, v173
	v_mul_f32_e32 v174, v41, v174
	v_mul_f32_e32 v175, v41, v175
	ds_write_b128 v209, v[172:175] offset:7168
	s_waitcnt lgkmcnt(0)
	s_barrier
; #define GAS __attribute__((address_space(1)))
; #define LAS __attribute__((address_space(3)))
; #define LDS_WAIT() asm volatile("s_waitcnt lgkmcnt(0)" ::: "memory")
; __device__ __forceinline__ unsigned pk4_fp8(float a, float b, float c, float d) {
;     a = fminf(fmaxf(a, -448.f), 448.f); b = fminf(fmaxf(b, -448.f), 448.f); c = fminf(fmaxf(c, -448.f), 448.f); d = fminf(fmaxf(d, -448.f), 448.f);
;     int w = __builtin_amdgcn_cvt_pk_fp8_f32(a, b, 0, false); w = __builtin_amdgcn_cvt_pk_fp8_f32(c, d, w, true); return (unsigned)w; }
;     const int pr = item >> 1, kb = 2 * (pr / nblk) + (item & 1), nb = pr % nblk, k0 = 64 * kb, n0 = 32 * nb;
;     const int nr = n0 + (lane & 31); const int sc = MAP == 1 ? src_col_in(nr) : nr;
;     float v[32];
; #pragma unroll
;     for (int i = 0; i < 32; ++i) v[i] = sc >= 0 ? W[(size_t)(k0 + 2 * i + (lane >> 5)) * Nsrc + sc] : 0.f;
; #pragma unroll
;     for (int i = 0; i < 32; ++i) { const int k = k0 + 2 * i + (lane >> 5); float x = v[i] * wscale; if (KS) x *= (k < ksplit ? ksA[k] : ksB[k - ksplit]); scr[(2 * i + (lane >> 5)) * 33 + (lane & 31)] = x; }
;     LDS_WAIT(); asm volatile("" ::: "memory");
;     const int c = lane & 7;
; #pragma unroll
;     for (int j = 0; j < 4; ++j) { const int n = (lane >> 3) + 8 * j; const LAS float* s = scr + (8 * c) * 33 + n;
;         const unsigned long long o = (unsigned long long)pg8::pk4_fp8(s[0 * 33], s[1 * 33], s[2 * 33], s[3 * 33]) | ((unsigned long long)pg8::pk4_fp8(s[4 * 33], s[5 * 33], s[6 * 33], s[7 * 33]) << 32);
;         *(GAS unsigned long long*)(WT + (size_t)(n0 + n) * K + k0 + 8 * c) = o; }
;     LDS_WAIT(); asm volatile("" ::: "memory");
; }
	s_add_u32 s8, s34, 0x8000
	s_addc_u32 s9, s35, 0
	global_load_dwordx4 v[144:147], v74, s[8:9]
	s_add_u32 s8, s8, 0x20000
	s_addc_u32 s9, s9, 0
	global_load_dwordx4 v[148:151], v74, s[8:9]
	s_add_u32 s8, s8, 0x20000
	s_addc_u32 s9, s9, 0
	global_load_dwordx4 v[152:155], v74, s[8:9]
	s_add_u32 s8, s8, 0x20000
	s_addc_u32 s9, s9, 0
	global_load_dwordx4 v[156:159], v74, s[8:9]
	s_add_u32 s8, s8, 0x20000
	s_addc_u32 s9, s9, 0
	global_load_dwordx4 v[160:163], v74, s[8:9]
	s_add_u32 s8, s8, 0x20000
	s_addc_u32 s9, s9, 0
	global_load_dwordx4 v[164:167], v74, s[8:9]
	s_add_u32 s8, s8, 0x20000
	s_addc_u32 s9, s9, 0
	global_load_dwordx4 v[168:171], v74, s[8:9]
	s_add_u32 s8, s8, 0x20000
	s_addc_u32 s9, s9, 0
	global_load_dwordx4 v[172:175], v74, s[8:9]
	s_add_u32 s6, s36, 0x1800000
	s_addc_u32 s7, s37, 0
	ds_read_b32 v226, v211
	ds_read_b32 v227, v211 offset:512
	ds_read_b32 v228, v211 offset:1024
	ds_read_b32 v229, v211 offset:1536
	ds_read_b32 v230, v211 offset:2048
	ds_read_b32 v231, v211 offset:2560
	ds_read_b32 v232, v211 offset:3072
	ds_read_b32 v233, v211 offset:3584
	ds_read_b32 v234, v211 offset:4096
	ds_read_b32 v235, v211 offset:4608
	ds_read_b32 v236, v211 offset:5120
	ds_read_b32 v237, v211 offset:5632
	ds_read_b32 v238, v211 offset:6144
	ds_read_b32 v239, v211 offset:6656
	ds_read_b32 v240, v211 offset:7168
	ds_read_b32 v241, v211 offset:7680
	s_waitcnt lgkmcnt(0)
	v_max_f32_e32 v226, v226, v226
	v_max_f32_e32 v227, v227, v227
	v_max_f32_e32 v228, v228, v228
	v_max_f32_e32 v229, v229, v229
	v_max_f32_e32 v230, v230, v230
	v_max_f32_e32 v231, v231, v231
	v_max_f32_e32 v232, v232, v232
	v_max_f32_e32 v233, v233, v233
	v_max_f32_e32 v234, v234, v234
	v_max_f32_e32 v235, v235, v235
	v_max_f32_e32 v236, v236, v236
	v_max_f32_e32 v237, v237, v237
	v_max_f32_e32 v238, v238, v238
	v_max_f32_e32 v239, v239, v239
	v_max_f32_e32 v240, v240, v240
	v_max_f32_e32 v241, v241, v241
	v_med3_f32 v226, v226, s62, v95
	v_med3_f32 v227, v227, s62, v95
	v_med3_f32 v228, v228, s62, v95
	v_med3_f32 v229, v229, s62, v95
	v_med3_f32 v230, v230, s62, v95
	v_med3_f32 v231, v231, s62, v95
	v_med3_f32 v232, v232, s62, v95
	v_med3_f32 v233, v233, s62, v95
	v_med3_f32 v234, v234, s62, v95
	v_med3_f32 v235, v235, s62, v95
	v_med3_f32 v236, v236, s62, v95
	v_med3_f32 v237, v237, s62, v95
	v_med3_f32 v238, v238, s62, v95
	v_med3_f32 v239, v239, s62, v95
	v_med3_f32 v240, v240, s62, v95
	v_med3_f32 v241, v241, s62, v95
	v_mov_b32_e32 v242, 0
	v_mov_b32_e32 v243, 0
	v_mov_b32_e32 v244, 0
	v_mov_b32_e32 v245, 0
	v_cvt_pk_fp8_f32 v242, v226, v227
	v_cvt_pk_fp8_f32 v243, v230, v231
	v_cvt_pk_fp8_f32 v244, v234, v235
	v_cvt_pk_fp8_f32 v245, v238, v239
	v_cvt_pk_fp8_f32 v242, v228, v229 op_sel:[0,0,1]
	v_cvt_pk_fp8_f32 v243, v232, v233 op_sel:[0,0,1]
	v_cvt_pk_fp8_f32 v244, v236, v237 op_sel:[0,0,1]
	v_cvt_pk_fp8_f32 v245, v240, v241 op_sel:[0,0,1]
	s_nop 0
	global_store_dwordx4 v77, v[242:245], s[6:7]
	ds_read_b32 v226, v213
	ds_read_b32 v227, v213 offset:512
	ds_read_b32 v228, v213 offset:1024
	ds_read_b32 v229, v213 offset:1536
	ds_read_b32 v230, v213 offset:2048
	ds_read_b32 v231, v213 offset:2560
	ds_read_b32 v232, v213 offset:3072
	ds_read_b32 v233, v213 offset:3584
	ds_read_b32 v234, v213 offset:4096
	ds_read_b32 v235, v213 offset:4608
	ds_read_b32 v236, v213 offset:5120
	ds_read_b32 v237, v213 offset:5632
	ds_read_b32 v238, v213 offset:6144
	ds_read_b32 v239, v213 offset:6656
	ds_read_b32 v240, v213 offset:7168
	ds_read_b32 v241, v213 offset:7680
	s_waitcnt lgkmcnt(0)
	v_max_f32_e32 v226, v226, v226
	v_max_f32_e32 v227, v227, v227
	v_max_f32_e32 v228, v228, v228
	v_max_f32_e32 v229, v229, v229
	v_max_f32_e32 v230, v230, v230
	v_max_f32_e32 v231, v231, v231
	v_max_f32_e32 v232, v232, v232
	v_max_f32_e32 v233, v233, v233
	v_max_f32_e32 v234, v234, v234
	v_max_f32_e32 v235, v235, v235
	v_max_f32_e32 v236, v236, v236
	v_max_f32_e32 v237, v237, v237
	v_max_f32_e32 v238, v238, v238
	v_max_f32_e32 v239, v239, v239
	v_max_f32_e32 v240, v240, v240
	v_max_f32_e32 v241, v241, v241
	v_med3_f32 v226, v226, s62, v95
	v_med3_f32 v227, v227, s62, v95
	v_med3_f32 v228, v228, s62, v95
	v_med3_f32 v229, v229, s62, v95
	v_med3_f32 v230, v230, s62, v95
	v_med3_f32 v231, v231, s62, v95
	v_med3_f32 v232, v232, s62, v95
	v_med3_f32 v233, v233, s62, v95
	v_med3_f32 v234, v234, s62, v95
	v_med3_f32 v235, v235, s62, v95
	v_med3_f32 v236, v236, s62, v95
	v_med3_f32 v237, v237, s62, v95
	v_med3_f32 v238, v238, s62, v95
	v_med3_f32 v239, v239, s62, v95
	v_med3_f32 v240, v240, s62, v95
	v_med3_f32 v241, v241, s62, v95
	v_mov_b32_e32 v242, 0
	v_mov_b32_e32 v243, 0
	v_mov_b32_e32 v244, 0
	v_mov_b32_e32 v245, 0
	v_cvt_pk_fp8_f32 v242, v226, v227
	v_cvt_pk_fp8_f32 v243, v230, v231
	v_cvt_pk_fp8_f32 v244, v234, v235
	v_cvt_pk_fp8_f32 v245, v238, v239
	v_cvt_pk_fp8_f32 v242, v228, v229 op_sel:[0,0,1]
	v_cvt_pk_fp8_f32 v243, v232, v233 op_sel:[0,0,1]
	v_cvt_pk_fp8_f32 v244, v236, v237 op_sel:[0,0,1]
	v_cvt_pk_fp8_f32 v245, v240, v241 op_sel:[0,0,1]
	s_nop 0
	global_store_dwordx4 v78, v[242:245], s[6:7]
	s_waitcnt vmcnt(12)
	v_mul_f32_e32 v176, v34, v176
	v_mul_f32_e32 v177, v34, v177
	v_mul_f32_e32 v178, v34, v178
	v_mul_f32_e32 v179, v34, v179
	ds_write_b128 v210, v[176:179]
	v_mul_f32_e32 v180, v35, v180
	v_mul_f32_e32 v181, v35, v181
	v_mul_f32_e32 v182, v35, v182
	v_mul_f32_e32 v183, v35, v183
	ds_write_b128 v210, v[180:183] offset:1024
	v_mul_f32_e32 v184, v36, v184
	v_mul_f32_e32 v185, v36, v185
	v_mul_f32_e32 v186, v36, v186
	v_mul_f32_e32 v187, v36, v187
	ds_write_b128 v210, v[184:187] offset:2048
	v_mul_f32_e32 v188, v37, v188
	v_mul_f32_e32 v189, v37, v189
	v_mul_f32_e32 v190, v37, v190
	v_mul_f32_e32 v191, v37, v191
	ds_write_b128 v210, v[188:191] offset:3072
	v_mul_f32_e32 v192, v38, v192
	v_mul_f32_e32 v193, v38, v193
	v_mul_f32_e32 v194, v38, v194
	v_mul_f32_e32 v195, v38, v195
	ds_write_b128 v210, v[192:195] offset:4096
	v_mul_f32_e32 v196, v39, v196
	v_mul_f32_e32 v197, v39, v197
	v_mul_f32_e32 v198, v39, v198
	v_mul_f32_e32 v199, v39, v199
	ds_write_b128 v210, v[196:199] offset:5120
	v_mul_f32_e32 v200, v40, v200
	v_mul_f32_e32 v201, v40, v201
	v_mul_f32_e32 v202, v40, v202
	v_mul_f32_e32 v203, v40, v203
	ds_write_b128 v210, v[200:203] offset:6144
	v_mul_f32_e32 v204, v41, v204
	v_mul_f32_e32 v205, v41, v205
	v_mul_f32_e32 v206, v41, v206
	v_mul_f32_e32 v207, v41, v207
	ds_write_b128 v210, v[204:207] offset:7168
	s_waitcnt lgkmcnt(0)
	s_barrier
; #define GAS __attribute__((address_space(1)))
; #define LAS __attribute__((address_space(3)))
; #define LDS_WAIT() asm volatile("s_waitcnt lgkmcnt(0)" ::: "memory")
; __device__ __forceinline__ unsigned pk4_fp8(float a, float b, float c, float d) {
;     a = fminf(fmaxf(a, -448.f), 448.f); b = fminf(fmaxf(b, -448.f), 448.f); c = fminf(fmaxf(c, -448.f), 448.f); d = fminf(fmaxf(d, -448.f), 448.f);
;     int w = __builtin_amdgcn_cvt_pk_fp8_f32(a, b, 0, false); w = __builtin_amdgcn_cvt_pk_fp8_f32(c, d, w, true); return (unsigned)w; }
;     const int pr = item >> 1, kb = 2 * (pr / nblk) + (item & 1), nb = pr % nblk, k0 = 64 * kb, n0 = 32 * nb;
;     const int nr = n0 + (lane & 31); const int sc = MAP == 1 ? src_col_in(nr) : nr;
;     float v[32];
; #pragma unroll
;     for (int i = 0; i < 32; ++i) v[i] = sc >= 0 ? W[(size_t)(k0 + 2 * i + (lane >> 5)) * Nsrc + sc] : 0.f;
; #pragma unroll
;     for (int i = 0; i < 32; ++i) { const int k = k0 + 2 * i + (lane >> 5); float x = v[i] * wscale; if (KS) x *= (k < ksplit ? ksA[k] : ksB[k - ksplit]); scr[(2 * i + (lane >> 5)) * 33 + (lane & 31)] = x; }
;     LDS_WAIT(); asm volatile("" ::: "memory");
;     const int c = lane & 7;
; #pragma unroll
;     for (int j = 0; j < 4; ++j) { const int n = (lane >> 3) + 8 * j; const LAS float* s = scr + (8 * c) * 33 + n;
;         const unsigned long long o = (unsigned long long)pg8::pk4_fp8(s[0 * 33], s[1 * 33], s[2 * 33], s[3 * 33]) | ((unsigned long long)pg8::pk4_fp8(s[4 * 33], s[5 * 33], s[6 * 33], s[7 * 33]) << 32);
;         *(GAS unsigned long long*)(WT + (size_t)(n0 + n) * K + k0 + 8 * c) = o; }
;     LDS_WAIT(); asm volatile("" ::: "memory");
; }
	s_add_u32 s8, s34, 0x9000
	s_addc_u32 s9, s35, 0
	global_load_dwordx4 v[176:179], v74, s[8:9]
	s_add_u32 s8, s8, 0x20000
	s_addc_u32 s9, s9, 0
	global_load_dwordx4 v[180:183], v74, s[8:9]
	s_add_u32 s8, s8, 0x20000
	s_addc_u32 s9, s9, 0
	global_load_dwordx4 v[184:187], v74, s[8:9]
	s_add_u32 s8, s8, 0x20000
	s_addc_u32 s9, s9, 0
	global_load_dwordx4 v[188:191], v74, s[8:9]
	s_add_u32 s8, s8, 0x20000
	s_addc_u32 s9, s9, 0
	global_load_dwordx4 v[192:195], v74, s[8:9]
	s_add_u32 s8, s8, 0x20000
	s_addc_u32 s9, s9, 0
	global_load_dwordx4 v[196:199], v74, s[8:9]
	s_add_u32 s8, s8, 0x20000
	s_addc_u32 s9, s9, 0
	global_load_dwordx4 v[200:203], v74, s[8:9]
	s_add_u32 s8, s8, 0x20000
	s_addc_u32 s9, s9, 0
	global_load_dwordx4 v[204:207], v74, s[8:9]
	s_add_u32 s6, s36, 0x1c00000
	s_addc_u32 s7, s37, 0
	ds_read_b32 v226, v212
	ds_read_b32 v227, v212 offset:512
	ds_read_b32 v228, v212 offset:1024
	ds_read_b32 v229, v212 offset:1536
	ds_read_b32 v230, v212 offset:2048
	ds_read_b32 v231, v212 offset:2560
	ds_read_b32 v232, v212 offset:3072
	ds_read_b32 v233, v212 offset:3584
	ds_read_b32 v234, v212 offset:4096
	ds_read_b32 v235, v212 offset:4608
	ds_read_b32 v236, v212 offset:5120
	ds_read_b32 v237, v212 offset:5632
	ds_read_b32 v238, v212 offset:6144
	ds_read_b32 v239, v212 offset:6656
	ds_read_b32 v240, v212 offset:7168
	ds_read_b32 v241, v212 offset:7680
	s_waitcnt lgkmcnt(0)
	v_max_f32_e32 v226, v226, v226
	v_max_f32_e32 v227, v227, v227
	v_max_f32_e32 v228, v228, v228
	v_max_f32_e32 v229, v229, v229
	v_max_f32_e32 v230, v230, v230
	v_max_f32_e32 v231, v231, v231
	v_max_f32_e32 v232, v232, v232
	v_max_f32_e32 v233, v233, v233
	v_max_f32_e32 v234, v234, v234
	v_max_f32_e32 v235, v235, v235
	v_max_f32_e32 v236, v236, v236
	v_max_f32_e32 v237, v237, v237
	v_max_f32_e32 v238, v238, v238
	v_max_f32_e32 v239, v239, v239
	v_max_f32_e32 v240, v240, v240
	v_max_f32_e32 v241, v241, v241
	v_med3_f32 v226, v226, s62, v95
	v_med3_f32 v227, v227, s62, v95
	v_med3_f32 v228, v228, s62, v95
	v_med3_f32 v229, v229, s62, v95
	v_med3_f32 v230, v230, s62, v95
	v_med3_f32 v231, v231, s62, v95
	v_med3_f32 v232, v232, s62, v95
	v_med3_f32 v233, v233, s62, v95
	v_med3_f32 v234, v234, s62, v95
	v_med3_f32 v235, v235, s62, v95
	v_med3_f32 v236, v236, s62, v95
	v_med3_f32 v237, v237, s62, v95
	v_med3_f32 v238, v238, s62, v95
	v_med3_f32 v239, v239, s62, v95
	v_med3_f32 v240, v240, s62, v95
	v_med3_f32 v241, v241, s62, v95
	v_mov_b32_e32 v242, 0
	v_mov_b32_e32 v243, 0
	v_mov_b32_e32 v244, 0
	v_mov_b32_e32 v245, 0
	v_cvt_pk_fp8_f32 v242, v226, v227
	v_cvt_pk_fp8_f32 v243, v230, v231
	v_cvt_pk_fp8_f32 v244, v234, v235
	v_cvt_pk_fp8_f32 v245, v238, v239
	v_cvt_pk_fp8_f32 v242, v228, v229 op_sel:[0,0,1]
	v_cvt_pk_fp8_f32 v243, v232, v233 op_sel:[0,0,1]
	v_cvt_pk_fp8_f32 v244, v236, v237 op_sel:[0,0,1]
	v_cvt_pk_fp8_f32 v245, v240, v241 op_sel:[0,0,1]
	s_nop 0
	global_store_dwordx4 v77, v[242:245], s[6:7]
	ds_read_b32 v226, v214
	ds_read_b32 v227, v214 offset:512
	ds_read_b32 v228, v214 offset:1024
	ds_read_b32 v229, v214 offset:1536
	ds_read_b32 v230, v214 offset:2048
	ds_read_b32 v231, v214 offset:2560
	ds_read_b32 v232, v214 offset:3072
	ds_read_b32 v233, v214 offset:3584
	ds_read_b32 v234, v214 offset:4096
	ds_read_b32 v235, v214 offset:4608
	ds_read_b32 v236, v214 offset:5120
	ds_read_b32 v237, v214 offset:5632
	ds_read_b32 v238, v214 offset:6144
	ds_read_b32 v239, v214 offset:6656
	ds_read_b32 v240, v214 offset:7168
	ds_read_b32 v241, v214 offset:7680
	s_waitcnt lgkmcnt(0)
	v_max_f32_e32 v226, v226, v226
	v_max_f32_e32 v227, v227, v227
	v_max_f32_e32 v228, v228, v228
	v_max_f32_e32 v229, v229, v229
	v_max_f32_e32 v230, v230, v230
	v_max_f32_e32 v231, v231, v231
	v_max_f32_e32 v232, v232, v232
	v_max_f32_e32 v233, v233, v233
	v_max_f32_e32 v234, v234, v234
	v_max_f32_e32 v235, v235, v235
	v_max_f32_e32 v236, v236, v236
	v_max_f32_e32 v237, v237, v237
	v_max_f32_e32 v238, v238, v238
	v_max_f32_e32 v239, v239, v239
	v_max_f32_e32 v240, v240, v240
	v_max_f32_e32 v241, v241, v241
	v_med3_f32 v226, v226, s62, v95
	v_med3_f32 v227, v227, s62, v95
	v_med3_f32 v228, v228, s62, v95
	v_med3_f32 v229, v229, s62, v95
	v_med3_f32 v230, v230, s62, v95
	v_med3_f32 v231, v231, s62, v95
	v_med3_f32 v232, v232, s62, v95
	v_med3_f32 v233, v233, s62, v95
	v_med3_f32 v234, v234, s62, v95
	v_med3_f32 v235, v235, s62, v95
	v_med3_f32 v236, v236, s62, v95
	v_med3_f32 v237, v237, s62, v95
	v_med3_f32 v238, v238, s62, v95
	v_med3_f32 v239, v239, s62, v95
	v_med3_f32 v240, v240, s62, v95
	v_med3_f32 v241, v241, s62, v95
	v_mov_b32_e32 v242, 0
	v_mov_b32_e32 v243, 0
	v_mov_b32_e32 v244, 0
	v_mov_b32_e32 v245, 0
	v_cvt_pk_fp8_f32 v242, v226, v227
	v_cvt_pk_fp8_f32 v243, v230, v231
	v_cvt_pk_fp8_f32 v244, v234, v235
	v_cvt_pk_fp8_f32 v245, v238, v239
	v_cvt_pk_fp8_f32 v242, v228, v229 op_sel:[0,0,1]
	v_cvt_pk_fp8_f32 v243, v232, v233 op_sel:[0,0,1]
	v_cvt_pk_fp8_f32 v244, v236, v237 op_sel:[0,0,1]
	v_cvt_pk_fp8_f32 v245, v240, v241 op_sel:[0,0,1]
	s_nop 0
	global_store_dwordx4 v78, v[242:245], s[6:7]
	s_waitcnt vmcnt(12)
	v_mul_f32_e32 v144, v34, v144
	v_mul_f32_e32 v145, v34, v145
	v_mul_f32_e32 v146, v34, v146
	v_mul_f32_e32 v147, v34, v147
	ds_write_b128 v209, v[144:147]
	v_mul_f32_e32 v148, v35, v148
	v_mul_f32_e32 v149, v35, v149
	v_mul_f32_e32 v150, v35, v150
	v_mul_f32_e32 v151, v35, v151
	ds_write_b128 v209, v[148:151] offset:1024
	v_mul_f32_e32 v152, v36, v152
	v_mul_f32_e32 v153, v36, v153
	v_mul_f32_e32 v154, v36, v154
	v_mul_f32_e32 v155, v36, v155
	ds_write_b128 v209, v[152:155] offset:2048
	v_mul_f32_e32 v156, v37, v156
	v_mul_f32_e32 v157, v37, v157
	v_mul_f32_e32 v158, v37, v158
	v_mul_f32_e32 v159, v37, v159
	ds_write_b128 v209, v[156:159] offset:3072
	v_mul_f32_e32 v160, v38, v160
	v_mul_f32_e32 v161, v38, v161
	v_mul_f32_e32 v162, v38, v162
	v_mul_f32_e32 v163, v38, v163
	ds_write_b128 v209, v[160:163] offset:4096
	v_mul_f32_e32 v164, v39, v164
	v_mul_f32_e32 v165, v39, v165
	v_mul_f32_e32 v166, v39, v166
	v_mul_f32_e32 v167, v39, v167
	ds_write_b128 v209, v[164:167] offset:5120
	v_mul_f32_e32 v168, v40, v168
	v_mul_f32_e32 v169, v40, v169
	v_mul_f32_e32 v170, v40, v170
	v_mul_f32_e32 v171, v40, v171
	ds_write_b128 v209, v[168:171] offset:6144
	v_mul_f32_e32 v172, v41, v172
	v_mul_f32_e32 v173, v41, v173
	v_mul_f32_e32 v174, v41, v174
	v_mul_f32_e32 v175, v41, v175
	ds_write_b128 v209, v[172:175] offset:7168
	s_waitcnt lgkmcnt(0)
	s_barrier
; #define GAS __attribute__((address_space(1)))
; #define LAS __attribute__((address_space(3)))
; #define LDS_WAIT() asm volatile("s_waitcnt lgkmcnt(0)" ::: "memory")
; __device__ __forceinline__ unsigned pk4_fp8(float a, float b, float c, float d) {
;     a = fminf(fmaxf(a, -448.f), 448.f); b = fminf(fmaxf(b, -448.f), 448.f); c = fminf(fmaxf(c, -448.f), 448.f); d = fminf(fmaxf(d, -448.f), 448.f);
;     int w = __builtin_amdgcn_cvt_pk_fp8_f32(a, b, 0, false); w = __builtin_amdgcn_cvt_pk_fp8_f32(c, d, w, true); return (unsigned)w; }
;     const int pr = item >> 1, kb = 2 * (pr / nblk) + (item & 1), nb = pr % nblk, k0 = 64 * kb, n0 = 32 * nb;
;     const int nr = n0 + (lane & 31); const int sc = MAP == 1 ? src_col_in(nr) : nr;
;     float v[32];
; #pragma unroll
;     for (int i = 0; i < 32; ++i) v[i] = sc >= 0 ? W[(size_t)(k0 + 2 * i + (lane >> 5)) * Nsrc + sc] : 0.f;
; #pragma unroll
;     for (int i = 0; i < 32; ++i) { const int k = k0 + 2 * i + (lane >> 5); float x = v[i] * wscale; if (KS) x *= (k < ksplit ? ksA[k] : ksB[k - ksplit]); scr[(2 * i + (lane >> 5)) * 33 + (lane & 31)] = x; }
;     LDS_WAIT(); asm volatile("" ::: "memory");
;     const int c = lane & 7;
; #pragma unroll
;     for (int j = 0; j < 4; ++j) { const int n = (lane >> 3) + 8 * j; const LAS float* s = scr + (8 * c) * 33 + n;
;         const unsigned long long o = (unsigned long long)pg8::pk4_fp8(s[0 * 33], s[1 * 33], s[2 * 33], s[3 * 33]) | ((unsigned long long)pg8::pk4_fp8(s[4 * 33], s[5 * 33], s[6 * 33], s[7 * 33]) << 32);
;         *(GAS unsigned long long*)(WT + (size_t)(n0 + n) * K + k0 + 8 * c) = o; }
;     LDS_WAIT(); asm volatile("" ::: "memory");
; }
	s_add_u32 s8, s34, 0xa000
	s_addc_u32 s9, s35, 0
	global_load_dwordx4 v[144:147], v74, s[8:9]
	s_add_u32 s8, s8, 0x20000
	s_addc_u32 s9, s9, 0
	global_load_dwordx4 v[148:151], v74, s[8:9]
	s_add_u32 s8, s8, 0x20000
	s_addc_u32 s9, s9, 0
	global_load_dwordx4 v[152:155], v74, s[8:9]
	s_add_u32 s8, s8, 0x20000
	s_addc_u32 s9, s9, 0
	global_load_dwordx4 v[156:159], v74, s[8:9]
	s_add_u32 s8, s8, 0x20000
	s_addc_u32 s9, s9, 0
	global_load_dwordx4 v[160:163], v74, s[8:9]
	s_add_u32 s8, s8, 0x20000
	s_addc_u32 s9, s9, 0
	global_load_dwordx4 v[164:167], v74, s[8:9]
	s_add_u32 s8, s8, 0x20000
	s_addc_u32 s9, s9, 0
	global_load_dwordx4 v[168:171], v74, s[8:9]
	s_add_u32 s8, s8, 0x20000
	s_addc_u32 s9, s9, 0
	global_load_dwordx4 v[172:175], v74, s[8:9]
	s_add_u32 s6, s36, 0x2000000
	s_addc_u32 s7, s37, 0
	ds_read_b32 v226, v211
	ds_read_b32 v227, v211 offset:512
	ds_read_b32 v228, v211 offset:1024
	ds_read_b32 v229, v211 offset:1536
	ds_read_b32 v230, v211 offset:2048
	ds_read_b32 v231, v211 offset:2560
	ds_read_b32 v232, v211 offset:3072
	ds_read_b32 v233, v211 offset:3584
	ds_read_b32 v234, v211 offset:4096
	ds_read_b32 v235, v211 offset:4608
	ds_read_b32 v236, v211 offset:5120
	ds_read_b32 v237, v211 offset:5632
	ds_read_b32 v238, v211 offset:6144
	ds_read_b32 v239, v211 offset:6656
	ds_read_b32 v240, v211 offset:7168
	ds_read_b32 v241, v211 offset:7680
	s_waitcnt lgkmcnt(0)
	v_max_f32_e32 v226, v226, v226
	v_max_f32_e32 v227, v227, v227
	v_max_f32_e32 v228, v228, v228
	v_max_f32_e32 v229, v229, v229
	v_max_f32_e32 v230, v230, v230
	v_max_f32_e32 v231, v231, v231
	v_max_f32_e32 v232, v232, v232
	v_max_f32_e32 v233, v233, v233
	v_max_f32_e32 v234, v234, v234
	v_max_f32_e32 v235, v235, v235
	v_max_f32_e32 v236, v236, v236
	v_max_f32_e32 v237, v237, v237
	v_max_f32_e32 v238, v238, v238
	v_max_f32_e32 v239, v239, v239
	v_max_f32_e32 v240, v240, v240
	v_max_f32_e32 v241, v241, v241
	v_med3_f32 v226, v226, s62, v95
	v_med3_f32 v227, v227, s62, v95
	v_med3_f32 v228, v228, s62, v95
	v_med3_f32 v229, v229, s62, v95
	v_med3_f32 v230, v230, s62, v95
	v_med3_f32 v231, v231, s62, v95
	v_med3_f32 v232, v232, s62, v95
	v_med3_f32 v233, v233, s62, v95
	v_med3_f32 v234, v234, s62, v95
	v_med3_f32 v235, v235, s62, v95
	v_med3_f32 v236, v236, s62, v95
	v_med3_f32 v237, v237, s62, v95
	v_med3_f32 v238, v238, s62, v95
	v_med3_f32 v239, v239, s62, v95
	v_med3_f32 v240, v240, s62, v95
	v_med3_f32 v241, v241, s62, v95
	v_mov_b32_e32 v242, 0
	v_mov_b32_e32 v243, 0
	v_mov_b32_e32 v244, 0
	v_mov_b32_e32 v245, 0
	v_cvt_pk_fp8_f32 v242, v226, v227
	v_cvt_pk_fp8_f32 v243, v230, v231
	v_cvt_pk_fp8_f32 v244, v234, v235
	v_cvt_pk_fp8_f32 v245, v238, v239
	v_cvt_pk_fp8_f32 v242, v228, v229 op_sel:[0,0,1]
	v_cvt_pk_fp8_f32 v243, v232, v233 op_sel:[0,0,1]
	v_cvt_pk_fp8_f32 v244, v236, v237 op_sel:[0,0,1]
	v_cvt_pk_fp8_f32 v245, v240, v241 op_sel:[0,0,1]
	s_nop 0
	global_store_dwordx4 v77, v[242:245], s[6:7]
	ds_read_b32 v226, v213
	ds_read_b32 v227, v213 offset:512
	ds_read_b32 v228, v213 offset:1024
	ds_read_b32 v229, v213 offset:1536
	ds_read_b32 v230, v213 offset:2048
	ds_read_b32 v231, v213 offset:2560
	ds_read_b32 v232, v213 offset:3072
	ds_read_b32 v233, v213 offset:3584
	ds_read_b32 v234, v213 offset:4096
	ds_read_b32 v235, v213 offset:4608
	ds_read_b32 v236, v213 offset:5120
	ds_read_b32 v237, v213 offset:5632
	ds_read_b32 v238, v213 offset:6144
	ds_read_b32 v239, v213 offset:6656
	ds_read_b32 v240, v213 offset:7168
	ds_read_b32 v241, v213 offset:7680
	s_waitcnt lgkmcnt(0)
	v_max_f32_e32 v226, v226, v226
	v_max_f32_e32 v227, v227, v227
	v_max_f32_e32 v228, v228, v228
	v_max_f32_e32 v229, v229, v229
	v_max_f32_e32 v230, v230, v230
	v_max_f32_e32 v231, v231, v231
	v_max_f32_e32 v232, v232, v232
	v_max_f32_e32 v233, v233, v233
	v_max_f32_e32 v234, v234, v234
	v_max_f32_e32 v235, v235, v235
	v_max_f32_e32 v236, v236, v236
	v_max_f32_e32 v237, v237, v237
	v_max_f32_e32 v238, v238, v238
	v_max_f32_e32 v239, v239, v239
	v_max_f32_e32 v240, v240, v240
	v_max_f32_e32 v241, v241, v241
	v_med3_f32 v226, v226, s62, v95
	v_med3_f32 v227, v227, s62, v95
	v_med3_f32 v228, v228, s62, v95
	v_med3_f32 v229, v229, s62, v95
	v_med3_f32 v230, v230, s62, v95
	v_med3_f32 v231, v231, s62, v95
	v_med3_f32 v232, v232, s62, v95
	v_med3_f32 v233, v233, s62, v95
	v_med3_f32 v234, v234, s62, v95
	v_med3_f32 v235, v235, s62, v95
	v_med3_f32 v236, v236, s62, v95
	v_med3_f32 v237, v237, s62, v95
	v_med3_f32 v238, v238, s62, v95
	v_med3_f32 v239, v239, s62, v95
	v_med3_f32 v240, v240, s62, v95
	v_med3_f32 v241, v241, s62, v95
	v_mov_b32_e32 v242, 0
	v_mov_b32_e32 v243, 0
	v_mov_b32_e32 v244, 0
	v_mov_b32_e32 v245, 0
	v_cvt_pk_fp8_f32 v242, v226, v227
	v_cvt_pk_fp8_f32 v243, v230, v231
	v_cvt_pk_fp8_f32 v244, v234, v235
	v_cvt_pk_fp8_f32 v245, v238, v239
	v_cvt_pk_fp8_f32 v242, v228, v229 op_sel:[0,0,1]
	v_cvt_pk_fp8_f32 v243, v232, v233 op_sel:[0,0,1]
	v_cvt_pk_fp8_f32 v244, v236, v237 op_sel:[0,0,1]
	v_cvt_pk_fp8_f32 v245, v240, v241 op_sel:[0,0,1]
	s_nop 0
	global_store_dwordx4 v78, v[242:245], s[6:7]
	s_waitcnt vmcnt(12)
	v_mul_f32_e32 v176, v34, v176
	v_mul_f32_e32 v177, v34, v177
	v_mul_f32_e32 v178, v34, v178
	v_mul_f32_e32 v179, v34, v179
	ds_write_b128 v210, v[176:179]
	v_mul_f32_e32 v180, v35, v180
	v_mul_f32_e32 v181, v35, v181
	v_mul_f32_e32 v182, v35, v182
	v_mul_f32_e32 v183, v35, v183
	ds_write_b128 v210, v[180:183] offset:1024
	v_mul_f32_e32 v184, v36, v184
	v_mul_f32_e32 v185, v36, v185
	v_mul_f32_e32 v186, v36, v186
	v_mul_f32_e32 v187, v36, v187
	ds_write_b128 v210, v[184:187] offset:2048
	v_mul_f32_e32 v188, v37, v188
	v_mul_f32_e32 v189, v37, v189
	v_mul_f32_e32 v190, v37, v190
	v_mul_f32_e32 v191, v37, v191
	ds_write_b128 v210, v[188:191] offset:3072
	v_mul_f32_e32 v192, v38, v192
	v_mul_f32_e32 v193, v38, v193
	v_mul_f32_e32 v194, v38, v194
	v_mul_f32_e32 v195, v38, v195
	ds_write_b128 v210, v[192:195] offset:4096
	v_mul_f32_e32 v196, v39, v196
	v_mul_f32_e32 v197, v39, v197
	v_mul_f32_e32 v198, v39, v198
	v_mul_f32_e32 v199, v39, v199
	ds_write_b128 v210, v[196:199] offset:5120
	v_mul_f32_e32 v200, v40, v200
	v_mul_f32_e32 v201, v40, v201
	v_mul_f32_e32 v202, v40, v202
	v_mul_f32_e32 v203, v40, v203
	ds_write_b128 v210, v[200:203] offset:6144
	v_mul_f32_e32 v204, v41, v204
	v_mul_f32_e32 v205, v41, v205
	v_mul_f32_e32 v206, v41, v206
	v_mul_f32_e32 v207, v41, v207
	ds_write_b128 v210, v[204:207] offset:7168
	s_waitcnt lgkmcnt(0)
	s_barrier
; #define GAS __attribute__((address_space(1)))
; #define LAS __attribute__((address_space(3)))
; #define LDS_WAIT() asm volatile("s_waitcnt lgkmcnt(0)" ::: "memory")
; __device__ __forceinline__ unsigned pk4_fp8(float a, float b, float c, float d) {
;     a = fminf(fmaxf(a, -448.f), 448.f); b = fminf(fmaxf(b, -448.f), 448.f); c = fminf(fmaxf(c, -448.f), 448.f); d = fminf(fmaxf(d, -448.f), 448.f);
;     int w = __builtin_amdgcn_cvt_pk_fp8_f32(a, b, 0, false); w = __builtin_amdgcn_cvt_pk_fp8_f32(c, d, w, true); return (unsigned)w; }
;     const int pr = item >> 1, kb = 2 * (pr / nblk) + (item & 1), nb = pr % nblk, k0 = 64 * kb, n0 = 32 * nb;
;     const int nr = n0 + (lane & 31); const int sc = MAP == 1 ? src_col_in(nr) : nr;
;     float v[32];
; #pragma unroll
;     for (int i = 0; i < 32; ++i) v[i] = sc >= 0 ? W[(size_t)(k0 + 2 * i + (lane >> 5)) * Nsrc + sc] : 0.f;
; #pragma unroll
;     for (int i = 0; i < 32; ++i) { const int k = k0 + 2 * i + (lane >> 5); float x = v[i] * wscale; if (KS) x *= (k < ksplit ? ksA[k] : ksB[k - ksplit]); scr[(2 * i + (lane >> 5)) * 33 + (lane & 31)] = x; }
;     LDS_WAIT(); asm volatile("" ::: "memory");
;     const int c = lane & 7;
; #pragma unroll
;     for (int j = 0; j < 4; ++j) { const int n = (lane >> 3) + 8 * j; const LAS float* s = scr + (8 * c) * 33 + n;
;         const unsigned long long o = (unsigned long long)pg8::pk4_fp8(s[0 * 33], s[1 * 33], s[2 * 33], s[3 * 33]) | ((unsigned long long)pg8::pk4_fp8(s[4 * 33], s[5 * 33], s[6 * 33], s[7 * 33]) << 32);
;         *(GAS unsigned long long*)(WT + (size_t)(n0 + n) * K + k0 + 8 * c) = o; }
;     LDS_WAIT(); asm volatile("" ::: "memory");
; }
	s_add_u32 s8, s34, 0xb000
	s_addc_u32 s9, s35, 0
	global_load_dwordx4 v[176:179], v74, s[8:9]
	s_add_u32 s8, s8, 0x20000
	s_addc_u32 s9, s9, 0
	global_load_dwordx4 v[180:183], v74, s[8:9]
	s_add_u32 s8, s8, 0x20000
	s_addc_u32 s9, s9, 0
	global_load_dwordx4 v[184:187], v74, s[8:9]
	s_add_u32 s8, s8, 0x20000
	s_addc_u32 s9, s9, 0
	global_load_dwordx4 v[188:191], v74, s[8:9]
	s_add_u32 s8, s8, 0x20000
	s_addc_u32 s9, s9, 0
	global_load_dwordx4 v[192:195], v74, s[8:9]
	s_add_u32 s8, s8, 0x20000
	s_addc_u32 s9, s9, 0
	global_load_dwordx4 v[196:199], v74, s[8:9]
	s_add_u32 s8, s8, 0x20000
	s_addc_u32 s9, s9, 0
	global_load_dwordx4 v[200:203], v74, s[8:9]
	s_add_u32 s8, s8, 0x20000
	s_addc_u32 s9, s9, 0
	global_load_dwordx4 v[204:207], v74, s[8:9]
	s_add_u32 s6, s36, 0x2400000
	s_addc_u32 s7, s37, 0
	ds_read_b32 v226, v212
	ds_read_b32 v227, v212 offset:512
	ds_read_b32 v228, v212 offset:1024
	ds_read_b32 v229, v212 offset:1536
	ds_read_b32 v230, v212 offset:2048
	ds_read_b32 v231, v212 offset:2560
	ds_read_b32 v232, v212 offset:3072
	ds_read_b32 v233, v212 offset:3584
	ds_read_b32 v234, v212 offset:4096
	ds_read_b32 v235, v212 offset:4608
	ds_read_b32 v236, v212 offset:5120
	ds_read_b32 v237, v212 offset:5632
	ds_read_b32 v238, v212 offset:6144
	ds_read_b32 v239, v212 offset:6656
	ds_read_b32 v240, v212 offset:7168
	ds_read_b32 v241, v212 offset:7680
	s_waitcnt lgkmcnt(0)
	v_max_f32_e32 v226, v226, v226
	v_max_f32_e32 v227, v227, v227
	v_max_f32_e32 v228, v228, v228
	v_max_f32_e32 v229, v229, v229
	v_max_f32_e32 v230, v230, v230
	v_max_f32_e32 v231, v231, v231
	v_max_f32_e32 v232, v232, v232
	v_max_f32_e32 v233, v233, v233
	v_max_f32_e32 v234, v234, v234
	v_max_f32_e32 v235, v235, v235
	v_max_f32_e32 v236, v236, v236
	v_max_f32_e32 v237, v237, v237
	v_max_f32_e32 v238, v238, v238
	v_max_f32_e32 v239, v239, v239
	v_max_f32_e32 v240, v240, v240
	v_max_f32_e32 v241, v241, v241
	v_med3_f32 v226, v226, s62, v95
	v_med3_f32 v227, v227, s62, v95
	v_med3_f32 v228, v228, s62, v95
	v_med3_f32 v229, v229, s62, v95
	v_med3_f32 v230, v230, s62, v95
	v_med3_f32 v231, v231, s62, v95
	v_med3_f32 v232, v232, s62, v95
	v_med3_f32 v233, v233, s62, v95
	v_med3_f32 v234, v234, s62, v95
	v_med3_f32 v235, v235, s62, v95
	v_med3_f32 v236, v236, s62, v95
	v_med3_f32 v237, v237, s62, v95
	v_med3_f32 v238, v238, s62, v95
	v_med3_f32 v239, v239, s62, v95
	v_med3_f32 v240, v240, s62, v95
	v_med3_f32 v241, v241, s62, v95
	v_mov_b32_e32 v242, 0
	v_mov_b32_e32 v243, 0
	v_mov_b32_e32 v244, 0
	v_mov_b32_e32 v245, 0
	v_cvt_pk_fp8_f32 v242, v226, v227
	v_cvt_pk_fp8_f32 v243, v230, v231
	v_cvt_pk_fp8_f32 v244, v234, v235
	v_cvt_pk_fp8_f32 v245, v238, v239
	v_cvt_pk_fp8_f32 v242, v228, v229 op_sel:[0,0,1]
	v_cvt_pk_fp8_f32 v243, v232, v233 op_sel:[0,0,1]
	v_cvt_pk_fp8_f32 v244, v236, v237 op_sel:[0,0,1]
	v_cvt_pk_fp8_f32 v245, v240, v241 op_sel:[0,0,1]
	s_nop 0
	global_store_dwordx4 v77, v[242:245], s[6:7]
	ds_read_b32 v226, v214
	ds_read_b32 v227, v214 offset:512
	ds_read_b32 v228, v214 offset:1024
	ds_read_b32 v229, v214 offset:1536
	ds_read_b32 v230, v214 offset:2048
	ds_read_b32 v231, v214 offset:2560
	ds_read_b32 v232, v214 offset:3072
	ds_read_b32 v233, v214 offset:3584
	ds_read_b32 v234, v214 offset:4096
	ds_read_b32 v235, v214 offset:4608
	ds_read_b32 v236, v214 offset:5120
	ds_read_b32 v237, v214 offset:5632
	ds_read_b32 v238, v214 offset:6144
	ds_read_b32 v239, v214 offset:6656
	ds_read_b32 v240, v214 offset:7168
	ds_read_b32 v241, v214 offset:7680
	s_waitcnt lgkmcnt(0)
	v_max_f32_e32 v226, v226, v226
	v_max_f32_e32 v227, v227, v227
	v_max_f32_e32 v228, v228, v228
	v_max_f32_e32 v229, v229, v229
	v_max_f32_e32 v230, v230, v230
	v_max_f32_e32 v231, v231, v231
	v_max_f32_e32 v232, v232, v232
	v_max_f32_e32 v233, v233, v233
	v_max_f32_e32 v234, v234, v234
	v_max_f32_e32 v235, v235, v235
	v_max_f32_e32 v236, v236, v236
	v_max_f32_e32 v237, v237, v237
	v_max_f32_e32 v238, v238, v238
	v_max_f32_e32 v239, v239, v239
	v_max_f32_e32 v240, v240, v240
	v_max_f32_e32 v241, v241, v241
	v_med3_f32 v226, v226, s62, v95
	v_med3_f32 v227, v227, s62, v95
	v_med3_f32 v228, v228, s62, v95
	v_med3_f32 v229, v229, s62, v95
	v_med3_f32 v230, v230, s62, v95
	v_med3_f32 v231, v231, s62, v95
	v_med3_f32 v232, v232, s62, v95
	v_med3_f32 v233, v233, s62, v95
	v_med3_f32 v234, v234, s62, v95
	v_med3_f32 v235, v235, s62, v95
	v_med3_f32 v236, v236, s62, v95
	v_med3_f32 v237, v237, s62, v95
	v_med3_f32 v238, v238, s62, v95
	v_med3_f32 v239, v239, s62, v95
	v_med3_f32 v240, v240, s62, v95
	v_med3_f32 v241, v241, s62, v95
	v_mov_b32_e32 v242, 0
	v_mov_b32_e32 v243, 0
	v_mov_b32_e32 v244, 0
	v_mov_b32_e32 v245, 0
	v_cvt_pk_fp8_f32 v242, v226, v227
	v_cvt_pk_fp8_f32 v243, v230, v231
	v_cvt_pk_fp8_f32 v244, v234, v235
	v_cvt_pk_fp8_f32 v245, v238, v239
	v_cvt_pk_fp8_f32 v242, v228, v229 op_sel:[0,0,1]
	v_cvt_pk_fp8_f32 v243, v232, v233 op_sel:[0,0,1]
	v_cvt_pk_fp8_f32 v244, v236, v237 op_sel:[0,0,1]
	v_cvt_pk_fp8_f32 v245, v240, v241 op_sel:[0,0,1]
	s_nop 0
	global_store_dwordx4 v78, v[242:245], s[6:7]
	s_waitcnt vmcnt(12)
	v_mul_f32_e32 v144, v34, v144
	v_mul_f32_e32 v145, v34, v145
	v_mul_f32_e32 v146, v34, v146
	v_mul_f32_e32 v147, v34, v147
	ds_write_b128 v209, v[144:147]
	v_mul_f32_e32 v148, v35, v148
	v_mul_f32_e32 v149, v35, v149
	v_mul_f32_e32 v150, v35, v150
	v_mul_f32_e32 v151, v35, v151
	ds_write_b128 v209, v[148:151] offset:1024
	v_mul_f32_e32 v152, v36, v152
	v_mul_f32_e32 v153, v36, v153
	v_mul_f32_e32 v154, v36, v154
	v_mul_f32_e32 v155, v36, v155
	ds_write_b128 v209, v[152:155] offset:2048
	v_mul_f32_e32 v156, v37, v156
	v_mul_f32_e32 v157, v37, v157
	v_mul_f32_e32 v158, v37, v158
	v_mul_f32_e32 v159, v37, v159
	ds_write_b128 v209, v[156:159] offset:3072
	v_mul_f32_e32 v160, v38, v160
	v_mul_f32_e32 v161, v38, v161
	v_mul_f32_e32 v162, v38, v162
	v_mul_f32_e32 v163, v38, v163
	ds_write_b128 v209, v[160:163] offset:4096
	v_mul_f32_e32 v164, v39, v164
	v_mul_f32_e32 v165, v39, v165
	v_mul_f32_e32 v166, v39, v166
	v_mul_f32_e32 v167, v39, v167
	ds_write_b128 v209, v[164:167] offset:5120
	v_mul_f32_e32 v168, v40, v168
	v_mul_f32_e32 v169, v40, v169
	v_mul_f32_e32 v170, v40, v170
	v_mul_f32_e32 v171, v40, v171
	ds_write_b128 v209, v[168:171] offset:6144
	v_mul_f32_e32 v172, v41, v172
	v_mul_f32_e32 v173, v41, v173
	v_mul_f32_e32 v174, v41, v174
	v_mul_f32_e32 v175, v41, v175
	ds_write_b128 v209, v[172:175] offset:7168
	s_waitcnt lgkmcnt(0)
	s_barrier
; #define GAS __attribute__((address_space(1)))
; #define LAS __attribute__((address_space(3)))
; #define LDS_WAIT() asm volatile("s_waitcnt lgkmcnt(0)" ::: "memory")
; __device__ __forceinline__ unsigned pk4_fp8(float a, float b, float c, float d) {
;     a = fminf(fmaxf(a, -448.f), 448.f); b = fminf(fmaxf(b, -448.f), 448.f); c = fminf(fmaxf(c, -448.f), 448.f); d = fminf(fmaxf(d, -448.f), 448.f);
;     int w = __builtin_amdgcn_cvt_pk_fp8_f32(a, b, 0, false); w = __builtin_amdgcn_cvt_pk_fp8_f32(c, d, w, true); return (unsigned)w; }
;     const int pr = item >> 1, kb = 2 * (pr / nblk) + (item & 1), nb = pr % nblk, k0 = 64 * kb, n0 = 32 * nb;
;     const int nr = n0 + (lane & 31); const int sc = MAP == 1 ? src_col_in(nr) : nr;
;     float v[32];
; #pragma unroll
;     for (int i = 0; i < 32; ++i) v[i] = sc >= 0 ? W[(size_t)(k0 + 2 * i + (lane >> 5)) * Nsrc + sc] : 0.f;
; #pragma unroll
;     for (int i = 0; i < 32; ++i) { const int k = k0 + 2 * i + (lane >> 5); float x = v[i] * wscale; if (KS) x *= (k < ksplit ? ksA[k] : ksB[k - ksplit]); scr[(2 * i + (lane >> 5)) * 33 + (lane & 31)] = x; }
;     LDS_WAIT(); asm volatile("" ::: "memory");
;     const int c = lane & 7;
; #pragma unroll
;     for (int j = 0; j < 4; ++j) { const int n = (lane >> 3) + 8 * j; const LAS float* s = scr + (8 * c) * 33 + n;
;         const unsigned long long o = (unsigned long long)pg8::pk4_fp8(s[0 * 33], s[1 * 33], s[2 * 33], s[3 * 33]) | ((unsigned long long)pg8::pk4_fp8(s[4 * 33], s[5 * 33], s[6 * 33], s[7 * 33]) << 32);
;         *(GAS unsigned long long*)(WT + (size_t)(n0 + n) * K + k0 + 8 * c) = o; }
;     LDS_WAIT(); asm volatile("" ::: "memory");
; }
	s_add_u32 s8, s34, 0xc000
	s_addc_u32 s9, s35, 0
	global_load_dwordx4 v[144:147], v74, s[8:9]
	s_add_u32 s8, s8, 0x20000
	s_addc_u32 s9, s9, 0
	global_load_dwordx4 v[148:151], v74, s[8:9]
	s_add_u32 s8, s8, 0x20000
	s_addc_u32 s9, s9, 0
	global_load_dwordx4 v[152:155], v74, s[8:9]
	s_add_u32 s8, s8, 0x20000
	s_addc_u32 s9, s9, 0
	global_load_dwordx4 v[156:159], v74, s[8:9]
	s_add_u32 s8, s8, 0x20000
	s_addc_u32 s9, s9, 0
	global_load_dwordx4 v[160:163], v74, s[8:9]
	s_add_u32 s8, s8, 0x20000
	s_addc_u32 s9, s9, 0
	global_load_dwordx4 v[164:167], v74, s[8:9]
	s_add_u32 s8, s8, 0x20000
	s_addc_u32 s9, s9, 0
	global_load_dwordx4 v[168:171], v74, s[8:9]
	s_add_u32 s8, s8, 0x20000
	s_addc_u32 s9, s9, 0
	global_load_dwordx4 v[172:175], v74, s[8:9]
	s_add_u32 s6, s36, 0x2800000
	s_addc_u32 s7, s37, 0
	ds_read_b32 v226, v211
	ds_read_b32 v227, v211 offset:512
	ds_read_b32 v228, v211 offset:1024
	ds_read_b32 v229, v211 offset:1536
	ds_read_b32 v230, v211 offset:2048
	ds_read_b32 v231, v211 offset:2560
	ds_read_b32 v232, v211 offset:3072
	ds_read_b32 v233, v211 offset:3584
	ds_read_b32 v234, v211 offset:4096
	ds_read_b32 v235, v211 offset:4608
	ds_read_b32 v236, v211 offset:5120
	ds_read_b32 v237, v211 offset:5632
	ds_read_b32 v238, v211 offset:6144
	ds_read_b32 v239, v211 offset:6656
	ds_read_b32 v240, v211 offset:7168
	ds_read_b32 v241, v211 offset:7680
	s_waitcnt lgkmcnt(0)
	v_max_f32_e32 v226, v226, v226
	v_max_f32_e32 v227, v227, v227
	v_max_f32_e32 v228, v228, v228
	v_max_f32_e32 v229, v229, v229
	v_max_f32_e32 v230, v230, v230
	v_max_f32_e32 v231, v231, v231
	v_max_f32_e32 v232, v232, v232
	v_max_f32_e32 v233, v233, v233
	v_max_f32_e32 v234, v234, v234
	v_max_f32_e32 v235, v235, v235
	v_max_f32_e32 v236, v236, v236
	v_max_f32_e32 v237, v237, v237
	v_max_f32_e32 v238, v238, v238
	v_max_f32_e32 v239, v239, v239
	v_max_f32_e32 v240, v240, v240
	v_max_f32_e32 v241, v241, v241
	v_med3_f32 v226, v226, s62, v95
	v_med3_f32 v227, v227, s62, v95
	v_med3_f32 v228, v228, s62, v95
	v_med3_f32 v229, v229, s62, v95
	v_med3_f32 v230, v230, s62, v95
	v_med3_f32 v231, v231, s62, v95
	v_med3_f32 v232, v232, s62, v95
	v_med3_f32 v233, v233, s62, v95
	v_med3_f32 v234, v234, s62, v95
	v_med3_f32 v235, v235, s62, v95
	v_med3_f32 v236, v236, s62, v95
	v_med3_f32 v237, v237, s62, v95
	v_med3_f32 v238, v238, s62, v95
	v_med3_f32 v239, v239, s62, v95
	v_med3_f32 v240, v240, s62, v95
	v_med3_f32 v241, v241, s62, v95
	v_mov_b32_e32 v242, 0
	v_mov_b32_e32 v243, 0
	v_mov_b32_e32 v244, 0
	v_mov_b32_e32 v245, 0
	v_cvt_pk_fp8_f32 v242, v226, v227
	v_cvt_pk_fp8_f32 v243, v230, v231
	v_cvt_pk_fp8_f32 v244, v234, v235
	v_cvt_pk_fp8_f32 v245, v238, v239
	v_cvt_pk_fp8_f32 v242, v228, v229 op_sel:[0,0,1]
	v_cvt_pk_fp8_f32 v243, v232, v233 op_sel:[0,0,1]
	v_cvt_pk_fp8_f32 v244, v236, v237 op_sel:[0,0,1]
	v_cvt_pk_fp8_f32 v245, v240, v241 op_sel:[0,0,1]
	s_nop 0
	global_store_dwordx4 v77, v[242:245], s[6:7]
	ds_read_b32 v226, v213
	ds_read_b32 v227, v213 offset:512
	ds_read_b32 v228, v213 offset:1024
	ds_read_b32 v229, v213 offset:1536
	ds_read_b32 v230, v213 offset:2048
	ds_read_b32 v231, v213 offset:2560
	ds_read_b32 v232, v213 offset:3072
	ds_read_b32 v233, v213 offset:3584
	ds_read_b32 v234, v213 offset:4096
	ds_read_b32 v235, v213 offset:4608
	ds_read_b32 v236, v213 offset:5120
	ds_read_b32 v237, v213 offset:5632
	ds_read_b32 v238, v213 offset:6144
	ds_read_b32 v239, v213 offset:6656
	ds_read_b32 v240, v213 offset:7168
	ds_read_b32 v241, v213 offset:7680
	s_waitcnt lgkmcnt(0)
	v_max_f32_e32 v226, v226, v226
	v_max_f32_e32 v227, v227, v227
	v_max_f32_e32 v228, v228, v228
	v_max_f32_e32 v229, v229, v229
	v_max_f32_e32 v230, v230, v230
	v_max_f32_e32 v231, v231, v231
	v_max_f32_e32 v232, v232, v232
	v_max_f32_e32 v233, v233, v233
	v_max_f32_e32 v234, v234, v234
	v_max_f32_e32 v235, v235, v235
	v_max_f32_e32 v236, v236, v236
	v_max_f32_e32 v237, v237, v237
	v_max_f32_e32 v238, v238, v238
	v_max_f32_e32 v239, v239, v239
	v_max_f32_e32 v240, v240, v240
	v_max_f32_e32 v241, v241, v241
	v_med3_f32 v226, v226, s62, v95
	v_med3_f32 v227, v227, s62, v95
	v_med3_f32 v228, v228, s62, v95
	v_med3_f32 v229, v229, s62, v95
	v_med3_f32 v230, v230, s62, v95
	v_med3_f32 v231, v231, s62, v95
	v_med3_f32 v232, v232, s62, v95
	v_med3_f32 v233, v233, s62, v95
	v_med3_f32 v234, v234, s62, v95
	v_med3_f32 v235, v235, s62, v95
	v_med3_f32 v236, v236, s62, v95
	v_med3_f32 v237, v237, s62, v95
	v_med3_f32 v238, v238, s62, v95
	v_med3_f32 v239, v239, s62, v95
	v_med3_f32 v240, v240, s62, v95
	v_med3_f32 v241, v241, s62, v95
	v_mov_b32_e32 v242, 0
	v_mov_b32_e32 v243, 0
	v_mov_b32_e32 v244, 0
	v_mov_b32_e32 v245, 0
	v_cvt_pk_fp8_f32 v242, v226, v227
	v_cvt_pk_fp8_f32 v243, v230, v231
	v_cvt_pk_fp8_f32 v244, v234, v235
	v_cvt_pk_fp8_f32 v245, v238, v239
	v_cvt_pk_fp8_f32 v242, v228, v229 op_sel:[0,0,1]
	v_cvt_pk_fp8_f32 v243, v232, v233 op_sel:[0,0,1]
	v_cvt_pk_fp8_f32 v244, v236, v237 op_sel:[0,0,1]
	v_cvt_pk_fp8_f32 v245, v240, v241 op_sel:[0,0,1]
	s_nop 0
	global_store_dwordx4 v78, v[242:245], s[6:7]
	s_waitcnt vmcnt(12)
	v_mul_f32_e32 v176, v34, v176
	v_mul_f32_e32 v177, v34, v177
	v_mul_f32_e32 v178, v34, v178
	v_mul_f32_e32 v179, v34, v179
	ds_write_b128 v210, v[176:179]
	v_mul_f32_e32 v180, v35, v180
	v_mul_f32_e32 v181, v35, v181
	v_mul_f32_e32 v182, v35, v182
	v_mul_f32_e32 v183, v35, v183
	ds_write_b128 v210, v[180:183] offset:1024
	v_mul_f32_e32 v184, v36, v184
	v_mul_f32_e32 v185, v36, v185
	v_mul_f32_e32 v186, v36, v186
	v_mul_f32_e32 v187, v36, v187
	ds_write_b128 v210, v[184:187] offset:2048
	v_mul_f32_e32 v188, v37, v188
	v_mul_f32_e32 v189, v37, v189
	v_mul_f32_e32 v190, v37, v190
	v_mul_f32_e32 v191, v37, v191
	ds_write_b128 v210, v[188:191] offset:3072
	v_mul_f32_e32 v192, v38, v192
	v_mul_f32_e32 v193, v38, v193
	v_mul_f32_e32 v194, v38, v194
	v_mul_f32_e32 v195, v38, v195
	ds_write_b128 v210, v[192:195] offset:4096
	v_mul_f32_e32 v196, v39, v196
	v_mul_f32_e32 v197, v39, v197
	v_mul_f32_e32 v198, v39, v198
	v_mul_f32_e32 v199, v39, v199
	ds_write_b128 v210, v[196:199] offset:5120
	v_mul_f32_e32 v200, v40, v200
	v_mul_f32_e32 v201, v40, v201
	v_mul_f32_e32 v202, v40, v202
	v_mul_f32_e32 v203, v40, v203
	ds_write_b128 v210, v[200:203] offset:6144
	v_mul_f32_e32 v204, v41, v204
	v_mul_f32_e32 v205, v41, v205
	v_mul_f32_e32 v206, v41, v206
	v_mul_f32_e32 v207, v41, v207
	ds_write_b128 v210, v[204:207] offset:7168
	s_waitcnt lgkmcnt(0)
	s_barrier
; #define GAS __attribute__((address_space(1)))
; #define LAS __attribute__((address_space(3)))
; #define LDS_WAIT() asm volatile("s_waitcnt lgkmcnt(0)" ::: "memory")
; __device__ __forceinline__ unsigned pk4_fp8(float a, float b, float c, float d) {
;     a = fminf(fmaxf(a, -448.f), 448.f); b = fminf(fmaxf(b, -448.f), 448.f); c = fminf(fmaxf(c, -448.f), 448.f); d = fminf(fmaxf(d, -448.f), 448.f);
;     int w = __builtin_amdgcn_cvt_pk_fp8_f32(a, b, 0, false); w = __builtin_amdgcn_cvt_pk_fp8_f32(c, d, w, true); return (unsigned)w; }
;     const int pr = item >> 1, kb = 2 * (pr / nblk) + (item & 1), nb = pr % nblk, k0 = 64 * kb, n0 = 32 * nb;
;     const int nr = n0 + (lane & 31); const int sc = MAP == 1 ? src_col_in(nr) : nr;
;     float v[32];
; #pragma unroll
;     for (int i = 0; i < 32; ++i) v[i] = sc >= 0 ? W[(size_t)(k0 + 2 * i + (lane >> 5)) * Nsrc + sc] : 0.f;
; #pragma unroll
;     for (int i = 0; i < 32; ++i) { const int k = k0 + 2 * i + (lane >> 5); float x = v[i] * wscale; if (KS) x *= (k < ksplit ? ksA[k] : ksB[k - ksplit]); scr[(2 * i + (lane >> 5)) * 33 + (lane & 31)] = x; }
;     LDS_WAIT(); asm volatile("" ::: "memory");
;     const int c = lane & 7;
; #pragma unroll
;     for (int j = 0; j < 4; ++j) { const int n = (lane >> 3) + 8 * j; const LAS float* s = scr + (8 * c) * 33 + n;
;         const unsigned long long o = (unsigned long long)pg8::pk4_fp8(s[0 * 33], s[1 * 33], s[2 * 33], s[3 * 33]) | ((unsigned long long)pg8::pk4_fp8(s[4 * 33], s[5 * 33], s[6 * 33], s[7 * 33]) << 32);
;         *(GAS unsigned long long*)(WT + (size_t)(n0 + n) * K + k0 + 8 * c) = o; }
;     LDS_WAIT(); asm volatile("" ::: "memory");
; }
	s_add_u32 s8, s34, 0xd000
	s_addc_u32 s9, s35, 0
	global_load_dwordx4 v[176:179], v74, s[8:9]
	s_add_u32 s8, s8, 0x20000
	s_addc_u32 s9, s9, 0
	global_load_dwordx4 v[180:183], v74, s[8:9]
	s_add_u32 s8, s8, 0x20000
	s_addc_u32 s9, s9, 0
	global_load_dwordx4 v[184:187], v74, s[8:9]
	s_add_u32 s8, s8, 0x20000
	s_addc_u32 s9, s9, 0
	global_load_dwordx4 v[188:191], v74, s[8:9]
	s_add_u32 s8, s8, 0x20000
	s_addc_u32 s9, s9, 0
	global_load_dwordx4 v[192:195], v74, s[8:9]
	s_add_u32 s8, s8, 0x20000
	s_addc_u32 s9, s9, 0
	global_load_dwordx4 v[196:199], v74, s[8:9]
	s_add_u32 s8, s8, 0x20000
	s_addc_u32 s9, s9, 0
	global_load_dwordx4 v[200:203], v74, s[8:9]
	s_add_u32 s8, s8, 0x20000
	s_addc_u32 s9, s9, 0
	global_load_dwordx4 v[204:207], v74, s[8:9]
	s_add_u32 s6, s36, 0x2c00000
	s_addc_u32 s7, s37, 0
	ds_read_b32 v226, v212
	ds_read_b32 v227, v212 offset:512
	ds_read_b32 v228, v212 offset:1024
	ds_read_b32 v229, v212 offset:1536
	ds_read_b32 v230, v212 offset:2048
	ds_read_b32 v231, v212 offset:2560
	ds_read_b32 v232, v212 offset:3072
	ds_read_b32 v233, v212 offset:3584
	ds_read_b32 v234, v212 offset:4096
	ds_read_b32 v235, v212 offset:4608
	ds_read_b32 v236, v212 offset:5120
	ds_read_b32 v237, v212 offset:5632
	ds_read_b32 v238, v212 offset:6144
	ds_read_b32 v239, v212 offset:6656
	ds_read_b32 v240, v212 offset:7168
	ds_read_b32 v241, v212 offset:7680
	s_waitcnt lgkmcnt(0)
	v_max_f32_e32 v226, v226, v226
	v_max_f32_e32 v227, v227, v227
	v_max_f32_e32 v228, v228, v228
	v_max_f32_e32 v229, v229, v229
	v_max_f32_e32 v230, v230, v230
	v_max_f32_e32 v231, v231, v231
	v_max_f32_e32 v232, v232, v232
	v_max_f32_e32 v233, v233, v233
	v_max_f32_e32 v234, v234, v234
	v_max_f32_e32 v235, v235, v235
	v_max_f32_e32 v236, v236, v236
	v_max_f32_e32 v237, v237, v237
	v_max_f32_e32 v238, v238, v238
	v_max_f32_e32 v239, v239, v239
	v_max_f32_e32 v240, v240, v240
	v_max_f32_e32 v241, v241, v241
	v_med3_f32 v226, v226, s62, v95
	v_med3_f32 v227, v227, s62, v95
	v_med3_f32 v228, v228, s62, v95
	v_med3_f32 v229, v229, s62, v95
	v_med3_f32 v230, v230, s62, v95
	v_med3_f32 v231, v231, s62, v95
	v_med3_f32 v232, v232, s62, v95
	v_med3_f32 v233, v233, s62, v95
	v_med3_f32 v234, v234, s62, v95
	v_med3_f32 v235, v235, s62, v95
	v_med3_f32 v236, v236, s62, v95
	v_med3_f32 v237, v237, s62, v95
	v_med3_f32 v238, v238, s62, v95
	v_med3_f32 v239, v239, s62, v95
	v_med3_f32 v240, v240, s62, v95
	v_med3_f32 v241, v241, s62, v95
	v_mov_b32_e32 v242, 0
	v_mov_b32_e32 v243, 0
	v_mov_b32_e32 v244, 0
	v_mov_b32_e32 v245, 0
	v_cvt_pk_fp8_f32 v242, v226, v227
	v_cvt_pk_fp8_f32 v243, v230, v231
	v_cvt_pk_fp8_f32 v244, v234, v235
	v_cvt_pk_fp8_f32 v245, v238, v239
	v_cvt_pk_fp8_f32 v242, v228, v229 op_sel:[0,0,1]
	v_cvt_pk_fp8_f32 v243, v232, v233 op_sel:[0,0,1]
	v_cvt_pk_fp8_f32 v244, v236, v237 op_sel:[0,0,1]
	v_cvt_pk_fp8_f32 v245, v240, v241 op_sel:[0,0,1]
	s_nop 0
	global_store_dwordx4 v77, v[242:245], s[6:7]
	ds_read_b32 v226, v214
	ds_read_b32 v227, v214 offset:512
	ds_read_b32 v228, v214 offset:1024
	ds_read_b32 v229, v214 offset:1536
	ds_read_b32 v230, v214 offset:2048
	ds_read_b32 v231, v214 offset:2560
	ds_read_b32 v232, v214 offset:3072
	ds_read_b32 v233, v214 offset:3584
	ds_read_b32 v234, v214 offset:4096
	ds_read_b32 v235, v214 offset:4608
	ds_read_b32 v236, v214 offset:5120
	ds_read_b32 v237, v214 offset:5632
	ds_read_b32 v238, v214 offset:6144
	ds_read_b32 v239, v214 offset:6656
	ds_read_b32 v240, v214 offset:7168
	ds_read_b32 v241, v214 offset:7680
	s_waitcnt lgkmcnt(0)
	v_max_f32_e32 v226, v226, v226
	v_max_f32_e32 v227, v227, v227
	v_max_f32_e32 v228, v228, v228
	v_max_f32_e32 v229, v229, v229
	v_max_f32_e32 v230, v230, v230
	v_max_f32_e32 v231, v231, v231
	v_max_f32_e32 v232, v232, v232
	v_max_f32_e32 v233, v233, v233
	v_max_f32_e32 v234, v234, v234
	v_max_f32_e32 v235, v235, v235
	v_max_f32_e32 v236, v236, v236
	v_max_f32_e32 v237, v237, v237
	v_max_f32_e32 v238, v238, v238
	v_max_f32_e32 v239, v239, v239
	v_max_f32_e32 v240, v240, v240
	v_max_f32_e32 v241, v241, v241
	v_med3_f32 v226, v226, s62, v95
	v_med3_f32 v227, v227, s62, v95
	v_med3_f32 v228, v228, s62, v95
	v_med3_f32 v229, v229, s62, v95
	v_med3_f32 v230, v230, s62, v95
	v_med3_f32 v231, v231, s62, v95
	v_med3_f32 v232, v232, s62, v95
	v_med3_f32 v233, v233, s62, v95
	v_med3_f32 v234, v234, s62, v95
	v_med3_f32 v235, v235, s62, v95
	v_med3_f32 v236, v236, s62, v95
	v_med3_f32 v237, v237, s62, v95
	v_med3_f32 v238, v238, s62, v95
	v_med3_f32 v239, v239, s62, v95
	v_med3_f32 v240, v240, s62, v95
	v_med3_f32 v241, v241, s62, v95
	v_mov_b32_e32 v242, 0
	v_mov_b32_e32 v243, 0
	v_mov_b32_e32 v244, 0
	v_mov_b32_e32 v245, 0
	v_cvt_pk_fp8_f32 v242, v226, v227
	v_cvt_pk_fp8_f32 v243, v230, v231
	v_cvt_pk_fp8_f32 v244, v234, v235
	v_cvt_pk_fp8_f32 v245, v238, v239
	v_cvt_pk_fp8_f32 v242, v228, v229 op_sel:[0,0,1]
	v_cvt_pk_fp8_f32 v243, v232, v233 op_sel:[0,0,1]
	v_cvt_pk_fp8_f32 v244, v236, v237 op_sel:[0,0,1]
	v_cvt_pk_fp8_f32 v245, v240, v241 op_sel:[0,0,1]
	s_nop 0
	global_store_dwordx4 v78, v[242:245], s[6:7]
	s_waitcnt vmcnt(12)
	v_mul_f32_e32 v144, v34, v144
	v_mul_f32_e32 v145, v34, v145
	v_mul_f32_e32 v146, v34, v146
	v_mul_f32_e32 v147, v34, v147
	ds_write_b128 v209, v[144:147]
	v_mul_f32_e32 v148, v35, v148
	v_mul_f32_e32 v149, v35, v149
	v_mul_f32_e32 v150, v35, v150
	v_mul_f32_e32 v151, v35, v151
	ds_write_b128 v209, v[148:151] offset:1024
	v_mul_f32_e32 v152, v36, v152
	v_mul_f32_e32 v153, v36, v153
	v_mul_f32_e32 v154, v36, v154
	v_mul_f32_e32 v155, v36, v155
	ds_write_b128 v209, v[152:155] offset:2048
	v_mul_f32_e32 v156, v37, v156
	v_mul_f32_e32 v157, v37, v157
	v_mul_f32_e32 v158, v37, v158
	v_mul_f32_e32 v159, v37, v159
	ds_write_b128 v209, v[156:159] offset:3072
	v_mul_f32_e32 v160, v38, v160
	v_mul_f32_e32 v161, v38, v161
	v_mul_f32_e32 v162, v38, v162
	v_mul_f32_e32 v163, v38, v163
	ds_write_b128 v209, v[160:163] offset:4096
	v_mul_f32_e32 v164, v39, v164
	v_mul_f32_e32 v165, v39, v165
	v_mul_f32_e32 v166, v39, v166
	v_mul_f32_e32 v167, v39, v167
	ds_write_b128 v209, v[164:167] offset:5120
	v_mul_f32_e32 v168, v40, v168
	v_mul_f32_e32 v169, v40, v169
	v_mul_f32_e32 v170, v40, v170
	v_mul_f32_e32 v171, v40, v171
	ds_write_b128 v209, v[168:171] offset:6144
	v_mul_f32_e32 v172, v41, v172
	v_mul_f32_e32 v173, v41, v173
	v_mul_f32_e32 v174, v41, v174
	v_mul_f32_e32 v175, v41, v175
	ds_write_b128 v209, v[172:175] offset:7168
	s_waitcnt lgkmcnt(0)
	s_barrier
; #define GAS __attribute__((address_space(1)))
;     const int pr = item >> 1, kb = 2 * (pr / nblk) + (item & 1), nb = pr % nblk, k0 = 64 * kb, n0 = 32 * nb;
;     const int nr = n0 + (lane & 31); const int sc = MAP == 1 ? src_col_in(nr) : nr;
;     float v[32];
; #pragma unroll
;     for (int i = 0; i < 32; ++i) v[i] = sc >= 0 ? W[(size_t)(k0 + 2 * i + (lane >> 5)) * Nsrc + sc] : 0.f;
; #pragma unroll
;     for (int i = 0; i < 32; ++i) { const int k = k0 + 2 * i + (lane >> 5); float x = v[i] * wscale; if (KS) x *= (k < ksplit ? ksA[k] : ksB[k - ksplit]); scr[(2 * i + (lane >> 5)) * 33 + (lane & 31)] = x; }
;     LDS_WAIT(); asm volatile("" ::: "memory");
;     const int c = lane & 7;
; #pragma unroll
;     for (int j = 0; j < 4; ++j) { const int n = (lane >> 3) + 8 * j; const LAS float* s = scr + (8 * c) * 33 + n;
;         const unsigned long long o = (unsigned long long)pg8::pk4_fp8(s[0 * 33], s[1 * 33], s[2 * 33], s[3 * 33]) | ((unsigned long long)pg8::pk4_fp8(s[4 * 33], s[5 * 33], s[6 * 33], s[7 * 33]) << 32);
;         *(GAS unsigned long long*)(WT + (size_t)(n0 + n) * K + k0 + 8 * c) = o; }
;     LDS_WAIT(); asm volatile("" ::: "memory");
; }
; __global__ void __launch_bounds__(NWAVES * 64, 2) hybrid_fwd(Args args) {
;     ...
;         for (int rep = 0; rep < REP_PRO; ++rep)
;         for (int it = gw; it < DEPTH * I_L; it += NGW) {
;             const int l = it / I_L; int r = it % I_L;
;             if (r < I_IN) { if (l >= PROJ_F8_FROM) p0_transpose_item_f8<true, 1>(args.in[2] + (size_t)l * DM * NSRC, DM, NSRC, NPROJ / 32, (unsigned char*)(ws + WS_WIN + l * SZ_WIN), WUP8_SCALE, args.in[1] + l * DM, args.in[1] + l * DM, DM, scr, r, lane);
;                 else p0_transpose_item<1, true>(args.in[2] + (size_t)l * DM * NSRC, DM, NSRC, NPROJ / 32, (bf16*)(ws + WS_WIN + l * SZ_WIN), args.in[1] + l * DM, args.in[1] + l * DM, DM, scr, r, lane); continue; } r -= I_IN;
;             if (r < I_O) { if (l >= WO_F8_FROM) p0_transpose_item_f8<true>(args.in[13] + (size_t)l * DM * DM, DM, DM, DM / 32, (unsigned char*)(ws + WS_WO + l * SZ_WO), 64.f, args.in[6] + l * 2048, args.in[12] + l * 2048, 2048, scr, r, lane);
;                 else p0_transpose_item<0, true>(args.in[13] + (size_t)l * DM * DM, DM, DM, DM / 32, (bf16*)(ws + WS_WO + l * SZ_WO), args.in[6] + l * 2048, args.in[12] + l * 2048, 2048, scr, r, lane); continue; } r -= I_O;
	s_add_u32 s8, s34, 0xe000
	s_addc_u32 s9, s35, 0
	global_load_dwordx4 v[144:147], v74, s[8:9]
	s_add_u32 s8, s8, 0x20000
	s_addc_u32 s9, s9, 0
	global_load_dwordx4 v[148:151], v74, s[8:9]
	s_add_u32 s8, s8, 0x20000
	s_addc_u32 s9, s9, 0
	global_load_dwordx4 v[152:155], v74, s[8:9]
	s_add_u32 s8, s8, 0x20000
	s_addc_u32 s9, s9, 0
	global_load_dwordx4 v[156:159], v74, s[8:9]
	s_add_u32 s8, s8, 0x20000
	s_addc_u32 s9, s9, 0
	global_load_dwordx4 v[160:163], v74, s[8:9]
	s_add_u32 s8, s8, 0x20000
	s_addc_u32 s9, s9, 0
	global_load_dwordx4 v[164:167], v74, s[8:9]
	s_add_u32 s8, s8, 0x20000
	s_addc_u32 s9, s9, 0
	global_load_dwordx4 v[168:171], v74, s[8:9]
	s_add_u32 s8, s8, 0x20000
	s_addc_u32 s9, s9, 0
	global_load_dwordx4 v[172:175], v74, s[8:9]
	s_add_u32 s6, s36, 0x3000000
	s_addc_u32 s7, s37, 0
	ds_read_b32 v226, v211
	ds_read_b32 v227, v211 offset:512
	ds_read_b32 v228, v211 offset:1024
	ds_read_b32 v229, v211 offset:1536
	ds_read_b32 v230, v211 offset:2048
	ds_read_b32 v231, v211 offset:2560
	ds_read_b32 v232, v211 offset:3072
	ds_read_b32 v233, v211 offset:3584
	ds_read_b32 v234, v211 offset:4096
	ds_read_b32 v235, v211 offset:4608
	ds_read_b32 v236, v211 offset:5120
	ds_read_b32 v237, v211 offset:5632
	ds_read_b32 v238, v211 offset:6144
	ds_read_b32 v239, v211 offset:6656
	ds_read_b32 v240, v211 offset:7168
	ds_read_b32 v241, v211 offset:7680
	s_waitcnt lgkmcnt(0)
	v_max_f32_e32 v226, v226, v226
	v_max_f32_e32 v227, v227, v227
	v_max_f32_e32 v228, v228, v228
	v_max_f32_e32 v229, v229, v229
	v_max_f32_e32 v230, v230, v230
	v_max_f32_e32 v231, v231, v231
	v_max_f32_e32 v232, v232, v232
	v_max_f32_e32 v233, v233, v233
	v_max_f32_e32 v234, v234, v234
	v_max_f32_e32 v235, v235, v235
	v_max_f32_e32 v236, v236, v236
	v_max_f32_e32 v237, v237, v237
	v_max_f32_e32 v238, v238, v238
	v_max_f32_e32 v239, v239, v239
	v_max_f32_e32 v240, v240, v240
	v_max_f32_e32 v241, v241, v241
	v_med3_f32 v226, v226, s62, v95
	v_med3_f32 v227, v227, s62, v95
	v_med3_f32 v228, v228, s62, v95
	v_med3_f32 v229, v229, s62, v95
	v_med3_f32 v230, v230, s62, v95
	v_med3_f32 v231, v231, s62, v95
	v_med3_f32 v232, v232, s62, v95
	v_med3_f32 v233, v233, s62, v95
	v_med3_f32 v234, v234, s62, v95
	v_med3_f32 v235, v235, s62, v95
	v_med3_f32 v236, v236, s62, v95
	v_med3_f32 v237, v237, s62, v95
	v_med3_f32 v238, v238, s62, v95
	v_med3_f32 v239, v239, s62, v95
	v_med3_f32 v240, v240, s62, v95
	v_med3_f32 v241, v241, s62, v95
	v_mov_b32_e32 v242, 0
	v_mov_b32_e32 v243, 0
	v_mov_b32_e32 v244, 0
	v_mov_b32_e32 v245, 0
	v_cvt_pk_fp8_f32 v242, v226, v227
	v_cvt_pk_fp8_f32 v243, v230, v231
	v_cvt_pk_fp8_f32 v244, v234, v235
	v_cvt_pk_fp8_f32 v245, v238, v239
	v_cvt_pk_fp8_f32 v242, v228, v229 op_sel:[0,0,1]
	v_cvt_pk_fp8_f32 v243, v232, v233 op_sel:[0,0,1]
	v_cvt_pk_fp8_f32 v244, v236, v237 op_sel:[0,0,1]
	v_cvt_pk_fp8_f32 v245, v240, v241 op_sel:[0,0,1]
	s_nop 0
	global_store_dwordx4 v77, v[242:245], s[6:7]
	ds_read_b32 v226, v213
	ds_read_b32 v227, v213 offset:512
	ds_read_b32 v228, v213 offset:1024
	ds_read_b32 v229, v213 offset:1536
	ds_read_b32 v230, v213 offset:2048
	ds_read_b32 v231, v213 offset:2560
	ds_read_b32 v232, v213 offset:3072
	ds_read_b32 v233, v213 offset:3584
	ds_read_b32 v234, v213 offset:4096
	ds_read_b32 v235, v213 offset:4608
	ds_read_b32 v236, v213 offset:5120
	ds_read_b32 v237, v213 offset:5632
	ds_read_b32 v238, v213 offset:6144
	ds_read_b32 v239, v213 offset:6656
	ds_read_b32 v240, v213 offset:7168
	ds_read_b32 v241, v213 offset:7680
	s_waitcnt lgkmcnt(0)
	v_max_f32_e32 v226, v226, v226
	v_max_f32_e32 v227, v227, v227
	v_max_f32_e32 v228, v228, v228
	v_max_f32_e32 v229, v229, v229
	v_max_f32_e32 v230, v230, v230
	v_max_f32_e32 v231, v231, v231
	v_max_f32_e32 v232, v232, v232
	v_max_f32_e32 v233, v233, v233
	v_max_f32_e32 v234, v234, v234
	v_max_f32_e32 v235, v235, v235
	v_max_f32_e32 v236, v236, v236
	v_max_f32_e32 v237, v237, v237
	v_max_f32_e32 v238, v238, v238
	v_max_f32_e32 v239, v239, v239
	v_max_f32_e32 v240, v240, v240
	v_max_f32_e32 v241, v241, v241
	v_med3_f32 v226, v226, s62, v95
	v_med3_f32 v227, v227, s62, v95
	v_med3_f32 v228, v228, s62, v95
	v_med3_f32 v229, v229, s62, v95
	v_med3_f32 v230, v230, s62, v95
	v_med3_f32 v231, v231, s62, v95
	v_med3_f32 v232, v232, s62, v95
	v_med3_f32 v233, v233, s62, v95
	v_med3_f32 v234, v234, s62, v95
	v_med3_f32 v235, v235, s62, v95
	v_med3_f32 v236, v236, s62, v95
	v_med3_f32 v237, v237, s62, v95
	v_med3_f32 v238, v238, s62, v95
	v_med3_f32 v239, v239, s62, v95
	v_med3_f32 v240, v240, s62, v95
	v_med3_f32 v241, v241, s62, v95
	v_mov_b32_e32 v242, 0
	v_mov_b32_e32 v243, 0
	v_mov_b32_e32 v244, 0
	v_mov_b32_e32 v245, 0
	v_cvt_pk_fp8_f32 v242, v226, v227
	v_cvt_pk_fp8_f32 v243, v230, v231
	v_cvt_pk_fp8_f32 v244, v234, v235
	v_cvt_pk_fp8_f32 v245, v238, v239
	v_cvt_pk_fp8_f32 v242, v228, v229 op_sel:[0,0,1]
	v_cvt_pk_fp8_f32 v243, v232, v233 op_sel:[0,0,1]
	v_cvt_pk_fp8_f32 v244, v236, v237 op_sel:[0,0,1]
	v_cvt_pk_fp8_f32 v245, v240, v241 op_sel:[0,0,1]
	s_nop 0
	global_store_dwordx4 v78, v[242:245], s[6:7]
	s_waitcnt vmcnt(12)
	v_mul_f32_e32 v176, v34, v176
	v_mul_f32_e32 v177, v34, v177
	v_mul_f32_e32 v178, v34, v178
	v_mul_f32_e32 v179, v34, v179
	ds_write_b128 v210, v[176:179]
	v_mul_f32_e32 v180, v35, v180
	v_mul_f32_e32 v181, v35, v181
	v_mul_f32_e32 v182, v35, v182
	v_mul_f32_e32 v183, v35, v183
	ds_write_b128 v210, v[180:183] offset:1024
	v_mul_f32_e32 v184, v36, v184
	v_mul_f32_e32 v185, v36, v185
	v_mul_f32_e32 v186, v36, v186
	v_mul_f32_e32 v187, v36, v187
	ds_write_b128 v210, v[184:187] offset:2048
	v_mul_f32_e32 v188, v37, v188
	v_mul_f32_e32 v189, v37, v189
	v_mul_f32_e32 v190, v37, v190
	v_mul_f32_e32 v191, v37, v191
	ds_write_b128 v210, v[188:191] offset:3072
	v_mul_f32_e32 v192, v38, v192
	v_mul_f32_e32 v193, v38, v193
	v_mul_f32_e32 v194, v38, v194
	v_mul_f32_e32 v195, v38, v195
	ds_write_b128 v210, v[192:195] offset:4096
	v_mul_f32_e32 v196, v39, v196
	v_mul_f32_e32 v197, v39, v197
	v_mul_f32_e32 v198, v39, v198
	v_mul_f32_e32 v199, v39, v199
	ds_write_b128 v210, v[196:199] offset:5120
	v_mul_f32_e32 v200, v40, v200
	v_mul_f32_e32 v201, v40, v201
	v_mul_f32_e32 v202, v40, v202
	v_mul_f32_e32 v203, v40, v203
	ds_write_b128 v210, v[200:203] offset:6144
	v_mul_f32_e32 v204, v41, v204
	v_mul_f32_e32 v205, v41, v205
	v_mul_f32_e32 v206, v41, v206
	v_mul_f32_e32 v207, v41, v207
	ds_write_b128 v210, v[204:207] offset:7168
	s_waitcnt lgkmcnt(0)
	s_barrier
; #define GAS __attribute__((address_space(1)))
;     const int pr = item >> 1, kb = 2 * (pr / nblk) + (item & 1), nb = pr % nblk, k0 = 64 * kb, n0 = 32 * nb;
;     const int nr = n0 + (lane & 31); const int sc = MAP == 1 ? src_col_in(nr) : nr;
;     float v[32];
; #pragma unroll
;     for (int i = 0; i < 32; ++i) v[i] = sc >= 0 ? W[(size_t)(k0 + 2 * i + (lane >> 5)) * Nsrc + sc] : 0.f;
; #pragma unroll
;     for (int i = 0; i < 32; ++i) { const int k = k0 + 2 * i + (lane >> 5); float x = v[i] * wscale; if (KS) x *= (k < ksplit ? ksA[k] : ksB[k - ksplit]); scr[(2 * i + (lane >> 5)) * 33 + (lane & 31)] = x; }
;     LDS_WAIT(); asm volatile("" ::: "memory");
;     const int c = lane & 7;
; #pragma unroll
;     for (int j = 0; j < 4; ++j) { const int n = (lane >> 3) + 8 * j; const LAS float* s = scr + (8 * c) * 33 + n;
;         const unsigned long long o = (unsigned long long)pg8::pk4_fp8(s[0 * 33], s[1 * 33], s[2 * 33], s[3 * 33]) | ((unsigned long long)pg8::pk4_fp8(s[4 * 33], s[5 * 33], s[6 * 33], s[7 * 33]) << 32);
;         *(GAS unsigned long long*)(WT + (size_t)(n0 + n) * K + k0 + 8 * c) = o; }
;     LDS_WAIT(); asm volatile("" ::: "memory");
; }
; __global__ void __launch_bounds__(NWAVES * 64, 2) hybrid_fwd(Args args) {
;     ...
;         for (int rep = 0; rep < REP_PRO; ++rep)
;         for (int it = gw; it < DEPTH * I_L; it += NGW) {
;             const int l = it / I_L; int r = it % I_L;
;             if (r < I_IN) { if (l >= PROJ_F8_FROM) p0_transpose_item_f8<true, 1>(args.in[2] + (size_t)l * DM * NSRC, DM, NSRC, NPROJ / 32, (unsigned char*)(ws + WS_WIN + l * SZ_WIN), WUP8_SCALE, args.in[1] + l * DM, args.in[1] + l * DM, DM, scr, r, lane);
;                 else p0_transpose_item<1, true>(args.in[2] + (size_t)l * DM * NSRC, DM, NSRC, NPROJ / 32, (bf16*)(ws + WS_WIN + l * SZ_WIN), args.in[1] + l * DM, args.in[1] + l * DM, DM, scr, r, lane); continue; } r -= I_IN;
;             if (r < I_O) { if (l >= WO_F8_FROM) p0_transpose_item_f8<true>(args.in[13] + (size_t)l * DM * DM, DM, DM, DM / 32, (unsigned char*)(ws + WS_WO + l * SZ_WO), 64.f, args.in[6] + l * 2048, args.in[12] + l * 2048, 2048, scr, r, lane);
;                 else p0_transpose_item<0, true>(args.in[13] + (size_t)l * DM * DM, DM, DM, DM / 32, (bf16*)(ws + WS_WO + l * SZ_WO), args.in[6] + l * 2048, args.in[12] + l * 2048, 2048, scr, r, lane); continue; } r -= I_O;
	s_add_u32 s8, s34, 0xf000
	s_addc_u32 s9, s35, 0
	global_load_dwordx4 v[176:179], v74, s[8:9]
	s_add_u32 s8, s8, 0x20000
	s_addc_u32 s9, s9, 0
	global_load_dwordx4 v[180:183], v74, s[8:9]
	s_add_u32 s8, s8, 0x20000
	s_addc_u32 s9, s9, 0
	global_load_dwordx4 v[184:187], v74, s[8:9]
	s_add_u32 s8, s8, 0x20000
	s_addc_u32 s9, s9, 0
	global_load_dwordx4 v[188:191], v74, s[8:9]
	s_add_u32 s8, s8, 0x20000
	s_addc_u32 s9, s9, 0
	global_load_dwordx4 v[192:195], v74, s[8:9]
	s_add_u32 s8, s8, 0x20000
	s_addc_u32 s9, s9, 0
	global_load_dwordx4 v[196:199], v74, s[8:9]
	s_add_u32 s8, s8, 0x20000
	s_addc_u32 s9, s9, 0
	global_load_dwordx4 v[200:203], v74, s[8:9]
	s_add_u32 s8, s8, 0x20000
	s_addc_u32 s9, s9, 0
	global_load_dwordx4 v[204:207], v74, s[8:9]
	s_add_u32 s6, s36, 0x3400000
	s_addc_u32 s7, s37, 0
	ds_read_b32 v226, v212
	ds_read_b32 v227, v212 offset:512
	ds_read_b32 v228, v212 offset:1024
	ds_read_b32 v229, v212 offset:1536
	ds_read_b32 v230, v212 offset:2048
	ds_read_b32 v231, v212 offset:2560
	ds_read_b32 v232, v212 offset:3072
	ds_read_b32 v233, v212 offset:3584
	ds_read_b32 v234, v212 offset:4096
	ds_read_b32 v235, v212 offset:4608
	ds_read_b32 v236, v212 offset:5120
	ds_read_b32 v237, v212 offset:5632
	ds_read_b32 v238, v212 offset:6144
	ds_read_b32 v239, v212 offset:6656
	ds_read_b32 v240, v212 offset:7168
	ds_read_b32 v241, v212 offset:7680
	s_waitcnt lgkmcnt(0)
	v_max_f32_e32 v226, v226, v226
	v_max_f32_e32 v227, v227, v227
	v_max_f32_e32 v228, v228, v228
	v_max_f32_e32 v229, v229, v229
	v_max_f32_e32 v230, v230, v230
	v_max_f32_e32 v231, v231, v231
	v_max_f32_e32 v232, v232, v232
	v_max_f32_e32 v233, v233, v233
	v_max_f32_e32 v234, v234, v234
	v_max_f32_e32 v235, v235, v235
	v_max_f32_e32 v236, v236, v236
	v_max_f32_e32 v237, v237, v237
	v_max_f32_e32 v238, v238, v238
	v_max_f32_e32 v239, v239, v239
	v_max_f32_e32 v240, v240, v240
	v_max_f32_e32 v241, v241, v241
	v_med3_f32 v226, v226, s62, v95
	v_med3_f32 v227, v227, s62, v95
	v_med3_f32 v228, v228, s62, v95
	v_med3_f32 v229, v229, s62, v95
	v_med3_f32 v230, v230, s62, v95
	v_med3_f32 v231, v231, s62, v95
	v_med3_f32 v232, v232, s62, v95
	v_med3_f32 v233, v233, s62, v95
	v_med3_f32 v234, v234, s62, v95
	v_med3_f32 v235, v235, s62, v95
	v_med3_f32 v236, v236, s62, v95
	v_med3_f32 v237, v237, s62, v95
	v_med3_f32 v238, v238, s62, v95
	v_med3_f32 v239, v239, s62, v95
	v_med3_f32 v240, v240, s62, v95
	v_med3_f32 v241, v241, s62, v95
	v_mov_b32_e32 v242, 0
	v_mov_b32_e32 v243, 0
	v_mov_b32_e32 v244, 0
	v_mov_b32_e32 v245, 0
	v_cvt_pk_fp8_f32 v242, v226, v227
	v_cvt_pk_fp8_f32 v243, v230, v231
	v_cvt_pk_fp8_f32 v244, v234, v235
	v_cvt_pk_fp8_f32 v245, v238, v239
	v_cvt_pk_fp8_f32 v242, v228, v229 op_sel:[0,0,1]
	v_cvt_pk_fp8_f32 v243, v232, v233 op_sel:[0,0,1]
	v_cvt_pk_fp8_f32 v244, v236, v237 op_sel:[0,0,1]
	v_cvt_pk_fp8_f32 v245, v240, v241 op_sel:[0,0,1]
	s_nop 0
	global_store_dwordx4 v77, v[242:245], s[6:7]
	ds_read_b32 v226, v214
	ds_read_b32 v227, v214 offset:512
	ds_read_b32 v228, v214 offset:1024
	ds_read_b32 v229, v214 offset:1536
	ds_read_b32 v230, v214 offset:2048
	ds_read_b32 v231, v214 offset:2560
	ds_read_b32 v232, v214 offset:3072
	ds_read_b32 v233, v214 offset:3584
	ds_read_b32 v234, v214 offset:4096
	ds_read_b32 v235, v214 offset:4608
	ds_read_b32 v236, v214 offset:5120
	ds_read_b32 v237, v214 offset:5632
	ds_read_b32 v238, v214 offset:6144
	ds_read_b32 v239, v214 offset:6656
	ds_read_b32 v240, v214 offset:7168
	ds_read_b32 v241, v214 offset:7680
	s_waitcnt lgkmcnt(0)
	v_max_f32_e32 v226, v226, v226
	v_max_f32_e32 v227, v227, v227
	v_max_f32_e32 v228, v228, v228
	v_max_f32_e32 v229, v229, v229
	v_max_f32_e32 v230, v230, v230
	v_max_f32_e32 v231, v231, v231
	v_max_f32_e32 v232, v232, v232
	v_max_f32_e32 v233, v233, v233
	v_max_f32_e32 v234, v234, v234
	v_max_f32_e32 v235, v235, v235
	v_max_f32_e32 v236, v236, v236
	v_max_f32_e32 v237, v237, v237
	v_max_f32_e32 v238, v238, v238
	v_max_f32_e32 v239, v239, v239
	v_max_f32_e32 v240, v240, v240
	v_max_f32_e32 v241, v241, v241
	v_med3_f32 v226, v226, s62, v95
	v_med3_f32 v227, v227, s62, v95
	v_med3_f32 v228, v228, s62, v95
	v_med3_f32 v229, v229, s62, v95
	v_med3_f32 v230, v230, s62, v95
	v_med3_f32 v231, v231, s62, v95
	v_med3_f32 v232, v232, s62, v95
	v_med3_f32 v233, v233, s62, v95
	v_med3_f32 v234, v234, s62, v95
	v_med3_f32 v235, v235, s62, v95
	v_med3_f32 v236, v236, s62, v95
	v_med3_f32 v237, v237, s62, v95
	v_med3_f32 v238, v238, s62, v95
	v_med3_f32 v239, v239, s62, v95
	v_med3_f32 v240, v240, s62, v95
	v_med3_f32 v241, v241, s62, v95
	v_mov_b32_e32 v242, 0
	v_mov_b32_e32 v243, 0
	v_mov_b32_e32 v244, 0
	v_mov_b32_e32 v245, 0
	v_cvt_pk_fp8_f32 v242, v226, v227
	v_cvt_pk_fp8_f32 v243, v230, v231
	v_cvt_pk_fp8_f32 v244, v234, v235
	v_cvt_pk_fp8_f32 v245, v238, v239
	v_cvt_pk_fp8_f32 v242, v228, v229 op_sel:[0,0,1]
	v_cvt_pk_fp8_f32 v243, v232, v233 op_sel:[0,0,1]
	v_cvt_pk_fp8_f32 v244, v236, v237 op_sel:[0,0,1]
	v_cvt_pk_fp8_f32 v245, v240, v241 op_sel:[0,0,1]
	s_nop 0
	global_store_dwordx4 v78, v[242:245], s[6:7]
	s_waitcnt vmcnt(12)
	v_mul_f32_e32 v144, v34, v144
	v_mul_f32_e32 v145, v34, v145
	v_mul_f32_e32 v146, v34, v146
	v_mul_f32_e32 v147, v34, v147
	ds_write_b128 v209, v[144:147]
	v_mul_f32_e32 v148, v35, v148
	v_mul_f32_e32 v149, v35, v149
	v_mul_f32_e32 v150, v35, v150
	v_mul_f32_e32 v151, v35, v151
	ds_write_b128 v209, v[148:151] offset:1024
	v_mul_f32_e32 v152, v36, v152
	v_mul_f32_e32 v153, v36, v153
	v_mul_f32_e32 v154, v36, v154
	v_mul_f32_e32 v155, v36, v155
	ds_write_b128 v209, v[152:155] offset:2048
	v_mul_f32_e32 v156, v37, v156
	v_mul_f32_e32 v157, v37, v157
	v_mul_f32_e32 v158, v37, v158
	v_mul_f32_e32 v159, v37, v159
	ds_write_b128 v209, v[156:159] offset:3072
	v_mul_f32_e32 v160, v38, v160
	v_mul_f32_e32 v161, v38, v161
	v_mul_f32_e32 v162, v38, v162
	v_mul_f32_e32 v163, v38, v163
	ds_write_b128 v209, v[160:163] offset:4096
	v_mul_f32_e32 v164, v39, v164
	v_mul_f32_e32 v165, v39, v165
	v_mul_f32_e32 v166, v39, v166
	v_mul_f32_e32 v167, v39, v167
	ds_write_b128 v209, v[164:167] offset:5120
	v_mul_f32_e32 v168, v40, v168
	v_mul_f32_e32 v169, v40, v169
	v_mul_f32_e32 v170, v40, v170
	v_mul_f32_e32 v171, v40, v171
	ds_write_b128 v209, v[168:171] offset:6144
	v_mul_f32_e32 v172, v41, v172
	v_mul_f32_e32 v173, v41, v173
	v_mul_f32_e32 v174, v41, v174
	v_mul_f32_e32 v175, v41, v175
	ds_write_b128 v209, v[172:175] offset:7168
	s_waitcnt lgkmcnt(0)
	s_barrier
; #define GAS __attribute__((address_space(1)))
;     const int pr = item >> 1, kb = 2 * (pr / nblk) + (item & 1), nb = pr % nblk, k0 = 64 * kb, n0 = 32 * nb;
;     const int nr = n0 + (lane & 31); const int sc = MAP == 1 ? src_col_in(nr) : nr;
;     float v[32];
; #pragma unroll
;     for (int i = 0; i < 32; ++i) v[i] = sc >= 0 ? W[(size_t)(k0 + 2 * i + (lane >> 5)) * Nsrc + sc] : 0.f;
; #pragma unroll
;     for (int i = 0; i < 32; ++i) { const int k = k0 + 2 * i + (lane >> 5); float x = v[i] * wscale; if (KS) x *= (k < ksplit ? ksA[k] : ksB[k - ksplit]); scr[(2 * i + (lane >> 5)) * 33 + (lane & 31)] = x; }
;     LDS_WAIT(); asm volatile("" ::: "memory");
;     const int c = lane & 7;
; #pragma unroll
;     for (int j = 0; j < 4; ++j) { const int n = (lane >> 3) + 8 * j; const LAS float* s = scr + (8 * c) * 33 + n;
;         const unsigned long long o = (unsigned long long)pg8::pk4_fp8(s[0 * 33], s[1 * 33], s[2 * 33], s[3 * 33]) | ((unsigned long long)pg8::pk4_fp8(s[4 * 33], s[5 * 33], s[6 * 33], s[7 * 33]) << 32);
;         *(GAS unsigned long long*)(WT + (size_t)(n0 + n) * K + k0 + 8 * c) = o; }
;     LDS_WAIT(); asm volatile("" ::: "memory");
; }
; __global__ void __launch_bounds__(NWAVES * 64, 2) hybrid_fwd(Args args) {
;     ...
;         for (int rep = 0; rep < REP_PRO; ++rep)
;         for (int it = gw; it < DEPTH * I_L; it += NGW) {
;             const int l = it / I_L; int r = it % I_L;
;             if (r < I_IN) { if (l >= PROJ_F8_FROM) p0_transpose_item_f8<true, 1>(args.in[2] + (size_t)l * DM * NSRC, DM, NSRC, NPROJ / 32, (unsigned char*)(ws + WS_WIN + l * SZ_WIN), WUP8_SCALE, args.in[1] + l * DM, args.in[1] + l * DM, DM, scr, r, lane);
;                 else p0_transpose_item<1, true>(args.in[2] + (size_t)l * DM * NSRC, DM, NSRC, NPROJ / 32, (bf16*)(ws + WS_WIN + l * SZ_WIN), args.in[1] + l * DM, args.in[1] + l * DM, DM, scr, r, lane); continue; } r -= I_IN;
;             if (r < I_O) { if (l >= WO_F8_FROM) p0_transpose_item_f8<true>(args.in[13] + (size_t)l * DM * DM, DM, DM, DM / 32, (unsigned char*)(ws + WS_WO + l * SZ_WO), 64.f, args.in[6] + l * 2048, args.in[12] + l * 2048, 2048, scr, r, lane);
;                 else p0_transpose_item<0, true>(args.in[13] + (size_t)l * DM * DM, DM, DM, DM / 32, (bf16*)(ws + WS_WO + l * SZ_WO), args.in[6] + l * 2048, args.in[12] + l * 2048, 2048, scr, r, lane); continue; } r -= I_O;
	s_mov_b64 s[8:9], s[38:39]
	global_load_dwordx4 v[144:147], v75, s[8:9]
	s_add_u32 s8, s8, 0x8000
	s_addc_u32 s9, s9, 0
	global_load_dwordx4 v[148:151], v75, s[8:9]
	s_add_u32 s8, s8, 0x8000
	s_addc_u32 s9, s9, 0
	global_load_dwordx4 v[152:155], v75, s[8:9]
	s_add_u32 s8, s8, 0x8000
	s_addc_u32 s9, s9, 0
	global_load_dwordx4 v[156:159], v75, s[8:9]
	s_add_u32 s8, s8, 0x8000
	s_addc_u32 s9, s9, 0
	global_load_dwordx4 v[160:163], v75, s[8:9]
	s_add_u32 s8, s8, 0x8000
	s_addc_u32 s9, s9, 0
	global_load_dwordx4 v[164:167], v75, s[8:9]
	s_add_u32 s8, s8, 0x8000
	s_addc_u32 s9, s9, 0
	global_load_dwordx4 v[168:171], v75, s[8:9]
	s_add_u32 s8, s8, 0x8000
	s_addc_u32 s9, s9, 0
	global_load_dwordx4 v[172:175], v75, s[8:9]
	s_add_u32 s6, s36, 0x3800000
	s_addc_u32 s7, s37, 0
	ds_read_b32 v226, v211
	ds_read_b32 v227, v211 offset:512
	ds_read_b32 v228, v211 offset:1024
	ds_read_b32 v229, v211 offset:1536
	ds_read_b32 v230, v211 offset:2048
	ds_read_b32 v231, v211 offset:2560
	ds_read_b32 v232, v211 offset:3072
	ds_read_b32 v233, v211 offset:3584
	ds_read_b32 v234, v211 offset:4096
	ds_read_b32 v235, v211 offset:4608
	ds_read_b32 v236, v211 offset:5120
	ds_read_b32 v237, v211 offset:5632
	ds_read_b32 v238, v211 offset:6144
	ds_read_b32 v239, v211 offset:6656
	ds_read_b32 v240, v211 offset:7168
	ds_read_b32 v241, v211 offset:7680
	s_waitcnt lgkmcnt(0)
	v_max_f32_e32 v226, v226, v226
	v_max_f32_e32 v227, v227, v227
	v_max_f32_e32 v228, v228, v228
	v_max_f32_e32 v229, v229, v229
	v_max_f32_e32 v230, v230, v230
	v_max_f32_e32 v231, v231, v231
	v_max_f32_e32 v232, v232, v232
	v_max_f32_e32 v233, v233, v233
	v_max_f32_e32 v234, v234, v234
	v_max_f32_e32 v235, v235, v235
	v_max_f32_e32 v236, v236, v236
	v_max_f32_e32 v237, v237, v237
	v_max_f32_e32 v238, v238, v238
	v_max_f32_e32 v239, v239, v239
	v_max_f32_e32 v240, v240, v240
	v_max_f32_e32 v241, v241, v241
	v_med3_f32 v226, v226, s62, v95
	v_med3_f32 v227, v227, s62, v95
	v_med3_f32 v228, v228, s62, v95
	v_med3_f32 v229, v229, s62, v95
	v_med3_f32 v230, v230, s62, v95
	v_med3_f32 v231, v231, s62, v95
	v_med3_f32 v232, v232, s62, v95
	v_med3_f32 v233, v233, s62, v95
	v_med3_f32 v234, v234, s62, v95
	v_med3_f32 v235, v235, s62, v95
	v_med3_f32 v236, v236, s62, v95
	v_med3_f32 v237, v237, s62, v95
	v_med3_f32 v238, v238, s62, v95
	v_med3_f32 v239, v239, s62, v95
	v_med3_f32 v240, v240, s62, v95
	v_med3_f32 v241, v241, s62, v95
	v_mov_b32_e32 v242, 0
	v_mov_b32_e32 v243, 0
	v_mov_b32_e32 v244, 0
	v_mov_b32_e32 v245, 0
	v_cvt_pk_fp8_f32 v242, v226, v227
	v_cvt_pk_fp8_f32 v243, v230, v231
	v_cvt_pk_fp8_f32 v244, v234, v235
	v_cvt_pk_fp8_f32 v245, v238, v239
	v_cvt_pk_fp8_f32 v242, v228, v229 op_sel:[0,0,1]
	v_cvt_pk_fp8_f32 v243, v232, v233 op_sel:[0,0,1]
	v_cvt_pk_fp8_f32 v244, v236, v237 op_sel:[0,0,1]
	v_cvt_pk_fp8_f32 v245, v240, v241 op_sel:[0,0,1]
	s_nop 0
	global_store_dwordx4 v77, v[242:245], s[6:7]
	ds_read_b32 v226, v213
	ds_read_b32 v227, v213 offset:512
	ds_read_b32 v228, v213 offset:1024
	ds_read_b32 v229, v213 offset:1536
	ds_read_b32 v230, v213 offset:2048
	ds_read_b32 v231, v213 offset:2560
	ds_read_b32 v232, v213 offset:3072
	ds_read_b32 v233, v213 offset:3584
	ds_read_b32 v234, v213 offset:4096
	ds_read_b32 v235, v213 offset:4608
	ds_read_b32 v236, v213 offset:5120
	ds_read_b32 v237, v213 offset:5632
	ds_read_b32 v238, v213 offset:6144
	ds_read_b32 v239, v213 offset:6656
	ds_read_b32 v240, v213 offset:7168
	ds_read_b32 v241, v213 offset:7680
	s_waitcnt lgkmcnt(0)
	v_max_f32_e32 v226, v226, v226
	v_max_f32_e32 v227, v227, v227
	v_max_f32_e32 v228, v228, v228
	v_max_f32_e32 v229, v229, v229
	v_max_f32_e32 v230, v230, v230
	v_max_f32_e32 v231, v231, v231
	v_max_f32_e32 v232, v232, v232
	v_max_f32_e32 v233, v233, v233
	v_max_f32_e32 v234, v234, v234
	v_max_f32_e32 v235, v235, v235
	v_max_f32_e32 v236, v236, v236
	v_max_f32_e32 v237, v237, v237
	v_max_f32_e32 v238, v238, v238
	v_max_f32_e32 v239, v239, v239
	v_max_f32_e32 v240, v240, v240
	v_max_f32_e32 v241, v241, v241
	v_med3_f32 v226, v226, s62, v95
	v_med3_f32 v227, v227, s62, v95
	v_med3_f32 v228, v228, s62, v95
	v_med3_f32 v229, v229, s62, v95
	v_med3_f32 v230, v230, s62, v95
	v_med3_f32 v231, v231, s62, v95
	v_med3_f32 v232, v232, s62, v95
	v_med3_f32 v233, v233, s62, v95
	v_med3_f32 v234, v234, s62, v95
	v_med3_f32 v235, v235, s62, v95
	v_med3_f32 v236, v236, s62, v95
	v_med3_f32 v237, v237, s62, v95
	v_med3_f32 v238, v238, s62, v95
	v_med3_f32 v239, v239, s62, v95
	v_med3_f32 v240, v240, s62, v95
	v_med3_f32 v241, v241, s62, v95
	v_mov_b32_e32 v242, 0
	v_mov_b32_e32 v243, 0
	v_mov_b32_e32 v244, 0
	v_mov_b32_e32 v245, 0
	v_cvt_pk_fp8_f32 v242, v226, v227
	v_cvt_pk_fp8_f32 v243, v230, v231
	v_cvt_pk_fp8_f32 v244, v234, v235
	v_cvt_pk_fp8_f32 v245, v238, v239
	v_cvt_pk_fp8_f32 v242, v228, v229 op_sel:[0,0,1]
	v_cvt_pk_fp8_f32 v243, v232, v233 op_sel:[0,0,1]
	v_cvt_pk_fp8_f32 v244, v236, v237 op_sel:[0,0,1]
	v_cvt_pk_fp8_f32 v245, v240, v241 op_sel:[0,0,1]
	s_nop 0
	global_store_dwordx4 v78, v[242:245], s[6:7]
	s_waitcnt vmcnt(12)
	v_mul_f32_e32 v176, v34, v176
	v_mul_f32_e32 v177, v34, v177
	v_mul_f32_e32 v178, v34, v178
	v_mul_f32_e32 v179, v34, v179
	ds_write_b128 v210, v[176:179]
	v_mul_f32_e32 v180, v35, v180
	v_mul_f32_e32 v181, v35, v181
	v_mul_f32_e32 v182, v35, v182
	v_mul_f32_e32 v183, v35, v183
	ds_write_b128 v210, v[180:183] offset:1024
	v_mul_f32_e32 v184, v36, v184
	v_mul_f32_e32 v185, v36, v185
	v_mul_f32_e32 v186, v36, v186
	v_mul_f32_e32 v187, v36, v187
	ds_write_b128 v210, v[184:187] offset:2048
	v_mul_f32_e32 v188, v37, v188
	v_mul_f32_e32 v189, v37, v189
	v_mul_f32_e32 v190, v37, v190
	v_mul_f32_e32 v191, v37, v191
	ds_write_b128 v210, v[188:191] offset:3072
	v_mul_f32_e32 v192, v38, v192
	v_mul_f32_e32 v193, v38, v193
	v_mul_f32_e32 v194, v38, v194
	v_mul_f32_e32 v195, v38, v195
	ds_write_b128 v210, v[192:195] offset:4096
	v_mul_f32_e32 v196, v39, v196
	v_mul_f32_e32 v197, v39, v197
	v_mul_f32_e32 v198, v39, v198
	v_mul_f32_e32 v199, v39, v199
	ds_write_b128 v210, v[196:199] offset:5120
	v_mul_f32_e32 v200, v40, v200
	v_mul_f32_e32 v201, v40, v201
	v_mul_f32_e32 v202, v40, v202
	v_mul_f32_e32 v203, v40, v203
	ds_write_b128 v210, v[200:203] offset:6144
	v_mul_f32_e32 v204, v41, v204
	v_mul_f32_e32 v205, v41, v205
	v_mul_f32_e32 v206, v41, v206
	v_mul_f32_e32 v207, v41, v207
	ds_write_b128 v210, v[204:207] offset:7168
	s_waitcnt lgkmcnt(0)
	s_barrier
; #define GAS __attribute__((address_space(1)))
;     const int pr = item >> 1, kb = 2 * (pr / nblk) + (item & 1), nb = pr % nblk, k0 = 64 * kb, n0 = 32 * nb;
;     const int nr = n0 + (lane & 31); const int sc = MAP == 1 ? src_col_in(nr) : nr;
;     float v[32];
; #pragma unroll
;     for (int i = 0; i < 32; ++i) v[i] = sc >= 0 ? W[(size_t)(k0 + 2 * i + (lane >> 5)) * Nsrc + sc] : 0.f;
; #pragma unroll
;     for (int i = 0; i < 32; ++i) { const int k = k0 + 2 * i + (lane >> 5); float x = v[i] * wscale; if (KS) x *= (k < ksplit ? ksA[k] : ksB[k - ksplit]); scr[(2 * i + (lane >> 5)) * 33 + (lane & 31)] = x; }
;     LDS_WAIT(); asm volatile("" ::: "memory");
;     const int c = lane & 7;
; #pragma unroll
;     for (int j = 0; j < 4; ++j) { const int n = (lane >> 3) + 8 * j; const LAS float* s = scr + (8 * c) * 33 + n;
;         const unsigned long long o = (unsigned long long)pg8::pk4_fp8(s[0 * 33], s[1 * 33], s[2 * 33], s[3 * 33]) | ((unsigned long long)pg8::pk4_fp8(s[4 * 33], s[5 * 33], s[6 * 33], s[7 * 33]) << 32);
;         *(GAS unsigned long long*)(WT + (size_t)(n0 + n) * K + k0 + 8 * c) = o; }
;     LDS_WAIT(); asm volatile("" ::: "memory");
; }
; __global__ void __launch_bounds__(NWAVES * 64, 2) hybrid_fwd(Args args) {
;     ...
;         for (int rep = 0; rep < REP_PRO; ++rep)
;         for (int it = gw; it < DEPTH * I_L; it += NGW) {
;             const int l = it / I_L; int r = it % I_L;
;             if (r < I_IN) { if (l >= PROJ_F8_FROM) p0_transpose_item_f8<true, 1>(args.in[2] + (size_t)l * DM * NSRC, DM, NSRC, NPROJ / 32, (unsigned char*)(ws + WS_WIN + l * SZ_WIN), WUP8_SCALE, args.in[1] + l * DM, args.in[1] + l * DM, DM, scr, r, lane);
;                 else p0_transpose_item<1, true>(args.in[2] + (size_t)l * DM * NSRC, DM, NSRC, NPROJ / 32, (bf16*)(ws + WS_WIN + l * SZ_WIN), args.in[1] + l * DM, args.in[1] + l * DM, DM, scr, r, lane); continue; } r -= I_IN;
;             if (r < I_O) { if (l >= WO_F8_FROM) p0_transpose_item_f8<true>(args.in[13] + (size_t)l * DM * DM, DM, DM, DM / 32, (unsigned char*)(ws + WS_WO + l * SZ_WO), 64.f, args.in[6] + l * 2048, args.in[12] + l * 2048, 2048, scr, r, lane);
;                 else p0_transpose_item<0, true>(args.in[13] + (size_t)l * DM * DM, DM, DM, DM / 32, (bf16*)(ws + WS_WO + l * SZ_WO), args.in[6] + l * 2048, args.in[12] + l * 2048, 2048, scr, r, lane); continue; } r -= I_O;
	s_add_u32 s8, s38, 0x1000
	s_addc_u32 s9, s39, 0
	global_load_dwordx4 v[176:179], v75, s[8:9]
	s_add_u32 s8, s8, 0x8000
	s_addc_u32 s9, s9, 0
	global_load_dwordx4 v[180:183], v75, s[8:9]
	s_add_u32 s8, s8, 0x8000
	s_addc_u32 s9, s9, 0
	global_load_dwordx4 v[184:187], v75, s[8:9]
	s_add_u32 s8, s8, 0x8000
	s_addc_u32 s9, s9, 0
	global_load_dwordx4 v[188:191], v75, s[8:9]
	s_add_u32 s8, s8, 0x8000
	s_addc_u32 s9, s9, 0
	global_load_dwordx4 v[192:195], v75, s[8:9]
	s_add_u32 s8, s8, 0x8000
	s_addc_u32 s9, s9, 0
	global_load_dwordx4 v[196:199], v75, s[8:9]
	s_add_u32 s8, s8, 0x8000
	s_addc_u32 s9, s9, 0
	global_load_dwordx4 v[200:203], v75, s[8:9]
	s_add_u32 s8, s8, 0x8000
	s_addc_u32 s9, s9, 0
	global_load_dwordx4 v[204:207], v75, s[8:9]
	s_add_u32 s6, s36, 0x3c00000
	s_addc_u32 s7, s37, 0
	ds_read_b32 v226, v212
	ds_read_b32 v227, v212 offset:512
	ds_read_b32 v228, v212 offset:1024
	ds_read_b32 v229, v212 offset:1536
	ds_read_b32 v230, v212 offset:2048
	ds_read_b32 v231, v212 offset:2560
	ds_read_b32 v232, v212 offset:3072
	ds_read_b32 v233, v212 offset:3584
	ds_read_b32 v234, v212 offset:4096
	ds_read_b32 v235, v212 offset:4608
	ds_read_b32 v236, v212 offset:5120
	ds_read_b32 v237, v212 offset:5632
	ds_read_b32 v238, v212 offset:6144
	ds_read_b32 v239, v212 offset:6656
	ds_read_b32 v240, v212 offset:7168
	ds_read_b32 v241, v212 offset:7680
	s_waitcnt lgkmcnt(0)
	v_max_f32_e32 v226, v226, v226
	v_max_f32_e32 v227, v227, v227
	v_max_f32_e32 v228, v228, v228
	v_max_f32_e32 v229, v229, v229
	v_max_f32_e32 v230, v230, v230
	v_max_f32_e32 v231, v231, v231
	v_max_f32_e32 v232, v232, v232
	v_max_f32_e32 v233, v233, v233
	v_max_f32_e32 v234, v234, v234
	v_max_f32_e32 v235, v235, v235
	v_max_f32_e32 v236, v236, v236
	v_max_f32_e32 v237, v237, v237
	v_max_f32_e32 v238, v238, v238
	v_max_f32_e32 v239, v239, v239
	v_max_f32_e32 v240, v240, v240
	v_max_f32_e32 v241, v241, v241
	v_med3_f32 v226, v226, s62, v95
	v_med3_f32 v227, v227, s62, v95
	v_med3_f32 v228, v228, s62, v95
	v_med3_f32 v229, v229, s62, v95
	v_med3_f32 v230, v230, s62, v95
	v_med3_f32 v231, v231, s62, v95
	v_med3_f32 v232, v232, s62, v95
	v_med3_f32 v233, v233, s62, v95
	v_med3_f32 v234, v234, s62, v95
	v_med3_f32 v235, v235, s62, v95
	v_med3_f32 v236, v236, s62, v95
	v_med3_f32 v237, v237, s62, v95
	v_med3_f32 v238, v238, s62, v95
	v_med3_f32 v239, v239, s62, v95
	v_med3_f32 v240, v240, s62, v95
	v_med3_f32 v241, v241, s62, v95
	v_mov_b32_e32 v242, 0
	v_mov_b32_e32 v243, 0
	v_mov_b32_e32 v244, 0
	v_mov_b32_e32 v245, 0
	v_cvt_pk_fp8_f32 v242, v226, v227
	v_cvt_pk_fp8_f32 v243, v230, v231
	v_cvt_pk_fp8_f32 v244, v234, v235
	v_cvt_pk_fp8_f32 v245, v238, v239
	v_cvt_pk_fp8_f32 v242, v228, v229 op_sel:[0,0,1]
	v_cvt_pk_fp8_f32 v243, v232, v233 op_sel:[0,0,1]
	v_cvt_pk_fp8_f32 v244, v236, v237 op_sel:[0,0,1]
	v_cvt_pk_fp8_f32 v245, v240, v241 op_sel:[0,0,1]
	s_nop 0
	global_store_dwordx4 v77, v[242:245], s[6:7]
	ds_read_b32 v226, v214
	ds_read_b32 v227, v214 offset:512
	ds_read_b32 v228, v214 offset:1024
	ds_read_b32 v229, v214 offset:1536
	ds_read_b32 v230, v214 offset:2048
	ds_read_b32 v231, v214 offset:2560
	ds_read_b32 v232, v214 offset:3072
	ds_read_b32 v233, v214 offset:3584
	ds_read_b32 v234, v214 offset:4096
	ds_read_b32 v235, v214 offset:4608
	ds_read_b32 v236, v214 offset:5120
	ds_read_b32 v237, v214 offset:5632
	ds_read_b32 v238, v214 offset:6144
	ds_read_b32 v239, v214 offset:6656
	ds_read_b32 v240, v214 offset:7168
	ds_read_b32 v241, v214 offset:7680
	s_waitcnt lgkmcnt(0)
	v_max_f32_e32 v226, v226, v226
	v_max_f32_e32 v227, v227, v227
	v_max_f32_e32 v228, v228, v228
	v_max_f32_e32 v229, v229, v229
	v_max_f32_e32 v230, v230, v230
	v_max_f32_e32 v231, v231, v231
	v_max_f32_e32 v232, v232, v232
	v_max_f32_e32 v233, v233, v233
	v_max_f32_e32 v234, v234, v234
	v_max_f32_e32 v235, v235, v235
	v_max_f32_e32 v236, v236, v236
	v_max_f32_e32 v237, v237, v237
	v_max_f32_e32 v238, v238, v238
	v_max_f32_e32 v239, v239, v239
	v_max_f32_e32 v240, v240, v240
	v_max_f32_e32 v241, v241, v241
	v_med3_f32 v226, v226, s62, v95
	v_med3_f32 v227, v227, s62, v95
	v_med3_f32 v228, v228, s62, v95
	v_med3_f32 v229, v229, s62, v95
	v_med3_f32 v230, v230, s62, v95
	v_med3_f32 v231, v231, s62, v95
	v_med3_f32 v232, v232, s62, v95
	v_med3_f32 v233, v233, s62, v95
	v_med3_f32 v234, v234, s62, v95
	v_med3_f32 v235, v235, s62, v95
	v_med3_f32 v236, v236, s62, v95
	v_med3_f32 v237, v237, s62, v95
	v_med3_f32 v238, v238, s62, v95
	v_med3_f32 v239, v239, s62, v95
	v_med3_f32 v240, v240, s62, v95
	v_med3_f32 v241, v241, s62, v95
	v_mov_b32_e32 v242, 0
	v_mov_b32_e32 v243, 0
	v_mov_b32_e32 v244, 0
	v_mov_b32_e32 v245, 0
	v_cvt_pk_fp8_f32 v242, v226, v227
	v_cvt_pk_fp8_f32 v243, v230, v231
	v_cvt_pk_fp8_f32 v244, v234, v235
	v_cvt_pk_fp8_f32 v245, v238, v239
	v_cvt_pk_fp8_f32 v242, v228, v229 op_sel:[0,0,1]
	v_cvt_pk_fp8_f32 v243, v232, v233 op_sel:[0,0,1]
	v_cvt_pk_fp8_f32 v244, v236, v237 op_sel:[0,0,1]
	v_cvt_pk_fp8_f32 v245, v240, v241 op_sel:[0,0,1]
	s_nop 0
	global_store_dwordx4 v78, v[242:245], s[6:7]
	s_waitcnt vmcnt(12)
	v_mul_f32_e32 v144, 0x43000000, v144
	v_mul_f32_e32 v145, 0x43000000, v145
	v_mul_f32_e32 v146, 0x43000000, v146
	v_mul_f32_e32 v147, 0x43000000, v147
	ds_write_b128 v209, v[144:147]
	v_mul_f32_e32 v148, 0x43000000, v148
	v_mul_f32_e32 v149, 0x43000000, v149
	v_mul_f32_e32 v150, 0x43000000, v150
	v_mul_f32_e32 v151, 0x43000000, v151
	ds_write_b128 v209, v[148:151] offset:1024
	v_mul_f32_e32 v152, 0x43000000, v152
	v_mul_f32_e32 v153, 0x43000000, v153
	v_mul_f32_e32 v154, 0x43000000, v154
	v_mul_f32_e32 v155, 0x43000000, v155
	ds_write_b128 v209, v[152:155] offset:2048
	v_mul_f32_e32 v156, 0x43000000, v156
	v_mul_f32_e32 v157, 0x43000000, v157
	v_mul_f32_e32 v158, 0x43000000, v158
	v_mul_f32_e32 v159, 0x43000000, v159
	ds_write_b128 v209, v[156:159] offset:3072
	v_mul_f32_e32 v160, 0x43000000, v160
	v_mul_f32_e32 v161, 0x43000000, v161
	v_mul_f32_e32 v162, 0x43000000, v162
	v_mul_f32_e32 v163, 0x43000000, v163
	ds_write_b128 v209, v[160:163] offset:4096
	v_mul_f32_e32 v164, 0x43000000, v164
	v_mul_f32_e32 v165, 0x43000000, v165
	v_mul_f32_e32 v166, 0x43000000, v166
	v_mul_f32_e32 v167, 0x43000000, v167
	ds_write_b128 v209, v[164:167] offset:5120
	v_mul_f32_e32 v168, 0x43000000, v168
	v_mul_f32_e32 v169, 0x43000000, v169
	v_mul_f32_e32 v170, 0x43000000, v170
	v_mul_f32_e32 v171, 0x43000000, v171
	ds_write_b128 v209, v[168:171] offset:6144
	v_mul_f32_e32 v172, 0x43000000, v172
	v_mul_f32_e32 v173, 0x43000000, v173
	v_mul_f32_e32 v174, 0x43000000, v174
	v_mul_f32_e32 v175, 0x43000000, v175
	ds_write_b128 v209, v[172:175] offset:7168
	s_waitcnt lgkmcnt(0)
	s_barrier
; #define GAS __attribute__((address_space(1)))
;     const int pr = item >> 1, kb = 2 * (pr / nblk) + (item & 1), nb = pr % nblk, k0 = 64 * kb, n0 = 32 * nb;
;     const int nr = n0 + (lane & 31); const int sc = MAP == 1 ? src_col_in(nr) : nr;
;     float v[32];
; #pragma unroll
;     for (int i = 0; i < 32; ++i) v[i] = sc >= 0 ? W[(size_t)(k0 + 2 * i + (lane >> 5)) * Nsrc + sc] : 0.f;
; #pragma unroll
;     for (int i = 0; i < 32; ++i) { const int k = k0 + 2 * i + (lane >> 5); float x = v[i] * wscale; if (KS) x *= (k < ksplit ? ksA[k] : ksB[k - ksplit]); scr[(2 * i + (lane >> 5)) * 33 + (lane & 31)] = x; }
;     LDS_WAIT(); asm volatile("" ::: "memory");
;     const int c = lane & 7;
; #pragma unroll
;     for (int j = 0; j < 4; ++j) { const int n = (lane >> 3) + 8 * j; const LAS float* s = scr + (8 * c) * 33 + n;
;         const unsigned long long o = (unsigned long long)pg8::pk4_fp8(s[0 * 33], s[1 * 33], s[2 * 33], s[3 * 33]) | ((unsigned long long)pg8::pk4_fp8(s[4 * 33], s[5 * 33], s[6 * 33], s[7 * 33]) << 32);
;         *(GAS unsigned long long*)(WT + (size_t)(n0 + n) * K + k0 + 8 * c) = o; }
;     LDS_WAIT(); asm volatile("" ::: "memory");
; }
; __global__ void __launch_bounds__(NWAVES * 64, 2) hybrid_fwd(Args args) {
;     ...
;         for (int rep = 0; rep < REP_PRO; ++rep)
;         for (int it = gw; it < DEPTH * I_L; it += NGW) {
;             const int l = it / I_L; int r = it % I_L;
;             if (r < I_IN) { if (l >= PROJ_F8_FROM) p0_transpose_item_f8<true, 1>(args.in[2] + (size_t)l * DM * NSRC, DM, NSRC, NPROJ / 32, (unsigned char*)(ws + WS_WIN + l * SZ_WIN), WUP8_SCALE, args.in[1] + l * DM, args.in[1] + l * DM, DM, scr, r, lane);
;                 else p0_transpose_item<1, true>(args.in[2] + (size_t)l * DM * NSRC, DM, NSRC, NPROJ / 32, (bf16*)(ws + WS_WIN + l * SZ_WIN), args.in[1] + l * DM, args.in[1] + l * DM, DM, scr, r, lane); continue; } r -= I_IN;
;             if (r < I_O) { if (l >= WO_F8_FROM) p0_transpose_item_f8<true>(args.in[13] + (size_t)l * DM * DM, DM, DM, DM / 32, (unsigned char*)(ws + WS_WO + l * SZ_WO), 64.f, args.in[6] + l * 2048, args.in[12] + l * 2048, 2048, scr, r, lane);
;                 else p0_transpose_item<0, true>(args.in[13] + (size_t)l * DM * DM, DM, DM, DM / 32, (bf16*)(ws + WS_WO + l * SZ_WO), args.in[6] + l * 2048, args.in[12] + l * 2048, 2048, scr, r, lane); continue; } r -= I_O;
	s_add_u32 s8, s38, 0x2000
	s_addc_u32 s9, s39, 0
	global_load_dwordx4 v[144:147], v75, s[8:9]
	s_add_u32 s8, s8, 0x8000
	s_addc_u32 s9, s9, 0
	global_load_dwordx4 v[148:151], v75, s[8:9]
	s_add_u32 s8, s8, 0x8000
	s_addc_u32 s9, s9, 0
	global_load_dwordx4 v[152:155], v75, s[8:9]
	s_add_u32 s8, s8, 0x8000
	s_addc_u32 s9, s9, 0
	global_load_dwordx4 v[156:159], v75, s[8:9]
	s_add_u32 s8, s8, 0x8000
	s_addc_u32 s9, s9, 0
	global_load_dwordx4 v[160:163], v75, s[8:9]
	s_add_u32 s8, s8, 0x8000
	s_addc_u32 s9, s9, 0
	global_load_dwordx4 v[164:167], v75, s[8:9]
	s_add_u32 s8, s8, 0x8000
	s_addc_u32 s9, s9, 0
	global_load_dwordx4 v[168:171], v75, s[8:9]
	s_add_u32 s8, s8, 0x8000
	s_addc_u32 s9, s9, 0
	global_load_dwordx4 v[172:175], v75, s[8:9]
	s_mov_b64 s[6:7], s[40:41]
	ds_read_b32 v226, v211
	ds_read_b32 v227, v211 offset:512
	ds_read_b32 v228, v211 offset:1024
	ds_read_b32 v229, v211 offset:1536
	ds_read_b32 v230, v211 offset:2048
	ds_read_b32 v231, v211 offset:2560
	ds_read_b32 v232, v211 offset:3072
	ds_read_b32 v233, v211 offset:3584
	ds_read_b32 v234, v211 offset:4096
	ds_read_b32 v235, v211 offset:4608
	ds_read_b32 v236, v211 offset:5120
	ds_read_b32 v237, v211 offset:5632
	ds_read_b32 v238, v211 offset:6144
	ds_read_b32 v239, v211 offset:6656
	ds_read_b32 v240, v211 offset:7168
	ds_read_b32 v241, v211 offset:7680
	s_waitcnt lgkmcnt(0)
	v_max_f32_e32 v226, v226, v226
	v_max_f32_e32 v227, v227, v227
	v_max_f32_e32 v228, v228, v228
	v_max_f32_e32 v229, v229, v229
	v_max_f32_e32 v230, v230, v230
	v_max_f32_e32 v231, v231, v231
	v_max_f32_e32 v232, v232, v232
	v_max_f32_e32 v233, v233, v233
	v_max_f32_e32 v234, v234, v234
	v_max_f32_e32 v235, v235, v235
	v_max_f32_e32 v236, v236, v236
	v_max_f32_e32 v237, v237, v237
	v_max_f32_e32 v238, v238, v238
	v_max_f32_e32 v239, v239, v239
	v_max_f32_e32 v240, v240, v240
	v_max_f32_e32 v241, v241, v241
	v_med3_f32 v226, v226, s62, v95
	v_med3_f32 v227, v227, s62, v95
	v_med3_f32 v228, v228, s62, v95
	v_med3_f32 v229, v229, s62, v95
	v_med3_f32 v230, v230, s62, v95
	v_med3_f32 v231, v231, s62, v95
	v_med3_f32 v232, v232, s62, v95
	v_med3_f32 v233, v233, s62, v95
	v_med3_f32 v234, v234, s62, v95
	v_med3_f32 v235, v235, s62, v95
	v_med3_f32 v236, v236, s62, v95
	v_med3_f32 v237, v237, s62, v95
	v_med3_f32 v238, v238, s62, v95
	v_med3_f32 v239, v239, s62, v95
	v_med3_f32 v240, v240, s62, v95
	v_med3_f32 v241, v241, s62, v95
	v_mov_b32_e32 v242, 0
	v_mov_b32_e32 v243, 0
	v_mov_b32_e32 v244, 0
	v_mov_b32_e32 v245, 0
	v_cvt_pk_fp8_f32 v242, v226, v227
	v_cvt_pk_fp8_f32 v243, v230, v231
	v_cvt_pk_fp8_f32 v244, v234, v235
	v_cvt_pk_fp8_f32 v245, v238, v239
	v_cvt_pk_fp8_f32 v242, v228, v229 op_sel:[0,0,1]
	v_cvt_pk_fp8_f32 v243, v232, v233 op_sel:[0,0,1]
	v_cvt_pk_fp8_f32 v244, v236, v237 op_sel:[0,0,1]
	v_cvt_pk_fp8_f32 v245, v240, v241 op_sel:[0,0,1]
	s_nop 0
	global_store_dwordx4 v79, v[242:245], s[6:7]
	ds_read_b32 v226, v213
	ds_read_b32 v227, v213 offset:512
	ds_read_b32 v228, v213 offset:1024
	ds_read_b32 v229, v213 offset:1536
	ds_read_b32 v230, v213 offset:2048
	ds_read_b32 v231, v213 offset:2560
	ds_read_b32 v232, v213 offset:3072
	ds_read_b32 v233, v213 offset:3584
	ds_read_b32 v234, v213 offset:4096
	ds_read_b32 v235, v213 offset:4608
	ds_read_b32 v236, v213 offset:5120
	ds_read_b32 v237, v213 offset:5632
	ds_read_b32 v238, v213 offset:6144
	ds_read_b32 v239, v213 offset:6656
	ds_read_b32 v240, v213 offset:7168
	ds_read_b32 v241, v213 offset:7680
	s_waitcnt lgkmcnt(0)
	v_max_f32_e32 v226, v226, v226
	v_max_f32_e32 v227, v227, v227
	v_max_f32_e32 v228, v228, v228
	v_max_f32_e32 v229, v229, v229
	v_max_f32_e32 v230, v230, v230
	v_max_f32_e32 v231, v231, v231
	v_max_f32_e32 v232, v232, v232
	v_max_f32_e32 v233, v233, v233
	v_max_f32_e32 v234, v234, v234
	v_max_f32_e32 v235, v235, v235
	v_max_f32_e32 v236, v236, v236
	v_max_f32_e32 v237, v237, v237
	v_max_f32_e32 v238, v238, v238
	v_max_f32_e32 v239, v239, v239
	v_max_f32_e32 v240, v240, v240
	v_max_f32_e32 v241, v241, v241
	v_med3_f32 v226, v226, s62, v95
	v_med3_f32 v227, v227, s62, v95
	v_med3_f32 v228, v228, s62, v95
	v_med3_f32 v229, v229, s62, v95
	v_med3_f32 v230, v230, s62, v95
	v_med3_f32 v231, v231, s62, v95
	v_med3_f32 v232, v232, s62, v95
	v_med3_f32 v233, v233, s62, v95
	v_med3_f32 v234, v234, s62, v95
	v_med3_f32 v235, v235, s62, v95
	v_med3_f32 v236, v236, s62, v95
	v_med3_f32 v237, v237, s62, v95
	v_med3_f32 v238, v238, s62, v95
	v_med3_f32 v239, v239, s62, v95
	v_med3_f32 v240, v240, s62, v95
	v_med3_f32 v241, v241, s62, v95
	v_mov_b32_e32 v242, 0
	v_mov_b32_e32 v243, 0
	v_mov_b32_e32 v244, 0
	v_mov_b32_e32 v245, 0
	v_cvt_pk_fp8_f32 v242, v226, v227
	v_cvt_pk_fp8_f32 v243, v230, v231
	v_cvt_pk_fp8_f32 v244, v234, v235
	v_cvt_pk_fp8_f32 v245, v238, v239
	v_cvt_pk_fp8_f32 v242, v228, v229 op_sel:[0,0,1]
	v_cvt_pk_fp8_f32 v243, v232, v233 op_sel:[0,0,1]
	v_cvt_pk_fp8_f32 v244, v236, v237 op_sel:[0,0,1]
	v_cvt_pk_fp8_f32 v245, v240, v241 op_sel:[0,0,1]
	s_nop 0
	global_store_dwordx4 v80, v[242:245], s[6:7]
	s_waitcnt vmcnt(12)
	v_mul_f32_e32 v176, 0x43000000, v176
	v_mul_f32_e32 v177, 0x43000000, v177
	v_mul_f32_e32 v178, 0x43000000, v178
	v_mul_f32_e32 v179, 0x43000000, v179
	ds_write_b128 v210, v[176:179]
	v_mul_f32_e32 v180, 0x43000000, v180
	v_mul_f32_e32 v181, 0x43000000, v181
	v_mul_f32_e32 v182, 0x43000000, v182
	v_mul_f32_e32 v183, 0x43000000, v183
	ds_write_b128 v210, v[180:183] offset:1024
	v_mul_f32_e32 v184, 0x43000000, v184
	v_mul_f32_e32 v185, 0x43000000, v185
	v_mul_f32_e32 v186, 0x43000000, v186
	v_mul_f32_e32 v187, 0x43000000, v187
	ds_write_b128 v210, v[184:187] offset:2048
	v_mul_f32_e32 v188, 0x43000000, v188
	v_mul_f32_e32 v189, 0x43000000, v189
	v_mul_f32_e32 v190, 0x43000000, v190
	v_mul_f32_e32 v191, 0x43000000, v191
	ds_write_b128 v210, v[188:191] offset:3072
	v_mul_f32_e32 v192, 0x43000000, v192
	v_mul_f32_e32 v193, 0x43000000, v193
	v_mul_f32_e32 v194, 0x43000000, v194
	v_mul_f32_e32 v195, 0x43000000, v195
	ds_write_b128 v210, v[192:195] offset:4096
	v_mul_f32_e32 v196, 0x43000000, v196
	v_mul_f32_e32 v197, 0x43000000, v197
	v_mul_f32_e32 v198, 0x43000000, v198
	v_mul_f32_e32 v199, 0x43000000, v199
	ds_write_b128 v210, v[196:199] offset:5120
	v_mul_f32_e32 v200, 0x43000000, v200
	v_mul_f32_e32 v201, 0x43000000, v201
	v_mul_f32_e32 v202, 0x43000000, v202
	v_mul_f32_e32 v203, 0x43000000, v203
	ds_write_b128 v210, v[200:203] offset:6144
	v_mul_f32_e32 v204, 0x43000000, v204
	v_mul_f32_e32 v205, 0x43000000, v205
	v_mul_f32_e32 v206, 0x43000000, v206
	v_mul_f32_e32 v207, 0x43000000, v207
	ds_write_b128 v210, v[204:207] offset:7168
	s_waitcnt lgkmcnt(0)
	s_barrier
; #define GAS __attribute__((address_space(1)))
;     const int pr = item >> 1, kb = 2 * (pr / nblk) + (item & 1), nb = pr % nblk, k0 = 64 * kb, n0 = 32 * nb;
;     const int nr = n0 + (lane & 31); const int sc = MAP == 1 ? src_col_in(nr) : nr;
;     float v[32];
; #pragma unroll
;     for (int i = 0; i < 32; ++i) v[i] = sc >= 0 ? W[(size_t)(k0 + 2 * i + (lane >> 5)) * Nsrc + sc] : 0.f;
; #pragma unroll
;     for (int i = 0; i < 32; ++i) { const int k = k0 + 2 * i + (lane >> 5); float x = v[i] * wscale; if (KS) x *= (k < ksplit ? ksA[k] : ksB[k - ksplit]); scr[(2 * i + (lane >> 5)) * 33 + (lane & 31)] = x; }
;     LDS_WAIT(); asm volatile("" ::: "memory");
;     const int c = lane & 7;
; #pragma unroll
;     for (int j = 0; j < 4; ++j) { const int n = (lane >> 3) + 8 * j; const LAS float* s = scr + (8 * c) * 33 + n;
;         const unsigned long long o = (unsigned long long)pg8::pk4_fp8(s[0 * 33], s[1 * 33], s[2 * 33], s[3 * 33]) | ((unsigned long long)pg8::pk4_fp8(s[4 * 33], s[5 * 33], s[6 * 33], s[7 * 33]) << 32);
;         *(GAS unsigned long long*)(WT + (size_t)(n0 + n) * K + k0 + 8 * c) = o; }
;     LDS_WAIT(); asm volatile("" ::: "memory");
; }
; __global__ void __launch_bounds__(NWAVES * 64, 2) hybrid_fwd(Args args) {
;     ...
;         for (int rep = 0; rep < REP_PRO; ++rep)
;         for (int it = gw; it < DEPTH * I_L; it += NGW) {
;             const int l = it / I_L; int r = it % I_L;
;             if (r < I_IN) { if (l >= PROJ_F8_FROM) p0_transpose_item_f8<true, 1>(args.in[2] + (size_t)l * DM * NSRC, DM, NSRC, NPROJ / 32, (unsigned char*)(ws + WS_WIN + l * SZ_WIN), WUP8_SCALE, args.in[1] + l * DM, args.in[1] + l * DM, DM, scr, r, lane);
;                 else p0_transpose_item<1, true>(args.in[2] + (size_t)l * DM * NSRC, DM, NSRC, NPROJ / 32, (bf16*)(ws + WS_WIN + l * SZ_WIN), args.in[1] + l * DM, args.in[1] + l * DM, DM, scr, r, lane); continue; } r -= I_IN;
;             if (r < I_O) { if (l >= WO_F8_FROM) p0_transpose_item_f8<true>(args.in[13] + (size_t)l * DM * DM, DM, DM, DM / 32, (unsigned char*)(ws + WS_WO + l * SZ_WO), 64.f, args.in[6] + l * 2048, args.in[12] + l * 2048, 2048, scr, r, lane);
;                 else p0_transpose_item<0, true>(args.in[13] + (size_t)l * DM * DM, DM, DM, DM / 32, (bf16*)(ws + WS_WO + l * SZ_WO), args.in[6] + l * 2048, args.in[12] + l * 2048, 2048, scr, r, lane); continue; } r -= I_O;
	s_add_u32 s8, s38, 0x3000
	s_addc_u32 s9, s39, 0
	global_load_dwordx4 v[176:179], v75, s[8:9]
	s_add_u32 s8, s8, 0x8000
	s_addc_u32 s9, s9, 0
	global_load_dwordx4 v[180:183], v75, s[8:9]
	s_add_u32 s8, s8, 0x8000
	s_addc_u32 s9, s9, 0
	global_load_dwordx4 v[184:187], v75, s[8:9]
	s_add_u32 s8, s8, 0x8000
	s_addc_u32 s9, s9, 0
	global_load_dwordx4 v[188:191], v75, s[8:9]
	s_add_u32 s8, s8, 0x8000
	s_addc_u32 s9, s9, 0
	global_load_dwordx4 v[192:195], v75, s[8:9]
	s_add_u32 s8, s8, 0x8000
	s_addc_u32 s9, s9, 0
	global_load_dwordx4 v[196:199], v75, s[8:9]
	s_add_u32 s8, s8, 0x8000
	s_addc_u32 s9, s9, 0
	global_load_dwordx4 v[200:203], v75, s[8:9]
	s_add_u32 s8, s8, 0x8000
	s_addc_u32 s9, s9, 0
	global_load_dwordx4 v[204:207], v75, s[8:9]
	s_add_u32 s6, s40, 0x1000000
	s_addc_u32 s7, s41, 0
	ds_read_b32 v226, v212
	ds_read_b32 v227, v212 offset:512
	ds_read_b32 v228, v212 offset:1024
	ds_read_b32 v229, v212 offset:1536
	ds_read_b32 v230, v212 offset:2048
	ds_read_b32 v231, v212 offset:2560
	ds_read_b32 v232, v212 offset:3072
	ds_read_b32 v233, v212 offset:3584
	ds_read_b32 v234, v212 offset:4096
	ds_read_b32 v235, v212 offset:4608
	ds_read_b32 v236, v212 offset:5120
	ds_read_b32 v237, v212 offset:5632
	ds_read_b32 v238, v212 offset:6144
	ds_read_b32 v239, v212 offset:6656
	ds_read_b32 v240, v212 offset:7168
	ds_read_b32 v241, v212 offset:7680
	s_waitcnt lgkmcnt(0)
	v_max_f32_e32 v226, v226, v226
	v_max_f32_e32 v227, v227, v227
	v_max_f32_e32 v228, v228, v228
	v_max_f32_e32 v229, v229, v229
	v_max_f32_e32 v230, v230, v230
	v_max_f32_e32 v231, v231, v231
	v_max_f32_e32 v232, v232, v232
	v_max_f32_e32 v233, v233, v233
	v_max_f32_e32 v234, v234, v234
	v_max_f32_e32 v235, v235, v235
	v_max_f32_e32 v236, v236, v236
	v_max_f32_e32 v237, v237, v237
	v_max_f32_e32 v238, v238, v238
	v_max_f32_e32 v239, v239, v239
	v_max_f32_e32 v240, v240, v240
	v_max_f32_e32 v241, v241, v241
	v_med3_f32 v226, v226, s62, v95
	v_med3_f32 v227, v227, s62, v95
	v_med3_f32 v228, v228, s62, v95
	v_med3_f32 v229, v229, s62, v95
	v_med3_f32 v230, v230, s62, v95
	v_med3_f32 v231, v231, s62, v95
	v_med3_f32 v232, v232, s62, v95
	v_med3_f32 v233, v233, s62, v95
	v_med3_f32 v234, v234, s62, v95
	v_med3_f32 v235, v235, s62, v95
	v_med3_f32 v236, v236, s62, v95
	v_med3_f32 v237, v237, s62, v95
	v_med3_f32 v238, v238, s62, v95
	v_med3_f32 v239, v239, s62, v95
	v_med3_f32 v240, v240, s62, v95
	v_med3_f32 v241, v241, s62, v95
	v_mov_b32_e32 v242, 0
	v_mov_b32_e32 v243, 0
	v_mov_b32_e32 v244, 0
	v_mov_b32_e32 v245, 0
	v_cvt_pk_fp8_f32 v242, v226, v227
	v_cvt_pk_fp8_f32 v243, v230, v231
	v_cvt_pk_fp8_f32 v244, v234, v235
	v_cvt_pk_fp8_f32 v245, v238, v239
	v_cvt_pk_fp8_f32 v242, v228, v229 op_sel:[0,0,1]
	v_cvt_pk_fp8_f32 v243, v232, v233 op_sel:[0,0,1]
	v_cvt_pk_fp8_f32 v244, v236, v237 op_sel:[0,0,1]
	v_cvt_pk_fp8_f32 v245, v240, v241 op_sel:[0,0,1]
	s_nop 0
	global_store_dwordx4 v79, v[242:245], s[6:7]
	ds_read_b32 v226, v214
	ds_read_b32 v227, v214 offset:512
	ds_read_b32 v228, v214 offset:1024
	ds_read_b32 v229, v214 offset:1536
	ds_read_b32 v230, v214 offset:2048
	ds_read_b32 v231, v214 offset:2560
	ds_read_b32 v232, v214 offset:3072
	ds_read_b32 v233, v214 offset:3584
	ds_read_b32 v234, v214 offset:4096
	ds_read_b32 v235, v214 offset:4608
	ds_read_b32 v236, v214 offset:5120
	ds_read_b32 v237, v214 offset:5632
	ds_read_b32 v238, v214 offset:6144
	ds_read_b32 v239, v214 offset:6656
	ds_read_b32 v240, v214 offset:7168
	ds_read_b32 v241, v214 offset:7680
	s_waitcnt lgkmcnt(0)
	v_max_f32_e32 v226, v226, v226
	v_max_f32_e32 v227, v227, v227
	v_max_f32_e32 v228, v228, v228
	v_max_f32_e32 v229, v229, v229
	v_max_f32_e32 v230, v230, v230
	v_max_f32_e32 v231, v231, v231
	v_max_f32_e32 v232, v232, v232
	v_max_f32_e32 v233, v233, v233
	v_max_f32_e32 v234, v234, v234
	v_max_f32_e32 v235, v235, v235
	v_max_f32_e32 v236, v236, v236
	v_max_f32_e32 v237, v237, v237
	v_max_f32_e32 v238, v238, v238
	v_max_f32_e32 v239, v239, v239
	v_max_f32_e32 v240, v240, v240
	v_max_f32_e32 v241, v241, v241
	v_med3_f32 v226, v226, s62, v95
	v_med3_f32 v227, v227, s62, v95
	v_med3_f32 v228, v228, s62, v95
	v_med3_f32 v229, v229, s62, v95
	v_med3_f32 v230, v230, s62, v95
	v_med3_f32 v231, v231, s62, v95
	v_med3_f32 v232, v232, s62, v95
	v_med3_f32 v233, v233, s62, v95
	v_med3_f32 v234, v234, s62, v95
	v_med3_f32 v235, v235, s62, v95
	v_med3_f32 v236, v236, s62, v95
	v_med3_f32 v237, v237, s62, v95
	v_med3_f32 v238, v238, s62, v95
	v_med3_f32 v239, v239, s62, v95
	v_med3_f32 v240, v240, s62, v95
	v_med3_f32 v241, v241, s62, v95
	v_mov_b32_e32 v242, 0
	v_mov_b32_e32 v243, 0
	v_mov_b32_e32 v244, 0
	v_mov_b32_e32 v245, 0
	v_cvt_pk_fp8_f32 v242, v226, v227
	v_cvt_pk_fp8_f32 v243, v230, v231
	v_cvt_pk_fp8_f32 v244, v234, v235
	v_cvt_pk_fp8_f32 v245, v238, v239
	v_cvt_pk_fp8_f32 v242, v228, v229 op_sel:[0,0,1]
	v_cvt_pk_fp8_f32 v243, v232, v233 op_sel:[0,0,1]
	v_cvt_pk_fp8_f32 v244, v236, v237 op_sel:[0,0,1]
	v_cvt_pk_fp8_f32 v245, v240, v241 op_sel:[0,0,1]
	s_nop 0
	global_store_dwordx4 v80, v[242:245], s[6:7]
	s_waitcnt vmcnt(12)
	v_mul_f32_e32 v144, 0x43000000, v144
	v_mul_f32_e32 v145, 0x43000000, v145
	v_mul_f32_e32 v146, 0x43000000, v146
	v_mul_f32_e32 v147, 0x43000000, v147
	ds_write_b128 v209, v[144:147]
	v_mul_f32_e32 v148, 0x43000000, v148
	v_mul_f32_e32 v149, 0x43000000, v149
	v_mul_f32_e32 v150, 0x43000000, v150
	v_mul_f32_e32 v151, 0x43000000, v151
	ds_write_b128 v209, v[148:151] offset:1024
	v_mul_f32_e32 v152, 0x43000000, v152
	v_mul_f32_e32 v153, 0x43000000, v153
	v_mul_f32_e32 v154, 0x43000000, v154
	v_mul_f32_e32 v155, 0x43000000, v155
	ds_write_b128 v209, v[152:155] offset:2048
	v_mul_f32_e32 v156, 0x43000000, v156
	v_mul_f32_e32 v157, 0x43000000, v157
	v_mul_f32_e32 v158, 0x43000000, v158
	v_mul_f32_e32 v159, 0x43000000, v159
	ds_write_b128 v209, v[156:159] offset:3072
	v_mul_f32_e32 v160, 0x43000000, v160
	v_mul_f32_e32 v161, 0x43000000, v161
	v_mul_f32_e32 v162, 0x43000000, v162
	v_mul_f32_e32 v163, 0x43000000, v163
	ds_write_b128 v209, v[160:163] offset:4096
	v_mul_f32_e32 v164, 0x43000000, v164
	v_mul_f32_e32 v165, 0x43000000, v165
	v_mul_f32_e32 v166, 0x43000000, v166
	v_mul_f32_e32 v167, 0x43000000, v167
	ds_write_b128 v209, v[164:167] offset:5120
	v_mul_f32_e32 v168, 0x43000000, v168
	v_mul_f32_e32 v169, 0x43000000, v169
	v_mul_f32_e32 v170, 0x43000000, v170
	v_mul_f32_e32 v171, 0x43000000, v171
	ds_write_b128 v209, v[168:171] offset:6144
	v_mul_f32_e32 v172, 0x43000000, v172
	v_mul_f32_e32 v173, 0x43000000, v173
	v_mul_f32_e32 v174, 0x43000000, v174
	v_mul_f32_e32 v175, 0x43000000, v175
	ds_write_b128 v209, v[172:175] offset:7168
	s_waitcnt lgkmcnt(0)
	s_barrier
; #define GAS __attribute__((address_space(1)))
;     const int pr = item >> 1, kb = 2 * (pr / nblk) + (item & 1), nb = pr % nblk, k0 = 64 * kb, n0 = 32 * nb;
;     const int nr = n0 + (lane & 31); const int sc = MAP == 1 ? src_col_in(nr) : nr;
;     float v[32];
; #pragma unroll
;     for (int i = 0; i < 32; ++i) v[i] = sc >= 0 ? W[(size_t)(k0 + 2 * i + (lane >> 5)) * Nsrc + sc] : 0.f;
; #pragma unroll
;     for (int i = 0; i < 32; ++i) { const int k = k0 + 2 * i + (lane >> 5); float x = v[i] * wscale; if (KS) x *= (k < ksplit ? ksA[k] : ksB[k - ksplit]); scr[(2 * i + (lane >> 5)) * 33 + (lane & 31)] = x; }
;     LDS_WAIT(); asm volatile("" ::: "memory");
;     const int c = lane & 7;
; #pragma unroll
;     for (int j = 0; j < 4; ++j) { const int n = (lane >> 3) + 8 * j; const LAS float* s = scr + (8 * c) * 33 + n;
;         const unsigned long long o = (unsigned long long)pg8::pk4_fp8(s[0 * 33], s[1 * 33], s[2 * 33], s[3 * 33]) | ((unsigned long long)pg8::pk4_fp8(s[4 * 33], s[5 * 33], s[6 * 33], s[7 * 33]) << 32);
;         *(GAS unsigned long long*)(WT + (size_t)(n0 + n) * K + k0 + 8 * c) = o; }
;     LDS_WAIT(); asm volatile("" ::: "memory");
; }
; __global__ void __launch_bounds__(NWAVES * 64, 2) hybrid_fwd(Args args) {
;     ...
;         for (int rep = 0; rep < REP_PRO; ++rep)
;         for (int it = gw; it < DEPTH * I_L; it += NGW) {
;             const int l = it / I_L; int r = it % I_L;
;             if (r < I_IN) { if (l >= PROJ_F8_FROM) p0_transpose_item_f8<true, 1>(args.in[2] + (size_t)l * DM * NSRC, DM, NSRC, NPROJ / 32, (unsigned char*)(ws + WS_WIN + l * SZ_WIN), WUP8_SCALE, args.in[1] + l * DM, args.in[1] + l * DM, DM, scr, r, lane);
;                 else p0_transpose_item<1, true>(args.in[2] + (size_t)l * DM * NSRC, DM, NSRC, NPROJ / 32, (bf16*)(ws + WS_WIN + l * SZ_WIN), args.in[1] + l * DM, args.in[1] + l * DM, DM, scr, r, lane); continue; } r -= I_IN;
;             if (r < I_O) { if (l >= WO_F8_FROM) p0_transpose_item_f8<true>(args.in[13] + (size_t)l * DM * DM, DM, DM, DM / 32, (unsigned char*)(ws + WS_WO + l * SZ_WO), 64.f, args.in[6] + l * 2048, args.in[12] + l * 2048, 2048, scr, r, lane);
;                 else p0_transpose_item<0, true>(args.in[13] + (size_t)l * DM * DM, DM, DM, DM / 32, (bf16*)(ws + WS_WO + l * SZ_WO), args.in[6] + l * 2048, args.in[12] + l * 2048, 2048, scr, r, lane); continue; } r -= I_O;
	s_add_u32 s8, s38, 0x4000000
	s_addc_u32 s9, s39, 0
	global_load_dwordx4 v[144:147], v75, s[8:9]
	s_add_u32 s8, s8, 0x8000
	s_addc_u32 s9, s9, 0
	global_load_dwordx4 v[148:151], v75, s[8:9]
	s_add_u32 s8, s8, 0x8000
	s_addc_u32 s9, s9, 0
	global_load_dwordx4 v[152:155], v75, s[8:9]
	s_add_u32 s8, s8, 0x8000
	s_addc_u32 s9, s9, 0
	global_load_dwordx4 v[156:159], v75, s[8:9]
	s_add_u32 s8, s8, 0x8000
	s_addc_u32 s9, s9, 0
	global_load_dwordx4 v[160:163], v75, s[8:9]
	s_add_u32 s8, s8, 0x8000
	s_addc_u32 s9, s9, 0
	global_load_dwordx4 v[164:167], v75, s[8:9]
	s_add_u32 s8, s8, 0x8000
	s_addc_u32 s9, s9, 0
	global_load_dwordx4 v[168:171], v75, s[8:9]
	s_add_u32 s8, s8, 0x8000
	s_addc_u32 s9, s9, 0
	global_load_dwordx4 v[172:175], v75, s[8:9]
	s_add_u32 s6, s40, 0x2000000
	s_addc_u32 s7, s41, 0
	ds_read_b32 v226, v211
	ds_read_b32 v227, v211 offset:512
	ds_read_b32 v228, v211 offset:1024
	ds_read_b32 v229, v211 offset:1536
	ds_read_b32 v230, v211 offset:2048
	ds_read_b32 v231, v211 offset:2560
	ds_read_b32 v232, v211 offset:3072
	ds_read_b32 v233, v211 offset:3584
	ds_read_b32 v234, v211 offset:4096
	ds_read_b32 v235, v211 offset:4608
	ds_read_b32 v236, v211 offset:5120
	ds_read_b32 v237, v211 offset:5632
	ds_read_b32 v238, v211 offset:6144
	ds_read_b32 v239, v211 offset:6656
	ds_read_b32 v240, v211 offset:7168
	ds_read_b32 v241, v211 offset:7680
	s_waitcnt lgkmcnt(0)
	v_max_f32_e32 v226, v226, v226
	v_max_f32_e32 v227, v227, v227
	v_max_f32_e32 v228, v228, v228
	v_max_f32_e32 v229, v229, v229
	v_max_f32_e32 v230, v230, v230
	v_max_f32_e32 v231, v231, v231
	v_max_f32_e32 v232, v232, v232
	v_max_f32_e32 v233, v233, v233
	v_max_f32_e32 v234, v234, v234
	v_max_f32_e32 v235, v235, v235
	v_max_f32_e32 v236, v236, v236
	v_max_f32_e32 v237, v237, v237
	v_max_f32_e32 v238, v238, v238
	v_max_f32_e32 v239, v239, v239
	v_max_f32_e32 v240, v240, v240
	v_max_f32_e32 v241, v241, v241
	v_med3_f32 v226, v226, s62, v95
	v_med3_f32 v227, v227, s62, v95
	v_med3_f32 v228, v228, s62, v95
	v_med3_f32 v229, v229, s62, v95
	v_med3_f32 v230, v230, s62, v95
	v_med3_f32 v231, v231, s62, v95
	v_med3_f32 v232, v232, s62, v95
	v_med3_f32 v233, v233, s62, v95
	v_med3_f32 v234, v234, s62, v95
	v_med3_f32 v235, v235, s62, v95
	v_med3_f32 v236, v236, s62, v95
	v_med3_f32 v237, v237, s62, v95
	v_med3_f32 v238, v238, s62, v95
	v_med3_f32 v239, v239, s62, v95
	v_med3_f32 v240, v240, s62, v95
	v_med3_f32 v241, v241, s62, v95
	v_mov_b32_e32 v242, 0
	v_mov_b32_e32 v243, 0
	v_mov_b32_e32 v244, 0
	v_mov_b32_e32 v245, 0
	v_cvt_pk_fp8_f32 v242, v226, v227
	v_cvt_pk_fp8_f32 v243, v230, v231
	v_cvt_pk_fp8_f32 v244, v234, v235
	v_cvt_pk_fp8_f32 v245, v238, v239
	v_cvt_pk_fp8_f32 v242, v228, v229 op_sel:[0,0,1]
	v_cvt_pk_fp8_f32 v243, v232, v233 op_sel:[0,0,1]
	v_cvt_pk_fp8_f32 v244, v236, v237 op_sel:[0,0,1]
	v_cvt_pk_fp8_f32 v245, v240, v241 op_sel:[0,0,1]
	s_nop 0
	global_store_dwordx4 v79, v[242:245], s[6:7]
	ds_read_b32 v226, v213
	ds_read_b32 v227, v213 offset:512
	ds_read_b32 v228, v213 offset:1024
	ds_read_b32 v229, v213 offset:1536
	ds_read_b32 v230, v213 offset:2048
	ds_read_b32 v231, v213 offset:2560
	ds_read_b32 v232, v213 offset:3072
	ds_read_b32 v233, v213 offset:3584
	ds_read_b32 v234, v213 offset:4096
	ds_read_b32 v235, v213 offset:4608
	ds_read_b32 v236, v213 offset:5120
	ds_read_b32 v237, v213 offset:5632
	ds_read_b32 v238, v213 offset:6144
	ds_read_b32 v239, v213 offset:6656
	ds_read_b32 v240, v213 offset:7168
	ds_read_b32 v241, v213 offset:7680
	s_waitcnt lgkmcnt(0)
	v_max_f32_e32 v226, v226, v226
	v_max_f32_e32 v227, v227, v227
	v_max_f32_e32 v228, v228, v228
	v_max_f32_e32 v229, v229, v229
	v_max_f32_e32 v230, v230, v230
	v_max_f32_e32 v231, v231, v231
	v_max_f32_e32 v232, v232, v232
	v_max_f32_e32 v233, v233, v233
	v_max_f32_e32 v234, v234, v234
	v_max_f32_e32 v235, v235, v235
	v_max_f32_e32 v236, v236, v236
	v_max_f32_e32 v237, v237, v237
	v_max_f32_e32 v238, v238, v238
	v_max_f32_e32 v239, v239, v239
	v_max_f32_e32 v240, v240, v240
	v_max_f32_e32 v241, v241, v241
	v_med3_f32 v226, v226, s62, v95
	v_med3_f32 v227, v227, s62, v95
	v_med3_f32 v228, v228, s62, v95
	v_med3_f32 v229, v229, s62, v95
	v_med3_f32 v230, v230, s62, v95
	v_med3_f32 v231, v231, s62, v95
	v_med3_f32 v232, v232, s62, v95
	v_med3_f32 v233, v233, s62, v95
	v_med3_f32 v234, v234, s62, v95
	v_med3_f32 v235, v235, s62, v95
	v_med3_f32 v236, v236, s62, v95
	v_med3_f32 v237, v237, s62, v95
	v_med3_f32 v238, v238, s62, v95
	v_med3_f32 v239, v239, s62, v95
	v_med3_f32 v240, v240, s62, v95
	v_med3_f32 v241, v241, s62, v95
	v_mov_b32_e32 v242, 0
	v_mov_b32_e32 v243, 0
	v_mov_b32_e32 v244, 0
	v_mov_b32_e32 v245, 0
	v_cvt_pk_fp8_f32 v242, v226, v227
	v_cvt_pk_fp8_f32 v243, v230, v231
	v_cvt_pk_fp8_f32 v244, v234, v235
	v_cvt_pk_fp8_f32 v245, v238, v239
	v_cvt_pk_fp8_f32 v242, v228, v229 op_sel:[0,0,1]
	v_cvt_pk_fp8_f32 v243, v232, v233 op_sel:[0,0,1]
	v_cvt_pk_fp8_f32 v244, v236, v237 op_sel:[0,0,1]
	v_cvt_pk_fp8_f32 v245, v240, v241 op_sel:[0,0,1]
	s_nop 0
	global_store_dwordx4 v80, v[242:245], s[6:7]
	s_waitcnt vmcnt(12)
	v_mul_f32_e32 v176, 0x43000000, v176
	v_mul_f32_e32 v177, 0x43000000, v177
	v_mul_f32_e32 v178, 0x43000000, v178
	v_mul_f32_e32 v179, 0x43000000, v179
	ds_write_b128 v210, v[176:179]
	v_mul_f32_e32 v180, 0x43000000, v180
	v_mul_f32_e32 v181, 0x43000000, v181
	v_mul_f32_e32 v182, 0x43000000, v182
	v_mul_f32_e32 v183, 0x43000000, v183
	ds_write_b128 v210, v[180:183] offset:1024
	v_mul_f32_e32 v184, 0x43000000, v184
	v_mul_f32_e32 v185, 0x43000000, v185
	v_mul_f32_e32 v186, 0x43000000, v186
	v_mul_f32_e32 v187, 0x43000000, v187
	ds_write_b128 v210, v[184:187] offset:2048
	v_mul_f32_e32 v188, 0x43000000, v188
	v_mul_f32_e32 v189, 0x43000000, v189
	v_mul_f32_e32 v190, 0x43000000, v190
	v_mul_f32_e32 v191, 0x43000000, v191
	ds_write_b128 v210, v[188:191] offset:3072
	v_mul_f32_e32 v192, 0x43000000, v192
	v_mul_f32_e32 v193, 0x43000000, v193
	v_mul_f32_e32 v194, 0x43000000, v194
	v_mul_f32_e32 v195, 0x43000000, v195
	ds_write_b128 v210, v[192:195] offset:4096
	v_mul_f32_e32 v196, 0x43000000, v196
	v_mul_f32_e32 v197, 0x43000000, v197
	v_mul_f32_e32 v198, 0x43000000, v198
	v_mul_f32_e32 v199, 0x43000000, v199
	ds_write_b128 v210, v[196:199] offset:5120
	v_mul_f32_e32 v200, 0x43000000, v200
	v_mul_f32_e32 v201, 0x43000000, v201
	v_mul_f32_e32 v202, 0x43000000, v202
	v_mul_f32_e32 v203, 0x43000000, v203
	ds_write_b128 v210, v[200:203] offset:6144
	v_mul_f32_e32 v204, 0x43000000, v204
	v_mul_f32_e32 v205, 0x43000000, v205
	v_mul_f32_e32 v206, 0x43000000, v206
	v_mul_f32_e32 v207, 0x43000000, v207
	ds_write_b128 v210, v[204:207] offset:7168
	s_waitcnt lgkmcnt(0)
	s_barrier
; #define GAS __attribute__((address_space(1)))
;     const int pr = item >> 1, kb = 2 * (pr / nblk) + (item & 1), nb = pr % nblk, k0 = 64 * kb, n0 = 32 * nb;
;     const int nr = n0 + (lane & 31); const int sc = MAP == 1 ? src_col_in(nr) : nr;
;     float v[32];
; #pragma unroll
;     for (int i = 0; i < 32; ++i) v[i] = sc >= 0 ? W[(size_t)(k0 + 2 * i + (lane >> 5)) * Nsrc + sc] : 0.f;
; #pragma unroll
;     for (int i = 0; i < 32; ++i) { const int k = k0 + 2 * i + (lane >> 5); float x = v[i] * wscale; if (KS) x *= (k < ksplit ? ksA[k] : ksB[k - ksplit]); scr[(2 * i + (lane >> 5)) * 33 + (lane & 31)] = x; }
;     LDS_WAIT(); asm volatile("" ::: "memory");
;     const int c = lane & 7;
; #pragma unroll
;     for (int j = 0; j < 4; ++j) { const int n = (lane >> 3) + 8 * j; const LAS float* s = scr + (8 * c) * 33 + n;
;         const unsigned long long o = (unsigned long long)pg8::pk4_fp8(s[0 * 33], s[1 * 33], s[2 * 33], s[3 * 33]) | ((unsigned long long)pg8::pk4_fp8(s[4 * 33], s[5 * 33], s[6 * 33], s[7 * 33]) << 32);
;         *(GAS unsigned long long*)(WT + (size_t)(n0 + n) * K + k0 + 8 * c) = o; }
;     LDS_WAIT(); asm volatile("" ::: "memory");
; }
; __global__ void __launch_bounds__(NWAVES * 64, 2) hybrid_fwd(Args args) {
;     ...
;         for (int rep = 0; rep < REP_PRO; ++rep)
;         for (int it = gw; it < DEPTH * I_L; it += NGW) {
;             const int l = it / I_L; int r = it % I_L;
;             if (r < I_IN) { if (l >= PROJ_F8_FROM) p0_transpose_item_f8<true, 1>(args.in[2] + (size_t)l * DM * NSRC, DM, NSRC, NPROJ / 32, (unsigned char*)(ws + WS_WIN + l * SZ_WIN), WUP8_SCALE, args.in[1] + l * DM, args.in[1] + l * DM, DM, scr, r, lane);
;                 else p0_transpose_item<1, true>(args.in[2] + (size_t)l * DM * NSRC, DM, NSRC, NPROJ / 32, (bf16*)(ws + WS_WIN + l * SZ_WIN), args.in[1] + l * DM, args.in[1] + l * DM, DM, scr, r, lane); continue; } r -= I_IN;
;             if (r < I_O) { if (l >= WO_F8_FROM) p0_transpose_item_f8<true>(args.in[13] + (size_t)l * DM * DM, DM, DM, DM / 32, (unsigned char*)(ws + WS_WO + l * SZ_WO), 64.f, args.in[6] + l * 2048, args.in[12] + l * 2048, 2048, scr, r, lane);
;                 else p0_transpose_item<0, true>(args.in[13] + (size_t)l * DM * DM, DM, DM, DM / 32, (bf16*)(ws + WS_WO + l * SZ_WO), args.in[6] + l * 2048, args.in[12] + l * 2048, 2048, scr, r, lane); continue; } r -= I_O;
	s_add_u32 s8, s38, 0x4001000
	s_addc_u32 s9, s39, 0
	global_load_dwordx4 v[176:179], v75, s[8:9]
	s_add_u32 s8, s8, 0x8000
	s_addc_u32 s9, s9, 0
	global_load_dwordx4 v[180:183], v75, s[8:9]
	s_add_u32 s8, s8, 0x8000
	s_addc_u32 s9, s9, 0
	global_load_dwordx4 v[184:187], v75, s[8:9]
	s_add_u32 s8, s8, 0x8000
	s_addc_u32 s9, s9, 0
	global_load_dwordx4 v[188:191], v75, s[8:9]
	s_add_u32 s8, s8, 0x8000
	s_addc_u32 s9, s9, 0
	global_load_dwordx4 v[192:195], v75, s[8:9]
	s_add_u32 s8, s8, 0x8000
	s_addc_u32 s9, s9, 0
	global_load_dwordx4 v[196:199], v75, s[8:9]
	s_add_u32 s8, s8, 0x8000
	s_addc_u32 s9, s9, 0
	global_load_dwordx4 v[200:203], v75, s[8:9]
	s_add_u32 s8, s8, 0x8000
	s_addc_u32 s9, s9, 0
	global_load_dwordx4 v[204:207], v75, s[8:9]
	s_add_u32 s6, s40, 0x3000000
	s_addc_u32 s7, s41, 0
	ds_read_b32 v226, v212
	ds_read_b32 v227, v212 offset:512
	ds_read_b32 v228, v212 offset:1024
	ds_read_b32 v229, v212 offset:1536
	ds_read_b32 v230, v212 offset:2048
	ds_read_b32 v231, v212 offset:2560
	ds_read_b32 v232, v212 offset:3072
	ds_read_b32 v233, v212 offset:3584
	ds_read_b32 v234, v212 offset:4096
	ds_read_b32 v235, v212 offset:4608
	ds_read_b32 v236, v212 offset:5120
	ds_read_b32 v237, v212 offset:5632
	ds_read_b32 v238, v212 offset:6144
	ds_read_b32 v239, v212 offset:6656
	ds_read_b32 v240, v212 offset:7168
	ds_read_b32 v241, v212 offset:7680
	s_waitcnt lgkmcnt(0)
	v_max_f32_e32 v226, v226, v226
	v_max_f32_e32 v227, v227, v227
	v_max_f32_e32 v228, v228, v228
	v_max_f32_e32 v229, v229, v229
	v_max_f32_e32 v230, v230, v230
	v_max_f32_e32 v231, v231, v231
	v_max_f32_e32 v232, v232, v232
	v_max_f32_e32 v233, v233, v233
	v_max_f32_e32 v234, v234, v234
	v_max_f32_e32 v235, v235, v235
	v_max_f32_e32 v236, v236, v236
	v_max_f32_e32 v237, v237, v237
	v_max_f32_e32 v238, v238, v238
	v_max_f32_e32 v239, v239, v239
	v_max_f32_e32 v240, v240, v240
	v_max_f32_e32 v241, v241, v241
	v_med3_f32 v226, v226, s62, v95
	v_med3_f32 v227, v227, s62, v95
	v_med3_f32 v228, v228, s62, v95
	v_med3_f32 v229, v229, s62, v95
	v_med3_f32 v230, v230, s62, v95
	v_med3_f32 v231, v231, s62, v95
	v_med3_f32 v232, v232, s62, v95
	v_med3_f32 v233, v233, s62, v95
	v_med3_f32 v234, v234, s62, v95
	v_med3_f32 v235, v235, s62, v95
	v_med3_f32 v236, v236, s62, v95
	v_med3_f32 v237, v237, s62, v95
	v_med3_f32 v238, v238, s62, v95
	v_med3_f32 v239, v239, s62, v95
	v_med3_f32 v240, v240, s62, v95
	v_med3_f32 v241, v241, s62, v95
	v_mov_b32_e32 v242, 0
	v_mov_b32_e32 v243, 0
	v_mov_b32_e32 v244, 0
	v_mov_b32_e32 v245, 0
	v_cvt_pk_fp8_f32 v242, v226, v227
	v_cvt_pk_fp8_f32 v243, v230, v231
	v_cvt_pk_fp8_f32 v244, v234, v235
	v_cvt_pk_fp8_f32 v245, v238, v239
	v_cvt_pk_fp8_f32 v242, v228, v229 op_sel:[0,0,1]
	v_cvt_pk_fp8_f32 v243, v232, v233 op_sel:[0,0,1]
	v_cvt_pk_fp8_f32 v244, v236, v237 op_sel:[0,0,1]
	v_cvt_pk_fp8_f32 v245, v240, v241 op_sel:[0,0,1]
	s_nop 0
	global_store_dwordx4 v79, v[242:245], s[6:7]
	ds_read_b32 v226, v214
	ds_read_b32 v227, v214 offset:512
	ds_read_b32 v228, v214 offset:1024
	ds_read_b32 v229, v214 offset:1536
	ds_read_b32 v230, v214 offset:2048
	ds_read_b32 v231, v214 offset:2560
	ds_read_b32 v232, v214 offset:3072
	ds_read_b32 v233, v214 offset:3584
	ds_read_b32 v234, v214 offset:4096
	ds_read_b32 v235, v214 offset:4608
	ds_read_b32 v236, v214 offset:5120
	ds_read_b32 v237, v214 offset:5632
	ds_read_b32 v238, v214 offset:6144
	ds_read_b32 v239, v214 offset:6656
	ds_read_b32 v240, v214 offset:7168
	ds_read_b32 v241, v214 offset:7680
	s_waitcnt lgkmcnt(0)
	v_max_f32_e32 v226, v226, v226
	v_max_f32_e32 v227, v227, v227
	v_max_f32_e32 v228, v228, v228
	v_max_f32_e32 v229, v229, v229
	v_max_f32_e32 v230, v230, v230
	v_max_f32_e32 v231, v231, v231
	v_max_f32_e32 v232, v232, v232
	v_max_f32_e32 v233, v233, v233
	v_max_f32_e32 v234, v234, v234
	v_max_f32_e32 v235, v235, v235
	v_max_f32_e32 v236, v236, v236
	v_max_f32_e32 v237, v237, v237
	v_max_f32_e32 v238, v238, v238
	v_max_f32_e32 v239, v239, v239
	v_max_f32_e32 v240, v240, v240
	v_max_f32_e32 v241, v241, v241
	v_med3_f32 v226, v226, s62, v95
	v_med3_f32 v227, v227, s62, v95
	v_med3_f32 v228, v228, s62, v95
	v_med3_f32 v229, v229, s62, v95
	v_med3_f32 v230, v230, s62, v95
	v_med3_f32 v231, v231, s62, v95
	v_med3_f32 v232, v232, s62, v95
	v_med3_f32 v233, v233, s62, v95
	v_med3_f32 v234, v234, s62, v95
	v_med3_f32 v235, v235, s62, v95
	v_med3_f32 v236, v236, s62, v95
	v_med3_f32 v237, v237, s62, v95
	v_med3_f32 v238, v238, s62, v95
	v_med3_f32 v239, v239, s62, v95
	v_med3_f32 v240, v240, s62, v95
	v_med3_f32 v241, v241, s62, v95
	v_mov_b32_e32 v242, 0
	v_mov_b32_e32 v243, 0
	v_mov_b32_e32 v244, 0
	v_mov_b32_e32 v245, 0
	v_cvt_pk_fp8_f32 v242, v226, v227
	v_cvt_pk_fp8_f32 v243, v230, v231
	v_cvt_pk_fp8_f32 v244, v234, v235
	v_cvt_pk_fp8_f32 v245, v238, v239
	v_cvt_pk_fp8_f32 v242, v228, v229 op_sel:[0,0,1]
	v_cvt_pk_fp8_f32 v243, v232, v233 op_sel:[0,0,1]
	v_cvt_pk_fp8_f32 v244, v236, v237 op_sel:[0,0,1]
	v_cvt_pk_fp8_f32 v245, v240, v241 op_sel:[0,0,1]
	s_nop 0
	global_store_dwordx4 v80, v[242:245], s[6:7]
	s_waitcnt vmcnt(12)
	v_mul_f32_e32 v144, 0x43000000, v144
	v_mul_f32_e32 v145, 0x43000000, v145
	v_mul_f32_e32 v146, 0x43000000, v146
	v_mul_f32_e32 v147, 0x43000000, v147
	ds_write_b128 v209, v[144:147]
	v_mul_f32_e32 v148, 0x43000000, v148
	v_mul_f32_e32 v149, 0x43000000, v149
	v_mul_f32_e32 v150, 0x43000000, v150
	v_mul_f32_e32 v151, 0x43000000, v151
	ds_write_b128 v209, v[148:151] offset:1024
	v_mul_f32_e32 v152, 0x43000000, v152
	v_mul_f32_e32 v153, 0x43000000, v153
	v_mul_f32_e32 v154, 0x43000000, v154
	v_mul_f32_e32 v155, 0x43000000, v155
	ds_write_b128 v209, v[152:155] offset:2048
	v_mul_f32_e32 v156, 0x43000000, v156
	v_mul_f32_e32 v157, 0x43000000, v157
	v_mul_f32_e32 v158, 0x43000000, v158
	v_mul_f32_e32 v159, 0x43000000, v159
	ds_write_b128 v209, v[156:159] offset:3072
	v_mul_f32_e32 v160, 0x43000000, v160
	v_mul_f32_e32 v161, 0x43000000, v161
	v_mul_f32_e32 v162, 0x43000000, v162
	v_mul_f32_e32 v163, 0x43000000, v163
	ds_write_b128 v209, v[160:163] offset:4096
	v_mul_f32_e32 v164, 0x43000000, v164
	v_mul_f32_e32 v165, 0x43000000, v165
	v_mul_f32_e32 v166, 0x43000000, v166
	v_mul_f32_e32 v167, 0x43000000, v167
	ds_write_b128 v209, v[164:167] offset:5120
	v_mul_f32_e32 v168, 0x43000000, v168
	v_mul_f32_e32 v169, 0x43000000, v169
	v_mul_f32_e32 v170, 0x43000000, v170
	v_mul_f32_e32 v171, 0x43000000, v171
	ds_write_b128 v209, v[168:171] offset:6144
	v_mul_f32_e32 v172, 0x43000000, v172
	v_mul_f32_e32 v173, 0x43000000, v173
	v_mul_f32_e32 v174, 0x43000000, v174
	v_mul_f32_e32 v175, 0x43000000, v175
	ds_write_b128 v209, v[172:175] offset:7168
	s_waitcnt lgkmcnt(0)
	s_barrier
; #define GAS __attribute__((address_space(1)))
;     const int pr = item >> 1, kb = 2 * (pr / nblk) + (item & 1), nb = pr % nblk, k0 = 64 * kb, n0 = 32 * nb;
;     const int nr = n0 + (lane & 31); const int sc = MAP == 1 ? src_col_in(nr) : nr;
;     float v[32];
; #pragma unroll
;     for (int i = 0; i < 32; ++i) v[i] = sc >= 0 ? W[(size_t)(k0 + 2 * i + (lane >> 5)) * Nsrc + sc] : 0.f;
; #pragma unroll
;     for (int i = 0; i < 32; ++i) { const int k = k0 + 2 * i + (lane >> 5); float x = v[i] * wscale; if (KS) x *= (k < ksplit ? ksA[k] : ksB[k - ksplit]); scr[(2 * i + (lane >> 5)) * 33 + (lane & 31)] = x; }
;     LDS_WAIT(); asm volatile("" ::: "memory");
;     const int c = lane & 7;
; #pragma unroll
;     for (int j = 0; j < 4; ++j) { const int n = (lane >> 3) + 8 * j; const LAS float* s = scr + (8 * c) * 33 + n;
;         const unsigned long long o = (unsigned long long)pg8::pk4_fp8(s[0 * 33], s[1 * 33], s[2 * 33], s[3 * 33]) | ((unsigned long long)pg8::pk4_fp8(s[4 * 33], s[5 * 33], s[6 * 33], s[7 * 33]) << 32);
;         *(GAS unsigned long long*)(WT + (size_t)(n0 + n) * K + k0 + 8 * c) = o; }
;     LDS_WAIT(); asm volatile("" ::: "memory");
; }
; __global__ void __launch_bounds__(NWAVES * 64, 2) hybrid_fwd(Args args) {
;     ...
;         for (int rep = 0; rep < REP_PRO; ++rep)
;         for (int it = gw; it < DEPTH * I_L; it += NGW) {
;             const int l = it / I_L; int r = it % I_L;
;             if (r < I_IN) { if (l >= PROJ_F8_FROM) p0_transpose_item_f8<true, 1>(args.in[2] + (size_t)l * DM * NSRC, DM, NSRC, NPROJ / 32, (unsigned char*)(ws + WS_WIN + l * SZ_WIN), WUP8_SCALE, args.in[1] + l * DM, args.in[1] + l * DM, DM, scr, r, lane);
;                 else p0_transpose_item<1, true>(args.in[2] + (size_t)l * DM * NSRC, DM, NSRC, NPROJ / 32, (bf16*)(ws + WS_WIN + l * SZ_WIN), args.in[1] + l * DM, args.in[1] + l * DM, DM, scr, r, lane); continue; } r -= I_IN;
;             if (r < I_O) { if (l >= WO_F8_FROM) p0_transpose_item_f8<true>(args.in[13] + (size_t)l * DM * DM, DM, DM, DM / 32, (unsigned char*)(ws + WS_WO + l * SZ_WO), 64.f, args.in[6] + l * 2048, args.in[12] + l * 2048, 2048, scr, r, lane);
;                 else p0_transpose_item<0, true>(args.in[13] + (size_t)l * DM * DM, DM, DM, DM / 32, (bf16*)(ws + WS_WO + l * SZ_WO), args.in[6] + l * 2048, args.in[12] + l * 2048, 2048, scr, r, lane); continue; } r -= I_O;
	s_add_u32 s8, s38, 0x4002000
	s_addc_u32 s9, s39, 0
	global_load_dwordx4 v[144:147], v75, s[8:9]
	s_add_u32 s8, s8, 0x8000
	s_addc_u32 s9, s9, 0
	global_load_dwordx4 v[148:151], v75, s[8:9]
	s_add_u32 s8, s8, 0x8000
	s_addc_u32 s9, s9, 0
	global_load_dwordx4 v[152:155], v75, s[8:9]
	s_add_u32 s8, s8, 0x8000
	s_addc_u32 s9, s9, 0
	global_load_dwordx4 v[156:159], v75, s[8:9]
	s_add_u32 s8, s8, 0x8000
	s_addc_u32 s9, s9, 0
	global_load_dwordx4 v[160:163], v75, s[8:9]
	s_add_u32 s8, s8, 0x8000
	s_addc_u32 s9, s9, 0
	global_load_dwordx4 v[164:167], v75, s[8:9]
	s_add_u32 s8, s8, 0x8000
	s_addc_u32 s9, s9, 0
	global_load_dwordx4 v[168:171], v75, s[8:9]
	s_add_u32 s8, s8, 0x8000
	s_addc_u32 s9, s9, 0
	global_load_dwordx4 v[172:175], v75, s[8:9]
	s_add_u32 s6, s40, 0x1000
	s_addc_u32 s7, s41, 0
	ds_read_b32 v226, v211
	ds_read_b32 v227, v211 offset:512
	ds_read_b32 v228, v211 offset:1024
	ds_read_b32 v229, v211 offset:1536
	ds_read_b32 v230, v211 offset:2048
	ds_read_b32 v231, v211 offset:2560
	ds_read_b32 v232, v211 offset:3072
	ds_read_b32 v233, v211 offset:3584
	ds_read_b32 v234, v211 offset:4096
	ds_read_b32 v235, v211 offset:4608
	ds_read_b32 v236, v211 offset:5120
	ds_read_b32 v237, v211 offset:5632
	ds_read_b32 v238, v211 offset:6144
	ds_read_b32 v239, v211 offset:6656
	ds_read_b32 v240, v211 offset:7168
	ds_read_b32 v241, v211 offset:7680
	s_waitcnt lgkmcnt(0)
	v_max_f32_e32 v226, v226, v226
	v_max_f32_e32 v227, v227, v227
	v_max_f32_e32 v228, v228, v228
	v_max_f32_e32 v229, v229, v229
	v_max_f32_e32 v230, v230, v230
	v_max_f32_e32 v231, v231, v231
	v_max_f32_e32 v232, v232, v232
	v_max_f32_e32 v233, v233, v233
	v_max_f32_e32 v234, v234, v234
	v_max_f32_e32 v235, v235, v235
	v_max_f32_e32 v236, v236, v236
	v_max_f32_e32 v237, v237, v237
	v_max_f32_e32 v238, v238, v238
	v_max_f32_e32 v239, v239, v239
	v_max_f32_e32 v240, v240, v240
	v_max_f32_e32 v241, v241, v241
	v_med3_f32 v226, v226, s62, v95
	v_med3_f32 v227, v227, s62, v95
	v_med3_f32 v228, v228, s62, v95
	v_med3_f32 v229, v229, s62, v95
	v_med3_f32 v230, v230, s62, v95
	v_med3_f32 v231, v231, s62, v95
	v_med3_f32 v232, v232, s62, v95
	v_med3_f32 v233, v233, s62, v95
	v_med3_f32 v234, v234, s62, v95
	v_med3_f32 v235, v235, s62, v95
	v_med3_f32 v236, v236, s62, v95
	v_med3_f32 v237, v237, s62, v95
	v_med3_f32 v238, v238, s62, v95
	v_med3_f32 v239, v239, s62, v95
	v_med3_f32 v240, v240, s62, v95
	v_med3_f32 v241, v241, s62, v95
	v_mov_b32_e32 v242, 0
	v_mov_b32_e32 v243, 0
	v_mov_b32_e32 v244, 0
	v_mov_b32_e32 v245, 0
	v_cvt_pk_fp8_f32 v242, v226, v227
	v_cvt_pk_fp8_f32 v243, v230, v231
	v_cvt_pk_fp8_f32 v244, v234, v235
	v_cvt_pk_fp8_f32 v245, v238, v239
	v_cvt_pk_fp8_f32 v242, v228, v229 op_sel:[0,0,1]
	v_cvt_pk_fp8_f32 v243, v232, v233 op_sel:[0,0,1]
	v_cvt_pk_fp8_f32 v244, v236, v237 op_sel:[0,0,1]
	v_cvt_pk_fp8_f32 v245, v240, v241 op_sel:[0,0,1]
	s_nop 0
	global_store_dwordx4 v79, v[242:245], s[6:7]
	ds_read_b32 v226, v213
	ds_read_b32 v227, v213 offset:512
	ds_read_b32 v228, v213 offset:1024
	ds_read_b32 v229, v213 offset:1536
	ds_read_b32 v230, v213 offset:2048
	ds_read_b32 v231, v213 offset:2560
	ds_read_b32 v232, v213 offset:3072
	ds_read_b32 v233, v213 offset:3584
	ds_read_b32 v234, v213 offset:4096
	ds_read_b32 v235, v213 offset:4608
	ds_read_b32 v236, v213 offset:5120
	ds_read_b32 v237, v213 offset:5632
	ds_read_b32 v238, v213 offset:6144
	ds_read_b32 v239, v213 offset:6656
	ds_read_b32 v240, v213 offset:7168
	ds_read_b32 v241, v213 offset:7680
	s_waitcnt lgkmcnt(0)
	v_max_f32_e32 v226, v226, v226
	v_max_f32_e32 v227, v227, v227
	v_max_f32_e32 v228, v228, v228
	v_max_f32_e32 v229, v229, v229
	v_max_f32_e32 v230, v230, v230
	v_max_f32_e32 v231, v231, v231
	v_max_f32_e32 v232, v232, v232
	v_max_f32_e32 v233, v233, v233
	v_max_f32_e32 v234, v234, v234
	v_max_f32_e32 v235, v235, v235
	v_max_f32_e32 v236, v236, v236
	v_max_f32_e32 v237, v237, v237
	v_max_f32_e32 v238, v238, v238
	v_max_f32_e32 v239, v239, v239
	v_max_f32_e32 v240, v240, v240
	v_max_f32_e32 v241, v241, v241
	v_med3_f32 v226, v226, s62, v95
	v_med3_f32 v227, v227, s62, v95
	v_med3_f32 v228, v228, s62, v95
	v_med3_f32 v229, v229, s62, v95
	v_med3_f32 v230, v230, s62, v95
	v_med3_f32 v231, v231, s62, v95
	v_med3_f32 v232, v232, s62, v95
	v_med3_f32 v233, v233, s62, v95
	v_med3_f32 v234, v234, s62, v95
	v_med3_f32 v235, v235, s62, v95
	v_med3_f32 v236, v236, s62, v95
	v_med3_f32 v237, v237, s62, v95
	v_med3_f32 v238, v238, s62, v95
	v_med3_f32 v239, v239, s62, v95
	v_med3_f32 v240, v240, s62, v95
	v_med3_f32 v241, v241, s62, v95
	v_mov_b32_e32 v242, 0
	v_mov_b32_e32 v243, 0
	v_mov_b32_e32 v244, 0
	v_mov_b32_e32 v245, 0
	v_cvt_pk_fp8_f32 v242, v226, v227
	v_cvt_pk_fp8_f32 v243, v230, v231
	v_cvt_pk_fp8_f32 v244, v234, v235
	v_cvt_pk_fp8_f32 v245, v238, v239
	v_cvt_pk_fp8_f32 v242, v228, v229 op_sel:[0,0,1]
	v_cvt_pk_fp8_f32 v243, v232, v233 op_sel:[0,0,1]
	v_cvt_pk_fp8_f32 v244, v236, v237 op_sel:[0,0,1]
	v_cvt_pk_fp8_f32 v245, v240, v241 op_sel:[0,0,1]
	s_nop 0
	global_store_dwordx4 v80, v[242:245], s[6:7]
	s_waitcnt vmcnt(12)
	v_mul_f32_e32 v176, 0x43000000, v176
	v_mul_f32_e32 v177, 0x43000000, v177
	v_mul_f32_e32 v178, 0x43000000, v178
	v_mul_f32_e32 v179, 0x43000000, v179
	ds_write_b128 v210, v[176:179]
	v_mul_f32_e32 v180, 0x43000000, v180
	v_mul_f32_e32 v181, 0x43000000, v181
	v_mul_f32_e32 v182, 0x43000000, v182
	v_mul_f32_e32 v183, 0x43000000, v183
	ds_write_b128 v210, v[180:183] offset:1024
	v_mul_f32_e32 v184, 0x43000000, v184
	v_mul_f32_e32 v185, 0x43000000, v185
	v_mul_f32_e32 v186, 0x43000000, v186
	v_mul_f32_e32 v187, 0x43000000, v187
	ds_write_b128 v210, v[184:187] offset:2048
	v_mul_f32_e32 v188, 0x43000000, v188
	v_mul_f32_e32 v189, 0x43000000, v189
	v_mul_f32_e32 v190, 0x43000000, v190
	v_mul_f32_e32 v191, 0x43000000, v191
	ds_write_b128 v210, v[188:191] offset:3072
	v_mul_f32_e32 v192, 0x43000000, v192
	v_mul_f32_e32 v193, 0x43000000, v193
	v_mul_f32_e32 v194, 0x43000000, v194
	v_mul_f32_e32 v195, 0x43000000, v195
	ds_write_b128 v210, v[192:195] offset:4096
	v_mul_f32_e32 v196, 0x43000000, v196
	v_mul_f32_e32 v197, 0x43000000, v197
	v_mul_f32_e32 v198, 0x43000000, v198
	v_mul_f32_e32 v199, 0x43000000, v199
	ds_write_b128 v210, v[196:199] offset:5120
	v_mul_f32_e32 v200, 0x43000000, v200
	v_mul_f32_e32 v201, 0x43000000, v201
	v_mul_f32_e32 v202, 0x43000000, v202
	v_mul_f32_e32 v203, 0x43000000, v203
	ds_write_b128 v210, v[200:203] offset:6144
	v_mul_f32_e32 v204, 0x43000000, v204
	v_mul_f32_e32 v205, 0x43000000, v205
	v_mul_f32_e32 v206, 0x43000000, v206
	v_mul_f32_e32 v207, 0x43000000, v207
	ds_write_b128 v210, v[204:207] offset:7168
	s_waitcnt lgkmcnt(0)
	s_barrier
; #define GAS __attribute__((address_space(1)))
;     const int pr = item >> 1, kb = 2 * (pr / nblk) + (item & 1), nb = pr % nblk, k0 = 64 * kb, n0 = 32 * nb;
;     const int nr = n0 + (lane & 31); const int sc = MAP == 1 ? src_col_in(nr) : nr;
;     float v[32];
; #pragma unroll
;     for (int i = 0; i < 32; ++i) v[i] = sc >= 0 ? W[(size_t)(k0 + 2 * i + (lane >> 5)) * Nsrc + sc] : 0.f;
; #pragma unroll
;     for (int i = 0; i < 32; ++i) { const int k = k0 + 2 * i + (lane >> 5); float x = v[i] * wscale; if (KS) x *= (k < ksplit ? ksA[k] : ksB[k - ksplit]); scr[(2 * i + (lane >> 5)) * 33 + (lane & 31)] = x; }
;     LDS_WAIT(); asm volatile("" ::: "memory");
;     const int c = lane & 7;
; #pragma unroll
;     for (int j = 0; j < 4; ++j) { const int n = (lane >> 3) + 8 * j; const LAS float* s = scr + (8 * c) * 33 + n;
;         const unsigned long long o = (unsigned long long)pg8::pk4_fp8(s[0 * 33], s[1 * 33], s[2 * 33], s[3 * 33]) | ((unsigned long long)pg8::pk4_fp8(s[4 * 33], s[5 * 33], s[6 * 33], s[7 * 33]) << 32);
;         *(GAS unsigned long long*)(WT + (size_t)(n0 + n) * K + k0 + 8 * c) = o; }
;     LDS_WAIT(); asm volatile("" ::: "memory");
; }
; __global__ void __launch_bounds__(NWAVES * 64, 2) hybrid_fwd(Args args) {
;     ...
;         for (int rep = 0; rep < REP_PRO; ++rep)
;         for (int it = gw; it < DEPTH * I_L; it += NGW) {
;             const int l = it / I_L; int r = it % I_L;
;             if (r < I_IN) { if (l >= PROJ_F8_FROM) p0_transpose_item_f8<true, 1>(args.in[2] + (size_t)l * DM * NSRC, DM, NSRC, NPROJ / 32, (unsigned char*)(ws + WS_WIN + l * SZ_WIN), WUP8_SCALE, args.in[1] + l * DM, args.in[1] + l * DM, DM, scr, r, lane);
;                 else p0_transpose_item<1, true>(args.in[2] + (size_t)l * DM * NSRC, DM, NSRC, NPROJ / 32, (bf16*)(ws + WS_WIN + l * SZ_WIN), args.in[1] + l * DM, args.in[1] + l * DM, DM, scr, r, lane); continue; } r -= I_IN;
;             if (r < I_O) { if (l >= WO_F8_FROM) p0_transpose_item_f8<true>(args.in[13] + (size_t)l * DM * DM, DM, DM, DM / 32, (unsigned char*)(ws + WS_WO + l * SZ_WO), 64.f, args.in[6] + l * 2048, args.in[12] + l * 2048, 2048, scr, r, lane);
;                 else p0_transpose_item<0, true>(args.in[13] + (size_t)l * DM * DM, DM, DM, DM / 32, (bf16*)(ws + WS_WO + l * SZ_WO), args.in[6] + l * 2048, args.in[12] + l * 2048, 2048, scr, r, lane); continue; } r -= I_O;
	s_add_u32 s8, s38, 0x4003000
	s_addc_u32 s9, s39, 0
	global_load_dwordx4 v[176:179], v75, s[8:9]
	s_add_u32 s8, s8, 0x8000
	s_addc_u32 s9, s9, 0
	global_load_dwordx4 v[180:183], v75, s[8:9]
	s_add_u32 s8, s8, 0x8000
	s_addc_u32 s9, s9, 0
	global_load_dwordx4 v[184:187], v75, s[8:9]
	s_add_u32 s8, s8, 0x8000
	s_addc_u32 s9, s9, 0
	global_load_dwordx4 v[188:191], v75, s[8:9]
	s_add_u32 s8, s8, 0x8000
	s_addc_u32 s9, s9, 0
	global_load_dwordx4 v[192:195], v75, s[8:9]
	s_add_u32 s8, s8, 0x8000
	s_addc_u32 s9, s9, 0
	global_load_dwordx4 v[196:199], v75, s[8:9]
	s_add_u32 s8, s8, 0x8000
	s_addc_u32 s9, s9, 0
	global_load_dwordx4 v[200:203], v75, s[8:9]
	s_add_u32 s8, s8, 0x8000
	s_addc_u32 s9, s9, 0
	global_load_dwordx4 v[204:207], v75, s[8:9]
	s_add_u32 s6, s40, 0x1001000
	s_addc_u32 s7, s41, 0
	ds_read_b32 v226, v212
	ds_read_b32 v227, v212 offset:512
	ds_read_b32 v228, v212 offset:1024
	ds_read_b32 v229, v212 offset:1536
	ds_read_b32 v230, v212 offset:2048
	ds_read_b32 v231, v212 offset:2560
	ds_read_b32 v232, v212 offset:3072
	ds_read_b32 v233, v212 offset:3584
	ds_read_b32 v234, v212 offset:4096
	ds_read_b32 v235, v212 offset:4608
	ds_read_b32 v236, v212 offset:5120
	ds_read_b32 v237, v212 offset:5632
	ds_read_b32 v238, v212 offset:6144
	ds_read_b32 v239, v212 offset:6656
	ds_read_b32 v240, v212 offset:7168
	ds_read_b32 v241, v212 offset:7680
	s_waitcnt lgkmcnt(0)
	v_max_f32_e32 v226, v226, v226
	v_max_f32_e32 v227, v227, v227
	v_max_f32_e32 v228, v228, v228
	v_max_f32_e32 v229, v229, v229
	v_max_f32_e32 v230, v230, v230
	v_max_f32_e32 v231, v231, v231
	v_max_f32_e32 v232, v232, v232
	v_max_f32_e32 v233, v233, v233
	v_max_f32_e32 v234, v234, v234
	v_max_f32_e32 v235, v235, v235
	v_max_f32_e32 v236, v236, v236
	v_max_f32_e32 v237, v237, v237
	v_max_f32_e32 v238, v238, v238
	v_max_f32_e32 v239, v239, v239
	v_max_f32_e32 v240, v240, v240
	v_max_f32_e32 v241, v241, v241
	v_med3_f32 v226, v226, s62, v95
	v_med3_f32 v227, v227, s62, v95
	v_med3_f32 v228, v228, s62, v95
	v_med3_f32 v229, v229, s62, v95
	v_med3_f32 v230, v230, s62, v95
	v_med3_f32 v231, v231, s62, v95
	v_med3_f32 v232, v232, s62, v95
	v_med3_f32 v233, v233, s62, v95
	v_med3_f32 v234, v234, s62, v95
	v_med3_f32 v235, v235, s62, v95
	v_med3_f32 v236, v236, s62, v95
	v_med3_f32 v237, v237, s62, v95
	v_med3_f32 v238, v238, s62, v95
	v_med3_f32 v239, v239, s62, v95
	v_med3_f32 v240, v240, s62, v95
	v_med3_f32 v241, v241, s62, v95
	v_mov_b32_e32 v242, 0
	v_mov_b32_e32 v243, 0
	v_mov_b32_e32 v244, 0
	v_mov_b32_e32 v245, 0
	v_cvt_pk_fp8_f32 v242, v226, v227
	v_cvt_pk_fp8_f32 v243, v230, v231
	v_cvt_pk_fp8_f32 v244, v234, v235
	v_cvt_pk_fp8_f32 v245, v238, v239
	v_cvt_pk_fp8_f32 v242, v228, v229 op_sel:[0,0,1]
	v_cvt_pk_fp8_f32 v243, v232, v233 op_sel:[0,0,1]
	v_cvt_pk_fp8_f32 v244, v236, v237 op_sel:[0,0,1]
	v_cvt_pk_fp8_f32 v245, v240, v241 op_sel:[0,0,1]
	s_nop 0
	global_store_dwordx4 v79, v[242:245], s[6:7]
	ds_read_b32 v226, v214
	ds_read_b32 v227, v214 offset:512
	ds_read_b32 v228, v214 offset:1024
	ds_read_b32 v229, v214 offset:1536
	ds_read_b32 v230, v214 offset:2048
	ds_read_b32 v231, v214 offset:2560
	ds_read_b32 v232, v214 offset:3072
	ds_read_b32 v233, v214 offset:3584
	ds_read_b32 v234, v214 offset:4096
	ds_read_b32 v235, v214 offset:4608
	ds_read_b32 v236, v214 offset:5120
	ds_read_b32 v237, v214 offset:5632
	ds_read_b32 v238, v214 offset:6144
	ds_read_b32 v239, v214 offset:6656
	ds_read_b32 v240, v214 offset:7168
	ds_read_b32 v241, v214 offset:7680
	s_waitcnt lgkmcnt(0)
	v_max_f32_e32 v226, v226, v226
	v_max_f32_e32 v227, v227, v227
	v_max_f32_e32 v228, v228, v228
	v_max_f32_e32 v229, v229, v229
	v_max_f32_e32 v230, v230, v230
	v_max_f32_e32 v231, v231, v231
	v_max_f32_e32 v232, v232, v232
	v_max_f32_e32 v233, v233, v233
	v_max_f32_e32 v234, v234, v234
	v_max_f32_e32 v235, v235, v235
	v_max_f32_e32 v236, v236, v236
	v_max_f32_e32 v237, v237, v237
	v_max_f32_e32 v238, v238, v238
	v_max_f32_e32 v239, v239, v239
	v_max_f32_e32 v240, v240, v240
	v_max_f32_e32 v241, v241, v241
	v_med3_f32 v226, v226, s62, v95
	v_med3_f32 v227, v227, s62, v95
	v_med3_f32 v228, v228, s62, v95
	v_med3_f32 v229, v229, s62, v95
	v_med3_f32 v230, v230, s62, v95
	v_med3_f32 v231, v231, s62, v95
	v_med3_f32 v232, v232, s62, v95
	v_med3_f32 v233, v233, s62, v95
	v_med3_f32 v234, v234, s62, v95
	v_med3_f32 v235, v235, s62, v95
	v_med3_f32 v236, v236, s62, v95
	v_med3_f32 v237, v237, s62, v95
	v_med3_f32 v238, v238, s62, v95
	v_med3_f32 v239, v239, s62, v95
	v_med3_f32 v240, v240, s62, v95
	v_med3_f32 v241, v241, s62, v95
	v_mov_b32_e32 v242, 0
	v_mov_b32_e32 v243, 0
	v_mov_b32_e32 v244, 0
	v_mov_b32_e32 v245, 0
	v_cvt_pk_fp8_f32 v242, v226, v227
	v_cvt_pk_fp8_f32 v243, v230, v231
	v_cvt_pk_fp8_f32 v244, v234, v235
	v_cvt_pk_fp8_f32 v245, v238, v239
	v_cvt_pk_fp8_f32 v242, v228, v229 op_sel:[0,0,1]
	v_cvt_pk_fp8_f32 v243, v232, v233 op_sel:[0,0,1]
	v_cvt_pk_fp8_f32 v244, v236, v237 op_sel:[0,0,1]
	v_cvt_pk_fp8_f32 v245, v240, v241 op_sel:[0,0,1]
	s_nop 0
	global_store_dwordx4 v80, v[242:245], s[6:7]
	s_waitcnt vmcnt(12)
	v_mul_f32_e32 v144, 0x43000000, v144
	v_mul_f32_e32 v145, 0x43000000, v145
	v_mul_f32_e32 v146, 0x43000000, v146
	v_mul_f32_e32 v147, 0x43000000, v147
	ds_write_b128 v209, v[144:147]
	v_mul_f32_e32 v148, 0x43000000, v148
	v_mul_f32_e32 v149, 0x43000000, v149
	v_mul_f32_e32 v150, 0x43000000, v150
	v_mul_f32_e32 v151, 0x43000000, v151
	ds_write_b128 v209, v[148:151] offset:1024
	v_mul_f32_e32 v152, 0x43000000, v152
	v_mul_f32_e32 v153, 0x43000000, v153
	v_mul_f32_e32 v154, 0x43000000, v154
	v_mul_f32_e32 v155, 0x43000000, v155
	ds_write_b128 v209, v[152:155] offset:2048
	v_mul_f32_e32 v156, 0x43000000, v156
	v_mul_f32_e32 v157, 0x43000000, v157
	v_mul_f32_e32 v158, 0x43000000, v158
	v_mul_f32_e32 v159, 0x43000000, v159
	ds_write_b128 v209, v[156:159] offset:3072
	v_mul_f32_e32 v160, 0x43000000, v160
	v_mul_f32_e32 v161, 0x43000000, v161
	v_mul_f32_e32 v162, 0x43000000, v162
	v_mul_f32_e32 v163, 0x43000000, v163
	ds_write_b128 v209, v[160:163] offset:4096
	v_mul_f32_e32 v164, 0x43000000, v164
	v_mul_f32_e32 v165, 0x43000000, v165
	v_mul_f32_e32 v166, 0x43000000, v166
	v_mul_f32_e32 v167, 0x43000000, v167
	ds_write_b128 v209, v[164:167] offset:5120
	v_mul_f32_e32 v168, 0x43000000, v168
	v_mul_f32_e32 v169, 0x43000000, v169
	v_mul_f32_e32 v170, 0x43000000, v170
	v_mul_f32_e32 v171, 0x43000000, v171
	ds_write_b128 v209, v[168:171] offset:6144
	v_mul_f32_e32 v172, 0x43000000, v172
	v_mul_f32_e32 v173, 0x43000000, v173
	v_mul_f32_e32 v174, 0x43000000, v174
	v_mul_f32_e32 v175, 0x43000000, v175
	ds_write_b128 v209, v[172:175] offset:7168
	s_waitcnt lgkmcnt(0)
	s_barrier
; #define GAS __attribute__((address_space(1)))
;     const int pr = item >> 1, kb = 2 * (pr / nblk) + (item & 1), nb = pr % nblk, k0 = 64 * kb, n0 = 32 * nb;
;     const int nr = n0 + (lane & 31); const int sc = MAP == 1 ? src_col_in(nr) : nr;
;     float v[32];
; #pragma unroll
;     for (int i = 0; i < 32; ++i) v[i] = sc >= 0 ? W[(size_t)(k0 + 2 * i + (lane >> 5)) * Nsrc + sc] : 0.f;
; #pragma unroll
;     for (int i = 0; i < 32; ++i) { const int k = k0 + 2 * i + (lane >> 5); float x = v[i] * wscale; if (KS) x *= (k < ksplit ? ksA[k] : ksB[k - ksplit]); scr[(2 * i + (lane >> 5)) * 33 + (lane & 31)] = x; }
;     LDS_WAIT(); asm volatile("" ::: "memory");
;     const int c = lane & 7;
; #pragma unroll
;     for (int j = 0; j < 4; ++j) { const int n = (lane >> 3) + 8 * j; const LAS float* s = scr + (8 * c) * 33 + n;
;         const unsigned long long o = (unsigned long long)pg8::pk4_fp8(s[0 * 33], s[1 * 33], s[2 * 33], s[3 * 33]) | ((unsigned long long)pg8::pk4_fp8(s[4 * 33], s[5 * 33], s[6 * 33], s[7 * 33]) << 32);
;         *(GAS unsigned long long*)(WT + (size_t)(n0 + n) * K + k0 + 8 * c) = o; }
;     LDS_WAIT(); asm volatile("" ::: "memory");
; }
; __global__ void __launch_bounds__(NWAVES * 64, 2) hybrid_fwd(Args args) {
;     ...
;         for (int rep = 0; rep < REP_PRO; ++rep)
;         for (int it = gw; it < DEPTH * I_L; it += NGW) {
;             const int l = it / I_L; int r = it % I_L;
;             if (r < I_IN) { if (l >= PROJ_F8_FROM) p0_transpose_item_f8<true, 1>(args.in[2] + (size_t)l * DM * NSRC, DM, NSRC, NPROJ / 32, (unsigned char*)(ws + WS_WIN + l * SZ_WIN), WUP8_SCALE, args.in[1] + l * DM, args.in[1] + l * DM, DM, scr, r, lane);
;                 else p0_transpose_item<1, true>(args.in[2] + (size_t)l * DM * NSRC, DM, NSRC, NPROJ / 32, (bf16*)(ws + WS_WIN + l * SZ_WIN), args.in[1] + l * DM, args.in[1] + l * DM, DM, scr, r, lane); continue; } r -= I_IN;
;             if (r < I_O) { if (l >= WO_F8_FROM) p0_transpose_item_f8<true>(args.in[13] + (size_t)l * DM * DM, DM, DM, DM / 32, (unsigned char*)(ws + WS_WO + l * SZ_WO), 64.f, args.in[6] + l * 2048, args.in[12] + l * 2048, 2048, scr, r, lane);
;                 else p0_transpose_item<0, true>(args.in[13] + (size_t)l * DM * DM, DM, DM, DM / 32, (bf16*)(ws + WS_WO + l * SZ_WO), args.in[6] + l * 2048, args.in[12] + l * 2048, 2048, scr, r, lane); continue; } r -= I_O;
	s_add_u32 s8, s38, 0x8000000
	s_addc_u32 s9, s39, 0
	global_load_dwordx4 v[144:147], v75, s[8:9]
	s_add_u32 s8, s8, 0x8000
	s_addc_u32 s9, s9, 0
	global_load_dwordx4 v[148:151], v75, s[8:9]
	s_add_u32 s8, s8, 0x8000
	s_addc_u32 s9, s9, 0
	global_load_dwordx4 v[152:155], v75, s[8:9]
	s_add_u32 s8, s8, 0x8000
	s_addc_u32 s9, s9, 0
	global_load_dwordx4 v[156:159], v75, s[8:9]
	s_add_u32 s8, s8, 0x8000
	s_addc_u32 s9, s9, 0
	global_load_dwordx4 v[160:163], v75, s[8:9]
	s_add_u32 s8, s8, 0x8000
	s_addc_u32 s9, s9, 0
	global_load_dwordx4 v[164:167], v75, s[8:9]
	s_add_u32 s8, s8, 0x8000
	s_addc_u32 s9, s9, 0
	global_load_dwordx4 v[168:171], v75, s[8:9]
	s_add_u32 s8, s8, 0x8000
	s_addc_u32 s9, s9, 0
	global_load_dwordx4 v[172:175], v75, s[8:9]
	s_add_u32 s6, s40, 0x2001000
	s_addc_u32 s7, s41, 0
	ds_read_b32 v226, v211
	ds_read_b32 v227, v211 offset:512
	ds_read_b32 v228, v211 offset:1024
	ds_read_b32 v229, v211 offset:1536
	ds_read_b32 v230, v211 offset:2048
	ds_read_b32 v231, v211 offset:2560
	ds_read_b32 v232, v211 offset:3072
	ds_read_b32 v233, v211 offset:3584
	ds_read_b32 v234, v211 offset:4096
	ds_read_b32 v235, v211 offset:4608
	ds_read_b32 v236, v211 offset:5120
	ds_read_b32 v237, v211 offset:5632
	ds_read_b32 v238, v211 offset:6144
	ds_read_b32 v239, v211 offset:6656
	ds_read_b32 v240, v211 offset:7168
	ds_read_b32 v241, v211 offset:7680
	s_waitcnt lgkmcnt(0)
	v_max_f32_e32 v226, v226, v226
	v_max_f32_e32 v227, v227, v227
	v_max_f32_e32 v228, v228, v228
	v_max_f32_e32 v229, v229, v229
	v_max_f32_e32 v230, v230, v230
	v_max_f32_e32 v231, v231, v231
	v_max_f32_e32 v232, v232, v232
	v_max_f32_e32 v233, v233, v233
	v_max_f32_e32 v234, v234, v234
	v_max_f32_e32 v235, v235, v235
	v_max_f32_e32 v236, v236, v236
	v_max_f32_e32 v237, v237, v237
	v_max_f32_e32 v238, v238, v238
	v_max_f32_e32 v239, v239, v239
	v_max_f32_e32 v240, v240, v240
	v_max_f32_e32 v241, v241, v241
	v_med3_f32 v226, v226, s62, v95
	v_med3_f32 v227, v227, s62, v95
	v_med3_f32 v228, v228, s62, v95
	v_med3_f32 v229, v229, s62, v95
	v_med3_f32 v230, v230, s62, v95
	v_med3_f32 v231, v231, s62, v95
	v_med3_f32 v232, v232, s62, v95
	v_med3_f32 v233, v233, s62, v95
	v_med3_f32 v234, v234, s62, v95
	v_med3_f32 v235, v235, s62, v95
	v_med3_f32 v236, v236, s62, v95
	v_med3_f32 v237, v237, s62, v95
	v_med3_f32 v238, v238, s62, v95
	v_med3_f32 v239, v239, s62, v95
	v_med3_f32 v240, v240, s62, v95
	v_med3_f32 v241, v241, s62, v95
	v_mov_b32_e32 v242, 0
	v_mov_b32_e32 v243, 0
	v_mov_b32_e32 v244, 0
	v_mov_b32_e32 v245, 0
	v_cvt_pk_fp8_f32 v242, v226, v227
	v_cvt_pk_fp8_f32 v243, v230, v231
	v_cvt_pk_fp8_f32 v244, v234, v235
	v_cvt_pk_fp8_f32 v245, v238, v239
	v_cvt_pk_fp8_f32 v242, v228, v229 op_sel:[0,0,1]
	v_cvt_pk_fp8_f32 v243, v232, v233 op_sel:[0,0,1]
	v_cvt_pk_fp8_f32 v244, v236, v237 op_sel:[0,0,1]
	v_cvt_pk_fp8_f32 v245, v240, v241 op_sel:[0,0,1]
	s_nop 0
	global_store_dwordx4 v79, v[242:245], s[6:7]
	ds_read_b32 v226, v213
	ds_read_b32 v227, v213 offset:512
	ds_read_b32 v228, v213 offset:1024
	ds_read_b32 v229, v213 offset:1536
	ds_read_b32 v230, v213 offset:2048
	ds_read_b32 v231, v213 offset:2560
	ds_read_b32 v232, v213 offset:3072
	ds_read_b32 v233, v213 offset:3584
	ds_read_b32 v234, v213 offset:4096
	ds_read_b32 v235, v213 offset:4608
	ds_read_b32 v236, v213 offset:5120
	ds_read_b32 v237, v213 offset:5632
	ds_read_b32 v238, v213 offset:6144
	ds_read_b32 v239, v213 offset:6656
	ds_read_b32 v240, v213 offset:7168
	ds_read_b32 v241, v213 offset:7680
	s_waitcnt lgkmcnt(0)
	v_max_f32_e32 v226, v226, v226
	v_max_f32_e32 v227, v227, v227
	v_max_f32_e32 v228, v228, v228
	v_max_f32_e32 v229, v229, v229
	v_max_f32_e32 v230, v230, v230
	v_max_f32_e32 v231, v231, v231
	v_max_f32_e32 v232, v232, v232
	v_max_f32_e32 v233, v233, v233
	v_max_f32_e32 v234, v234, v234
	v_max_f32_e32 v235, v235, v235
	v_max_f32_e32 v236, v236, v236
	v_max_f32_e32 v237, v237, v237
	v_max_f32_e32 v238, v238, v238
	v_max_f32_e32 v239, v239, v239
	v_max_f32_e32 v240, v240, v240
	v_max_f32_e32 v241, v241, v241
	v_med3_f32 v226, v226, s62, v95
	v_med3_f32 v227, v227, s62, v95
	v_med3_f32 v228, v228, s62, v95
	v_med3_f32 v229, v229, s62, v95
	v_med3_f32 v230, v230, s62, v95
	v_med3_f32 v231, v231, s62, v95
	v_med3_f32 v232, v232, s62, v95
	v_med3_f32 v233, v233, s62, v95
	v_med3_f32 v234, v234, s62, v95
	v_med3_f32 v235, v235, s62, v95
	v_med3_f32 v236, v236, s62, v95
	v_med3_f32 v237, v237, s62, v95
	v_med3_f32 v238, v238, s62, v95
	v_med3_f32 v239, v239, s62, v95
	v_med3_f32 v240, v240, s62, v95
	v_med3_f32 v241, v241, s62, v95
	v_mov_b32_e32 v242, 0
	v_mov_b32_e32 v243, 0
	v_mov_b32_e32 v244, 0
	v_mov_b32_e32 v245, 0
	v_cvt_pk_fp8_f32 v242, v226, v227
	v_cvt_pk_fp8_f32 v243, v230, v231
	v_cvt_pk_fp8_f32 v244, v234, v235
	v_cvt_pk_fp8_f32 v245, v238, v239
	v_cvt_pk_fp8_f32 v242, v228, v229 op_sel:[0,0,1]
	v_cvt_pk_fp8_f32 v243, v232, v233 op_sel:[0,0,1]
	v_cvt_pk_fp8_f32 v244, v236, v237 op_sel:[0,0,1]
	v_cvt_pk_fp8_f32 v245, v240, v241 op_sel:[0,0,1]
	s_nop 0
	global_store_dwordx4 v80, v[242:245], s[6:7]
	s_waitcnt vmcnt(12)
	v_mul_f32_e32 v176, 0x43000000, v176
	v_mul_f32_e32 v177, 0x43000000, v177
	v_mul_f32_e32 v178, 0x43000000, v178
	v_mul_f32_e32 v179, 0x43000000, v179
	ds_write_b128 v210, v[176:179]
	v_mul_f32_e32 v180, 0x43000000, v180
	v_mul_f32_e32 v181, 0x43000000, v181
	v_mul_f32_e32 v182, 0x43000000, v182
	v_mul_f32_e32 v183, 0x43000000, v183
	ds_write_b128 v210, v[180:183] offset:1024
	v_mul_f32_e32 v184, 0x43000000, v184
	v_mul_f32_e32 v185, 0x43000000, v185
	v_mul_f32_e32 v186, 0x43000000, v186
	v_mul_f32_e32 v187, 0x43000000, v187
	ds_write_b128 v210, v[184:187] offset:2048
	v_mul_f32_e32 v188, 0x43000000, v188
	v_mul_f32_e32 v189, 0x43000000, v189
	v_mul_f32_e32 v190, 0x43000000, v190
	v_mul_f32_e32 v191, 0x43000000, v191
	ds_write_b128 v210, v[188:191] offset:3072
	v_mul_f32_e32 v192, 0x43000000, v192
	v_mul_f32_e32 v193, 0x43000000, v193
	v_mul_f32_e32 v194, 0x43000000, v194
	v_mul_f32_e32 v195, 0x43000000, v195
	ds_write_b128 v210, v[192:195] offset:4096
	v_mul_f32_e32 v196, 0x43000000, v196
	v_mul_f32_e32 v197, 0x43000000, v197
	v_mul_f32_e32 v198, 0x43000000, v198
	v_mul_f32_e32 v199, 0x43000000, v199
	ds_write_b128 v210, v[196:199] offset:5120
	v_mul_f32_e32 v200, 0x43000000, v200
	v_mul_f32_e32 v201, 0x43000000, v201
	v_mul_f32_e32 v202, 0x43000000, v202
	v_mul_f32_e32 v203, 0x43000000, v203
	ds_write_b128 v210, v[200:203] offset:6144
	v_mul_f32_e32 v204, 0x43000000, v204
	v_mul_f32_e32 v205, 0x43000000, v205
	v_mul_f32_e32 v206, 0x43000000, v206
	v_mul_f32_e32 v207, 0x43000000, v207
	ds_write_b128 v210, v[204:207] offset:7168
	s_waitcnt lgkmcnt(0)
	s_barrier
; #define GAS __attribute__((address_space(1)))
;     const int pr = item >> 1, kb = 2 * (pr / nblk) + (item & 1), nb = pr % nblk, k0 = 64 * kb, n0 = 32 * nb;
;     const int nr = n0 + (lane & 31); const int sc = MAP == 1 ? src_col_in(nr) : nr;
;     float v[32];
; #pragma unroll
;     for (int i = 0; i < 32; ++i) v[i] = sc >= 0 ? W[(size_t)(k0 + 2 * i + (lane >> 5)) * Nsrc + sc] : 0.f;
; #pragma unroll
;     for (int i = 0; i < 32; ++i) { const int k = k0 + 2 * i + (lane >> 5); float x = v[i] * wscale; if (KS) x *= (k < ksplit ? ksA[k] : ksB[k - ksplit]); scr[(2 * i + (lane >> 5)) * 33 + (lane & 31)] = x; }
;     LDS_WAIT(); asm volatile("" ::: "memory");
;     const int c = lane & 7;
; #pragma unroll
;     for (int j = 0; j < 4; ++j) { const int n = (lane >> 3) + 8 * j; const LAS float* s = scr + (8 * c) * 33 + n;
;         const unsigned long long o = (unsigned long long)pg8::pk4_fp8(s[0 * 33], s[1 * 33], s[2 * 33], s[3 * 33]) | ((unsigned long long)pg8::pk4_fp8(s[4 * 33], s[5 * 33], s[6 * 33], s[7 * 33]) << 32);
;         *(GAS unsigned long long*)(WT + (size_t)(n0 + n) * K + k0 + 8 * c) = o; }
;     LDS_WAIT(); asm volatile("" ::: "memory");
; }
; __global__ void __launch_bounds__(NWAVES * 64, 2) hybrid_fwd(Args args) {
;     ...
;         for (int rep = 0; rep < REP_PRO; ++rep)
;         for (int it = gw; it < DEPTH * I_L; it += NGW) {
;             const int l = it / I_L; int r = it % I_L;
;             if (r < I_IN) { if (l >= PROJ_F8_FROM) p0_transpose_item_f8<true, 1>(args.in[2] + (size_t)l * DM * NSRC, DM, NSRC, NPROJ / 32, (unsigned char*)(ws + WS_WIN + l * SZ_WIN), WUP8_SCALE, args.in[1] + l * DM, args.in[1] + l * DM, DM, scr, r, lane);
;                 else p0_transpose_item<1, true>(args.in[2] + (size_t)l * DM * NSRC, DM, NSRC, NPROJ / 32, (bf16*)(ws + WS_WIN + l * SZ_WIN), args.in[1] + l * DM, args.in[1] + l * DM, DM, scr, r, lane); continue; } r -= I_IN;
;             if (r < I_O) { if (l >= WO_F8_FROM) p0_transpose_item_f8<true>(args.in[13] + (size_t)l * DM * DM, DM, DM, DM / 32, (unsigned char*)(ws + WS_WO + l * SZ_WO), 64.f, args.in[6] + l * 2048, args.in[12] + l * 2048, 2048, scr, r, lane);
;                 else p0_transpose_item<0, true>(args.in[13] + (size_t)l * DM * DM, DM, DM, DM / 32, (bf16*)(ws + WS_WO + l * SZ_WO), args.in[6] + l * 2048, args.in[12] + l * 2048, 2048, scr, r, lane); continue; } r -= I_O;
	s_add_u32 s8, s38, 0x8001000
	s_addc_u32 s9, s39, 0
	global_load_dwordx4 v[176:179], v75, s[8:9]
	s_add_u32 s8, s8, 0x8000
	s_addc_u32 s9, s9, 0
	global_load_dwordx4 v[180:183], v75, s[8:9]
	s_add_u32 s8, s8, 0x8000
	s_addc_u32 s9, s9, 0
	global_load_dwordx4 v[184:187], v75, s[8:9]
	s_add_u32 s8, s8, 0x8000
	s_addc_u32 s9, s9, 0
	global_load_dwordx4 v[188:191], v75, s[8:9]
	s_add_u32 s8, s8, 0x8000
	s_addc_u32 s9, s9, 0
	global_load_dwordx4 v[192:195], v75, s[8:9]
	s_add_u32 s8, s8, 0x8000
	s_addc_u32 s9, s9, 0
	global_load_dwordx4 v[196:199], v75, s[8:9]
	s_add_u32 s8, s8, 0x8000
	s_addc_u32 s9, s9, 0
	global_load_dwordx4 v[200:203], v75, s[8:9]
	s_add_u32 s8, s8, 0x8000
	s_addc_u32 s9, s9, 0
	global_load_dwordx4 v[204:207], v75, s[8:9]
	s_add_u32 s6, s40, 0x3001000
	s_addc_u32 s7, s41, 0
	ds_read_b32 v226, v212
	ds_read_b32 v227, v212 offset:512
	ds_read_b32 v228, v212 offset:1024
	ds_read_b32 v229, v212 offset:1536
	ds_read_b32 v230, v212 offset:2048
	ds_read_b32 v231, v212 offset:2560
	ds_read_b32 v232, v212 offset:3072
	ds_read_b32 v233, v212 offset:3584
	ds_read_b32 v234, v212 offset:4096
	ds_read_b32 v235, v212 offset:4608
	ds_read_b32 v236, v212 offset:5120
	ds_read_b32 v237, v212 offset:5632
	ds_read_b32 v238, v212 offset:6144
	ds_read_b32 v239, v212 offset:6656
	ds_read_b32 v240, v212 offset:7168
	ds_read_b32 v241, v212 offset:7680
	s_waitcnt lgkmcnt(0)
	v_max_f32_e32 v226, v226, v226
	v_max_f32_e32 v227, v227, v227
	v_max_f32_e32 v228, v228, v228
	v_max_f32_e32 v229, v229, v229
	v_max_f32_e32 v230, v230, v230
	v_max_f32_e32 v231, v231, v231
	v_max_f32_e32 v232, v232, v232
	v_max_f32_e32 v233, v233, v233
	v_max_f32_e32 v234, v234, v234
	v_max_f32_e32 v235, v235, v235
	v_max_f32_e32 v236, v236, v236
	v_max_f32_e32 v237, v237, v237
	v_max_f32_e32 v238, v238, v238
	v_max_f32_e32 v239, v239, v239
	v_max_f32_e32 v240, v240, v240
	v_max_f32_e32 v241, v241, v241
	v_med3_f32 v226, v226, s62, v95
	v_med3_f32 v227, v227, s62, v95
	v_med3_f32 v228, v228, s62, v95
	v_med3_f32 v229, v229, s62, v95
	v_med3_f32 v230, v230, s62, v95
	v_med3_f32 v231, v231, s62, v95
	v_med3_f32 v232, v232, s62, v95
	v_med3_f32 v233, v233, s62, v95
	v_med3_f32 v234, v234, s62, v95
	v_med3_f32 v235, v235, s62, v95
	v_med3_f32 v236, v236, s62, v95
	v_med3_f32 v237, v237, s62, v95
	v_med3_f32 v238, v238, s62, v95
	v_med3_f32 v239, v239, s62, v95
	v_med3_f32 v240, v240, s62, v95
	v_med3_f32 v241, v241, s62, v95
	v_mov_b32_e32 v242, 0
	v_mov_b32_e32 v243, 0
	v_mov_b32_e32 v244, 0
	v_mov_b32_e32 v245, 0
	v_cvt_pk_fp8_f32 v242, v226, v227
	v_cvt_pk_fp8_f32 v243, v230, v231
	v_cvt_pk_fp8_f32 v244, v234, v235
	v_cvt_pk_fp8_f32 v245, v238, v239
	v_cvt_pk_fp8_f32 v242, v228, v229 op_sel:[0,0,1]
	v_cvt_pk_fp8_f32 v243, v232, v233 op_sel:[0,0,1]
	v_cvt_pk_fp8_f32 v244, v236, v237 op_sel:[0,0,1]
	v_cvt_pk_fp8_f32 v245, v240, v241 op_sel:[0,0,1]
	s_nop 0
	global_store_dwordx4 v79, v[242:245], s[6:7]
	ds_read_b32 v226, v214
	ds_read_b32 v227, v214 offset:512
	ds_read_b32 v228, v214 offset:1024
	ds_read_b32 v229, v214 offset:1536
	ds_read_b32 v230, v214 offset:2048
	ds_read_b32 v231, v214 offset:2560
	ds_read_b32 v232, v214 offset:3072
	ds_read_b32 v233, v214 offset:3584
	ds_read_b32 v234, v214 offset:4096
	ds_read_b32 v235, v214 offset:4608
	ds_read_b32 v236, v214 offset:5120
	ds_read_b32 v237, v214 offset:5632
	ds_read_b32 v238, v214 offset:6144
	ds_read_b32 v239, v214 offset:6656
	ds_read_b32 v240, v214 offset:7168
	ds_read_b32 v241, v214 offset:7680
	s_waitcnt lgkmcnt(0)
	v_max_f32_e32 v226, v226, v226
	v_max_f32_e32 v227, v227, v227
	v_max_f32_e32 v228, v228, v228
	v_max_f32_e32 v229, v229, v229
	v_max_f32_e32 v230, v230, v230
	v_max_f32_e32 v231, v231, v231
	v_max_f32_e32 v232, v232, v232
	v_max_f32_e32 v233, v233, v233
	v_max_f32_e32 v234, v234, v234
	v_max_f32_e32 v235, v235, v235
	v_max_f32_e32 v236, v236, v236
	v_max_f32_e32 v237, v237, v237
	v_max_f32_e32 v238, v238, v238
	v_max_f32_e32 v239, v239, v239
	v_max_f32_e32 v240, v240, v240
	v_max_f32_e32 v241, v241, v241
	v_med3_f32 v226, v226, s62, v95
	v_med3_f32 v227, v227, s62, v95
	v_med3_f32 v228, v228, s62, v95
	v_med3_f32 v229, v229, s62, v95
	v_med3_f32 v230, v230, s62, v95
	v_med3_f32 v231, v231, s62, v95
	v_med3_f32 v232, v232, s62, v95
	v_med3_f32 v233, v233, s62, v95
	v_med3_f32 v234, v234, s62, v95
	v_med3_f32 v235, v235, s62, v95
	v_med3_f32 v236, v236, s62, v95
	v_med3_f32 v237, v237, s62, v95
	v_med3_f32 v238, v238, s62, v95
	v_med3_f32 v239, v239, s62, v95
	v_med3_f32 v240, v240, s62, v95
	v_med3_f32 v241, v241, s62, v95
	v_mov_b32_e32 v242, 0
	v_mov_b32_e32 v243, 0
	v_mov_b32_e32 v244, 0
	v_mov_b32_e32 v245, 0
	v_cvt_pk_fp8_f32 v242, v226, v227
	v_cvt_pk_fp8_f32 v243, v230, v231
	v_cvt_pk_fp8_f32 v244, v234, v235
	v_cvt_pk_fp8_f32 v245, v238, v239
	v_cvt_pk_fp8_f32 v242, v228, v229 op_sel:[0,0,1]
	v_cvt_pk_fp8_f32 v243, v232, v233 op_sel:[0,0,1]
	v_cvt_pk_fp8_f32 v244, v236, v237 op_sel:[0,0,1]
	v_cvt_pk_fp8_f32 v245, v240, v241 op_sel:[0,0,1]
	s_nop 0
	global_store_dwordx4 v80, v[242:245], s[6:7]
	s_waitcnt vmcnt(12)
	v_mul_f32_e32 v144, 0x43000000, v144
	v_mul_f32_e32 v145, 0x43000000, v145
	v_mul_f32_e32 v146, 0x43000000, v146
	v_mul_f32_e32 v147, 0x43000000, v147
	ds_write_b128 v209, v[144:147]
	v_mul_f32_e32 v148, 0x43000000, v148
	v_mul_f32_e32 v149, 0x43000000, v149
	v_mul_f32_e32 v150, 0x43000000, v150
	v_mul_f32_e32 v151, 0x43000000, v151
	ds_write_b128 v209, v[148:151] offset:1024
	v_mul_f32_e32 v152, 0x43000000, v152
	v_mul_f32_e32 v153, 0x43000000, v153
	v_mul_f32_e32 v154, 0x43000000, v154
	v_mul_f32_e32 v155, 0x43000000, v155
	ds_write_b128 v209, v[152:155] offset:2048
	v_mul_f32_e32 v156, 0x43000000, v156
	v_mul_f32_e32 v157, 0x43000000, v157
	v_mul_f32_e32 v158, 0x43000000, v158
	v_mul_f32_e32 v159, 0x43000000, v159
	ds_write_b128 v209, v[156:159] offset:3072
	v_mul_f32_e32 v160, 0x43000000, v160
	v_mul_f32_e32 v161, 0x43000000, v161
	v_mul_f32_e32 v162, 0x43000000, v162
	v_mul_f32_e32 v163, 0x43000000, v163
	ds_write_b128 v209, v[160:163] offset:4096
	v_mul_f32_e32 v164, 0x43000000, v164
	v_mul_f32_e32 v165, 0x43000000, v165
	v_mul_f32_e32 v166, 0x43000000, v166
	v_mul_f32_e32 v167, 0x43000000, v167
	ds_write_b128 v209, v[164:167] offset:5120
	v_mul_f32_e32 v168, 0x43000000, v168
	v_mul_f32_e32 v169, 0x43000000, v169
	v_mul_f32_e32 v170, 0x43000000, v170
	v_mul_f32_e32 v171, 0x43000000, v171
	ds_write_b128 v209, v[168:171] offset:6144
	v_mul_f32_e32 v172, 0x43000000, v172
	v_mul_f32_e32 v173, 0x43000000, v173
	v_mul_f32_e32 v174, 0x43000000, v174
	v_mul_f32_e32 v175, 0x43000000, v175
	ds_write_b128 v209, v[172:175] offset:7168
	s_waitcnt lgkmcnt(0)
	s_barrier
; #define GAS __attribute__((address_space(1)))
;     const int pr = item >> 1, kb = 2 * (pr / nblk) + (item & 1), nb = pr % nblk, k0 = 64 * kb, n0 = 32 * nb;
;     const int nr = n0 + (lane & 31); const int sc = MAP == 1 ? src_col_in(nr) : nr;
;     float v[32];
; #pragma unroll
;     for (int i = 0; i < 32; ++i) v[i] = sc >= 0 ? W[(size_t)(k0 + 2 * i + (lane >> 5)) * Nsrc + sc] : 0.f;
; #pragma unroll
;     for (int i = 0; i < 32; ++i) { const int k = k0 + 2 * i + (lane >> 5); float x = v[i] * wscale; if (KS) x *= (k < ksplit ? ksA[k] : ksB[k - ksplit]); scr[(2 * i + (lane >> 5)) * 33 + (lane & 31)] = x; }
;     LDS_WAIT(); asm volatile("" ::: "memory");
;     const int c = lane & 7;
; #pragma unroll
;     for (int j = 0; j < 4; ++j) { const int n = (lane >> 3) + 8 * j; const LAS float* s = scr + (8 * c) * 33 + n;
;         const unsigned long long o = (unsigned long long)pg8::pk4_fp8(s[0 * 33], s[1 * 33], s[2 * 33], s[3 * 33]) | ((unsigned long long)pg8::pk4_fp8(s[4 * 33], s[5 * 33], s[6 * 33], s[7 * 33]) << 32);
;         *(GAS unsigned long long*)(WT + (size_t)(n0 + n) * K + k0 + 8 * c) = o; }
;     LDS_WAIT(); asm volatile("" ::: "memory");
; }
; __global__ void __launch_bounds__(NWAVES * 64, 2) hybrid_fwd(Args args) {
;     ...
;         for (int rep = 0; rep < REP_PRO; ++rep)
;         for (int it = gw; it < DEPTH * I_L; it += NGW) {
;             const int l = it / I_L; int r = it % I_L;
;             if (r < I_IN) { if (l >= PROJ_F8_FROM) p0_transpose_item_f8<true, 1>(args.in[2] + (size_t)l * DM * NSRC, DM, NSRC, NPROJ / 32, (unsigned char*)(ws + WS_WIN + l * SZ_WIN), WUP8_SCALE, args.in[1] + l * DM, args.in[1] + l * DM, DM, scr, r, lane);
;                 else p0_transpose_item<1, true>(args.in[2] + (size_t)l * DM * NSRC, DM, NSRC, NPROJ / 32, (bf16*)(ws + WS_WIN + l * SZ_WIN), args.in[1] + l * DM, args.in[1] + l * DM, DM, scr, r, lane); continue; } r -= I_IN;
;             if (r < I_O) { if (l >= WO_F8_FROM) p0_transpose_item_f8<true>(args.in[13] + (size_t)l * DM * DM, DM, DM, DM / 32, (unsigned char*)(ws + WS_WO + l * SZ_WO), 64.f, args.in[6] + l * 2048, args.in[12] + l * 2048, 2048, scr, r, lane);
;                 else p0_transpose_item<0, true>(args.in[13] + (size_t)l * DM * DM, DM, DM, DM / 32, (bf16*)(ws + WS_WO + l * SZ_WO), args.in[6] + l * 2048, args.in[12] + l * 2048, 2048, scr, r, lane); continue; } r -= I_O;
	s_add_u32 s8, s38, 0x8002000
	s_addc_u32 s9, s39, 0
	global_load_dwordx4 v[144:147], v75, s[8:9]
	s_add_u32 s8, s8, 0x8000
	s_addc_u32 s9, s9, 0
	global_load_dwordx4 v[148:151], v75, s[8:9]
	s_add_u32 s8, s8, 0x8000
	s_addc_u32 s9, s9, 0
	global_load_dwordx4 v[152:155], v75, s[8:9]
	s_add_u32 s8, s8, 0x8000
	s_addc_u32 s9, s9, 0
	global_load_dwordx4 v[156:159], v75, s[8:9]
	s_add_u32 s8, s8, 0x8000
	s_addc_u32 s9, s9, 0
	global_load_dwordx4 v[160:163], v75, s[8:9]
	s_add_u32 s8, s8, 0x8000
	s_addc_u32 s9, s9, 0
	global_load_dwordx4 v[164:167], v75, s[8:9]
	s_add_u32 s8, s8, 0x8000
	s_addc_u32 s9, s9, 0
	global_load_dwordx4 v[168:171], v75, s[8:9]
	s_add_u32 s8, s8, 0x8000
	s_addc_u32 s9, s9, 0
	global_load_dwordx4 v[172:175], v75, s[8:9]
	s_add_u32 s6, s40, 0x2000
	s_addc_u32 s7, s41, 0
	ds_read_b32 v226, v211
	ds_read_b32 v227, v211 offset:512
	ds_read_b32 v228, v211 offset:1024
	ds_read_b32 v229, v211 offset:1536
	ds_read_b32 v230, v211 offset:2048
	ds_read_b32 v231, v211 offset:2560
	ds_read_b32 v232, v211 offset:3072
	ds_read_b32 v233, v211 offset:3584
	ds_read_b32 v234, v211 offset:4096
	ds_read_b32 v235, v211 offset:4608
	ds_read_b32 v236, v211 offset:5120
	ds_read_b32 v237, v211 offset:5632
	ds_read_b32 v238, v211 offset:6144
	ds_read_b32 v239, v211 offset:6656
	ds_read_b32 v240, v211 offset:7168
	ds_read_b32 v241, v211 offset:7680
	s_waitcnt lgkmcnt(0)
	v_max_f32_e32 v226, v226, v226
	v_max_f32_e32 v227, v227, v227
	v_max_f32_e32 v228, v228, v228
	v_max_f32_e32 v229, v229, v229
	v_max_f32_e32 v230, v230, v230
	v_max_f32_e32 v231, v231, v231
	v_max_f32_e32 v232, v232, v232
	v_max_f32_e32 v233, v233, v233
	v_max_f32_e32 v234, v234, v234
	v_max_f32_e32 v235, v235, v235
	v_max_f32_e32 v236, v236, v236
	v_max_f32_e32 v237, v237, v237
	v_max_f32_e32 v238, v238, v238
	v_max_f32_e32 v239, v239, v239
	v_max_f32_e32 v240, v240, v240
	v_max_f32_e32 v241, v241, v241
	v_med3_f32 v226, v226, s62, v95
	v_med3_f32 v227, v227, s62, v95
	v_med3_f32 v228, v228, s62, v95
	v_med3_f32 v229, v229, s62, v95
	v_med3_f32 v230, v230, s62, v95
	v_med3_f32 v231, v231, s62, v95
	v_med3_f32 v232, v232, s62, v95
	v_med3_f32 v233, v233, s62, v95
	v_med3_f32 v234, v234, s62, v95
	v_med3_f32 v235, v235, s62, v95
	v_med3_f32 v236, v236, s62, v95
	v_med3_f32 v237, v237, s62, v95
	v_med3_f32 v238, v238, s62, v95
	v_med3_f32 v239, v239, s62, v95
	v_med3_f32 v240, v240, s62, v95
	v_med3_f32 v241, v241, s62, v95
	v_mov_b32_e32 v242, 0
	v_mov_b32_e32 v243, 0
	v_mov_b32_e32 v244, 0
	v_mov_b32_e32 v245, 0
	v_cvt_pk_fp8_f32 v242, v226, v227
	v_cvt_pk_fp8_f32 v243, v230, v231
	v_cvt_pk_fp8_f32 v244, v234, v235
	v_cvt_pk_fp8_f32 v245, v238, v239
	v_cvt_pk_fp8_f32 v242, v228, v229 op_sel:[0,0,1]
	v_cvt_pk_fp8_f32 v243, v232, v233 op_sel:[0,0,1]
	v_cvt_pk_fp8_f32 v244, v236, v237 op_sel:[0,0,1]
	v_cvt_pk_fp8_f32 v245, v240, v241 op_sel:[0,0,1]
	s_nop 0
	global_store_dwordx4 v79, v[242:245], s[6:7]
	ds_read_b32 v226, v213
	ds_read_b32 v227, v213 offset:512
	ds_read_b32 v228, v213 offset:1024
	ds_read_b32 v229, v213 offset:1536
	ds_read_b32 v230, v213 offset:2048
	ds_read_b32 v231, v213 offset:2560
	ds_read_b32 v232, v213 offset:3072
	ds_read_b32 v233, v213 offset:3584
	ds_read_b32 v234, v213 offset:4096
	ds_read_b32 v235, v213 offset:4608
	ds_read_b32 v236, v213 offset:5120
	ds_read_b32 v237, v213 offset:5632
	ds_read_b32 v238, v213 offset:6144
	ds_read_b32 v239, v213 offset:6656
	ds_read_b32 v240, v213 offset:7168
	ds_read_b32 v241, v213 offset:7680
	s_waitcnt lgkmcnt(0)
	v_max_f32_e32 v226, v226, v226
	v_max_f32_e32 v227, v227, v227
	v_max_f32_e32 v228, v228, v228
	v_max_f32_e32 v229, v229, v229
	v_max_f32_e32 v230, v230, v230
	v_max_f32_e32 v231, v231, v231
	v_max_f32_e32 v232, v232, v232
	v_max_f32_e32 v233, v233, v233
	v_max_f32_e32 v234, v234, v234
	v_max_f32_e32 v235, v235, v235
	v_max_f32_e32 v236, v236, v236
	v_max_f32_e32 v237, v237, v237
	v_max_f32_e32 v238, v238, v238
	v_max_f32_e32 v239, v239, v239
	v_max_f32_e32 v240, v240, v240
	v_max_f32_e32 v241, v241, v241
	v_med3_f32 v226, v226, s62, v95
	v_med3_f32 v227, v227, s62, v95
	v_med3_f32 v228, v228, s62, v95
	v_med3_f32 v229, v229, s62, v95
	v_med3_f32 v230, v230, s62, v95
	v_med3_f32 v231, v231, s62, v95
	v_med3_f32 v232, v232, s62, v95
	v_med3_f32 v233, v233, s62, v95
	v_med3_f32 v234, v234, s62, v95
	v_med3_f32 v235, v235, s62, v95
	v_med3_f32 v236, v236, s62, v95
	v_med3_f32 v237, v237, s62, v95
	v_med3_f32 v238, v238, s62, v95
	v_med3_f32 v239, v239, s62, v95
	v_med3_f32 v240, v240, s62, v95
	v_med3_f32 v241, v241, s62, v95
	v_mov_b32_e32 v242, 0
	v_mov_b32_e32 v243, 0
	v_mov_b32_e32 v244, 0
	v_mov_b32_e32 v245, 0
	v_cvt_pk_fp8_f32 v242, v226, v227
	v_cvt_pk_fp8_f32 v243, v230, v231
	v_cvt_pk_fp8_f32 v244, v234, v235
	v_cvt_pk_fp8_f32 v245, v238, v239
	v_cvt_pk_fp8_f32 v242, v228, v229 op_sel:[0,0,1]
	v_cvt_pk_fp8_f32 v243, v232, v233 op_sel:[0,0,1]
	v_cvt_pk_fp8_f32 v244, v236, v237 op_sel:[0,0,1]
	v_cvt_pk_fp8_f32 v245, v240, v241 op_sel:[0,0,1]
	s_nop 0
	global_store_dwordx4 v80, v[242:245], s[6:7]
	s_waitcnt vmcnt(12)
	v_mul_f32_e32 v176, 0x43000000, v176
	v_mul_f32_e32 v177, 0x43000000, v177
	v_mul_f32_e32 v178, 0x43000000, v178
	v_mul_f32_e32 v179, 0x43000000, v179
	ds_write_b128 v210, v[176:179]
	v_mul_f32_e32 v180, 0x43000000, v180
	v_mul_f32_e32 v181, 0x43000000, v181
	v_mul_f32_e32 v182, 0x43000000, v182
	v_mul_f32_e32 v183, 0x43000000, v183
	ds_write_b128 v210, v[180:183] offset:1024
	v_mul_f32_e32 v184, 0x43000000, v184
	v_mul_f32_e32 v185, 0x43000000, v185
	v_mul_f32_e32 v186, 0x43000000, v186
	v_mul_f32_e32 v187, 0x43000000, v187
	ds_write_b128 v210, v[184:187] offset:2048
	v_mul_f32_e32 v188, 0x43000000, v188
	v_mul_f32_e32 v189, 0x43000000, v189
	v_mul_f32_e32 v190, 0x43000000, v190
	v_mul_f32_e32 v191, 0x43000000, v191
	ds_write_b128 v210, v[188:191] offset:3072
	v_mul_f32_e32 v192, 0x43000000, v192
	v_mul_f32_e32 v193, 0x43000000, v193
	v_mul_f32_e32 v194, 0x43000000, v194
	v_mul_f32_e32 v195, 0x43000000, v195
	ds_write_b128 v210, v[192:195] offset:4096
	v_mul_f32_e32 v196, 0x43000000, v196
	v_mul_f32_e32 v197, 0x43000000, v197
	v_mul_f32_e32 v198, 0x43000000, v198
	v_mul_f32_e32 v199, 0x43000000, v199
	ds_write_b128 v210, v[196:199] offset:5120
	v_mul_f32_e32 v200, 0x43000000, v200
	v_mul_f32_e32 v201, 0x43000000, v201
	v_mul_f32_e32 v202, 0x43000000, v202
	v_mul_f32_e32 v203, 0x43000000, v203
	ds_write_b128 v210, v[200:203] offset:6144
	v_mul_f32_e32 v204, 0x43000000, v204
	v_mul_f32_e32 v205, 0x43000000, v205
	v_mul_f32_e32 v206, 0x43000000, v206
	v_mul_f32_e32 v207, 0x43000000, v207
	ds_write_b128 v210, v[204:207] offset:7168
	s_waitcnt lgkmcnt(0)
	s_barrier
; #define GAS __attribute__((address_space(1)))
;     const int pr = item >> 1, kb = 2 * (pr / nblk) + (item & 1), nb = pr % nblk, k0 = 64 * kb, n0 = 32 * nb;
;     const int nr = n0 + (lane & 31); const int sc = MAP == 1 ? src_col_in(nr) : nr;
;     float v[32];
; #pragma unroll
;     for (int i = 0; i < 32; ++i) v[i] = sc >= 0 ? W[(size_t)(k0 + 2 * i + (lane >> 5)) * Nsrc + sc] : 0.f;
; #pragma unroll
;     for (int i = 0; i < 32; ++i) { const int k = k0 + 2 * i + (lane >> 5); float x = v[i] * wscale; if (KS) x *= (k < ksplit ? ksA[k] : ksB[k - ksplit]); scr[(2 * i + (lane >> 5)) * 33 + (lane & 31)] = x; }
;     LDS_WAIT(); asm volatile("" ::: "memory");
;     const int c = lane & 7;
; #pragma unroll
;     for (int j = 0; j < 4; ++j) { const int n = (lane >> 3) + 8 * j; const LAS float* s = scr + (8 * c) * 33 + n;
;         const unsigned long long o = (unsigned long long)pg8::pk4_fp8(s[0 * 33], s[1 * 33], s[2 * 33], s[3 * 33]) | ((unsigned long long)pg8::pk4_fp8(s[4 * 33], s[5 * 33], s[6 * 33], s[7 * 33]) << 32);
;         *(GAS unsigned long long*)(WT + (size_t)(n0 + n) * K + k0 + 8 * c) = o; }
;     LDS_WAIT(); asm volatile("" ::: "memory");
; }
; __global__ void __launch_bounds__(NWAVES * 64, 2) hybrid_fwd(Args args) {
;     ...
;         for (int rep = 0; rep < REP_PRO; ++rep)
;         for (int it = gw; it < DEPTH * I_L; it += NGW) {
;             const int l = it / I_L; int r = it % I_L;
;             if (r < I_IN) { if (l >= PROJ_F8_FROM) p0_transpose_item_f8<true, 1>(args.in[2] + (size_t)l * DM * NSRC, DM, NSRC, NPROJ / 32, (unsigned char*)(ws + WS_WIN + l * SZ_WIN), WUP8_SCALE, args.in[1] + l * DM, args.in[1] + l * DM, DM, scr, r, lane);
;                 else p0_transpose_item<1, true>(args.in[2] + (size_t)l * DM * NSRC, DM, NSRC, NPROJ / 32, (bf16*)(ws + WS_WIN + l * SZ_WIN), args.in[1] + l * DM, args.in[1] + l * DM, DM, scr, r, lane); continue; } r -= I_IN;
;             if (r < I_O) { if (l >= WO_F8_FROM) p0_transpose_item_f8<true>(args.in[13] + (size_t)l * DM * DM, DM, DM, DM / 32, (unsigned char*)(ws + WS_WO + l * SZ_WO), 64.f, args.in[6] + l * 2048, args.in[12] + l * 2048, 2048, scr, r, lane);
;                 else p0_transpose_item<0, true>(args.in[13] + (size_t)l * DM * DM, DM, DM, DM / 32, (bf16*)(ws + WS_WO + l * SZ_WO), args.in[6] + l * 2048, args.in[12] + l * 2048, 2048, scr, r, lane); continue; } r -= I_O;
	s_add_u32 s8, s38, 0x8003000
	s_addc_u32 s9, s39, 0
	global_load_dwordx4 v[176:179], v75, s[8:9]
	s_add_u32 s8, s8, 0x8000
	s_addc_u32 s9, s9, 0
	global_load_dwordx4 v[180:183], v75, s[8:9]
	s_add_u32 s8, s8, 0x8000
	s_addc_u32 s9, s9, 0
	global_load_dwordx4 v[184:187], v75, s[8:9]
	s_add_u32 s8, s8, 0x8000
	s_addc_u32 s9, s9, 0
	global_load_dwordx4 v[188:191], v75, s[8:9]
	s_add_u32 s8, s8, 0x8000
	s_addc_u32 s9, s9, 0
	global_load_dwordx4 v[192:195], v75, s[8:9]
	s_add_u32 s8, s8, 0x8000
	s_addc_u32 s9, s9, 0
	global_load_dwordx4 v[196:199], v75, s[8:9]
	s_add_u32 s8, s8, 0x8000
	s_addc_u32 s9, s9, 0
	global_load_dwordx4 v[200:203], v75, s[8:9]
	s_add_u32 s8, s8, 0x8000
	s_addc_u32 s9, s9, 0
	global_load_dwordx4 v[204:207], v75, s[8:9]
	s_add_u32 s6, s40, 0x1002000
	s_addc_u32 s7, s41, 0
	ds_read_b32 v226, v212
	ds_read_b32 v227, v212 offset:512
	ds_read_b32 v228, v212 offset:1024
	ds_read_b32 v229, v212 offset:1536
	ds_read_b32 v230, v212 offset:2048
	ds_read_b32 v231, v212 offset:2560
	ds_read_b32 v232, v212 offset:3072
	ds_read_b32 v233, v212 offset:3584
	ds_read_b32 v234, v212 offset:4096
	ds_read_b32 v235, v212 offset:4608
	ds_read_b32 v236, v212 offset:5120
	ds_read_b32 v237, v212 offset:5632
	ds_read_b32 v238, v212 offset:6144
	ds_read_b32 v239, v212 offset:6656
	ds_read_b32 v240, v212 offset:7168
	ds_read_b32 v241, v212 offset:7680
	s_waitcnt lgkmcnt(0)
	v_max_f32_e32 v226, v226, v226
	v_max_f32_e32 v227, v227, v227
	v_max_f32_e32 v228, v228, v228
	v_max_f32_e32 v229, v229, v229
	v_max_f32_e32 v230, v230, v230
	v_max_f32_e32 v231, v231, v231
	v_max_f32_e32 v232, v232, v232
	v_max_f32_e32 v233, v233, v233
	v_max_f32_e32 v234, v234, v234
	v_max_f32_e32 v235, v235, v235
	v_max_f32_e32 v236, v236, v236
	v_max_f32_e32 v237, v237, v237
	v_max_f32_e32 v238, v238, v238
	v_max_f32_e32 v239, v239, v239
	v_max_f32_e32 v240, v240, v240
	v_max_f32_e32 v241, v241, v241
	v_med3_f32 v226, v226, s62, v95
	v_med3_f32 v227, v227, s62, v95
	v_med3_f32 v228, v228, s62, v95
	v_med3_f32 v229, v229, s62, v95
	v_med3_f32 v230, v230, s62, v95
	v_med3_f32 v231, v231, s62, v95
	v_med3_f32 v232, v232, s62, v95
	v_med3_f32 v233, v233, s62, v95
	v_med3_f32 v234, v234, s62, v95
	v_med3_f32 v235, v235, s62, v95
	v_med3_f32 v236, v236, s62, v95
	v_med3_f32 v237, v237, s62, v95
	v_med3_f32 v238, v238, s62, v95
	v_med3_f32 v239, v239, s62, v95
	v_med3_f32 v240, v240, s62, v95
	v_med3_f32 v241, v241, s62, v95
	v_mov_b32_e32 v242, 0
	v_mov_b32_e32 v243, 0
	v_mov_b32_e32 v244, 0
	v_mov_b32_e32 v245, 0
	v_cvt_pk_fp8_f32 v242, v226, v227
	v_cvt_pk_fp8_f32 v243, v230, v231
	v_cvt_pk_fp8_f32 v244, v234, v235
	v_cvt_pk_fp8_f32 v245, v238, v239
	v_cvt_pk_fp8_f32 v242, v228, v229 op_sel:[0,0,1]
	v_cvt_pk_fp8_f32 v243, v232, v233 op_sel:[0,0,1]
	v_cvt_pk_fp8_f32 v244, v236, v237 op_sel:[0,0,1]
	v_cvt_pk_fp8_f32 v245, v240, v241 op_sel:[0,0,1]
	s_nop 0
	global_store_dwordx4 v79, v[242:245], s[6:7]
	ds_read_b32 v226, v214
	ds_read_b32 v227, v214 offset:512
	ds_read_b32 v228, v214 offset:1024
	ds_read_b32 v229, v214 offset:1536
	ds_read_b32 v230, v214 offset:2048
	ds_read_b32 v231, v214 offset:2560
	ds_read_b32 v232, v214 offset:3072
	ds_read_b32 v233, v214 offset:3584
	ds_read_b32 v234, v214 offset:4096
	ds_read_b32 v235, v214 offset:4608
	ds_read_b32 v236, v214 offset:5120
	ds_read_b32 v237, v214 offset:5632
	ds_read_b32 v238, v214 offset:6144
	ds_read_b32 v239, v214 offset:6656
	ds_read_b32 v240, v214 offset:7168
	ds_read_b32 v241, v214 offset:7680
	s_waitcnt lgkmcnt(0)
	v_max_f32_e32 v226, v226, v226
	v_max_f32_e32 v227, v227, v227
	v_max_f32_e32 v228, v228, v228
	v_max_f32_e32 v229, v229, v229
	v_max_f32_e32 v230, v230, v230
	v_max_f32_e32 v231, v231, v231
	v_max_f32_e32 v232, v232, v232
	v_max_f32_e32 v233, v233, v233
	v_max_f32_e32 v234, v234, v234
	v_max_f32_e32 v235, v235, v235
	v_max_f32_e32 v236, v236, v236
	v_max_f32_e32 v237, v237, v237
	v_max_f32_e32 v238, v238, v238
	v_max_f32_e32 v239, v239, v239
	v_max_f32_e32 v240, v240, v240
	v_max_f32_e32 v241, v241, v241
	v_med3_f32 v226, v226, s62, v95
	v_med3_f32 v227, v227, s62, v95
	v_med3_f32 v228, v228, s62, v95
	v_med3_f32 v229, v229, s62, v95
	v_med3_f32 v230, v230, s62, v95
	v_med3_f32 v231, v231, s62, v95
	v_med3_f32 v232, v232, s62, v95
	v_med3_f32 v233, v233, s62, v95
	v_med3_f32 v234, v234, s62, v95
	v_med3_f32 v235, v235, s62, v95
	v_med3_f32 v236, v236, s62, v95
	v_med3_f32 v237, v237, s62, v95
	v_med3_f32 v238, v238, s62, v95
	v_med3_f32 v239, v239, s62, v95
	v_med3_f32 v240, v240, s62, v95
	v_med3_f32 v241, v241, s62, v95
	v_mov_b32_e32 v242, 0
	v_mov_b32_e32 v243, 0
	v_mov_b32_e32 v244, 0
	v_mov_b32_e32 v245, 0
	v_cvt_pk_fp8_f32 v242, v226, v227
	v_cvt_pk_fp8_f32 v243, v230, v231
	v_cvt_pk_fp8_f32 v244, v234, v235
	v_cvt_pk_fp8_f32 v245, v238, v239
	v_cvt_pk_fp8_f32 v242, v228, v229 op_sel:[0,0,1]
	v_cvt_pk_fp8_f32 v243, v232, v233 op_sel:[0,0,1]
	v_cvt_pk_fp8_f32 v244, v236, v237 op_sel:[0,0,1]
	v_cvt_pk_fp8_f32 v245, v240, v241 op_sel:[0,0,1]
	s_nop 0
	global_store_dwordx4 v80, v[242:245], s[6:7]
	s_waitcnt vmcnt(12)
	v_mul_f32_e32 v144, 0x43000000, v144
	v_mul_f32_e32 v145, 0x43000000, v145
	v_mul_f32_e32 v146, 0x43000000, v146
	v_mul_f32_e32 v147, 0x43000000, v147
	ds_write_b128 v209, v[144:147]
	v_mul_f32_e32 v148, 0x43000000, v148
	v_mul_f32_e32 v149, 0x43000000, v149
	v_mul_f32_e32 v150, 0x43000000, v150
	v_mul_f32_e32 v151, 0x43000000, v151
	ds_write_b128 v209, v[148:151] offset:1024
	v_mul_f32_e32 v152, 0x43000000, v152
	v_mul_f32_e32 v153, 0x43000000, v153
	v_mul_f32_e32 v154, 0x43000000, v154
	v_mul_f32_e32 v155, 0x43000000, v155
	ds_write_b128 v209, v[152:155] offset:2048
	v_mul_f32_e32 v156, 0x43000000, v156
	v_mul_f32_e32 v157, 0x43000000, v157
	v_mul_f32_e32 v158, 0x43000000, v158
	v_mul_f32_e32 v159, 0x43000000, v159
	ds_write_b128 v209, v[156:159] offset:3072
	v_mul_f32_e32 v160, 0x43000000, v160
	v_mul_f32_e32 v161, 0x43000000, v161
	v_mul_f32_e32 v162, 0x43000000, v162
	v_mul_f32_e32 v163, 0x43000000, v163
	ds_write_b128 v209, v[160:163] offset:4096
	v_mul_f32_e32 v164, 0x43000000, v164
	v_mul_f32_e32 v165, 0x43000000, v165
	v_mul_f32_e32 v166, 0x43000000, v166
	v_mul_f32_e32 v167, 0x43000000, v167
	ds_write_b128 v209, v[164:167] offset:5120
	v_mul_f32_e32 v168, 0x43000000, v168
	v_mul_f32_e32 v169, 0x43000000, v169
	v_mul_f32_e32 v170, 0x43000000, v170
	v_mul_f32_e32 v171, 0x43000000, v171
	ds_write_b128 v209, v[168:171] offset:6144
	v_mul_f32_e32 v172, 0x43000000, v172
	v_mul_f32_e32 v173, 0x43000000, v173
	v_mul_f32_e32 v174, 0x43000000, v174
	v_mul_f32_e32 v175, 0x43000000, v175
	ds_write_b128 v209, v[172:175] offset:7168
	s_waitcnt lgkmcnt(0)
	s_barrier
; #define GAS __attribute__((address_space(1)))
; #define LAS __attribute__((address_space(3)))
; #define LDS_WAIT() asm volatile("s_waitcnt lgkmcnt(0)" ::: "memory")
;     const int pr = item >> 1, kb = 2 * (pr / nblk) + (item & 1), nb = pr % nblk, k0 = 64 * kb, n0 = 32 * nb;
;     const int nr = n0 + (lane & 31); const int sc = MAP == 1 ? src_col_in(nr) : nr;
;     float v[32];
; #pragma unroll
;     for (int i = 0; i < 32; ++i) v[i] = sc >= 0 ? W[(size_t)(k0 + 2 * i + (lane >> 5)) * Nsrc + sc] : 0.f;
; #pragma unroll
;     for (int i = 0; i < 32; ++i) { const int k = k0 + 2 * i + (lane >> 5); float x = v[i] * wscale; if (KS) x *= (k < ksplit ? ksA[k] : ksB[k - ksplit]); scr[(2 * i + (lane >> 5)) * 33 + (lane & 31)] = x; }
;     LDS_WAIT(); asm volatile("" ::: "memory");
;     const int c = lane & 7;
; #pragma unroll
;     for (int j = 0; j < 4; ++j) { const int n = (lane >> 3) + 8 * j; const LAS float* s = scr + (8 * c) * 33 + n;
;         const unsigned long long o = (unsigned long long)pg8::pk4_fp8(s[0 * 33], s[1 * 33], s[2 * 33], s[3 * 33]) | ((unsigned long long)pg8::pk4_fp8(s[4 * 33], s[5 * 33], s[6 * 33], s[7 * 33]) << 32);
;         *(GAS unsigned long long*)(WT + (size_t)(n0 + n) * K + k0 + 8 * c) = o; }
;     LDS_WAIT(); asm volatile("" ::: "memory");
; }
; __global__ void __launch_bounds__(NWAVES * 64, 2) hybrid_fwd(Args args) {
;     ...
;             p0_transpose_item_f8<false>(args.in[16] + (size_t)l * FF * DM, FF, DM, DM / 32, (unsigned char*)(ws + WS_WDN + l * SZ_WDN), 128.f, args.in[16], args.in[16], 0, scr, r, lane);
	s_add_u32 s8, s38, 0xc000000
	s_addc_u32 s9, s39, 0
	global_load_dwordx4 v[144:147], v75, s[8:9]
	s_add_u32 s8, s8, 0x8000
	s_addc_u32 s9, s9, 0
	global_load_dwordx4 v[148:151], v75, s[8:9]
	s_add_u32 s8, s8, 0x8000
	s_addc_u32 s9, s9, 0
	global_load_dwordx4 v[152:155], v75, s[8:9]
	s_add_u32 s8, s8, 0x8000
	s_addc_u32 s9, s9, 0
	global_load_dwordx4 v[156:159], v75, s[8:9]
	s_add_u32 s8, s8, 0x8000
	s_addc_u32 s9, s9, 0
	global_load_dwordx4 v[160:163], v75, s[8:9]
	s_add_u32 s8, s8, 0x8000
	s_addc_u32 s9, s9, 0
	global_load_dwordx4 v[164:167], v75, s[8:9]
	s_add_u32 s8, s8, 0x8000
	s_addc_u32 s9, s9, 0
	global_load_dwordx4 v[168:171], v75, s[8:9]
	s_add_u32 s8, s8, 0x8000
	s_addc_u32 s9, s9, 0
	global_load_dwordx4 v[172:175], v75, s[8:9]
	s_add_u32 s6, s40, 0x2002000
	s_addc_u32 s7, s41, 0
	ds_read_b32 v226, v211
	ds_read_b32 v227, v211 offset:512
	ds_read_b32 v228, v211 offset:1024
	ds_read_b32 v229, v211 offset:1536
	ds_read_b32 v230, v211 offset:2048
	ds_read_b32 v231, v211 offset:2560
	ds_read_b32 v232, v211 offset:3072
	ds_read_b32 v233, v211 offset:3584
	ds_read_b32 v234, v211 offset:4096
	ds_read_b32 v235, v211 offset:4608
	ds_read_b32 v236, v211 offset:5120
	ds_read_b32 v237, v211 offset:5632
	ds_read_b32 v238, v211 offset:6144
	ds_read_b32 v239, v211 offset:6656
	ds_read_b32 v240, v211 offset:7168
	ds_read_b32 v241, v211 offset:7680
	s_waitcnt lgkmcnt(0)
	v_max_f32_e32 v226, v226, v226
	v_max_f32_e32 v227, v227, v227
	v_max_f32_e32 v228, v228, v228
	v_max_f32_e32 v229, v229, v229
	v_max_f32_e32 v230, v230, v230
	v_max_f32_e32 v231, v231, v231
	v_max_f32_e32 v232, v232, v232
	v_max_f32_e32 v233, v233, v233
	v_max_f32_e32 v234, v234, v234
	v_max_f32_e32 v235, v235, v235
	v_max_f32_e32 v236, v236, v236
	v_max_f32_e32 v237, v237, v237
	v_max_f32_e32 v238, v238, v238
	v_max_f32_e32 v239, v239, v239
	v_max_f32_e32 v240, v240, v240
	v_max_f32_e32 v241, v241, v241
	v_med3_f32 v226, v226, s62, v95
	v_med3_f32 v227, v227, s62, v95
	v_med3_f32 v228, v228, s62, v95
	v_med3_f32 v229, v229, s62, v95
	v_med3_f32 v230, v230, s62, v95
	v_med3_f32 v231, v231, s62, v95
	v_med3_f32 v232, v232, s62, v95
	v_med3_f32 v233, v233, s62, v95
	v_med3_f32 v234, v234, s62, v95
	v_med3_f32 v235, v235, s62, v95
	v_med3_f32 v236, v236, s62, v95
	v_med3_f32 v237, v237, s62, v95
	v_med3_f32 v238, v238, s62, v95
	v_med3_f32 v239, v239, s62, v95
	v_med3_f32 v240, v240, s62, v95
	v_med3_f32 v241, v241, s62, v95
	v_mov_b32_e32 v242, 0
	v_mov_b32_e32 v243, 0
	v_mov_b32_e32 v244, 0
	v_mov_b32_e32 v245, 0
	v_cvt_pk_fp8_f32 v242, v226, v227
	v_cvt_pk_fp8_f32 v243, v230, v231
	v_cvt_pk_fp8_f32 v244, v234, v235
	v_cvt_pk_fp8_f32 v245, v238, v239
	v_cvt_pk_fp8_f32 v242, v228, v229 op_sel:[0,0,1]
	v_cvt_pk_fp8_f32 v243, v232, v233 op_sel:[0,0,1]
	v_cvt_pk_fp8_f32 v244, v236, v237 op_sel:[0,0,1]
	v_cvt_pk_fp8_f32 v245, v240, v241 op_sel:[0,0,1]
	s_nop 0
	global_store_dwordx4 v79, v[242:245], s[6:7]
	ds_read_b32 v226, v213
	ds_read_b32 v227, v213 offset:512
	ds_read_b32 v228, v213 offset:1024
	ds_read_b32 v229, v213 offset:1536
	ds_read_b32 v230, v213 offset:2048
	ds_read_b32 v231, v213 offset:2560
	ds_read_b32 v232, v213 offset:3072
	ds_read_b32 v233, v213 offset:3584
	ds_read_b32 v234, v213 offset:4096
	ds_read_b32 v235, v213 offset:4608
	ds_read_b32 v236, v213 offset:5120
	ds_read_b32 v237, v213 offset:5632
	ds_read_b32 v238, v213 offset:6144
	ds_read_b32 v239, v213 offset:6656
	ds_read_b32 v240, v213 offset:7168
	ds_read_b32 v241, v213 offset:7680
	s_waitcnt lgkmcnt(0)
	v_max_f32_e32 v226, v226, v226
	v_max_f32_e32 v227, v227, v227
	v_max_f32_e32 v228, v228, v228
	v_max_f32_e32 v229, v229, v229
	v_max_f32_e32 v230, v230, v230
	v_max_f32_e32 v231, v231, v231
	v_max_f32_e32 v232, v232, v232
	v_max_f32_e32 v233, v233, v233
	v_max_f32_e32 v234, v234, v234
	v_max_f32_e32 v235, v235, v235
	v_max_f32_e32 v236, v236, v236
	v_max_f32_e32 v237, v237, v237
	v_max_f32_e32 v238, v238, v238
	v_max_f32_e32 v239, v239, v239
	v_max_f32_e32 v240, v240, v240
	v_max_f32_e32 v241, v241, v241
	v_med3_f32 v226, v226, s62, v95
	v_med3_f32 v227, v227, s62, v95
	v_med3_f32 v228, v228, s62, v95
	v_med3_f32 v229, v229, s62, v95
	v_med3_f32 v230, v230, s62, v95
	v_med3_f32 v231, v231, s62, v95
	v_med3_f32 v232, v232, s62, v95
	v_med3_f32 v233, v233, s62, v95
	v_med3_f32 v234, v234, s62, v95
	v_med3_f32 v235, v235, s62, v95
	v_med3_f32 v236, v236, s62, v95
	v_med3_f32 v237, v237, s62, v95
	v_med3_f32 v238, v238, s62, v95
	v_med3_f32 v239, v239, s62, v95
	v_med3_f32 v240, v240, s62, v95
	v_med3_f32 v241, v241, s62, v95
	v_mov_b32_e32 v242, 0
	v_mov_b32_e32 v243, 0
	v_mov_b32_e32 v244, 0
	v_mov_b32_e32 v245, 0
	v_cvt_pk_fp8_f32 v242, v226, v227
	v_cvt_pk_fp8_f32 v243, v230, v231
	v_cvt_pk_fp8_f32 v244, v234, v235
	v_cvt_pk_fp8_f32 v245, v238, v239
	v_cvt_pk_fp8_f32 v242, v228, v229 op_sel:[0,0,1]
	v_cvt_pk_fp8_f32 v243, v232, v233 op_sel:[0,0,1]
	v_cvt_pk_fp8_f32 v244, v236, v237 op_sel:[0,0,1]
	v_cvt_pk_fp8_f32 v245, v240, v241 op_sel:[0,0,1]
	s_nop 0
	global_store_dwordx4 v80, v[242:245], s[6:7]
	s_waitcnt vmcnt(12)
	v_mul_f32_e32 v176, 0x43000000, v176
	v_mul_f32_e32 v177, 0x43000000, v177
	v_mul_f32_e32 v178, 0x43000000, v178
	v_mul_f32_e32 v179, 0x43000000, v179
	ds_write_b128 v210, v[176:179]
	v_mul_f32_e32 v180, 0x43000000, v180
	v_mul_f32_e32 v181, 0x43000000, v181
	v_mul_f32_e32 v182, 0x43000000, v182
	v_mul_f32_e32 v183, 0x43000000, v183
	ds_write_b128 v210, v[180:183] offset:1024
	v_mul_f32_e32 v184, 0x43000000, v184
	v_mul_f32_e32 v185, 0x43000000, v185
	v_mul_f32_e32 v186, 0x43000000, v186
	v_mul_f32_e32 v187, 0x43000000, v187
	ds_write_b128 v210, v[184:187] offset:2048
	v_mul_f32_e32 v188, 0x43000000, v188
	v_mul_f32_e32 v189, 0x43000000, v189
	v_mul_f32_e32 v190, 0x43000000, v190
	v_mul_f32_e32 v191, 0x43000000, v191
	ds_write_b128 v210, v[188:191] offset:3072
	v_mul_f32_e32 v192, 0x43000000, v192
	v_mul_f32_e32 v193, 0x43000000, v193
	v_mul_f32_e32 v194, 0x43000000, v194
	v_mul_f32_e32 v195, 0x43000000, v195
	ds_write_b128 v210, v[192:195] offset:4096
	v_mul_f32_e32 v196, 0x43000000, v196
	v_mul_f32_e32 v197, 0x43000000, v197
	v_mul_f32_e32 v198, 0x43000000, v198
	v_mul_f32_e32 v199, 0x43000000, v199
	ds_write_b128 v210, v[196:199] offset:5120
	v_mul_f32_e32 v200, 0x43000000, v200
	v_mul_f32_e32 v201, 0x43000000, v201
	v_mul_f32_e32 v202, 0x43000000, v202
	v_mul_f32_e32 v203, 0x43000000, v203
	ds_write_b128 v210, v[200:203] offset:6144
	v_mul_f32_e32 v204, 0x43000000, v204
	v_mul_f32_e32 v205, 0x43000000, v205
	v_mul_f32_e32 v206, 0x43000000, v206
	v_mul_f32_e32 v207, 0x43000000, v207
	ds_write_b128 v210, v[204:207] offset:7168
	s_waitcnt lgkmcnt(0)
	s_barrier
; #define GAS __attribute__((address_space(1)))
; #define LAS __attribute__((address_space(3)))
; #define LDS_WAIT() asm volatile("s_waitcnt lgkmcnt(0)" ::: "memory")
;     const int pr = item >> 1, kb = 2 * (pr / nblk) + (item & 1), nb = pr % nblk, k0 = 64 * kb, n0 = 32 * nb;
;     const int nr = n0 + (lane & 31); const int sc = MAP == 1 ? src_col_in(nr) : nr;
;     float v[32];
; #pragma unroll
;     for (int i = 0; i < 32; ++i) v[i] = sc >= 0 ? W[(size_t)(k0 + 2 * i + (lane >> 5)) * Nsrc + sc] : 0.f;
; #pragma unroll
;     for (int i = 0; i < 32; ++i) { const int k = k0 + 2 * i + (lane >> 5); float x = v[i] * wscale; if (KS) x *= (k < ksplit ? ksA[k] : ksB[k - ksplit]); scr[(2 * i + (lane >> 5)) * 33 + (lane & 31)] = x; }
;     LDS_WAIT(); asm volatile("" ::: "memory");
;     const int c = lane & 7;
; #pragma unroll
;     for (int j = 0; j < 4; ++j) { const int n = (lane >> 3) + 8 * j; const LAS float* s = scr + (8 * c) * 33 + n;
;         const unsigned long long o = (unsigned long long)pg8::pk4_fp8(s[0 * 33], s[1 * 33], s[2 * 33], s[3 * 33]) | ((unsigned long long)pg8::pk4_fp8(s[4 * 33], s[5 * 33], s[6 * 33], s[7 * 33]) << 32);
;         *(GAS unsigned long long*)(WT + (size_t)(n0 + n) * K + k0 + 8 * c) = o; }
;     LDS_WAIT(); asm volatile("" ::: "memory");
; }
; __global__ void __launch_bounds__(NWAVES * 64, 2) hybrid_fwd(Args args) {
;     ...
;             p0_transpose_item_f8<false>(args.in[16] + (size_t)l * FF * DM, FF, DM, DM / 32, (unsigned char*)(ws + WS_WDN + l * SZ_WDN), 128.f, args.in[16], args.in[16], 0, scr, r, lane);
	s_add_u32 s8, s38, 0xc001000
	s_addc_u32 s9, s39, 0
	global_load_dwordx4 v[176:179], v75, s[8:9]
	s_add_u32 s8, s8, 0x8000
	s_addc_u32 s9, s9, 0
	global_load_dwordx4 v[180:183], v75, s[8:9]
	s_add_u32 s8, s8, 0x8000
	s_addc_u32 s9, s9, 0
	global_load_dwordx4 v[184:187], v75, s[8:9]
	s_add_u32 s8, s8, 0x8000
	s_addc_u32 s9, s9, 0
	global_load_dwordx4 v[188:191], v75, s[8:9]
	s_add_u32 s8, s8, 0x8000
	s_addc_u32 s9, s9, 0
	global_load_dwordx4 v[192:195], v75, s[8:9]
	s_add_u32 s8, s8, 0x8000
	s_addc_u32 s9, s9, 0
	global_load_dwordx4 v[196:199], v75, s[8:9]
	s_add_u32 s8, s8, 0x8000
	s_addc_u32 s9, s9, 0
	global_load_dwordx4 v[200:203], v75, s[8:9]
	s_add_u32 s8, s8, 0x8000
	s_addc_u32 s9, s9, 0
	global_load_dwordx4 v[204:207], v75, s[8:9]
	s_add_u32 s6, s40, 0x3002000
	s_addc_u32 s7, s41, 0
	ds_read_b32 v226, v212
	ds_read_b32 v227, v212 offset:512
	ds_read_b32 v228, v212 offset:1024
	ds_read_b32 v229, v212 offset:1536
	ds_read_b32 v230, v212 offset:2048
	ds_read_b32 v231, v212 offset:2560
	ds_read_b32 v232, v212 offset:3072
	ds_read_b32 v233, v212 offset:3584
	ds_read_b32 v234, v212 offset:4096
	ds_read_b32 v235, v212 offset:4608
	ds_read_b32 v236, v212 offset:5120
	ds_read_b32 v237, v212 offset:5632
	ds_read_b32 v238, v212 offset:6144
	ds_read_b32 v239, v212 offset:6656
	ds_read_b32 v240, v212 offset:7168
	ds_read_b32 v241, v212 offset:7680
	s_waitcnt lgkmcnt(0)
	v_max_f32_e32 v226, v226, v226
	v_max_f32_e32 v227, v227, v227
	v_max_f32_e32 v228, v228, v228
	v_max_f32_e32 v229, v229, v229
	v_max_f32_e32 v230, v230, v230
	v_max_f32_e32 v231, v231, v231
	v_max_f32_e32 v232, v232, v232
	v_max_f32_e32 v233, v233, v233
	v_max_f32_e32 v234, v234, v234
	v_max_f32_e32 v235, v235, v235
	v_max_f32_e32 v236, v236, v236
	v_max_f32_e32 v237, v237, v237
	v_max_f32_e32 v238, v238, v238
	v_max_f32_e32 v239, v239, v239
	v_max_f32_e32 v240, v240, v240
	v_max_f32_e32 v241, v241, v241
	v_med3_f32 v226, v226, s62, v95
	v_med3_f32 v227, v227, s62, v95
	v_med3_f32 v228, v228, s62, v95
	v_med3_f32 v229, v229, s62, v95
	v_med3_f32 v230, v230, s62, v95
	v_med3_f32 v231, v231, s62, v95
	v_med3_f32 v232, v232, s62, v95
	v_med3_f32 v233, v233, s62, v95
	v_med3_f32 v234, v234, s62, v95
	v_med3_f32 v235, v235, s62, v95
	v_med3_f32 v236, v236, s62, v95
	v_med3_f32 v237, v237, s62, v95
	v_med3_f32 v238, v238, s62, v95
	v_med3_f32 v239, v239, s62, v95
	v_med3_f32 v240, v240, s62, v95
	v_med3_f32 v241, v241, s62, v95
	v_mov_b32_e32 v242, 0
	v_mov_b32_e32 v243, 0
	v_mov_b32_e32 v244, 0
	v_mov_b32_e32 v245, 0
	v_cvt_pk_fp8_f32 v242, v226, v227
	v_cvt_pk_fp8_f32 v243, v230, v231
	v_cvt_pk_fp8_f32 v244, v234, v235
	v_cvt_pk_fp8_f32 v245, v238, v239
	v_cvt_pk_fp8_f32 v242, v228, v229 op_sel:[0,0,1]
	v_cvt_pk_fp8_f32 v243, v232, v233 op_sel:[0,0,1]
	v_cvt_pk_fp8_f32 v244, v236, v237 op_sel:[0,0,1]
	v_cvt_pk_fp8_f32 v245, v240, v241 op_sel:[0,0,1]
	s_nop 0
	global_store_dwordx4 v79, v[242:245], s[6:7]
	ds_read_b32 v226, v214
	ds_read_b32 v227, v214 offset:512
	ds_read_b32 v228, v214 offset:1024
	ds_read_b32 v229, v214 offset:1536
	ds_read_b32 v230, v214 offset:2048
	ds_read_b32 v231, v214 offset:2560
	ds_read_b32 v232, v214 offset:3072
	ds_read_b32 v233, v214 offset:3584
	ds_read_b32 v234, v214 offset:4096
	ds_read_b32 v235, v214 offset:4608
	ds_read_b32 v236, v214 offset:5120
	ds_read_b32 v237, v214 offset:5632
	ds_read_b32 v238, v214 offset:6144
	ds_read_b32 v239, v214 offset:6656
	ds_read_b32 v240, v214 offset:7168
	ds_read_b32 v241, v214 offset:7680
	s_waitcnt lgkmcnt(0)
	v_max_f32_e32 v226, v226, v226
	v_max_f32_e32 v227, v227, v227
	v_max_f32_e32 v228, v228, v228
	v_max_f32_e32 v229, v229, v229
	v_max_f32_e32 v230, v230, v230
	v_max_f32_e32 v231, v231, v231
	v_max_f32_e32 v232, v232, v232
	v_max_f32_e32 v233, v233, v233
	v_max_f32_e32 v234, v234, v234
	v_max_f32_e32 v235, v235, v235
	v_max_f32_e32 v236, v236, v236
	v_max_f32_e32 v237, v237, v237
	v_max_f32_e32 v238, v238, v238
	v_max_f32_e32 v239, v239, v239
	v_max_f32_e32 v240, v240, v240
	v_max_f32_e32 v241, v241, v241
	v_med3_f32 v226, v226, s62, v95
	v_med3_f32 v227, v227, s62, v95
	v_med3_f32 v228, v228, s62, v95
	v_med3_f32 v229, v229, s62, v95
	v_med3_f32 v230, v230, s62, v95
	v_med3_f32 v231, v231, s62, v95
	v_med3_f32 v232, v232, s62, v95
	v_med3_f32 v233, v233, s62, v95
	v_med3_f32 v234, v234, s62, v95
	v_med3_f32 v235, v235, s62, v95
	v_med3_f32 v236, v236, s62, v95
	v_med3_f32 v237, v237, s62, v95
	v_med3_f32 v238, v238, s62, v95
	v_med3_f32 v239, v239, s62, v95
	v_med3_f32 v240, v240, s62, v95
	v_med3_f32 v241, v241, s62, v95
	v_mov_b32_e32 v242, 0
	v_mov_b32_e32 v243, 0
	v_mov_b32_e32 v244, 0
	v_mov_b32_e32 v245, 0
	v_cvt_pk_fp8_f32 v242, v226, v227
	v_cvt_pk_fp8_f32 v243, v230, v231
	v_cvt_pk_fp8_f32 v244, v234, v235
	v_cvt_pk_fp8_f32 v245, v238, v239
	v_cvt_pk_fp8_f32 v242, v228, v229 op_sel:[0,0,1]
	v_cvt_pk_fp8_f32 v243, v232, v233 op_sel:[0,0,1]
	v_cvt_pk_fp8_f32 v244, v236, v237 op_sel:[0,0,1]
	v_cvt_pk_fp8_f32 v245, v240, v241 op_sel:[0,0,1]
	s_nop 0
	global_store_dwordx4 v80, v[242:245], s[6:7]
	s_waitcnt vmcnt(12)
	v_mul_f32_e32 v144, 0x43000000, v144
	v_mul_f32_e32 v145, 0x43000000, v145
	v_mul_f32_e32 v146, 0x43000000, v146
	v_mul_f32_e32 v147, 0x43000000, v147
	ds_write_b128 v209, v[144:147]
	v_mul_f32_e32 v148, 0x43000000, v148
	v_mul_f32_e32 v149, 0x43000000, v149
	v_mul_f32_e32 v150, 0x43000000, v150
	v_mul_f32_e32 v151, 0x43000000, v151
	ds_write_b128 v209, v[148:151] offset:1024
	v_mul_f32_e32 v152, 0x43000000, v152
	v_mul_f32_e32 v153, 0x43000000, v153
	v_mul_f32_e32 v154, 0x43000000, v154
	v_mul_f32_e32 v155, 0x43000000, v155
	ds_write_b128 v209, v[152:155] offset:2048
	v_mul_f32_e32 v156, 0x43000000, v156
	v_mul_f32_e32 v157, 0x43000000, v157
	v_mul_f32_e32 v158, 0x43000000, v158
	v_mul_f32_e32 v159, 0x43000000, v159
	ds_write_b128 v209, v[156:159] offset:3072
	v_mul_f32_e32 v160, 0x43000000, v160
	v_mul_f32_e32 v161, 0x43000000, v161
	v_mul_f32_e32 v162, 0x43000000, v162
	v_mul_f32_e32 v163, 0x43000000, v163
	ds_write_b128 v209, v[160:163] offset:4096
	v_mul_f32_e32 v164, 0x43000000, v164
	v_mul_f32_e32 v165, 0x43000000, v165
	v_mul_f32_e32 v166, 0x43000000, v166
	v_mul_f32_e32 v167, 0x43000000, v167
	ds_write_b128 v209, v[164:167] offset:5120
	v_mul_f32_e32 v168, 0x43000000, v168
	v_mul_f32_e32 v169, 0x43000000, v169
	v_mul_f32_e32 v170, 0x43000000, v170
	v_mul_f32_e32 v171, 0x43000000, v171
	ds_write_b128 v209, v[168:171] offset:6144
	v_mul_f32_e32 v172, 0x43000000, v172
	v_mul_f32_e32 v173, 0x43000000, v173
	v_mul_f32_e32 v174, 0x43000000, v174
	v_mul_f32_e32 v175, 0x43000000, v175
	ds_write_b128 v209, v[172:175] offset:7168
	s_waitcnt lgkmcnt(0)
	s_barrier
; #define GAS __attribute__((address_space(1)))
; #define LAS __attribute__((address_space(3)))
; #define LDS_WAIT() asm volatile("s_waitcnt lgkmcnt(0)" ::: "memory")
;     const int pr = item >> 1, kb = 2 * (pr / nblk) + (item & 1), nb = pr % nblk, k0 = 64 * kb, n0 = 32 * nb;
;     const int nr = n0 + (lane & 31); const int sc = MAP == 1 ? src_col_in(nr) : nr;
;     float v[32];
; #pragma unroll
;     for (int i = 0; i < 32; ++i) v[i] = sc >= 0 ? W[(size_t)(k0 + 2 * i + (lane >> 5)) * Nsrc + sc] : 0.f;
; #pragma unroll
;     for (int i = 0; i < 32; ++i) { const int k = k0 + 2 * i + (lane >> 5); float x = v[i] * wscale; if (KS) x *= (k < ksplit ? ksA[k] : ksB[k - ksplit]); scr[(2 * i + (lane >> 5)) * 33 + (lane & 31)] = x; }
;     LDS_WAIT(); asm volatile("" ::: "memory");
;     const int c = lane & 7;
; #pragma unroll
;     for (int j = 0; j < 4; ++j) { const int n = (lane >> 3) + 8 * j; const LAS float* s = scr + (8 * c) * 33 + n;
;         const unsigned long long o = (unsigned long long)pg8::pk4_fp8(s[0 * 33], s[1 * 33], s[2 * 33], s[3 * 33]) | ((unsigned long long)pg8::pk4_fp8(s[4 * 33], s[5 * 33], s[6 * 33], s[7 * 33]) << 32);
;         *(GAS unsigned long long*)(WT + (size_t)(n0 + n) * K + k0 + 8 * c) = o; }
;     LDS_WAIT(); asm volatile("" ::: "memory");
; }
; __global__ void __launch_bounds__(NWAVES * 64, 2) hybrid_fwd(Args args) {
;     ...
;             p0_transpose_item_f8<false>(args.in[16] + (size_t)l * FF * DM, FF, DM, DM / 32, (unsigned char*)(ws + WS_WDN + l * SZ_WDN), 128.f, args.in[16], args.in[16], 0, scr, r, lane);
	s_add_u32 s8, s38, 0xc002000
	s_addc_u32 s9, s39, 0
	global_load_dwordx4 v[144:147], v75, s[8:9]
	s_add_u32 s8, s8, 0x8000
	s_addc_u32 s9, s9, 0
	global_load_dwordx4 v[148:151], v75, s[8:9]
	s_add_u32 s8, s8, 0x8000
	s_addc_u32 s9, s9, 0
	global_load_dwordx4 v[152:155], v75, s[8:9]
	s_add_u32 s8, s8, 0x8000
	s_addc_u32 s9, s9, 0
	global_load_dwordx4 v[156:159], v75, s[8:9]
	s_add_u32 s8, s8, 0x8000
	s_addc_u32 s9, s9, 0
	global_load_dwordx4 v[160:163], v75, s[8:9]
	s_add_u32 s8, s8, 0x8000
	s_addc_u32 s9, s9, 0
	global_load_dwordx4 v[164:167], v75, s[8:9]
	s_add_u32 s8, s8, 0x8000
	s_addc_u32 s9, s9, 0
	global_load_dwordx4 v[168:171], v75, s[8:9]
	s_add_u32 s8, s8, 0x8000
	s_addc_u32 s9, s9, 0
	global_load_dwordx4 v[172:175], v75, s[8:9]
	s_add_u32 s6, s40, 0x3000
	s_addc_u32 s7, s41, 0
	ds_read_b32 v226, v211
	ds_read_b32 v227, v211 offset:512
	ds_read_b32 v228, v211 offset:1024
	ds_read_b32 v229, v211 offset:1536
	ds_read_b32 v230, v211 offset:2048
	ds_read_b32 v231, v211 offset:2560
	ds_read_b32 v232, v211 offset:3072
	ds_read_b32 v233, v211 offset:3584
	ds_read_b32 v234, v211 offset:4096
	ds_read_b32 v235, v211 offset:4608
	ds_read_b32 v236, v211 offset:5120
	ds_read_b32 v237, v211 offset:5632
	ds_read_b32 v238, v211 offset:6144
	ds_read_b32 v239, v211 offset:6656
	ds_read_b32 v240, v211 offset:7168
	ds_read_b32 v241, v211 offset:7680
	s_waitcnt lgkmcnt(0)
	v_max_f32_e32 v226, v226, v226
	v_max_f32_e32 v227, v227, v227
	v_max_f32_e32 v228, v228, v228
	v_max_f32_e32 v229, v229, v229
	v_max_f32_e32 v230, v230, v230
	v_max_f32_e32 v231, v231, v231
	v_max_f32_e32 v232, v232, v232
	v_max_f32_e32 v233, v233, v233
	v_max_f32_e32 v234, v234, v234
	v_max_f32_e32 v235, v235, v235
	v_max_f32_e32 v236, v236, v236
	v_max_f32_e32 v237, v237, v237
	v_max_f32_e32 v238, v238, v238
	v_max_f32_e32 v239, v239, v239
	v_max_f32_e32 v240, v240, v240
	v_max_f32_e32 v241, v241, v241
	v_med3_f32 v226, v226, s62, v95
	v_med3_f32 v227, v227, s62, v95
	v_med3_f32 v228, v228, s62, v95
	v_med3_f32 v229, v229, s62, v95
	v_med3_f32 v230, v230, s62, v95
	v_med3_f32 v231, v231, s62, v95
	v_med3_f32 v232, v232, s62, v95
	v_med3_f32 v233, v233, s62, v95
	v_med3_f32 v234, v234, s62, v95
	v_med3_f32 v235, v235, s62, v95
	v_med3_f32 v236, v236, s62, v95
	v_med3_f32 v237, v237, s62, v95
	v_med3_f32 v238, v238, s62, v95
	v_med3_f32 v239, v239, s62, v95
	v_med3_f32 v240, v240, s62, v95
	v_med3_f32 v241, v241, s62, v95
	v_mov_b32_e32 v242, 0
	v_mov_b32_e32 v243, 0
	v_mov_b32_e32 v244, 0
	v_mov_b32_e32 v245, 0
	v_cvt_pk_fp8_f32 v242, v226, v227
	v_cvt_pk_fp8_f32 v243, v230, v231
	v_cvt_pk_fp8_f32 v244, v234, v235
	v_cvt_pk_fp8_f32 v245, v238, v239
	v_cvt_pk_fp8_f32 v242, v228, v229 op_sel:[0,0,1]
	v_cvt_pk_fp8_f32 v243, v232, v233 op_sel:[0,0,1]
	v_cvt_pk_fp8_f32 v244, v236, v237 op_sel:[0,0,1]
	v_cvt_pk_fp8_f32 v245, v240, v241 op_sel:[0,0,1]
	s_nop 0
	global_store_dwordx4 v79, v[242:245], s[6:7]
	ds_read_b32 v226, v213
	ds_read_b32 v227, v213 offset:512
	ds_read_b32 v228, v213 offset:1024
	ds_read_b32 v229, v213 offset:1536
	ds_read_b32 v230, v213 offset:2048
	ds_read_b32 v231, v213 offset:2560
	ds_read_b32 v232, v213 offset:3072
	ds_read_b32 v233, v213 offset:3584
	ds_read_b32 v234, v213 offset:4096
	ds_read_b32 v235, v213 offset:4608
	ds_read_b32 v236, v213 offset:5120
	ds_read_b32 v237, v213 offset:5632
	ds_read_b32 v238, v213 offset:6144
	ds_read_b32 v239, v213 offset:6656
	ds_read_b32 v240, v213 offset:7168
	ds_read_b32 v241, v213 offset:7680
	s_waitcnt lgkmcnt(0)
	v_max_f32_e32 v226, v226, v226
	v_max_f32_e32 v227, v227, v227
	v_max_f32_e32 v228, v228, v228
	v_max_f32_e32 v229, v229, v229
	v_max_f32_e32 v230, v230, v230
	v_max_f32_e32 v231, v231, v231
	v_max_f32_e32 v232, v232, v232
	v_max_f32_e32 v233, v233, v233
	v_max_f32_e32 v234, v234, v234
	v_max_f32_e32 v235, v235, v235
	v_max_f32_e32 v236, v236, v236
	v_max_f32_e32 v237, v237, v237
	v_max_f32_e32 v238, v238, v238
	v_max_f32_e32 v239, v239, v239
	v_max_f32_e32 v240, v240, v240
	v_max_f32_e32 v241, v241, v241
	v_med3_f32 v226, v226, s62, v95
	v_med3_f32 v227, v227, s62, v95
	v_med3_f32 v228, v228, s62, v95
	v_med3_f32 v229, v229, s62, v95
	v_med3_f32 v230, v230, s62, v95
	v_med3_f32 v231, v231, s62, v95
	v_med3_f32 v232, v232, s62, v95
	v_med3_f32 v233, v233, s62, v95
	v_med3_f32 v234, v234, s62, v95
	v_med3_f32 v235, v235, s62, v95
	v_med3_f32 v236, v236, s62, v95
	v_med3_f32 v237, v237, s62, v95
	v_med3_f32 v238, v238, s62, v95
	v_med3_f32 v239, v239, s62, v95
	v_med3_f32 v240, v240, s62, v95
	v_med3_f32 v241, v241, s62, v95
	v_mov_b32_e32 v242, 0
	v_mov_b32_e32 v243, 0
	v_mov_b32_e32 v244, 0
	v_mov_b32_e32 v245, 0
	v_cvt_pk_fp8_f32 v242, v226, v227
	v_cvt_pk_fp8_f32 v243, v230, v231
	v_cvt_pk_fp8_f32 v244, v234, v235
	v_cvt_pk_fp8_f32 v245, v238, v239
	v_cvt_pk_fp8_f32 v242, v228, v229 op_sel:[0,0,1]
	v_cvt_pk_fp8_f32 v243, v232, v233 op_sel:[0,0,1]
	v_cvt_pk_fp8_f32 v244, v236, v237 op_sel:[0,0,1]
	v_cvt_pk_fp8_f32 v245, v240, v241 op_sel:[0,0,1]
	s_nop 0
	global_store_dwordx4 v80, v[242:245], s[6:7]
	s_waitcnt vmcnt(12)
	v_mul_f32_e32 v176, 0x43000000, v176
	v_mul_f32_e32 v177, 0x43000000, v177
	v_mul_f32_e32 v178, 0x43000000, v178
	v_mul_f32_e32 v179, 0x43000000, v179
	ds_write_b128 v210, v[176:179]
	v_mul_f32_e32 v180, 0x43000000, v180
	v_mul_f32_e32 v181, 0x43000000, v181
	v_mul_f32_e32 v182, 0x43000000, v182
	v_mul_f32_e32 v183, 0x43000000, v183
	ds_write_b128 v210, v[180:183] offset:1024
	v_mul_f32_e32 v184, 0x43000000, v184
	v_mul_f32_e32 v185, 0x43000000, v185
	v_mul_f32_e32 v186, 0x43000000, v186
	v_mul_f32_e32 v187, 0x43000000, v187
	ds_write_b128 v210, v[184:187] offset:2048
	v_mul_f32_e32 v188, 0x43000000, v188
	v_mul_f32_e32 v189, 0x43000000, v189
	v_mul_f32_e32 v190, 0x43000000, v190
	v_mul_f32_e32 v191, 0x43000000, v191
	ds_write_b128 v210, v[188:191] offset:3072
	v_mul_f32_e32 v192, 0x43000000, v192
	v_mul_f32_e32 v193, 0x43000000, v193
	v_mul_f32_e32 v194, 0x43000000, v194
	v_mul_f32_e32 v195, 0x43000000, v195
	ds_write_b128 v210, v[192:195] offset:4096
	v_mul_f32_e32 v196, 0x43000000, v196
	v_mul_f32_e32 v197, 0x43000000, v197
	v_mul_f32_e32 v198, 0x43000000, v198
	v_mul_f32_e32 v199, 0x43000000, v199
	ds_write_b128 v210, v[196:199] offset:5120
	v_mul_f32_e32 v200, 0x43000000, v200
	v_mul_f32_e32 v201, 0x43000000, v201
	v_mul_f32_e32 v202, 0x43000000, v202
	v_mul_f32_e32 v203, 0x43000000, v203
	ds_write_b128 v210, v[200:203] offset:6144
	v_mul_f32_e32 v204, 0x43000000, v204
	v_mul_f32_e32 v205, 0x43000000, v205
	v_mul_f32_e32 v206, 0x43000000, v206
	v_mul_f32_e32 v207, 0x43000000, v207
	ds_write_b128 v210, v[204:207] offset:7168
	s_waitcnt lgkmcnt(0)
	s_barrier
; #define GAS __attribute__((address_space(1)))
; #define LAS __attribute__((address_space(3)))
; #define LDS_WAIT() asm volatile("s_waitcnt lgkmcnt(0)" ::: "memory")
;     const int pr = item >> 1, kb = 2 * (pr / nblk) + (item & 1), nb = pr % nblk, k0 = 64 * kb, n0 = 32 * nb;
;     const int nr = n0 + (lane & 31); const int sc = MAP == 1 ? src_col_in(nr) : nr;
;     float v[32];
; #pragma unroll
;     for (int i = 0; i < 32; ++i) v[i] = sc >= 0 ? W[(size_t)(k0 + 2 * i + (lane >> 5)) * Nsrc + sc] : 0.f;
; #pragma unroll
;     for (int i = 0; i < 32; ++i) { const int k = k0 + 2 * i + (lane >> 5); float x = v[i] * wscale; if (KS) x *= (k < ksplit ? ksA[k] : ksB[k - ksplit]); scr[(2 * i + (lane >> 5)) * 33 + (lane & 31)] = x; }
;     LDS_WAIT(); asm volatile("" ::: "memory");
;     const int c = lane & 7;
; #pragma unroll
;     for (int j = 0; j < 4; ++j) { const int n = (lane >> 3) + 8 * j; const LAS float* s = scr + (8 * c) * 33 + n;
;         const unsigned long long o = (unsigned long long)pg8::pk4_fp8(s[0 * 33], s[1 * 33], s[2 * 33], s[3 * 33]) | ((unsigned long long)pg8::pk4_fp8(s[4 * 33], s[5 * 33], s[6 * 33], s[7 * 33]) << 32);
;         *(GAS unsigned long long*)(WT + (size_t)(n0 + n) * K + k0 + 8 * c) = o; }
;     LDS_WAIT(); asm volatile("" ::: "memory");
; }
; __global__ void __launch_bounds__(NWAVES * 64, 2) hybrid_fwd(Args args) {
;     ...
;             p0_transpose_item_f8<false>(args.in[16] + (size_t)l * FF * DM, FF, DM, DM / 32, (unsigned char*)(ws + WS_WDN + l * SZ_WDN), 128.f, args.in[16], args.in[16], 0, scr, r, lane);
	s_add_u32 s8, s38, 0xc003000
	s_addc_u32 s9, s39, 0
	global_load_dwordx4 v[176:179], v75, s[8:9]
	s_add_u32 s8, s8, 0x8000
	s_addc_u32 s9, s9, 0
	global_load_dwordx4 v[180:183], v75, s[8:9]
	s_add_u32 s8, s8, 0x8000
	s_addc_u32 s9, s9, 0
	global_load_dwordx4 v[184:187], v75, s[8:9]
	s_add_u32 s8, s8, 0x8000
	s_addc_u32 s9, s9, 0
	global_load_dwordx4 v[188:191], v75, s[8:9]
	s_add_u32 s8, s8, 0x8000
	s_addc_u32 s9, s9, 0
	global_load_dwordx4 v[192:195], v75, s[8:9]
	s_add_u32 s8, s8, 0x8000
	s_addc_u32 s9, s9, 0
	global_load_dwordx4 v[196:199], v75, s[8:9]
	s_add_u32 s8, s8, 0x8000
	s_addc_u32 s9, s9, 0
	global_load_dwordx4 v[200:203], v75, s[8:9]
	s_add_u32 s8, s8, 0x8000
	s_addc_u32 s9, s9, 0
	global_load_dwordx4 v[204:207], v75, s[8:9]
	s_add_u32 s6, s40, 0x1003000
	s_addc_u32 s7, s41, 0
	ds_read_b32 v226, v212
	ds_read_b32 v227, v212 offset:512
	ds_read_b32 v228, v212 offset:1024
	ds_read_b32 v229, v212 offset:1536
	ds_read_b32 v230, v212 offset:2048
	ds_read_b32 v231, v212 offset:2560
	ds_read_b32 v232, v212 offset:3072
	ds_read_b32 v233, v212 offset:3584
	ds_read_b32 v234, v212 offset:4096
	ds_read_b32 v235, v212 offset:4608
	ds_read_b32 v236, v212 offset:5120
	ds_read_b32 v237, v212 offset:5632
	ds_read_b32 v238, v212 offset:6144
	ds_read_b32 v239, v212 offset:6656
	ds_read_b32 v240, v212 offset:7168
	ds_read_b32 v241, v212 offset:7680
	s_waitcnt lgkmcnt(0)
	v_max_f32_e32 v226, v226, v226
	v_max_f32_e32 v227, v227, v227
	v_max_f32_e32 v228, v228, v228
	v_max_f32_e32 v229, v229, v229
	v_max_f32_e32 v230, v230, v230
	v_max_f32_e32 v231, v231, v231
	v_max_f32_e32 v232, v232, v232
	v_max_f32_e32 v233, v233, v233
	v_max_f32_e32 v234, v234, v234
	v_max_f32_e32 v235, v235, v235
	v_max_f32_e32 v236, v236, v236
	v_max_f32_e32 v237, v237, v237
	v_max_f32_e32 v238, v238, v238
	v_max_f32_e32 v239, v239, v239
	v_max_f32_e32 v240, v240, v240
	v_max_f32_e32 v241, v241, v241
	v_med3_f32 v226, v226, s62, v95
	v_med3_f32 v227, v227, s62, v95
	v_med3_f32 v228, v228, s62, v95
	v_med3_f32 v229, v229, s62, v95
	v_med3_f32 v230, v230, s62, v95
	v_med3_f32 v231, v231, s62, v95
	v_med3_f32 v232, v232, s62, v95
	v_med3_f32 v233, v233, s62, v95
	v_med3_f32 v234, v234, s62, v95
	v_med3_f32 v235, v235, s62, v95
	v_med3_f32 v236, v236, s62, v95
	v_med3_f32 v237, v237, s62, v95
	v_med3_f32 v238, v238, s62, v95
	v_med3_f32 v239, v239, s62, v95
	v_med3_f32 v240, v240, s62, v95
	v_med3_f32 v241, v241, s62, v95
	v_mov_b32_e32 v242, 0
	v_mov_b32_e32 v243, 0
	v_mov_b32_e32 v244, 0
	v_mov_b32_e32 v245, 0
	v_cvt_pk_fp8_f32 v242, v226, v227
	v_cvt_pk_fp8_f32 v243, v230, v231
	v_cvt_pk_fp8_f32 v244, v234, v235
	v_cvt_pk_fp8_f32 v245, v238, v239
	v_cvt_pk_fp8_f32 v242, v228, v229 op_sel:[0,0,1]
	v_cvt_pk_fp8_f32 v243, v232, v233 op_sel:[0,0,1]
	v_cvt_pk_fp8_f32 v244, v236, v237 op_sel:[0,0,1]
	v_cvt_pk_fp8_f32 v245, v240, v241 op_sel:[0,0,1]
	s_nop 0
	global_store_dwordx4 v79, v[242:245], s[6:7]
	ds_read_b32 v226, v214
	ds_read_b32 v227, v214 offset:512
	ds_read_b32 v228, v214 offset:1024
	ds_read_b32 v229, v214 offset:1536
	ds_read_b32 v230, v214 offset:2048
	ds_read_b32 v231, v214 offset:2560
	ds_read_b32 v232, v214 offset:3072
	ds_read_b32 v233, v214 offset:3584
	ds_read_b32 v234, v214 offset:4096
	ds_read_b32 v235, v214 offset:4608
	ds_read_b32 v236, v214 offset:5120
	ds_read_b32 v237, v214 offset:5632
	ds_read_b32 v238, v214 offset:6144
	ds_read_b32 v239, v214 offset:6656
	ds_read_b32 v240, v214 offset:7168
	ds_read_b32 v241, v214 offset:7680
	s_waitcnt lgkmcnt(0)
	v_max_f32_e32 v226, v226, v226
	v_max_f32_e32 v227, v227, v227
	v_max_f32_e32 v228, v228, v228
	v_max_f32_e32 v229, v229, v229
	v_max_f32_e32 v230, v230, v230
	v_max_f32_e32 v231, v231, v231
	v_max_f32_e32 v232, v232, v232
	v_max_f32_e32 v233, v233, v233
	v_max_f32_e32 v234, v234, v234
	v_max_f32_e32 v235, v235, v235
	v_max_f32_e32 v236, v236, v236
	v_max_f32_e32 v237, v237, v237
	v_max_f32_e32 v238, v238, v238
	v_max_f32_e32 v239, v239, v239
	v_max_f32_e32 v240, v240, v240
	v_max_f32_e32 v241, v241, v241
	v_med3_f32 v226, v226, s62, v95
	v_med3_f32 v227, v227, s62, v95
	v_med3_f32 v228, v228, s62, v95
	v_med3_f32 v229, v229, s62, v95
	v_med3_f32 v230, v230, s62, v95
	v_med3_f32 v231, v231, s62, v95
	v_med3_f32 v232, v232, s62, v95
	v_med3_f32 v233, v233, s62, v95
	v_med3_f32 v234, v234, s62, v95
	v_med3_f32 v235, v235, s62, v95
	v_med3_f32 v236, v236, s62, v95
	v_med3_f32 v237, v237, s62, v95
	v_med3_f32 v238, v238, s62, v95
	v_med3_f32 v239, v239, s62, v95
	v_med3_f32 v240, v240, s62, v95
	v_med3_f32 v241, v241, s62, v95
	v_mov_b32_e32 v242, 0
	v_mov_b32_e32 v243, 0
	v_mov_b32_e32 v244, 0
	v_mov_b32_e32 v245, 0
	v_cvt_pk_fp8_f32 v242, v226, v227
	v_cvt_pk_fp8_f32 v243, v230, v231
	v_cvt_pk_fp8_f32 v244, v234, v235
	v_cvt_pk_fp8_f32 v245, v238, v239
	v_cvt_pk_fp8_f32 v242, v228, v229 op_sel:[0,0,1]
	v_cvt_pk_fp8_f32 v243, v232, v233 op_sel:[0,0,1]
	v_cvt_pk_fp8_f32 v244, v236, v237 op_sel:[0,0,1]
	v_cvt_pk_fp8_f32 v245, v240, v241 op_sel:[0,0,1]
	s_nop 0
	global_store_dwordx4 v80, v[242:245], s[6:7]
	s_waitcnt vmcnt(12)
	v_mul_f32_e32 v144, 0x43000000, v144
	v_mul_f32_e32 v145, 0x43000000, v145
	v_mul_f32_e32 v146, 0x43000000, v146
	v_mul_f32_e32 v147, 0x43000000, v147
	ds_write_b128 v209, v[144:147]
	v_mul_f32_e32 v148, 0x43000000, v148
	v_mul_f32_e32 v149, 0x43000000, v149
	v_mul_f32_e32 v150, 0x43000000, v150
	v_mul_f32_e32 v151, 0x43000000, v151
	ds_write_b128 v209, v[148:151] offset:1024
	v_mul_f32_e32 v152, 0x43000000, v152
	v_mul_f32_e32 v153, 0x43000000, v153
	v_mul_f32_e32 v154, 0x43000000, v154
	v_mul_f32_e32 v155, 0x43000000, v155
	ds_write_b128 v209, v[152:155] offset:2048
	v_mul_f32_e32 v156, 0x43000000, v156
	v_mul_f32_e32 v157, 0x43000000, v157
	v_mul_f32_e32 v158, 0x43000000, v158
	v_mul_f32_e32 v159, 0x43000000, v159
	ds_write_b128 v209, v[156:159] offset:3072
	v_mul_f32_e32 v160, 0x43000000, v160
	v_mul_f32_e32 v161, 0x43000000, v161
	v_mul_f32_e32 v162, 0x43000000, v162
	v_mul_f32_e32 v163, 0x43000000, v163
	ds_write_b128 v209, v[160:163] offset:4096
	v_mul_f32_e32 v164, 0x43000000, v164
	v_mul_f32_e32 v165, 0x43000000, v165
	v_mul_f32_e32 v166, 0x43000000, v166
	v_mul_f32_e32 v167, 0x43000000, v167
	ds_write_b128 v209, v[164:167] offset:5120
	v_mul_f32_e32 v168, 0x43000000, v168
	v_mul_f32_e32 v169, 0x43000000, v169
	v_mul_f32_e32 v170, 0x43000000, v170
	v_mul_f32_e32 v171, 0x43000000, v171
	ds_write_b128 v209, v[168:171] offset:6144
	v_mul_f32_e32 v172, 0x43000000, v172
	v_mul_f32_e32 v173, 0x43000000, v173
	v_mul_f32_e32 v174, 0x43000000, v174
	v_mul_f32_e32 v175, 0x43000000, v175
	ds_write_b128 v209, v[172:175] offset:7168
	s_waitcnt lgkmcnt(0)
	s_barrier
; #define GAS __attribute__((address_space(1)))
; #define LAS __attribute__((address_space(3)))
; #define LDS_WAIT() asm volatile("s_waitcnt lgkmcnt(0)" ::: "memory")
;     const int pr = item >> 1, kb = 2 * (pr / nblk) + (item & 1), nb = pr % nblk, k0 = 64 * kb, n0 = 32 * nb;
;     const int nr = n0 + (lane & 31); const int sc = MAP == 1 ? src_col_in(nr) : nr;
;     float v[32];
; #pragma unroll
;     for (int i = 0; i < 32; ++i) v[i] = sc >= 0 ? W[(size_t)(k0 + 2 * i + (lane >> 5)) * Nsrc + sc] : 0.f;
; #pragma unroll
;     for (int i = 0; i < 32; ++i) { const int k = k0 + 2 * i + (lane >> 5); float x = v[i] * wscale; if (KS) x *= (k < ksplit ? ksA[k] : ksB[k - ksplit]); scr[(2 * i + (lane >> 5)) * 33 + (lane & 31)] = x; }
;     LDS_WAIT(); asm volatile("" ::: "memory");
;     const int c = lane & 7;
; #pragma unroll
;     for (int j = 0; j < 4; ++j) { const int n = (lane >> 3) + 8 * j; const LAS float* s = scr + (8 * c) * 33 + n;
;         const unsigned long long o = (unsigned long long)pg8::pk4_fp8(s[0 * 33], s[1 * 33], s[2 * 33], s[3 * 33]) | ((unsigned long long)pg8::pk4_fp8(s[4 * 33], s[5 * 33], s[6 * 33], s[7 * 33]) << 32);
;         *(GAS unsigned long long*)(WT + (size_t)(n0 + n) * K + k0 + 8 * c) = o; }
;     LDS_WAIT(); asm volatile("" ::: "memory");
; }
; __global__ void __launch_bounds__(NWAVES * 64, 2) hybrid_fwd(Args args) {
;     ...
;             p0_transpose_item_f8<false>(args.in[16] + (size_t)l * FF * DM, FF, DM, DM / 32, (unsigned char*)(ws + WS_WDN + l * SZ_WDN), 128.f, args.in[16], args.in[16], 0, scr, r, lane);
	s_mov_b64 s[8:9], s[42:43]
	global_load_dwordx4 v[144:147], v75, s[8:9]
	s_add_u32 s8, s8, 0x8000
	s_addc_u32 s9, s9, 0
	global_load_dwordx4 v[148:151], v75, s[8:9]
	s_add_u32 s8, s8, 0x8000
	s_addc_u32 s9, s9, 0
	global_load_dwordx4 v[152:155], v75, s[8:9]
	s_add_u32 s8, s8, 0x8000
	s_addc_u32 s9, s9, 0
	global_load_dwordx4 v[156:159], v75, s[8:9]
	s_add_u32 s8, s8, 0x8000
	s_addc_u32 s9, s9, 0
	global_load_dwordx4 v[160:163], v75, s[8:9]
	s_add_u32 s8, s8, 0x8000
	s_addc_u32 s9, s9, 0
	global_load_dwordx4 v[164:167], v75, s[8:9]
	s_add_u32 s8, s8, 0x8000
	s_addc_u32 s9, s9, 0
	global_load_dwordx4 v[168:171], v75, s[8:9]
	s_add_u32 s8, s8, 0x8000
	s_addc_u32 s9, s9, 0
	global_load_dwordx4 v[172:175], v75, s[8:9]
	s_add_u32 s6, s40, 0x2003000
	s_addc_u32 s7, s41, 0
	ds_read_b32 v226, v211
	ds_read_b32 v227, v211 offset:512
	ds_read_b32 v228, v211 offset:1024
	ds_read_b32 v229, v211 offset:1536
	ds_read_b32 v230, v211 offset:2048
	ds_read_b32 v231, v211 offset:2560
	ds_read_b32 v232, v211 offset:3072
	ds_read_b32 v233, v211 offset:3584
	ds_read_b32 v234, v211 offset:4096
	ds_read_b32 v235, v211 offset:4608
	ds_read_b32 v236, v211 offset:5120
	ds_read_b32 v237, v211 offset:5632
	ds_read_b32 v238, v211 offset:6144
	ds_read_b32 v239, v211 offset:6656
	ds_read_b32 v240, v211 offset:7168
	ds_read_b32 v241, v211 offset:7680
	s_waitcnt lgkmcnt(0)
	v_max_f32_e32 v226, v226, v226
	v_max_f32_e32 v227, v227, v227
	v_max_f32_e32 v228, v228, v228
	v_max_f32_e32 v229, v229, v229
	v_max_f32_e32 v230, v230, v230
	v_max_f32_e32 v231, v231, v231
	v_max_f32_e32 v232, v232, v232
	v_max_f32_e32 v233, v233, v233
	v_max_f32_e32 v234, v234, v234
	v_max_f32_e32 v235, v235, v235
	v_max_f32_e32 v236, v236, v236
	v_max_f32_e32 v237, v237, v237
	v_max_f32_e32 v238, v238, v238
	v_max_f32_e32 v239, v239, v239
	v_max_f32_e32 v240, v240, v240
	v_max_f32_e32 v241, v241, v241
	v_med3_f32 v226, v226, s62, v95
	v_med3_f32 v227, v227, s62, v95
	v_med3_f32 v228, v228, s62, v95
	v_med3_f32 v229, v229, s62, v95
	v_med3_f32 v230, v230, s62, v95
	v_med3_f32 v231, v231, s62, v95
	v_med3_f32 v232, v232, s62, v95
	v_med3_f32 v233, v233, s62, v95
	v_med3_f32 v234, v234, s62, v95
	v_med3_f32 v235, v235, s62, v95
	v_med3_f32 v236, v236, s62, v95
	v_med3_f32 v237, v237, s62, v95
	v_med3_f32 v238, v238, s62, v95
	v_med3_f32 v239, v239, s62, v95
	v_med3_f32 v240, v240, s62, v95
	v_med3_f32 v241, v241, s62, v95
	v_mov_b32_e32 v242, 0
	v_mov_b32_e32 v243, 0
	v_mov_b32_e32 v244, 0
	v_mov_b32_e32 v245, 0
	v_cvt_pk_fp8_f32 v242, v226, v227
	v_cvt_pk_fp8_f32 v243, v230, v231
	v_cvt_pk_fp8_f32 v244, v234, v235
	v_cvt_pk_fp8_f32 v245, v238, v239
	v_cvt_pk_fp8_f32 v242, v228, v229 op_sel:[0,0,1]
	v_cvt_pk_fp8_f32 v243, v232, v233 op_sel:[0,0,1]
	v_cvt_pk_fp8_f32 v244, v236, v237 op_sel:[0,0,1]
	v_cvt_pk_fp8_f32 v245, v240, v241 op_sel:[0,0,1]
	s_nop 0
	global_store_dwordx4 v79, v[242:245], s[6:7]
	ds_read_b32 v226, v213
	ds_read_b32 v227, v213 offset:512
	ds_read_b32 v228, v213 offset:1024
	ds_read_b32 v229, v213 offset:1536
	ds_read_b32 v230, v213 offset:2048
	ds_read_b32 v231, v213 offset:2560
	ds_read_b32 v232, v213 offset:3072
	ds_read_b32 v233, v213 offset:3584
	ds_read_b32 v234, v213 offset:4096
	ds_read_b32 v235, v213 offset:4608
	ds_read_b32 v236, v213 offset:5120
	ds_read_b32 v237, v213 offset:5632
	ds_read_b32 v238, v213 offset:6144
	ds_read_b32 v239, v213 offset:6656
	ds_read_b32 v240, v213 offset:7168
	ds_read_b32 v241, v213 offset:7680
	s_waitcnt lgkmcnt(0)
	v_max_f32_e32 v226, v226, v226
	v_max_f32_e32 v227, v227, v227
	v_max_f32_e32 v228, v228, v228
	v_max_f32_e32 v229, v229, v229
	v_max_f32_e32 v230, v230, v230
	v_max_f32_e32 v231, v231, v231
	v_max_f32_e32 v232, v232, v232
	v_max_f32_e32 v233, v233, v233
	v_max_f32_e32 v234, v234, v234
	v_max_f32_e32 v235, v235, v235
	v_max_f32_e32 v236, v236, v236
	v_max_f32_e32 v237, v237, v237
	v_max_f32_e32 v238, v238, v238
	v_max_f32_e32 v239, v239, v239
	v_max_f32_e32 v240, v240, v240
	v_max_f32_e32 v241, v241, v241
	v_med3_f32 v226, v226, s62, v95
	v_med3_f32 v227, v227, s62, v95
	v_med3_f32 v228, v228, s62, v95
	v_med3_f32 v229, v229, s62, v95
	v_med3_f32 v230, v230, s62, v95
	v_med3_f32 v231, v231, s62, v95
	v_med3_f32 v232, v232, s62, v95
	v_med3_f32 v233, v233, s62, v95
	v_med3_f32 v234, v234, s62, v95
	v_med3_f32 v235, v235, s62, v95
	v_med3_f32 v236, v236, s62, v95
	v_med3_f32 v237, v237, s62, v95
	v_med3_f32 v238, v238, s62, v95
	v_med3_f32 v239, v239, s62, v95
	v_med3_f32 v240, v240, s62, v95
	v_med3_f32 v241, v241, s62, v95
	v_mov_b32_e32 v242, 0
	v_mov_b32_e32 v243, 0
	v_mov_b32_e32 v244, 0
	v_mov_b32_e32 v245, 0
	v_cvt_pk_fp8_f32 v242, v226, v227
	v_cvt_pk_fp8_f32 v243, v230, v231
	v_cvt_pk_fp8_f32 v244, v234, v235
	v_cvt_pk_fp8_f32 v245, v238, v239
	v_cvt_pk_fp8_f32 v242, v228, v229 op_sel:[0,0,1]
	v_cvt_pk_fp8_f32 v243, v232, v233 op_sel:[0,0,1]
	v_cvt_pk_fp8_f32 v244, v236, v237 op_sel:[0,0,1]
	v_cvt_pk_fp8_f32 v245, v240, v241 op_sel:[0,0,1]
	s_nop 0
	global_store_dwordx4 v80, v[242:245], s[6:7]
	s_branch .Lco3_hop_skip
.Lco3_hop_192:
	s_branch .LBB0_192
; #define GAS __attribute__((address_space(1)))
; #define LAS __attribute__((address_space(3)))
; #define LDS_WAIT() asm volatile("s_waitcnt lgkmcnt(0)" ::: "memory")
;     const int pr = item >> 1, kb = 2 * (pr / nblk) + (item & 1), nb = pr % nblk, k0 = 64 * kb, n0 = 32 * nb;
;     const int nr = n0 + (lane & 31); const int sc = MAP == 1 ? src_col_in(nr) : nr;
;     float v[32];
; #pragma unroll
;     for (int i = 0; i < 32; ++i) v[i] = sc >= 0 ? W[(size_t)(k0 + 2 * i + (lane >> 5)) * Nsrc + sc] : 0.f;
; #pragma unroll
;     for (int i = 0; i < 32; ++i) { const int k = k0 + 2 * i + (lane >> 5); float x = v[i] * wscale; if (KS) x *= (k < ksplit ? ksA[k] : ksB[k - ksplit]); scr[(2 * i + (lane >> 5)) * 33 + (lane & 31)] = x; }
;     LDS_WAIT(); asm volatile("" ::: "memory");
;     const int c = lane & 7;
; #pragma unroll
;     for (int j = 0; j < 4; ++j) { const int n = (lane >> 3) + 8 * j; const LAS float* s = scr + (8 * c) * 33 + n;
;         const unsigned long long o = (unsigned long long)pg8::pk4_fp8(s[0 * 33], s[1 * 33], s[2 * 33], s[3 * 33]) | ((unsigned long long)pg8::pk4_fp8(s[4 * 33], s[5 * 33], s[6 * 33], s[7 * 33]) << 32);
;         *(GAS unsigned long long*)(WT + (size_t)(n0 + n) * K + k0 + 8 * c) = o; }
;     LDS_WAIT(); asm volatile("" ::: "memory");
; }
; __global__ void __launch_bounds__(NWAVES * 64, 2) hybrid_fwd(Args args) {
;     ...
;             p0_transpose_item_f8<false>(args.in[16] + (size_t)l * FF * DM, FF, DM, DM / 32, (unsigned char*)(ws + WS_WDN + l * SZ_WDN), 128.f, args.in[16], args.in[16], 0, scr, r, lane);
.Lco3_hop_skip:
	s_waitcnt vmcnt(12)
	v_mul_f32_e32 v176, 0x43000000, v176
	v_mul_f32_e32 v177, 0x43000000, v177
	v_mul_f32_e32 v178, 0x43000000, v178
	v_mul_f32_e32 v179, 0x43000000, v179
	ds_write_b128 v210, v[176:179]
	v_mul_f32_e32 v180, 0x43000000, v180
	v_mul_f32_e32 v181, 0x43000000, v181
	v_mul_f32_e32 v182, 0x43000000, v182
	v_mul_f32_e32 v183, 0x43000000, v183
	ds_write_b128 v210, v[180:183] offset:1024
	v_mul_f32_e32 v184, 0x43000000, v184
	v_mul_f32_e32 v185, 0x43000000, v185
	v_mul_f32_e32 v186, 0x43000000, v186
	v_mul_f32_e32 v187, 0x43000000, v187
	ds_write_b128 v210, v[184:187] offset:2048
	v_mul_f32_e32 v188, 0x43000000, v188
	v_mul_f32_e32 v189, 0x43000000, v189
	v_mul_f32_e32 v190, 0x43000000, v190
	v_mul_f32_e32 v191, 0x43000000, v191
	ds_write_b128 v210, v[188:191] offset:3072
	v_mul_f32_e32 v192, 0x43000000, v192
	v_mul_f32_e32 v193, 0x43000000, v193
	v_mul_f32_e32 v194, 0x43000000, v194
	v_mul_f32_e32 v195, 0x43000000, v195
	ds_write_b128 v210, v[192:195] offset:4096
	v_mul_f32_e32 v196, 0x43000000, v196
	v_mul_f32_e32 v197, 0x43000000, v197
	v_mul_f32_e32 v198, 0x43000000, v198
	v_mul_f32_e32 v199, 0x43000000, v199
	ds_write_b128 v210, v[196:199] offset:5120
	v_mul_f32_e32 v200, 0x43000000, v200
	v_mul_f32_e32 v201, 0x43000000, v201
	v_mul_f32_e32 v202, 0x43000000, v202
	v_mul_f32_e32 v203, 0x43000000, v203
	ds_write_b128 v210, v[200:203] offset:6144
	v_mul_f32_e32 v204, 0x43000000, v204
	v_mul_f32_e32 v205, 0x43000000, v205
	v_mul_f32_e32 v206, 0x43000000, v206
	v_mul_f32_e32 v207, 0x43000000, v207
	ds_write_b128 v210, v[204:207] offset:7168
	s_waitcnt lgkmcnt(0)
	s_barrier
	s_add_u32 s8, s42, 0x1000
	s_addc_u32 s9, s43, 0
	global_load_dwordx4 v[176:179], v75, s[8:9]
	s_add_u32 s8, s8, 0x8000
	s_addc_u32 s9, s9, 0
	global_load_dwordx4 v[180:183], v75, s[8:9]
	s_add_u32 s8, s8, 0x8000
	s_addc_u32 s9, s9, 0
	global_load_dwordx4 v[184:187], v75, s[8:9]
	s_add_u32 s8, s8, 0x8000
	s_addc_u32 s9, s9, 0
	global_load_dwordx4 v[188:191], v75, s[8:9]
	s_add_u32 s8, s8, 0x8000
	s_addc_u32 s9, s9, 0
	global_load_dwordx4 v[192:195], v75, s[8:9]
	s_add_u32 s8, s8, 0x8000
	s_addc_u32 s9, s9, 0
	global_load_dwordx4 v[196:199], v75, s[8:9]
	s_add_u32 s8, s8, 0x8000
	s_addc_u32 s9, s9, 0
	global_load_dwordx4 v[200:203], v75, s[8:9]
	s_add_u32 s8, s8, 0x8000
	s_addc_u32 s9, s9, 0
	global_load_dwordx4 v[204:207], v75, s[8:9]
	s_add_u32 s6, s40, 0x3003000
	s_addc_u32 s7, s41, 0
	ds_read_b32 v226, v212
	ds_read_b32 v227, v212 offset:512
	ds_read_b32 v228, v212 offset:1024
	ds_read_b32 v229, v212 offset:1536
	ds_read_b32 v230, v212 offset:2048
	ds_read_b32 v231, v212 offset:2560
	ds_read_b32 v232, v212 offset:3072
	ds_read_b32 v233, v212 offset:3584
	ds_read_b32 v234, v212 offset:4096
	ds_read_b32 v235, v212 offset:4608
	ds_read_b32 v236, v212 offset:5120
	ds_read_b32 v237, v212 offset:5632
	ds_read_b32 v238, v212 offset:6144
	ds_read_b32 v239, v212 offset:6656
	ds_read_b32 v240, v212 offset:7168
	ds_read_b32 v241, v212 offset:7680
	s_waitcnt lgkmcnt(0)
	v_max_f32_e32 v226, v226, v226
	v_max_f32_e32 v227, v227, v227
	v_max_f32_e32 v228, v228, v228
	v_max_f32_e32 v229, v229, v229
	v_max_f32_e32 v230, v230, v230
	v_max_f32_e32 v231, v231, v231
	v_max_f32_e32 v232, v232, v232
	v_max_f32_e32 v233, v233, v233
	v_max_f32_e32 v234, v234, v234
	v_max_f32_e32 v235, v235, v235
	v_max_f32_e32 v236, v236, v236
	v_max_f32_e32 v237, v237, v237
	v_max_f32_e32 v238, v238, v238
	v_max_f32_e32 v239, v239, v239
	v_max_f32_e32 v240, v240, v240
	v_max_f32_e32 v241, v241, v241
	v_med3_f32 v226, v226, s62, v95
	v_med3_f32 v227, v227, s62, v95
	v_med3_f32 v228, v228, s62, v95
	v_med3_f32 v229, v229, s62, v95
	v_med3_f32 v230, v230, s62, v95
	v_med3_f32 v231, v231, s62, v95
	v_med3_f32 v232, v232, s62, v95
	v_med3_f32 v233, v233, s62, v95
	v_med3_f32 v234, v234, s62, v95
	v_med3_f32 v235, v235, s62, v95
	v_med3_f32 v236, v236, s62, v95
	v_med3_f32 v237, v237, s62, v95
	v_med3_f32 v238, v238, s62, v95
	v_med3_f32 v239, v239, s62, v95
	v_med3_f32 v240, v240, s62, v95
	v_med3_f32 v241, v241, s62, v95
	v_mov_b32_e32 v242, 0
	v_mov_b32_e32 v243, 0
	v_mov_b32_e32 v244, 0
	v_mov_b32_e32 v245, 0
	v_cvt_pk_fp8_f32 v242, v226, v227
	v_cvt_pk_fp8_f32 v243, v230, v231
	v_cvt_pk_fp8_f32 v244, v234, v235
	v_cvt_pk_fp8_f32 v245, v238, v239
	v_cvt_pk_fp8_f32 v242, v228, v229 op_sel:[0,0,1]
	v_cvt_pk_fp8_f32 v243, v232, v233 op_sel:[0,0,1]
	v_cvt_pk_fp8_f32 v244, v236, v237 op_sel:[0,0,1]
	v_cvt_pk_fp8_f32 v245, v240, v241 op_sel:[0,0,1]
	s_nop 0
	global_store_dwordx4 v79, v[242:245], s[6:7]
	ds_read_b32 v226, v214
	ds_read_b32 v227, v214 offset:512
	ds_read_b32 v228, v214 offset:1024
	ds_read_b32 v229, v214 offset:1536
	ds_read_b32 v230, v214 offset:2048
	ds_read_b32 v231, v214 offset:2560
	ds_read_b32 v232, v214 offset:3072
	ds_read_b32 v233, v214 offset:3584
	ds_read_b32 v234, v214 offset:4096
	ds_read_b32 v235, v214 offset:4608
	ds_read_b32 v236, v214 offset:5120
	ds_read_b32 v237, v214 offset:5632
	ds_read_b32 v238, v214 offset:6144
	ds_read_b32 v239, v214 offset:6656
	ds_read_b32 v240, v214 offset:7168
	ds_read_b32 v241, v214 offset:7680
	s_waitcnt lgkmcnt(0)
; #define GAS __attribute__((address_space(1)))
; #define LAS __attribute__((address_space(3)))
; #define LDS_WAIT() asm volatile("s_waitcnt lgkmcnt(0)" ::: "memory")
;     const int pr = item >> 1, kb = 2 * (pr / nblk) + (item & 1), nb = pr % nblk, k0 = 64 * kb, n0 = 32 * nb;
;     const int nr = n0 + (lane & 31); const int sc = MAP == 1 ? src_col_in(nr) : nr;
;     float v[32];
; #pragma unroll
;     for (int i = 0; i < 32; ++i) v[i] = sc >= 0 ? W[(size_t)(k0 + 2 * i + (lane >> 5)) * Nsrc + sc] : 0.f;
; #pragma unroll
;     for (int i = 0; i < 32; ++i) { const int k = k0 + 2 * i + (lane >> 5); float x = v[i] * wscale; if (KS) x *= (k < ksplit ? ksA[k] : ksB[k - ksplit]); scr[(2 * i + (lane >> 5)) * 33 + (lane & 31)] = x; }
;     LDS_WAIT(); asm volatile("" ::: "memory");
;     const int c = lane & 7;
; #pragma unroll
;     for (int j = 0; j < 4; ++j) { const int n = (lane >> 3) + 8 * j; const LAS float* s = scr + (8 * c) * 33 + n;
;         const unsigned long long o = (unsigned long long)pg8::pk4_fp8(s[0 * 33], s[1 * 33], s[2 * 33], s[3 * 33]) | ((unsigned long long)pg8::pk4_fp8(s[4 * 33], s[5 * 33], s[6 * 33], s[7 * 33]) << 32);
;         *(GAS unsigned long long*)(WT + (size_t)(n0 + n) * K + k0 + 8 * c) = o; }
;     LDS_WAIT(); asm volatile("" ::: "memory");
; }
; __global__ void __launch_bounds__(NWAVES * 64, 2) hybrid_fwd(Args args) {
;     ...
;             p0_transpose_item_f8<false>(args.in[16] + (size_t)l * FF * DM, FF, DM, DM / 32, (unsigned char*)(ws + WS_WDN + l * SZ_WDN), 128.f, args.in[16], args.in[16], 0, scr, r, lane);
	v_max_f32_e32 v226, v226, v226
	v_max_f32_e32 v227, v227, v227
	v_max_f32_e32 v228, v228, v228
	v_max_f32_e32 v229, v229, v229
	v_max_f32_e32 v230, v230, v230
	v_max_f32_e32 v231, v231, v231
	v_max_f32_e32 v232, v232, v232
	v_max_f32_e32 v233, v233, v233
	v_max_f32_e32 v234, v234, v234
	v_max_f32_e32 v235, v235, v235
	v_max_f32_e32 v236, v236, v236
	v_max_f32_e32 v237, v237, v237
	v_max_f32_e32 v238, v238, v238
	v_max_f32_e32 v239, v239, v239
	v_max_f32_e32 v240, v240, v240
	v_max_f32_e32 v241, v241, v241
	v_med3_f32 v226, v226, s62, v95
	v_med3_f32 v227, v227, s62, v95
	v_med3_f32 v228, v228, s62, v95
	v_med3_f32 v229, v229, s62, v95
	v_med3_f32 v230, v230, s62, v95
	v_med3_f32 v231, v231, s62, v95
	v_med3_f32 v232, v232, s62, v95
	v_med3_f32 v233, v233, s62, v95
	v_med3_f32 v234, v234, s62, v95
	v_med3_f32 v235, v235, s62, v95
	v_med3_f32 v236, v236, s62, v95
	v_med3_f32 v237, v237, s62, v95
	v_med3_f32 v238, v238, s62, v95
	v_med3_f32 v239, v239, s62, v95
	v_med3_f32 v240, v240, s62, v95
	v_med3_f32 v241, v241, s62, v95
	v_mov_b32_e32 v242, 0
	v_mov_b32_e32 v243, 0
	v_mov_b32_e32 v244, 0
	v_mov_b32_e32 v245, 0
	v_cvt_pk_fp8_f32 v242, v226, v227
	v_cvt_pk_fp8_f32 v243, v230, v231
	v_cvt_pk_fp8_f32 v244, v234, v235
	v_cvt_pk_fp8_f32 v245, v238, v239
	v_cvt_pk_fp8_f32 v242, v228, v229 op_sel:[0,0,1]
	v_cvt_pk_fp8_f32 v243, v232, v233 op_sel:[0,0,1]
	v_cvt_pk_fp8_f32 v244, v236, v237 op_sel:[0,0,1]
	v_cvt_pk_fp8_f32 v245, v240, v241 op_sel:[0,0,1]
	s_nop 0
	global_store_dwordx4 v80, v[242:245], s[6:7]
	s_waitcnt vmcnt(12)
	v_mul_f32_e32 v144, 0x43000000, v144
	v_mul_f32_e32 v145, 0x43000000, v145
	v_mul_f32_e32 v146, 0x43000000, v146
	v_mul_f32_e32 v147, 0x43000000, v147
	ds_write_b128 v209, v[144:147]
	v_mul_f32_e32 v148, 0x43000000, v148
	v_mul_f32_e32 v149, 0x43000000, v149
	v_mul_f32_e32 v150, 0x43000000, v150
	v_mul_f32_e32 v151, 0x43000000, v151
	ds_write_b128 v209, v[148:151] offset:1024
	v_mul_f32_e32 v152, 0x43000000, v152
	v_mul_f32_e32 v153, 0x43000000, v153
	v_mul_f32_e32 v154, 0x43000000, v154
	v_mul_f32_e32 v155, 0x43000000, v155
	ds_write_b128 v209, v[152:155] offset:2048
	v_mul_f32_e32 v156, 0x43000000, v156
	v_mul_f32_e32 v157, 0x43000000, v157
	v_mul_f32_e32 v158, 0x43000000, v158
	v_mul_f32_e32 v159, 0x43000000, v159
	ds_write_b128 v209, v[156:159] offset:3072
	v_mul_f32_e32 v160, 0x43000000, v160
	v_mul_f32_e32 v161, 0x43000000, v161
	v_mul_f32_e32 v162, 0x43000000, v162
	v_mul_f32_e32 v163, 0x43000000, v163
	ds_write_b128 v209, v[160:163] offset:4096
	v_mul_f32_e32 v164, 0x43000000, v164
	v_mul_f32_e32 v165, 0x43000000, v165
	v_mul_f32_e32 v166, 0x43000000, v166
	v_mul_f32_e32 v167, 0x43000000, v167
	ds_write_b128 v209, v[164:167] offset:5120
	v_mul_f32_e32 v168, 0x43000000, v168
	v_mul_f32_e32 v169, 0x43000000, v169
	v_mul_f32_e32 v170, 0x43000000, v170
	v_mul_f32_e32 v171, 0x43000000, v171
	ds_write_b128 v209, v[168:171] offset:6144
	v_mul_f32_e32 v172, 0x43000000, v172
	v_mul_f32_e32 v173, 0x43000000, v173
	v_mul_f32_e32 v174, 0x43000000, v174
	v_mul_f32_e32 v175, 0x43000000, v175
	ds_write_b128 v209, v[172:175] offset:7168
	s_waitcnt lgkmcnt(0)
	s_barrier
	s_add_u32 s8, s42, 0x2000
	s_addc_u32 s9, s43, 0
	global_load_dwordx4 v[144:147], v75, s[8:9]
	s_add_u32 s8, s8, 0x8000
	s_addc_u32 s9, s9, 0
	global_load_dwordx4 v[148:151], v75, s[8:9]
	s_add_u32 s8, s8, 0x8000
	s_addc_u32 s9, s9, 0
	global_load_dwordx4 v[152:155], v75, s[8:9]
	s_add_u32 s8, s8, 0x8000
	s_addc_u32 s9, s9, 0
	global_load_dwordx4 v[156:159], v75, s[8:9]
	s_add_u32 s8, s8, 0x8000
	s_addc_u32 s9, s9, 0
	global_load_dwordx4 v[160:163], v75, s[8:9]
	s_add_u32 s8, s8, 0x8000
	s_addc_u32 s9, s9, 0
	global_load_dwordx4 v[164:167], v75, s[8:9]
	s_add_u32 s8, s8, 0x8000
	s_addc_u32 s9, s9, 0
	global_load_dwordx4 v[168:171], v75, s[8:9]
	s_add_u32 s8, s8, 0x8000
	s_addc_u32 s9, s9, 0
	global_load_dwordx4 v[172:175], v75, s[8:9]
	s_mov_b64 s[6:7], s[44:45]
	ds_read_b32 v226, v211
	ds_read_b32 v227, v211 offset:512
	ds_read_b32 v228, v211 offset:1024
	ds_read_b32 v229, v211 offset:1536
	ds_read_b32 v230, v211 offset:2048
	ds_read_b32 v231, v211 offset:2560
	ds_read_b32 v232, v211 offset:3072
	ds_read_b32 v233, v211 offset:3584
	ds_read_b32 v234, v211 offset:4096
	ds_read_b32 v235, v211 offset:4608
	ds_read_b32 v236, v211 offset:5120
	ds_read_b32 v237, v211 offset:5632
	ds_read_b32 v238, v211 offset:6144
	ds_read_b32 v239, v211 offset:6656
	ds_read_b32 v240, v211 offset:7168
	ds_read_b32 v241, v211 offset:7680
	s_waitcnt lgkmcnt(0)
	v_max_f32_e32 v226, v226, v226
	v_max_f32_e32 v227, v227, v227
	v_max_f32_e32 v228, v228, v228
	v_max_f32_e32 v229, v229, v229
	v_max_f32_e32 v230, v230, v230
	v_max_f32_e32 v231, v231, v231
	v_max_f32_e32 v232, v232, v232
	v_max_f32_e32 v233, v233, v233
	v_max_f32_e32 v234, v234, v234
	v_max_f32_e32 v235, v235, v235
	v_max_f32_e32 v236, v236, v236
	v_max_f32_e32 v237, v237, v237
	v_max_f32_e32 v238, v238, v238
	v_max_f32_e32 v239, v239, v239
	v_max_f32_e32 v240, v240, v240
	v_max_f32_e32 v241, v241, v241
	v_med3_f32 v226, v226, s62, v95
	v_med3_f32 v227, v227, s62, v95
	v_med3_f32 v228, v228, s62, v95
	v_med3_f32 v229, v229, s62, v95
	v_med3_f32 v230, v230, s62, v95
	v_med3_f32 v231, v231, s62, v95
	v_med3_f32 v232, v232, s62, v95
	v_med3_f32 v233, v233, s62, v95
	v_med3_f32 v234, v234, s62, v95
	v_med3_f32 v235, v235, s62, v95
	v_med3_f32 v236, v236, s62, v95
	v_med3_f32 v237, v237, s62, v95
	v_med3_f32 v238, v238, s62, v95
	v_med3_f32 v239, v239, s62, v95
	v_med3_f32 v240, v240, s62, v95
	v_med3_f32 v241, v241, s62, v95
	v_mov_b32_e32 v242, 0
	v_mov_b32_e32 v243, 0
	v_mov_b32_e32 v244, 0
	v_mov_b32_e32 v245, 0
	v_cvt_pk_fp8_f32 v242, v226, v227
	v_cvt_pk_fp8_f32 v243, v230, v231
	v_cvt_pk_fp8_f32 v244, v234, v235
	v_cvt_pk_fp8_f32 v245, v238, v239
	v_cvt_pk_fp8_f32 v242, v228, v229 op_sel:[0,0,1]
	v_cvt_pk_fp8_f32 v243, v232, v233 op_sel:[0,0,1]
	v_cvt_pk_fp8_f32 v244, v236, v237 op_sel:[0,0,1]
	v_cvt_pk_fp8_f32 v245, v240, v241 op_sel:[0,0,1]
	s_nop 0
	global_store_dwordx4 v79, v[242:245], s[6:7]
	ds_read_b32 v226, v213
	ds_read_b32 v227, v213 offset:512
	ds_read_b32 v228, v213 offset:1024
	ds_read_b32 v229, v213 offset:1536
	ds_read_b32 v230, v213 offset:2048
	ds_read_b32 v231, v213 offset:2560
	ds_read_b32 v232, v213 offset:3072
	ds_read_b32 v233, v213 offset:3584
	ds_read_b32 v234, v213 offset:4096
	ds_read_b32 v235, v213 offset:4608
	ds_read_b32 v236, v213 offset:5120
	ds_read_b32 v237, v213 offset:5632
	ds_read_b32 v238, v213 offset:6144
	ds_read_b32 v239, v213 offset:6656
	ds_read_b32 v240, v213 offset:7168
	ds_read_b32 v241, v213 offset:7680
	s_waitcnt lgkmcnt(0)
; #define GAS __attribute__((address_space(1)))
; #define LAS __attribute__((address_space(3)))
; #define LDS_WAIT() asm volatile("s_waitcnt lgkmcnt(0)" ::: "memory")
;     const int pr = item >> 1, kb = 2 * (pr / nblk) + (item & 1), nb = pr % nblk, k0 = 64 * kb, n0 = 32 * nb;
;     const int nr = n0 + (lane & 31); const int sc = MAP == 1 ? src_col_in(nr) : nr;
;     float v[32];
; #pragma unroll
;     for (int i = 0; i < 32; ++i) v[i] = sc >= 0 ? W[(size_t)(k0 + 2 * i + (lane >> 5)) * Nsrc + sc] : 0.f;
; #pragma unroll
;     for (int i = 0; i < 32; ++i) { const int k = k0 + 2 * i + (lane >> 5); float x = v[i] * wscale; if (KS) x *= (k < ksplit ? ksA[k] : ksB[k - ksplit]); scr[(2 * i + (lane >> 5)) * 33 + (lane & 31)] = x; }
;     LDS_WAIT(); asm volatile("" ::: "memory");
;     const int c = lane & 7;
; #pragma unroll
;     for (int j = 0; j < 4; ++j) { const int n = (lane >> 3) + 8 * j; const LAS float* s = scr + (8 * c) * 33 + n;
;         const unsigned long long o = (unsigned long long)pg8::pk4_fp8(s[0 * 33], s[1 * 33], s[2 * 33], s[3 * 33]) | ((unsigned long long)pg8::pk4_fp8(s[4 * 33], s[5 * 33], s[6 * 33], s[7 * 33]) << 32);
;         *(GAS unsigned long long*)(WT + (size_t)(n0 + n) * K + k0 + 8 * c) = o; }
;     LDS_WAIT(); asm volatile("" ::: "memory");
; }
; __global__ void __launch_bounds__(NWAVES * 64, 2) hybrid_fwd(Args args) {
;     ...
;             p0_transpose_item_f8<false>(args.in[16] + (size_t)l * FF * DM, FF, DM, DM / 32, (unsigned char*)(ws + WS_WDN + l * SZ_WDN), 128.f, args.in[16], args.in[16], 0, scr, r, lane);
	v_max_f32_e32 v226, v226, v226
	v_max_f32_e32 v227, v227, v227
	v_max_f32_e32 v228, v228, v228
	v_max_f32_e32 v229, v229, v229
	v_max_f32_e32 v230, v230, v230
	v_max_f32_e32 v231, v231, v231
	v_max_f32_e32 v232, v232, v232
	v_max_f32_e32 v233, v233, v233
	v_max_f32_e32 v234, v234, v234
	v_max_f32_e32 v235, v235, v235
	v_max_f32_e32 v236, v236, v236
	v_max_f32_e32 v237, v237, v237
	v_max_f32_e32 v238, v238, v238
	v_max_f32_e32 v239, v239, v239
	v_max_f32_e32 v240, v240, v240
	v_max_f32_e32 v241, v241, v241
	v_med3_f32 v226, v226, s62, v95
	v_med3_f32 v227, v227, s62, v95
	v_med3_f32 v228, v228, s62, v95
	v_med3_f32 v229, v229, s62, v95
	v_med3_f32 v230, v230, s62, v95
	v_med3_f32 v231, v231, s62, v95
	v_med3_f32 v232, v232, s62, v95
	v_med3_f32 v233, v233, s62, v95
	v_med3_f32 v234, v234, s62, v95
	v_med3_f32 v235, v235, s62, v95
	v_med3_f32 v236, v236, s62, v95
	v_med3_f32 v237, v237, s62, v95
	v_med3_f32 v238, v238, s62, v95
	v_med3_f32 v239, v239, s62, v95
	v_med3_f32 v240, v240, s62, v95
	v_med3_f32 v241, v241, s62, v95
	v_mov_b32_e32 v242, 0
	v_mov_b32_e32 v243, 0
	v_mov_b32_e32 v244, 0
	v_mov_b32_e32 v245, 0
	v_cvt_pk_fp8_f32 v242, v226, v227
	v_cvt_pk_fp8_f32 v243, v230, v231
	v_cvt_pk_fp8_f32 v244, v234, v235
	v_cvt_pk_fp8_f32 v245, v238, v239
	v_cvt_pk_fp8_f32 v242, v228, v229 op_sel:[0,0,1]
	v_cvt_pk_fp8_f32 v243, v232, v233 op_sel:[0,0,1]
	v_cvt_pk_fp8_f32 v244, v236, v237 op_sel:[0,0,1]
	v_cvt_pk_fp8_f32 v245, v240, v241 op_sel:[0,0,1]
	s_nop 0
	global_store_dwordx4 v80, v[242:245], s[6:7]
	s_waitcnt vmcnt(12)
	v_mul_f32_e32 v176, 0x43000000, v176
	v_mul_f32_e32 v177, 0x43000000, v177
	v_mul_f32_e32 v178, 0x43000000, v178
	v_mul_f32_e32 v179, 0x43000000, v179
	ds_write_b128 v210, v[176:179]
	v_mul_f32_e32 v180, 0x43000000, v180
	v_mul_f32_e32 v181, 0x43000000, v181
	v_mul_f32_e32 v182, 0x43000000, v182
	v_mul_f32_e32 v183, 0x43000000, v183
	ds_write_b128 v210, v[180:183] offset:1024
	v_mul_f32_e32 v184, 0x43000000, v184
	v_mul_f32_e32 v185, 0x43000000, v185
	v_mul_f32_e32 v186, 0x43000000, v186
	v_mul_f32_e32 v187, 0x43000000, v187
	ds_write_b128 v210, v[184:187] offset:2048
	v_mul_f32_e32 v188, 0x43000000, v188
	v_mul_f32_e32 v189, 0x43000000, v189
	v_mul_f32_e32 v190, 0x43000000, v190
	v_mul_f32_e32 v191, 0x43000000, v191
	ds_write_b128 v210, v[188:191] offset:3072
	v_mul_f32_e32 v192, 0x43000000, v192
	v_mul_f32_e32 v193, 0x43000000, v193
	v_mul_f32_e32 v194, 0x43000000, v194
	v_mul_f32_e32 v195, 0x43000000, v195
	ds_write_b128 v210, v[192:195] offset:4096
	v_mul_f32_e32 v196, 0x43000000, v196
	v_mul_f32_e32 v197, 0x43000000, v197
	v_mul_f32_e32 v198, 0x43000000, v198
	v_mul_f32_e32 v199, 0x43000000, v199
	ds_write_b128 v210, v[196:199] offset:5120
	v_mul_f32_e32 v200, 0x43000000, v200
	v_mul_f32_e32 v201, 0x43000000, v201
	v_mul_f32_e32 v202, 0x43000000, v202
	v_mul_f32_e32 v203, 0x43000000, v203
	ds_write_b128 v210, v[200:203] offset:6144
	v_mul_f32_e32 v204, 0x43000000, v204
	v_mul_f32_e32 v205, 0x43000000, v205
	v_mul_f32_e32 v206, 0x43000000, v206
	v_mul_f32_e32 v207, 0x43000000, v207
	ds_write_b128 v210, v[204:207] offset:7168
	s_waitcnt lgkmcnt(0)
	s_barrier
	s_add_u32 s8, s42, 0x3000
	s_addc_u32 s9, s43, 0
	global_load_dwordx4 v[176:179], v75, s[8:9]
	s_add_u32 s8, s8, 0x8000
	s_addc_u32 s9, s9, 0
	global_load_dwordx4 v[180:183], v75, s[8:9]
	s_add_u32 s8, s8, 0x8000
	s_addc_u32 s9, s9, 0
	global_load_dwordx4 v[184:187], v75, s[8:9]
	s_add_u32 s8, s8, 0x8000
	s_addc_u32 s9, s9, 0
	global_load_dwordx4 v[188:191], v75, s[8:9]
	s_add_u32 s8, s8, 0x8000
	s_addc_u32 s9, s9, 0
	global_load_dwordx4 v[192:195], v75, s[8:9]
	s_add_u32 s8, s8, 0x8000
	s_addc_u32 s9, s9, 0
	global_load_dwordx4 v[196:199], v75, s[8:9]
	s_add_u32 s8, s8, 0x8000
	s_addc_u32 s9, s9, 0
	global_load_dwordx4 v[200:203], v75, s[8:9]
	s_add_u32 s8, s8, 0x8000
	s_addc_u32 s9, s9, 0
	global_load_dwordx4 v[204:207], v75, s[8:9]
	s_add_u32 s6, s44, 0x1000000
	s_addc_u32 s7, s45, 0
	ds_read_b32 v226, v212
	ds_read_b32 v227, v212 offset:512
	ds_read_b32 v228, v212 offset:1024
	ds_read_b32 v229, v212 offset:1536
	ds_read_b32 v230, v212 offset:2048
	ds_read_b32 v231, v212 offset:2560
	ds_read_b32 v232, v212 offset:3072
	ds_read_b32 v233, v212 offset:3584
	ds_read_b32 v234, v212 offset:4096
	ds_read_b32 v235, v212 offset:4608
	ds_read_b32 v236, v212 offset:5120
	ds_read_b32 v237, v212 offset:5632
	ds_read_b32 v238, v212 offset:6144
	ds_read_b32 v239, v212 offset:6656
	ds_read_b32 v240, v212 offset:7168
	ds_read_b32 v241, v212 offset:7680
	s_waitcnt lgkmcnt(0)
	v_max_f32_e32 v226, v226, v226
	v_max_f32_e32 v227, v227, v227
	v_max_f32_e32 v228, v228, v228
	v_max_f32_e32 v229, v229, v229
	v_max_f32_e32 v230, v230, v230
	v_max_f32_e32 v231, v231, v231
	v_max_f32_e32 v232, v232, v232
	v_max_f32_e32 v233, v233, v233
	v_max_f32_e32 v234, v234, v234
	v_max_f32_e32 v235, v235, v235
	v_max_f32_e32 v236, v236, v236
	v_max_f32_e32 v237, v237, v237
	v_max_f32_e32 v238, v238, v238
	v_max_f32_e32 v239, v239, v239
	v_max_f32_e32 v240, v240, v240
	v_max_f32_e32 v241, v241, v241
	v_med3_f32 v226, v226, s62, v95
	v_med3_f32 v227, v227, s62, v95
	v_med3_f32 v228, v228, s62, v95
	v_med3_f32 v229, v229, s62, v95
	v_med3_f32 v230, v230, s62, v95
	v_med3_f32 v231, v231, s62, v95
	v_med3_f32 v232, v232, s62, v95
	v_med3_f32 v233, v233, s62, v95
	v_med3_f32 v234, v234, s62, v95
	v_med3_f32 v235, v235, s62, v95
	v_med3_f32 v236, v236, s62, v95
	v_med3_f32 v237, v237, s62, v95
	v_med3_f32 v238, v238, s62, v95
	v_med3_f32 v239, v239, s62, v95
	v_med3_f32 v240, v240, s62, v95
	v_med3_f32 v241, v241, s62, v95
	v_mov_b32_e32 v242, 0
	v_mov_b32_e32 v243, 0
	v_mov_b32_e32 v244, 0
	v_mov_b32_e32 v245, 0
	v_cvt_pk_fp8_f32 v242, v226, v227
	v_cvt_pk_fp8_f32 v243, v230, v231
	v_cvt_pk_fp8_f32 v244, v234, v235
	v_cvt_pk_fp8_f32 v245, v238, v239
	v_cvt_pk_fp8_f32 v242, v228, v229 op_sel:[0,0,1]
	v_cvt_pk_fp8_f32 v243, v232, v233 op_sel:[0,0,1]
	v_cvt_pk_fp8_f32 v244, v236, v237 op_sel:[0,0,1]
	v_cvt_pk_fp8_f32 v245, v240, v241 op_sel:[0,0,1]
	s_nop 0
	global_store_dwordx4 v79, v[242:245], s[6:7]
	ds_read_b32 v226, v214
	ds_read_b32 v227, v214 offset:512
	ds_read_b32 v228, v214 offset:1024
	ds_read_b32 v229, v214 offset:1536
	ds_read_b32 v230, v214 offset:2048
	ds_read_b32 v231, v214 offset:2560
	ds_read_b32 v232, v214 offset:3072
	ds_read_b32 v233, v214 offset:3584
	ds_read_b32 v234, v214 offset:4096
	ds_read_b32 v235, v214 offset:4608
	ds_read_b32 v236, v214 offset:5120
	ds_read_b32 v237, v214 offset:5632
	ds_read_b32 v238, v214 offset:6144
	ds_read_b32 v239, v214 offset:6656
	ds_read_b32 v240, v214 offset:7168
	ds_read_b32 v241, v214 offset:7680
	s_waitcnt lgkmcnt(0)
; #define GAS __attribute__((address_space(1)))
; #define LAS __attribute__((address_space(3)))
; #define LDS_WAIT() asm volatile("s_waitcnt lgkmcnt(0)" ::: "memory")
;     const int pr = item >> 1, kb = 2 * (pr / nblk) + (item & 1), nb = pr % nblk, k0 = 64 * kb, n0 = 32 * nb;
;     const int nr = n0 + (lane & 31); const int sc = MAP == 1 ? src_col_in(nr) : nr;
;     float v[32];
; #pragma unroll
;     for (int i = 0; i < 32; ++i) v[i] = sc >= 0 ? W[(size_t)(k0 + 2 * i + (lane >> 5)) * Nsrc + sc] : 0.f;
; #pragma unroll
;     for (int i = 0; i < 32; ++i) { const int k = k0 + 2 * i + (lane >> 5); float x = v[i] * wscale; if (KS) x *= (k < ksplit ? ksA[k] : ksB[k - ksplit]); scr[(2 * i + (lane >> 5)) * 33 + (lane & 31)] = x; }
;     LDS_WAIT(); asm volatile("" ::: "memory");
;     const int c = lane & 7;
; #pragma unroll
;     for (int j = 0; j < 4; ++j) { const int n = (lane >> 3) + 8 * j; const LAS float* s = scr + (8 * c) * 33 + n;
;         const unsigned long long o = (unsigned long long)pg8::pk4_fp8(s[0 * 33], s[1 * 33], s[2 * 33], s[3 * 33]) | ((unsigned long long)pg8::pk4_fp8(s[4 * 33], s[5 * 33], s[6 * 33], s[7 * 33]) << 32);
;         *(GAS unsigned long long*)(WT + (size_t)(n0 + n) * K + k0 + 8 * c) = o; }
;     LDS_WAIT(); asm volatile("" ::: "memory");
; }
; __global__ void __launch_bounds__(NWAVES * 64, 2) hybrid_fwd(Args args) {
;     ...
;             p0_transpose_item_f8<false>(args.in[16] + (size_t)l * FF * DM, FF, DM, DM / 32, (unsigned char*)(ws + WS_WDN + l * SZ_WDN), 128.f, args.in[16], args.in[16], 0, scr, r, lane);
	v_max_f32_e32 v226, v226, v226
	v_max_f32_e32 v227, v227, v227
	v_max_f32_e32 v228, v228, v228
	v_max_f32_e32 v229, v229, v229
	v_max_f32_e32 v230, v230, v230
	v_max_f32_e32 v231, v231, v231
	v_max_f32_e32 v232, v232, v232
	v_max_f32_e32 v233, v233, v233
	v_max_f32_e32 v234, v234, v234
	v_max_f32_e32 v235, v235, v235
	v_max_f32_e32 v236, v236, v236
	v_max_f32_e32 v237, v237, v237
	v_max_f32_e32 v238, v238, v238
	v_max_f32_e32 v239, v239, v239
	v_max_f32_e32 v240, v240, v240
	v_max_f32_e32 v241, v241, v241
	v_med3_f32 v226, v226, s62, v95
	v_med3_f32 v227, v227, s62, v95
	v_med3_f32 v228, v228, s62, v95
	v_med3_f32 v229, v229, s62, v95
	v_med3_f32 v230, v230, s62, v95
	v_med3_f32 v231, v231, s62, v95
	v_med3_f32 v232, v232, s62, v95
	v_med3_f32 v233, v233, s62, v95
	v_med3_f32 v234, v234, s62, v95
	v_med3_f32 v235, v235, s62, v95
	v_med3_f32 v236, v236, s62, v95
	v_med3_f32 v237, v237, s62, v95
	v_med3_f32 v238, v238, s62, v95
	v_med3_f32 v239, v239, s62, v95
	v_med3_f32 v240, v240, s62, v95
	v_med3_f32 v241, v241, s62, v95
	v_mov_b32_e32 v242, 0
	v_mov_b32_e32 v243, 0
	v_mov_b32_e32 v244, 0
	v_mov_b32_e32 v245, 0
	v_cvt_pk_fp8_f32 v242, v226, v227
	v_cvt_pk_fp8_f32 v243, v230, v231
	v_cvt_pk_fp8_f32 v244, v234, v235
	v_cvt_pk_fp8_f32 v245, v238, v239
	v_cvt_pk_fp8_f32 v242, v228, v229 op_sel:[0,0,1]
	v_cvt_pk_fp8_f32 v243, v232, v233 op_sel:[0,0,1]
	v_cvt_pk_fp8_f32 v244, v236, v237 op_sel:[0,0,1]
	v_cvt_pk_fp8_f32 v245, v240, v241 op_sel:[0,0,1]
	s_nop 0
	global_store_dwordx4 v80, v[242:245], s[6:7]
	s_waitcnt vmcnt(12)
	v_mul_f32_e32 v144, 0x43000000, v144
	v_mul_f32_e32 v145, 0x43000000, v145
	v_mul_f32_e32 v146, 0x43000000, v146
	v_mul_f32_e32 v147, 0x43000000, v147
	ds_write_b128 v209, v[144:147]
	v_mul_f32_e32 v148, 0x43000000, v148
	v_mul_f32_e32 v149, 0x43000000, v149
	v_mul_f32_e32 v150, 0x43000000, v150
	v_mul_f32_e32 v151, 0x43000000, v151
	ds_write_b128 v209, v[148:151] offset:1024
	v_mul_f32_e32 v152, 0x43000000, v152
	v_mul_f32_e32 v153, 0x43000000, v153
	v_mul_f32_e32 v154, 0x43000000, v154
	v_mul_f32_e32 v155, 0x43000000, v155
	ds_write_b128 v209, v[152:155] offset:2048
	v_mul_f32_e32 v156, 0x43000000, v156
	v_mul_f32_e32 v157, 0x43000000, v157
	v_mul_f32_e32 v158, 0x43000000, v158
	v_mul_f32_e32 v159, 0x43000000, v159
	ds_write_b128 v209, v[156:159] offset:3072
	v_mul_f32_e32 v160, 0x43000000, v160
	v_mul_f32_e32 v161, 0x43000000, v161
	v_mul_f32_e32 v162, 0x43000000, v162
	v_mul_f32_e32 v163, 0x43000000, v163
	ds_write_b128 v209, v[160:163] offset:4096
	v_mul_f32_e32 v164, 0x43000000, v164
	v_mul_f32_e32 v165, 0x43000000, v165
	v_mul_f32_e32 v166, 0x43000000, v166
	v_mul_f32_e32 v167, 0x43000000, v167
	ds_write_b128 v209, v[164:167] offset:5120
	v_mul_f32_e32 v168, 0x43000000, v168
	v_mul_f32_e32 v169, 0x43000000, v169
	v_mul_f32_e32 v170, 0x43000000, v170
	v_mul_f32_e32 v171, 0x43000000, v171
	ds_write_b128 v209, v[168:171] offset:6144
	v_mul_f32_e32 v172, 0x43000000, v172
	v_mul_f32_e32 v173, 0x43000000, v173
	v_mul_f32_e32 v174, 0x43000000, v174
	v_mul_f32_e32 v175, 0x43000000, v175
	ds_write_b128 v209, v[172:175] offset:7168
	s_waitcnt lgkmcnt(0)
	s_barrier
	s_add_u32 s8, s42, 0x4000000
	s_addc_u32 s9, s43, 0
	global_load_dwordx4 v[144:147], v75, s[8:9]
	s_add_u32 s8, s8, 0x8000
	s_addc_u32 s9, s9, 0
	global_load_dwordx4 v[148:151], v75, s[8:9]
	s_add_u32 s8, s8, 0x8000
	s_addc_u32 s9, s9, 0
	global_load_dwordx4 v[152:155], v75, s[8:9]
	s_add_u32 s8, s8, 0x8000
	s_addc_u32 s9, s9, 0
	global_load_dwordx4 v[156:159], v75, s[8:9]
	s_add_u32 s8, s8, 0x8000
	s_addc_u32 s9, s9, 0
	global_load_dwordx4 v[160:163], v75, s[8:9]
	s_add_u32 s8, s8, 0x8000
	s_addc_u32 s9, s9, 0
	global_load_dwordx4 v[164:167], v75, s[8:9]
	s_add_u32 s8, s8, 0x8000
	s_addc_u32 s9, s9, 0
	global_load_dwordx4 v[168:171], v75, s[8:9]
	s_add_u32 s8, s8, 0x8000
	s_addc_u32 s9, s9, 0
	global_load_dwordx4 v[172:175], v75, s[8:9]
	s_add_u32 s6, s44, 0x2000000
	s_addc_u32 s7, s45, 0
	ds_read_b32 v226, v211
	ds_read_b32 v227, v211 offset:512
	ds_read_b32 v228, v211 offset:1024
	ds_read_b32 v229, v211 offset:1536
	ds_read_b32 v230, v211 offset:2048
	ds_read_b32 v231, v211 offset:2560
	ds_read_b32 v232, v211 offset:3072
	ds_read_b32 v233, v211 offset:3584
	ds_read_b32 v234, v211 offset:4096
	ds_read_b32 v235, v211 offset:4608
	ds_read_b32 v236, v211 offset:5120
	ds_read_b32 v237, v211 offset:5632
	ds_read_b32 v238, v211 offset:6144
	ds_read_b32 v239, v211 offset:6656
	ds_read_b32 v240, v211 offset:7168
	ds_read_b32 v241, v211 offset:7680
	s_waitcnt lgkmcnt(0)
	v_max_f32_e32 v226, v226, v226
	v_max_f32_e32 v227, v227, v227
	v_max_f32_e32 v228, v228, v228
	v_max_f32_e32 v229, v229, v229
	v_max_f32_e32 v230, v230, v230
	v_max_f32_e32 v231, v231, v231
	v_max_f32_e32 v232, v232, v232
	v_max_f32_e32 v233, v233, v233
	v_max_f32_e32 v234, v234, v234
	v_max_f32_e32 v235, v235, v235
	v_max_f32_e32 v236, v236, v236
	v_max_f32_e32 v237, v237, v237
	v_max_f32_e32 v238, v238, v238
	v_max_f32_e32 v239, v239, v239
	v_max_f32_e32 v240, v240, v240
	v_max_f32_e32 v241, v241, v241
	v_med3_f32 v226, v226, s62, v95
	v_med3_f32 v227, v227, s62, v95
	v_med3_f32 v228, v228, s62, v95
	v_med3_f32 v229, v229, s62, v95
	v_med3_f32 v230, v230, s62, v95
	v_med3_f32 v231, v231, s62, v95
	v_med3_f32 v232, v232, s62, v95
	v_med3_f32 v233, v233, s62, v95
	v_med3_f32 v234, v234, s62, v95
	v_med3_f32 v235, v235, s62, v95
	v_med3_f32 v236, v236, s62, v95
	v_med3_f32 v237, v237, s62, v95
	v_med3_f32 v238, v238, s62, v95
	v_med3_f32 v239, v239, s62, v95
	v_med3_f32 v240, v240, s62, v95
	v_med3_f32 v241, v241, s62, v95
	v_mov_b32_e32 v242, 0
	v_mov_b32_e32 v243, 0
	v_mov_b32_e32 v244, 0
	v_mov_b32_e32 v245, 0
	v_cvt_pk_fp8_f32 v242, v226, v227
	v_cvt_pk_fp8_f32 v243, v230, v231
	v_cvt_pk_fp8_f32 v244, v234, v235
	v_cvt_pk_fp8_f32 v245, v238, v239
	v_cvt_pk_fp8_f32 v242, v228, v229 op_sel:[0,0,1]
	v_cvt_pk_fp8_f32 v243, v232, v233 op_sel:[0,0,1]
	v_cvt_pk_fp8_f32 v244, v236, v237 op_sel:[0,0,1]
	v_cvt_pk_fp8_f32 v245, v240, v241 op_sel:[0,0,1]
	s_nop 0
	global_store_dwordx4 v79, v[242:245], s[6:7]
	ds_read_b32 v226, v213
	ds_read_b32 v227, v213 offset:512
	ds_read_b32 v228, v213 offset:1024
	ds_read_b32 v229, v213 offset:1536
	ds_read_b32 v230, v213 offset:2048
	ds_read_b32 v231, v213 offset:2560
	ds_read_b32 v232, v213 offset:3072
	ds_read_b32 v233, v213 offset:3584
	ds_read_b32 v234, v213 offset:4096
	ds_read_b32 v235, v213 offset:4608
	ds_read_b32 v236, v213 offset:5120
	ds_read_b32 v237, v213 offset:5632
	ds_read_b32 v238, v213 offset:6144
	ds_read_b32 v239, v213 offset:6656
	ds_read_b32 v240, v213 offset:7168
	ds_read_b32 v241, v213 offset:7680
	s_waitcnt lgkmcnt(0)
; #define GAS __attribute__((address_space(1)))
; #define LAS __attribute__((address_space(3)))
; #define LDS_WAIT() asm volatile("s_waitcnt lgkmcnt(0)" ::: "memory")
;     const int pr = item >> 1, kb = 2 * (pr / nblk) + (item & 1), nb = pr % nblk, k0 = 64 * kb, n0 = 32 * nb;
;     const int nr = n0 + (lane & 31); const int sc = MAP == 1 ? src_col_in(nr) : nr;
;     float v[32];
; #pragma unroll
;     for (int i = 0; i < 32; ++i) v[i] = sc >= 0 ? W[(size_t)(k0 + 2 * i + (lane >> 5)) * Nsrc + sc] : 0.f;
; #pragma unroll
;     for (int i = 0; i < 32; ++i) { const int k = k0 + 2 * i + (lane >> 5); float x = v[i] * wscale; if (KS) x *= (k < ksplit ? ksA[k] : ksB[k - ksplit]); scr[(2 * i + (lane >> 5)) * 33 + (lane & 31)] = x; }
;     LDS_WAIT(); asm volatile("" ::: "memory");
;     const int c = lane & 7;
; #pragma unroll
;     for (int j = 0; j < 4; ++j) { const int n = (lane >> 3) + 8 * j; const LAS float* s = scr + (8 * c) * 33 + n;
;         const unsigned long long o = (unsigned long long)pg8::pk4_fp8(s[0 * 33], s[1 * 33], s[2 * 33], s[3 * 33]) | ((unsigned long long)pg8::pk4_fp8(s[4 * 33], s[5 * 33], s[6 * 33], s[7 * 33]) << 32);
;         *(GAS unsigned long long*)(WT + (size_t)(n0 + n) * K + k0 + 8 * c) = o; }
;     LDS_WAIT(); asm volatile("" ::: "memory");
; }
; __global__ void __launch_bounds__(NWAVES * 64, 2) hybrid_fwd(Args args) {
;     ...
;             p0_transpose_item_f8<false>(args.in[16] + (size_t)l * FF * DM, FF, DM, DM / 32, (unsigned char*)(ws + WS_WDN + l * SZ_WDN), 128.f, args.in[16], args.in[16], 0, scr, r, lane);
	v_max_f32_e32 v226, v226, v226
	v_max_f32_e32 v227, v227, v227
	v_max_f32_e32 v228, v228, v228
	v_max_f32_e32 v229, v229, v229
	v_max_f32_e32 v230, v230, v230
	v_max_f32_e32 v231, v231, v231
	v_max_f32_e32 v232, v232, v232
	v_max_f32_e32 v233, v233, v233
	v_max_f32_e32 v234, v234, v234
	v_max_f32_e32 v235, v235, v235
	v_max_f32_e32 v236, v236, v236
	v_max_f32_e32 v237, v237, v237
	v_max_f32_e32 v238, v238, v238
	v_max_f32_e32 v239, v239, v239
	v_max_f32_e32 v240, v240, v240
	v_max_f32_e32 v241, v241, v241
	v_med3_f32 v226, v226, s62, v95
	v_med3_f32 v227, v227, s62, v95
	v_med3_f32 v228, v228, s62, v95
	v_med3_f32 v229, v229, s62, v95
	v_med3_f32 v230, v230, s62, v95
	v_med3_f32 v231, v231, s62, v95
	v_med3_f32 v232, v232, s62, v95
	v_med3_f32 v233, v233, s62, v95
	v_med3_f32 v234, v234, s62, v95
	v_med3_f32 v235, v235, s62, v95
	v_med3_f32 v236, v236, s62, v95
	v_med3_f32 v237, v237, s62, v95
	v_med3_f32 v238, v238, s62, v95
	v_med3_f32 v239, v239, s62, v95
	v_med3_f32 v240, v240, s62, v95
	v_med3_f32 v241, v241, s62, v95
	v_mov_b32_e32 v242, 0
	v_mov_b32_e32 v243, 0
	v_mov_b32_e32 v244, 0
	v_mov_b32_e32 v245, 0
	v_cvt_pk_fp8_f32 v242, v226, v227
	v_cvt_pk_fp8_f32 v243, v230, v231
	v_cvt_pk_fp8_f32 v244, v234, v235
	v_cvt_pk_fp8_f32 v245, v238, v239
	v_cvt_pk_fp8_f32 v242, v228, v229 op_sel:[0,0,1]
	v_cvt_pk_fp8_f32 v243, v232, v233 op_sel:[0,0,1]
	v_cvt_pk_fp8_f32 v244, v236, v237 op_sel:[0,0,1]
	v_cvt_pk_fp8_f32 v245, v240, v241 op_sel:[0,0,1]
	s_nop 0
	global_store_dwordx4 v80, v[242:245], s[6:7]
	s_waitcnt vmcnt(12)
	v_mul_f32_e32 v176, 0x43000000, v176
	v_mul_f32_e32 v177, 0x43000000, v177
	v_mul_f32_e32 v178, 0x43000000, v178
	v_mul_f32_e32 v179, 0x43000000, v179
	ds_write_b128 v210, v[176:179]
	v_mul_f32_e32 v180, 0x43000000, v180
	v_mul_f32_e32 v181, 0x43000000, v181
	v_mul_f32_e32 v182, 0x43000000, v182
	v_mul_f32_e32 v183, 0x43000000, v183
	ds_write_b128 v210, v[180:183] offset:1024
	v_mul_f32_e32 v184, 0x43000000, v184
	v_mul_f32_e32 v185, 0x43000000, v185
	v_mul_f32_e32 v186, 0x43000000, v186
	v_mul_f32_e32 v187, 0x43000000, v187
	ds_write_b128 v210, v[184:187] offset:2048
	v_mul_f32_e32 v188, 0x43000000, v188
	v_mul_f32_e32 v189, 0x43000000, v189
	v_mul_f32_e32 v190, 0x43000000, v190
	v_mul_f32_e32 v191, 0x43000000, v191
	ds_write_b128 v210, v[188:191] offset:3072
	v_mul_f32_e32 v192, 0x43000000, v192
	v_mul_f32_e32 v193, 0x43000000, v193
	v_mul_f32_e32 v194, 0x43000000, v194
	v_mul_f32_e32 v195, 0x43000000, v195
	ds_write_b128 v210, v[192:195] offset:4096
	v_mul_f32_e32 v196, 0x43000000, v196
	v_mul_f32_e32 v197, 0x43000000, v197
	v_mul_f32_e32 v198, 0x43000000, v198
	v_mul_f32_e32 v199, 0x43000000, v199
	ds_write_b128 v210, v[196:199] offset:5120
	v_mul_f32_e32 v200, 0x43000000, v200
	v_mul_f32_e32 v201, 0x43000000, v201
	v_mul_f32_e32 v202, 0x43000000, v202
	v_mul_f32_e32 v203, 0x43000000, v203
	ds_write_b128 v210, v[200:203] offset:6144
	v_mul_f32_e32 v204, 0x43000000, v204
	v_mul_f32_e32 v205, 0x43000000, v205
	v_mul_f32_e32 v206, 0x43000000, v206
	v_mul_f32_e32 v207, 0x43000000, v207
	ds_write_b128 v210, v[204:207] offset:7168
	s_waitcnt lgkmcnt(0)
	s_barrier
	s_add_u32 s8, s42, 0x4001000
	s_addc_u32 s9, s43, 0
	global_load_dwordx4 v[176:179], v75, s[8:9]
	s_add_u32 s8, s8, 0x8000
	s_addc_u32 s9, s9, 0
	global_load_dwordx4 v[180:183], v75, s[8:9]
	s_add_u32 s8, s8, 0x8000
	s_addc_u32 s9, s9, 0
	global_load_dwordx4 v[184:187], v75, s[8:9]
	s_add_u32 s8, s8, 0x8000
	s_addc_u32 s9, s9, 0
	global_load_dwordx4 v[188:191], v75, s[8:9]
	s_add_u32 s8, s8, 0x8000
	s_addc_u32 s9, s9, 0
	global_load_dwordx4 v[192:195], v75, s[8:9]
	s_add_u32 s8, s8, 0x8000
	s_addc_u32 s9, s9, 0
	global_load_dwordx4 v[196:199], v75, s[8:9]
	s_add_u32 s8, s8, 0x8000
	s_addc_u32 s9, s9, 0
	global_load_dwordx4 v[200:203], v75, s[8:9]
	s_add_u32 s8, s8, 0x8000
	s_addc_u32 s9, s9, 0
	global_load_dwordx4 v[204:207], v75, s[8:9]
	s_add_u32 s6, s44, 0x3000000
	s_addc_u32 s7, s45, 0
	ds_read_b32 v226, v212
	ds_read_b32 v227, v212 offset:512
	ds_read_b32 v228, v212 offset:1024
	ds_read_b32 v229, v212 offset:1536
	ds_read_b32 v230, v212 offset:2048
	ds_read_b32 v231, v212 offset:2560
	ds_read_b32 v232, v212 offset:3072
	ds_read_b32 v233, v212 offset:3584
	ds_read_b32 v234, v212 offset:4096
	ds_read_b32 v235, v212 offset:4608
	ds_read_b32 v236, v212 offset:5120
	ds_read_b32 v237, v212 offset:5632
	ds_read_b32 v238, v212 offset:6144
	ds_read_b32 v239, v212 offset:6656
	ds_read_b32 v240, v212 offset:7168
	ds_read_b32 v241, v212 offset:7680
	s_waitcnt lgkmcnt(0)
	v_max_f32_e32 v226, v226, v226
	v_max_f32_e32 v227, v227, v227
	v_max_f32_e32 v228, v228, v228
	v_max_f32_e32 v229, v229, v229
	v_max_f32_e32 v230, v230, v230
	v_max_f32_e32 v231, v231, v231
	v_max_f32_e32 v232, v232, v232
	v_max_f32_e32 v233, v233, v233
	v_max_f32_e32 v234, v234, v234
	v_max_f32_e32 v235, v235, v235
	v_max_f32_e32 v236, v236, v236
	v_max_f32_e32 v237, v237, v237
	v_max_f32_e32 v238, v238, v238
	v_max_f32_e32 v239, v239, v239
	v_max_f32_e32 v240, v240, v240
	v_max_f32_e32 v241, v241, v241
	v_med3_f32 v226, v226, s62, v95
	v_med3_f32 v227, v227, s62, v95
	v_med3_f32 v228, v228, s62, v95
	v_med3_f32 v229, v229, s62, v95
	v_med3_f32 v230, v230, s62, v95
	v_med3_f32 v231, v231, s62, v95
	v_med3_f32 v232, v232, s62, v95
	v_med3_f32 v233, v233, s62, v95
	v_med3_f32 v234, v234, s62, v95
	v_med3_f32 v235, v235, s62, v95
	v_med3_f32 v236, v236, s62, v95
	v_med3_f32 v237, v237, s62, v95
	v_med3_f32 v238, v238, s62, v95
	v_med3_f32 v239, v239, s62, v95
	v_med3_f32 v240, v240, s62, v95
	v_med3_f32 v241, v241, s62, v95
	v_mov_b32_e32 v242, 0
	v_mov_b32_e32 v243, 0
	v_mov_b32_e32 v244, 0
	v_mov_b32_e32 v245, 0
	v_cvt_pk_fp8_f32 v242, v226, v227
	v_cvt_pk_fp8_f32 v243, v230, v231
	v_cvt_pk_fp8_f32 v244, v234, v235
	v_cvt_pk_fp8_f32 v245, v238, v239
	v_cvt_pk_fp8_f32 v242, v228, v229 op_sel:[0,0,1]
	v_cvt_pk_fp8_f32 v243, v232, v233 op_sel:[0,0,1]
	v_cvt_pk_fp8_f32 v244, v236, v237 op_sel:[0,0,1]
	v_cvt_pk_fp8_f32 v245, v240, v241 op_sel:[0,0,1]
	s_nop 0
	global_store_dwordx4 v79, v[242:245], s[6:7]
	ds_read_b32 v226, v214
	ds_read_b32 v227, v214 offset:512
	ds_read_b32 v228, v214 offset:1024
	ds_read_b32 v229, v214 offset:1536
	ds_read_b32 v230, v214 offset:2048
	ds_read_b32 v231, v214 offset:2560
	ds_read_b32 v232, v214 offset:3072
	ds_read_b32 v233, v214 offset:3584
	ds_read_b32 v234, v214 offset:4096
	ds_read_b32 v235, v214 offset:4608
	ds_read_b32 v236, v214 offset:5120
	ds_read_b32 v237, v214 offset:5632
	ds_read_b32 v238, v214 offset:6144
	ds_read_b32 v239, v214 offset:6656
	ds_read_b32 v240, v214 offset:7168
	ds_read_b32 v241, v214 offset:7680
	s_waitcnt lgkmcnt(0)
; #define GAS __attribute__((address_space(1)))
; #define LAS __attribute__((address_space(3)))
; #define LDS_WAIT() asm volatile("s_waitcnt lgkmcnt(0)" ::: "memory")
;     const int pr = item >> 1, kb = 2 * (pr / nblk) + (item & 1), nb = pr % nblk, k0 = 64 * kb, n0 = 32 * nb;
;     const int nr = n0 + (lane & 31); const int sc = MAP == 1 ? src_col_in(nr) : nr;
;     float v[32];
; #pragma unroll
;     for (int i = 0; i < 32; ++i) v[i] = sc >= 0 ? W[(size_t)(k0 + 2 * i + (lane >> 5)) * Nsrc + sc] : 0.f;
; #pragma unroll
;     for (int i = 0; i < 32; ++i) { const int k = k0 + 2 * i + (lane >> 5); float x = v[i] * wscale; if (KS) x *= (k < ksplit ? ksA[k] : ksB[k - ksplit]); scr[(2 * i + (lane >> 5)) * 33 + (lane & 31)] = x; }
;     LDS_WAIT(); asm volatile("" ::: "memory");
;     const int c = lane & 7;
; #pragma unroll
;     for (int j = 0; j < 4; ++j) { const int n = (lane >> 3) + 8 * j; const LAS float* s = scr + (8 * c) * 33 + n;
;         const unsigned long long o = (unsigned long long)pg8::pk4_fp8(s[0 * 33], s[1 * 33], s[2 * 33], s[3 * 33]) | ((unsigned long long)pg8::pk4_fp8(s[4 * 33], s[5 * 33], s[6 * 33], s[7 * 33]) << 32);
;         *(GAS unsigned long long*)(WT + (size_t)(n0 + n) * K + k0 + 8 * c) = o; }
;     LDS_WAIT(); asm volatile("" ::: "memory");
; }
; __global__ void __launch_bounds__(NWAVES * 64, 2) hybrid_fwd(Args args) {
;     ...
;             p0_transpose_item_f8<false>(args.in[16] + (size_t)l * FF * DM, FF, DM, DM / 32, (unsigned char*)(ws + WS_WDN + l * SZ_WDN), 128.f, args.in[16], args.in[16], 0, scr, r, lane);
	v_max_f32_e32 v226, v226, v226
	v_max_f32_e32 v227, v227, v227
	v_max_f32_e32 v228, v228, v228
	v_max_f32_e32 v229, v229, v229
	v_max_f32_e32 v230, v230, v230
	v_max_f32_e32 v231, v231, v231
	v_max_f32_e32 v232, v232, v232
	v_max_f32_e32 v233, v233, v233
	v_max_f32_e32 v234, v234, v234
	v_max_f32_e32 v235, v235, v235
	v_max_f32_e32 v236, v236, v236
	v_max_f32_e32 v237, v237, v237
	v_max_f32_e32 v238, v238, v238
	v_max_f32_e32 v239, v239, v239
	v_max_f32_e32 v240, v240, v240
	v_max_f32_e32 v241, v241, v241
	v_med3_f32 v226, v226, s62, v95
	v_med3_f32 v227, v227, s62, v95
	v_med3_f32 v228, v228, s62, v95
	v_med3_f32 v229, v229, s62, v95
	v_med3_f32 v230, v230, s62, v95
	v_med3_f32 v231, v231, s62, v95
	v_med3_f32 v232, v232, s62, v95
	v_med3_f32 v233, v233, s62, v95
	v_med3_f32 v234, v234, s62, v95
	v_med3_f32 v235, v235, s62, v95
	v_med3_f32 v236, v236, s62, v95
	v_med3_f32 v237, v237, s62, v95
	v_med3_f32 v238, v238, s62, v95
	v_med3_f32 v239, v239, s62, v95
	v_med3_f32 v240, v240, s62, v95
	v_med3_f32 v241, v241, s62, v95
	v_mov_b32_e32 v242, 0
	v_mov_b32_e32 v243, 0
	v_mov_b32_e32 v244, 0
	v_mov_b32_e32 v245, 0
	v_cvt_pk_fp8_f32 v242, v226, v227
	v_cvt_pk_fp8_f32 v243, v230, v231
	v_cvt_pk_fp8_f32 v244, v234, v235
	v_cvt_pk_fp8_f32 v245, v238, v239
	v_cvt_pk_fp8_f32 v242, v228, v229 op_sel:[0,0,1]
	v_cvt_pk_fp8_f32 v243, v232, v233 op_sel:[0,0,1]
	v_cvt_pk_fp8_f32 v244, v236, v237 op_sel:[0,0,1]
	v_cvt_pk_fp8_f32 v245, v240, v241 op_sel:[0,0,1]
	s_nop 0
	global_store_dwordx4 v80, v[242:245], s[6:7]
	s_waitcnt vmcnt(12)
	v_mul_f32_e32 v144, 0x43000000, v144
	v_mul_f32_e32 v145, 0x43000000, v145
	v_mul_f32_e32 v146, 0x43000000, v146
	v_mul_f32_e32 v147, 0x43000000, v147
	ds_write_b128 v209, v[144:147]
	v_mul_f32_e32 v148, 0x43000000, v148
	v_mul_f32_e32 v149, 0x43000000, v149
	v_mul_f32_e32 v150, 0x43000000, v150
	v_mul_f32_e32 v151, 0x43000000, v151
	ds_write_b128 v209, v[148:151] offset:1024
	v_mul_f32_e32 v152, 0x43000000, v152
	v_mul_f32_e32 v153, 0x43000000, v153
	v_mul_f32_e32 v154, 0x43000000, v154
	v_mul_f32_e32 v155, 0x43000000, v155
	ds_write_b128 v209, v[152:155] offset:2048
	v_mul_f32_e32 v156, 0x43000000, v156
	v_mul_f32_e32 v157, 0x43000000, v157
	v_mul_f32_e32 v158, 0x43000000, v158
	v_mul_f32_e32 v159, 0x43000000, v159
	ds_write_b128 v209, v[156:159] offset:3072
	v_mul_f32_e32 v160, 0x43000000, v160
	v_mul_f32_e32 v161, 0x43000000, v161
	v_mul_f32_e32 v162, 0x43000000, v162
	v_mul_f32_e32 v163, 0x43000000, v163
	ds_write_b128 v209, v[160:163] offset:4096
	v_mul_f32_e32 v164, 0x43000000, v164
	v_mul_f32_e32 v165, 0x43000000, v165
	v_mul_f32_e32 v166, 0x43000000, v166
	v_mul_f32_e32 v167, 0x43000000, v167
	ds_write_b128 v209, v[164:167] offset:5120
	v_mul_f32_e32 v168, 0x43000000, v168
	v_mul_f32_e32 v169, 0x43000000, v169
	v_mul_f32_e32 v170, 0x43000000, v170
	v_mul_f32_e32 v171, 0x43000000, v171
	ds_write_b128 v209, v[168:171] offset:6144
	v_mul_f32_e32 v172, 0x43000000, v172
	v_mul_f32_e32 v173, 0x43000000, v173
	v_mul_f32_e32 v174, 0x43000000, v174
	v_mul_f32_e32 v175, 0x43000000, v175
	ds_write_b128 v209, v[172:175] offset:7168
	s_waitcnt lgkmcnt(0)
	s_barrier
	s_add_u32 s8, s42, 0x4002000
	s_addc_u32 s9, s43, 0
	global_load_dwordx4 v[144:147], v75, s[8:9]
	s_add_u32 s8, s8, 0x8000
	s_addc_u32 s9, s9, 0
	global_load_dwordx4 v[148:151], v75, s[8:9]
	s_add_u32 s8, s8, 0x8000
	s_addc_u32 s9, s9, 0
	global_load_dwordx4 v[152:155], v75, s[8:9]
	s_add_u32 s8, s8, 0x8000
	s_addc_u32 s9, s9, 0
	global_load_dwordx4 v[156:159], v75, s[8:9]
	s_add_u32 s8, s8, 0x8000
	s_addc_u32 s9, s9, 0
	global_load_dwordx4 v[160:163], v75, s[8:9]
	s_add_u32 s8, s8, 0x8000
	s_addc_u32 s9, s9, 0
	global_load_dwordx4 v[164:167], v75, s[8:9]
	s_add_u32 s8, s8, 0x8000
	s_addc_u32 s9, s9, 0
	global_load_dwordx4 v[168:171], v75, s[8:9]
	s_add_u32 s8, s8, 0x8000
	s_addc_u32 s9, s9, 0
	global_load_dwordx4 v[172:175], v75, s[8:9]
	s_add_u32 s6, s44, 0x1000
	s_addc_u32 s7, s45, 0
	ds_read_b32 v226, v211
	ds_read_b32 v227, v211 offset:512
	ds_read_b32 v228, v211 offset:1024
	ds_read_b32 v229, v211 offset:1536
	ds_read_b32 v230, v211 offset:2048
	ds_read_b32 v231, v211 offset:2560
	ds_read_b32 v232, v211 offset:3072
	ds_read_b32 v233, v211 offset:3584
	ds_read_b32 v234, v211 offset:4096
	ds_read_b32 v235, v211 offset:4608
	ds_read_b32 v236, v211 offset:5120
	ds_read_b32 v237, v211 offset:5632
	ds_read_b32 v238, v211 offset:6144
	ds_read_b32 v239, v211 offset:6656
	ds_read_b32 v240, v211 offset:7168
	ds_read_b32 v241, v211 offset:7680
	s_waitcnt lgkmcnt(0)
	v_max_f32_e32 v226, v226, v226
	v_max_f32_e32 v227, v227, v227
	v_max_f32_e32 v228, v228, v228
	v_max_f32_e32 v229, v229, v229
	v_max_f32_e32 v230, v230, v230
	v_max_f32_e32 v231, v231, v231
	v_max_f32_e32 v232, v232, v232
	v_max_f32_e32 v233, v233, v233
	v_max_f32_e32 v234, v234, v234
	v_max_f32_e32 v235, v235, v235
	v_max_f32_e32 v236, v236, v236
	v_max_f32_e32 v237, v237, v237
	v_max_f32_e32 v238, v238, v238
	v_max_f32_e32 v239, v239, v239
	v_max_f32_e32 v240, v240, v240
	v_max_f32_e32 v241, v241, v241
	v_med3_f32 v226, v226, s62, v95
	v_med3_f32 v227, v227, s62, v95
	v_med3_f32 v228, v228, s62, v95
	v_med3_f32 v229, v229, s62, v95
	v_med3_f32 v230, v230, s62, v95
	v_med3_f32 v231, v231, s62, v95
	v_med3_f32 v232, v232, s62, v95
	v_med3_f32 v233, v233, s62, v95
	v_med3_f32 v234, v234, s62, v95
	v_med3_f32 v235, v235, s62, v95
	v_med3_f32 v236, v236, s62, v95
	v_med3_f32 v237, v237, s62, v95
	v_med3_f32 v238, v238, s62, v95
	v_med3_f32 v239, v239, s62, v95
	v_med3_f32 v240, v240, s62, v95
	v_med3_f32 v241, v241, s62, v95
	v_mov_b32_e32 v242, 0
	v_mov_b32_e32 v243, 0
	v_mov_b32_e32 v244, 0
	v_mov_b32_e32 v245, 0
	v_cvt_pk_fp8_f32 v242, v226, v227
	v_cvt_pk_fp8_f32 v243, v230, v231
	v_cvt_pk_fp8_f32 v244, v234, v235
	v_cvt_pk_fp8_f32 v245, v238, v239
	v_cvt_pk_fp8_f32 v242, v228, v229 op_sel:[0,0,1]
	v_cvt_pk_fp8_f32 v243, v232, v233 op_sel:[0,0,1]
	v_cvt_pk_fp8_f32 v244, v236, v237 op_sel:[0,0,1]
	v_cvt_pk_fp8_f32 v245, v240, v241 op_sel:[0,0,1]
	s_nop 0
	global_store_dwordx4 v79, v[242:245], s[6:7]
	ds_read_b32 v226, v213
	ds_read_b32 v227, v213 offset:512
	ds_read_b32 v228, v213 offset:1024
	ds_read_b32 v229, v213 offset:1536
	ds_read_b32 v230, v213 offset:2048
	ds_read_b32 v231, v213 offset:2560
	ds_read_b32 v232, v213 offset:3072
	ds_read_b32 v233, v213 offset:3584
	ds_read_b32 v234, v213 offset:4096
	ds_read_b32 v235, v213 offset:4608
	ds_read_b32 v236, v213 offset:5120
	ds_read_b32 v237, v213 offset:5632
	ds_read_b32 v238, v213 offset:6144
	ds_read_b32 v239, v213 offset:6656
	ds_read_b32 v240, v213 offset:7168
	ds_read_b32 v241, v213 offset:7680
	s_waitcnt lgkmcnt(0)
; #define GAS __attribute__((address_space(1)))
; #define LAS __attribute__((address_space(3)))
; #define LDS_WAIT() asm volatile("s_waitcnt lgkmcnt(0)" ::: "memory")
;     const int pr = item >> 1, kb = 2 * (pr / nblk) + (item & 1), nb = pr % nblk, k0 = 64 * kb, n0 = 32 * nb;
;     const int nr = n0 + (lane & 31); const int sc = MAP == 1 ? src_col_in(nr) : nr;
;     float v[32];
; #pragma unroll
;     for (int i = 0; i < 32; ++i) v[i] = sc >= 0 ? W[(size_t)(k0 + 2 * i + (lane >> 5)) * Nsrc + sc] : 0.f;
; #pragma unroll
;     for (int i = 0; i < 32; ++i) { const int k = k0 + 2 * i + (lane >> 5); float x = v[i] * wscale; if (KS) x *= (k < ksplit ? ksA[k] : ksB[k - ksplit]); scr[(2 * i + (lane >> 5)) * 33 + (lane & 31)] = x; }
;     LDS_WAIT(); asm volatile("" ::: "memory");
;     const int c = lane & 7;
; #pragma unroll
;     for (int j = 0; j < 4; ++j) { const int n = (lane >> 3) + 8 * j; const LAS float* s = scr + (8 * c) * 33 + n;
;         const unsigned long long o = (unsigned long long)pg8::pk4_fp8(s[0 * 33], s[1 * 33], s[2 * 33], s[3 * 33]) | ((unsigned long long)pg8::pk4_fp8(s[4 * 33], s[5 * 33], s[6 * 33], s[7 * 33]) << 32);
;         *(GAS unsigned long long*)(WT + (size_t)(n0 + n) * K + k0 + 8 * c) = o; }
;     LDS_WAIT(); asm volatile("" ::: "memory");
; }
; __global__ void __launch_bounds__(NWAVES * 64, 2) hybrid_fwd(Args args) {
;     ...
;             p0_transpose_item_f8<false>(args.in[16] + (size_t)l * FF * DM, FF, DM, DM / 32, (unsigned char*)(ws + WS_WDN + l * SZ_WDN), 128.f, args.in[16], args.in[16], 0, scr, r, lane);
	v_max_f32_e32 v226, v226, v226
	v_max_f32_e32 v227, v227, v227
	v_max_f32_e32 v228, v228, v228
	v_max_f32_e32 v229, v229, v229
	v_max_f32_e32 v230, v230, v230
	v_max_f32_e32 v231, v231, v231
	v_max_f32_e32 v232, v232, v232
	v_max_f32_e32 v233, v233, v233
	v_max_f32_e32 v234, v234, v234
	v_max_f32_e32 v235, v235, v235
	v_max_f32_e32 v236, v236, v236
	v_max_f32_e32 v237, v237, v237
	v_max_f32_e32 v238, v238, v238
	v_max_f32_e32 v239, v239, v239
	v_max_f32_e32 v240, v240, v240
	v_max_f32_e32 v241, v241, v241
	v_med3_f32 v226, v226, s62, v95
	v_med3_f32 v227, v227, s62, v95
	v_med3_f32 v228, v228, s62, v95
	v_med3_f32 v229, v229, s62, v95
	v_med3_f32 v230, v230, s62, v95
	v_med3_f32 v231, v231, s62, v95
	v_med3_f32 v232, v232, s62, v95
	v_med3_f32 v233, v233, s62, v95
	v_med3_f32 v234, v234, s62, v95
	v_med3_f32 v235, v235, s62, v95
	v_med3_f32 v236, v236, s62, v95
	v_med3_f32 v237, v237, s62, v95
	v_med3_f32 v238, v238, s62, v95
	v_med3_f32 v239, v239, s62, v95
	v_med3_f32 v240, v240, s62, v95
	v_med3_f32 v241, v241, s62, v95
	v_mov_b32_e32 v242, 0
	v_mov_b32_e32 v243, 0
	v_mov_b32_e32 v244, 0
	v_mov_b32_e32 v245, 0
	v_cvt_pk_fp8_f32 v242, v226, v227
	v_cvt_pk_fp8_f32 v243, v230, v231
	v_cvt_pk_fp8_f32 v244, v234, v235
	v_cvt_pk_fp8_f32 v245, v238, v239
	v_cvt_pk_fp8_f32 v242, v228, v229 op_sel:[0,0,1]
	v_cvt_pk_fp8_f32 v243, v232, v233 op_sel:[0,0,1]
	v_cvt_pk_fp8_f32 v244, v236, v237 op_sel:[0,0,1]
	v_cvt_pk_fp8_f32 v245, v240, v241 op_sel:[0,0,1]
	s_nop 0
	global_store_dwordx4 v80, v[242:245], s[6:7]
	s_waitcnt vmcnt(12)
	v_mul_f32_e32 v176, 0x43000000, v176
	v_mul_f32_e32 v177, 0x43000000, v177
	v_mul_f32_e32 v178, 0x43000000, v178
	v_mul_f32_e32 v179, 0x43000000, v179
	ds_write_b128 v210, v[176:179]
	v_mul_f32_e32 v180, 0x43000000, v180
	v_mul_f32_e32 v181, 0x43000000, v181
	v_mul_f32_e32 v182, 0x43000000, v182
	v_mul_f32_e32 v183, 0x43000000, v183
	ds_write_b128 v210, v[180:183] offset:1024
	v_mul_f32_e32 v184, 0x43000000, v184
	v_mul_f32_e32 v185, 0x43000000, v185
	v_mul_f32_e32 v186, 0x43000000, v186
	v_mul_f32_e32 v187, 0x43000000, v187
	ds_write_b128 v210, v[184:187] offset:2048
	v_mul_f32_e32 v188, 0x43000000, v188
	v_mul_f32_e32 v189, 0x43000000, v189
	v_mul_f32_e32 v190, 0x43000000, v190
	v_mul_f32_e32 v191, 0x43000000, v191
	ds_write_b128 v210, v[188:191] offset:3072
	v_mul_f32_e32 v192, 0x43000000, v192
	v_mul_f32_e32 v193, 0x43000000, v193
	v_mul_f32_e32 v194, 0x43000000, v194
	v_mul_f32_e32 v195, 0x43000000, v195
	ds_write_b128 v210, v[192:195] offset:4096
	v_mul_f32_e32 v196, 0x43000000, v196
	v_mul_f32_e32 v197, 0x43000000, v197
	v_mul_f32_e32 v198, 0x43000000, v198
	v_mul_f32_e32 v199, 0x43000000, v199
	ds_write_b128 v210, v[196:199] offset:5120
	v_mul_f32_e32 v200, 0x43000000, v200
	v_mul_f32_e32 v201, 0x43000000, v201
	v_mul_f32_e32 v202, 0x43000000, v202
	v_mul_f32_e32 v203, 0x43000000, v203
	ds_write_b128 v210, v[200:203] offset:6144
	v_mul_f32_e32 v204, 0x43000000, v204
	v_mul_f32_e32 v205, 0x43000000, v205
	v_mul_f32_e32 v206, 0x43000000, v206
	v_mul_f32_e32 v207, 0x43000000, v207
	ds_write_b128 v210, v[204:207] offset:7168
	s_waitcnt lgkmcnt(0)
	s_barrier
	s_add_u32 s8, s42, 0x4003000
	s_addc_u32 s9, s43, 0
	global_load_dwordx4 v[176:179], v75, s[8:9]
	s_add_u32 s8, s8, 0x8000
	s_addc_u32 s9, s9, 0
	global_load_dwordx4 v[180:183], v75, s[8:9]
	s_add_u32 s8, s8, 0x8000
	s_addc_u32 s9, s9, 0
	global_load_dwordx4 v[184:187], v75, s[8:9]
	s_add_u32 s8, s8, 0x8000
	s_addc_u32 s9, s9, 0
	global_load_dwordx4 v[188:191], v75, s[8:9]
	s_add_u32 s8, s8, 0x8000
	s_addc_u32 s9, s9, 0
	global_load_dwordx4 v[192:195], v75, s[8:9]
	s_add_u32 s8, s8, 0x8000
	s_addc_u32 s9, s9, 0
	global_load_dwordx4 v[196:199], v75, s[8:9]
	s_add_u32 s8, s8, 0x8000
	s_addc_u32 s9, s9, 0
	global_load_dwordx4 v[200:203], v75, s[8:9]
	s_add_u32 s8, s8, 0x8000
	s_addc_u32 s9, s9, 0
	global_load_dwordx4 v[204:207], v75, s[8:9]
	s_add_u32 s6, s44, 0x1001000
	s_addc_u32 s7, s45, 0
	ds_read_b32 v226, v212
	ds_read_b32 v227, v212 offset:512
	ds_read_b32 v228, v212 offset:1024
	ds_read_b32 v229, v212 offset:1536
	ds_read_b32 v230, v212 offset:2048
	ds_read_b32 v231, v212 offset:2560
	ds_read_b32 v232, v212 offset:3072
	ds_read_b32 v233, v212 offset:3584
	ds_read_b32 v234, v212 offset:4096
	ds_read_b32 v235, v212 offset:4608
	ds_read_b32 v236, v212 offset:5120
	ds_read_b32 v237, v212 offset:5632
	ds_read_b32 v238, v212 offset:6144
	ds_read_b32 v239, v212 offset:6656
	ds_read_b32 v240, v212 offset:7168
	ds_read_b32 v241, v212 offset:7680
	s_waitcnt lgkmcnt(0)
	v_max_f32_e32 v226, v226, v226
	v_max_f32_e32 v227, v227, v227
	v_max_f32_e32 v228, v228, v228
	v_max_f32_e32 v229, v229, v229
	v_max_f32_e32 v230, v230, v230
	v_max_f32_e32 v231, v231, v231
	v_max_f32_e32 v232, v232, v232
	v_max_f32_e32 v233, v233, v233
	v_max_f32_e32 v234, v234, v234
	v_max_f32_e32 v235, v235, v235
	v_max_f32_e32 v236, v236, v236
	v_max_f32_e32 v237, v237, v237
	v_max_f32_e32 v238, v238, v238
	v_max_f32_e32 v239, v239, v239
	v_max_f32_e32 v240, v240, v240
	v_max_f32_e32 v241, v241, v241
	v_med3_f32 v226, v226, s62, v95
	v_med3_f32 v227, v227, s62, v95
	v_med3_f32 v228, v228, s62, v95
	v_med3_f32 v229, v229, s62, v95
	v_med3_f32 v230, v230, s62, v95
	v_med3_f32 v231, v231, s62, v95
	v_med3_f32 v232, v232, s62, v95
	v_med3_f32 v233, v233, s62, v95
	v_med3_f32 v234, v234, s62, v95
	v_med3_f32 v235, v235, s62, v95
	v_med3_f32 v236, v236, s62, v95
	v_med3_f32 v237, v237, s62, v95
	v_med3_f32 v238, v238, s62, v95
	v_med3_f32 v239, v239, s62, v95
	v_med3_f32 v240, v240, s62, v95
	v_med3_f32 v241, v241, s62, v95
	v_mov_b32_e32 v242, 0
	v_mov_b32_e32 v243, 0
	v_mov_b32_e32 v244, 0
	v_mov_b32_e32 v245, 0
	v_cvt_pk_fp8_f32 v242, v226, v227
	v_cvt_pk_fp8_f32 v243, v230, v231
	v_cvt_pk_fp8_f32 v244, v234, v235
	v_cvt_pk_fp8_f32 v245, v238, v239
	v_cvt_pk_fp8_f32 v242, v228, v229 op_sel:[0,0,1]
	v_cvt_pk_fp8_f32 v243, v232, v233 op_sel:[0,0,1]
	v_cvt_pk_fp8_f32 v244, v236, v237 op_sel:[0,0,1]
	v_cvt_pk_fp8_f32 v245, v240, v241 op_sel:[0,0,1]
	s_nop 0
	global_store_dwordx4 v79, v[242:245], s[6:7]
	ds_read_b32 v226, v214
	ds_read_b32 v227, v214 offset:512
	ds_read_b32 v228, v214 offset:1024
	ds_read_b32 v229, v214 offset:1536
	ds_read_b32 v230, v214 offset:2048
	ds_read_b32 v231, v214 offset:2560
	ds_read_b32 v232, v214 offset:3072
	ds_read_b32 v233, v214 offset:3584
	ds_read_b32 v234, v214 offset:4096
	ds_read_b32 v235, v214 offset:4608
	ds_read_b32 v236, v214 offset:5120
	ds_read_b32 v237, v214 offset:5632
	ds_read_b32 v238, v214 offset:6144
	ds_read_b32 v239, v214 offset:6656
	ds_read_b32 v240, v214 offset:7168
	ds_read_b32 v241, v214 offset:7680
	s_waitcnt lgkmcnt(0)
; #define GAS __attribute__((address_space(1)))
; #define LAS __attribute__((address_space(3)))
; #define LDS_WAIT() asm volatile("s_waitcnt lgkmcnt(0)" ::: "memory")
;     const int pr = item >> 1, kb = 2 * (pr / nblk) + (item & 1), nb = pr % nblk, k0 = 64 * kb, n0 = 32 * nb;
;     const int nr = n0 + (lane & 31); const int sc = MAP == 1 ? src_col_in(nr) : nr;
;     float v[32];
; #pragma unroll
;     for (int i = 0; i < 32; ++i) v[i] = sc >= 0 ? W[(size_t)(k0 + 2 * i + (lane >> 5)) * Nsrc + sc] : 0.f;
; #pragma unroll
;     for (int i = 0; i < 32; ++i) { const int k = k0 + 2 * i + (lane >> 5); float x = v[i] * wscale; if (KS) x *= (k < ksplit ? ksA[k] : ksB[k - ksplit]); scr[(2 * i + (lane >> 5)) * 33 + (lane & 31)] = x; }
;     LDS_WAIT(); asm volatile("" ::: "memory");
;     const int c = lane & 7;
; #pragma unroll
;     for (int j = 0; j < 4; ++j) { const int n = (lane >> 3) + 8 * j; const LAS float* s = scr + (8 * c) * 33 + n;
;         const unsigned long long o = (unsigned long long)pg8::pk4_fp8(s[0 * 33], s[1 * 33], s[2 * 33], s[3 * 33]) | ((unsigned long long)pg8::pk4_fp8(s[4 * 33], s[5 * 33], s[6 * 33], s[7 * 33]) << 32);
;         *(GAS unsigned long long*)(WT + (size_t)(n0 + n) * K + k0 + 8 * c) = o; }
;     LDS_WAIT(); asm volatile("" ::: "memory");
; }
; __global__ void __launch_bounds__(NWAVES * 64, 2) hybrid_fwd(Args args) {
;     ...
;             p0_transpose_item_f8<false>(args.in[16] + (size_t)l * FF * DM, FF, DM, DM / 32, (unsigned char*)(ws + WS_WDN + l * SZ_WDN), 128.f, args.in[16], args.in[16], 0, scr, r, lane);
	v_max_f32_e32 v226, v226, v226
	v_max_f32_e32 v227, v227, v227
	v_max_f32_e32 v228, v228, v228
	v_max_f32_e32 v229, v229, v229
	v_max_f32_e32 v230, v230, v230
	v_max_f32_e32 v231, v231, v231
	v_max_f32_e32 v232, v232, v232
	v_max_f32_e32 v233, v233, v233
	v_max_f32_e32 v234, v234, v234
	v_max_f32_e32 v235, v235, v235
	v_max_f32_e32 v236, v236, v236
	v_max_f32_e32 v237, v237, v237
	v_max_f32_e32 v238, v238, v238
	v_max_f32_e32 v239, v239, v239
	v_max_f32_e32 v240, v240, v240
	v_max_f32_e32 v241, v241, v241
	v_med3_f32 v226, v226, s62, v95
	v_med3_f32 v227, v227, s62, v95
	v_med3_f32 v228, v228, s62, v95
	v_med3_f32 v229, v229, s62, v95
	v_med3_f32 v230, v230, s62, v95
	v_med3_f32 v231, v231, s62, v95
	v_med3_f32 v232, v232, s62, v95
	v_med3_f32 v233, v233, s62, v95
	v_med3_f32 v234, v234, s62, v95
	v_med3_f32 v235, v235, s62, v95
	v_med3_f32 v236, v236, s62, v95
	v_med3_f32 v237, v237, s62, v95
	v_med3_f32 v238, v238, s62, v95
	v_med3_f32 v239, v239, s62, v95
	v_med3_f32 v240, v240, s62, v95
	v_med3_f32 v241, v241, s62, v95
	v_mov_b32_e32 v242, 0
	v_mov_b32_e32 v243, 0
	v_mov_b32_e32 v244, 0
	v_mov_b32_e32 v245, 0
	v_cvt_pk_fp8_f32 v242, v226, v227
	v_cvt_pk_fp8_f32 v243, v230, v231
	v_cvt_pk_fp8_f32 v244, v234, v235
	v_cvt_pk_fp8_f32 v245, v238, v239
	v_cvt_pk_fp8_f32 v242, v228, v229 op_sel:[0,0,1]
	v_cvt_pk_fp8_f32 v243, v232, v233 op_sel:[0,0,1]
	v_cvt_pk_fp8_f32 v244, v236, v237 op_sel:[0,0,1]
	v_cvt_pk_fp8_f32 v245, v240, v241 op_sel:[0,0,1]
	s_nop 0
	global_store_dwordx4 v80, v[242:245], s[6:7]
	s_waitcnt vmcnt(12)
	v_mul_f32_e32 v144, 0x43000000, v144
	v_mul_f32_e32 v145, 0x43000000, v145
	v_mul_f32_e32 v146, 0x43000000, v146
	v_mul_f32_e32 v147, 0x43000000, v147
	ds_write_b128 v209, v[144:147]
	v_mul_f32_e32 v148, 0x43000000, v148
	v_mul_f32_e32 v149, 0x43000000, v149
	v_mul_f32_e32 v150, 0x43000000, v150
	v_mul_f32_e32 v151, 0x43000000, v151
	ds_write_b128 v209, v[148:151] offset:1024
	v_mul_f32_e32 v152, 0x43000000, v152
	v_mul_f32_e32 v153, 0x43000000, v153
	v_mul_f32_e32 v154, 0x43000000, v154
	v_mul_f32_e32 v155, 0x43000000, v155
	ds_write_b128 v209, v[152:155] offset:2048
	v_mul_f32_e32 v156, 0x43000000, v156
	v_mul_f32_e32 v157, 0x43000000, v157
	v_mul_f32_e32 v158, 0x43000000, v158
	v_mul_f32_e32 v159, 0x43000000, v159
	ds_write_b128 v209, v[156:159] offset:3072
	v_mul_f32_e32 v160, 0x43000000, v160
	v_mul_f32_e32 v161, 0x43000000, v161
	v_mul_f32_e32 v162, 0x43000000, v162
	v_mul_f32_e32 v163, 0x43000000, v163
	ds_write_b128 v209, v[160:163] offset:4096
	v_mul_f32_e32 v164, 0x43000000, v164
	v_mul_f32_e32 v165, 0x43000000, v165
	v_mul_f32_e32 v166, 0x43000000, v166
	v_mul_f32_e32 v167, 0x43000000, v167
	ds_write_b128 v209, v[164:167] offset:5120
	v_mul_f32_e32 v168, 0x43000000, v168
	v_mul_f32_e32 v169, 0x43000000, v169
	v_mul_f32_e32 v170, 0x43000000, v170
	v_mul_f32_e32 v171, 0x43000000, v171
	ds_write_b128 v209, v[168:171] offset:6144
	v_mul_f32_e32 v172, 0x43000000, v172
	v_mul_f32_e32 v173, 0x43000000, v173
	v_mul_f32_e32 v174, 0x43000000, v174
	v_mul_f32_e32 v175, 0x43000000, v175
	ds_write_b128 v209, v[172:175] offset:7168
	s_waitcnt lgkmcnt(0)
	s_barrier
	s_add_u32 s8, s42, 0x8000000
	s_addc_u32 s9, s43, 0
	global_load_dwordx4 v[144:147], v75, s[8:9]
	s_add_u32 s8, s8, 0x8000
	s_addc_u32 s9, s9, 0
	global_load_dwordx4 v[148:151], v75, s[8:9]
	s_add_u32 s8, s8, 0x8000
	s_addc_u32 s9, s9, 0
	global_load_dwordx4 v[152:155], v75, s[8:9]
	s_add_u32 s8, s8, 0x8000
	s_addc_u32 s9, s9, 0
	global_load_dwordx4 v[156:159], v75, s[8:9]
	s_add_u32 s8, s8, 0x8000
	s_addc_u32 s9, s9, 0
	global_load_dwordx4 v[160:163], v75, s[8:9]
	s_add_u32 s8, s8, 0x8000
	s_addc_u32 s9, s9, 0
	global_load_dwordx4 v[164:167], v75, s[8:9]
	s_add_u32 s8, s8, 0x8000
	s_addc_u32 s9, s9, 0
	global_load_dwordx4 v[168:171], v75, s[8:9]
	s_add_u32 s8, s8, 0x8000
	s_addc_u32 s9, s9, 0
	global_load_dwordx4 v[172:175], v75, s[8:9]
	s_add_u32 s6, s44, 0x2001000
	s_addc_u32 s7, s45, 0
	ds_read_b32 v226, v211
	ds_read_b32 v227, v211 offset:512
	ds_read_b32 v228, v211 offset:1024
	ds_read_b32 v229, v211 offset:1536
	ds_read_b32 v230, v211 offset:2048
	ds_read_b32 v231, v211 offset:2560
	ds_read_b32 v232, v211 offset:3072
	ds_read_b32 v233, v211 offset:3584
	ds_read_b32 v234, v211 offset:4096
	ds_read_b32 v235, v211 offset:4608
	ds_read_b32 v236, v211 offset:5120
	ds_read_b32 v237, v211 offset:5632
	ds_read_b32 v238, v211 offset:6144
	ds_read_b32 v239, v211 offset:6656
	ds_read_b32 v240, v211 offset:7168
	ds_read_b32 v241, v211 offset:7680
	s_waitcnt lgkmcnt(0)
	v_max_f32_e32 v226, v226, v226
	v_max_f32_e32 v227, v227, v227
	v_max_f32_e32 v228, v228, v228
	v_max_f32_e32 v229, v229, v229
	v_max_f32_e32 v230, v230, v230
	v_max_f32_e32 v231, v231, v231
	v_max_f32_e32 v232, v232, v232
	v_max_f32_e32 v233, v233, v233
	v_max_f32_e32 v234, v234, v234
	v_max_f32_e32 v235, v235, v235
	v_max_f32_e32 v236, v236, v236
	v_max_f32_e32 v237, v237, v237
	v_max_f32_e32 v238, v238, v238
	v_max_f32_e32 v239, v239, v239
	v_max_f32_e32 v240, v240, v240
	v_max_f32_e32 v241, v241, v241
	v_med3_f32 v226, v226, s62, v95
	v_med3_f32 v227, v227, s62, v95
	v_med3_f32 v228, v228, s62, v95
	v_med3_f32 v229, v229, s62, v95
	v_med3_f32 v230, v230, s62, v95
	v_med3_f32 v231, v231, s62, v95
	v_med3_f32 v232, v232, s62, v95
	v_med3_f32 v233, v233, s62, v95
	v_med3_f32 v234, v234, s62, v95
	v_med3_f32 v235, v235, s62, v95
	v_med3_f32 v236, v236, s62, v95
	v_med3_f32 v237, v237, s62, v95
	v_med3_f32 v238, v238, s62, v95
	v_med3_f32 v239, v239, s62, v95
	v_med3_f32 v240, v240, s62, v95
	v_med3_f32 v241, v241, s62, v95
	v_mov_b32_e32 v242, 0
	v_mov_b32_e32 v243, 0
	v_mov_b32_e32 v244, 0
	v_mov_b32_e32 v245, 0
	v_cvt_pk_fp8_f32 v242, v226, v227
	v_cvt_pk_fp8_f32 v243, v230, v231
	v_cvt_pk_fp8_f32 v244, v234, v235
	v_cvt_pk_fp8_f32 v245, v238, v239
	v_cvt_pk_fp8_f32 v242, v228, v229 op_sel:[0,0,1]
	v_cvt_pk_fp8_f32 v243, v232, v233 op_sel:[0,0,1]
	v_cvt_pk_fp8_f32 v244, v236, v237 op_sel:[0,0,1]
	v_cvt_pk_fp8_f32 v245, v240, v241 op_sel:[0,0,1]
	s_nop 0
	global_store_dwordx4 v79, v[242:245], s[6:7]
	ds_read_b32 v226, v213
	ds_read_b32 v227, v213 offset:512
	ds_read_b32 v228, v213 offset:1024
	ds_read_b32 v229, v213 offset:1536
	ds_read_b32 v230, v213 offset:2048
	ds_read_b32 v231, v213 offset:2560
	ds_read_b32 v232, v213 offset:3072
	ds_read_b32 v233, v213 offset:3584
	ds_read_b32 v234, v213 offset:4096
	ds_read_b32 v235, v213 offset:4608
	ds_read_b32 v236, v213 offset:5120
	ds_read_b32 v237, v213 offset:5632
	ds_read_b32 v238, v213 offset:6144
	ds_read_b32 v239, v213 offset:6656
	ds_read_b32 v240, v213 offset:7168
	ds_read_b32 v241, v213 offset:7680
	s_waitcnt lgkmcnt(0)
; #define GAS __attribute__((address_space(1)))
; #define LAS __attribute__((address_space(3)))
; #define LDS_WAIT() asm volatile("s_waitcnt lgkmcnt(0)" ::: "memory")
;     const int pr = item >> 1, kb = 2 * (pr / nblk) + (item & 1), nb = pr % nblk, k0 = 64 * kb, n0 = 32 * nb;
;     const int nr = n0 + (lane & 31); const int sc = MAP == 1 ? src_col_in(nr) : nr;
;     float v[32];
; #pragma unroll
;     for (int i = 0; i < 32; ++i) v[i] = sc >= 0 ? W[(size_t)(k0 + 2 * i + (lane >> 5)) * Nsrc + sc] : 0.f;
; #pragma unroll
;     for (int i = 0; i < 32; ++i) { const int k = k0 + 2 * i + (lane >> 5); float x = v[i] * wscale; if (KS) x *= (k < ksplit ? ksA[k] : ksB[k - ksplit]); scr[(2 * i + (lane >> 5)) * 33 + (lane & 31)] = x; }
;     LDS_WAIT(); asm volatile("" ::: "memory");
;     const int c = lane & 7;
; #pragma unroll
;     for (int j = 0; j < 4; ++j) { const int n = (lane >> 3) + 8 * j; const LAS float* s = scr + (8 * c) * 33 + n;
;         const unsigned long long o = (unsigned long long)pg8::pk4_fp8(s[0 * 33], s[1 * 33], s[2 * 33], s[3 * 33]) | ((unsigned long long)pg8::pk4_fp8(s[4 * 33], s[5 * 33], s[6 * 33], s[7 * 33]) << 32);
;         *(GAS unsigned long long*)(WT + (size_t)(n0 + n) * K + k0 + 8 * c) = o; }
;     LDS_WAIT(); asm volatile("" ::: "memory");
; }
; __global__ void __launch_bounds__(NWAVES * 64, 2) hybrid_fwd(Args args) {
;     ...
;             p0_transpose_item_f8<false>(args.in[16] + (size_t)l * FF * DM, FF, DM, DM / 32, (unsigned char*)(ws + WS_WDN + l * SZ_WDN), 128.f, args.in[16], args.in[16], 0, scr, r, lane);
	v_max_f32_e32 v226, v226, v226
	v_max_f32_e32 v227, v227, v227
	v_max_f32_e32 v228, v228, v228
	v_max_f32_e32 v229, v229, v229
	v_max_f32_e32 v230, v230, v230
	v_max_f32_e32 v231, v231, v231
	v_max_f32_e32 v232, v232, v232
	v_max_f32_e32 v233, v233, v233
	v_max_f32_e32 v234, v234, v234
	v_max_f32_e32 v235, v235, v235
	v_max_f32_e32 v236, v236, v236
	v_max_f32_e32 v237, v237, v237
	v_max_f32_e32 v238, v238, v238
	v_max_f32_e32 v239, v239, v239
	v_max_f32_e32 v240, v240, v240
	v_max_f32_e32 v241, v241, v241
	v_med3_f32 v226, v226, s62, v95
	v_med3_f32 v227, v227, s62, v95
	v_med3_f32 v228, v228, s62, v95
	v_med3_f32 v229, v229, s62, v95
	v_med3_f32 v230, v230, s62, v95
	v_med3_f32 v231, v231, s62, v95
	v_med3_f32 v232, v232, s62, v95
	v_med3_f32 v233, v233, s62, v95
	v_med3_f32 v234, v234, s62, v95
	v_med3_f32 v235, v235, s62, v95
	v_med3_f32 v236, v236, s62, v95
	v_med3_f32 v237, v237, s62, v95
	v_med3_f32 v238, v238, s62, v95
	v_med3_f32 v239, v239, s62, v95
	v_med3_f32 v240, v240, s62, v95
	v_med3_f32 v241, v241, s62, v95
	v_mov_b32_e32 v242, 0
	v_mov_b32_e32 v243, 0
	v_mov_b32_e32 v244, 0
	v_mov_b32_e32 v245, 0
	v_cvt_pk_fp8_f32 v242, v226, v227
	v_cvt_pk_fp8_f32 v243, v230, v231
	v_cvt_pk_fp8_f32 v244, v234, v235
	v_cvt_pk_fp8_f32 v245, v238, v239
	v_cvt_pk_fp8_f32 v242, v228, v229 op_sel:[0,0,1]
	v_cvt_pk_fp8_f32 v243, v232, v233 op_sel:[0,0,1]
	v_cvt_pk_fp8_f32 v244, v236, v237 op_sel:[0,0,1]
	v_cvt_pk_fp8_f32 v245, v240, v241 op_sel:[0,0,1]
	s_nop 0
	global_store_dwordx4 v80, v[242:245], s[6:7]
	s_waitcnt vmcnt(12)
	v_mul_f32_e32 v176, 0x43000000, v176
	v_mul_f32_e32 v177, 0x43000000, v177
	v_mul_f32_e32 v178, 0x43000000, v178
	v_mul_f32_e32 v179, 0x43000000, v179
	ds_write_b128 v210, v[176:179]
	v_mul_f32_e32 v180, 0x43000000, v180
	v_mul_f32_e32 v181, 0x43000000, v181
	v_mul_f32_e32 v182, 0x43000000, v182
	v_mul_f32_e32 v183, 0x43000000, v183
	ds_write_b128 v210, v[180:183] offset:1024
	v_mul_f32_e32 v184, 0x43000000, v184
	v_mul_f32_e32 v185, 0x43000000, v185
	v_mul_f32_e32 v186, 0x43000000, v186
	v_mul_f32_e32 v187, 0x43000000, v187
	ds_write_b128 v210, v[184:187] offset:2048
	v_mul_f32_e32 v188, 0x43000000, v188
	v_mul_f32_e32 v189, 0x43000000, v189
	v_mul_f32_e32 v190, 0x43000000, v190
	v_mul_f32_e32 v191, 0x43000000, v191
	ds_write_b128 v210, v[188:191] offset:3072
	v_mul_f32_e32 v192, 0x43000000, v192
	v_mul_f32_e32 v193, 0x43000000, v193
	v_mul_f32_e32 v194, 0x43000000, v194
	v_mul_f32_e32 v195, 0x43000000, v195
	ds_write_b128 v210, v[192:195] offset:4096
	v_mul_f32_e32 v196, 0x43000000, v196
	v_mul_f32_e32 v197, 0x43000000, v197
	v_mul_f32_e32 v198, 0x43000000, v198
	v_mul_f32_e32 v199, 0x43000000, v199
	ds_write_b128 v210, v[196:199] offset:5120
	v_mul_f32_e32 v200, 0x43000000, v200
	v_mul_f32_e32 v201, 0x43000000, v201
	v_mul_f32_e32 v202, 0x43000000, v202
	v_mul_f32_e32 v203, 0x43000000, v203
	ds_write_b128 v210, v[200:203] offset:6144
	v_mul_f32_e32 v204, 0x43000000, v204
	v_mul_f32_e32 v205, 0x43000000, v205
	v_mul_f32_e32 v206, 0x43000000, v206
	v_mul_f32_e32 v207, 0x43000000, v207
	ds_write_b128 v210, v[204:207] offset:7168
	s_waitcnt lgkmcnt(0)
	s_barrier
	s_add_u32 s8, s42, 0x8001000
	s_addc_u32 s9, s43, 0
	global_load_dwordx4 v[176:179], v75, s[8:9]
	s_add_u32 s8, s8, 0x8000
	s_addc_u32 s9, s9, 0
	global_load_dwordx4 v[180:183], v75, s[8:9]
	s_add_u32 s8, s8, 0x8000
	s_addc_u32 s9, s9, 0
	global_load_dwordx4 v[184:187], v75, s[8:9]
	s_add_u32 s8, s8, 0x8000
	s_addc_u32 s9, s9, 0
	global_load_dwordx4 v[188:191], v75, s[8:9]
	s_add_u32 s8, s8, 0x8000
	s_addc_u32 s9, s9, 0
	global_load_dwordx4 v[192:195], v75, s[8:9]
	s_add_u32 s8, s8, 0x8000
	s_addc_u32 s9, s9, 0
	global_load_dwordx4 v[196:199], v75, s[8:9]
	s_add_u32 s8, s8, 0x8000
	s_addc_u32 s9, s9, 0
	global_load_dwordx4 v[200:203], v75, s[8:9]
	s_add_u32 s8, s8, 0x8000
	s_addc_u32 s9, s9, 0
	global_load_dwordx4 v[204:207], v75, s[8:9]
	s_add_u32 s6, s44, 0x3001000
	s_addc_u32 s7, s45, 0
	ds_read_b32 v226, v212
	ds_read_b32 v227, v212 offset:512
	ds_read_b32 v228, v212 offset:1024
	ds_read_b32 v229, v212 offset:1536
	ds_read_b32 v230, v212 offset:2048
	ds_read_b32 v231, v212 offset:2560
	ds_read_b32 v232, v212 offset:3072
	ds_read_b32 v233, v212 offset:3584
	ds_read_b32 v234, v212 offset:4096
	ds_read_b32 v235, v212 offset:4608
	ds_read_b32 v236, v212 offset:5120
	ds_read_b32 v237, v212 offset:5632
	ds_read_b32 v238, v212 offset:6144
	ds_read_b32 v239, v212 offset:6656
	ds_read_b32 v240, v212 offset:7168
	ds_read_b32 v241, v212 offset:7680
	s_waitcnt lgkmcnt(0)
	v_max_f32_e32 v226, v226, v226
	v_max_f32_e32 v227, v227, v227
	v_max_f32_e32 v228, v228, v228
	v_max_f32_e32 v229, v229, v229
	v_max_f32_e32 v230, v230, v230
	v_max_f32_e32 v231, v231, v231
	v_max_f32_e32 v232, v232, v232
	v_max_f32_e32 v233, v233, v233
	v_max_f32_e32 v234, v234, v234
	v_max_f32_e32 v235, v235, v235
	v_max_f32_e32 v236, v236, v236
	v_max_f32_e32 v237, v237, v237
	v_max_f32_e32 v238, v238, v238
	v_max_f32_e32 v239, v239, v239
	v_max_f32_e32 v240, v240, v240
	v_max_f32_e32 v241, v241, v241
	v_med3_f32 v226, v226, s62, v95
	v_med3_f32 v227, v227, s62, v95
	v_med3_f32 v228, v228, s62, v95
	v_med3_f32 v229, v229, s62, v95
	v_med3_f32 v230, v230, s62, v95
	v_med3_f32 v231, v231, s62, v95
	v_med3_f32 v232, v232, s62, v95
	v_med3_f32 v233, v233, s62, v95
	v_med3_f32 v234, v234, s62, v95
	v_med3_f32 v235, v235, s62, v95
	v_med3_f32 v236, v236, s62, v95
	v_med3_f32 v237, v237, s62, v95
	v_med3_f32 v238, v238, s62, v95
	v_med3_f32 v239, v239, s62, v95
	v_med3_f32 v240, v240, s62, v95
	v_med3_f32 v241, v241, s62, v95
	v_mov_b32_e32 v242, 0
	v_mov_b32_e32 v243, 0
	v_mov_b32_e32 v244, 0
	v_mov_b32_e32 v245, 0
	v_cvt_pk_fp8_f32 v242, v226, v227
	v_cvt_pk_fp8_f32 v243, v230, v231
	v_cvt_pk_fp8_f32 v244, v234, v235
	v_cvt_pk_fp8_f32 v245, v238, v239
	v_cvt_pk_fp8_f32 v242, v228, v229 op_sel:[0,0,1]
	v_cvt_pk_fp8_f32 v243, v232, v233 op_sel:[0,0,1]
	v_cvt_pk_fp8_f32 v244, v236, v237 op_sel:[0,0,1]
	v_cvt_pk_fp8_f32 v245, v240, v241 op_sel:[0,0,1]
	s_nop 0
	global_store_dwordx4 v79, v[242:245], s[6:7]
	ds_read_b32 v226, v214
	ds_read_b32 v227, v214 offset:512
	ds_read_b32 v228, v214 offset:1024
	ds_read_b32 v229, v214 offset:1536
	ds_read_b32 v230, v214 offset:2048
	ds_read_b32 v231, v214 offset:2560
	ds_read_b32 v232, v214 offset:3072
	ds_read_b32 v233, v214 offset:3584
	ds_read_b32 v234, v214 offset:4096
	ds_read_b32 v235, v214 offset:4608
	ds_read_b32 v236, v214 offset:5120
	ds_read_b32 v237, v214 offset:5632
	ds_read_b32 v238, v214 offset:6144
	ds_read_b32 v239, v214 offset:6656
	ds_read_b32 v240, v214 offset:7168
	ds_read_b32 v241, v214 offset:7680
	s_waitcnt lgkmcnt(0)
; #define GAS __attribute__((address_space(1)))
; #define LAS __attribute__((address_space(3)))
; #define LDS_WAIT() asm volatile("s_waitcnt lgkmcnt(0)" ::: "memory")
;     const int pr = item >> 1, kb = 2 * (pr / nblk) + (item & 1), nb = pr % nblk, k0 = 64 * kb, n0 = 32 * nb;
;     const int nr = n0 + (lane & 31); const int sc = MAP == 1 ? src_col_in(nr) : nr;
;     float v[32];
; #pragma unroll
;     for (int i = 0; i < 32; ++i) v[i] = sc >= 0 ? W[(size_t)(k0 + 2 * i + (lane >> 5)) * Nsrc + sc] : 0.f;
; #pragma unroll
;     for (int i = 0; i < 32; ++i) { const int k = k0 + 2 * i + (lane >> 5); float x = v[i] * wscale; if (KS) x *= (k < ksplit ? ksA[k] : ksB[k - ksplit]); scr[(2 * i + (lane >> 5)) * 33 + (lane & 31)] = x; }
;     LDS_WAIT(); asm volatile("" ::: "memory");
;     const int c = lane & 7;
; #pragma unroll
;     for (int j = 0; j < 4; ++j) { const int n = (lane >> 3) + 8 * j; const LAS float* s = scr + (8 * c) * 33 + n;
;         const unsigned long long o = (unsigned long long)pg8::pk4_fp8(s[0 * 33], s[1 * 33], s[2 * 33], s[3 * 33]) | ((unsigned long long)pg8::pk4_fp8(s[4 * 33], s[5 * 33], s[6 * 33], s[7 * 33]) << 32);
;         *(GAS unsigned long long*)(WT + (size_t)(n0 + n) * K + k0 + 8 * c) = o; }
;     LDS_WAIT(); asm volatile("" ::: "memory");
; }
; __global__ void __launch_bounds__(NWAVES * 64, 2) hybrid_fwd(Args args) {
;     ...
;             p0_transpose_item_f8<false>(args.in[16] + (size_t)l * FF * DM, FF, DM, DM / 32, (unsigned char*)(ws + WS_WDN + l * SZ_WDN), 128.f, args.in[16], args.in[16], 0, scr, r, lane);
	v_max_f32_e32 v226, v226, v226
	v_max_f32_e32 v227, v227, v227
	v_max_f32_e32 v228, v228, v228
	v_max_f32_e32 v229, v229, v229
	v_max_f32_e32 v230, v230, v230
	v_max_f32_e32 v231, v231, v231
	v_max_f32_e32 v232, v232, v232
	v_max_f32_e32 v233, v233, v233
	v_max_f32_e32 v234, v234, v234
	v_max_f32_e32 v235, v235, v235
	v_max_f32_e32 v236, v236, v236
	v_max_f32_e32 v237, v237, v237
	v_max_f32_e32 v238, v238, v238
	v_max_f32_e32 v239, v239, v239
	v_max_f32_e32 v240, v240, v240
	v_max_f32_e32 v241, v241, v241
	v_med3_f32 v226, v226, s62, v95
	v_med3_f32 v227, v227, s62, v95
	v_med3_f32 v228, v228, s62, v95
	v_med3_f32 v229, v229, s62, v95
	v_med3_f32 v230, v230, s62, v95
	v_med3_f32 v231, v231, s62, v95
	v_med3_f32 v232, v232, s62, v95
	v_med3_f32 v233, v233, s62, v95
	v_med3_f32 v234, v234, s62, v95
	v_med3_f32 v235, v235, s62, v95
	v_med3_f32 v236, v236, s62, v95
	v_med3_f32 v237, v237, s62, v95
	v_med3_f32 v238, v238, s62, v95
	v_med3_f32 v239, v239, s62, v95
	v_med3_f32 v240, v240, s62, v95
	v_med3_f32 v241, v241, s62, v95
	v_mov_b32_e32 v242, 0
	v_mov_b32_e32 v243, 0
	v_mov_b32_e32 v244, 0
	v_mov_b32_e32 v245, 0
	v_cvt_pk_fp8_f32 v242, v226, v227
	v_cvt_pk_fp8_f32 v243, v230, v231
	v_cvt_pk_fp8_f32 v244, v234, v235
	v_cvt_pk_fp8_f32 v245, v238, v239
	v_cvt_pk_fp8_f32 v242, v228, v229 op_sel:[0,0,1]
	v_cvt_pk_fp8_f32 v243, v232, v233 op_sel:[0,0,1]
	v_cvt_pk_fp8_f32 v244, v236, v237 op_sel:[0,0,1]
	v_cvt_pk_fp8_f32 v245, v240, v241 op_sel:[0,0,1]
	s_nop 0
	global_store_dwordx4 v80, v[242:245], s[6:7]
	s_waitcnt vmcnt(12)
	v_mul_f32_e32 v144, 0x43000000, v144
	v_mul_f32_e32 v145, 0x43000000, v145
	v_mul_f32_e32 v146, 0x43000000, v146
	v_mul_f32_e32 v147, 0x43000000, v147
	ds_write_b128 v209, v[144:147]
	v_mul_f32_e32 v148, 0x43000000, v148
	v_mul_f32_e32 v149, 0x43000000, v149
	v_mul_f32_e32 v150, 0x43000000, v150
	v_mul_f32_e32 v151, 0x43000000, v151
	ds_write_b128 v209, v[148:151] offset:1024
	v_mul_f32_e32 v152, 0x43000000, v152
	v_mul_f32_e32 v153, 0x43000000, v153
	v_mul_f32_e32 v154, 0x43000000, v154
	v_mul_f32_e32 v155, 0x43000000, v155
	ds_write_b128 v209, v[152:155] offset:2048
	v_mul_f32_e32 v156, 0x43000000, v156
	v_mul_f32_e32 v157, 0x43000000, v157
	v_mul_f32_e32 v158, 0x43000000, v158
	v_mul_f32_e32 v159, 0x43000000, v159
	ds_write_b128 v209, v[156:159] offset:3072
	v_mul_f32_e32 v160, 0x43000000, v160
	v_mul_f32_e32 v161, 0x43000000, v161
	v_mul_f32_e32 v162, 0x43000000, v162
	v_mul_f32_e32 v163, 0x43000000, v163
	ds_write_b128 v209, v[160:163] offset:4096
	v_mul_f32_e32 v164, 0x43000000, v164
	v_mul_f32_e32 v165, 0x43000000, v165
	v_mul_f32_e32 v166, 0x43000000, v166
	v_mul_f32_e32 v167, 0x43000000, v167
	ds_write_b128 v209, v[164:167] offset:5120
	v_mul_f32_e32 v168, 0x43000000, v168
	v_mul_f32_e32 v169, 0x43000000, v169
	v_mul_f32_e32 v170, 0x43000000, v170
	v_mul_f32_e32 v171, 0x43000000, v171
	ds_write_b128 v209, v[168:171] offset:6144
	v_mul_f32_e32 v172, 0x43000000, v172
	v_mul_f32_e32 v173, 0x43000000, v173
	v_mul_f32_e32 v174, 0x43000000, v174
	v_mul_f32_e32 v175, 0x43000000, v175
	ds_write_b128 v209, v[172:175] offset:7168
	s_waitcnt lgkmcnt(0)
	s_barrier
	s_add_u32 s8, s42, 0x8002000
	s_addc_u32 s9, s43, 0
	global_load_dwordx4 v[144:147], v75, s[8:9]
	s_add_u32 s8, s8, 0x8000
	s_addc_u32 s9, s9, 0
	global_load_dwordx4 v[148:151], v75, s[8:9]
	s_add_u32 s8, s8, 0x8000
	s_addc_u32 s9, s9, 0
	global_load_dwordx4 v[152:155], v75, s[8:9]
	s_add_u32 s8, s8, 0x8000
	s_addc_u32 s9, s9, 0
	global_load_dwordx4 v[156:159], v75, s[8:9]
	s_add_u32 s8, s8, 0x8000
	s_addc_u32 s9, s9, 0
	global_load_dwordx4 v[160:163], v75, s[8:9]
	s_add_u32 s8, s8, 0x8000
	s_addc_u32 s9, s9, 0
	global_load_dwordx4 v[164:167], v75, s[8:9]
	s_add_u32 s8, s8, 0x8000
	s_addc_u32 s9, s9, 0
	global_load_dwordx4 v[168:171], v75, s[8:9]
	s_add_u32 s8, s8, 0x8000
	s_addc_u32 s9, s9, 0
	global_load_dwordx4 v[172:175], v75, s[8:9]
	s_add_u32 s6, s44, 0x2000
	s_addc_u32 s7, s45, 0
	ds_read_b32 v226, v211
	ds_read_b32 v227, v211 offset:512
	ds_read_b32 v228, v211 offset:1024
	ds_read_b32 v229, v211 offset:1536
	ds_read_b32 v230, v211 offset:2048
	ds_read_b32 v231, v211 offset:2560
	ds_read_b32 v232, v211 offset:3072
	ds_read_b32 v233, v211 offset:3584
	ds_read_b32 v234, v211 offset:4096
	ds_read_b32 v235, v211 offset:4608
	ds_read_b32 v236, v211 offset:5120
	ds_read_b32 v237, v211 offset:5632
	ds_read_b32 v238, v211 offset:6144
	ds_read_b32 v239, v211 offset:6656
	ds_read_b32 v240, v211 offset:7168
	ds_read_b32 v241, v211 offset:7680
	s_waitcnt lgkmcnt(0)
	v_max_f32_e32 v226, v226, v226
	v_max_f32_e32 v227, v227, v227
	v_max_f32_e32 v228, v228, v228
	v_max_f32_e32 v229, v229, v229
	v_max_f32_e32 v230, v230, v230
	v_max_f32_e32 v231, v231, v231
	v_max_f32_e32 v232, v232, v232
	v_max_f32_e32 v233, v233, v233
	v_max_f32_e32 v234, v234, v234
	v_max_f32_e32 v235, v235, v235
	v_max_f32_e32 v236, v236, v236
	v_max_f32_e32 v237, v237, v237
	v_max_f32_e32 v238, v238, v238
	v_max_f32_e32 v239, v239, v239
	v_max_f32_e32 v240, v240, v240
	v_max_f32_e32 v241, v241, v241
	v_med3_f32 v226, v226, s62, v95
	v_med3_f32 v227, v227, s62, v95
	v_med3_f32 v228, v228, s62, v95
	v_med3_f32 v229, v229, s62, v95
	v_med3_f32 v230, v230, s62, v95
	v_med3_f32 v231, v231, s62, v95
	v_med3_f32 v232, v232, s62, v95
	v_med3_f32 v233, v233, s62, v95
	v_med3_f32 v234, v234, s62, v95
	v_med3_f32 v235, v235, s62, v95
	v_med3_f32 v236, v236, s62, v95
	v_med3_f32 v237, v237, s62, v95
	v_med3_f32 v238, v238, s62, v95
	v_med3_f32 v239, v239, s62, v95
	v_med3_f32 v240, v240, s62, v95
	v_med3_f32 v241, v241, s62, v95
	v_mov_b32_e32 v242, 0
	v_mov_b32_e32 v243, 0
	v_mov_b32_e32 v244, 0
	v_mov_b32_e32 v245, 0
	v_cvt_pk_fp8_f32 v242, v226, v227
	v_cvt_pk_fp8_f32 v243, v230, v231
	v_cvt_pk_fp8_f32 v244, v234, v235
	v_cvt_pk_fp8_f32 v245, v238, v239
	v_cvt_pk_fp8_f32 v242, v228, v229 op_sel:[0,0,1]
	v_cvt_pk_fp8_f32 v243, v232, v233 op_sel:[0,0,1]
	v_cvt_pk_fp8_f32 v244, v236, v237 op_sel:[0,0,1]
	v_cvt_pk_fp8_f32 v245, v240, v241 op_sel:[0,0,1]
	s_nop 0
	global_store_dwordx4 v79, v[242:245], s[6:7]
	ds_read_b32 v226, v213
	ds_read_b32 v227, v213 offset:512
	ds_read_b32 v228, v213 offset:1024
	ds_read_b32 v229, v213 offset:1536
	ds_read_b32 v230, v213 offset:2048
	ds_read_b32 v231, v213 offset:2560
	ds_read_b32 v232, v213 offset:3072
	ds_read_b32 v233, v213 offset:3584
	ds_read_b32 v234, v213 offset:4096
	ds_read_b32 v235, v213 offset:4608
	ds_read_b32 v236, v213 offset:5120
	ds_read_b32 v237, v213 offset:5632
	ds_read_b32 v238, v213 offset:6144
	ds_read_b32 v239, v213 offset:6656
	ds_read_b32 v240, v213 offset:7168
	ds_read_b32 v241, v213 offset:7680
	s_waitcnt lgkmcnt(0)
; #define GAS __attribute__((address_space(1)))
; #define LAS __attribute__((address_space(3)))
; #define LDS_WAIT() asm volatile("s_waitcnt lgkmcnt(0)" ::: "memory")
;     const int pr = item >> 1, kb = 2 * (pr / nblk) + (item & 1), nb = pr % nblk, k0 = 64 * kb, n0 = 32 * nb;
;     const int nr = n0 + (lane & 31); const int sc = MAP == 1 ? src_col_in(nr) : nr;
;     float v[32];
; #pragma unroll
;     for (int i = 0; i < 32; ++i) v[i] = sc >= 0 ? W[(size_t)(k0 + 2 * i + (lane >> 5)) * Nsrc + sc] : 0.f;
; #pragma unroll
;     for (int i = 0; i < 32; ++i) { const int k = k0 + 2 * i + (lane >> 5); float x = v[i] * wscale; if (KS) x *= (k < ksplit ? ksA[k] : ksB[k - ksplit]); scr[(2 * i + (lane >> 5)) * 33 + (lane & 31)] = x; }
;     LDS_WAIT(); asm volatile("" ::: "memory");
;     const int c = lane & 7;
; #pragma unroll
;     for (int j = 0; j < 4; ++j) { const int n = (lane >> 3) + 8 * j; const LAS float* s = scr + (8 * c) * 33 + n;
;         const unsigned long long o = (unsigned long long)pg8::pk4_fp8(s[0 * 33], s[1 * 33], s[2 * 33], s[3 * 33]) | ((unsigned long long)pg8::pk4_fp8(s[4 * 33], s[5 * 33], s[6 * 33], s[7 * 33]) << 32);
;         *(GAS unsigned long long*)(WT + (size_t)(n0 + n) * K + k0 + 8 * c) = o; }
;     LDS_WAIT(); asm volatile("" ::: "memory");
; }
; __global__ void __launch_bounds__(NWAVES * 64, 2) hybrid_fwd(Args args) {
;     ...
;             p0_transpose_item_f8<false>(args.in[16] + (size_t)l * FF * DM, FF, DM, DM / 32, (unsigned char*)(ws + WS_WDN + l * SZ_WDN), 128.f, args.in[16], args.in[16], 0, scr, r, lane);
	v_max_f32_e32 v226, v226, v226
	v_max_f32_e32 v227, v227, v227
	v_max_f32_e32 v228, v228, v228
	v_max_f32_e32 v229, v229, v229
	v_max_f32_e32 v230, v230, v230
	v_max_f32_e32 v231, v231, v231
	v_max_f32_e32 v232, v232, v232
	v_max_f32_e32 v233, v233, v233
	v_max_f32_e32 v234, v234, v234
	v_max_f32_e32 v235, v235, v235
	v_max_f32_e32 v236, v236, v236
	v_max_f32_e32 v237, v237, v237
	v_max_f32_e32 v238, v238, v238
	v_max_f32_e32 v239, v239, v239
	v_max_f32_e32 v240, v240, v240
	v_max_f32_e32 v241, v241, v241
	v_med3_f32 v226, v226, s62, v95
	v_med3_f32 v227, v227, s62, v95
	v_med3_f32 v228, v228, s62, v95
	v_med3_f32 v229, v229, s62, v95
	v_med3_f32 v230, v230, s62, v95
	v_med3_f32 v231, v231, s62, v95
	v_med3_f32 v232, v232, s62, v95
	v_med3_f32 v233, v233, s62, v95
	v_med3_f32 v234, v234, s62, v95
	v_med3_f32 v235, v235, s62, v95
	v_med3_f32 v236, v236, s62, v95
	v_med3_f32 v237, v237, s62, v95
	v_med3_f32 v238, v238, s62, v95
	v_med3_f32 v239, v239, s62, v95
	v_med3_f32 v240, v240, s62, v95
	v_med3_f32 v241, v241, s62, v95
	v_mov_b32_e32 v242, 0
	v_mov_b32_e32 v243, 0
	v_mov_b32_e32 v244, 0
	v_mov_b32_e32 v245, 0
	v_cvt_pk_fp8_f32 v242, v226, v227
	v_cvt_pk_fp8_f32 v243, v230, v231
	v_cvt_pk_fp8_f32 v244, v234, v235
	v_cvt_pk_fp8_f32 v245, v238, v239
	v_cvt_pk_fp8_f32 v242, v228, v229 op_sel:[0,0,1]
	v_cvt_pk_fp8_f32 v243, v232, v233 op_sel:[0,0,1]
	v_cvt_pk_fp8_f32 v244, v236, v237 op_sel:[0,0,1]
	v_cvt_pk_fp8_f32 v245, v240, v241 op_sel:[0,0,1]
	s_nop 0
	global_store_dwordx4 v80, v[242:245], s[6:7]
	s_waitcnt vmcnt(12)
	v_mul_f32_e32 v176, 0x43000000, v176
	v_mul_f32_e32 v177, 0x43000000, v177
	v_mul_f32_e32 v178, 0x43000000, v178
	v_mul_f32_e32 v179, 0x43000000, v179
	ds_write_b128 v210, v[176:179]
	v_mul_f32_e32 v180, 0x43000000, v180
	v_mul_f32_e32 v181, 0x43000000, v181
	v_mul_f32_e32 v182, 0x43000000, v182
	v_mul_f32_e32 v183, 0x43000000, v183
	ds_write_b128 v210, v[180:183] offset:1024
	v_mul_f32_e32 v184, 0x43000000, v184
	v_mul_f32_e32 v185, 0x43000000, v185
	v_mul_f32_e32 v186, 0x43000000, v186
	v_mul_f32_e32 v187, 0x43000000, v187
	ds_write_b128 v210, v[184:187] offset:2048
	v_mul_f32_e32 v188, 0x43000000, v188
	v_mul_f32_e32 v189, 0x43000000, v189
	v_mul_f32_e32 v190, 0x43000000, v190
	v_mul_f32_e32 v191, 0x43000000, v191
	ds_write_b128 v210, v[188:191] offset:3072
	v_mul_f32_e32 v192, 0x43000000, v192
	v_mul_f32_e32 v193, 0x43000000, v193
	v_mul_f32_e32 v194, 0x43000000, v194
	v_mul_f32_e32 v195, 0x43000000, v195
	ds_write_b128 v210, v[192:195] offset:4096
	v_mul_f32_e32 v196, 0x43000000, v196
	v_mul_f32_e32 v197, 0x43000000, v197
	v_mul_f32_e32 v198, 0x43000000, v198
	v_mul_f32_e32 v199, 0x43000000, v199
	ds_write_b128 v210, v[196:199] offset:5120
	v_mul_f32_e32 v200, 0x43000000, v200
	v_mul_f32_e32 v201, 0x43000000, v201
	v_mul_f32_e32 v202, 0x43000000, v202
	v_mul_f32_e32 v203, 0x43000000, v203
	ds_write_b128 v210, v[200:203] offset:6144
	v_mul_f32_e32 v204, 0x43000000, v204
	v_mul_f32_e32 v205, 0x43000000, v205
	v_mul_f32_e32 v206, 0x43000000, v206
	v_mul_f32_e32 v207, 0x43000000, v207
	ds_write_b128 v210, v[204:207] offset:7168
	s_waitcnt lgkmcnt(0)
	s_barrier
	s_add_u32 s8, s42, 0x8003000
	s_addc_u32 s9, s43, 0
	global_load_dwordx4 v[176:179], v75, s[8:9]
	s_add_u32 s8, s8, 0x8000
	s_addc_u32 s9, s9, 0
	global_load_dwordx4 v[180:183], v75, s[8:9]
	s_add_u32 s8, s8, 0x8000
	s_addc_u32 s9, s9, 0
	global_load_dwordx4 v[184:187], v75, s[8:9]
	s_add_u32 s8, s8, 0x8000
	s_addc_u32 s9, s9, 0
	global_load_dwordx4 v[188:191], v75, s[8:9]
	s_add_u32 s8, s8, 0x8000
	s_addc_u32 s9, s9, 0
	global_load_dwordx4 v[192:195], v75, s[8:9]
	s_add_u32 s8, s8, 0x8000
	s_addc_u32 s9, s9, 0
	global_load_dwordx4 v[196:199], v75, s[8:9]
	s_add_u32 s8, s8, 0x8000
	s_addc_u32 s9, s9, 0
	global_load_dwordx4 v[200:203], v75, s[8:9]
	s_add_u32 s8, s8, 0x8000
	s_addc_u32 s9, s9, 0
	global_load_dwordx4 v[204:207], v75, s[8:9]
	s_add_u32 s6, s44, 0x1002000
	s_addc_u32 s7, s45, 0
	ds_read_b32 v226, v212
	ds_read_b32 v227, v212 offset:512
	ds_read_b32 v228, v212 offset:1024
	ds_read_b32 v229, v212 offset:1536
	ds_read_b32 v230, v212 offset:2048
	ds_read_b32 v231, v212 offset:2560
	ds_read_b32 v232, v212 offset:3072
	ds_read_b32 v233, v212 offset:3584
	ds_read_b32 v234, v212 offset:4096
	ds_read_b32 v235, v212 offset:4608
	ds_read_b32 v236, v212 offset:5120
	ds_read_b32 v237, v212 offset:5632
	ds_read_b32 v238, v212 offset:6144
	ds_read_b32 v239, v212 offset:6656
	ds_read_b32 v240, v212 offset:7168
	ds_read_b32 v241, v212 offset:7680
	s_waitcnt lgkmcnt(0)
	v_max_f32_e32 v226, v226, v226
	v_max_f32_e32 v227, v227, v227
	v_max_f32_e32 v228, v228, v228
	v_max_f32_e32 v229, v229, v229
	v_max_f32_e32 v230, v230, v230
	v_max_f32_e32 v231, v231, v231
	v_max_f32_e32 v232, v232, v232
	v_max_f32_e32 v233, v233, v233
	v_max_f32_e32 v234, v234, v234
	v_max_f32_e32 v235, v235, v235
	v_max_f32_e32 v236, v236, v236
	v_max_f32_e32 v237, v237, v237
	v_max_f32_e32 v238, v238, v238
	v_max_f32_e32 v239, v239, v239
	v_max_f32_e32 v240, v240, v240
	v_max_f32_e32 v241, v241, v241
	v_med3_f32 v226, v226, s62, v95
	v_med3_f32 v227, v227, s62, v95
	v_med3_f32 v228, v228, s62, v95
	v_med3_f32 v229, v229, s62, v95
	v_med3_f32 v230, v230, s62, v95
	v_med3_f32 v231, v231, s62, v95
	v_med3_f32 v232, v232, s62, v95
	v_med3_f32 v233, v233, s62, v95
	v_med3_f32 v234, v234, s62, v95
	v_med3_f32 v235, v235, s62, v95
	v_med3_f32 v236, v236, s62, v95
	v_med3_f32 v237, v237, s62, v95
	v_med3_f32 v238, v238, s62, v95
	v_med3_f32 v239, v239, s62, v95
	v_med3_f32 v240, v240, s62, v95
	v_med3_f32 v241, v241, s62, v95
	v_mov_b32_e32 v242, 0
	v_mov_b32_e32 v243, 0
	v_mov_b32_e32 v244, 0
	v_mov_b32_e32 v245, 0
	v_cvt_pk_fp8_f32 v242, v226, v227
	v_cvt_pk_fp8_f32 v243, v230, v231
	v_cvt_pk_fp8_f32 v244, v234, v235
	v_cvt_pk_fp8_f32 v245, v238, v239
	v_cvt_pk_fp8_f32 v242, v228, v229 op_sel:[0,0,1]
	v_cvt_pk_fp8_f32 v243, v232, v233 op_sel:[0,0,1]
	v_cvt_pk_fp8_f32 v244, v236, v237 op_sel:[0,0,1]
	v_cvt_pk_fp8_f32 v245, v240, v241 op_sel:[0,0,1]
	s_nop 0
	global_store_dwordx4 v79, v[242:245], s[6:7]
	ds_read_b32 v226, v214
	ds_read_b32 v227, v214 offset:512
	ds_read_b32 v228, v214 offset:1024
	ds_read_b32 v229, v214 offset:1536
	ds_read_b32 v230, v214 offset:2048
	ds_read_b32 v231, v214 offset:2560
	ds_read_b32 v232, v214 offset:3072
	ds_read_b32 v233, v214 offset:3584
	ds_read_b32 v234, v214 offset:4096
	ds_read_b32 v235, v214 offset:4608
	ds_read_b32 v236, v214 offset:5120
	ds_read_b32 v237, v214 offset:5632
	ds_read_b32 v238, v214 offset:6144
	ds_read_b32 v239, v214 offset:6656
	ds_read_b32 v240, v214 offset:7168
	ds_read_b32 v241, v214 offset:7680
	s_waitcnt lgkmcnt(0)
; #define GAS __attribute__((address_space(1)))
; #define LAS __attribute__((address_space(3)))
; #define LDS_WAIT() asm volatile("s_waitcnt lgkmcnt(0)" ::: "memory")
;     const int pr = item >> 1, kb = 2 * (pr / nblk) + (item & 1), nb = pr % nblk, k0 = 64 * kb, n0 = 32 * nb;
;     const int nr = n0 + (lane & 31); const int sc = MAP == 1 ? src_col_in(nr) : nr;
;     float v[32];
; #pragma unroll
;     for (int i = 0; i < 32; ++i) v[i] = sc >= 0 ? W[(size_t)(k0 + 2 * i + (lane >> 5)) * Nsrc + sc] : 0.f;
; #pragma unroll
;     for (int i = 0; i < 32; ++i) { const int k = k0 + 2 * i + (lane >> 5); float x = v[i] * wscale; if (KS) x *= (k < ksplit ? ksA[k] : ksB[k - ksplit]); scr[(2 * i + (lane >> 5)) * 33 + (lane & 31)] = x; }
;     LDS_WAIT(); asm volatile("" ::: "memory");
;     const int c = lane & 7;
; #pragma unroll
;     for (int j = 0; j < 4; ++j) { const int n = (lane >> 3) + 8 * j; const LAS float* s = scr + (8 * c) * 33 + n;
;         const unsigned long long o = (unsigned long long)pg8::pk4_fp8(s[0 * 33], s[1 * 33], s[2 * 33], s[3 * 33]) | ((unsigned long long)pg8::pk4_fp8(s[4 * 33], s[5 * 33], s[6 * 33], s[7 * 33]) << 32);
;         *(GAS unsigned long long*)(WT + (size_t)(n0 + n) * K + k0 + 8 * c) = o; }
;     LDS_WAIT(); asm volatile("" ::: "memory");
; }
; __global__ void __launch_bounds__(NWAVES * 64, 2) hybrid_fwd(Args args) {
;     ...
;             p0_transpose_item_f8<false>(args.in[16] + (size_t)l * FF * DM, FF, DM, DM / 32, (unsigned char*)(ws + WS_WDN + l * SZ_WDN), 128.f, args.in[16], args.in[16], 0, scr, r, lane);
	v_max_f32_e32 v226, v226, v226
	v_max_f32_e32 v227, v227, v227
	v_max_f32_e32 v228, v228, v228
	v_max_f32_e32 v229, v229, v229
	v_max_f32_e32 v230, v230, v230
	v_max_f32_e32 v231, v231, v231
	v_max_f32_e32 v232, v232, v232
	v_max_f32_e32 v233, v233, v233
	v_max_f32_e32 v234, v234, v234
	v_max_f32_e32 v235, v235, v235
	v_max_f32_e32 v236, v236, v236
	v_max_f32_e32 v237, v237, v237
	v_max_f32_e32 v238, v238, v238
	v_max_f32_e32 v239, v239, v239
	v_max_f32_e32 v240, v240, v240
	v_max_f32_e32 v241, v241, v241
	v_med3_f32 v226, v226, s62, v95
	v_med3_f32 v227, v227, s62, v95
	v_med3_f32 v228, v228, s62, v95
	v_med3_f32 v229, v229, s62, v95
	v_med3_f32 v230, v230, s62, v95
	v_med3_f32 v231, v231, s62, v95
	v_med3_f32 v232, v232, s62, v95
	v_med3_f32 v233, v233, s62, v95
	v_med3_f32 v234, v234, s62, v95
	v_med3_f32 v235, v235, s62, v95
	v_med3_f32 v236, v236, s62, v95
	v_med3_f32 v237, v237, s62, v95
	v_med3_f32 v238, v238, s62, v95
	v_med3_f32 v239, v239, s62, v95
	v_med3_f32 v240, v240, s62, v95
	v_med3_f32 v241, v241, s62, v95
	v_mov_b32_e32 v242, 0
	v_mov_b32_e32 v243, 0
	v_mov_b32_e32 v244, 0
	v_mov_b32_e32 v245, 0
	v_cvt_pk_fp8_f32 v242, v226, v227
	v_cvt_pk_fp8_f32 v243, v230, v231
	v_cvt_pk_fp8_f32 v244, v234, v235
	v_cvt_pk_fp8_f32 v245, v238, v239
	v_cvt_pk_fp8_f32 v242, v228, v229 op_sel:[0,0,1]
	v_cvt_pk_fp8_f32 v243, v232, v233 op_sel:[0,0,1]
	v_cvt_pk_fp8_f32 v244, v236, v237 op_sel:[0,0,1]
	v_cvt_pk_fp8_f32 v245, v240, v241 op_sel:[0,0,1]
	s_nop 0
	global_store_dwordx4 v80, v[242:245], s[6:7]
	s_waitcnt vmcnt(12)
	v_mul_f32_e32 v144, 0x43000000, v144
	v_mul_f32_e32 v145, 0x43000000, v145
	v_mul_f32_e32 v146, 0x43000000, v146
	v_mul_f32_e32 v147, 0x43000000, v147
	ds_write_b128 v209, v[144:147]
	v_mul_f32_e32 v148, 0x43000000, v148
	v_mul_f32_e32 v149, 0x43000000, v149
	v_mul_f32_e32 v150, 0x43000000, v150
	v_mul_f32_e32 v151, 0x43000000, v151
	ds_write_b128 v209, v[148:151] offset:1024
	v_mul_f32_e32 v152, 0x43000000, v152
	v_mul_f32_e32 v153, 0x43000000, v153
	v_mul_f32_e32 v154, 0x43000000, v154
	v_mul_f32_e32 v155, 0x43000000, v155
	ds_write_b128 v209, v[152:155] offset:2048
	v_mul_f32_e32 v156, 0x43000000, v156
	v_mul_f32_e32 v157, 0x43000000, v157
	v_mul_f32_e32 v158, 0x43000000, v158
	v_mul_f32_e32 v159, 0x43000000, v159
	ds_write_b128 v209, v[156:159] offset:3072
	v_mul_f32_e32 v160, 0x43000000, v160
	v_mul_f32_e32 v161, 0x43000000, v161
	v_mul_f32_e32 v162, 0x43000000, v162
	v_mul_f32_e32 v163, 0x43000000, v163
	ds_write_b128 v209, v[160:163] offset:4096
	v_mul_f32_e32 v164, 0x43000000, v164
	v_mul_f32_e32 v165, 0x43000000, v165
	v_mul_f32_e32 v166, 0x43000000, v166
	v_mul_f32_e32 v167, 0x43000000, v167
	ds_write_b128 v209, v[164:167] offset:5120
	v_mul_f32_e32 v168, 0x43000000, v168
	v_mul_f32_e32 v169, 0x43000000, v169
	v_mul_f32_e32 v170, 0x43000000, v170
	v_mul_f32_e32 v171, 0x43000000, v171
	ds_write_b128 v209, v[168:171] offset:6144
	v_mul_f32_e32 v172, 0x43000000, v172
	v_mul_f32_e32 v173, 0x43000000, v173
	v_mul_f32_e32 v174, 0x43000000, v174
	v_mul_f32_e32 v175, 0x43000000, v175
	ds_write_b128 v209, v[172:175] offset:7168
	s_waitcnt lgkmcnt(0)
	s_barrier
	s_add_u32 s8, s42, 0xc000000
	s_addc_u32 s9, s43, 0
	global_load_dwordx4 v[144:147], v75, s[8:9]
	s_add_u32 s8, s8, 0x8000
	s_addc_u32 s9, s9, 0
	global_load_dwordx4 v[148:151], v75, s[8:9]
	s_add_u32 s8, s8, 0x8000
	s_addc_u32 s9, s9, 0
	global_load_dwordx4 v[152:155], v75, s[8:9]
	s_add_u32 s8, s8, 0x8000
	s_addc_u32 s9, s9, 0
	global_load_dwordx4 v[156:159], v75, s[8:9]
	s_add_u32 s8, s8, 0x8000
	s_addc_u32 s9, s9, 0
	global_load_dwordx4 v[160:163], v75, s[8:9]
	s_add_u32 s8, s8, 0x8000
	s_addc_u32 s9, s9, 0
	global_load_dwordx4 v[164:167], v75, s[8:9]
	s_add_u32 s8, s8, 0x8000
	s_addc_u32 s9, s9, 0
	global_load_dwordx4 v[168:171], v75, s[8:9]
	s_add_u32 s8, s8, 0x8000
	s_addc_u32 s9, s9, 0
	global_load_dwordx4 v[172:175], v75, s[8:9]
	s_add_u32 s6, s44, 0x2002000
	s_addc_u32 s7, s45, 0
	ds_read_b32 v226, v211
	ds_read_b32 v227, v211 offset:512
	ds_read_b32 v228, v211 offset:1024
	ds_read_b32 v229, v211 offset:1536
	ds_read_b32 v230, v211 offset:2048
	ds_read_b32 v231, v211 offset:2560
	ds_read_b32 v232, v211 offset:3072
	ds_read_b32 v233, v211 offset:3584
	ds_read_b32 v234, v211 offset:4096
	ds_read_b32 v235, v211 offset:4608
	ds_read_b32 v236, v211 offset:5120
	ds_read_b32 v237, v211 offset:5632
	ds_read_b32 v238, v211 offset:6144
	ds_read_b32 v239, v211 offset:6656
	ds_read_b32 v240, v211 offset:7168
	ds_read_b32 v241, v211 offset:7680
	s_waitcnt lgkmcnt(0)
	v_max_f32_e32 v226, v226, v226
	v_max_f32_e32 v227, v227, v227
	v_max_f32_e32 v228, v228, v228
	v_max_f32_e32 v229, v229, v229
	v_max_f32_e32 v230, v230, v230
	v_max_f32_e32 v231, v231, v231
	v_max_f32_e32 v232, v232, v232
	v_max_f32_e32 v233, v233, v233
	v_max_f32_e32 v234, v234, v234
	v_max_f32_e32 v235, v235, v235
	v_max_f32_e32 v236, v236, v236
	v_max_f32_e32 v237, v237, v237
	v_max_f32_e32 v238, v238, v238
	v_max_f32_e32 v239, v239, v239
	v_max_f32_e32 v240, v240, v240
	v_max_f32_e32 v241, v241, v241
	v_med3_f32 v226, v226, s62, v95
	v_med3_f32 v227, v227, s62, v95
	v_med3_f32 v228, v228, s62, v95
	v_med3_f32 v229, v229, s62, v95
	v_med3_f32 v230, v230, s62, v95
	v_med3_f32 v231, v231, s62, v95
	v_med3_f32 v232, v232, s62, v95
	v_med3_f32 v233, v233, s62, v95
	v_med3_f32 v234, v234, s62, v95
	v_med3_f32 v235, v235, s62, v95
	v_med3_f32 v236, v236, s62, v95
	v_med3_f32 v237, v237, s62, v95
	v_med3_f32 v238, v238, s62, v95
	v_med3_f32 v239, v239, s62, v95
	v_med3_f32 v240, v240, s62, v95
	v_med3_f32 v241, v241, s62, v95
	v_mov_b32_e32 v242, 0
	v_mov_b32_e32 v243, 0
	v_mov_b32_e32 v244, 0
	v_mov_b32_e32 v245, 0
	v_cvt_pk_fp8_f32 v242, v226, v227
	v_cvt_pk_fp8_f32 v243, v230, v231
	v_cvt_pk_fp8_f32 v244, v234, v235
	v_cvt_pk_fp8_f32 v245, v238, v239
	v_cvt_pk_fp8_f32 v242, v228, v229 op_sel:[0,0,1]
	v_cvt_pk_fp8_f32 v243, v232, v233 op_sel:[0,0,1]
	v_cvt_pk_fp8_f32 v244, v236, v237 op_sel:[0,0,1]
	v_cvt_pk_fp8_f32 v245, v240, v241 op_sel:[0,0,1]
	s_nop 0
	global_store_dwordx4 v79, v[242:245], s[6:7]
	ds_read_b32 v226, v213
	ds_read_b32 v227, v213 offset:512
	ds_read_b32 v228, v213 offset:1024
	ds_read_b32 v229, v213 offset:1536
	ds_read_b32 v230, v213 offset:2048
	ds_read_b32 v231, v213 offset:2560
	ds_read_b32 v232, v213 offset:3072
	ds_read_b32 v233, v213 offset:3584
	ds_read_b32 v234, v213 offset:4096
	ds_read_b32 v235, v213 offset:4608
	ds_read_b32 v236, v213 offset:5120
	ds_read_b32 v237, v213 offset:5632
	ds_read_b32 v238, v213 offset:6144
	ds_read_b32 v239, v213 offset:6656
	ds_read_b32 v240, v213 offset:7168
	ds_read_b32 v241, v213 offset:7680
	s_waitcnt lgkmcnt(0)
; #define GAS __attribute__((address_space(1)))
; #define LAS __attribute__((address_space(3)))
; #define LDS_WAIT() asm volatile("s_waitcnt lgkmcnt(0)" ::: "memory")
;     const int pr = item >> 1, kb = 2 * (pr / nblk) + (item & 1), nb = pr % nblk, k0 = 64 * kb, n0 = 32 * nb;
;     const int nr = n0 + (lane & 31); const int sc = MAP == 1 ? src_col_in(nr) : nr;
;     float v[32];
; #pragma unroll
;     for (int i = 0; i < 32; ++i) v[i] = sc >= 0 ? W[(size_t)(k0 + 2 * i + (lane >> 5)) * Nsrc + sc] : 0.f;
; #pragma unroll
;     for (int i = 0; i < 32; ++i) { const int k = k0 + 2 * i + (lane >> 5); float x = v[i] * wscale; if (KS) x *= (k < ksplit ? ksA[k] : ksB[k - ksplit]); scr[(2 * i + (lane >> 5)) * 33 + (lane & 31)] = x; }
;     LDS_WAIT(); asm volatile("" ::: "memory");
;     const int c = lane & 7;
; #pragma unroll
;     for (int j = 0; j < 4; ++j) { const int n = (lane >> 3) + 8 * j; const LAS float* s = scr + (8 * c) * 33 + n;
;         const unsigned long long o = (unsigned long long)pg8::pk4_fp8(s[0 * 33], s[1 * 33], s[2 * 33], s[3 * 33]) | ((unsigned long long)pg8::pk4_fp8(s[4 * 33], s[5 * 33], s[6 * 33], s[7 * 33]) << 32);
;         *(GAS unsigned long long*)(WT + (size_t)(n0 + n) * K + k0 + 8 * c) = o; }
;     LDS_WAIT(); asm volatile("" ::: "memory");
; }
; __global__ void __launch_bounds__(NWAVES * 64, 2) hybrid_fwd(Args args) {
;     ...
;             p0_transpose_item_f8<false>(args.in[16] + (size_t)l * FF * DM, FF, DM, DM / 32, (unsigned char*)(ws + WS_WDN + l * SZ_WDN), 128.f, args.in[16], args.in[16], 0, scr, r, lane);
	v_max_f32_e32 v226, v226, v226
	v_max_f32_e32 v227, v227, v227
	v_max_f32_e32 v228, v228, v228
	v_max_f32_e32 v229, v229, v229
	v_max_f32_e32 v230, v230, v230
	v_max_f32_e32 v231, v231, v231
	v_max_f32_e32 v232, v232, v232
	v_max_f32_e32 v233, v233, v233
	v_max_f32_e32 v234, v234, v234
	v_max_f32_e32 v235, v235, v235
	v_max_f32_e32 v236, v236, v236
	v_max_f32_e32 v237, v237, v237
	v_max_f32_e32 v238, v238, v238
	v_max_f32_e32 v239, v239, v239
	v_max_f32_e32 v240, v240, v240
	v_max_f32_e32 v241, v241, v241
	v_med3_f32 v226, v226, s62, v95
	v_med3_f32 v227, v227, s62, v95
	v_med3_f32 v228, v228, s62, v95
	v_med3_f32 v229, v229, s62, v95
	v_med3_f32 v230, v230, s62, v95
	v_med3_f32 v231, v231, s62, v95
	v_med3_f32 v232, v232, s62, v95
	v_med3_f32 v233, v233, s62, v95
	v_med3_f32 v234, v234, s62, v95
	v_med3_f32 v235, v235, s62, v95
	v_med3_f32 v236, v236, s62, v95
	v_med3_f32 v237, v237, s62, v95
	v_med3_f32 v238, v238, s62, v95
	v_med3_f32 v239, v239, s62, v95
	v_med3_f32 v240, v240, s62, v95
	v_med3_f32 v241, v241, s62, v95
	v_mov_b32_e32 v242, 0
	v_mov_b32_e32 v243, 0
	v_mov_b32_e32 v244, 0
	v_mov_b32_e32 v245, 0
	v_cvt_pk_fp8_f32 v242, v226, v227
	v_cvt_pk_fp8_f32 v243, v230, v231
	v_cvt_pk_fp8_f32 v244, v234, v235
	v_cvt_pk_fp8_f32 v245, v238, v239
	v_cvt_pk_fp8_f32 v242, v228, v229 op_sel:[0,0,1]
	v_cvt_pk_fp8_f32 v243, v232, v233 op_sel:[0,0,1]
	v_cvt_pk_fp8_f32 v244, v236, v237 op_sel:[0,0,1]
	v_cvt_pk_fp8_f32 v245, v240, v241 op_sel:[0,0,1]
	s_nop 0
	global_store_dwordx4 v80, v[242:245], s[6:7]
	s_waitcnt vmcnt(12)
	v_mul_f32_e32 v176, 0x43000000, v176
	v_mul_f32_e32 v177, 0x43000000, v177
	v_mul_f32_e32 v178, 0x43000000, v178
	v_mul_f32_e32 v179, 0x43000000, v179
	ds_write_b128 v210, v[176:179]
	v_mul_f32_e32 v180, 0x43000000, v180
	v_mul_f32_e32 v181, 0x43000000, v181
	v_mul_f32_e32 v182, 0x43000000, v182
	v_mul_f32_e32 v183, 0x43000000, v183
	ds_write_b128 v210, v[180:183] offset:1024
	v_mul_f32_e32 v184, 0x43000000, v184
	v_mul_f32_e32 v185, 0x43000000, v185
	v_mul_f32_e32 v186, 0x43000000, v186
	v_mul_f32_e32 v187, 0x43000000, v187
	ds_write_b128 v210, v[184:187] offset:2048
	v_mul_f32_e32 v188, 0x43000000, v188
	v_mul_f32_e32 v189, 0x43000000, v189
	v_mul_f32_e32 v190, 0x43000000, v190
	v_mul_f32_e32 v191, 0x43000000, v191
	ds_write_b128 v210, v[188:191] offset:3072
	v_mul_f32_e32 v192, 0x43000000, v192
	v_mul_f32_e32 v193, 0x43000000, v193
	v_mul_f32_e32 v194, 0x43000000, v194
	v_mul_f32_e32 v195, 0x43000000, v195
	ds_write_b128 v210, v[192:195] offset:4096
	v_mul_f32_e32 v196, 0x43000000, v196
	v_mul_f32_e32 v197, 0x43000000, v197
	v_mul_f32_e32 v198, 0x43000000, v198
	v_mul_f32_e32 v199, 0x43000000, v199
	ds_write_b128 v210, v[196:199] offset:5120
	v_mul_f32_e32 v200, 0x43000000, v200
	v_mul_f32_e32 v201, 0x43000000, v201
	v_mul_f32_e32 v202, 0x43000000, v202
	v_mul_f32_e32 v203, 0x43000000, v203
	ds_write_b128 v210, v[200:203] offset:6144
	v_mul_f32_e32 v204, 0x43000000, v204
	v_mul_f32_e32 v205, 0x43000000, v205
	v_mul_f32_e32 v206, 0x43000000, v206
	v_mul_f32_e32 v207, 0x43000000, v207
	ds_write_b128 v210, v[204:207] offset:7168
	s_waitcnt lgkmcnt(0)
	s_barrier
	s_add_u32 s8, s42, 0xc001000
	s_addc_u32 s9, s43, 0
	global_load_dwordx4 v[176:179], v75, s[8:9]
	s_add_u32 s8, s8, 0x8000
	s_addc_u32 s9, s9, 0
	global_load_dwordx4 v[180:183], v75, s[8:9]
	s_add_u32 s8, s8, 0x8000
	s_addc_u32 s9, s9, 0
	global_load_dwordx4 v[184:187], v75, s[8:9]
	s_add_u32 s8, s8, 0x8000
	s_addc_u32 s9, s9, 0
	global_load_dwordx4 v[188:191], v75, s[8:9]
	s_add_u32 s8, s8, 0x8000
	s_addc_u32 s9, s9, 0
	global_load_dwordx4 v[192:195], v75, s[8:9]
	s_add_u32 s8, s8, 0x8000
	s_addc_u32 s9, s9, 0
	global_load_dwordx4 v[196:199], v75, s[8:9]
	s_add_u32 s8, s8, 0x8000
	s_addc_u32 s9, s9, 0
	global_load_dwordx4 v[200:203], v75, s[8:9]
	s_add_u32 s8, s8, 0x8000
	s_addc_u32 s9, s9, 0
	global_load_dwordx4 v[204:207], v75, s[8:9]
	s_add_u32 s6, s44, 0x3002000
	s_addc_u32 s7, s45, 0
	ds_read_b32 v226, v212
	ds_read_b32 v227, v212 offset:512
	ds_read_b32 v228, v212 offset:1024
	ds_read_b32 v229, v212 offset:1536
	ds_read_b32 v230, v212 offset:2048
	ds_read_b32 v231, v212 offset:2560
	ds_read_b32 v232, v212 offset:3072
	ds_read_b32 v233, v212 offset:3584
	ds_read_b32 v234, v212 offset:4096
	ds_read_b32 v235, v212 offset:4608
	ds_read_b32 v236, v212 offset:5120
	ds_read_b32 v237, v212 offset:5632
	ds_read_b32 v238, v212 offset:6144
	ds_read_b32 v239, v212 offset:6656
	ds_read_b32 v240, v212 offset:7168
	ds_read_b32 v241, v212 offset:7680
	s_waitcnt lgkmcnt(0)
	v_max_f32_e32 v226, v226, v226
	v_max_f32_e32 v227, v227, v227
	v_max_f32_e32 v228, v228, v228
	v_max_f32_e32 v229, v229, v229
	v_max_f32_e32 v230, v230, v230
	v_max_f32_e32 v231, v231, v231
	v_max_f32_e32 v232, v232, v232
	v_max_f32_e32 v233, v233, v233
	v_max_f32_e32 v234, v234, v234
	v_max_f32_e32 v235, v235, v235
	v_max_f32_e32 v236, v236, v236
	v_max_f32_e32 v237, v237, v237
	v_max_f32_e32 v238, v238, v238
	v_max_f32_e32 v239, v239, v239
	v_max_f32_e32 v240, v240, v240
	v_max_f32_e32 v241, v241, v241
	v_med3_f32 v226, v226, s62, v95
	v_med3_f32 v227, v227, s62, v95
	v_med3_f32 v228, v228, s62, v95
	v_med3_f32 v229, v229, s62, v95
	v_med3_f32 v230, v230, s62, v95
	v_med3_f32 v231, v231, s62, v95
	v_med3_f32 v232, v232, s62, v95
	v_med3_f32 v233, v233, s62, v95
	v_med3_f32 v234, v234, s62, v95
	v_med3_f32 v235, v235, s62, v95
	v_med3_f32 v236, v236, s62, v95
	v_med3_f32 v237, v237, s62, v95
	v_med3_f32 v238, v238, s62, v95
	v_med3_f32 v239, v239, s62, v95
	v_med3_f32 v240, v240, s62, v95
	v_med3_f32 v241, v241, s62, v95
	v_mov_b32_e32 v242, 0
	v_mov_b32_e32 v243, 0
	v_mov_b32_e32 v244, 0
	v_mov_b32_e32 v245, 0
	v_cvt_pk_fp8_f32 v242, v226, v227
	v_cvt_pk_fp8_f32 v243, v230, v231
	v_cvt_pk_fp8_f32 v244, v234, v235
	v_cvt_pk_fp8_f32 v245, v238, v239
	v_cvt_pk_fp8_f32 v242, v228, v229 op_sel:[0,0,1]
	v_cvt_pk_fp8_f32 v243, v232, v233 op_sel:[0,0,1]
	v_cvt_pk_fp8_f32 v244, v236, v237 op_sel:[0,0,1]
	v_cvt_pk_fp8_f32 v245, v240, v241 op_sel:[0,0,1]
	s_nop 0
	global_store_dwordx4 v79, v[242:245], s[6:7]
	ds_read_b32 v226, v214
	ds_read_b32 v227, v214 offset:512
	ds_read_b32 v228, v214 offset:1024
	ds_read_b32 v229, v214 offset:1536
	ds_read_b32 v230, v214 offset:2048
	ds_read_b32 v231, v214 offset:2560
	ds_read_b32 v232, v214 offset:3072
	ds_read_b32 v233, v214 offset:3584
	ds_read_b32 v234, v214 offset:4096
	ds_read_b32 v235, v214 offset:4608
	ds_read_b32 v236, v214 offset:5120
	ds_read_b32 v237, v214 offset:5632
	ds_read_b32 v238, v214 offset:6144
	ds_read_b32 v239, v214 offset:6656
	ds_read_b32 v240, v214 offset:7168
	ds_read_b32 v241, v214 offset:7680
	s_waitcnt lgkmcnt(0)
; #define GAS __attribute__((address_space(1)))
; #define LAS __attribute__((address_space(3)))
; #define LDS_WAIT() asm volatile("s_waitcnt lgkmcnt(0)" ::: "memory")
;     const int pr = item >> 1, kb = 2 * (pr / nblk) + (item & 1), nb = pr % nblk, k0 = 64 * kb, n0 = 32 * nb;
;     const int nr = n0 + (lane & 31); const int sc = MAP == 1 ? src_col_in(nr) : nr;
;     float v[32];
; #pragma unroll
;     for (int i = 0; i < 32; ++i) v[i] = sc >= 0 ? W[(size_t)(k0 + 2 * i + (lane >> 5)) * Nsrc + sc] : 0.f;
; #pragma unroll
;     for (int i = 0; i < 32; ++i) { const int k = k0 + 2 * i + (lane >> 5); float x = v[i] * wscale; if (KS) x *= (k < ksplit ? ksA[k] : ksB[k - ksplit]); scr[(2 * i + (lane >> 5)) * 33 + (lane & 31)] = x; }
;     LDS_WAIT(); asm volatile("" ::: "memory");
;     const int c = lane & 7;
; #pragma unroll
;     for (int j = 0; j < 4; ++j) { const int n = (lane >> 3) + 8 * j; const LAS float* s = scr + (8 * c) * 33 + n;
;         const unsigned long long o = (unsigned long long)pg8::pk4_fp8(s[0 * 33], s[1 * 33], s[2 * 33], s[3 * 33]) | ((unsigned long long)pg8::pk4_fp8(s[4 * 33], s[5 * 33], s[6 * 33], s[7 * 33]) << 32);
;         *(GAS unsigned long long*)(WT + (size_t)(n0 + n) * K + k0 + 8 * c) = o; }
;     LDS_WAIT(); asm volatile("" ::: "memory");
; }
; __global__ void __launch_bounds__(NWAVES * 64, 2) hybrid_fwd(Args args) {
;     ...
;             p0_transpose_item_f8<false>(args.in[16] + (size_t)l * FF * DM, FF, DM, DM / 32, (unsigned char*)(ws + WS_WDN + l * SZ_WDN), 128.f, args.in[16], args.in[16], 0, scr, r, lane);
	v_max_f32_e32 v226, v226, v226
	v_max_f32_e32 v227, v227, v227
	v_max_f32_e32 v228, v228, v228
	v_max_f32_e32 v229, v229, v229
	v_max_f32_e32 v230, v230, v230
	v_max_f32_e32 v231, v231, v231
	v_max_f32_e32 v232, v232, v232
	v_max_f32_e32 v233, v233, v233
	v_max_f32_e32 v234, v234, v234
	v_max_f32_e32 v235, v235, v235
	v_max_f32_e32 v236, v236, v236
	v_max_f32_e32 v237, v237, v237
	v_max_f32_e32 v238, v238, v238
	v_max_f32_e32 v239, v239, v239
	v_max_f32_e32 v240, v240, v240
	v_max_f32_e32 v241, v241, v241
	v_med3_f32 v226, v226, s62, v95
	v_med3_f32 v227, v227, s62, v95
	v_med3_f32 v228, v228, s62, v95
	v_med3_f32 v229, v229, s62, v95
	v_med3_f32 v230, v230, s62, v95
	v_med3_f32 v231, v231, s62, v95
	v_med3_f32 v232, v232, s62, v95
	v_med3_f32 v233, v233, s62, v95
	v_med3_f32 v234, v234, s62, v95
	v_med3_f32 v235, v235, s62, v95
	v_med3_f32 v236, v236, s62, v95
	v_med3_f32 v237, v237, s62, v95
	v_med3_f32 v238, v238, s62, v95
	v_med3_f32 v239, v239, s62, v95
	v_med3_f32 v240, v240, s62, v95
	v_med3_f32 v241, v241, s62, v95
	v_mov_b32_e32 v242, 0
	v_mov_b32_e32 v243, 0
	v_mov_b32_e32 v244, 0
	v_mov_b32_e32 v245, 0
	v_cvt_pk_fp8_f32 v242, v226, v227
	v_cvt_pk_fp8_f32 v243, v230, v231
	v_cvt_pk_fp8_f32 v244, v234, v235
	v_cvt_pk_fp8_f32 v245, v238, v239
	v_cvt_pk_fp8_f32 v242, v228, v229 op_sel:[0,0,1]
	v_cvt_pk_fp8_f32 v243, v232, v233 op_sel:[0,0,1]
	v_cvt_pk_fp8_f32 v244, v236, v237 op_sel:[0,0,1]
	v_cvt_pk_fp8_f32 v245, v240, v241 op_sel:[0,0,1]
	s_nop 0
	global_store_dwordx4 v80, v[242:245], s[6:7]
	s_waitcnt vmcnt(12)
	v_mul_f32_e32 v144, 0x43000000, v144
	v_mul_f32_e32 v145, 0x43000000, v145
	v_mul_f32_e32 v146, 0x43000000, v146
	v_mul_f32_e32 v147, 0x43000000, v147
	ds_write_b128 v209, v[144:147]
	v_mul_f32_e32 v148, 0x43000000, v148
	v_mul_f32_e32 v149, 0x43000000, v149
	v_mul_f32_e32 v150, 0x43000000, v150
	v_mul_f32_e32 v151, 0x43000000, v151
	ds_write_b128 v209, v[148:151] offset:1024
	v_mul_f32_e32 v152, 0x43000000, v152
	v_mul_f32_e32 v153, 0x43000000, v153
	v_mul_f32_e32 v154, 0x43000000, v154
	v_mul_f32_e32 v155, 0x43000000, v155
	ds_write_b128 v209, v[152:155] offset:2048
	v_mul_f32_e32 v156, 0x43000000, v156
	v_mul_f32_e32 v157, 0x43000000, v157
	v_mul_f32_e32 v158, 0x43000000, v158
	v_mul_f32_e32 v159, 0x43000000, v159
	ds_write_b128 v209, v[156:159] offset:3072
	v_mul_f32_e32 v160, 0x43000000, v160
	v_mul_f32_e32 v161, 0x43000000, v161
	v_mul_f32_e32 v162, 0x43000000, v162
	v_mul_f32_e32 v163, 0x43000000, v163
	ds_write_b128 v209, v[160:163] offset:4096
	v_mul_f32_e32 v164, 0x43000000, v164
	v_mul_f32_e32 v165, 0x43000000, v165
	v_mul_f32_e32 v166, 0x43000000, v166
	v_mul_f32_e32 v167, 0x43000000, v167
	ds_write_b128 v209, v[164:167] offset:5120
	v_mul_f32_e32 v168, 0x43000000, v168
	v_mul_f32_e32 v169, 0x43000000, v169
	v_mul_f32_e32 v170, 0x43000000, v170
	v_mul_f32_e32 v171, 0x43000000, v171
	ds_write_b128 v209, v[168:171] offset:6144
	v_mul_f32_e32 v172, 0x43000000, v172
	v_mul_f32_e32 v173, 0x43000000, v173
	v_mul_f32_e32 v174, 0x43000000, v174
	v_mul_f32_e32 v175, 0x43000000, v175
	ds_write_b128 v209, v[172:175] offset:7168
	s_waitcnt lgkmcnt(0)
	s_barrier
	s_add_u32 s8, s42, 0xc002000
	s_addc_u32 s9, s43, 0
	global_load_dwordx4 v[144:147], v75, s[8:9]
	s_add_u32 s8, s8, 0x8000
	s_addc_u32 s9, s9, 0
	global_load_dwordx4 v[148:151], v75, s[8:9]
	s_add_u32 s8, s8, 0x8000
	s_addc_u32 s9, s9, 0
	global_load_dwordx4 v[152:155], v75, s[8:9]
	s_add_u32 s8, s8, 0x8000
	s_addc_u32 s9, s9, 0
	global_load_dwordx4 v[156:159], v75, s[8:9]
	s_add_u32 s8, s8, 0x8000
	s_addc_u32 s9, s9, 0
	global_load_dwordx4 v[160:163], v75, s[8:9]
	s_add_u32 s8, s8, 0x8000
	s_addc_u32 s9, s9, 0
	global_load_dwordx4 v[164:167], v75, s[8:9]
	s_add_u32 s8, s8, 0x8000
	s_addc_u32 s9, s9, 0
	global_load_dwordx4 v[168:171], v75, s[8:9]
	s_add_u32 s8, s8, 0x8000
	s_addc_u32 s9, s9, 0
	global_load_dwordx4 v[172:175], v75, s[8:9]
	s_add_u32 s6, s44, 0x3000
	s_addc_u32 s7, s45, 0
	ds_read_b32 v226, v211
	ds_read_b32 v227, v211 offset:512
	ds_read_b32 v228, v211 offset:1024
	ds_read_b32 v229, v211 offset:1536
	ds_read_b32 v230, v211 offset:2048
	ds_read_b32 v231, v211 offset:2560
	ds_read_b32 v232, v211 offset:3072
	ds_read_b32 v233, v211 offset:3584
	ds_read_b32 v234, v211 offset:4096
	ds_read_b32 v235, v211 offset:4608
	ds_read_b32 v236, v211 offset:5120
	ds_read_b32 v237, v211 offset:5632
	ds_read_b32 v238, v211 offset:6144
	ds_read_b32 v239, v211 offset:6656
	ds_read_b32 v240, v211 offset:7168
	ds_read_b32 v241, v211 offset:7680
	s_waitcnt lgkmcnt(0)
	v_max_f32_e32 v226, v226, v226
	v_max_f32_e32 v227, v227, v227
	v_max_f32_e32 v228, v228, v228
	v_max_f32_e32 v229, v229, v229
	v_max_f32_e32 v230, v230, v230
	v_max_f32_e32 v231, v231, v231
	v_max_f32_e32 v232, v232, v232
	v_max_f32_e32 v233, v233, v233
	v_max_f32_e32 v234, v234, v234
	v_max_f32_e32 v235, v235, v235
	v_max_f32_e32 v236, v236, v236
	v_max_f32_e32 v237, v237, v237
	v_max_f32_e32 v238, v238, v238
	v_max_f32_e32 v239, v239, v239
	v_max_f32_e32 v240, v240, v240
	v_max_f32_e32 v241, v241, v241
	v_med3_f32 v226, v226, s62, v95
	v_med3_f32 v227, v227, s62, v95
	v_med3_f32 v228, v228, s62, v95
	v_med3_f32 v229, v229, s62, v95
	v_med3_f32 v230, v230, s62, v95
	v_med3_f32 v231, v231, s62, v95
	v_med3_f32 v232, v232, s62, v95
	v_med3_f32 v233, v233, s62, v95
	v_med3_f32 v234, v234, s62, v95
	v_med3_f32 v235, v235, s62, v95
	v_med3_f32 v236, v236, s62, v95
	v_med3_f32 v237, v237, s62, v95
	v_med3_f32 v238, v238, s62, v95
	v_med3_f32 v239, v239, s62, v95
	v_med3_f32 v240, v240, s62, v95
	v_med3_f32 v241, v241, s62, v95
	v_mov_b32_e32 v242, 0
	v_mov_b32_e32 v243, 0
	v_mov_b32_e32 v244, 0
	v_mov_b32_e32 v245, 0
	v_cvt_pk_fp8_f32 v242, v226, v227
	v_cvt_pk_fp8_f32 v243, v230, v231
	v_cvt_pk_fp8_f32 v244, v234, v235
	v_cvt_pk_fp8_f32 v245, v238, v239
	v_cvt_pk_fp8_f32 v242, v228, v229 op_sel:[0,0,1]
	v_cvt_pk_fp8_f32 v243, v232, v233 op_sel:[0,0,1]
	v_cvt_pk_fp8_f32 v244, v236, v237 op_sel:[0,0,1]
	v_cvt_pk_fp8_f32 v245, v240, v241 op_sel:[0,0,1]
	s_nop 0
	global_store_dwordx4 v79, v[242:245], s[6:7]
	ds_read_b32 v226, v213
	ds_read_b32 v227, v213 offset:512
	ds_read_b32 v228, v213 offset:1024
	ds_read_b32 v229, v213 offset:1536
	ds_read_b32 v230, v213 offset:2048
	ds_read_b32 v231, v213 offset:2560
	ds_read_b32 v232, v213 offset:3072
	ds_read_b32 v233, v213 offset:3584
	ds_read_b32 v234, v213 offset:4096
	ds_read_b32 v235, v213 offset:4608
	ds_read_b32 v236, v213 offset:5120
	ds_read_b32 v237, v213 offset:5632
	ds_read_b32 v238, v213 offset:6144
	ds_read_b32 v239, v213 offset:6656
	ds_read_b32 v240, v213 offset:7168
	ds_read_b32 v241, v213 offset:7680
	s_waitcnt lgkmcnt(0)
; #define GAS __attribute__((address_space(1)))
; #define LAS __attribute__((address_space(3)))
; #define LDS_WAIT() asm volatile("s_waitcnt lgkmcnt(0)" ::: "memory")
;     const int pr = item >> 1, kb = 2 * (pr / nblk) + (item & 1), nb = pr % nblk, k0 = 64 * kb, n0 = 32 * nb;
;     const int nr = n0 + (lane & 31); const int sc = MAP == 1 ? src_col_in(nr) : nr;
;     float v[32];
; #pragma unroll
;     for (int i = 0; i < 32; ++i) v[i] = sc >= 0 ? W[(size_t)(k0 + 2 * i + (lane >> 5)) * Nsrc + sc] : 0.f;
; #pragma unroll
;     for (int i = 0; i < 32; ++i) { const int k = k0 + 2 * i + (lane >> 5); float x = v[i] * wscale; if (KS) x *= (k < ksplit ? ksA[k] : ksB[k - ksplit]); scr[(2 * i + (lane >> 5)) * 33 + (lane & 31)] = x; }
;     LDS_WAIT(); asm volatile("" ::: "memory");
;     const int c = lane & 7;
; #pragma unroll
;     for (int j = 0; j < 4; ++j) { const int n = (lane >> 3) + 8 * j; const LAS float* s = scr + (8 * c) * 33 + n;
;         const unsigned long long o = (unsigned long long)pg8::pk4_fp8(s[0 * 33], s[1 * 33], s[2 * 33], s[3 * 33]) | ((unsigned long long)pg8::pk4_fp8(s[4 * 33], s[5 * 33], s[6 * 33], s[7 * 33]) << 32);
;         *(GAS unsigned long long*)(WT + (size_t)(n0 + n) * K + k0 + 8 * c) = o; }
;     LDS_WAIT(); asm volatile("" ::: "memory");
; }
; __global__ void __launch_bounds__(NWAVES * 64, 2) hybrid_fwd(Args args) {
;     ...
;             p0_transpose_item_f8<false>(args.in[16] + (size_t)l * FF * DM, FF, DM, DM / 32, (unsigned char*)(ws + WS_WDN + l * SZ_WDN), 128.f, args.in[16], args.in[16], 0, scr, r, lane);
	v_max_f32_e32 v226, v226, v226
	v_max_f32_e32 v227, v227, v227
	v_max_f32_e32 v228, v228, v228
	v_max_f32_e32 v229, v229, v229
	v_max_f32_e32 v230, v230, v230
	v_max_f32_e32 v231, v231, v231
	v_max_f32_e32 v232, v232, v232
	v_max_f32_e32 v233, v233, v233
	v_max_f32_e32 v234, v234, v234
	v_max_f32_e32 v235, v235, v235
	v_max_f32_e32 v236, v236, v236
	v_max_f32_e32 v237, v237, v237
	v_max_f32_e32 v238, v238, v238
	v_max_f32_e32 v239, v239, v239
	v_max_f32_e32 v240, v240, v240
	v_max_f32_e32 v241, v241, v241
	v_med3_f32 v226, v226, s62, v95
	v_med3_f32 v227, v227, s62, v95
	v_med3_f32 v228, v228, s62, v95
	v_med3_f32 v229, v229, s62, v95
	v_med3_f32 v230, v230, s62, v95
	v_med3_f32 v231, v231, s62, v95
	v_med3_f32 v232, v232, s62, v95
	v_med3_f32 v233, v233, s62, v95
	v_med3_f32 v234, v234, s62, v95
	v_med3_f32 v235, v235, s62, v95
	v_med3_f32 v236, v236, s62, v95
	v_med3_f32 v237, v237, s62, v95
	v_med3_f32 v238, v238, s62, v95
	v_med3_f32 v239, v239, s62, v95
	v_med3_f32 v240, v240, s62, v95
	v_med3_f32 v241, v241, s62, v95
	v_mov_b32_e32 v242, 0
	v_mov_b32_e32 v243, 0
	v_mov_b32_e32 v244, 0
	v_mov_b32_e32 v245, 0
	v_cvt_pk_fp8_f32 v242, v226, v227
	v_cvt_pk_fp8_f32 v243, v230, v231
	v_cvt_pk_fp8_f32 v244, v234, v235
	v_cvt_pk_fp8_f32 v245, v238, v239
	v_cvt_pk_fp8_f32 v242, v228, v229 op_sel:[0,0,1]
	v_cvt_pk_fp8_f32 v243, v232, v233 op_sel:[0,0,1]
	v_cvt_pk_fp8_f32 v244, v236, v237 op_sel:[0,0,1]
	v_cvt_pk_fp8_f32 v245, v240, v241 op_sel:[0,0,1]
	s_nop 0
	global_store_dwordx4 v80, v[242:245], s[6:7]
	s_waitcnt vmcnt(12)
	v_mul_f32_e32 v176, 0x43000000, v176
	v_mul_f32_e32 v177, 0x43000000, v177
	v_mul_f32_e32 v178, 0x43000000, v178
	v_mul_f32_e32 v179, 0x43000000, v179
	ds_write_b128 v210, v[176:179]
	v_mul_f32_e32 v180, 0x43000000, v180
	v_mul_f32_e32 v181, 0x43000000, v181
	v_mul_f32_e32 v182, 0x43000000, v182
	v_mul_f32_e32 v183, 0x43000000, v183
	ds_write_b128 v210, v[180:183] offset:1024
	v_mul_f32_e32 v184, 0x43000000, v184
	v_mul_f32_e32 v185, 0x43000000, v185
	v_mul_f32_e32 v186, 0x43000000, v186
	v_mul_f32_e32 v187, 0x43000000, v187
	ds_write_b128 v210, v[184:187] offset:2048
	v_mul_f32_e32 v188, 0x43000000, v188
	v_mul_f32_e32 v189, 0x43000000, v189
	v_mul_f32_e32 v190, 0x43000000, v190
	v_mul_f32_e32 v191, 0x43000000, v191
	ds_write_b128 v210, v[188:191] offset:3072
	v_mul_f32_e32 v192, 0x43000000, v192
	v_mul_f32_e32 v193, 0x43000000, v193
	v_mul_f32_e32 v194, 0x43000000, v194
	v_mul_f32_e32 v195, 0x43000000, v195
	ds_write_b128 v210, v[192:195] offset:4096
	v_mul_f32_e32 v196, 0x43000000, v196
	v_mul_f32_e32 v197, 0x43000000, v197
	v_mul_f32_e32 v198, 0x43000000, v198
	v_mul_f32_e32 v199, 0x43000000, v199
	ds_write_b128 v210, v[196:199] offset:5120
	v_mul_f32_e32 v200, 0x43000000, v200
	v_mul_f32_e32 v201, 0x43000000, v201
	v_mul_f32_e32 v202, 0x43000000, v202
	v_mul_f32_e32 v203, 0x43000000, v203
	ds_write_b128 v210, v[200:203] offset:6144
	v_mul_f32_e32 v204, 0x43000000, v204
	v_mul_f32_e32 v205, 0x43000000, v205
	v_mul_f32_e32 v206, 0x43000000, v206
	v_mul_f32_e32 v207, 0x43000000, v207
	ds_write_b128 v210, v[204:207] offset:7168
	s_waitcnt lgkmcnt(0)
	s_barrier
	s_add_u32 s8, s42, 0xc003000
	s_addc_u32 s9, s43, 0
	global_load_dwordx4 v[176:179], v75, s[8:9]
	s_add_u32 s8, s8, 0x8000
	s_addc_u32 s9, s9, 0
	global_load_dwordx4 v[180:183], v75, s[8:9]
	s_add_u32 s8, s8, 0x8000
	s_addc_u32 s9, s9, 0
	global_load_dwordx4 v[184:187], v75, s[8:9]
	s_add_u32 s8, s8, 0x8000
	s_addc_u32 s9, s9, 0
	global_load_dwordx4 v[188:191], v75, s[8:9]
	s_add_u32 s8, s8, 0x8000
	s_addc_u32 s9, s9, 0
	global_load_dwordx4 v[192:195], v75, s[8:9]
	s_add_u32 s8, s8, 0x8000
	s_addc_u32 s9, s9, 0
	global_load_dwordx4 v[196:199], v75, s[8:9]
	s_add_u32 s8, s8, 0x8000
	s_addc_u32 s9, s9, 0
	global_load_dwordx4 v[200:203], v75, s[8:9]
	s_add_u32 s8, s8, 0x8000
	s_addc_u32 s9, s9, 0
	global_load_dwordx4 v[204:207], v75, s[8:9]
	s_add_u32 s6, s44, 0x1003000
	s_addc_u32 s7, s45, 0
	ds_read_b32 v226, v212
	ds_read_b32 v227, v212 offset:512
	ds_read_b32 v228, v212 offset:1024
	ds_read_b32 v229, v212 offset:1536
	ds_read_b32 v230, v212 offset:2048
	ds_read_b32 v231, v212 offset:2560
	ds_read_b32 v232, v212 offset:3072
	ds_read_b32 v233, v212 offset:3584
	ds_read_b32 v234, v212 offset:4096
	ds_read_b32 v235, v212 offset:4608
	ds_read_b32 v236, v212 offset:5120
	ds_read_b32 v237, v212 offset:5632
	ds_read_b32 v238, v212 offset:6144
	ds_read_b32 v239, v212 offset:6656
	ds_read_b32 v240, v212 offset:7168
	ds_read_b32 v241, v212 offset:7680
	s_waitcnt lgkmcnt(0)
	v_max_f32_e32 v226, v226, v226
	v_max_f32_e32 v227, v227, v227
	v_max_f32_e32 v228, v228, v228
	v_max_f32_e32 v229, v229, v229
	v_max_f32_e32 v230, v230, v230
	v_max_f32_e32 v231, v231, v231
	v_max_f32_e32 v232, v232, v232
	v_max_f32_e32 v233, v233, v233
	v_max_f32_e32 v234, v234, v234
	v_max_f32_e32 v235, v235, v235
	v_max_f32_e32 v236, v236, v236
	v_max_f32_e32 v237, v237, v237
	v_max_f32_e32 v238, v238, v238
	v_max_f32_e32 v239, v239, v239
	v_max_f32_e32 v240, v240, v240
	v_max_f32_e32 v241, v241, v241
	v_med3_f32 v226, v226, s62, v95
	v_med3_f32 v227, v227, s62, v95
	v_med3_f32 v228, v228, s62, v95
	v_med3_f32 v229, v229, s62, v95
	v_med3_f32 v230, v230, s62, v95
	v_med3_f32 v231, v231, s62, v95
	v_med3_f32 v232, v232, s62, v95
	v_med3_f32 v233, v233, s62, v95
	v_med3_f32 v234, v234, s62, v95
	v_med3_f32 v235, v235, s62, v95
	v_med3_f32 v236, v236, s62, v95
	v_med3_f32 v237, v237, s62, v95
	v_med3_f32 v238, v238, s62, v95
	v_med3_f32 v239, v239, s62, v95
	v_med3_f32 v240, v240, s62, v95
	v_med3_f32 v241, v241, s62, v95
	v_mov_b32_e32 v242, 0
	v_mov_b32_e32 v243, 0
	v_mov_b32_e32 v244, 0
	v_mov_b32_e32 v245, 0
	v_cvt_pk_fp8_f32 v242, v226, v227
	v_cvt_pk_fp8_f32 v243, v230, v231
	v_cvt_pk_fp8_f32 v244, v234, v235
	v_cvt_pk_fp8_f32 v245, v238, v239
	v_cvt_pk_fp8_f32 v242, v228, v229 op_sel:[0,0,1]
	v_cvt_pk_fp8_f32 v243, v232, v233 op_sel:[0,0,1]
	v_cvt_pk_fp8_f32 v244, v236, v237 op_sel:[0,0,1]
	v_cvt_pk_fp8_f32 v245, v240, v241 op_sel:[0,0,1]
	s_nop 0
	global_store_dwordx4 v79, v[242:245], s[6:7]
	ds_read_b32 v226, v214
	ds_read_b32 v227, v214 offset:512
	ds_read_b32 v228, v214 offset:1024
	ds_read_b32 v229, v214 offset:1536
	ds_read_b32 v230, v214 offset:2048
	ds_read_b32 v231, v214 offset:2560
	ds_read_b32 v232, v214 offset:3072
	ds_read_b32 v233, v214 offset:3584
	ds_read_b32 v234, v214 offset:4096
	ds_read_b32 v235, v214 offset:4608
	ds_read_b32 v236, v214 offset:5120
	ds_read_b32 v237, v214 offset:5632
	ds_read_b32 v238, v214 offset:6144
	ds_read_b32 v239, v214 offset:6656
	ds_read_b32 v240, v214 offset:7168
	ds_read_b32 v241, v214 offset:7680
	s_waitcnt lgkmcnt(0)
; #define GAS __attribute__((address_space(1)))
; #define LAS __attribute__((address_space(3)))
; #define LDS_WAIT() asm volatile("s_waitcnt lgkmcnt(0)" ::: "memory")
; __device__ __forceinline__ int src_col_in(int c) {
;     if (c < 5120) { const int blk = c >> 7, p = c & 127; const bool rope = blk < 16 || ((((blk - 16) >> 2) & 1) == 0); const int d = rope ? (p >> 1) + 64 * (p & 1) : p; return blk * 128 + d; }
;     if (c < OFF_Z) return c + 2096;
;     if (c < OFF_G) return c - 4048;
;     if (c < OFF_DT) return 5120 + (c - OFF_G);
;     if (c < NSRC) return c;
;     return -1;
; }
;     const int pr = item >> 1, kb = 2 * (pr / nblk) + (item & 1), nb = pr % nblk, k0 = 64 * kb, n0 = 32 * nb;
;     const int nr = n0 + (lane & 31); const int sc = MAP == 1 ? src_col_in(nr) : nr;
;     float v[32];
; #pragma unroll
;     for (int i = 0; i < 32; ++i) v[i] = sc >= 0 ? W[(size_t)(k0 + 2 * i + (lane >> 5)) * Nsrc + sc] : 0.f;
; #pragma unroll
;     for (int i = 0; i < 32; ++i) { const int k = k0 + 2 * i + (lane >> 5); float x = v[i] * wscale; if (KS) x *= (k < ksplit ? ksA[k] : ksB[k - ksplit]); scr[(2 * i + (lane >> 5)) * 33 + (lane & 31)] = x; }
;     LDS_WAIT(); asm volatile("" ::: "memory");
;     const int c = lane & 7;
; #pragma unroll
;     for (int j = 0; j < 4; ++j) { const int n = (lane >> 3) + 8 * j; const LAS float* s = scr + (8 * c) * 33 + n;
;         const unsigned long long o = (unsigned long long)pg8::pk4_fp8(s[0 * 33], s[1 * 33], s[2 * 33], s[3 * 33]) | ((unsigned long long)pg8::pk4_fp8(s[4 * 33], s[5 * 33], s[6 * 33], s[7 * 33]) << 32);
;         *(GAS unsigned long long*)(WT + (size_t)(n0 + n) * K + k0 + 8 * c) = o; }
;     LDS_WAIT(); asm volatile("" ::: "memory");
; }
	v_max_f32_e32 v226, v226, v226
	v_max_f32_e32 v227, v227, v227
	v_max_f32_e32 v228, v228, v228
	v_max_f32_e32 v229, v229, v229
	v_max_f32_e32 v230, v230, v230
	v_max_f32_e32 v231, v231, v231
	v_max_f32_e32 v232, v232, v232
	v_max_f32_e32 v233, v233, v233
	v_max_f32_e32 v234, v234, v234
	v_max_f32_e32 v235, v235, v235
	v_max_f32_e32 v236, v236, v236
	v_max_f32_e32 v237, v237, v237
	v_max_f32_e32 v238, v238, v238
	v_max_f32_e32 v239, v239, v239
	v_max_f32_e32 v240, v240, v240
	v_max_f32_e32 v241, v241, v241
	v_med3_f32 v226, v226, s62, v95
	v_med3_f32 v227, v227, s62, v95
	v_med3_f32 v228, v228, s62, v95
	v_med3_f32 v229, v229, s62, v95
	v_med3_f32 v230, v230, s62, v95
	v_med3_f32 v231, v231, s62, v95
	v_med3_f32 v232, v232, s62, v95
	v_med3_f32 v233, v233, s62, v95
	v_med3_f32 v234, v234, s62, v95
	v_med3_f32 v235, v235, s62, v95
	v_med3_f32 v236, v236, s62, v95
	v_med3_f32 v237, v237, s62, v95
	v_med3_f32 v238, v238, s62, v95
	v_med3_f32 v239, v239, s62, v95
	v_med3_f32 v240, v240, s62, v95
	v_med3_f32 v241, v241, s62, v95
	v_mov_b32_e32 v242, 0
	v_mov_b32_e32 v243, 0
	v_mov_b32_e32 v244, 0
	v_mov_b32_e32 v245, 0
	v_cvt_pk_fp8_f32 v242, v226, v227
	v_cvt_pk_fp8_f32 v243, v230, v231
	v_cvt_pk_fp8_f32 v244, v234, v235
	v_cvt_pk_fp8_f32 v245, v238, v239
	v_cvt_pk_fp8_f32 v242, v228, v229 op_sel:[0,0,1]
	v_cvt_pk_fp8_f32 v243, v232, v233 op_sel:[0,0,1]
	v_cvt_pk_fp8_f32 v244, v236, v237 op_sel:[0,0,1]
	v_cvt_pk_fp8_f32 v245, v240, v241 op_sel:[0,0,1]
	s_nop 0
	global_store_dwordx4 v80, v[242:245], s[6:7]
	s_waitcnt vmcnt(12)
	v_mul_f32_e32 v144, 0x43000000, v144
	v_mul_f32_e32 v145, 0x43000000, v145
	v_mul_f32_e32 v146, 0x43000000, v146
	v_mul_f32_e32 v147, 0x43000000, v147
	ds_write_b128 v209, v[144:147]
	v_mul_f32_e32 v148, 0x43000000, v148
	v_mul_f32_e32 v149, 0x43000000, v149
	v_mul_f32_e32 v150, 0x43000000, v150
	v_mul_f32_e32 v151, 0x43000000, v151
	ds_write_b128 v209, v[148:151] offset:1024
	v_mul_f32_e32 v152, 0x43000000, v152
	v_mul_f32_e32 v153, 0x43000000, v153
	v_mul_f32_e32 v154, 0x43000000, v154
	v_mul_f32_e32 v155, 0x43000000, v155
	ds_write_b128 v209, v[152:155] offset:2048
	v_mul_f32_e32 v156, 0x43000000, v156
	v_mul_f32_e32 v157, 0x43000000, v157
	v_mul_f32_e32 v158, 0x43000000, v158
	v_mul_f32_e32 v159, 0x43000000, v159
	ds_write_b128 v209, v[156:159] offset:3072
	v_mul_f32_e32 v160, 0x43000000, v160
	v_mul_f32_e32 v161, 0x43000000, v161
	v_mul_f32_e32 v162, 0x43000000, v162
	v_mul_f32_e32 v163, 0x43000000, v163
	ds_write_b128 v209, v[160:163] offset:4096
	v_mul_f32_e32 v164, 0x43000000, v164
	v_mul_f32_e32 v165, 0x43000000, v165
	v_mul_f32_e32 v166, 0x43000000, v166
	v_mul_f32_e32 v167, 0x43000000, v167
	ds_write_b128 v209, v[164:167] offset:5120
	v_mul_f32_e32 v168, 0x43000000, v168
	v_mul_f32_e32 v169, 0x43000000, v169
	v_mul_f32_e32 v170, 0x43000000, v170
	v_mul_f32_e32 v171, 0x43000000, v171
	ds_write_b128 v209, v[168:171] offset:6144
	v_mul_f32_e32 v172, 0x43000000, v172
	v_mul_f32_e32 v173, 0x43000000, v173
	v_mul_f32_e32 v174, 0x43000000, v174
	v_mul_f32_e32 v175, 0x43000000, v175
	ds_write_b128 v209, v[172:175] offset:7168
	s_waitcnt lgkmcnt(0)
	s_barrier
	s_add_i32 s24, s23, 0
	s_lshl_b32 s20, s24, 7
	s_cmp_lt_u32 s24, 40
	s_cselect_b32 s21, 0, 0x830
	s_cmp_lt_u32 s24, 72
	s_cselect_b32 s21, s21, 0xfffff030
	s_add_i32 s20, s20, s21
	s_lshl_b32 s20, s20, 2
	s_add_u32 s8, s46, s20
	s_addc_u32 s9, s47, 0
	global_load_dwordx4 v[144:147], v76, s[8:9]
	s_add_u32 s8, s8, 0x16280
	s_addc_u32 s9, s9, 0
	global_load_dwordx4 v[148:151], v76, s[8:9]
	s_add_u32 s8, s8, 0x16280
	s_addc_u32 s9, s9, 0
	global_load_dwordx4 v[152:155], v76, s[8:9]
	s_add_u32 s8, s8, 0x16280
	s_addc_u32 s9, s9, 0
	global_load_dwordx4 v[156:159], v76, s[8:9]
	s_add_u32 s8, s8, 0x16280
	s_addc_u32 s9, s9, 0
	global_load_dwordx4 v[160:163], v76, s[8:9]
	s_add_u32 s8, s8, 0x16280
	s_addc_u32 s9, s9, 0
	global_load_dwordx4 v[164:167], v76, s[8:9]
	s_add_u32 s8, s8, 0x16280
	s_addc_u32 s9, s9, 0
	global_load_dwordx4 v[168:171], v76, s[8:9]
	s_add_u32 s8, s8, 0x16280
	s_addc_u32 s9, s9, 0
	global_load_dwordx4 v[172:175], v76, s[8:9]
	s_add_u32 s6, s44, 0x2003000
	s_addc_u32 s7, s45, 0
	ds_read_b32 v226, v211
	ds_read_b32 v227, v211 offset:512
	ds_read_b32 v228, v211 offset:1024
	ds_read_b32 v229, v211 offset:1536
	ds_read_b32 v230, v211 offset:2048
	ds_read_b32 v231, v211 offset:2560
	ds_read_b32 v232, v211 offset:3072
	ds_read_b32 v233, v211 offset:3584
	ds_read_b32 v234, v211 offset:4096
	ds_read_b32 v235, v211 offset:4608
	ds_read_b32 v236, v211 offset:5120
	ds_read_b32 v237, v211 offset:5632
	ds_read_b32 v238, v211 offset:6144
	ds_read_b32 v239, v211 offset:6656
	ds_read_b32 v240, v211 offset:7168
	ds_read_b32 v241, v211 offset:7680
	s_waitcnt lgkmcnt(0)
; #define GAS __attribute__((address_space(1)))
; #define LAS __attribute__((address_space(3)))
; #define LDS_WAIT() asm volatile("s_waitcnt lgkmcnt(0)" ::: "memory")
;     const int pr = item >> 1, kb = 2 * (pr / nblk) + (item & 1), nb = pr % nblk, k0 = 64 * kb, n0 = 32 * nb;
;     const int nr = n0 + (lane & 31); const int sc = MAP == 1 ? src_col_in(nr) : nr;
;     float v[32];
; #pragma unroll
;     for (int i = 0; i < 32; ++i) v[i] = sc >= 0 ? W[(size_t)(k0 + 2 * i + (lane >> 5)) * Nsrc + sc] : 0.f;
; #pragma unroll
;     for (int i = 0; i < 32; ++i) { const int k = k0 + 2 * i + (lane >> 5); float x = v[i] * wscale; if (KS) x *= (k < ksplit ? ksA[k] : ksB[k - ksplit]); scr[(2 * i + (lane >> 5)) * 33 + (lane & 31)] = x; }
;     LDS_WAIT(); asm volatile("" ::: "memory");
;     const int c = lane & 7;
; #pragma unroll
;     for (int j = 0; j < 4; ++j) { const int n = (lane >> 3) + 8 * j; const LAS float* s = scr + (8 * c) * 33 + n;
;         const unsigned long long o = (unsigned long long)pg8::pk4_fp8(s[0 * 33], s[1 * 33], s[2 * 33], s[3 * 33]) | ((unsigned long long)pg8::pk4_fp8(s[4 * 33], s[5 * 33], s[6 * 33], s[7 * 33]) << 32);
;         *(GAS unsigned long long*)(WT + (size_t)(n0 + n) * K + k0 + 8 * c) = o; }
;     LDS_WAIT(); asm volatile("" ::: "memory");
; }
	v_max_f32_e32 v226, v226, v226
	v_max_f32_e32 v227, v227, v227
	v_max_f32_e32 v228, v228, v228
	v_max_f32_e32 v229, v229, v229
	v_max_f32_e32 v230, v230, v230
	v_max_f32_e32 v231, v231, v231
	v_max_f32_e32 v232, v232, v232
	v_max_f32_e32 v233, v233, v233
	v_max_f32_e32 v234, v234, v234
	v_max_f32_e32 v235, v235, v235
	v_max_f32_e32 v236, v236, v236
	v_max_f32_e32 v237, v237, v237
	v_max_f32_e32 v238, v238, v238
	v_max_f32_e32 v239, v239, v239
	v_max_f32_e32 v240, v240, v240
	v_max_f32_e32 v241, v241, v241
	v_med3_f32 v226, v226, s62, v95
	v_med3_f32 v227, v227, s62, v95
	v_med3_f32 v228, v228, s62, v95
	v_med3_f32 v229, v229, s62, v95
	v_med3_f32 v230, v230, s62, v95
	v_med3_f32 v231, v231, s62, v95
	v_med3_f32 v232, v232, s62, v95
	v_med3_f32 v233, v233, s62, v95
	v_med3_f32 v234, v234, s62, v95
	v_med3_f32 v235, v235, s62, v95
	v_med3_f32 v236, v236, s62, v95
	v_med3_f32 v237, v237, s62, v95
	v_med3_f32 v238, v238, s62, v95
	v_med3_f32 v239, v239, s62, v95
	v_med3_f32 v240, v240, s62, v95
	v_med3_f32 v241, v241, s62, v95
	v_mov_b32_e32 v242, 0
	v_mov_b32_e32 v243, 0
	v_mov_b32_e32 v244, 0
	v_mov_b32_e32 v245, 0
	v_cvt_pk_fp8_f32 v242, v226, v227
	v_cvt_pk_fp8_f32 v243, v230, v231
	v_cvt_pk_fp8_f32 v244, v234, v235
	v_cvt_pk_fp8_f32 v245, v238, v239
	v_cvt_pk_fp8_f32 v242, v228, v229 op_sel:[0,0,1]
	v_cvt_pk_fp8_f32 v243, v232, v233 op_sel:[0,0,1]
	v_cvt_pk_fp8_f32 v244, v236, v237 op_sel:[0,0,1]
	v_cvt_pk_fp8_f32 v245, v240, v241 op_sel:[0,0,1]
	s_nop 0
	global_store_dwordx4 v79, v[242:245], s[6:7]
	ds_read_b32 v226, v213
	ds_read_b32 v227, v213 offset:512
	ds_read_b32 v228, v213 offset:1024
	ds_read_b32 v229, v213 offset:1536
	ds_read_b32 v230, v213 offset:2048
	ds_read_b32 v231, v213 offset:2560
	ds_read_b32 v232, v213 offset:3072
	ds_read_b32 v233, v213 offset:3584
	ds_read_b32 v234, v213 offset:4096
	ds_read_b32 v235, v213 offset:4608
	ds_read_b32 v236, v213 offset:5120
	ds_read_b32 v237, v213 offset:5632
	ds_read_b32 v238, v213 offset:6144
	ds_read_b32 v239, v213 offset:6656
	ds_read_b32 v240, v213 offset:7168
	ds_read_b32 v241, v213 offset:7680
	s_waitcnt lgkmcnt(0)
	v_max_f32_e32 v226, v226, v226
	v_max_f32_e32 v227, v227, v227
	v_max_f32_e32 v228, v228, v228
	v_max_f32_e32 v229, v229, v229
	v_max_f32_e32 v230, v230, v230
	v_max_f32_e32 v231, v231, v231
	v_max_f32_e32 v232, v232, v232
	v_max_f32_e32 v233, v233, v233
	v_max_f32_e32 v234, v234, v234
	v_max_f32_e32 v235, v235, v235
	v_max_f32_e32 v236, v236, v236
	v_max_f32_e32 v237, v237, v237
	v_max_f32_e32 v238, v238, v238
	v_max_f32_e32 v239, v239, v239
	v_max_f32_e32 v240, v240, v240
	v_max_f32_e32 v241, v241, v241
	v_med3_f32 v226, v226, s62, v95
	v_med3_f32 v227, v227, s62, v95
	v_med3_f32 v228, v228, s62, v95
	v_med3_f32 v229, v229, s62, v95
	v_med3_f32 v230, v230, s62, v95
	v_med3_f32 v231, v231, s62, v95
	v_med3_f32 v232, v232, s62, v95
	v_med3_f32 v233, v233, s62, v95
	v_med3_f32 v234, v234, s62, v95
	v_med3_f32 v235, v235, s62, v95
	v_med3_f32 v236, v236, s62, v95
	v_med3_f32 v237, v237, s62, v95
	v_med3_f32 v238, v238, s62, v95
	v_med3_f32 v239, v239, s62, v95
	v_med3_f32 v240, v240, s62, v95
	v_med3_f32 v241, v241, s62, v95
	v_mov_b32_e32 v242, 0
	v_mov_b32_e32 v243, 0
	v_mov_b32_e32 v244, 0
	v_mov_b32_e32 v245, 0
	v_cvt_pk_fp8_f32 v242, v226, v227
	v_cvt_pk_fp8_f32 v243, v230, v231
	v_cvt_pk_fp8_f32 v244, v234, v235
	v_cvt_pk_fp8_f32 v245, v238, v239
	v_cvt_pk_fp8_f32 v242, v228, v229 op_sel:[0,0,1]
	v_cvt_pk_fp8_f32 v243, v232, v233 op_sel:[0,0,1]
	v_cvt_pk_fp8_f32 v244, v236, v237 op_sel:[0,0,1]
	v_cvt_pk_fp8_f32 v245, v240, v241 op_sel:[0,0,1]
	s_nop 0
	global_store_dwordx4 v80, v[242:245], s[6:7]
	s_waitcnt vmcnt(12)
	v_mul_f32_e32 v176, 0x43000000, v176
	v_mul_f32_e32 v177, 0x43000000, v177
	v_mul_f32_e32 v178, 0x43000000, v178
	v_mul_f32_e32 v179, 0x43000000, v179
	ds_write_b128 v210, v[176:179]
	v_mul_f32_e32 v180, 0x43000000, v180
	v_mul_f32_e32 v181, 0x43000000, v181
	v_mul_f32_e32 v182, 0x43000000, v182
	v_mul_f32_e32 v183, 0x43000000, v183
	ds_write_b128 v210, v[180:183] offset:1024
	v_mul_f32_e32 v184, 0x43000000, v184
	v_mul_f32_e32 v185, 0x43000000, v185
	v_mul_f32_e32 v186, 0x43000000, v186
	v_mul_f32_e32 v187, 0x43000000, v187
	ds_write_b128 v210, v[184:187] offset:2048
	v_mul_f32_e32 v188, 0x43000000, v188
	v_mul_f32_e32 v189, 0x43000000, v189
	v_mul_f32_e32 v190, 0x43000000, v190
	v_mul_f32_e32 v191, 0x43000000, v191
	ds_write_b128 v210, v[188:191] offset:3072
	v_mul_f32_e32 v192, 0x43000000, v192
	v_mul_f32_e32 v193, 0x43000000, v193
	v_mul_f32_e32 v194, 0x43000000, v194
	v_mul_f32_e32 v195, 0x43000000, v195
	ds_write_b128 v210, v[192:195] offset:4096
	v_mul_f32_e32 v196, 0x43000000, v196
	v_mul_f32_e32 v197, 0x43000000, v197
	v_mul_f32_e32 v198, 0x43000000, v198
	v_mul_f32_e32 v199, 0x43000000, v199
	ds_write_b128 v210, v[196:199] offset:5120
	v_mul_f32_e32 v200, 0x43000000, v200
	v_mul_f32_e32 v201, 0x43000000, v201
	v_mul_f32_e32 v202, 0x43000000, v202
	v_mul_f32_e32 v203, 0x43000000, v203
	ds_write_b128 v210, v[200:203] offset:6144
	v_mul_f32_e32 v204, 0x43000000, v204
	v_mul_f32_e32 v205, 0x43000000, v205
	v_mul_f32_e32 v206, 0x43000000, v206
	v_mul_f32_e32 v207, 0x43000000, v207
	ds_write_b128 v210, v[204:207] offset:7168
	s_waitcnt lgkmcnt(0)
	s_barrier
; #define GAS __attribute__((address_space(1)))
; #define LAS __attribute__((address_space(3)))
; #define LDS_WAIT() asm volatile("s_waitcnt lgkmcnt(0)" ::: "memory")
; __device__ __forceinline__ int nat_dim(int p) { return (p >> 1) + 64 * (p & 1); }
; template <int MAP, bool KS, bool KPERM = false>
; __device__ __forceinline__ void p0_transpose_item(const float* W, int K, int Nsrc, int nblk, bf16* WT, const float* ksA, const float* ksB, int ksplit, LAS float* scr, int item, int lane) {
;     const int kb = item / nblk, nb = item % nblk, k0 = 64 * kb, n0 = 32 * nb;
;     const int nr = n0 + (lane & 31); const int sc = MAP == 1 ? src_col_in(nr) : (MAP == 2 ? nat_dim(nr) : nr);
;     float v[32];
; #pragma unroll
;     for (int i = 0; i < 32; ++i) { const int k = k0 + 2 * i + (lane >> 5); const int ksrc = KPERM ? ((k & ~127) + nat_dim(k & 127)) : k;
;         v[i] = sc >= 0 ? W[(size_t)ksrc * Nsrc + sc] : 0.f; }
; #pragma unroll
;     for (int i = 0; i < 32; ++i) { const int kk = 2 * i + (lane >> 5); const int k = k0 + kk;
;         if (KS) v[i] *= (k < ksplit ? ksA[k] : ksB[k - ksplit]);
;         scr[kk * 33 + (lane & 31)] = v[i]; }
;     const int pr = item >> 1, kb = 2 * (pr / nblk) + (item & 1), nb = pr % nblk, k0 = 64 * kb, n0 = 32 * nb;
;     const int nr = n0 + (lane & 31); const int sc = MAP == 1 ? src_col_in(nr) : nr;
;     float v[32];
; #pragma unroll
;     for (int i = 0; i < 32; ++i) v[i] = sc >= 0 ? W[(size_t)(k0 + 2 * i + (lane >> 5)) * Nsrc + sc] : 0.f;
; #pragma unroll
;     for (int i = 0; i < 32; ++i) { const int k = k0 + 2 * i + (lane >> 5); float x = v[i] * wscale; if (KS) x *= (k < ksplit ? ksA[k] : ksB[k - ksplit]); scr[(2 * i + (lane >> 5)) * 33 + (lane & 31)] = x; }
;     LDS_WAIT(); asm volatile("" ::: "memory");
;     const int c = lane & 7;
; #pragma unroll
;     for (int j = 0; j < 4; ++j) { const int n = (lane >> 3) + 8 * j; const LAS float* s = scr + (8 * c) * 33 + n;
;         const unsigned long long o = (unsigned long long)pg8::pk4_fp8(s[0 * 33], s[1 * 33], s[2 * 33], s[3 * 33]) | ((unsigned long long)pg8::pk4_fp8(s[4 * 33], s[5 * 33], s[6 * 33], s[7 * 33]) << 32);
;         *(GAS unsigned long long*)(WT + (size_t)(n0 + n) * K + k0 + 8 * c) = o; }
;     LDS_WAIT(); asm volatile("" ::: "memory");
; }
	s_add_i32 s24, s23, 8
	s_lshl_b32 s20, s24, 7
	s_cmp_lt_u32 s24, 40
	s_cselect_b32 s21, 0, 0x830
	s_cmp_lt_u32 s24, 72
	s_cselect_b32 s21, s21, 0xfffff030
	s_add_i32 s20, s20, s21
	s_lshl_b32 s20, s20, 2
	s_add_u32 s8, s46, s20
	s_addc_u32 s9, s47, 0
	global_load_dwordx4 v[176:179], v76, s[8:9]
	s_add_u32 s8, s8, 0x16280
	s_addc_u32 s9, s9, 0
	global_load_dwordx4 v[180:183], v76, s[8:9]
	s_add_u32 s8, s8, 0x16280
	s_addc_u32 s9, s9, 0
	global_load_dwordx4 v[184:187], v76, s[8:9]
	s_add_u32 s8, s8, 0x16280
	s_addc_u32 s9, s9, 0
	global_load_dwordx4 v[188:191], v76, s[8:9]
	s_add_u32 s8, s8, 0x16280
	s_addc_u32 s9, s9, 0
	global_load_dwordx4 v[192:195], v76, s[8:9]
	s_add_u32 s8, s8, 0x16280
	s_addc_u32 s9, s9, 0
	global_load_dwordx4 v[196:199], v76, s[8:9]
	s_add_u32 s8, s8, 0x16280
	s_addc_u32 s9, s9, 0
	global_load_dwordx4 v[200:203], v76, s[8:9]
	s_add_u32 s8, s8, 0x16280
	s_addc_u32 s9, s9, 0
	global_load_dwordx4 v[204:207], v76, s[8:9]
	s_add_u32 s6, s44, 0x3003000
	s_addc_u32 s7, s45, 0
	ds_read_b32 v226, v212
	ds_read_b32 v227, v212 offset:512
	ds_read_b32 v228, v212 offset:1024
	ds_read_b32 v229, v212 offset:1536
	ds_read_b32 v230, v212 offset:2048
	ds_read_b32 v231, v212 offset:2560
	ds_read_b32 v232, v212 offset:3072
	ds_read_b32 v233, v212 offset:3584
	ds_read_b32 v234, v212 offset:4096
	ds_read_b32 v235, v212 offset:4608
	ds_read_b32 v236, v212 offset:5120
	ds_read_b32 v237, v212 offset:5632
	ds_read_b32 v238, v212 offset:6144
	ds_read_b32 v239, v212 offset:6656
	ds_read_b32 v240, v212 offset:7168
	ds_read_b32 v241, v212 offset:7680
	s_waitcnt lgkmcnt(0)
	v_max_f32_e32 v226, v226, v226
	v_max_f32_e32 v227, v227, v227
	v_max_f32_e32 v228, v228, v228
	v_max_f32_e32 v229, v229, v229
	v_max_f32_e32 v230, v230, v230
	v_max_f32_e32 v231, v231, v231
	v_max_f32_e32 v232, v232, v232
	v_max_f32_e32 v233, v233, v233
	v_max_f32_e32 v234, v234, v234
	v_max_f32_e32 v235, v235, v235
	v_max_f32_e32 v236, v236, v236
	v_max_f32_e32 v237, v237, v237
	v_max_f32_e32 v238, v238, v238
	v_max_f32_e32 v239, v239, v239
	v_max_f32_e32 v240, v240, v240
	v_max_f32_e32 v241, v241, v241
	v_med3_f32 v226, v226, s62, v95
	v_med3_f32 v227, v227, s62, v95
	v_med3_f32 v228, v228, s62, v95
	v_med3_f32 v229, v229, s62, v95
	v_med3_f32 v230, v230, s62, v95
	v_med3_f32 v231, v231, s62, v95
	v_med3_f32 v232, v232, s62, v95
	v_med3_f32 v233, v233, s62, v95
	v_med3_f32 v234, v234, s62, v95
	v_med3_f32 v235, v235, s62, v95
	v_med3_f32 v236, v236, s62, v95
	v_med3_f32 v237, v237, s62, v95
	v_med3_f32 v238, v238, s62, v95
	v_med3_f32 v239, v239, s62, v95
	v_med3_f32 v240, v240, s62, v95
	v_med3_f32 v241, v241, s62, v95
	v_mov_b32_e32 v242, 0
	v_mov_b32_e32 v243, 0
	v_mov_b32_e32 v244, 0
	v_mov_b32_e32 v245, 0
	v_cvt_pk_fp8_f32 v242, v226, v227
	v_cvt_pk_fp8_f32 v243, v230, v231
	v_cvt_pk_fp8_f32 v244, v234, v235
	v_cvt_pk_fp8_f32 v245, v238, v239
	v_cvt_pk_fp8_f32 v242, v228, v229 op_sel:[0,0,1]
	v_cvt_pk_fp8_f32 v243, v232, v233 op_sel:[0,0,1]
	v_cvt_pk_fp8_f32 v244, v236, v237 op_sel:[0,0,1]
	v_cvt_pk_fp8_f32 v245, v240, v241 op_sel:[0,0,1]
	s_nop 0
	global_store_dwordx4 v79, v[242:245], s[6:7]
	ds_read_b32 v226, v214
	ds_read_b32 v227, v214 offset:512
	ds_read_b32 v228, v214 offset:1024
	ds_read_b32 v229, v214 offset:1536
	ds_read_b32 v230, v214 offset:2048
	ds_read_b32 v231, v214 offset:2560
	ds_read_b32 v232, v214 offset:3072
	ds_read_b32 v233, v214 offset:3584
	ds_read_b32 v234, v214 offset:4096
	ds_read_b32 v235, v214 offset:4608
	ds_read_b32 v236, v214 offset:5120
	ds_read_b32 v237, v214 offset:5632
	ds_read_b32 v238, v214 offset:6144
	ds_read_b32 v239, v214 offset:6656
	ds_read_b32 v240, v214 offset:7168
	ds_read_b32 v241, v214 offset:7680
	s_waitcnt lgkmcnt(0)
	v_max_f32_e32 v226, v226, v226
	v_max_f32_e32 v227, v227, v227
	v_max_f32_e32 v228, v228, v228
	v_max_f32_e32 v229, v229, v229
	v_max_f32_e32 v230, v230, v230
	v_max_f32_e32 v231, v231, v231
	v_max_f32_e32 v232, v232, v232
	v_max_f32_e32 v233, v233, v233
	v_max_f32_e32 v234, v234, v234
	v_max_f32_e32 v235, v235, v235
	v_max_f32_e32 v236, v236, v236
	v_max_f32_e32 v237, v237, v237
	v_max_f32_e32 v238, v238, v238
	v_max_f32_e32 v239, v239, v239
	v_max_f32_e32 v240, v240, v240
	v_max_f32_e32 v241, v241, v241
	v_med3_f32 v226, v226, s62, v95
	v_med3_f32 v227, v227, s62, v95
	v_med3_f32 v228, v228, s62, v95
	v_med3_f32 v229, v229, s62, v95
	v_med3_f32 v230, v230, s62, v95
	v_med3_f32 v231, v231, s62, v95
	v_med3_f32 v232, v232, s62, v95
	v_med3_f32 v233, v233, s62, v95
	v_med3_f32 v234, v234, s62, v95
	v_med3_f32 v235, v235, s62, v95
	v_med3_f32 v236, v236, s62, v95
	v_med3_f32 v237, v237, s62, v95
	v_med3_f32 v238, v238, s62, v95
	v_med3_f32 v239, v239, s62, v95
	v_med3_f32 v240, v240, s62, v95
	v_med3_f32 v241, v241, s62, v95
	v_mov_b32_e32 v242, 0
	v_mov_b32_e32 v243, 0
	v_mov_b32_e32 v244, 0
	v_mov_b32_e32 v245, 0
	v_cvt_pk_fp8_f32 v242, v226, v227
	v_cvt_pk_fp8_f32 v243, v230, v231
	v_cvt_pk_fp8_f32 v244, v234, v235
	v_cvt_pk_fp8_f32 v245, v238, v239
	v_cvt_pk_fp8_f32 v242, v228, v229 op_sel:[0,0,1]
	v_cvt_pk_fp8_f32 v243, v232, v233 op_sel:[0,0,1]
	v_cvt_pk_fp8_f32 v244, v236, v237 op_sel:[0,0,1]
	v_cvt_pk_fp8_f32 v245, v240, v241 op_sel:[0,0,1]
	s_nop 0
	global_store_dwordx4 v80, v[242:245], s[6:7]
	s_waitcnt vmcnt(12)
	v_mul_f32_e32 v144, v42, v144
	v_mul_f32_e32 v145, v42, v145
	v_mul_f32_e32 v146, v42, v146
	v_mul_f32_e32 v147, v42, v147
	ds_write_b128 v209, v[144:147]
	v_mul_f32_e32 v148, v43, v148
	v_mul_f32_e32 v149, v43, v149
	v_mul_f32_e32 v150, v43, v150
	v_mul_f32_e32 v151, v43, v151
	ds_write_b128 v209, v[148:151] offset:1024
	v_mul_f32_e32 v152, v44, v152
	v_mul_f32_e32 v153, v44, v153
	v_mul_f32_e32 v154, v44, v154
	v_mul_f32_e32 v155, v44, v155
	ds_write_b128 v209, v[152:155] offset:2048
	v_mul_f32_e32 v156, v45, v156
	v_mul_f32_e32 v157, v45, v157
	v_mul_f32_e32 v158, v45, v158
	v_mul_f32_e32 v159, v45, v159
	ds_write_b128 v209, v[156:159] offset:3072
	v_mul_f32_e32 v160, v46, v160
	v_mul_f32_e32 v161, v46, v161
	v_mul_f32_e32 v162, v46, v162
	v_mul_f32_e32 v163, v46, v163
	ds_write_b128 v209, v[160:163] offset:4096
	v_mul_f32_e32 v164, v47, v164
	v_mul_f32_e32 v165, v47, v165
	v_mul_f32_e32 v166, v47, v166
	v_mul_f32_e32 v167, v47, v167
	ds_write_b128 v209, v[164:167] offset:5120
	v_mul_f32_e32 v168, v48, v168
	v_mul_f32_e32 v169, v48, v169
	v_mul_f32_e32 v170, v48, v170
	v_mul_f32_e32 v171, v48, v171
	ds_write_b128 v209, v[168:171] offset:6144
	v_mul_f32_e32 v172, v49, v172
	v_mul_f32_e32 v173, v49, v173
	v_mul_f32_e32 v174, v49, v174
	v_mul_f32_e32 v175, v49, v175
	ds_write_b128 v209, v[172:175] offset:7168
	s_waitcnt lgkmcnt(0)
	s_barrier
; #define GAS __attribute__((address_space(1)))
; #define LAS __attribute__((address_space(3)))
; #define LDS_WAIT() asm volatile("s_waitcnt lgkmcnt(0)" ::: "memory")
; __device__ __forceinline__ unsigned pk2(float lo, float hi) { return f2bf(lo) | (f2bf(hi) << 16); }
; __device__ __forceinline__ int nat_dim(int p) { return (p >> 1) + 64 * (p & 1); }
; __device__ __forceinline__ int src_col_in(int c) {
;     if (c < 5120) { const int blk = c >> 7, p = c & 127; const bool rope = blk < 16 || ((((blk - 16) >> 2) & 1) == 0); const int d = rope ? (p >> 1) + 64 * (p & 1) : p; return blk * 128 + d; }
;     if (c < OFF_Z) return c + 2096;
;     if (c < OFF_G) return c - 4048;
;     if (c < OFF_DT) return 5120 + (c - OFF_G);
;     if (c < NSRC) return c;
;     return -1;
; }
; template <int MAP, bool KS, bool KPERM = false>
; __device__ __forceinline__ void p0_transpose_item(const float* W, int K, int Nsrc, int nblk, bf16* WT, const float* ksA, const float* ksB, int ksplit, LAS float* scr, int item, int lane) {
;     const int kb = item / nblk, nb = item % nblk, k0 = 64 * kb, n0 = 32 * nb;
;     const int nr = n0 + (lane & 31); const int sc = MAP == 1 ? src_col_in(nr) : (MAP == 2 ? nat_dim(nr) : nr);
;     float v[32];
; #pragma unroll
;     for (int i = 0; i < 32; ++i) { const int k = k0 + 2 * i + (lane >> 5); const int ksrc = KPERM ? ((k & ~127) + nat_dim(k & 127)) : k;
;         v[i] = sc >= 0 ? W[(size_t)ksrc * Nsrc + sc] : 0.f; }
; #pragma unroll
;     for (int i = 0; i < 32; ++i) { const int kk = 2 * i + (lane >> 5); const int k = k0 + kk;
;         if (KS) v[i] *= (k < ksplit ? ksA[k] : ksB[k - ksplit]);
;         scr[kk * 33 + (lane & 31)] = v[i]; }
;     LDS_WAIT(); asm volatile("" ::: "memory");
;     const int c = lane & 7;
; #pragma unroll
;     for (int j = 0; j < 4; ++j) { const int n = (lane >> 3) + 8 * j; const LAS float* s = scr + (8 * c) * 33 + n;
;         v4u o; o.x = pk2(s[0 * 33], s[1 * 33]); o.y = pk2(s[2 * 33], s[3 * 33]); o.z = pk2(s[4 * 33], s[5 * 33]); o.w = pk2(s[6 * 33], s[7 * 33]);
;         *(GAS v4u*)(WT + (size_t)(n0 + n) * K + k0 + 8 * c) = o; }
;     LDS_WAIT(); asm volatile("" ::: "memory");
; }
	s_add_i32 s24, s23, 16
	s_lshl_b32 s20, s24, 7
	s_cmp_lt_u32 s24, 40
	s_cselect_b32 s21, 0, 0x830
	s_cmp_lt_u32 s24, 72
	s_cselect_b32 s21, s21, 0xfffff030
	s_add_i32 s20, s20, s21
	s_lshl_b32 s20, s20, 2
	s_add_u32 s8, s46, s20
	s_addc_u32 s9, s47, 0
	global_load_dwordx4 v[144:147], v76, s[8:9]
	s_add_u32 s8, s8, 0x16280
	s_addc_u32 s9, s9, 0
	global_load_dwordx4 v[148:151], v76, s[8:9]
	s_add_u32 s8, s8, 0x16280
	s_addc_u32 s9, s9, 0
	global_load_dwordx4 v[152:155], v76, s[8:9]
	s_add_u32 s8, s8, 0x16280
	s_addc_u32 s9, s9, 0
	global_load_dwordx4 v[156:159], v76, s[8:9]
	s_add_u32 s8, s8, 0x16280
	s_addc_u32 s9, s9, 0
	global_load_dwordx4 v[160:163], v76, s[8:9]
	s_add_u32 s8, s8, 0x16280
	s_addc_u32 s9, s9, 0
	global_load_dwordx4 v[164:167], v76, s[8:9]
	s_add_u32 s8, s8, 0x16280
	s_addc_u32 s9, s9, 0
	global_load_dwordx4 v[168:171], v76, s[8:9]
	s_add_u32 s8, s8, 0x16280
	s_addc_u32 s9, s9, 0
	global_load_dwordx4 v[172:175], v76, s[8:9]
	s_add_i32 s24, s23, 0
	s_mul_i32 s20, s24, 0x100000
	s_add_u32 s6, s48, s20
	s_addc_u32 s7, s49, 0
	s_cmp_lt_u32 s24, 16
	s_cselect_b32 s20, 1, 0
	s_sub_i32 s21, s24, 16
	s_bitcmp0_b32 s21, 2
	s_cselect_b32 s21, 1, 0
	s_cmp_lt_u32 s24, 40
	s_cselect_b32 s21, s21, 0
	s_or_b32 s20, s20, s21
	s_cmp_lg_u32 s20, 0
	s_cselect_b64 s[20:21], -1, 0
	v_cndmask_b32_e64 v91, v83, v87, s[20:21]
	v_cndmask_b32_e64 v92, v84, v88, s[20:21]
	v_cndmask_b32_e64 v93, v85, v89, s[20:21]
	v_cndmask_b32_e64 v94, v86, v90, s[20:21]
	ds_read_b32 v226, v112
	ds_read_b32 v227, v112 offset:512
	ds_read_b32 v228, v112 offset:1024
	ds_read_b32 v229, v112 offset:1536
	ds_read_b32 v230, v112 offset:2048
	ds_read_b32 v231, v112 offset:2560
	ds_read_b32 v232, v112 offset:3072
	ds_read_b32 v233, v112 offset:3584
	s_waitcnt lgkmcnt(0)
	v_bfe_u32 v120, v226, 16, 1
	v_bfe_u32 v121, v227, 16, 1
	v_bfe_u32 v122, v228, 16, 1
	v_bfe_u32 v123, v229, 16, 1
	v_bfe_u32 v124, v230, 16, 1
	v_bfe_u32 v125, v231, 16, 1
	v_bfe_u32 v126, v232, 16, 1
	v_bfe_u32 v127, v233, 16, 1
	v_add3_u32 v226, v226, v120, s63
	v_add3_u32 v227, v227, v121, s63
	v_add3_u32 v228, v228, v122, s63
	v_add3_u32 v229, v229, v123, s63
	v_add3_u32 v230, v230, v124, s63
	v_add3_u32 v231, v231, v125, s63
	v_add3_u32 v232, v232, v126, s63
	v_add3_u32 v233, v233, v127, s63
	v_perm_b32 v242, v227, v226, s64
	v_perm_b32 v243, v229, v228, s64
	v_perm_b32 v244, v231, v230, s64
	v_perm_b32 v245, v233, v232, s64
	s_nop 0
	global_store_dwordx4 v91, v[242:245], s[6:7]
	ds_read_b32 v226, v114
	ds_read_b32 v227, v114 offset:512
	ds_read_b32 v228, v114 offset:1024
	ds_read_b32 v229, v114 offset:1536
	ds_read_b32 v230, v114 offset:2048
	ds_read_b32 v231, v114 offset:2560
	ds_read_b32 v232, v114 offset:3072
	ds_read_b32 v233, v114 offset:3584
	s_waitcnt lgkmcnt(0)
	v_bfe_u32 v120, v226, 16, 1
	v_bfe_u32 v121, v227, 16, 1
	v_bfe_u32 v122, v228, 16, 1
	v_bfe_u32 v123, v229, 16, 1
	v_bfe_u32 v124, v230, 16, 1
	v_bfe_u32 v125, v231, 16, 1
	v_bfe_u32 v126, v232, 16, 1
	v_bfe_u32 v127, v233, 16, 1
	v_add3_u32 v226, v226, v120, s63
	v_add3_u32 v227, v227, v121, s63
	v_add3_u32 v228, v228, v122, s63
	v_add3_u32 v229, v229, v123, s63
	v_add3_u32 v230, v230, v124, s63
	v_add3_u32 v231, v231, v125, s63
	v_add3_u32 v232, v232, v126, s63
	v_add3_u32 v233, v233, v127, s63
	v_perm_b32 v242, v227, v226, s64
	v_perm_b32 v243, v229, v228, s64
	v_perm_b32 v244, v231, v230, s64
	v_perm_b32 v245, v233, v232, s64
	s_nop 0
	global_store_dwordx4 v92, v[242:245], s[6:7]
	ds_read_b32 v226, v116
	ds_read_b32 v227, v116 offset:512
	ds_read_b32 v228, v116 offset:1024
	ds_read_b32 v229, v116 offset:1536
	ds_read_b32 v230, v116 offset:2048
	ds_read_b32 v231, v116 offset:2560
	ds_read_b32 v232, v116 offset:3072
	ds_read_b32 v233, v116 offset:3584
	s_waitcnt lgkmcnt(0)
	v_bfe_u32 v120, v226, 16, 1
	v_bfe_u32 v121, v227, 16, 1
	v_bfe_u32 v122, v228, 16, 1
	v_bfe_u32 v123, v229, 16, 1
	v_bfe_u32 v124, v230, 16, 1
	v_bfe_u32 v125, v231, 16, 1
	v_bfe_u32 v126, v232, 16, 1
	v_bfe_u32 v127, v233, 16, 1
	v_add3_u32 v226, v226, v120, s63
	v_add3_u32 v227, v227, v121, s63
	v_add3_u32 v228, v228, v122, s63
	v_add3_u32 v229, v229, v123, s63
	v_add3_u32 v230, v230, v124, s63
	v_add3_u32 v231, v231, v125, s63
	v_add3_u32 v232, v232, v126, s63
	v_add3_u32 v233, v233, v127, s63
	v_perm_b32 v242, v227, v226, s64
	v_perm_b32 v243, v229, v228, s64
	v_perm_b32 v244, v231, v230, s64
	v_perm_b32 v245, v233, v232, s64
	s_nop 0
	global_store_dwordx4 v93, v[242:245], s[6:7]
	ds_read_b32 v226, v118
	ds_read_b32 v227, v118 offset:512
	ds_read_b32 v228, v118 offset:1024
	ds_read_b32 v229, v118 offset:1536
	ds_read_b32 v230, v118 offset:2048
	ds_read_b32 v231, v118 offset:2560
	ds_read_b32 v232, v118 offset:3072
	ds_read_b32 v233, v118 offset:3584
	s_waitcnt lgkmcnt(0)
	v_bfe_u32 v120, v226, 16, 1
	v_bfe_u32 v121, v227, 16, 1
	v_bfe_u32 v122, v228, 16, 1
	v_bfe_u32 v123, v229, 16, 1
	v_bfe_u32 v124, v230, 16, 1
	v_bfe_u32 v125, v231, 16, 1
	v_bfe_u32 v126, v232, 16, 1
	v_bfe_u32 v127, v233, 16, 1
	v_add3_u32 v226, v226, v120, s63
	v_add3_u32 v227, v227, v121, s63
	v_add3_u32 v228, v228, v122, s63
	v_add3_u32 v229, v229, v123, s63
	v_add3_u32 v230, v230, v124, s63
	v_add3_u32 v231, v231, v125, s63
	v_add3_u32 v232, v232, v126, s63
	v_add3_u32 v233, v233, v127, s63
	v_perm_b32 v242, v227, v226, s64
	v_perm_b32 v243, v229, v228, s64
	v_perm_b32 v244, v231, v230, s64
	v_perm_b32 v245, v233, v232, s64
	s_nop 0
	global_store_dwordx4 v94, v[242:245], s[6:7]
	s_waitcnt vmcnt(14)
	v_mul_f32_e32 v176, v42, v176
	v_mul_f32_e32 v177, v42, v177
	v_mul_f32_e32 v178, v42, v178
	v_mul_f32_e32 v179, v42, v179
	ds_write_b128 v210, v[176:179]
	v_mul_f32_e32 v180, v43, v180
	v_mul_f32_e32 v181, v43, v181
	v_mul_f32_e32 v182, v43, v182
	v_mul_f32_e32 v183, v43, v183
	ds_write_b128 v210, v[180:183] offset:1024
	v_mul_f32_e32 v184, v44, v184
	v_mul_f32_e32 v185, v44, v185
	v_mul_f32_e32 v186, v44, v186
	v_mul_f32_e32 v187, v44, v187
	ds_write_b128 v210, v[184:187] offset:2048
	v_mul_f32_e32 v188, v45, v188
	v_mul_f32_e32 v189, v45, v189
	v_mul_f32_e32 v190, v45, v190
	v_mul_f32_e32 v191, v45, v191
	ds_write_b128 v210, v[188:191] offset:3072
	v_mul_f32_e32 v192, v46, v192
	v_mul_f32_e32 v193, v46, v193
	v_mul_f32_e32 v194, v46, v194
	v_mul_f32_e32 v195, v46, v195
	ds_write_b128 v210, v[192:195] offset:4096
	v_mul_f32_e32 v196, v47, v196
	v_mul_f32_e32 v197, v47, v197
	v_mul_f32_e32 v198, v47, v198
	v_mul_f32_e32 v199, v47, v199
	ds_write_b128 v210, v[196:199] offset:5120
	v_mul_f32_e32 v200, v48, v200
	v_mul_f32_e32 v201, v48, v201
	v_mul_f32_e32 v202, v48, v202
	v_mul_f32_e32 v203, v48, v203
	ds_write_b128 v210, v[200:203] offset:6144
	v_mul_f32_e32 v204, v49, v204
	v_mul_f32_e32 v205, v49, v205
	v_mul_f32_e32 v206, v49, v206
	v_mul_f32_e32 v207, v49, v207
	ds_write_b128 v210, v[204:207] offset:7168
	s_waitcnt lgkmcnt(0)
	s_barrier
; #define GAS __attribute__((address_space(1)))
; #define LAS __attribute__((address_space(3)))
; #define LDS_WAIT() asm volatile("s_waitcnt lgkmcnt(0)" ::: "memory")
; __device__ __forceinline__ unsigned pk2(float lo, float hi) { return f2bf(lo) | (f2bf(hi) << 16); }
; __device__ __forceinline__ int nat_dim(int p) { return (p >> 1) + 64 * (p & 1); }
; __device__ __forceinline__ int src_col_in(int c) {
;     if (c < 5120) { const int blk = c >> 7, p = c & 127; const bool rope = blk < 16 || ((((blk - 16) >> 2) & 1) == 0); const int d = rope ? (p >> 1) + 64 * (p & 1) : p; return blk * 128 + d; }
;     if (c < OFF_Z) return c + 2096;
;     if (c < OFF_G) return c - 4048;
;     if (c < OFF_DT) return 5120 + (c - OFF_G);
;     if (c < NSRC) return c;
;     return -1;
; }
; template <int MAP, bool KS, bool KPERM = false>
; __device__ __forceinline__ void p0_transpose_item(const float* W, int K, int Nsrc, int nblk, bf16* WT, const float* ksA, const float* ksB, int ksplit, LAS float* scr, int item, int lane) {
;     const int kb = item / nblk, nb = item % nblk, k0 = 64 * kb, n0 = 32 * nb;
;     const int nr = n0 + (lane & 31); const int sc = MAP == 1 ? src_col_in(nr) : (MAP == 2 ? nat_dim(nr) : nr);
;     float v[32];
; #pragma unroll
;     for (int i = 0; i < 32; ++i) { const int k = k0 + 2 * i + (lane >> 5); const int ksrc = KPERM ? ((k & ~127) + nat_dim(k & 127)) : k;
;         v[i] = sc >= 0 ? W[(size_t)ksrc * Nsrc + sc] : 0.f; }
; #pragma unroll
;     for (int i = 0; i < 32; ++i) { const int kk = 2 * i + (lane >> 5); const int k = k0 + kk;
;         if (KS) v[i] *= (k < ksplit ? ksA[k] : ksB[k - ksplit]);
;         scr[kk * 33 + (lane & 31)] = v[i]; }
;     LDS_WAIT(); asm volatile("" ::: "memory");
;     const int c = lane & 7;
; #pragma unroll
;     for (int j = 0; j < 4; ++j) { const int n = (lane >> 3) + 8 * j; const LAS float* s = scr + (8 * c) * 33 + n;
;         v4u o; o.x = pk2(s[0 * 33], s[1 * 33]); o.y = pk2(s[2 * 33], s[3 * 33]); o.z = pk2(s[4 * 33], s[5 * 33]); o.w = pk2(s[6 * 33], s[7 * 33]);
;         *(GAS v4u*)(WT + (size_t)(n0 + n) * K + k0 + 8 * c) = o; }
;     LDS_WAIT(); asm volatile("" ::: "memory");
; }
	s_add_i32 s24, s23, 24
	s_lshl_b32 s20, s24, 7
	s_cmp_lt_u32 s24, 40
	s_cselect_b32 s21, 0, 0x830
	s_cmp_lt_u32 s24, 72
	s_cselect_b32 s21, s21, 0xfffff030
	s_add_i32 s20, s20, s21
	s_lshl_b32 s20, s20, 2
	s_add_u32 s8, s46, s20
	s_addc_u32 s9, s47, 0
	global_load_dwordx4 v[176:179], v76, s[8:9]
	s_add_u32 s8, s8, 0x16280
	s_addc_u32 s9, s9, 0
	global_load_dwordx4 v[180:183], v76, s[8:9]
	s_add_u32 s8, s8, 0x16280
	s_addc_u32 s9, s9, 0
	global_load_dwordx4 v[184:187], v76, s[8:9]
	s_add_u32 s8, s8, 0x16280
	s_addc_u32 s9, s9, 0
	global_load_dwordx4 v[188:191], v76, s[8:9]
	s_add_u32 s8, s8, 0x16280
	s_addc_u32 s9, s9, 0
	global_load_dwordx4 v[192:195], v76, s[8:9]
	s_add_u32 s8, s8, 0x16280
	s_addc_u32 s9, s9, 0
	global_load_dwordx4 v[196:199], v76, s[8:9]
	s_add_u32 s8, s8, 0x16280
	s_addc_u32 s9, s9, 0
	global_load_dwordx4 v[200:203], v76, s[8:9]
	s_add_u32 s8, s8, 0x16280
	s_addc_u32 s9, s9, 0
	global_load_dwordx4 v[204:207], v76, s[8:9]
	s_add_i32 s24, s23, 8
	s_mul_i32 s20, s24, 0x100000
	s_add_u32 s6, s48, s20
	s_addc_u32 s7, s49, 0
	s_cmp_lt_u32 s24, 16
	s_cselect_b32 s20, 1, 0
	s_sub_i32 s21, s24, 16
	s_bitcmp0_b32 s21, 2
	s_cselect_b32 s21, 1, 0
	s_cmp_lt_u32 s24, 40
	s_cselect_b32 s21, s21, 0
	s_or_b32 s20, s20, s21
	s_cmp_lg_u32 s20, 0
	s_cselect_b64 s[20:21], -1, 0
	v_cndmask_b32_e64 v91, v83, v87, s[20:21]
	v_cndmask_b32_e64 v92, v84, v88, s[20:21]
	v_cndmask_b32_e64 v93, v85, v89, s[20:21]
	v_cndmask_b32_e64 v94, v86, v90, s[20:21]
	ds_read_b32 v226, v113
	ds_read_b32 v227, v113 offset:512
	ds_read_b32 v228, v113 offset:1024
	ds_read_b32 v229, v113 offset:1536
	ds_read_b32 v230, v113 offset:2048
	ds_read_b32 v231, v113 offset:2560
	ds_read_b32 v232, v113 offset:3072
	ds_read_b32 v233, v113 offset:3584
	s_waitcnt lgkmcnt(0)
	v_bfe_u32 v120, v226, 16, 1
	v_bfe_u32 v121, v227, 16, 1
	v_bfe_u32 v122, v228, 16, 1
	v_bfe_u32 v123, v229, 16, 1
	v_bfe_u32 v124, v230, 16, 1
	v_bfe_u32 v125, v231, 16, 1
	v_bfe_u32 v126, v232, 16, 1
	v_bfe_u32 v127, v233, 16, 1
	v_add3_u32 v226, v226, v120, s63
	v_add3_u32 v227, v227, v121, s63
	v_add3_u32 v228, v228, v122, s63
	v_add3_u32 v229, v229, v123, s63
	v_add3_u32 v230, v230, v124, s63
	v_add3_u32 v231, v231, v125, s63
	v_add3_u32 v232, v232, v126, s63
	v_add3_u32 v233, v233, v127, s63
	v_perm_b32 v242, v227, v226, s64
	v_perm_b32 v243, v229, v228, s64
	v_perm_b32 v244, v231, v230, s64
	v_perm_b32 v245, v233, v232, s64
	s_nop 0
	global_store_dwordx4 v91, v[242:245], s[6:7]
	ds_read_b32 v226, v115
	ds_read_b32 v227, v115 offset:512
	ds_read_b32 v228, v115 offset:1024
	ds_read_b32 v229, v115 offset:1536
	ds_read_b32 v230, v115 offset:2048
	ds_read_b32 v231, v115 offset:2560
	ds_read_b32 v232, v115 offset:3072
	ds_read_b32 v233, v115 offset:3584
	s_waitcnt lgkmcnt(0)
	v_bfe_u32 v120, v226, 16, 1
	v_bfe_u32 v121, v227, 16, 1
	v_bfe_u32 v122, v228, 16, 1
	v_bfe_u32 v123, v229, 16, 1
	v_bfe_u32 v124, v230, 16, 1
	v_bfe_u32 v125, v231, 16, 1
	v_bfe_u32 v126, v232, 16, 1
	v_bfe_u32 v127, v233, 16, 1
	v_add3_u32 v226, v226, v120, s63
	v_add3_u32 v227, v227, v121, s63
	v_add3_u32 v228, v228, v122, s63
	v_add3_u32 v229, v229, v123, s63
	v_add3_u32 v230, v230, v124, s63
	v_add3_u32 v231, v231, v125, s63
	v_add3_u32 v232, v232, v126, s63
	v_add3_u32 v233, v233, v127, s63
	v_perm_b32 v242, v227, v226, s64
	v_perm_b32 v243, v229, v228, s64
	v_perm_b32 v244, v231, v230, s64
	v_perm_b32 v245, v233, v232, s64
	s_nop 0
	global_store_dwordx4 v92, v[242:245], s[6:7]
	ds_read_b32 v226, v117
	ds_read_b32 v227, v117 offset:512
	ds_read_b32 v228, v117 offset:1024
	ds_read_b32 v229, v117 offset:1536
	ds_read_b32 v230, v117 offset:2048
	ds_read_b32 v231, v117 offset:2560
	ds_read_b32 v232, v117 offset:3072
	ds_read_b32 v233, v117 offset:3584
	s_waitcnt lgkmcnt(0)
	v_bfe_u32 v120, v226, 16, 1
	v_bfe_u32 v121, v227, 16, 1
	v_bfe_u32 v122, v228, 16, 1
	v_bfe_u32 v123, v229, 16, 1
	v_bfe_u32 v124, v230, 16, 1
	v_bfe_u32 v125, v231, 16, 1
	v_bfe_u32 v126, v232, 16, 1
	v_bfe_u32 v127, v233, 16, 1
	v_add3_u32 v226, v226, v120, s63
	v_add3_u32 v227, v227, v121, s63
	v_add3_u32 v228, v228, v122, s63
	v_add3_u32 v229, v229, v123, s63
	v_add3_u32 v230, v230, v124, s63
	v_add3_u32 v231, v231, v125, s63
	v_add3_u32 v232, v232, v126, s63
	v_add3_u32 v233, v233, v127, s63
	v_perm_b32 v242, v227, v226, s64
	v_perm_b32 v243, v229, v228, s64
	v_perm_b32 v244, v231, v230, s64
	v_perm_b32 v245, v233, v232, s64
	s_nop 0
	global_store_dwordx4 v93, v[242:245], s[6:7]
	ds_read_b32 v226, v119
	ds_read_b32 v227, v119 offset:512
	ds_read_b32 v228, v119 offset:1024
	ds_read_b32 v229, v119 offset:1536
	ds_read_b32 v230, v119 offset:2048
	ds_read_b32 v231, v119 offset:2560
	ds_read_b32 v232, v119 offset:3072
	ds_read_b32 v233, v119 offset:3584
	s_waitcnt lgkmcnt(0)
	v_bfe_u32 v120, v226, 16, 1
	v_bfe_u32 v121, v227, 16, 1
	v_bfe_u32 v122, v228, 16, 1
	v_bfe_u32 v123, v229, 16, 1
	v_bfe_u32 v124, v230, 16, 1
	v_bfe_u32 v125, v231, 16, 1
	v_bfe_u32 v126, v232, 16, 1
	v_bfe_u32 v127, v233, 16, 1
	v_add3_u32 v226, v226, v120, s63
	v_add3_u32 v227, v227, v121, s63
	v_add3_u32 v228, v228, v122, s63
	v_add3_u32 v229, v229, v123, s63
	v_add3_u32 v230, v230, v124, s63
	v_add3_u32 v231, v231, v125, s63
	v_add3_u32 v232, v232, v126, s63
	v_add3_u32 v233, v233, v127, s63
	v_perm_b32 v242, v227, v226, s64
	v_perm_b32 v243, v229, v228, s64
	v_perm_b32 v244, v231, v230, s64
	v_perm_b32 v245, v233, v232, s64
	s_nop 0
	global_store_dwordx4 v94, v[242:245], s[6:7]
	s_waitcnt vmcnt(16)
	v_mul_f32_e32 v144, v42, v144
	v_mul_f32_e32 v145, v42, v145
	v_mul_f32_e32 v146, v42, v146
	v_mul_f32_e32 v147, v42, v147
	ds_write_b128 v209, v[144:147]
	v_mul_f32_e32 v148, v43, v148
	v_mul_f32_e32 v149, v43, v149
	v_mul_f32_e32 v150, v43, v150
	v_mul_f32_e32 v151, v43, v151
	ds_write_b128 v209, v[148:151] offset:1024
	v_mul_f32_e32 v152, v44, v152
	v_mul_f32_e32 v153, v44, v153
	v_mul_f32_e32 v154, v44, v154
	v_mul_f32_e32 v155, v44, v155
	ds_write_b128 v209, v[152:155] offset:2048
	v_mul_f32_e32 v156, v45, v156
	v_mul_f32_e32 v157, v45, v157
	v_mul_f32_e32 v158, v45, v158
	v_mul_f32_e32 v159, v45, v159
	ds_write_b128 v209, v[156:159] offset:3072
	v_mul_f32_e32 v160, v46, v160
	v_mul_f32_e32 v161, v46, v161
	v_mul_f32_e32 v162, v46, v162
	v_mul_f32_e32 v163, v46, v163
	ds_write_b128 v209, v[160:163] offset:4096
	v_mul_f32_e32 v164, v47, v164
	v_mul_f32_e32 v165, v47, v165
	v_mul_f32_e32 v166, v47, v166
	v_mul_f32_e32 v167, v47, v167
	ds_write_b128 v209, v[164:167] offset:5120
	v_mul_f32_e32 v168, v48, v168
	v_mul_f32_e32 v169, v48, v169
	v_mul_f32_e32 v170, v48, v170
	v_mul_f32_e32 v171, v48, v171
	ds_write_b128 v209, v[168:171] offset:6144
	v_mul_f32_e32 v172, v49, v172
	v_mul_f32_e32 v173, v49, v173
	v_mul_f32_e32 v174, v49, v174
	v_mul_f32_e32 v175, v49, v175
	ds_write_b128 v209, v[172:175] offset:7168
	s_waitcnt lgkmcnt(0)
	s_barrier
; #define GAS __attribute__((address_space(1)))
; #define LAS __attribute__((address_space(3)))
; #define LDS_WAIT() asm volatile("s_waitcnt lgkmcnt(0)" ::: "memory")
; __device__ __forceinline__ unsigned pk2(float lo, float hi) { return f2bf(lo) | (f2bf(hi) << 16); }
; __device__ __forceinline__ int nat_dim(int p) { return (p >> 1) + 64 * (p & 1); }
; __device__ __forceinline__ int src_col_in(int c) {
;     if (c < 5120) { const int blk = c >> 7, p = c & 127; const bool rope = blk < 16 || ((((blk - 16) >> 2) & 1) == 0); const int d = rope ? (p >> 1) + 64 * (p & 1) : p; return blk * 128 + d; }
;     if (c < OFF_Z) return c + 2096;
;     if (c < OFF_G) return c - 4048;
;     if (c < OFF_DT) return 5120 + (c - OFF_G);
;     if (c < NSRC) return c;
;     return -1;
; }
; template <int MAP, bool KS, bool KPERM = false>
; __device__ __forceinline__ void p0_transpose_item(const float* W, int K, int Nsrc, int nblk, bf16* WT, const float* ksA, const float* ksB, int ksplit, LAS float* scr, int item, int lane) {
;     const int kb = item / nblk, nb = item % nblk, k0 = 64 * kb, n0 = 32 * nb;
;     const int nr = n0 + (lane & 31); const int sc = MAP == 1 ? src_col_in(nr) : (MAP == 2 ? nat_dim(nr) : nr);
;     float v[32];
; #pragma unroll
;     for (int i = 0; i < 32; ++i) { const int k = k0 + 2 * i + (lane >> 5); const int ksrc = KPERM ? ((k & ~127) + nat_dim(k & 127)) : k;
;         v[i] = sc >= 0 ? W[(size_t)ksrc * Nsrc + sc] : 0.f; }
; #pragma unroll
;     for (int i = 0; i < 32; ++i) { const int kk = 2 * i + (lane >> 5); const int k = k0 + kk;
;         if (KS) v[i] *= (k < ksplit ? ksA[k] : ksB[k - ksplit]);
;         scr[kk * 33 + (lane & 31)] = v[i]; }
;     LDS_WAIT(); asm volatile("" ::: "memory");
;     const int c = lane & 7;
; #pragma unroll
;     for (int j = 0; j < 4; ++j) { const int n = (lane >> 3) + 8 * j; const LAS float* s = scr + (8 * c) * 33 + n;
;         v4u o; o.x = pk2(s[0 * 33], s[1 * 33]); o.y = pk2(s[2 * 33], s[3 * 33]); o.z = pk2(s[4 * 33], s[5 * 33]); o.w = pk2(s[6 * 33], s[7 * 33]);
;         *(GAS v4u*)(WT + (size_t)(n0 + n) * K + k0 + 8 * c) = o; }
;     LDS_WAIT(); asm volatile("" ::: "memory");
; }
	s_add_i32 s24, s23, 32
	s_lshl_b32 s20, s24, 7
	s_cmp_lt_u32 s24, 40
	s_cselect_b32 s21, 0, 0x830
	s_cmp_lt_u32 s24, 72
	s_cselect_b32 s21, s21, 0xfffff030
	s_add_i32 s20, s20, s21
	s_lshl_b32 s20, s20, 2
	s_add_u32 s8, s46, s20
	s_addc_u32 s9, s47, 0
	global_load_dwordx4 v[144:147], v76, s[8:9]
	s_add_u32 s8, s8, 0x16280
	s_addc_u32 s9, s9, 0
	global_load_dwordx4 v[148:151], v76, s[8:9]
	s_add_u32 s8, s8, 0x16280
	s_addc_u32 s9, s9, 0
	global_load_dwordx4 v[152:155], v76, s[8:9]
	s_add_u32 s8, s8, 0x16280
	s_addc_u32 s9, s9, 0
	global_load_dwordx4 v[156:159], v76, s[8:9]
	s_add_u32 s8, s8, 0x16280
	s_addc_u32 s9, s9, 0
	global_load_dwordx4 v[160:163], v76, s[8:9]
	s_add_u32 s8, s8, 0x16280
	s_addc_u32 s9, s9, 0
	global_load_dwordx4 v[164:167], v76, s[8:9]
	s_add_u32 s8, s8, 0x16280
	s_addc_u32 s9, s9, 0
	global_load_dwordx4 v[168:171], v76, s[8:9]
	s_add_u32 s8, s8, 0x16280
	s_addc_u32 s9, s9, 0
	global_load_dwordx4 v[172:175], v76, s[8:9]
	s_add_i32 s24, s23, 16
	s_mul_i32 s20, s24, 0x100000
	s_add_u32 s6, s48, s20
	s_addc_u32 s7, s49, 0
	s_cmp_lt_u32 s24, 16
	s_cselect_b32 s20, 1, 0
	s_sub_i32 s21, s24, 16
	s_bitcmp0_b32 s21, 2
	s_cselect_b32 s21, 1, 0
	s_cmp_lt_u32 s24, 40
	s_cselect_b32 s21, s21, 0
	s_or_b32 s20, s20, s21
	s_cmp_lg_u32 s20, 0
	s_cselect_b64 s[20:21], -1, 0
	v_cndmask_b32_e64 v91, v83, v87, s[20:21]
	v_cndmask_b32_e64 v92, v84, v88, s[20:21]
	v_cndmask_b32_e64 v93, v85, v89, s[20:21]
	v_cndmask_b32_e64 v94, v86, v90, s[20:21]
	ds_read_b32 v226, v112
	ds_read_b32 v227, v112 offset:512
	ds_read_b32 v228, v112 offset:1024
	ds_read_b32 v229, v112 offset:1536
	ds_read_b32 v230, v112 offset:2048
	ds_read_b32 v231, v112 offset:2560
	ds_read_b32 v232, v112 offset:3072
	ds_read_b32 v233, v112 offset:3584
	s_waitcnt lgkmcnt(0)
	v_bfe_u32 v120, v226, 16, 1
	v_bfe_u32 v121, v227, 16, 1
	v_bfe_u32 v122, v228, 16, 1
	v_bfe_u32 v123, v229, 16, 1
	v_bfe_u32 v124, v230, 16, 1
	v_bfe_u32 v125, v231, 16, 1
	v_bfe_u32 v126, v232, 16, 1
	v_bfe_u32 v127, v233, 16, 1
	v_add3_u32 v226, v226, v120, s63
	v_add3_u32 v227, v227, v121, s63
	v_add3_u32 v228, v228, v122, s63
	v_add3_u32 v229, v229, v123, s63
	v_add3_u32 v230, v230, v124, s63
	v_add3_u32 v231, v231, v125, s63
	v_add3_u32 v232, v232, v126, s63
	v_add3_u32 v233, v233, v127, s63
	v_perm_b32 v242, v227, v226, s64
	v_perm_b32 v243, v229, v228, s64
	v_perm_b32 v244, v231, v230, s64
	v_perm_b32 v245, v233, v232, s64
	s_nop 0
	global_store_dwordx4 v91, v[242:245], s[6:7]
	ds_read_b32 v226, v114
	ds_read_b32 v227, v114 offset:512
	ds_read_b32 v228, v114 offset:1024
	ds_read_b32 v229, v114 offset:1536
	ds_read_b32 v230, v114 offset:2048
	ds_read_b32 v231, v114 offset:2560
	ds_read_b32 v232, v114 offset:3072
	ds_read_b32 v233, v114 offset:3584
	s_waitcnt lgkmcnt(0)
	v_bfe_u32 v120, v226, 16, 1
	v_bfe_u32 v121, v227, 16, 1
	v_bfe_u32 v122, v228, 16, 1
	v_bfe_u32 v123, v229, 16, 1
	v_bfe_u32 v124, v230, 16, 1
	v_bfe_u32 v125, v231, 16, 1
	v_bfe_u32 v126, v232, 16, 1
	v_bfe_u32 v127, v233, 16, 1
	v_add3_u32 v226, v226, v120, s63
	v_add3_u32 v227, v227, v121, s63
	v_add3_u32 v228, v228, v122, s63
	v_add3_u32 v229, v229, v123, s63
	v_add3_u32 v230, v230, v124, s63
	v_add3_u32 v231, v231, v125, s63
	v_add3_u32 v232, v232, v126, s63
	v_add3_u32 v233, v233, v127, s63
	v_perm_b32 v242, v227, v226, s64
	v_perm_b32 v243, v229, v228, s64
	v_perm_b32 v244, v231, v230, s64
	v_perm_b32 v245, v233, v232, s64
	s_nop 0
	global_store_dwordx4 v92, v[242:245], s[6:7]
	ds_read_b32 v226, v116
	ds_read_b32 v227, v116 offset:512
	ds_read_b32 v228, v116 offset:1024
	ds_read_b32 v229, v116 offset:1536
	ds_read_b32 v230, v116 offset:2048
	ds_read_b32 v231, v116 offset:2560
	ds_read_b32 v232, v116 offset:3072
	ds_read_b32 v233, v116 offset:3584
	s_waitcnt lgkmcnt(0)
	v_bfe_u32 v120, v226, 16, 1
	v_bfe_u32 v121, v227, 16, 1
	v_bfe_u32 v122, v228, 16, 1
	v_bfe_u32 v123, v229, 16, 1
	v_bfe_u32 v124, v230, 16, 1
	v_bfe_u32 v125, v231, 16, 1
	v_bfe_u32 v126, v232, 16, 1
	v_bfe_u32 v127, v233, 16, 1
	v_add3_u32 v226, v226, v120, s63
	v_add3_u32 v227, v227, v121, s63
	v_add3_u32 v228, v228, v122, s63
	v_add3_u32 v229, v229, v123, s63
	v_add3_u32 v230, v230, v124, s63
	v_add3_u32 v231, v231, v125, s63
	v_add3_u32 v232, v232, v126, s63
	v_add3_u32 v233, v233, v127, s63
	v_perm_b32 v242, v227, v226, s64
	v_perm_b32 v243, v229, v228, s64
	v_perm_b32 v244, v231, v230, s64
	v_perm_b32 v245, v233, v232, s64
	s_nop 0
	global_store_dwordx4 v93, v[242:245], s[6:7]
	ds_read_b32 v226, v118
	ds_read_b32 v227, v118 offset:512
	ds_read_b32 v228, v118 offset:1024
	ds_read_b32 v229, v118 offset:1536
	ds_read_b32 v230, v118 offset:2048
	ds_read_b32 v231, v118 offset:2560
	ds_read_b32 v232, v118 offset:3072
	ds_read_b32 v233, v118 offset:3584
	s_waitcnt lgkmcnt(0)
	v_bfe_u32 v120, v226, 16, 1
	v_bfe_u32 v121, v227, 16, 1
	v_bfe_u32 v122, v228, 16, 1
	v_bfe_u32 v123, v229, 16, 1
	v_bfe_u32 v124, v230, 16, 1
	v_bfe_u32 v125, v231, 16, 1
	v_bfe_u32 v126, v232, 16, 1
	v_bfe_u32 v127, v233, 16, 1
	v_add3_u32 v226, v226, v120, s63
	v_add3_u32 v227, v227, v121, s63
	v_add3_u32 v228, v228, v122, s63
	v_add3_u32 v229, v229, v123, s63
	v_add3_u32 v230, v230, v124, s63
	v_add3_u32 v231, v231, v125, s63
	v_add3_u32 v232, v232, v126, s63
	v_add3_u32 v233, v233, v127, s63
	v_perm_b32 v242, v227, v226, s64
	v_perm_b32 v243, v229, v228, s64
	v_perm_b32 v244, v231, v230, s64
	v_perm_b32 v245, v233, v232, s64
	s_nop 0
	global_store_dwordx4 v94, v[242:245], s[6:7]
	s_waitcnt vmcnt(16)
	v_mul_f32_e32 v176, v42, v176
	v_mul_f32_e32 v177, v42, v177
	v_mul_f32_e32 v178, v42, v178
	v_mul_f32_e32 v179, v42, v179
	ds_write_b128 v210, v[176:179]
	v_mul_f32_e32 v180, v43, v180
	v_mul_f32_e32 v181, v43, v181
	v_mul_f32_e32 v182, v43, v182
	v_mul_f32_e32 v183, v43, v183
	ds_write_b128 v210, v[180:183] offset:1024
	v_mul_f32_e32 v184, v44, v184
	v_mul_f32_e32 v185, v44, v185
	v_mul_f32_e32 v186, v44, v186
	v_mul_f32_e32 v187, v44, v187
	ds_write_b128 v210, v[184:187] offset:2048
	v_mul_f32_e32 v188, v45, v188
	v_mul_f32_e32 v189, v45, v189
	v_mul_f32_e32 v190, v45, v190
	v_mul_f32_e32 v191, v45, v191
	ds_write_b128 v210, v[188:191] offset:3072
	v_mul_f32_e32 v192, v46, v192
	v_mul_f32_e32 v193, v46, v193
	v_mul_f32_e32 v194, v46, v194
	v_mul_f32_e32 v195, v46, v195
	ds_write_b128 v210, v[192:195] offset:4096
	v_mul_f32_e32 v196, v47, v196
	v_mul_f32_e32 v197, v47, v197
	v_mul_f32_e32 v198, v47, v198
	v_mul_f32_e32 v199, v47, v199
	ds_write_b128 v210, v[196:199] offset:5120
	v_mul_f32_e32 v200, v48, v200
	v_mul_f32_e32 v201, v48, v201
	v_mul_f32_e32 v202, v48, v202
	v_mul_f32_e32 v203, v48, v203
	ds_write_b128 v210, v[200:203] offset:6144
	v_mul_f32_e32 v204, v49, v204
	v_mul_f32_e32 v205, v49, v205
	v_mul_f32_e32 v206, v49, v206
	v_mul_f32_e32 v207, v49, v207
	ds_write_b128 v210, v[204:207] offset:7168
	s_waitcnt lgkmcnt(0)
	s_barrier
; #define GAS __attribute__((address_space(1)))
; #define LAS __attribute__((address_space(3)))
; #define LDS_WAIT() asm volatile("s_waitcnt lgkmcnt(0)" ::: "memory")
; __device__ __forceinline__ unsigned pk2(float lo, float hi) { return f2bf(lo) | (f2bf(hi) << 16); }
; __device__ __forceinline__ int nat_dim(int p) { return (p >> 1) + 64 * (p & 1); }
; __device__ __forceinline__ int src_col_in(int c) {
;     if (c < 5120) { const int blk = c >> 7, p = c & 127; const bool rope = blk < 16 || ((((blk - 16) >> 2) & 1) == 0); const int d = rope ? (p >> 1) + 64 * (p & 1) : p; return blk * 128 + d; }
;     if (c < OFF_Z) return c + 2096;
;     if (c < OFF_G) return c - 4048;
;     if (c < OFF_DT) return 5120 + (c - OFF_G);
;     if (c < NSRC) return c;
;     return -1;
; }
; template <int MAP, bool KS, bool KPERM = false>
; __device__ __forceinline__ void p0_transpose_item(const float* W, int K, int Nsrc, int nblk, bf16* WT, const float* ksA, const float* ksB, int ksplit, LAS float* scr, int item, int lane) {
;     const int kb = item / nblk, nb = item % nblk, k0 = 64 * kb, n0 = 32 * nb;
;     const int nr = n0 + (lane & 31); const int sc = MAP == 1 ? src_col_in(nr) : (MAP == 2 ? nat_dim(nr) : nr);
;     float v[32];
; #pragma unroll
;     for (int i = 0; i < 32; ++i) { const int k = k0 + 2 * i + (lane >> 5); const int ksrc = KPERM ? ((k & ~127) + nat_dim(k & 127)) : k;
;         v[i] = sc >= 0 ? W[(size_t)ksrc * Nsrc + sc] : 0.f; }
; #pragma unroll
;     for (int i = 0; i < 32; ++i) { const int kk = 2 * i + (lane >> 5); const int k = k0 + kk;
;         if (KS) v[i] *= (k < ksplit ? ksA[k] : ksB[k - ksplit]);
;         scr[kk * 33 + (lane & 31)] = v[i]; }
;     LDS_WAIT(); asm volatile("" ::: "memory");
;     const int c = lane & 7;
; #pragma unroll
;     for (int j = 0; j < 4; ++j) { const int n = (lane >> 3) + 8 * j; const LAS float* s = scr + (8 * c) * 33 + n;
;         v4u o; o.x = pk2(s[0 * 33], s[1 * 33]); o.y = pk2(s[2 * 33], s[3 * 33]); o.z = pk2(s[4 * 33], s[5 * 33]); o.w = pk2(s[6 * 33], s[7 * 33]);
;         *(GAS v4u*)(WT + (size_t)(n0 + n) * K + k0 + 8 * c) = o; }
;     LDS_WAIT(); asm volatile("" ::: "memory");
; }
	s_add_i32 s24, s23, 40
	s_lshl_b32 s20, s24, 7
	s_cmp_lt_u32 s24, 40
	s_cselect_b32 s21, 0, 0x830
	s_cmp_lt_u32 s24, 72
	s_cselect_b32 s21, s21, 0xfffff030
	s_add_i32 s20, s20, s21
	s_lshl_b32 s20, s20, 2
	s_add_u32 s8, s46, s20
	s_addc_u32 s9, s47, 0
	global_load_dwordx4 v[176:179], v76, s[8:9]
	s_add_u32 s8, s8, 0x16280
	s_addc_u32 s9, s9, 0
	global_load_dwordx4 v[180:183], v76, s[8:9]
	s_add_u32 s8, s8, 0x16280
	s_addc_u32 s9, s9, 0
	global_load_dwordx4 v[184:187], v76, s[8:9]
	s_add_u32 s8, s8, 0x16280
	s_addc_u32 s9, s9, 0
	global_load_dwordx4 v[188:191], v76, s[8:9]
	s_add_u32 s8, s8, 0x16280
	s_addc_u32 s9, s9, 0
	global_load_dwordx4 v[192:195], v76, s[8:9]
	s_add_u32 s8, s8, 0x16280
	s_addc_u32 s9, s9, 0
	global_load_dwordx4 v[196:199], v76, s[8:9]
	s_add_u32 s8, s8, 0x16280
	s_addc_u32 s9, s9, 0
	global_load_dwordx4 v[200:203], v76, s[8:9]
	s_add_u32 s8, s8, 0x16280
	s_addc_u32 s9, s9, 0
	global_load_dwordx4 v[204:207], v76, s[8:9]
	s_add_i32 s24, s23, 24
	s_mul_i32 s20, s24, 0x100000
	s_add_u32 s6, s48, s20
	s_addc_u32 s7, s49, 0
	s_cmp_lt_u32 s24, 16
	s_cselect_b32 s20, 1, 0
	s_sub_i32 s21, s24, 16
	s_bitcmp0_b32 s21, 2
	s_cselect_b32 s21, 1, 0
	s_cmp_lt_u32 s24, 40
	s_cselect_b32 s21, s21, 0
	s_or_b32 s20, s20, s21
	s_cmp_lg_u32 s20, 0
	s_cselect_b64 s[20:21], -1, 0
	v_cndmask_b32_e64 v91, v83, v87, s[20:21]
	v_cndmask_b32_e64 v92, v84, v88, s[20:21]
	v_cndmask_b32_e64 v93, v85, v89, s[20:21]
	v_cndmask_b32_e64 v94, v86, v90, s[20:21]
	ds_read_b32 v226, v113
	ds_read_b32 v227, v113 offset:512
	ds_read_b32 v228, v113 offset:1024
	ds_read_b32 v229, v113 offset:1536
	ds_read_b32 v230, v113 offset:2048
	ds_read_b32 v231, v113 offset:2560
	ds_read_b32 v232, v113 offset:3072
	ds_read_b32 v233, v113 offset:3584
	s_waitcnt lgkmcnt(0)
	v_bfe_u32 v120, v226, 16, 1
	v_bfe_u32 v121, v227, 16, 1
	v_bfe_u32 v122, v228, 16, 1
	v_bfe_u32 v123, v229, 16, 1
	v_bfe_u32 v124, v230, 16, 1
	v_bfe_u32 v125, v231, 16, 1
	v_bfe_u32 v126, v232, 16, 1
	v_bfe_u32 v127, v233, 16, 1
	v_add3_u32 v226, v226, v120, s63
	v_add3_u32 v227, v227, v121, s63
	v_add3_u32 v228, v228, v122, s63
	v_add3_u32 v229, v229, v123, s63
	v_add3_u32 v230, v230, v124, s63
	v_add3_u32 v231, v231, v125, s63
	v_add3_u32 v232, v232, v126, s63
	v_add3_u32 v233, v233, v127, s63
	v_perm_b32 v242, v227, v226, s64
	v_perm_b32 v243, v229, v228, s64
	v_perm_b32 v244, v231, v230, s64
	v_perm_b32 v245, v233, v232, s64
	s_nop 0
	global_store_dwordx4 v91, v[242:245], s[6:7]
	ds_read_b32 v226, v115
	ds_read_b32 v227, v115 offset:512
	ds_read_b32 v228, v115 offset:1024
	ds_read_b32 v229, v115 offset:1536
	ds_read_b32 v230, v115 offset:2048
	ds_read_b32 v231, v115 offset:2560
	ds_read_b32 v232, v115 offset:3072
	ds_read_b32 v233, v115 offset:3584
	s_waitcnt lgkmcnt(0)
	v_bfe_u32 v120, v226, 16, 1
	v_bfe_u32 v121, v227, 16, 1
	v_bfe_u32 v122, v228, 16, 1
	v_bfe_u32 v123, v229, 16, 1
	v_bfe_u32 v124, v230, 16, 1
	v_bfe_u32 v125, v231, 16, 1
	v_bfe_u32 v126, v232, 16, 1
	v_bfe_u32 v127, v233, 16, 1
	v_add3_u32 v226, v226, v120, s63
	v_add3_u32 v227, v227, v121, s63
	v_add3_u32 v228, v228, v122, s63
	v_add3_u32 v229, v229, v123, s63
	v_add3_u32 v230, v230, v124, s63
	v_add3_u32 v231, v231, v125, s63
	v_add3_u32 v232, v232, v126, s63
	v_add3_u32 v233, v233, v127, s63
	v_perm_b32 v242, v227, v226, s64
	v_perm_b32 v243, v229, v228, s64
	v_perm_b32 v244, v231, v230, s64
	v_perm_b32 v245, v233, v232, s64
	s_nop 0
	global_store_dwordx4 v92, v[242:245], s[6:7]
	ds_read_b32 v226, v117
	ds_read_b32 v227, v117 offset:512
	ds_read_b32 v228, v117 offset:1024
	ds_read_b32 v229, v117 offset:1536
	ds_read_b32 v230, v117 offset:2048
	ds_read_b32 v231, v117 offset:2560
	ds_read_b32 v232, v117 offset:3072
	ds_read_b32 v233, v117 offset:3584
	s_waitcnt lgkmcnt(0)
	v_bfe_u32 v120, v226, 16, 1
	v_bfe_u32 v121, v227, 16, 1
	v_bfe_u32 v122, v228, 16, 1
	v_bfe_u32 v123, v229, 16, 1
	v_bfe_u32 v124, v230, 16, 1
	v_bfe_u32 v125, v231, 16, 1
	v_bfe_u32 v126, v232, 16, 1
	v_bfe_u32 v127, v233, 16, 1
	v_add3_u32 v226, v226, v120, s63
	v_add3_u32 v227, v227, v121, s63
	v_add3_u32 v228, v228, v122, s63
	v_add3_u32 v229, v229, v123, s63
	v_add3_u32 v230, v230, v124, s63
	v_add3_u32 v231, v231, v125, s63
	v_add3_u32 v232, v232, v126, s63
	v_add3_u32 v233, v233, v127, s63
	v_perm_b32 v242, v227, v226, s64
	v_perm_b32 v243, v229, v228, s64
	v_perm_b32 v244, v231, v230, s64
	v_perm_b32 v245, v233, v232, s64
	s_nop 0
	global_store_dwordx4 v93, v[242:245], s[6:7]
	ds_read_b32 v226, v119
	ds_read_b32 v227, v119 offset:512
	ds_read_b32 v228, v119 offset:1024
	ds_read_b32 v229, v119 offset:1536
	ds_read_b32 v230, v119 offset:2048
	ds_read_b32 v231, v119 offset:2560
	ds_read_b32 v232, v119 offset:3072
	ds_read_b32 v233, v119 offset:3584
	s_waitcnt lgkmcnt(0)
	v_bfe_u32 v120, v226, 16, 1
	v_bfe_u32 v121, v227, 16, 1
	v_bfe_u32 v122, v228, 16, 1
	v_bfe_u32 v123, v229, 16, 1
	v_bfe_u32 v124, v230, 16, 1
	v_bfe_u32 v125, v231, 16, 1
	v_bfe_u32 v126, v232, 16, 1
	v_bfe_u32 v127, v233, 16, 1
	v_add3_u32 v226, v226, v120, s63
	v_add3_u32 v227, v227, v121, s63
	v_add3_u32 v228, v228, v122, s63
	v_add3_u32 v229, v229, v123, s63
	v_add3_u32 v230, v230, v124, s63
	v_add3_u32 v231, v231, v125, s63
	v_add3_u32 v232, v232, v126, s63
	v_add3_u32 v233, v233, v127, s63
	v_perm_b32 v242, v227, v226, s64
	v_perm_b32 v243, v229, v228, s64
	v_perm_b32 v244, v231, v230, s64
	v_perm_b32 v245, v233, v232, s64
	s_nop 0
	global_store_dwordx4 v94, v[242:245], s[6:7]
	s_waitcnt vmcnt(16)
	v_mul_f32_e32 v144, v42, v144
	v_mul_f32_e32 v145, v42, v145
	v_mul_f32_e32 v146, v42, v146
	v_mul_f32_e32 v147, v42, v147
	ds_write_b128 v209, v[144:147]
	v_mul_f32_e32 v148, v43, v148
	v_mul_f32_e32 v149, v43, v149
	v_mul_f32_e32 v150, v43, v150
	v_mul_f32_e32 v151, v43, v151
	ds_write_b128 v209, v[148:151] offset:1024
	v_mul_f32_e32 v152, v44, v152
	v_mul_f32_e32 v153, v44, v153
	v_mul_f32_e32 v154, v44, v154
	v_mul_f32_e32 v155, v44, v155
	ds_write_b128 v209, v[152:155] offset:2048
	v_mul_f32_e32 v156, v45, v156
	v_mul_f32_e32 v157, v45, v157
	v_mul_f32_e32 v158, v45, v158
	v_mul_f32_e32 v159, v45, v159
	ds_write_b128 v209, v[156:159] offset:3072
	v_mul_f32_e32 v160, v46, v160
	v_mul_f32_e32 v161, v46, v161
	v_mul_f32_e32 v162, v46, v162
	v_mul_f32_e32 v163, v46, v163
	ds_write_b128 v209, v[160:163] offset:4096
	v_mul_f32_e32 v164, v47, v164
	v_mul_f32_e32 v165, v47, v165
	v_mul_f32_e32 v166, v47, v166
	v_mul_f32_e32 v167, v47, v167
	ds_write_b128 v209, v[164:167] offset:5120
	v_mul_f32_e32 v168, v48, v168
	v_mul_f32_e32 v169, v48, v169
	v_mul_f32_e32 v170, v48, v170
	v_mul_f32_e32 v171, v48, v171
	ds_write_b128 v209, v[168:171] offset:6144
	v_mul_f32_e32 v172, v49, v172
	v_mul_f32_e32 v173, v49, v173
	v_mul_f32_e32 v174, v49, v174
	v_mul_f32_e32 v175, v49, v175
	ds_write_b128 v209, v[172:175] offset:7168
	s_waitcnt lgkmcnt(0)
	s_barrier
; #define GAS __attribute__((address_space(1)))
; #define LAS __attribute__((address_space(3)))
; #define LDS_WAIT() asm volatile("s_waitcnt lgkmcnt(0)" ::: "memory")
; __device__ __forceinline__ unsigned pk2(float lo, float hi) { return f2bf(lo) | (f2bf(hi) << 16); }
; __device__ __forceinline__ int nat_dim(int p) { return (p >> 1) + 64 * (p & 1); }
; __device__ __forceinline__ int src_col_in(int c) {
;     if (c < 5120) { const int blk = c >> 7, p = c & 127; const bool rope = blk < 16 || ((((blk - 16) >> 2) & 1) == 0); const int d = rope ? (p >> 1) + 64 * (p & 1) : p; return blk * 128 + d; }
;     if (c < OFF_Z) return c + 2096;
;     if (c < OFF_G) return c - 4048;
;     if (c < OFF_DT) return 5120 + (c - OFF_G);
;     if (c < NSRC) return c;
;     return -1;
; }
; template <int MAP, bool KS, bool KPERM = false>
; __device__ __forceinline__ void p0_transpose_item(const float* W, int K, int Nsrc, int nblk, bf16* WT, const float* ksA, const float* ksB, int ksplit, LAS float* scr, int item, int lane) {
;     const int kb = item / nblk, nb = item % nblk, k0 = 64 * kb, n0 = 32 * nb;
;     const int nr = n0 + (lane & 31); const int sc = MAP == 1 ? src_col_in(nr) : (MAP == 2 ? nat_dim(nr) : nr);
;     float v[32];
; #pragma unroll
;     for (int i = 0; i < 32; ++i) { const int k = k0 + 2 * i + (lane >> 5); const int ksrc = KPERM ? ((k & ~127) + nat_dim(k & 127)) : k;
;         v[i] = sc >= 0 ? W[(size_t)ksrc * Nsrc + sc] : 0.f; }
; #pragma unroll
;     for (int i = 0; i < 32; ++i) { const int kk = 2 * i + (lane >> 5); const int k = k0 + kk;
;         if (KS) v[i] *= (k < ksplit ? ksA[k] : ksB[k - ksplit]);
;         scr[kk * 33 + (lane & 31)] = v[i]; }
;     LDS_WAIT(); asm volatile("" ::: "memory");
;     const int c = lane & 7;
; #pragma unroll
;     for (int j = 0; j < 4; ++j) { const int n = (lane >> 3) + 8 * j; const LAS float* s = scr + (8 * c) * 33 + n;
;         v4u o; o.x = pk2(s[0 * 33], s[1 * 33]); o.y = pk2(s[2 * 33], s[3 * 33]); o.z = pk2(s[4 * 33], s[5 * 33]); o.w = pk2(s[6 * 33], s[7 * 33]);
;         *(GAS v4u*)(WT + (size_t)(n0 + n) * K + k0 + 8 * c) = o; }
;     LDS_WAIT(); asm volatile("" ::: "memory");
; }
	s_add_i32 s24, s23, 48
	s_lshl_b32 s20, s24, 7
	s_cmp_lt_u32 s24, 40
	s_cselect_b32 s21, 0, 0x830
	s_cmp_lt_u32 s24, 72
	s_cselect_b32 s21, s21, 0xfffff030
	s_add_i32 s20, s20, s21
	s_lshl_b32 s20, s20, 2
	s_add_u32 s8, s46, s20
	s_addc_u32 s9, s47, 0
	global_load_dwordx4 v[144:147], v76, s[8:9]
	s_add_u32 s8, s8, 0x16280
	s_addc_u32 s9, s9, 0
	global_load_dwordx4 v[148:151], v76, s[8:9]
	s_add_u32 s8, s8, 0x16280
	s_addc_u32 s9, s9, 0
	global_load_dwordx4 v[152:155], v76, s[8:9]
	s_add_u32 s8, s8, 0x16280
	s_addc_u32 s9, s9, 0
	global_load_dwordx4 v[156:159], v76, s[8:9]
	s_add_u32 s8, s8, 0x16280
	s_addc_u32 s9, s9, 0
	global_load_dwordx4 v[160:163], v76, s[8:9]
	s_add_u32 s8, s8, 0x16280
	s_addc_u32 s9, s9, 0
	global_load_dwordx4 v[164:167], v76, s[8:9]
	s_add_u32 s8, s8, 0x16280
	s_addc_u32 s9, s9, 0
	global_load_dwordx4 v[168:171], v76, s[8:9]
	s_add_u32 s8, s8, 0x16280
	s_addc_u32 s9, s9, 0
	global_load_dwordx4 v[172:175], v76, s[8:9]
	s_add_i32 s24, s23, 32
	s_mul_i32 s20, s24, 0x100000
	s_add_u32 s6, s48, s20
	s_addc_u32 s7, s49, 0
	s_cmp_lt_u32 s24, 16
	s_cselect_b32 s20, 1, 0
	s_sub_i32 s21, s24, 16
	s_bitcmp0_b32 s21, 2
	s_cselect_b32 s21, 1, 0
	s_cmp_lt_u32 s24, 40
	s_cselect_b32 s21, s21, 0
	s_or_b32 s20, s20, s21
	s_cmp_lg_u32 s20, 0
	s_cselect_b64 s[20:21], -1, 0
	v_cndmask_b32_e64 v91, v83, v87, s[20:21]
	v_cndmask_b32_e64 v92, v84, v88, s[20:21]
	v_cndmask_b32_e64 v93, v85, v89, s[20:21]
	v_cndmask_b32_e64 v94, v86, v90, s[20:21]
	ds_read_b32 v226, v112
	ds_read_b32 v227, v112 offset:512
	ds_read_b32 v228, v112 offset:1024
	ds_read_b32 v229, v112 offset:1536
	ds_read_b32 v230, v112 offset:2048
	ds_read_b32 v231, v112 offset:2560
	ds_read_b32 v232, v112 offset:3072
	ds_read_b32 v233, v112 offset:3584
	s_waitcnt lgkmcnt(0)
	v_bfe_u32 v120, v226, 16, 1
	v_bfe_u32 v121, v227, 16, 1
	v_bfe_u32 v122, v228, 16, 1
	v_bfe_u32 v123, v229, 16, 1
	v_bfe_u32 v124, v230, 16, 1
	v_bfe_u32 v125, v231, 16, 1
	v_bfe_u32 v126, v232, 16, 1
	v_bfe_u32 v127, v233, 16, 1
	v_add3_u32 v226, v226, v120, s63
	v_add3_u32 v227, v227, v121, s63
	v_add3_u32 v228, v228, v122, s63
	v_add3_u32 v229, v229, v123, s63
	v_add3_u32 v230, v230, v124, s63
	v_add3_u32 v231, v231, v125, s63
	v_add3_u32 v232, v232, v126, s63
	v_add3_u32 v233, v233, v127, s63
	v_perm_b32 v242, v227, v226, s64
	v_perm_b32 v243, v229, v228, s64
	v_perm_b32 v244, v231, v230, s64
	v_perm_b32 v245, v233, v232, s64
	s_nop 0
	global_store_dwordx4 v91, v[242:245], s[6:7]
	ds_read_b32 v226, v114
	ds_read_b32 v227, v114 offset:512
	ds_read_b32 v228, v114 offset:1024
	ds_read_b32 v229, v114 offset:1536
	ds_read_b32 v230, v114 offset:2048
	ds_read_b32 v231, v114 offset:2560
	ds_read_b32 v232, v114 offset:3072
	ds_read_b32 v233, v114 offset:3584
	s_waitcnt lgkmcnt(0)
	v_bfe_u32 v120, v226, 16, 1
	v_bfe_u32 v121, v227, 16, 1
	v_bfe_u32 v122, v228, 16, 1
	v_bfe_u32 v123, v229, 16, 1
	v_bfe_u32 v124, v230, 16, 1
	v_bfe_u32 v125, v231, 16, 1
	v_bfe_u32 v126, v232, 16, 1
	v_bfe_u32 v127, v233, 16, 1
	v_add3_u32 v226, v226, v120, s63
	v_add3_u32 v227, v227, v121, s63
	v_add3_u32 v228, v228, v122, s63
	v_add3_u32 v229, v229, v123, s63
	v_add3_u32 v230, v230, v124, s63
	v_add3_u32 v231, v231, v125, s63
	v_add3_u32 v232, v232, v126, s63
	v_add3_u32 v233, v233, v127, s63
	v_perm_b32 v242, v227, v226, s64
	v_perm_b32 v243, v229, v228, s64
	v_perm_b32 v244, v231, v230, s64
	v_perm_b32 v245, v233, v232, s64
	s_nop 0
	global_store_dwordx4 v92, v[242:245], s[6:7]
	ds_read_b32 v226, v116
	ds_read_b32 v227, v116 offset:512
	ds_read_b32 v228, v116 offset:1024
	ds_read_b32 v229, v116 offset:1536
	ds_read_b32 v230, v116 offset:2048
	ds_read_b32 v231, v116 offset:2560
	ds_read_b32 v232, v116 offset:3072
	ds_read_b32 v233, v116 offset:3584
	s_waitcnt lgkmcnt(0)
	v_bfe_u32 v120, v226, 16, 1
	v_bfe_u32 v121, v227, 16, 1
	v_bfe_u32 v122, v228, 16, 1
	v_bfe_u32 v123, v229, 16, 1
	v_bfe_u32 v124, v230, 16, 1
	v_bfe_u32 v125, v231, 16, 1
	v_bfe_u32 v126, v232, 16, 1
	v_bfe_u32 v127, v233, 16, 1
	v_add3_u32 v226, v226, v120, s63
	v_add3_u32 v227, v227, v121, s63
	v_add3_u32 v228, v228, v122, s63
	v_add3_u32 v229, v229, v123, s63
	v_add3_u32 v230, v230, v124, s63
	v_add3_u32 v231, v231, v125, s63
	v_add3_u32 v232, v232, v126, s63
	v_add3_u32 v233, v233, v127, s63
	v_perm_b32 v242, v227, v226, s64
	v_perm_b32 v243, v229, v228, s64
	v_perm_b32 v244, v231, v230, s64
	v_perm_b32 v245, v233, v232, s64
	s_nop 0
	global_store_dwordx4 v93, v[242:245], s[6:7]
	ds_read_b32 v226, v118
	ds_read_b32 v227, v118 offset:512
	ds_read_b32 v228, v118 offset:1024
	ds_read_b32 v229, v118 offset:1536
	ds_read_b32 v230, v118 offset:2048
	ds_read_b32 v231, v118 offset:2560
	ds_read_b32 v232, v118 offset:3072
	ds_read_b32 v233, v118 offset:3584
	s_waitcnt lgkmcnt(0)
	v_bfe_u32 v120, v226, 16, 1
	v_bfe_u32 v121, v227, 16, 1
	v_bfe_u32 v122, v228, 16, 1
	v_bfe_u32 v123, v229, 16, 1
	v_bfe_u32 v124, v230, 16, 1
	v_bfe_u32 v125, v231, 16, 1
	v_bfe_u32 v126, v232, 16, 1
	v_bfe_u32 v127, v233, 16, 1
	v_add3_u32 v226, v226, v120, s63
	v_add3_u32 v227, v227, v121, s63
	v_add3_u32 v228, v228, v122, s63
	v_add3_u32 v229, v229, v123, s63
	v_add3_u32 v230, v230, v124, s63
	v_add3_u32 v231, v231, v125, s63
	v_add3_u32 v232, v232, v126, s63
	v_add3_u32 v233, v233, v127, s63
	v_perm_b32 v242, v227, v226, s64
	v_perm_b32 v243, v229, v228, s64
	v_perm_b32 v244, v231, v230, s64
	v_perm_b32 v245, v233, v232, s64
	s_nop 0
	global_store_dwordx4 v94, v[242:245], s[6:7]
	s_waitcnt vmcnt(16)
	v_mul_f32_e32 v176, v42, v176
	v_mul_f32_e32 v177, v42, v177
	v_mul_f32_e32 v178, v42, v178
	v_mul_f32_e32 v179, v42, v179
	ds_write_b128 v210, v[176:179]
	v_mul_f32_e32 v180, v43, v180
	v_mul_f32_e32 v181, v43, v181
	v_mul_f32_e32 v182, v43, v182
	v_mul_f32_e32 v183, v43, v183
	ds_write_b128 v210, v[180:183] offset:1024
	v_mul_f32_e32 v184, v44, v184
	v_mul_f32_e32 v185, v44, v185
	v_mul_f32_e32 v186, v44, v186
	v_mul_f32_e32 v187, v44, v187
	ds_write_b128 v210, v[184:187] offset:2048
	v_mul_f32_e32 v188, v45, v188
	v_mul_f32_e32 v189, v45, v189
	v_mul_f32_e32 v190, v45, v190
	v_mul_f32_e32 v191, v45, v191
	ds_write_b128 v210, v[188:191] offset:3072
	v_mul_f32_e32 v192, v46, v192
	v_mul_f32_e32 v193, v46, v193
	v_mul_f32_e32 v194, v46, v194
	v_mul_f32_e32 v195, v46, v195
	ds_write_b128 v210, v[192:195] offset:4096
	v_mul_f32_e32 v196, v47, v196
	v_mul_f32_e32 v197, v47, v197
	v_mul_f32_e32 v198, v47, v198
	v_mul_f32_e32 v199, v47, v199
	ds_write_b128 v210, v[196:199] offset:5120
	v_mul_f32_e32 v200, v48, v200
	v_mul_f32_e32 v201, v48, v201
	v_mul_f32_e32 v202, v48, v202
	v_mul_f32_e32 v203, v48, v203
	ds_write_b128 v210, v[200:203] offset:6144
	v_mul_f32_e32 v204, v49, v204
	v_mul_f32_e32 v205, v49, v205
	v_mul_f32_e32 v206, v49, v206
	v_mul_f32_e32 v207, v49, v207
	ds_write_b128 v210, v[204:207] offset:7168
	s_waitcnt lgkmcnt(0)
	s_barrier
; #define GAS __attribute__((address_space(1)))
; #define LAS __attribute__((address_space(3)))
; #define LDS_WAIT() asm volatile("s_waitcnt lgkmcnt(0)" ::: "memory")
; __device__ __forceinline__ unsigned pk2(float lo, float hi) { return f2bf(lo) | (f2bf(hi) << 16); }
; __device__ __forceinline__ int nat_dim(int p) { return (p >> 1) + 64 * (p & 1); }
; __device__ __forceinline__ int src_col_in(int c) {
;     if (c < 5120) { const int blk = c >> 7, p = c & 127; const bool rope = blk < 16 || ((((blk - 16) >> 2) & 1) == 0); const int d = rope ? (p >> 1) + 64 * (p & 1) : p; return blk * 128 + d; }
;     if (c < OFF_Z) return c + 2096;
;     if (c < OFF_G) return c - 4048;
;     if (c < OFF_DT) return 5120 + (c - OFF_G);
;     if (c < NSRC) return c;
;     return -1;
; }
; template <int MAP, bool KS, bool KPERM = false>
; __device__ __forceinline__ void p0_transpose_item(const float* W, int K, int Nsrc, int nblk, bf16* WT, const float* ksA, const float* ksB, int ksplit, LAS float* scr, int item, int lane) {
;     const int kb = item / nblk, nb = item % nblk, k0 = 64 * kb, n0 = 32 * nb;
;     const int nr = n0 + (lane & 31); const int sc = MAP == 1 ? src_col_in(nr) : (MAP == 2 ? nat_dim(nr) : nr);
;     float v[32];
; #pragma unroll
;     for (int i = 0; i < 32; ++i) { const int k = k0 + 2 * i + (lane >> 5); const int ksrc = KPERM ? ((k & ~127) + nat_dim(k & 127)) : k;
;         v[i] = sc >= 0 ? W[(size_t)ksrc * Nsrc + sc] : 0.f; }
; #pragma unroll
;     for (int i = 0; i < 32; ++i) { const int kk = 2 * i + (lane >> 5); const int k = k0 + kk;
;         if (KS) v[i] *= (k < ksplit ? ksA[k] : ksB[k - ksplit]);
;         scr[kk * 33 + (lane & 31)] = v[i]; }
;     LDS_WAIT(); asm volatile("" ::: "memory");
;     const int c = lane & 7;
; #pragma unroll
;     for (int j = 0; j < 4; ++j) { const int n = (lane >> 3) + 8 * j; const LAS float* s = scr + (8 * c) * 33 + n;
;         v4u o; o.x = pk2(s[0 * 33], s[1 * 33]); o.y = pk2(s[2 * 33], s[3 * 33]); o.z = pk2(s[4 * 33], s[5 * 33]); o.w = pk2(s[6 * 33], s[7 * 33]);
;         *(GAS v4u*)(WT + (size_t)(n0 + n) * K + k0 + 8 * c) = o; }
;     LDS_WAIT(); asm volatile("" ::: "memory");
; }
	s_add_i32 s24, s23, 56
	s_lshl_b32 s20, s24, 7
	s_cmp_lt_u32 s24, 40
	s_cselect_b32 s21, 0, 0x830
	s_cmp_lt_u32 s24, 72
	s_cselect_b32 s21, s21, 0xfffff030
	s_add_i32 s20, s20, s21
	s_lshl_b32 s20, s20, 2
	s_add_u32 s8, s46, s20
	s_addc_u32 s9, s47, 0
	global_load_dwordx4 v[176:179], v76, s[8:9]
	s_add_u32 s8, s8, 0x16280
	s_addc_u32 s9, s9, 0
	global_load_dwordx4 v[180:183], v76, s[8:9]
	s_add_u32 s8, s8, 0x16280
	s_addc_u32 s9, s9, 0
	global_load_dwordx4 v[184:187], v76, s[8:9]
	s_add_u32 s8, s8, 0x16280
	s_addc_u32 s9, s9, 0
	global_load_dwordx4 v[188:191], v76, s[8:9]
	s_add_u32 s8, s8, 0x16280
	s_addc_u32 s9, s9, 0
	global_load_dwordx4 v[192:195], v76, s[8:9]
	s_add_u32 s8, s8, 0x16280
	s_addc_u32 s9, s9, 0
	global_load_dwordx4 v[196:199], v76, s[8:9]
	s_add_u32 s8, s8, 0x16280
	s_addc_u32 s9, s9, 0
	global_load_dwordx4 v[200:203], v76, s[8:9]
	s_add_u32 s8, s8, 0x16280
	s_addc_u32 s9, s9, 0
	global_load_dwordx4 v[204:207], v76, s[8:9]
	s_add_i32 s24, s23, 40
	s_mul_i32 s20, s24, 0x100000
	s_add_u32 s6, s48, s20
	s_addc_u32 s7, s49, 0
	s_cmp_lt_u32 s24, 16
	s_cselect_b32 s20, 1, 0
	s_sub_i32 s21, s24, 16
	s_bitcmp0_b32 s21, 2
	s_cselect_b32 s21, 1, 0
	s_cmp_lt_u32 s24, 40
	s_cselect_b32 s21, s21, 0
	s_or_b32 s20, s20, s21
	s_cmp_lg_u32 s20, 0
	s_cselect_b64 s[20:21], -1, 0
	v_cndmask_b32_e64 v91, v83, v87, s[20:21]
	v_cndmask_b32_e64 v92, v84, v88, s[20:21]
	v_cndmask_b32_e64 v93, v85, v89, s[20:21]
	v_cndmask_b32_e64 v94, v86, v90, s[20:21]
	ds_read_b32 v226, v113
	ds_read_b32 v227, v113 offset:512
	ds_read_b32 v228, v113 offset:1024
	ds_read_b32 v229, v113 offset:1536
	ds_read_b32 v230, v113 offset:2048
	ds_read_b32 v231, v113 offset:2560
	ds_read_b32 v232, v113 offset:3072
	ds_read_b32 v233, v113 offset:3584
	s_waitcnt lgkmcnt(0)
	v_bfe_u32 v120, v226, 16, 1
	v_bfe_u32 v121, v227, 16, 1
	v_bfe_u32 v122, v228, 16, 1
	v_bfe_u32 v123, v229, 16, 1
	v_bfe_u32 v124, v230, 16, 1
	v_bfe_u32 v125, v231, 16, 1
	v_bfe_u32 v126, v232, 16, 1
	v_bfe_u32 v127, v233, 16, 1
	v_add3_u32 v226, v226, v120, s63
	v_add3_u32 v227, v227, v121, s63
	v_add3_u32 v228, v228, v122, s63
	v_add3_u32 v229, v229, v123, s63
	v_add3_u32 v230, v230, v124, s63
	v_add3_u32 v231, v231, v125, s63
	v_add3_u32 v232, v232, v126, s63
	v_add3_u32 v233, v233, v127, s63
	v_perm_b32 v242, v227, v226, s64
	v_perm_b32 v243, v229, v228, s64
	v_perm_b32 v244, v231, v230, s64
	v_perm_b32 v245, v233, v232, s64
	s_nop 0
	global_store_dwordx4 v91, v[242:245], s[6:7]
	ds_read_b32 v226, v115
	ds_read_b32 v227, v115 offset:512
	ds_read_b32 v228, v115 offset:1024
	ds_read_b32 v229, v115 offset:1536
	ds_read_b32 v230, v115 offset:2048
	ds_read_b32 v231, v115 offset:2560
	ds_read_b32 v232, v115 offset:3072
	ds_read_b32 v233, v115 offset:3584
	s_waitcnt lgkmcnt(0)
	v_bfe_u32 v120, v226, 16, 1
	v_bfe_u32 v121, v227, 16, 1
	v_bfe_u32 v122, v228, 16, 1
	v_bfe_u32 v123, v229, 16, 1
	v_bfe_u32 v124, v230, 16, 1
	v_bfe_u32 v125, v231, 16, 1
	v_bfe_u32 v126, v232, 16, 1
	v_bfe_u32 v127, v233, 16, 1
	v_add3_u32 v226, v226, v120, s63
	v_add3_u32 v227, v227, v121, s63
	v_add3_u32 v228, v228, v122, s63
	v_add3_u32 v229, v229, v123, s63
	v_add3_u32 v230, v230, v124, s63
	v_add3_u32 v231, v231, v125, s63
	v_add3_u32 v232, v232, v126, s63
	v_add3_u32 v233, v233, v127, s63
	v_perm_b32 v242, v227, v226, s64
	v_perm_b32 v243, v229, v228, s64
	v_perm_b32 v244, v231, v230, s64
	v_perm_b32 v245, v233, v232, s64
	s_nop 0
	global_store_dwordx4 v92, v[242:245], s[6:7]
	ds_read_b32 v226, v117
	ds_read_b32 v227, v117 offset:512
	ds_read_b32 v228, v117 offset:1024
	ds_read_b32 v229, v117 offset:1536
	ds_read_b32 v230, v117 offset:2048
	ds_read_b32 v231, v117 offset:2560
	ds_read_b32 v232, v117 offset:3072
	ds_read_b32 v233, v117 offset:3584
	s_waitcnt lgkmcnt(0)
	v_bfe_u32 v120, v226, 16, 1
	v_bfe_u32 v121, v227, 16, 1
	v_bfe_u32 v122, v228, 16, 1
	v_bfe_u32 v123, v229, 16, 1
	v_bfe_u32 v124, v230, 16, 1
	v_bfe_u32 v125, v231, 16, 1
	v_bfe_u32 v126, v232, 16, 1
	v_bfe_u32 v127, v233, 16, 1
	v_add3_u32 v226, v226, v120, s63
	v_add3_u32 v227, v227, v121, s63
	v_add3_u32 v228, v228, v122, s63
	v_add3_u32 v229, v229, v123, s63
	v_add3_u32 v230, v230, v124, s63
	v_add3_u32 v231, v231, v125, s63
	v_add3_u32 v232, v232, v126, s63
	v_add3_u32 v233, v233, v127, s63
	v_perm_b32 v242, v227, v226, s64
	v_perm_b32 v243, v229, v228, s64
	v_perm_b32 v244, v231, v230, s64
	v_perm_b32 v245, v233, v232, s64
	s_nop 0
	global_store_dwordx4 v93, v[242:245], s[6:7]
	ds_read_b32 v226, v119
	ds_read_b32 v227, v119 offset:512
	ds_read_b32 v228, v119 offset:1024
	ds_read_b32 v229, v119 offset:1536
	ds_read_b32 v230, v119 offset:2048
	ds_read_b32 v231, v119 offset:2560
	ds_read_b32 v232, v119 offset:3072
	ds_read_b32 v233, v119 offset:3584
	s_waitcnt lgkmcnt(0)
	v_bfe_u32 v120, v226, 16, 1
	v_bfe_u32 v121, v227, 16, 1
	v_bfe_u32 v122, v228, 16, 1
	v_bfe_u32 v123, v229, 16, 1
	v_bfe_u32 v124, v230, 16, 1
	v_bfe_u32 v125, v231, 16, 1
	v_bfe_u32 v126, v232, 16, 1
	v_bfe_u32 v127, v233, 16, 1
	v_add3_u32 v226, v226, v120, s63
	v_add3_u32 v227, v227, v121, s63
	v_add3_u32 v228, v228, v122, s63
	v_add3_u32 v229, v229, v123, s63
	v_add3_u32 v230, v230, v124, s63
	v_add3_u32 v231, v231, v125, s63
	v_add3_u32 v232, v232, v126, s63
	v_add3_u32 v233, v233, v127, s63
	v_perm_b32 v242, v227, v226, s64
	v_perm_b32 v243, v229, v228, s64
	v_perm_b32 v244, v231, v230, s64
	v_perm_b32 v245, v233, v232, s64
	s_nop 0
	global_store_dwordx4 v94, v[242:245], s[6:7]
	s_waitcnt vmcnt(16)
	v_mul_f32_e32 v144, v42, v144
	v_mul_f32_e32 v145, v42, v145
	v_mul_f32_e32 v146, v42, v146
	v_mul_f32_e32 v147, v42, v147
	ds_write_b128 v209, v[144:147]
	v_mul_f32_e32 v148, v43, v148
	v_mul_f32_e32 v149, v43, v149
	v_mul_f32_e32 v150, v43, v150
	v_mul_f32_e32 v151, v43, v151
	ds_write_b128 v209, v[148:151] offset:1024
	v_mul_f32_e32 v152, v44, v152
	v_mul_f32_e32 v153, v44, v153
	v_mul_f32_e32 v154, v44, v154
	v_mul_f32_e32 v155, v44, v155
	ds_write_b128 v209, v[152:155] offset:2048
	v_mul_f32_e32 v156, v45, v156
	v_mul_f32_e32 v157, v45, v157
	v_mul_f32_e32 v158, v45, v158
	v_mul_f32_e32 v159, v45, v159
	ds_write_b128 v209, v[156:159] offset:3072
	v_mul_f32_e32 v160, v46, v160
	v_mul_f32_e32 v161, v46, v161
	v_mul_f32_e32 v162, v46, v162
	v_mul_f32_e32 v163, v46, v163
	ds_write_b128 v209, v[160:163] offset:4096
	v_mul_f32_e32 v164, v47, v164
	v_mul_f32_e32 v165, v47, v165
	v_mul_f32_e32 v166, v47, v166
	v_mul_f32_e32 v167, v47, v167
	ds_write_b128 v209, v[164:167] offset:5120
	v_mul_f32_e32 v168, v48, v168
	v_mul_f32_e32 v169, v48, v169
	v_mul_f32_e32 v170, v48, v170
	v_mul_f32_e32 v171, v48, v171
	ds_write_b128 v209, v[168:171] offset:6144
	v_mul_f32_e32 v172, v49, v172
	v_mul_f32_e32 v173, v49, v173
	v_mul_f32_e32 v174, v49, v174
	v_mul_f32_e32 v175, v49, v175
	ds_write_b128 v209, v[172:175] offset:7168
	s_waitcnt lgkmcnt(0)
	s_barrier
; #define GAS __attribute__((address_space(1)))
; #define LAS __attribute__((address_space(3)))
; #define LDS_WAIT() asm volatile("s_waitcnt lgkmcnt(0)" ::: "memory")
; __device__ __forceinline__ unsigned pk2(float lo, float hi) { return f2bf(lo) | (f2bf(hi) << 16); }
; __device__ __forceinline__ int nat_dim(int p) { return (p >> 1) + 64 * (p & 1); }
; __device__ __forceinline__ int src_col_in(int c) {
;     if (c < 5120) { const int blk = c >> 7, p = c & 127; const bool rope = blk < 16 || ((((blk - 16) >> 2) & 1) == 0); const int d = rope ? (p >> 1) + 64 * (p & 1) : p; return blk * 128 + d; }
;     if (c < OFF_Z) return c + 2096;
;     if (c < OFF_G) return c - 4048;
;     if (c < OFF_DT) return 5120 + (c - OFF_G);
;     if (c < NSRC) return c;
;     return -1;
; }
; template <int MAP, bool KS, bool KPERM = false>
; __device__ __forceinline__ void p0_transpose_item(const float* W, int K, int Nsrc, int nblk, bf16* WT, const float* ksA, const float* ksB, int ksplit, LAS float* scr, int item, int lane) {
;     const int kb = item / nblk, nb = item % nblk, k0 = 64 * kb, n0 = 32 * nb;
;     const int nr = n0 + (lane & 31); const int sc = MAP == 1 ? src_col_in(nr) : (MAP == 2 ? nat_dim(nr) : nr);
;     float v[32];
; #pragma unroll
;     for (int i = 0; i < 32; ++i) { const int k = k0 + 2 * i + (lane >> 5); const int ksrc = KPERM ? ((k & ~127) + nat_dim(k & 127)) : k;
;         v[i] = sc >= 0 ? W[(size_t)ksrc * Nsrc + sc] : 0.f; }
; #pragma unroll
;     for (int i = 0; i < 32; ++i) { const int kk = 2 * i + (lane >> 5); const int k = k0 + kk;
;         if (KS) v[i] *= (k < ksplit ? ksA[k] : ksB[k - ksplit]);
;         scr[kk * 33 + (lane & 31)] = v[i]; }
;     LDS_WAIT(); asm volatile("" ::: "memory");
;     const int c = lane & 7;
; #pragma unroll
;     for (int j = 0; j < 4; ++j) { const int n = (lane >> 3) + 8 * j; const LAS float* s = scr + (8 * c) * 33 + n;
;         v4u o; o.x = pk2(s[0 * 33], s[1 * 33]); o.y = pk2(s[2 * 33], s[3 * 33]); o.z = pk2(s[4 * 33], s[5 * 33]); o.w = pk2(s[6 * 33], s[7 * 33]);
;         *(GAS v4u*)(WT + (size_t)(n0 + n) * K + k0 + 8 * c) = o; }
;     LDS_WAIT(); asm volatile("" ::: "memory");
; }
	s_add_i32 s24, s23, 64
	s_lshl_b32 s20, s24, 7
	s_cmp_lt_u32 s24, 40
	s_cselect_b32 s21, 0, 0x830
	s_cmp_lt_u32 s24, 72
	s_cselect_b32 s21, s21, 0xfffff030
	s_add_i32 s20, s20, s21
	s_lshl_b32 s20, s20, 2
	s_add_u32 s8, s46, s20
	s_addc_u32 s9, s47, 0
	global_load_dwordx4 v[144:147], v76, s[8:9]
	s_add_u32 s8, s8, 0x16280
	s_addc_u32 s9, s9, 0
	global_load_dwordx4 v[148:151], v76, s[8:9]
	s_add_u32 s8, s8, 0x16280
	s_addc_u32 s9, s9, 0
	global_load_dwordx4 v[152:155], v76, s[8:9]
	s_add_u32 s8, s8, 0x16280
	s_addc_u32 s9, s9, 0
	global_load_dwordx4 v[156:159], v76, s[8:9]
	s_add_u32 s8, s8, 0x16280
	s_addc_u32 s9, s9, 0
	global_load_dwordx4 v[160:163], v76, s[8:9]
	s_add_u32 s8, s8, 0x16280
	s_addc_u32 s9, s9, 0
	global_load_dwordx4 v[164:167], v76, s[8:9]
	s_add_u32 s8, s8, 0x16280
	s_addc_u32 s9, s9, 0
	global_load_dwordx4 v[168:171], v76, s[8:9]
	s_add_u32 s8, s8, 0x16280
	s_addc_u32 s9, s9, 0
	global_load_dwordx4 v[172:175], v76, s[8:9]
	s_add_i32 s24, s23, 48
	s_mul_i32 s20, s24, 0x100000
	s_add_u32 s6, s48, s20
	s_addc_u32 s7, s49, 0
	s_cmp_lt_u32 s24, 16
	s_cselect_b32 s20, 1, 0
	s_sub_i32 s21, s24, 16
	s_bitcmp0_b32 s21, 2
	s_cselect_b32 s21, 1, 0
	s_cmp_lt_u32 s24, 40
	s_cselect_b32 s21, s21, 0
	s_or_b32 s20, s20, s21
	s_cmp_lg_u32 s20, 0
	s_cselect_b64 s[20:21], -1, 0
	v_cndmask_b32_e64 v91, v83, v87, s[20:21]
	v_cndmask_b32_e64 v92, v84, v88, s[20:21]
	v_cndmask_b32_e64 v93, v85, v89, s[20:21]
	v_cndmask_b32_e64 v94, v86, v90, s[20:21]
	ds_read_b32 v226, v112
	ds_read_b32 v227, v112 offset:512
	ds_read_b32 v228, v112 offset:1024
	ds_read_b32 v229, v112 offset:1536
	ds_read_b32 v230, v112 offset:2048
	ds_read_b32 v231, v112 offset:2560
	ds_read_b32 v232, v112 offset:3072
	ds_read_b32 v233, v112 offset:3584
	s_waitcnt lgkmcnt(0)
	v_bfe_u32 v120, v226, 16, 1
	v_bfe_u32 v121, v227, 16, 1
	v_bfe_u32 v122, v228, 16, 1
	v_bfe_u32 v123, v229, 16, 1
	v_bfe_u32 v124, v230, 16, 1
	v_bfe_u32 v125, v231, 16, 1
	v_bfe_u32 v126, v232, 16, 1
	v_bfe_u32 v127, v233, 16, 1
	v_add3_u32 v226, v226, v120, s63
	v_add3_u32 v227, v227, v121, s63
	v_add3_u32 v228, v228, v122, s63
	v_add3_u32 v229, v229, v123, s63
	v_add3_u32 v230, v230, v124, s63
	v_add3_u32 v231, v231, v125, s63
	v_add3_u32 v232, v232, v126, s63
	v_add3_u32 v233, v233, v127, s63
	v_perm_b32 v242, v227, v226, s64
	v_perm_b32 v243, v229, v228, s64
	v_perm_b32 v244, v231, v230, s64
	v_perm_b32 v245, v233, v232, s64
	s_nop 0
	global_store_dwordx4 v91, v[242:245], s[6:7]
	ds_read_b32 v226, v114
	ds_read_b32 v227, v114 offset:512
	ds_read_b32 v228, v114 offset:1024
	ds_read_b32 v229, v114 offset:1536
	ds_read_b32 v230, v114 offset:2048
	ds_read_b32 v231, v114 offset:2560
	ds_read_b32 v232, v114 offset:3072
	ds_read_b32 v233, v114 offset:3584
	s_waitcnt lgkmcnt(0)
	v_bfe_u32 v120, v226, 16, 1
	v_bfe_u32 v121, v227, 16, 1
	v_bfe_u32 v122, v228, 16, 1
	v_bfe_u32 v123, v229, 16, 1
	v_bfe_u32 v124, v230, 16, 1
	v_bfe_u32 v125, v231, 16, 1
	v_bfe_u32 v126, v232, 16, 1
	v_bfe_u32 v127, v233, 16, 1
	v_add3_u32 v226, v226, v120, s63
	v_add3_u32 v227, v227, v121, s63
	v_add3_u32 v228, v228, v122, s63
	v_add3_u32 v229, v229, v123, s63
	v_add3_u32 v230, v230, v124, s63
	v_add3_u32 v231, v231, v125, s63
	v_add3_u32 v232, v232, v126, s63
	v_add3_u32 v233, v233, v127, s63
	v_perm_b32 v242, v227, v226, s64
	v_perm_b32 v243, v229, v228, s64
	v_perm_b32 v244, v231, v230, s64
	v_perm_b32 v245, v233, v232, s64
	s_nop 0
	global_store_dwordx4 v92, v[242:245], s[6:7]
	ds_read_b32 v226, v116
	ds_read_b32 v227, v116 offset:512
	ds_read_b32 v228, v116 offset:1024
	ds_read_b32 v229, v116 offset:1536
	ds_read_b32 v230, v116 offset:2048
	ds_read_b32 v231, v116 offset:2560
	ds_read_b32 v232, v116 offset:3072
	ds_read_b32 v233, v116 offset:3584
	s_waitcnt lgkmcnt(0)
	v_bfe_u32 v120, v226, 16, 1
	v_bfe_u32 v121, v227, 16, 1
	v_bfe_u32 v122, v228, 16, 1
	v_bfe_u32 v123, v229, 16, 1
	v_bfe_u32 v124, v230, 16, 1
	v_bfe_u32 v125, v231, 16, 1
	v_bfe_u32 v126, v232, 16, 1
	v_bfe_u32 v127, v233, 16, 1
	v_add3_u32 v226, v226, v120, s63
	v_add3_u32 v227, v227, v121, s63
	v_add3_u32 v228, v228, v122, s63
	v_add3_u32 v229, v229, v123, s63
	v_add3_u32 v230, v230, v124, s63
	v_add3_u32 v231, v231, v125, s63
	v_add3_u32 v232, v232, v126, s63
	v_add3_u32 v233, v233, v127, s63
	v_perm_b32 v242, v227, v226, s64
	v_perm_b32 v243, v229, v228, s64
	v_perm_b32 v244, v231, v230, s64
	v_perm_b32 v245, v233, v232, s64
	s_nop 0
	global_store_dwordx4 v93, v[242:245], s[6:7]
	ds_read_b32 v226, v118
	ds_read_b32 v227, v118 offset:512
	ds_read_b32 v228, v118 offset:1024
	ds_read_b32 v229, v118 offset:1536
	ds_read_b32 v230, v118 offset:2048
	ds_read_b32 v231, v118 offset:2560
	ds_read_b32 v232, v118 offset:3072
	ds_read_b32 v233, v118 offset:3584
	s_waitcnt lgkmcnt(0)
	v_bfe_u32 v120, v226, 16, 1
	v_bfe_u32 v121, v227, 16, 1
	v_bfe_u32 v122, v228, 16, 1
	v_bfe_u32 v123, v229, 16, 1
	v_bfe_u32 v124, v230, 16, 1
	v_bfe_u32 v125, v231, 16, 1
	v_bfe_u32 v126, v232, 16, 1
	v_bfe_u32 v127, v233, 16, 1
	v_add3_u32 v226, v226, v120, s63
	v_add3_u32 v227, v227, v121, s63
	v_add3_u32 v228, v228, v122, s63
	v_add3_u32 v229, v229, v123, s63
	v_add3_u32 v230, v230, v124, s63
	v_add3_u32 v231, v231, v125, s63
	v_add3_u32 v232, v232, v126, s63
	v_add3_u32 v233, v233, v127, s63
	v_perm_b32 v242, v227, v226, s64
	v_perm_b32 v243, v229, v228, s64
	v_perm_b32 v244, v231, v230, s64
	v_perm_b32 v245, v233, v232, s64
	s_nop 0
	global_store_dwordx4 v94, v[242:245], s[6:7]
	s_waitcnt vmcnt(16)
	v_mul_f32_e32 v176, v42, v176
	v_mul_f32_e32 v177, v42, v177
	v_mul_f32_e32 v178, v42, v178
	v_mul_f32_e32 v179, v42, v179
	ds_write_b128 v210, v[176:179]
	v_mul_f32_e32 v180, v43, v180
	v_mul_f32_e32 v181, v43, v181
	v_mul_f32_e32 v182, v43, v182
	v_mul_f32_e32 v183, v43, v183
	ds_write_b128 v210, v[180:183] offset:1024
	v_mul_f32_e32 v184, v44, v184
	v_mul_f32_e32 v185, v44, v185
	v_mul_f32_e32 v186, v44, v186
	v_mul_f32_e32 v187, v44, v187
	ds_write_b128 v210, v[184:187] offset:2048
	v_mul_f32_e32 v188, v45, v188
	v_mul_f32_e32 v189, v45, v189
	v_mul_f32_e32 v190, v45, v190
	v_mul_f32_e32 v191, v45, v191
	ds_write_b128 v210, v[188:191] offset:3072
	v_mul_f32_e32 v192, v46, v192
	v_mul_f32_e32 v193, v46, v193
	v_mul_f32_e32 v194, v46, v194
	v_mul_f32_e32 v195, v46, v195
	ds_write_b128 v210, v[192:195] offset:4096
	v_mul_f32_e32 v196, v47, v196
	v_mul_f32_e32 v197, v47, v197
	v_mul_f32_e32 v198, v47, v198
	v_mul_f32_e32 v199, v47, v199
	ds_write_b128 v210, v[196:199] offset:5120
	v_mul_f32_e32 v200, v48, v200
	v_mul_f32_e32 v201, v48, v201
	v_mul_f32_e32 v202, v48, v202
	v_mul_f32_e32 v203, v48, v203
	ds_write_b128 v210, v[200:203] offset:6144
	v_mul_f32_e32 v204, v49, v204
	v_mul_f32_e32 v205, v49, v205
	v_mul_f32_e32 v206, v49, v206
	v_mul_f32_e32 v207, v49, v207
	ds_write_b128 v210, v[204:207] offset:7168
	s_waitcnt lgkmcnt(0)
	s_barrier
; #define GAS __attribute__((address_space(1)))
; #define LAS __attribute__((address_space(3)))
; #define LDS_WAIT() asm volatile("s_waitcnt lgkmcnt(0)" ::: "memory")
; __device__ __forceinline__ unsigned pk2(float lo, float hi) { return f2bf(lo) | (f2bf(hi) << 16); }
; __device__ __forceinline__ int nat_dim(int p) { return (p >> 1) + 64 * (p & 1); }
; __device__ __forceinline__ int src_col_in(int c) {
;     if (c < 5120) { const int blk = c >> 7, p = c & 127; const bool rope = blk < 16 || ((((blk - 16) >> 2) & 1) == 0); const int d = rope ? (p >> 1) + 64 * (p & 1) : p; return blk * 128 + d; }
;     if (c < OFF_Z) return c + 2096;
;     if (c < OFF_G) return c - 4048;
;     if (c < OFF_DT) return 5120 + (c - OFF_G);
;     if (c < NSRC) return c;
;     return -1;
; }
; template <int MAP, bool KS, bool KPERM = false>
; __device__ __forceinline__ void p0_transpose_item(const float* W, int K, int Nsrc, int nblk, bf16* WT, const float* ksA, const float* ksB, int ksplit, LAS float* scr, int item, int lane) {
;     const int kb = item / nblk, nb = item % nblk, k0 = 64 * kb, n0 = 32 * nb;
;     const int nr = n0 + (lane & 31); const int sc = MAP == 1 ? src_col_in(nr) : (MAP == 2 ? nat_dim(nr) : nr);
;     float v[32];
; #pragma unroll
;     for (int i = 0; i < 32; ++i) { const int k = k0 + 2 * i + (lane >> 5); const int ksrc = KPERM ? ((k & ~127) + nat_dim(k & 127)) : k;
;         v[i] = sc >= 0 ? W[(size_t)ksrc * Nsrc + sc] : 0.f; }
; #pragma unroll
;     for (int i = 0; i < 32; ++i) { const int kk = 2 * i + (lane >> 5); const int k = k0 + kk;
;         if (KS) v[i] *= (k < ksplit ? ksA[k] : ksB[k - ksplit]);
;         scr[kk * 33 + (lane & 31)] = v[i]; }
;     LDS_WAIT(); asm volatile("" ::: "memory");
;     const int c = lane & 7;
; #pragma unroll
;     for (int j = 0; j < 4; ++j) { const int n = (lane >> 3) + 8 * j; const LAS float* s = scr + (8 * c) * 33 + n;
;         v4u o; o.x = pk2(s[0 * 33], s[1 * 33]); o.y = pk2(s[2 * 33], s[3 * 33]); o.z = pk2(s[4 * 33], s[5 * 33]); o.w = pk2(s[6 * 33], s[7 * 33]);
;         *(GAS v4u*)(WT + (size_t)(n0 + n) * K + k0 + 8 * c) = o; }
;     LDS_WAIT(); asm volatile("" ::: "memory");
; }
	s_add_i32 s24, s23, 72
	s_lshl_b32 s20, s24, 7
	s_cmp_lt_u32 s24, 40
	s_cselect_b32 s21, 0, 0x830
	s_cmp_lt_u32 s24, 72
	s_cselect_b32 s21, s21, 0xfffff030
	s_add_i32 s20, s20, s21
	s_lshl_b32 s20, s20, 2
	s_add_u32 s8, s46, s20
	s_addc_u32 s9, s47, 0
	global_load_dwordx4 v[176:179], v76, s[8:9]
	s_add_u32 s8, s8, 0x16280
	s_addc_u32 s9, s9, 0
	global_load_dwordx4 v[180:183], v76, s[8:9]
	s_add_u32 s8, s8, 0x16280
	s_addc_u32 s9, s9, 0
	global_load_dwordx4 v[184:187], v76, s[8:9]
	s_add_u32 s8, s8, 0x16280
	s_addc_u32 s9, s9, 0
	global_load_dwordx4 v[188:191], v76, s[8:9]
	s_add_u32 s8, s8, 0x16280
	s_addc_u32 s9, s9, 0
	global_load_dwordx4 v[192:195], v76, s[8:9]
	s_add_u32 s8, s8, 0x16280
	s_addc_u32 s9, s9, 0
	global_load_dwordx4 v[196:199], v76, s[8:9]
	s_add_u32 s8, s8, 0x16280
	s_addc_u32 s9, s9, 0
	global_load_dwordx4 v[200:203], v76, s[8:9]
	s_add_u32 s8, s8, 0x16280
	s_addc_u32 s9, s9, 0
	global_load_dwordx4 v[204:207], v76, s[8:9]
	s_add_i32 s24, s23, 56
	s_mul_i32 s20, s24, 0x100000
	s_add_u32 s6, s48, s20
	s_addc_u32 s7, s49, 0
	s_cmp_lt_u32 s24, 16
	s_cselect_b32 s20, 1, 0
	s_sub_i32 s21, s24, 16
	s_bitcmp0_b32 s21, 2
	s_cselect_b32 s21, 1, 0
	s_cmp_lt_u32 s24, 40
	s_cselect_b32 s21, s21, 0
	s_or_b32 s20, s20, s21
	s_cmp_lg_u32 s20, 0
	s_cselect_b64 s[20:21], -1, 0
	v_cndmask_b32_e64 v91, v83, v87, s[20:21]
	v_cndmask_b32_e64 v92, v84, v88, s[20:21]
	v_cndmask_b32_e64 v93, v85, v89, s[20:21]
	v_cndmask_b32_e64 v94, v86, v90, s[20:21]
	ds_read_b32 v226, v113
	ds_read_b32 v227, v113 offset:512
	ds_read_b32 v228, v113 offset:1024
	ds_read_b32 v229, v113 offset:1536
	ds_read_b32 v230, v113 offset:2048
	ds_read_b32 v231, v113 offset:2560
	ds_read_b32 v232, v113 offset:3072
	ds_read_b32 v233, v113 offset:3584
	s_waitcnt lgkmcnt(0)
	v_bfe_u32 v120, v226, 16, 1
	v_bfe_u32 v121, v227, 16, 1
	v_bfe_u32 v122, v228, 16, 1
	v_bfe_u32 v123, v229, 16, 1
	v_bfe_u32 v124, v230, 16, 1
	v_bfe_u32 v125, v231, 16, 1
	v_bfe_u32 v126, v232, 16, 1
	v_bfe_u32 v127, v233, 16, 1
	v_add3_u32 v226, v226, v120, s63
	v_add3_u32 v227, v227, v121, s63
	v_add3_u32 v228, v228, v122, s63
	v_add3_u32 v229, v229, v123, s63
	v_add3_u32 v230, v230, v124, s63
	v_add3_u32 v231, v231, v125, s63
	v_add3_u32 v232, v232, v126, s63
	v_add3_u32 v233, v233, v127, s63
	v_perm_b32 v242, v227, v226, s64
	v_perm_b32 v243, v229, v228, s64
	v_perm_b32 v244, v231, v230, s64
	v_perm_b32 v245, v233, v232, s64
	s_nop 0
	global_store_dwordx4 v91, v[242:245], s[6:7]
	ds_read_b32 v226, v115
	ds_read_b32 v227, v115 offset:512
	ds_read_b32 v228, v115 offset:1024
	ds_read_b32 v229, v115 offset:1536
	ds_read_b32 v230, v115 offset:2048
	ds_read_b32 v231, v115 offset:2560
	ds_read_b32 v232, v115 offset:3072
	ds_read_b32 v233, v115 offset:3584
	s_waitcnt lgkmcnt(0)
	v_bfe_u32 v120, v226, 16, 1
	v_bfe_u32 v121, v227, 16, 1
	v_bfe_u32 v122, v228, 16, 1
	v_bfe_u32 v123, v229, 16, 1
	v_bfe_u32 v124, v230, 16, 1
	v_bfe_u32 v125, v231, 16, 1
	v_bfe_u32 v126, v232, 16, 1
	v_bfe_u32 v127, v233, 16, 1
	v_add3_u32 v226, v226, v120, s63
	v_add3_u32 v227, v227, v121, s63
	v_add3_u32 v228, v228, v122, s63
	v_add3_u32 v229, v229, v123, s63
	v_add3_u32 v230, v230, v124, s63
	v_add3_u32 v231, v231, v125, s63
	v_add3_u32 v232, v232, v126, s63
	v_add3_u32 v233, v233, v127, s63
	v_perm_b32 v242, v227, v226, s64
	v_perm_b32 v243, v229, v228, s64
	v_perm_b32 v244, v231, v230, s64
	v_perm_b32 v245, v233, v232, s64
	s_nop 0
	global_store_dwordx4 v92, v[242:245], s[6:7]
	ds_read_b32 v226, v117
	ds_read_b32 v227, v117 offset:512
	ds_read_b32 v228, v117 offset:1024
	ds_read_b32 v229, v117 offset:1536
	ds_read_b32 v230, v117 offset:2048
	ds_read_b32 v231, v117 offset:2560
	ds_read_b32 v232, v117 offset:3072
	ds_read_b32 v233, v117 offset:3584
	s_waitcnt lgkmcnt(0)
	v_bfe_u32 v120, v226, 16, 1
	v_bfe_u32 v121, v227, 16, 1
	v_bfe_u32 v122, v228, 16, 1
	v_bfe_u32 v123, v229, 16, 1
	v_bfe_u32 v124, v230, 16, 1
	v_bfe_u32 v125, v231, 16, 1
	v_bfe_u32 v126, v232, 16, 1
	v_bfe_u32 v127, v233, 16, 1
	v_add3_u32 v226, v226, v120, s63
	v_add3_u32 v227, v227, v121, s63
	v_add3_u32 v228, v228, v122, s63
	v_add3_u32 v229, v229, v123, s63
	v_add3_u32 v230, v230, v124, s63
	v_add3_u32 v231, v231, v125, s63
	v_add3_u32 v232, v232, v126, s63
	v_add3_u32 v233, v233, v127, s63
	v_perm_b32 v242, v227, v226, s64
	v_perm_b32 v243, v229, v228, s64
	v_perm_b32 v244, v231, v230, s64
	v_perm_b32 v245, v233, v232, s64
	s_nop 0
	global_store_dwordx4 v93, v[242:245], s[6:7]
	ds_read_b32 v226, v119
	ds_read_b32 v227, v119 offset:512
	ds_read_b32 v228, v119 offset:1024
	ds_read_b32 v229, v119 offset:1536
	ds_read_b32 v230, v119 offset:2048
	ds_read_b32 v231, v119 offset:2560
	ds_read_b32 v232, v119 offset:3072
	ds_read_b32 v233, v119 offset:3584
	s_waitcnt lgkmcnt(0)
	v_bfe_u32 v120, v226, 16, 1
	v_bfe_u32 v121, v227, 16, 1
	v_bfe_u32 v122, v228, 16, 1
	v_bfe_u32 v123, v229, 16, 1
	v_bfe_u32 v124, v230, 16, 1
	v_bfe_u32 v125, v231, 16, 1
	v_bfe_u32 v126, v232, 16, 1
	v_bfe_u32 v127, v233, 16, 1
	v_add3_u32 v226, v226, v120, s63
	v_add3_u32 v227, v227, v121, s63
	v_add3_u32 v228, v228, v122, s63
	v_add3_u32 v229, v229, v123, s63
	v_add3_u32 v230, v230, v124, s63
	v_add3_u32 v231, v231, v125, s63
	v_add3_u32 v232, v232, v126, s63
	v_add3_u32 v233, v233, v127, s63
	v_perm_b32 v242, v227, v226, s64
	v_perm_b32 v243, v229, v228, s64
	v_perm_b32 v244, v231, v230, s64
	v_perm_b32 v245, v233, v232, s64
	s_nop 0
	global_store_dwordx4 v94, v[242:245], s[6:7]
	s_waitcnt vmcnt(16)
	v_mul_f32_e32 v144, v42, v144
	v_mul_f32_e32 v145, v42, v145
	v_mul_f32_e32 v146, v42, v146
	v_mul_f32_e32 v147, v42, v147
	ds_write_b128 v209, v[144:147]
	v_mul_f32_e32 v148, v43, v148
	v_mul_f32_e32 v149, v43, v149
	v_mul_f32_e32 v150, v43, v150
	v_mul_f32_e32 v151, v43, v151
	ds_write_b128 v209, v[148:151] offset:1024
	v_mul_f32_e32 v152, v44, v152
	v_mul_f32_e32 v153, v44, v153
	v_mul_f32_e32 v154, v44, v154
	v_mul_f32_e32 v155, v44, v155
	ds_write_b128 v209, v[152:155] offset:2048
	v_mul_f32_e32 v156, v45, v156
	v_mul_f32_e32 v157, v45, v157
	v_mul_f32_e32 v158, v45, v158
	v_mul_f32_e32 v159, v45, v159
	ds_write_b128 v209, v[156:159] offset:3072
	v_mul_f32_e32 v160, v46, v160
	v_mul_f32_e32 v161, v46, v161
	v_mul_f32_e32 v162, v46, v162
	v_mul_f32_e32 v163, v46, v163
	ds_write_b128 v209, v[160:163] offset:4096
	v_mul_f32_e32 v164, v47, v164
	v_mul_f32_e32 v165, v47, v165
	v_mul_f32_e32 v166, v47, v166
	v_mul_f32_e32 v167, v47, v167
	ds_write_b128 v209, v[164:167] offset:5120
	v_mul_f32_e32 v168, v48, v168
	v_mul_f32_e32 v169, v48, v169
	v_mul_f32_e32 v170, v48, v170
	v_mul_f32_e32 v171, v48, v171
	ds_write_b128 v209, v[168:171] offset:6144
	v_mul_f32_e32 v172, v49, v172
	v_mul_f32_e32 v173, v49, v173
	v_mul_f32_e32 v174, v49, v174
	v_mul_f32_e32 v175, v49, v175
	ds_write_b128 v209, v[172:175] offset:7168
	s_waitcnt lgkmcnt(0)
	s_barrier
; #define GAS __attribute__((address_space(1)))
; #define LAS __attribute__((address_space(3)))
; #define LDS_WAIT() asm volatile("s_waitcnt lgkmcnt(0)" ::: "memory")
; __device__ __forceinline__ unsigned pk2(float lo, float hi) { return f2bf(lo) | (f2bf(hi) << 16); }
; __device__ __forceinline__ int nat_dim(int p) { return (p >> 1) + 64 * (p & 1); }
; __device__ __forceinline__ int src_col_in(int c) {
;     if (c < 5120) { const int blk = c >> 7, p = c & 127; const bool rope = blk < 16 || ((((blk - 16) >> 2) & 1) == 0); const int d = rope ? (p >> 1) + 64 * (p & 1) : p; return blk * 128 + d; }
;     if (c < OFF_Z) return c + 2096;
;     if (c < OFF_G) return c - 4048;
;     if (c < OFF_DT) return 5120 + (c - OFF_G);
;     if (c < NSRC) return c;
;     return -1;
; }
; template <int MAP, bool KS, bool KPERM = false>
; __device__ __forceinline__ void p0_transpose_item(const float* W, int K, int Nsrc, int nblk, bf16* WT, const float* ksA, const float* ksB, int ksplit, LAS float* scr, int item, int lane) {
;     const int kb = item / nblk, nb = item % nblk, k0 = 64 * kb, n0 = 32 * nb;
;     const int nr = n0 + (lane & 31); const int sc = MAP == 1 ? src_col_in(nr) : (MAP == 2 ? nat_dim(nr) : nr);
;     float v[32];
; #pragma unroll
;     for (int i = 0; i < 32; ++i) { const int k = k0 + 2 * i + (lane >> 5); const int ksrc = KPERM ? ((k & ~127) + nat_dim(k & 127)) : k;
;         v[i] = sc >= 0 ? W[(size_t)ksrc * Nsrc + sc] : 0.f; }
; #pragma unroll
;     for (int i = 0; i < 32; ++i) { const int kk = 2 * i + (lane >> 5); const int k = k0 + kk;
;         if (KS) v[i] *= (k < ksplit ? ksA[k] : ksB[k - ksplit]);
;         scr[kk * 33 + (lane & 31)] = v[i]; }
;     LDS_WAIT(); asm volatile("" ::: "memory");
;     const int c = lane & 7;
; #pragma unroll
;     for (int j = 0; j < 4; ++j) { const int n = (lane >> 3) + 8 * j; const LAS float* s = scr + (8 * c) * 33 + n;
;         v4u o; o.x = pk2(s[0 * 33], s[1 * 33]); o.y = pk2(s[2 * 33], s[3 * 33]); o.z = pk2(s[4 * 33], s[5 * 33]); o.w = pk2(s[6 * 33], s[7 * 33]);
;         *(GAS v4u*)(WT + (size_t)(n0 + n) * K + k0 + 8 * c) = o; }
;     LDS_WAIT(); asm volatile("" ::: "memory");
; }
	s_add_i32 s24, s23, 80
	s_lshl_b32 s20, s24, 7
	s_cmp_lt_u32 s24, 40
	s_cselect_b32 s21, 0, 0x830
	s_cmp_lt_u32 s24, 72
	s_cselect_b32 s21, s21, 0xfffff030
	s_add_i32 s20, s20, s21
	s_lshl_b32 s20, s20, 2
	s_add_u32 s8, s46, s20
	s_addc_u32 s9, s47, 0
	global_load_dwordx4 v[144:147], v76, s[8:9]
	s_add_u32 s8, s8, 0x16280
	s_addc_u32 s9, s9, 0
	global_load_dwordx4 v[148:151], v76, s[8:9]
	s_add_u32 s8, s8, 0x16280
	s_addc_u32 s9, s9, 0
	global_load_dwordx4 v[152:155], v76, s[8:9]
	s_add_u32 s8, s8, 0x16280
	s_addc_u32 s9, s9, 0
	global_load_dwordx4 v[156:159], v76, s[8:9]
	s_add_u32 s8, s8, 0x16280
	s_addc_u32 s9, s9, 0
	global_load_dwordx4 v[160:163], v76, s[8:9]
	s_add_u32 s8, s8, 0x16280
	s_addc_u32 s9, s9, 0
	global_load_dwordx4 v[164:167], v76, s[8:9]
	s_add_u32 s8, s8, 0x16280
	s_addc_u32 s9, s9, 0
	global_load_dwordx4 v[168:171], v76, s[8:9]
	s_add_u32 s8, s8, 0x16280
	s_addc_u32 s9, s9, 0
	global_load_dwordx4 v[172:175], v76, s[8:9]
	s_add_i32 s24, s23, 64
	s_mul_i32 s20, s24, 0x100000
	s_add_u32 s6, s48, s20
	s_addc_u32 s7, s49, 0
	s_cmp_lt_u32 s24, 16
	s_cselect_b32 s20, 1, 0
	s_sub_i32 s21, s24, 16
	s_bitcmp0_b32 s21, 2
	s_cselect_b32 s21, 1, 0
	s_cmp_lt_u32 s24, 40
	s_cselect_b32 s21, s21, 0
	s_or_b32 s20, s20, s21
	s_cmp_lg_u32 s20, 0
	s_cselect_b64 s[20:21], -1, 0
	v_cndmask_b32_e64 v91, v83, v87, s[20:21]
	v_cndmask_b32_e64 v92, v84, v88, s[20:21]
	v_cndmask_b32_e64 v93, v85, v89, s[20:21]
	v_cndmask_b32_e64 v94, v86, v90, s[20:21]
	ds_read_b32 v226, v112
	ds_read_b32 v227, v112 offset:512
	ds_read_b32 v228, v112 offset:1024
	ds_read_b32 v229, v112 offset:1536
	ds_read_b32 v230, v112 offset:2048
	ds_read_b32 v231, v112 offset:2560
	ds_read_b32 v232, v112 offset:3072
	ds_read_b32 v233, v112 offset:3584
	s_waitcnt lgkmcnt(0)
	v_bfe_u32 v120, v226, 16, 1
	v_bfe_u32 v121, v227, 16, 1
	v_bfe_u32 v122, v228, 16, 1
	v_bfe_u32 v123, v229, 16, 1
	v_bfe_u32 v124, v230, 16, 1
	v_bfe_u32 v125, v231, 16, 1
	v_bfe_u32 v126, v232, 16, 1
	v_bfe_u32 v127, v233, 16, 1
	v_add3_u32 v226, v226, v120, s63
	v_add3_u32 v227, v227, v121, s63
	v_add3_u32 v228, v228, v122, s63
	v_add3_u32 v229, v229, v123, s63
	v_add3_u32 v230, v230, v124, s63
	v_add3_u32 v231, v231, v125, s63
	v_add3_u32 v232, v232, v126, s63
	v_add3_u32 v233, v233, v127, s63
	v_perm_b32 v242, v227, v226, s64
	v_perm_b32 v243, v229, v228, s64
	v_perm_b32 v244, v231, v230, s64
	v_perm_b32 v245, v233, v232, s64
	s_nop 0
	global_store_dwordx4 v91, v[242:245], s[6:7]
	ds_read_b32 v226, v114
	ds_read_b32 v227, v114 offset:512
	ds_read_b32 v228, v114 offset:1024
	ds_read_b32 v229, v114 offset:1536
	ds_read_b32 v230, v114 offset:2048
	ds_read_b32 v231, v114 offset:2560
	ds_read_b32 v232, v114 offset:3072
	ds_read_b32 v233, v114 offset:3584
	s_waitcnt lgkmcnt(0)
	v_bfe_u32 v120, v226, 16, 1
	v_bfe_u32 v121, v227, 16, 1
	v_bfe_u32 v122, v228, 16, 1
	v_bfe_u32 v123, v229, 16, 1
	v_bfe_u32 v124, v230, 16, 1
	v_bfe_u32 v125, v231, 16, 1
	v_bfe_u32 v126, v232, 16, 1
	v_bfe_u32 v127, v233, 16, 1
	v_add3_u32 v226, v226, v120, s63
	v_add3_u32 v227, v227, v121, s63
	v_add3_u32 v228, v228, v122, s63
	v_add3_u32 v229, v229, v123, s63
	v_add3_u32 v230, v230, v124, s63
	v_add3_u32 v231, v231, v125, s63
	v_add3_u32 v232, v232, v126, s63
	v_add3_u32 v233, v233, v127, s63
	v_perm_b32 v242, v227, v226, s64
	v_perm_b32 v243, v229, v228, s64
	v_perm_b32 v244, v231, v230, s64
	v_perm_b32 v245, v233, v232, s64
	s_nop 0
	global_store_dwordx4 v92, v[242:245], s[6:7]
	ds_read_b32 v226, v116
	ds_read_b32 v227, v116 offset:512
	ds_read_b32 v228, v116 offset:1024
	ds_read_b32 v229, v116 offset:1536
	ds_read_b32 v230, v116 offset:2048
	ds_read_b32 v231, v116 offset:2560
	ds_read_b32 v232, v116 offset:3072
	ds_read_b32 v233, v116 offset:3584
	s_waitcnt lgkmcnt(0)
	v_bfe_u32 v120, v226, 16, 1
	v_bfe_u32 v121, v227, 16, 1
	v_bfe_u32 v122, v228, 16, 1
	v_bfe_u32 v123, v229, 16, 1
	v_bfe_u32 v124, v230, 16, 1
	v_bfe_u32 v125, v231, 16, 1
	v_bfe_u32 v126, v232, 16, 1
	v_bfe_u32 v127, v233, 16, 1
	v_add3_u32 v226, v226, v120, s63
	v_add3_u32 v227, v227, v121, s63
	v_add3_u32 v228, v228, v122, s63
	v_add3_u32 v229, v229, v123, s63
	v_add3_u32 v230, v230, v124, s63
	v_add3_u32 v231, v231, v125, s63
	v_add3_u32 v232, v232, v126, s63
	v_add3_u32 v233, v233, v127, s63
	v_perm_b32 v242, v227, v226, s64
	v_perm_b32 v243, v229, v228, s64
	v_perm_b32 v244, v231, v230, s64
	v_perm_b32 v245, v233, v232, s64
	s_nop 0
	global_store_dwordx4 v93, v[242:245], s[6:7]
	ds_read_b32 v226, v118
	ds_read_b32 v227, v118 offset:512
	ds_read_b32 v228, v118 offset:1024
	ds_read_b32 v229, v118 offset:1536
	ds_read_b32 v230, v118 offset:2048
	ds_read_b32 v231, v118 offset:2560
	ds_read_b32 v232, v118 offset:3072
	ds_read_b32 v233, v118 offset:3584
	s_waitcnt lgkmcnt(0)
	v_bfe_u32 v120, v226, 16, 1
	v_bfe_u32 v121, v227, 16, 1
	v_bfe_u32 v122, v228, 16, 1
	v_bfe_u32 v123, v229, 16, 1
	v_bfe_u32 v124, v230, 16, 1
	v_bfe_u32 v125, v231, 16, 1
	v_bfe_u32 v126, v232, 16, 1
	v_bfe_u32 v127, v233, 16, 1
	v_add3_u32 v226, v226, v120, s63
	v_add3_u32 v227, v227, v121, s63
	v_add3_u32 v228, v228, v122, s63
	v_add3_u32 v229, v229, v123, s63
	v_add3_u32 v230, v230, v124, s63
	v_add3_u32 v231, v231, v125, s63
	v_add3_u32 v232, v232, v126, s63
	v_add3_u32 v233, v233, v127, s63
	v_perm_b32 v242, v227, v226, s64
	v_perm_b32 v243, v229, v228, s64
	v_perm_b32 v244, v231, v230, s64
	v_perm_b32 v245, v233, v232, s64
	s_nop 0
	global_store_dwordx4 v94, v[242:245], s[6:7]
	s_waitcnt vmcnt(16)
	v_mul_f32_e32 v176, v42, v176
	v_mul_f32_e32 v177, v42, v177
	v_mul_f32_e32 v178, v42, v178
	v_mul_f32_e32 v179, v42, v179
	ds_write_b128 v210, v[176:179]
	v_mul_f32_e32 v180, v43, v180
	v_mul_f32_e32 v181, v43, v181
	v_mul_f32_e32 v182, v43, v182
	v_mul_f32_e32 v183, v43, v183
	ds_write_b128 v210, v[180:183] offset:1024
	v_mul_f32_e32 v184, v44, v184
	v_mul_f32_e32 v185, v44, v185
	v_mul_f32_e32 v186, v44, v186
	v_mul_f32_e32 v187, v44, v187
	ds_write_b128 v210, v[184:187] offset:2048
	v_mul_f32_e32 v188, v45, v188
	v_mul_f32_e32 v189, v45, v189
	v_mul_f32_e32 v190, v45, v190
	v_mul_f32_e32 v191, v45, v191
	ds_write_b128 v210, v[188:191] offset:3072
	v_mul_f32_e32 v192, v46, v192
	v_mul_f32_e32 v193, v46, v193
	v_mul_f32_e32 v194, v46, v194
	v_mul_f32_e32 v195, v46, v195
	ds_write_b128 v210, v[192:195] offset:4096
	v_mul_f32_e32 v196, v47, v196
	v_mul_f32_e32 v197, v47, v197
	v_mul_f32_e32 v198, v47, v198
	v_mul_f32_e32 v199, v47, v199
	ds_write_b128 v210, v[196:199] offset:5120
	v_mul_f32_e32 v200, v48, v200
	v_mul_f32_e32 v201, v48, v201
	v_mul_f32_e32 v202, v48, v202
	v_mul_f32_e32 v203, v48, v203
	ds_write_b128 v210, v[200:203] offset:6144
	v_mul_f32_e32 v204, v49, v204
	v_mul_f32_e32 v205, v49, v205
	v_mul_f32_e32 v206, v49, v206
	v_mul_f32_e32 v207, v49, v207
	ds_write_b128 v210, v[204:207] offset:7168
	s_waitcnt lgkmcnt(0)
	s_barrier
; #define GAS __attribute__((address_space(1)))
; #define LAS __attribute__((address_space(3)))
; #define LDS_WAIT() asm volatile("s_waitcnt lgkmcnt(0)" ::: "memory")
; __device__ __forceinline__ unsigned pk2(float lo, float hi) { return f2bf(lo) | (f2bf(hi) << 16); }
; __device__ __forceinline__ int nat_dim(int p) { return (p >> 1) + 64 * (p & 1); }
; __device__ __forceinline__ int src_col_in(int c) {
;     if (c < 5120) { const int blk = c >> 7, p = c & 127; const bool rope = blk < 16 || ((((blk - 16) >> 2) & 1) == 0); const int d = rope ? (p >> 1) + 64 * (p & 1) : p; return blk * 128 + d; }
;     if (c < OFF_Z) return c + 2096;
;     if (c < OFF_G) return c - 4048;
;     if (c < OFF_DT) return 5120 + (c - OFF_G);
;     if (c < NSRC) return c;
;     return -1;
; }
; template <int MAP, bool KS, bool KPERM = false>
; __device__ __forceinline__ void p0_transpose_item(const float* W, int K, int Nsrc, int nblk, bf16* WT, const float* ksA, const float* ksB, int ksplit, LAS float* scr, int item, int lane) {
;     const int kb = item / nblk, nb = item % nblk, k0 = 64 * kb, n0 = 32 * nb;
;     const int nr = n0 + (lane & 31); const int sc = MAP == 1 ? src_col_in(nr) : (MAP == 2 ? nat_dim(nr) : nr);
;     float v[32];
; #pragma unroll
;     for (int i = 0; i < 32; ++i) { const int k = k0 + 2 * i + (lane >> 5); const int ksrc = KPERM ? ((k & ~127) + nat_dim(k & 127)) : k;
;         v[i] = sc >= 0 ? W[(size_t)ksrc * Nsrc + sc] : 0.f; }
; #pragma unroll
;     for (int i = 0; i < 32; ++i) { const int kk = 2 * i + (lane >> 5); const int k = k0 + kk;
;         if (KS) v[i] *= (k < ksplit ? ksA[k] : ksB[k - ksplit]);
;         scr[kk * 33 + (lane & 31)] = v[i]; }
;     LDS_WAIT(); asm volatile("" ::: "memory");
;     const int c = lane & 7;
; #pragma unroll
;     for (int j = 0; j < 4; ++j) { const int n = (lane >> 3) + 8 * j; const LAS float* s = scr + (8 * c) * 33 + n;
;         v4u o; o.x = pk2(s[0 * 33], s[1 * 33]); o.y = pk2(s[2 * 33], s[3 * 33]); o.z = pk2(s[4 * 33], s[5 * 33]); o.w = pk2(s[6 * 33], s[7 * 33]);
;         *(GAS v4u*)(WT + (size_t)(n0 + n) * K + k0 + 8 * c) = o; }
;     LDS_WAIT(); asm volatile("" ::: "memory");
; }
	s_add_i32 s24, s23, 0
	s_lshl_b32 s20, s24, 7
	s_cmp_lt_u32 s24, 40
	s_cselect_b32 s21, 0, 0x830
	s_cmp_lt_u32 s24, 72
	s_cselect_b32 s21, s21, 0xfffff030
	s_add_i32 s20, s20, s21
	s_lshl_b32 s20, s20, 2
	s_add_u32 s8, s50, s20
	s_addc_u32 s9, s51, 0
	global_load_dwordx4 v[176:179], v76, s[8:9]
	s_add_u32 s8, s8, 0x16280
	s_addc_u32 s9, s9, 0
	global_load_dwordx4 v[180:183], v76, s[8:9]
	s_add_u32 s8, s8, 0x16280
	s_addc_u32 s9, s9, 0
	global_load_dwordx4 v[184:187], v76, s[8:9]
	s_add_u32 s8, s8, 0x16280
	s_addc_u32 s9, s9, 0
	global_load_dwordx4 v[188:191], v76, s[8:9]
	s_add_u32 s8, s8, 0x16280
	s_addc_u32 s9, s9, 0
	global_load_dwordx4 v[192:195], v76, s[8:9]
	s_add_u32 s8, s8, 0x16280
	s_addc_u32 s9, s9, 0
	global_load_dwordx4 v[196:199], v76, s[8:9]
	s_add_u32 s8, s8, 0x16280
	s_addc_u32 s9, s9, 0
	global_load_dwordx4 v[200:203], v76, s[8:9]
	s_add_u32 s8, s8, 0x16280
	s_addc_u32 s9, s9, 0
	global_load_dwordx4 v[204:207], v76, s[8:9]
	s_add_i32 s24, s23, 72
	s_mul_i32 s20, s24, 0x100000
	s_add_u32 s6, s48, s20
	s_addc_u32 s7, s49, 0
	s_cmp_lt_u32 s24, 16
	s_cselect_b32 s20, 1, 0
	s_sub_i32 s21, s24, 16
	s_bitcmp0_b32 s21, 2
	s_cselect_b32 s21, 1, 0
	s_cmp_lt_u32 s24, 40
	s_cselect_b32 s21, s21, 0
	s_or_b32 s20, s20, s21
	s_cmp_lg_u32 s20, 0
	s_cselect_b64 s[20:21], -1, 0
	v_cndmask_b32_e64 v91, v83, v87, s[20:21]
	v_cndmask_b32_e64 v92, v84, v88, s[20:21]
	v_cndmask_b32_e64 v93, v85, v89, s[20:21]
	v_cndmask_b32_e64 v94, v86, v90, s[20:21]
	ds_read_b32 v226, v113
	ds_read_b32 v227, v113 offset:512
	ds_read_b32 v228, v113 offset:1024
	ds_read_b32 v229, v113 offset:1536
	ds_read_b32 v230, v113 offset:2048
	ds_read_b32 v231, v113 offset:2560
	ds_read_b32 v232, v113 offset:3072
	ds_read_b32 v233, v113 offset:3584
	s_waitcnt lgkmcnt(0)
	v_bfe_u32 v120, v226, 16, 1
	v_bfe_u32 v121, v227, 16, 1
	v_bfe_u32 v122, v228, 16, 1
	v_bfe_u32 v123, v229, 16, 1
	v_bfe_u32 v124, v230, 16, 1
	v_bfe_u32 v125, v231, 16, 1
	v_bfe_u32 v126, v232, 16, 1
	v_bfe_u32 v127, v233, 16, 1
	v_add3_u32 v226, v226, v120, s63
	v_add3_u32 v227, v227, v121, s63
	v_add3_u32 v228, v228, v122, s63
	v_add3_u32 v229, v229, v123, s63
	v_add3_u32 v230, v230, v124, s63
	v_add3_u32 v231, v231, v125, s63
	v_add3_u32 v232, v232, v126, s63
	v_add3_u32 v233, v233, v127, s63
	v_perm_b32 v242, v227, v226, s64
	v_perm_b32 v243, v229, v228, s64
	v_perm_b32 v244, v231, v230, s64
	v_perm_b32 v245, v233, v232, s64
	s_nop 0
	global_store_dwordx4 v91, v[242:245], s[6:7]
	ds_read_b32 v226, v115
	ds_read_b32 v227, v115 offset:512
	ds_read_b32 v228, v115 offset:1024
	ds_read_b32 v229, v115 offset:1536
	ds_read_b32 v230, v115 offset:2048
	ds_read_b32 v231, v115 offset:2560
	ds_read_b32 v232, v115 offset:3072
	ds_read_b32 v233, v115 offset:3584
	s_waitcnt lgkmcnt(0)
	v_bfe_u32 v120, v226, 16, 1
	v_bfe_u32 v121, v227, 16, 1
	v_bfe_u32 v122, v228, 16, 1
	v_bfe_u32 v123, v229, 16, 1
	v_bfe_u32 v124, v230, 16, 1
	v_bfe_u32 v125, v231, 16, 1
	v_bfe_u32 v126, v232, 16, 1
	v_bfe_u32 v127, v233, 16, 1
	v_add3_u32 v226, v226, v120, s63
	v_add3_u32 v227, v227, v121, s63
	v_add3_u32 v228, v228, v122, s63
	v_add3_u32 v229, v229, v123, s63
	v_add3_u32 v230, v230, v124, s63
	v_add3_u32 v231, v231, v125, s63
	v_add3_u32 v232, v232, v126, s63
	v_add3_u32 v233, v233, v127, s63
	v_perm_b32 v242, v227, v226, s64
	v_perm_b32 v243, v229, v228, s64
	v_perm_b32 v244, v231, v230, s64
	v_perm_b32 v245, v233, v232, s64
	s_nop 0
	global_store_dwordx4 v92, v[242:245], s[6:7]
	ds_read_b32 v226, v117
	ds_read_b32 v227, v117 offset:512
	ds_read_b32 v228, v117 offset:1024
	ds_read_b32 v229, v117 offset:1536
	ds_read_b32 v230, v117 offset:2048
	ds_read_b32 v231, v117 offset:2560
	ds_read_b32 v232, v117 offset:3072
	ds_read_b32 v233, v117 offset:3584
	s_waitcnt lgkmcnt(0)
	v_bfe_u32 v120, v226, 16, 1
	v_bfe_u32 v121, v227, 16, 1
	v_bfe_u32 v122, v228, 16, 1
	v_bfe_u32 v123, v229, 16, 1
	v_bfe_u32 v124, v230, 16, 1
	v_bfe_u32 v125, v231, 16, 1
	v_bfe_u32 v126, v232, 16, 1
	v_bfe_u32 v127, v233, 16, 1
	v_add3_u32 v226, v226, v120, s63
	v_add3_u32 v227, v227, v121, s63
	v_add3_u32 v228, v228, v122, s63
	v_add3_u32 v229, v229, v123, s63
	v_add3_u32 v230, v230, v124, s63
	v_add3_u32 v231, v231, v125, s63
	v_add3_u32 v232, v232, v126, s63
	v_add3_u32 v233, v233, v127, s63
	v_perm_b32 v242, v227, v226, s64
	v_perm_b32 v243, v229, v228, s64
	v_perm_b32 v244, v231, v230, s64
	v_perm_b32 v245, v233, v232, s64
	s_nop 0
	global_store_dwordx4 v93, v[242:245], s[6:7]
	ds_read_b32 v226, v119
	ds_read_b32 v227, v119 offset:512
	ds_read_b32 v228, v119 offset:1024
	ds_read_b32 v229, v119 offset:1536
	ds_read_b32 v230, v119 offset:2048
	ds_read_b32 v231, v119 offset:2560
	ds_read_b32 v232, v119 offset:3072
	ds_read_b32 v233, v119 offset:3584
	s_waitcnt lgkmcnt(0)
	v_bfe_u32 v120, v226, 16, 1
	v_bfe_u32 v121, v227, 16, 1
	v_bfe_u32 v122, v228, 16, 1
	v_bfe_u32 v123, v229, 16, 1
	v_bfe_u32 v124, v230, 16, 1
	v_bfe_u32 v125, v231, 16, 1
	v_bfe_u32 v126, v232, 16, 1
	v_bfe_u32 v127, v233, 16, 1
	v_add3_u32 v226, v226, v120, s63
	v_add3_u32 v227, v227, v121, s63
	v_add3_u32 v228, v228, v122, s63
	v_add3_u32 v229, v229, v123, s63
	v_add3_u32 v230, v230, v124, s63
	v_add3_u32 v231, v231, v125, s63
	v_add3_u32 v232, v232, v126, s63
	v_add3_u32 v233, v233, v127, s63
	v_perm_b32 v242, v227, v226, s64
	v_perm_b32 v243, v229, v228, s64
	v_perm_b32 v244, v231, v230, s64
	v_perm_b32 v245, v233, v232, s64
	s_nop 0
	global_store_dwordx4 v94, v[242:245], s[6:7]
	s_waitcnt vmcnt(16)
	v_mul_f32_e32 v144, v42, v144
	v_mul_f32_e32 v145, v42, v145
	v_mul_f32_e32 v146, v42, v146
	v_mul_f32_e32 v147, v42, v147
	ds_write_b128 v209, v[144:147]
	v_mul_f32_e32 v148, v43, v148
	v_mul_f32_e32 v149, v43, v149
	v_mul_f32_e32 v150, v43, v150
	v_mul_f32_e32 v151, v43, v151
	ds_write_b128 v209, v[148:151] offset:1024
	v_mul_f32_e32 v152, v44, v152
	v_mul_f32_e32 v153, v44, v153
	v_mul_f32_e32 v154, v44, v154
	v_mul_f32_e32 v155, v44, v155
	ds_write_b128 v209, v[152:155] offset:2048
	v_mul_f32_e32 v156, v45, v156
	v_mul_f32_e32 v157, v45, v157
	v_mul_f32_e32 v158, v45, v158
	v_mul_f32_e32 v159, v45, v159
	ds_write_b128 v209, v[156:159] offset:3072
	v_mul_f32_e32 v160, v46, v160
	v_mul_f32_e32 v161, v46, v161
	v_mul_f32_e32 v162, v46, v162
	v_mul_f32_e32 v163, v46, v163
	ds_write_b128 v209, v[160:163] offset:4096
	v_mul_f32_e32 v164, v47, v164
	v_mul_f32_e32 v165, v47, v165
	v_mul_f32_e32 v166, v47, v166
	v_mul_f32_e32 v167, v47, v167
	ds_write_b128 v209, v[164:167] offset:5120
	v_mul_f32_e32 v168, v48, v168
	v_mul_f32_e32 v169, v48, v169
	v_mul_f32_e32 v170, v48, v170
	v_mul_f32_e32 v171, v48, v171
	ds_write_b128 v209, v[168:171] offset:6144
	v_mul_f32_e32 v172, v49, v172
	v_mul_f32_e32 v173, v49, v173
	v_mul_f32_e32 v174, v49, v174
	v_mul_f32_e32 v175, v49, v175
	ds_write_b128 v209, v[172:175] offset:7168
	s_waitcnt lgkmcnt(0)
	s_barrier
; #define GAS __attribute__((address_space(1)))
; #define LAS __attribute__((address_space(3)))
; #define LDS_WAIT() asm volatile("s_waitcnt lgkmcnt(0)" ::: "memory")
; __device__ __forceinline__ unsigned pk2(float lo, float hi) { return f2bf(lo) | (f2bf(hi) << 16); }
; __device__ __forceinline__ int nat_dim(int p) { return (p >> 1) + 64 * (p & 1); }
; __device__ __forceinline__ int src_col_in(int c) {
;     if (c < 5120) { const int blk = c >> 7, p = c & 127; const bool rope = blk < 16 || ((((blk - 16) >> 2) & 1) == 0); const int d = rope ? (p >> 1) + 64 * (p & 1) : p; return blk * 128 + d; }
;     if (c < OFF_Z) return c + 2096;
;     if (c < OFF_G) return c - 4048;
;     if (c < OFF_DT) return 5120 + (c - OFF_G);
;     if (c < NSRC) return c;
;     return -1;
; }
; template <int MAP, bool KS, bool KPERM = false>
; __device__ __forceinline__ void p0_transpose_item(const float* W, int K, int Nsrc, int nblk, bf16* WT, const float* ksA, const float* ksB, int ksplit, LAS float* scr, int item, int lane) {
;     const int kb = item / nblk, nb = item % nblk, k0 = 64 * kb, n0 = 32 * nb;
;     const int nr = n0 + (lane & 31); const int sc = MAP == 1 ? src_col_in(nr) : (MAP == 2 ? nat_dim(nr) : nr);
;     float v[32];
; #pragma unroll
;     for (int i = 0; i < 32; ++i) { const int k = k0 + 2 * i + (lane >> 5); const int ksrc = KPERM ? ((k & ~127) + nat_dim(k & 127)) : k;
;         v[i] = sc >= 0 ? W[(size_t)ksrc * Nsrc + sc] : 0.f; }
; #pragma unroll
;     for (int i = 0; i < 32; ++i) { const int kk = 2 * i + (lane >> 5); const int k = k0 + kk;
;         if (KS) v[i] *= (k < ksplit ? ksA[k] : ksB[k - ksplit]);
;         scr[kk * 33 + (lane & 31)] = v[i]; }
;     LDS_WAIT(); asm volatile("" ::: "memory");
;     const int c = lane & 7;
; #pragma unroll
;     for (int j = 0; j < 4; ++j) { const int n = (lane >> 3) + 8 * j; const LAS float* s = scr + (8 * c) * 33 + n;
;         v4u o; o.x = pk2(s[0 * 33], s[1 * 33]); o.y = pk2(s[2 * 33], s[3 * 33]); o.z = pk2(s[4 * 33], s[5 * 33]); o.w = pk2(s[6 * 33], s[7 * 33]);
;         *(GAS v4u*)(WT + (size_t)(n0 + n) * K + k0 + 8 * c) = o; }
;     LDS_WAIT(); asm volatile("" ::: "memory");
; }
	s_add_i32 s24, s23, 8
	s_lshl_b32 s20, s24, 7
	s_cmp_lt_u32 s24, 40
	s_cselect_b32 s21, 0, 0x830
	s_cmp_lt_u32 s24, 72
	s_cselect_b32 s21, s21, 0xfffff030
	s_add_i32 s20, s20, s21
	s_lshl_b32 s20, s20, 2
	s_add_u32 s8, s50, s20
	s_addc_u32 s9, s51, 0
	global_load_dwordx4 v[144:147], v76, s[8:9]
	s_add_u32 s8, s8, 0x16280
	s_addc_u32 s9, s9, 0
	global_load_dwordx4 v[148:151], v76, s[8:9]
	s_add_u32 s8, s8, 0x16280
	s_addc_u32 s9, s9, 0
	global_load_dwordx4 v[152:155], v76, s[8:9]
	s_add_u32 s8, s8, 0x16280
	s_addc_u32 s9, s9, 0
	global_load_dwordx4 v[156:159], v76, s[8:9]
	s_add_u32 s8, s8, 0x16280
	s_addc_u32 s9, s9, 0
	global_load_dwordx4 v[160:163], v76, s[8:9]
	s_add_u32 s8, s8, 0x16280
	s_addc_u32 s9, s9, 0
	global_load_dwordx4 v[164:167], v76, s[8:9]
	s_add_u32 s8, s8, 0x16280
	s_addc_u32 s9, s9, 0
	global_load_dwordx4 v[168:171], v76, s[8:9]
	s_add_u32 s8, s8, 0x16280
	s_addc_u32 s9, s9, 0
	global_load_dwordx4 v[172:175], v76, s[8:9]
	s_add_i32 s24, s23, 80
	s_mul_i32 s20, s24, 0x100000
	s_add_u32 s6, s48, s20
	s_addc_u32 s7, s49, 0
	s_cmp_lt_u32 s24, 16
	s_cselect_b32 s20, 1, 0
	s_sub_i32 s21, s24, 16
	s_bitcmp0_b32 s21, 2
	s_cselect_b32 s21, 1, 0
	s_cmp_lt_u32 s24, 40
	s_cselect_b32 s21, s21, 0
	s_or_b32 s20, s20, s21
	s_cmp_lg_u32 s20, 0
	s_cselect_b64 s[20:21], -1, 0
	v_cndmask_b32_e64 v91, v83, v87, s[20:21]
	v_cndmask_b32_e64 v92, v84, v88, s[20:21]
	v_cndmask_b32_e64 v93, v85, v89, s[20:21]
	v_cndmask_b32_e64 v94, v86, v90, s[20:21]
	ds_read_b32 v226, v112
	ds_read_b32 v227, v112 offset:512
	ds_read_b32 v228, v112 offset:1024
	ds_read_b32 v229, v112 offset:1536
	ds_read_b32 v230, v112 offset:2048
	ds_read_b32 v231, v112 offset:2560
	ds_read_b32 v232, v112 offset:3072
	ds_read_b32 v233, v112 offset:3584
	s_waitcnt lgkmcnt(0)
	v_bfe_u32 v120, v226, 16, 1
	v_bfe_u32 v121, v227, 16, 1
	v_bfe_u32 v122, v228, 16, 1
	v_bfe_u32 v123, v229, 16, 1
	v_bfe_u32 v124, v230, 16, 1
	v_bfe_u32 v125, v231, 16, 1
	v_bfe_u32 v126, v232, 16, 1
	v_bfe_u32 v127, v233, 16, 1
	v_add3_u32 v226, v226, v120, s63
	v_add3_u32 v227, v227, v121, s63
	v_add3_u32 v228, v228, v122, s63
	v_add3_u32 v229, v229, v123, s63
	v_add3_u32 v230, v230, v124, s63
	v_add3_u32 v231, v231, v125, s63
	v_add3_u32 v232, v232, v126, s63
	v_add3_u32 v233, v233, v127, s63
	v_perm_b32 v242, v227, v226, s64
	v_perm_b32 v243, v229, v228, s64
	v_perm_b32 v244, v231, v230, s64
	v_perm_b32 v245, v233, v232, s64
	s_nop 0
	global_store_dwordx4 v91, v[242:245], s[6:7]
	ds_read_b32 v226, v114
	ds_read_b32 v227, v114 offset:512
	ds_read_b32 v228, v114 offset:1024
	ds_read_b32 v229, v114 offset:1536
	ds_read_b32 v230, v114 offset:2048
	ds_read_b32 v231, v114 offset:2560
	ds_read_b32 v232, v114 offset:3072
	ds_read_b32 v233, v114 offset:3584
	s_waitcnt lgkmcnt(0)
	v_bfe_u32 v120, v226, 16, 1
	v_bfe_u32 v121, v227, 16, 1
	v_bfe_u32 v122, v228, 16, 1
	v_bfe_u32 v123, v229, 16, 1
	v_bfe_u32 v124, v230, 16, 1
	v_bfe_u32 v125, v231, 16, 1
	v_bfe_u32 v126, v232, 16, 1
	v_bfe_u32 v127, v233, 16, 1
	v_add3_u32 v226, v226, v120, s63
	v_add3_u32 v227, v227, v121, s63
	v_add3_u32 v228, v228, v122, s63
	v_add3_u32 v229, v229, v123, s63
	v_add3_u32 v230, v230, v124, s63
	v_add3_u32 v231, v231, v125, s63
	v_add3_u32 v232, v232, v126, s63
	v_add3_u32 v233, v233, v127, s63
	v_perm_b32 v242, v227, v226, s64
	v_perm_b32 v243, v229, v228, s64
	v_perm_b32 v244, v231, v230, s64
	v_perm_b32 v245, v233, v232, s64
	s_nop 0
	global_store_dwordx4 v92, v[242:245], s[6:7]
	ds_read_b32 v226, v116
	ds_read_b32 v227, v116 offset:512
	ds_read_b32 v228, v116 offset:1024
	ds_read_b32 v229, v116 offset:1536
	ds_read_b32 v230, v116 offset:2048
	ds_read_b32 v231, v116 offset:2560
	ds_read_b32 v232, v116 offset:3072
	ds_read_b32 v233, v116 offset:3584
	s_waitcnt lgkmcnt(0)
	v_bfe_u32 v120, v226, 16, 1
	v_bfe_u32 v121, v227, 16, 1
	v_bfe_u32 v122, v228, 16, 1
	v_bfe_u32 v123, v229, 16, 1
	v_bfe_u32 v124, v230, 16, 1
	v_bfe_u32 v125, v231, 16, 1
	v_bfe_u32 v126, v232, 16, 1
	v_bfe_u32 v127, v233, 16, 1
	v_add3_u32 v226, v226, v120, s63
	v_add3_u32 v227, v227, v121, s63
	v_add3_u32 v228, v228, v122, s63
	v_add3_u32 v229, v229, v123, s63
	v_add3_u32 v230, v230, v124, s63
	v_add3_u32 v231, v231, v125, s63
	v_add3_u32 v232, v232, v126, s63
	v_add3_u32 v233, v233, v127, s63
	v_perm_b32 v242, v227, v226, s64
	v_perm_b32 v243, v229, v228, s64
	v_perm_b32 v244, v231, v230, s64
	v_perm_b32 v245, v233, v232, s64
	s_nop 0
	global_store_dwordx4 v93, v[242:245], s[6:7]
	ds_read_b32 v226, v118
	ds_read_b32 v227, v118 offset:512
	ds_read_b32 v228, v118 offset:1024
	ds_read_b32 v229, v118 offset:1536
	ds_read_b32 v230, v118 offset:2048
	ds_read_b32 v231, v118 offset:2560
	ds_read_b32 v232, v118 offset:3072
	ds_read_b32 v233, v118 offset:3584
	s_waitcnt lgkmcnt(0)
	v_bfe_u32 v120, v226, 16, 1
	v_bfe_u32 v121, v227, 16, 1
	v_bfe_u32 v122, v228, 16, 1
	v_bfe_u32 v123, v229, 16, 1
	v_bfe_u32 v124, v230, 16, 1
	v_bfe_u32 v125, v231, 16, 1
	v_bfe_u32 v126, v232, 16, 1
	v_bfe_u32 v127, v233, 16, 1
	v_add3_u32 v226, v226, v120, s63
	v_add3_u32 v227, v227, v121, s63
	v_add3_u32 v228, v228, v122, s63
	v_add3_u32 v229, v229, v123, s63
	v_add3_u32 v230, v230, v124, s63
	v_add3_u32 v231, v231, v125, s63
	v_add3_u32 v232, v232, v126, s63
	v_add3_u32 v233, v233, v127, s63
	v_perm_b32 v242, v227, v226, s64
	v_perm_b32 v243, v229, v228, s64
	v_perm_b32 v244, v231, v230, s64
	v_perm_b32 v245, v233, v232, s64
	s_nop 0
	global_store_dwordx4 v94, v[242:245], s[6:7]
	s_waitcnt vmcnt(16)
	v_mul_f32_e32 v176, v50, v176
	v_mul_f32_e32 v177, v50, v177
	v_mul_f32_e32 v178, v50, v178
	v_mul_f32_e32 v179, v50, v179
	ds_write_b128 v210, v[176:179]
	v_mul_f32_e32 v180, v51, v180
	v_mul_f32_e32 v181, v51, v181
	v_mul_f32_e32 v182, v51, v182
	v_mul_f32_e32 v183, v51, v183
	ds_write_b128 v210, v[180:183] offset:1024
	v_mul_f32_e32 v184, v52, v184
	v_mul_f32_e32 v185, v52, v185
	v_mul_f32_e32 v186, v52, v186
	v_mul_f32_e32 v187, v52, v187
	ds_write_b128 v210, v[184:187] offset:2048
	v_mul_f32_e32 v188, v53, v188
	v_mul_f32_e32 v189, v53, v189
	v_mul_f32_e32 v190, v53, v190
	v_mul_f32_e32 v191, v53, v191
	ds_write_b128 v210, v[188:191] offset:3072
	v_mul_f32_e32 v192, v54, v192
	v_mul_f32_e32 v193, v54, v193
	v_mul_f32_e32 v194, v54, v194
	v_mul_f32_e32 v195, v54, v195
	ds_write_b128 v210, v[192:195] offset:4096
	v_mul_f32_e32 v196, v55, v196
	v_mul_f32_e32 v197, v55, v197
	v_mul_f32_e32 v198, v55, v198
	v_mul_f32_e32 v199, v55, v199
	ds_write_b128 v210, v[196:199] offset:5120
	v_mul_f32_e32 v200, v56, v200
	v_mul_f32_e32 v201, v56, v201
	v_mul_f32_e32 v202, v56, v202
	v_mul_f32_e32 v203, v56, v203
	ds_write_b128 v210, v[200:203] offset:6144
	v_mul_f32_e32 v204, v57, v204
	v_mul_f32_e32 v205, v57, v205
	v_mul_f32_e32 v206, v57, v206
	v_mul_f32_e32 v207, v57, v207
	ds_write_b128 v210, v[204:207] offset:7168
	s_waitcnt lgkmcnt(0)
	s_barrier
; #define GAS __attribute__((address_space(1)))
; #define LAS __attribute__((address_space(3)))
; #define LDS_WAIT() asm volatile("s_waitcnt lgkmcnt(0)" ::: "memory")
; __device__ __forceinline__ int src_col_in(int c) {
;     if (c < 5120) { const int blk = c >> 7, p = c & 127; const bool rope = blk < 16 || ((((blk - 16) >> 2) & 1) == 0); const int d = rope ? (p >> 1) + 64 * (p & 1) : p; return blk * 128 + d; }
;     if (c < OFF_Z) return c + 2096;
;     if (c < OFF_G) return c - 4048;
;     if (c < OFF_DT) return 5120 + (c - OFF_G);
;     if (c < NSRC) return c;
;     return -1;
; }
;     const int pr = item >> 1, kb = 2 * (pr / nblk) + (item & 1), nb = pr % nblk, k0 = 64 * kb, n0 = 32 * nb;
;     const int nr = n0 + (lane & 31); const int sc = MAP == 1 ? src_col_in(nr) : nr;
;     float v[32];
; #pragma unroll
;     for (int i = 0; i < 32; ++i) v[i] = sc >= 0 ? W[(size_t)(k0 + 2 * i + (lane >> 5)) * Nsrc + sc] : 0.f;
; #pragma unroll
;     for (int i = 0; i < 32; ++i) { const int k = k0 + 2 * i + (lane >> 5); float x = v[i] * wscale; if (KS) x *= (k < ksplit ? ksA[k] : ksB[k - ksplit]); scr[(2 * i + (lane >> 5)) * 33 + (lane & 31)] = x; }
;     LDS_WAIT(); asm volatile("" ::: "memory");
;     const int c = lane & 7;
; #pragma unroll
;     for (int j = 0; j < 4; ++j) { const int n = (lane >> 3) + 8 * j; const LAS float* s = scr + (8 * c) * 33 + n;
;         const unsigned long long o = (unsigned long long)pg8::pk4_fp8(s[0 * 33], s[1 * 33], s[2 * 33], s[3 * 33]) | ((unsigned long long)pg8::pk4_fp8(s[4 * 33], s[5 * 33], s[6 * 33], s[7 * 33]) << 32);
;         *(GAS unsigned long long*)(WT + (size_t)(n0 + n) * K + k0 + 8 * c) = o; }
;     LDS_WAIT(); asm volatile("" ::: "memory");
; }
	s_add_i32 s24, s23, 16
	s_lshl_b32 s20, s24, 7
	s_cmp_lt_u32 s24, 40
	s_cselect_b32 s21, 0, 0x830
	s_cmp_lt_u32 s24, 72
	s_cselect_b32 s21, s21, 0xfffff030
	s_add_i32 s20, s20, s21
	s_lshl_b32 s20, s20, 2
	s_add_u32 s8, s50, s20
	s_addc_u32 s9, s51, 0
	global_load_dwordx4 v[176:179], v76, s[8:9]
	s_add_u32 s8, s8, 0x16280
	s_addc_u32 s9, s9, 0
	global_load_dwordx4 v[180:183], v76, s[8:9]
	s_add_u32 s8, s8, 0x16280
	s_addc_u32 s9, s9, 0
	global_load_dwordx4 v[184:187], v76, s[8:9]
	s_add_u32 s8, s8, 0x16280
	s_addc_u32 s9, s9, 0
	global_load_dwordx4 v[188:191], v76, s[8:9]
	s_add_u32 s8, s8, 0x16280
	s_addc_u32 s9, s9, 0
	global_load_dwordx4 v[192:195], v76, s[8:9]
	s_add_u32 s8, s8, 0x16280
	s_addc_u32 s9, s9, 0
	global_load_dwordx4 v[196:199], v76, s[8:9]
	s_add_u32 s8, s8, 0x16280
	s_addc_u32 s9, s9, 0
	global_load_dwordx4 v[200:203], v76, s[8:9]
	s_add_u32 s8, s8, 0x16280
	s_addc_u32 s9, s9, 0
	global_load_dwordx4 v[204:207], v76, s[8:9]
	s_add_i32 s24, s23, 0
	s_mul_i32 s20, s24, 0x80000
	s_add_u32 s6, s52, s20
	s_addc_u32 s7, s53, 0
	s_cmp_lt_u32 s24, 16
	s_cselect_b32 s20, 1, 0
	s_sub_i32 s21, s24, 16
	s_bitcmp0_b32 s21, 2
	s_cselect_b32 s21, 1, 0
	s_cmp_lt_u32 s24, 40
	s_cselect_b32 s21, s21, 0
	s_or_b32 s20, s20, s21
	s_cmp_lg_u32 s20, 0
	s_cselect_b64 s[20:21], -1, 0
	v_cndmask_b32_e64 v91, v77, v81, s[20:21]
	v_cndmask_b32_e64 v92, v78, v82, s[20:21]
	ds_read_b32 v226, v212
	ds_read_b32 v227, v212 offset:512
	ds_read_b32 v228, v212 offset:1024
	ds_read_b32 v229, v212 offset:1536
	ds_read_b32 v230, v212 offset:2048
	ds_read_b32 v231, v212 offset:2560
	ds_read_b32 v232, v212 offset:3072
	ds_read_b32 v233, v212 offset:3584
	ds_read_b32 v234, v212 offset:4096
	ds_read_b32 v235, v212 offset:4608
	ds_read_b32 v236, v212 offset:5120
	ds_read_b32 v237, v212 offset:5632
	ds_read_b32 v238, v212 offset:6144
	ds_read_b32 v239, v212 offset:6656
	ds_read_b32 v240, v212 offset:7168
	ds_read_b32 v241, v212 offset:7680
	s_waitcnt lgkmcnt(0)
	v_max_f32_e32 v226, v226, v226
	v_max_f32_e32 v227, v227, v227
	v_max_f32_e32 v228, v228, v228
	v_max_f32_e32 v229, v229, v229
	v_max_f32_e32 v230, v230, v230
	v_max_f32_e32 v231, v231, v231
	v_max_f32_e32 v232, v232, v232
	v_max_f32_e32 v233, v233, v233
	v_max_f32_e32 v234, v234, v234
	v_max_f32_e32 v235, v235, v235
	v_max_f32_e32 v236, v236, v236
	v_max_f32_e32 v237, v237, v237
	v_max_f32_e32 v238, v238, v238
	v_max_f32_e32 v239, v239, v239
	v_max_f32_e32 v240, v240, v240
	v_max_f32_e32 v241, v241, v241
	v_med3_f32 v226, v226, s62, v95
	v_med3_f32 v227, v227, s62, v95
	v_med3_f32 v228, v228, s62, v95
	v_med3_f32 v229, v229, s62, v95
	v_med3_f32 v230, v230, s62, v95
	v_med3_f32 v231, v231, s62, v95
	v_med3_f32 v232, v232, s62, v95
	v_med3_f32 v233, v233, s62, v95
	v_med3_f32 v234, v234, s62, v95
	v_med3_f32 v235, v235, s62, v95
	v_med3_f32 v236, v236, s62, v95
	v_med3_f32 v237, v237, s62, v95
	v_med3_f32 v238, v238, s62, v95
	v_med3_f32 v239, v239, s62, v95
	v_med3_f32 v240, v240, s62, v95
	v_med3_f32 v241, v241, s62, v95
	v_mov_b32_e32 v242, 0
	v_mov_b32_e32 v243, 0
	v_mov_b32_e32 v244, 0
	v_mov_b32_e32 v245, 0
	v_cvt_pk_fp8_f32 v242, v226, v227
	v_cvt_pk_fp8_f32 v243, v230, v231
	v_cvt_pk_fp8_f32 v244, v234, v235
	v_cvt_pk_fp8_f32 v245, v238, v239
	v_cvt_pk_fp8_f32 v242, v228, v229 op_sel:[0,0,1]
	v_cvt_pk_fp8_f32 v243, v232, v233 op_sel:[0,0,1]
	v_cvt_pk_fp8_f32 v244, v236, v237 op_sel:[0,0,1]
	v_cvt_pk_fp8_f32 v245, v240, v241 op_sel:[0,0,1]
	s_nop 0
	global_store_dwordx4 v91, v[242:245], s[6:7]
	ds_read_b32 v226, v214
	ds_read_b32 v227, v214 offset:512
	ds_read_b32 v228, v214 offset:1024
	ds_read_b32 v229, v214 offset:1536
	ds_read_b32 v230, v214 offset:2048
	ds_read_b32 v231, v214 offset:2560
	ds_read_b32 v232, v214 offset:3072
	ds_read_b32 v233, v214 offset:3584
	ds_read_b32 v234, v214 offset:4096
	ds_read_b32 v235, v214 offset:4608
	ds_read_b32 v236, v214 offset:5120
	ds_read_b32 v237, v214 offset:5632
	ds_read_b32 v238, v214 offset:6144
	ds_read_b32 v239, v214 offset:6656
	ds_read_b32 v240, v214 offset:7168
	ds_read_b32 v241, v214 offset:7680
	s_waitcnt lgkmcnt(0)
	v_max_f32_e32 v226, v226, v226
	v_max_f32_e32 v227, v227, v227
	v_max_f32_e32 v228, v228, v228
	v_max_f32_e32 v229, v229, v229
	v_max_f32_e32 v230, v230, v230
	v_max_f32_e32 v231, v231, v231
	v_max_f32_e32 v232, v232, v232
	v_max_f32_e32 v233, v233, v233
	v_max_f32_e32 v234, v234, v234
	v_max_f32_e32 v235, v235, v235
	v_max_f32_e32 v236, v236, v236
	v_max_f32_e32 v237, v237, v237
	v_max_f32_e32 v238, v238, v238
	v_max_f32_e32 v239, v239, v239
	v_max_f32_e32 v240, v240, v240
	v_max_f32_e32 v241, v241, v241
	v_med3_f32 v226, v226, s62, v95
	v_med3_f32 v227, v227, s62, v95
	v_med3_f32 v228, v228, s62, v95
	v_med3_f32 v229, v229, s62, v95
	v_med3_f32 v230, v230, s62, v95
	v_med3_f32 v231, v231, s62, v95
	v_med3_f32 v232, v232, s62, v95
	v_med3_f32 v233, v233, s62, v95
	v_med3_f32 v234, v234, s62, v95
	v_med3_f32 v235, v235, s62, v95
	v_med3_f32 v236, v236, s62, v95
	v_med3_f32 v237, v237, s62, v95
	v_med3_f32 v238, v238, s62, v95
	v_med3_f32 v239, v239, s62, v95
	v_med3_f32 v240, v240, s62, v95
	v_med3_f32 v241, v241, s62, v95
	v_mov_b32_e32 v242, 0
	v_mov_b32_e32 v243, 0
	v_mov_b32_e32 v244, 0
	v_mov_b32_e32 v245, 0
	v_cvt_pk_fp8_f32 v242, v226, v227
	v_cvt_pk_fp8_f32 v243, v230, v231
	v_cvt_pk_fp8_f32 v244, v234, v235
	v_cvt_pk_fp8_f32 v245, v238, v239
	v_cvt_pk_fp8_f32 v242, v228, v229 op_sel:[0,0,1]
	v_cvt_pk_fp8_f32 v243, v232, v233 op_sel:[0,0,1]
	v_cvt_pk_fp8_f32 v244, v236, v237 op_sel:[0,0,1]
	v_cvt_pk_fp8_f32 v245, v240, v241 op_sel:[0,0,1]
	s_nop 0
	global_store_dwordx4 v92, v[242:245], s[6:7]
	s_waitcnt vmcnt(14)
	v_mul_f32_e32 v144, v50, v144
	v_mul_f32_e32 v145, v50, v145
	v_mul_f32_e32 v146, v50, v146
	v_mul_f32_e32 v147, v50, v147
	ds_write_b128 v209, v[144:147]
	v_mul_f32_e32 v148, v51, v148
	v_mul_f32_e32 v149, v51, v149
	v_mul_f32_e32 v150, v51, v150
	v_mul_f32_e32 v151, v51, v151
	ds_write_b128 v209, v[148:151] offset:1024
	v_mul_f32_e32 v152, v52, v152
	v_mul_f32_e32 v153, v52, v153
	v_mul_f32_e32 v154, v52, v154
	v_mul_f32_e32 v155, v52, v155
	ds_write_b128 v209, v[152:155] offset:2048
	v_mul_f32_e32 v156, v53, v156
	v_mul_f32_e32 v157, v53, v157
	v_mul_f32_e32 v158, v53, v158
	v_mul_f32_e32 v159, v53, v159
	ds_write_b128 v209, v[156:159] offset:3072
	v_mul_f32_e32 v160, v54, v160
	v_mul_f32_e32 v161, v54, v161
	v_mul_f32_e32 v162, v54, v162
	v_mul_f32_e32 v163, v54, v163
	ds_write_b128 v209, v[160:163] offset:4096
	v_mul_f32_e32 v164, v55, v164
	v_mul_f32_e32 v165, v55, v165
	v_mul_f32_e32 v166, v55, v166
	v_mul_f32_e32 v167, v55, v167
	ds_write_b128 v209, v[164:167] offset:5120
	v_mul_f32_e32 v168, v56, v168
	v_mul_f32_e32 v169, v56, v169
	v_mul_f32_e32 v170, v56, v170
	v_mul_f32_e32 v171, v56, v171
	ds_write_b128 v209, v[168:171] offset:6144
	v_mul_f32_e32 v172, v57, v172
	v_mul_f32_e32 v173, v57, v173
	v_mul_f32_e32 v174, v57, v174
	v_mul_f32_e32 v175, v57, v175
	ds_write_b128 v209, v[172:175] offset:7168
	s_waitcnt lgkmcnt(0)
	s_barrier
; #define GAS __attribute__((address_space(1)))
; #define LAS __attribute__((address_space(3)))
; #define LDS_WAIT() asm volatile("s_waitcnt lgkmcnt(0)" ::: "memory")
; __device__ __forceinline__ int src_col_in(int c) {
;     if (c < 5120) { const int blk = c >> 7, p = c & 127; const bool rope = blk < 16 || ((((blk - 16) >> 2) & 1) == 0); const int d = rope ? (p >> 1) + 64 * (p & 1) : p; return blk * 128 + d; }
;     if (c < OFF_Z) return c + 2096;
;     if (c < OFF_G) return c - 4048;
;     if (c < OFF_DT) return 5120 + (c - OFF_G);
;     if (c < NSRC) return c;
;     return -1;
; }
;     const int pr = item >> 1, kb = 2 * (pr / nblk) + (item & 1), nb = pr % nblk, k0 = 64 * kb, n0 = 32 * nb;
;     const int nr = n0 + (lane & 31); const int sc = MAP == 1 ? src_col_in(nr) : nr;
;     float v[32];
; #pragma unroll
;     for (int i = 0; i < 32; ++i) v[i] = sc >= 0 ? W[(size_t)(k0 + 2 * i + (lane >> 5)) * Nsrc + sc] : 0.f;
; #pragma unroll
;     for (int i = 0; i < 32; ++i) { const int k = k0 + 2 * i + (lane >> 5); float x = v[i] * wscale; if (KS) x *= (k < ksplit ? ksA[k] : ksB[k - ksplit]); scr[(2 * i + (lane >> 5)) * 33 + (lane & 31)] = x; }
;     LDS_WAIT(); asm volatile("" ::: "memory");
;     const int c = lane & 7;
; #pragma unroll
;     for (int j = 0; j < 4; ++j) { const int n = (lane >> 3) + 8 * j; const LAS float* s = scr + (8 * c) * 33 + n;
;         const unsigned long long o = (unsigned long long)pg8::pk4_fp8(s[0 * 33], s[1 * 33], s[2 * 33], s[3 * 33]) | ((unsigned long long)pg8::pk4_fp8(s[4 * 33], s[5 * 33], s[6 * 33], s[7 * 33]) << 32);
;         *(GAS unsigned long long*)(WT + (size_t)(n0 + n) * K + k0 + 8 * c) = o; }
;     LDS_WAIT(); asm volatile("" ::: "memory");
; }
	s_add_i32 s24, s23, 24
	s_lshl_b32 s20, s24, 7
	s_cmp_lt_u32 s24, 40
	s_cselect_b32 s21, 0, 0x830
	s_cmp_lt_u32 s24, 72
	s_cselect_b32 s21, s21, 0xfffff030
	s_add_i32 s20, s20, s21
	s_lshl_b32 s20, s20, 2
	s_add_u32 s8, s50, s20
	s_addc_u32 s9, s51, 0
	global_load_dwordx4 v[144:147], v76, s[8:9]
	s_add_u32 s8, s8, 0x16280
	s_addc_u32 s9, s9, 0
	global_load_dwordx4 v[148:151], v76, s[8:9]
	s_add_u32 s8, s8, 0x16280
	s_addc_u32 s9, s9, 0
	global_load_dwordx4 v[152:155], v76, s[8:9]
	s_add_u32 s8, s8, 0x16280
	s_addc_u32 s9, s9, 0
	global_load_dwordx4 v[156:159], v76, s[8:9]
	s_add_u32 s8, s8, 0x16280
	s_addc_u32 s9, s9, 0
	global_load_dwordx4 v[160:163], v76, s[8:9]
	s_add_u32 s8, s8, 0x16280
	s_addc_u32 s9, s9, 0
	global_load_dwordx4 v[164:167], v76, s[8:9]
	s_add_u32 s8, s8, 0x16280
	s_addc_u32 s9, s9, 0
	global_load_dwordx4 v[168:171], v76, s[8:9]
	s_add_u32 s8, s8, 0x16280
	s_addc_u32 s9, s9, 0
	global_load_dwordx4 v[172:175], v76, s[8:9]
	s_add_i32 s24, s23, 8
	s_mul_i32 s20, s24, 0x80000
	s_add_u32 s6, s52, s20
	s_addc_u32 s7, s53, 0
	s_cmp_lt_u32 s24, 16
	s_cselect_b32 s20, 1, 0
	s_sub_i32 s21, s24, 16
	s_bitcmp0_b32 s21, 2
	s_cselect_b32 s21, 1, 0
	s_cmp_lt_u32 s24, 40
	s_cselect_b32 s21, s21, 0
	s_or_b32 s20, s20, s21
	s_cmp_lg_u32 s20, 0
	s_cselect_b64 s[20:21], -1, 0
	v_cndmask_b32_e64 v91, v77, v81, s[20:21]
	v_cndmask_b32_e64 v92, v78, v82, s[20:21]
	ds_read_b32 v226, v211
	ds_read_b32 v227, v211 offset:512
	ds_read_b32 v228, v211 offset:1024
	ds_read_b32 v229, v211 offset:1536
	ds_read_b32 v230, v211 offset:2048
	ds_read_b32 v231, v211 offset:2560
	ds_read_b32 v232, v211 offset:3072
	ds_read_b32 v233, v211 offset:3584
	ds_read_b32 v234, v211 offset:4096
	ds_read_b32 v235, v211 offset:4608
	ds_read_b32 v236, v211 offset:5120
	ds_read_b32 v237, v211 offset:5632
	ds_read_b32 v238, v211 offset:6144
	ds_read_b32 v239, v211 offset:6656
	ds_read_b32 v240, v211 offset:7168
	ds_read_b32 v241, v211 offset:7680
	s_waitcnt lgkmcnt(0)
	v_max_f32_e32 v226, v226, v226
	v_max_f32_e32 v227, v227, v227
	v_max_f32_e32 v228, v228, v228
	v_max_f32_e32 v229, v229, v229
	v_max_f32_e32 v230, v230, v230
	v_max_f32_e32 v231, v231, v231
	v_max_f32_e32 v232, v232, v232
	v_max_f32_e32 v233, v233, v233
	v_max_f32_e32 v234, v234, v234
	v_max_f32_e32 v235, v235, v235
	v_max_f32_e32 v236, v236, v236
	v_max_f32_e32 v237, v237, v237
	v_max_f32_e32 v238, v238, v238
	v_max_f32_e32 v239, v239, v239
	v_max_f32_e32 v240, v240, v240
	v_max_f32_e32 v241, v241, v241
	v_med3_f32 v226, v226, s62, v95
	v_med3_f32 v227, v227, s62, v95
	v_med3_f32 v228, v228, s62, v95
	v_med3_f32 v229, v229, s62, v95
	v_med3_f32 v230, v230, s62, v95
	v_med3_f32 v231, v231, s62, v95
	v_med3_f32 v232, v232, s62, v95
	v_med3_f32 v233, v233, s62, v95
	v_med3_f32 v234, v234, s62, v95
	v_med3_f32 v235, v235, s62, v95
	v_med3_f32 v236, v236, s62, v95
	v_med3_f32 v237, v237, s62, v95
	v_med3_f32 v238, v238, s62, v95
	v_med3_f32 v239, v239, s62, v95
	v_med3_f32 v240, v240, s62, v95
	v_med3_f32 v241, v241, s62, v95
	v_mov_b32_e32 v242, 0
	v_mov_b32_e32 v243, 0
	v_mov_b32_e32 v244, 0
	v_mov_b32_e32 v245, 0
	v_cvt_pk_fp8_f32 v242, v226, v227
	v_cvt_pk_fp8_f32 v243, v230, v231
	v_cvt_pk_fp8_f32 v244, v234, v235
	v_cvt_pk_fp8_f32 v245, v238, v239
	v_cvt_pk_fp8_f32 v242, v228, v229 op_sel:[0,0,1]
	v_cvt_pk_fp8_f32 v243, v232, v233 op_sel:[0,0,1]
	v_cvt_pk_fp8_f32 v244, v236, v237 op_sel:[0,0,1]
	v_cvt_pk_fp8_f32 v245, v240, v241 op_sel:[0,0,1]
	s_nop 0
	global_store_dwordx4 v91, v[242:245], s[6:7]
	ds_read_b32 v226, v213
	ds_read_b32 v227, v213 offset:512
	ds_read_b32 v228, v213 offset:1024
	ds_read_b32 v229, v213 offset:1536
	ds_read_b32 v230, v213 offset:2048
	ds_read_b32 v231, v213 offset:2560
	ds_read_b32 v232, v213 offset:3072
	ds_read_b32 v233, v213 offset:3584
	ds_read_b32 v234, v213 offset:4096
	ds_read_b32 v235, v213 offset:4608
	ds_read_b32 v236, v213 offset:5120
	ds_read_b32 v237, v213 offset:5632
	ds_read_b32 v238, v213 offset:6144
	ds_read_b32 v239, v213 offset:6656
	ds_read_b32 v240, v213 offset:7168
	ds_read_b32 v241, v213 offset:7680
	s_waitcnt lgkmcnt(0)
	v_max_f32_e32 v226, v226, v226
	v_max_f32_e32 v227, v227, v227
	v_max_f32_e32 v228, v228, v228
	v_max_f32_e32 v229, v229, v229
	v_max_f32_e32 v230, v230, v230
	v_max_f32_e32 v231, v231, v231
	v_max_f32_e32 v232, v232, v232
	v_max_f32_e32 v233, v233, v233
	v_max_f32_e32 v234, v234, v234
	v_max_f32_e32 v235, v235, v235
	v_max_f32_e32 v236, v236, v236
	v_max_f32_e32 v237, v237, v237
	v_max_f32_e32 v238, v238, v238
	v_max_f32_e32 v239, v239, v239
	v_max_f32_e32 v240, v240, v240
	v_max_f32_e32 v241, v241, v241
	v_med3_f32 v226, v226, s62, v95
	v_med3_f32 v227, v227, s62, v95
	v_med3_f32 v228, v228, s62, v95
	v_med3_f32 v229, v229, s62, v95
	v_med3_f32 v230, v230, s62, v95
	v_med3_f32 v231, v231, s62, v95
	v_med3_f32 v232, v232, s62, v95
	v_med3_f32 v233, v233, s62, v95
	v_med3_f32 v234, v234, s62, v95
	v_med3_f32 v235, v235, s62, v95
	v_med3_f32 v236, v236, s62, v95
	v_med3_f32 v237, v237, s62, v95
	v_med3_f32 v238, v238, s62, v95
	v_med3_f32 v239, v239, s62, v95
	v_med3_f32 v240, v240, s62, v95
	v_med3_f32 v241, v241, s62, v95
	v_mov_b32_e32 v242, 0
	v_mov_b32_e32 v243, 0
	v_mov_b32_e32 v244, 0
	v_mov_b32_e32 v245, 0
	v_cvt_pk_fp8_f32 v242, v226, v227
	v_cvt_pk_fp8_f32 v243, v230, v231
	v_cvt_pk_fp8_f32 v244, v234, v235
	v_cvt_pk_fp8_f32 v245, v238, v239
	v_cvt_pk_fp8_f32 v242, v228, v229 op_sel:[0,0,1]
	v_cvt_pk_fp8_f32 v243, v232, v233 op_sel:[0,0,1]
	v_cvt_pk_fp8_f32 v244, v236, v237 op_sel:[0,0,1]
	v_cvt_pk_fp8_f32 v245, v240, v241 op_sel:[0,0,1]
	s_nop 0
	global_store_dwordx4 v92, v[242:245], s[6:7]
	s_waitcnt vmcnt(12)
	v_mul_f32_e32 v176, v50, v176
	v_mul_f32_e32 v177, v50, v177
	v_mul_f32_e32 v178, v50, v178
	v_mul_f32_e32 v179, v50, v179
	ds_write_b128 v210, v[176:179]
	v_mul_f32_e32 v180, v51, v180
	v_mul_f32_e32 v181, v51, v181
	v_mul_f32_e32 v182, v51, v182
	v_mul_f32_e32 v183, v51, v183
	ds_write_b128 v210, v[180:183] offset:1024
	v_mul_f32_e32 v184, v52, v184
	v_mul_f32_e32 v185, v52, v185
	v_mul_f32_e32 v186, v52, v186
	v_mul_f32_e32 v187, v52, v187
	ds_write_b128 v210, v[184:187] offset:2048
	v_mul_f32_e32 v188, v53, v188
	v_mul_f32_e32 v189, v53, v189
	v_mul_f32_e32 v190, v53, v190
	v_mul_f32_e32 v191, v53, v191
	ds_write_b128 v210, v[188:191] offset:3072
	v_mul_f32_e32 v192, v54, v192
	v_mul_f32_e32 v193, v54, v193
	v_mul_f32_e32 v194, v54, v194
	v_mul_f32_e32 v195, v54, v195
	ds_write_b128 v210, v[192:195] offset:4096
	v_mul_f32_e32 v196, v55, v196
	v_mul_f32_e32 v197, v55, v197
	v_mul_f32_e32 v198, v55, v198
	v_mul_f32_e32 v199, v55, v199
	ds_write_b128 v210, v[196:199] offset:5120
	v_mul_f32_e32 v200, v56, v200
	v_mul_f32_e32 v201, v56, v201
	v_mul_f32_e32 v202, v56, v202
	v_mul_f32_e32 v203, v56, v203
	ds_write_b128 v210, v[200:203] offset:6144
	v_mul_f32_e32 v204, v57, v204
	v_mul_f32_e32 v205, v57, v205
	v_mul_f32_e32 v206, v57, v206
	v_mul_f32_e32 v207, v57, v207
	ds_write_b128 v210, v[204:207] offset:7168
	s_waitcnt lgkmcnt(0)
	s_barrier
; #define GAS __attribute__((address_space(1)))
; #define LAS __attribute__((address_space(3)))
; #define LDS_WAIT() asm volatile("s_waitcnt lgkmcnt(0)" ::: "memory")
; __device__ __forceinline__ int src_col_in(int c) {
;     if (c < 5120) { const int blk = c >> 7, p = c & 127; const bool rope = blk < 16 || ((((blk - 16) >> 2) & 1) == 0); const int d = rope ? (p >> 1) + 64 * (p & 1) : p; return blk * 128 + d; }
;     if (c < OFF_Z) return c + 2096;
;     if (c < OFF_G) return c - 4048;
;     if (c < OFF_DT) return 5120 + (c - OFF_G);
;     if (c < NSRC) return c;
;     return -1;
; }
;     const int pr = item >> 1, kb = 2 * (pr / nblk) + (item & 1), nb = pr % nblk, k0 = 64 * kb, n0 = 32 * nb;
;     const int nr = n0 + (lane & 31); const int sc = MAP == 1 ? src_col_in(nr) : nr;
;     float v[32];
; #pragma unroll
;     for (int i = 0; i < 32; ++i) v[i] = sc >= 0 ? W[(size_t)(k0 + 2 * i + (lane >> 5)) * Nsrc + sc] : 0.f;
; #pragma unroll
;     for (int i = 0; i < 32; ++i) { const int k = k0 + 2 * i + (lane >> 5); float x = v[i] * wscale; if (KS) x *= (k < ksplit ? ksA[k] : ksB[k - ksplit]); scr[(2 * i + (lane >> 5)) * 33 + (lane & 31)] = x; }
;     LDS_WAIT(); asm volatile("" ::: "memory");
;     const int c = lane & 7;
; #pragma unroll
;     for (int j = 0; j < 4; ++j) { const int n = (lane >> 3) + 8 * j; const LAS float* s = scr + (8 * c) * 33 + n;
;         const unsigned long long o = (unsigned long long)pg8::pk4_fp8(s[0 * 33], s[1 * 33], s[2 * 33], s[3 * 33]) | ((unsigned long long)pg8::pk4_fp8(s[4 * 33], s[5 * 33], s[6 * 33], s[7 * 33]) << 32);
;         *(GAS unsigned long long*)(WT + (size_t)(n0 + n) * K + k0 + 8 * c) = o; }
;     LDS_WAIT(); asm volatile("" ::: "memory");
; }
	s_add_i32 s24, s23, 32
	s_lshl_b32 s20, s24, 7
	s_cmp_lt_u32 s24, 40
	s_cselect_b32 s21, 0, 0x830
	s_cmp_lt_u32 s24, 72
	s_cselect_b32 s21, s21, 0xfffff030
	s_add_i32 s20, s20, s21
	s_lshl_b32 s20, s20, 2
	s_add_u32 s8, s50, s20
	s_addc_u32 s9, s51, 0
	global_load_dwordx4 v[176:179], v76, s[8:9]
	s_add_u32 s8, s8, 0x16280
	s_addc_u32 s9, s9, 0
	global_load_dwordx4 v[180:183], v76, s[8:9]
	s_add_u32 s8, s8, 0x16280
	s_addc_u32 s9, s9, 0
	global_load_dwordx4 v[184:187], v76, s[8:9]
	s_add_u32 s8, s8, 0x16280
	s_addc_u32 s9, s9, 0
	global_load_dwordx4 v[188:191], v76, s[8:9]
	s_add_u32 s8, s8, 0x16280
	s_addc_u32 s9, s9, 0
	global_load_dwordx4 v[192:195], v76, s[8:9]
	s_add_u32 s8, s8, 0x16280
	s_addc_u32 s9, s9, 0
	global_load_dwordx4 v[196:199], v76, s[8:9]
	s_add_u32 s8, s8, 0x16280
	s_addc_u32 s9, s9, 0
	global_load_dwordx4 v[200:203], v76, s[8:9]
	s_add_u32 s8, s8, 0x16280
	s_addc_u32 s9, s9, 0
	global_load_dwordx4 v[204:207], v76, s[8:9]
	s_add_i32 s24, s23, 16
	s_mul_i32 s20, s24, 0x80000
	s_add_u32 s6, s52, s20
	s_addc_u32 s7, s53, 0
	s_cmp_lt_u32 s24, 16
	s_cselect_b32 s20, 1, 0
	s_sub_i32 s21, s24, 16
	s_bitcmp0_b32 s21, 2
	s_cselect_b32 s21, 1, 0
	s_cmp_lt_u32 s24, 40
	s_cselect_b32 s21, s21, 0
	s_or_b32 s20, s20, s21
	s_cmp_lg_u32 s20, 0
	s_cselect_b64 s[20:21], -1, 0
	v_cndmask_b32_e64 v91, v77, v81, s[20:21]
	v_cndmask_b32_e64 v92, v78, v82, s[20:21]
	ds_read_b32 v226, v212
	ds_read_b32 v227, v212 offset:512
	ds_read_b32 v228, v212 offset:1024
	ds_read_b32 v229, v212 offset:1536
	ds_read_b32 v230, v212 offset:2048
	ds_read_b32 v231, v212 offset:2560
	ds_read_b32 v232, v212 offset:3072
	ds_read_b32 v233, v212 offset:3584
	ds_read_b32 v234, v212 offset:4096
	ds_read_b32 v235, v212 offset:4608
	ds_read_b32 v236, v212 offset:5120
	ds_read_b32 v237, v212 offset:5632
	ds_read_b32 v238, v212 offset:6144
	ds_read_b32 v239, v212 offset:6656
	ds_read_b32 v240, v212 offset:7168
	ds_read_b32 v241, v212 offset:7680
	s_waitcnt lgkmcnt(0)
	v_max_f32_e32 v226, v226, v226
	v_max_f32_e32 v227, v227, v227
	v_max_f32_e32 v228, v228, v228
	v_max_f32_e32 v229, v229, v229
	v_max_f32_e32 v230, v230, v230
	v_max_f32_e32 v231, v231, v231
	v_max_f32_e32 v232, v232, v232
	v_max_f32_e32 v233, v233, v233
	v_max_f32_e32 v234, v234, v234
	v_max_f32_e32 v235, v235, v235
	v_max_f32_e32 v236, v236, v236
	v_max_f32_e32 v237, v237, v237
	v_max_f32_e32 v238, v238, v238
	v_max_f32_e32 v239, v239, v239
	v_max_f32_e32 v240, v240, v240
	v_max_f32_e32 v241, v241, v241
	v_med3_f32 v226, v226, s62, v95
	v_med3_f32 v227, v227, s62, v95
	v_med3_f32 v228, v228, s62, v95
	v_med3_f32 v229, v229, s62, v95
	v_med3_f32 v230, v230, s62, v95
	v_med3_f32 v231, v231, s62, v95
	v_med3_f32 v232, v232, s62, v95
	v_med3_f32 v233, v233, s62, v95
	v_med3_f32 v234, v234, s62, v95
	v_med3_f32 v235, v235, s62, v95
	v_med3_f32 v236, v236, s62, v95
	v_med3_f32 v237, v237, s62, v95
	v_med3_f32 v238, v238, s62, v95
	v_med3_f32 v239, v239, s62, v95
	v_med3_f32 v240, v240, s62, v95
	v_med3_f32 v241, v241, s62, v95
	v_mov_b32_e32 v242, 0
	v_mov_b32_e32 v243, 0
	v_mov_b32_e32 v244, 0
	v_mov_b32_e32 v245, 0
	v_cvt_pk_fp8_f32 v242, v226, v227
	v_cvt_pk_fp8_f32 v243, v230, v231
	v_cvt_pk_fp8_f32 v244, v234, v235
	v_cvt_pk_fp8_f32 v245, v238, v239
	v_cvt_pk_fp8_f32 v242, v228, v229 op_sel:[0,0,1]
	v_cvt_pk_fp8_f32 v243, v232, v233 op_sel:[0,0,1]
	v_cvt_pk_fp8_f32 v244, v236, v237 op_sel:[0,0,1]
	v_cvt_pk_fp8_f32 v245, v240, v241 op_sel:[0,0,1]
	s_nop 0
	global_store_dwordx4 v91, v[242:245], s[6:7]
	ds_read_b32 v226, v214
	ds_read_b32 v227, v214 offset:512
	ds_read_b32 v228, v214 offset:1024
	ds_read_b32 v229, v214 offset:1536
	ds_read_b32 v230, v214 offset:2048
	ds_read_b32 v231, v214 offset:2560
	ds_read_b32 v232, v214 offset:3072
	ds_read_b32 v233, v214 offset:3584
	ds_read_b32 v234, v214 offset:4096
	ds_read_b32 v235, v214 offset:4608
	ds_read_b32 v236, v214 offset:5120
	ds_read_b32 v237, v214 offset:5632
	ds_read_b32 v238, v214 offset:6144
	ds_read_b32 v239, v214 offset:6656
	ds_read_b32 v240, v214 offset:7168
	ds_read_b32 v241, v214 offset:7680
	s_waitcnt lgkmcnt(0)
	v_max_f32_e32 v226, v226, v226
	v_max_f32_e32 v227, v227, v227
	v_max_f32_e32 v228, v228, v228
	v_max_f32_e32 v229, v229, v229
	v_max_f32_e32 v230, v230, v230
	v_max_f32_e32 v231, v231, v231
	v_max_f32_e32 v232, v232, v232
	v_max_f32_e32 v233, v233, v233
	v_max_f32_e32 v234, v234, v234
	v_max_f32_e32 v235, v235, v235
	v_max_f32_e32 v236, v236, v236
	v_max_f32_e32 v237, v237, v237
	v_max_f32_e32 v238, v238, v238
	v_max_f32_e32 v239, v239, v239
	v_max_f32_e32 v240, v240, v240
	v_max_f32_e32 v241, v241, v241
	v_med3_f32 v226, v226, s62, v95
	v_med3_f32 v227, v227, s62, v95
	v_med3_f32 v228, v228, s62, v95
	v_med3_f32 v229, v229, s62, v95
	v_med3_f32 v230, v230, s62, v95
	v_med3_f32 v231, v231, s62, v95
	v_med3_f32 v232, v232, s62, v95
	v_med3_f32 v233, v233, s62, v95
	v_med3_f32 v234, v234, s62, v95
	v_med3_f32 v235, v235, s62, v95
	v_med3_f32 v236, v236, s62, v95
	v_med3_f32 v237, v237, s62, v95
	v_med3_f32 v238, v238, s62, v95
	v_med3_f32 v239, v239, s62, v95
	v_med3_f32 v240, v240, s62, v95
	v_med3_f32 v241, v241, s62, v95
	v_mov_b32_e32 v242, 0
	v_mov_b32_e32 v243, 0
	v_mov_b32_e32 v244, 0
	v_mov_b32_e32 v245, 0
	v_cvt_pk_fp8_f32 v242, v226, v227
	v_cvt_pk_fp8_f32 v243, v230, v231
	v_cvt_pk_fp8_f32 v244, v234, v235
	v_cvt_pk_fp8_f32 v245, v238, v239
	v_cvt_pk_fp8_f32 v242, v228, v229 op_sel:[0,0,1]
	v_cvt_pk_fp8_f32 v243, v232, v233 op_sel:[0,0,1]
	v_cvt_pk_fp8_f32 v244, v236, v237 op_sel:[0,0,1]
	v_cvt_pk_fp8_f32 v245, v240, v241 op_sel:[0,0,1]
	s_nop 0
	global_store_dwordx4 v92, v[242:245], s[6:7]
	s_waitcnt vmcnt(12)
	v_mul_f32_e32 v144, v50, v144
	v_mul_f32_e32 v145, v50, v145
	v_mul_f32_e32 v146, v50, v146
	v_mul_f32_e32 v147, v50, v147
	ds_write_b128 v209, v[144:147]
	v_mul_f32_e32 v148, v51, v148
	v_mul_f32_e32 v149, v51, v149
	v_mul_f32_e32 v150, v51, v150
	v_mul_f32_e32 v151, v51, v151
	ds_write_b128 v209, v[148:151] offset:1024
	v_mul_f32_e32 v152, v52, v152
	v_mul_f32_e32 v153, v52, v153
	v_mul_f32_e32 v154, v52, v154
	v_mul_f32_e32 v155, v52, v155
	ds_write_b128 v209, v[152:155] offset:2048
	v_mul_f32_e32 v156, v53, v156
	v_mul_f32_e32 v157, v53, v157
	v_mul_f32_e32 v158, v53, v158
	v_mul_f32_e32 v159, v53, v159
	ds_write_b128 v209, v[156:159] offset:3072
	v_mul_f32_e32 v160, v54, v160
	v_mul_f32_e32 v161, v54, v161
	v_mul_f32_e32 v162, v54, v162
	v_mul_f32_e32 v163, v54, v163
	ds_write_b128 v209, v[160:163] offset:4096
	v_mul_f32_e32 v164, v55, v164
	v_mul_f32_e32 v165, v55, v165
	v_mul_f32_e32 v166, v55, v166
	v_mul_f32_e32 v167, v55, v167
	ds_write_b128 v209, v[164:167] offset:5120
	v_mul_f32_e32 v168, v56, v168
	v_mul_f32_e32 v169, v56, v169
	v_mul_f32_e32 v170, v56, v170
	v_mul_f32_e32 v171, v56, v171
	ds_write_b128 v209, v[168:171] offset:6144
	v_mul_f32_e32 v172, v57, v172
	v_mul_f32_e32 v173, v57, v173
	v_mul_f32_e32 v174, v57, v174
	v_mul_f32_e32 v175, v57, v175
	ds_write_b128 v209, v[172:175] offset:7168
	s_waitcnt lgkmcnt(0)
	s_barrier
; #define GAS __attribute__((address_space(1)))
; #define LAS __attribute__((address_space(3)))
; #define LDS_WAIT() asm volatile("s_waitcnt lgkmcnt(0)" ::: "memory")
; __device__ __forceinline__ int src_col_in(int c) {
;     if (c < 5120) { const int blk = c >> 7, p = c & 127; const bool rope = blk < 16 || ((((blk - 16) >> 2) & 1) == 0); const int d = rope ? (p >> 1) + 64 * (p & 1) : p; return blk * 128 + d; }
;     if (c < OFF_Z) return c + 2096;
;     if (c < OFF_G) return c - 4048;
;     if (c < OFF_DT) return 5120 + (c - OFF_G);
;     if (c < NSRC) return c;
;     return -1;
; }
;     const int pr = item >> 1, kb = 2 * (pr / nblk) + (item & 1), nb = pr % nblk, k0 = 64 * kb, n0 = 32 * nb;
;     const int nr = n0 + (lane & 31); const int sc = MAP == 1 ? src_col_in(nr) : nr;
;     float v[32];
; #pragma unroll
;     for (int i = 0; i < 32; ++i) v[i] = sc >= 0 ? W[(size_t)(k0 + 2 * i + (lane >> 5)) * Nsrc + sc] : 0.f;
; #pragma unroll
;     for (int i = 0; i < 32; ++i) { const int k = k0 + 2 * i + (lane >> 5); float x = v[i] * wscale; if (KS) x *= (k < ksplit ? ksA[k] : ksB[k - ksplit]); scr[(2 * i + (lane >> 5)) * 33 + (lane & 31)] = x; }
;     LDS_WAIT(); asm volatile("" ::: "memory");
;     const int c = lane & 7;
; #pragma unroll
;     for (int j = 0; j < 4; ++j) { const int n = (lane >> 3) + 8 * j; const LAS float* s = scr + (8 * c) * 33 + n;
;         const unsigned long long o = (unsigned long long)pg8::pk4_fp8(s[0 * 33], s[1 * 33], s[2 * 33], s[3 * 33]) | ((unsigned long long)pg8::pk4_fp8(s[4 * 33], s[5 * 33], s[6 * 33], s[7 * 33]) << 32);
;         *(GAS unsigned long long*)(WT + (size_t)(n0 + n) * K + k0 + 8 * c) = o; }
;     LDS_WAIT(); asm volatile("" ::: "memory");
; }
	s_add_i32 s24, s23, 40
	s_lshl_b32 s20, s24, 7
	s_cmp_lt_u32 s24, 40
	s_cselect_b32 s21, 0, 0x830
	s_cmp_lt_u32 s24, 72
	s_cselect_b32 s21, s21, 0xfffff030
	s_add_i32 s20, s20, s21
	s_lshl_b32 s20, s20, 2
	s_add_u32 s8, s50, s20
	s_addc_u32 s9, s51, 0
	global_load_dwordx4 v[144:147], v76, s[8:9]
	s_add_u32 s8, s8, 0x16280
	s_addc_u32 s9, s9, 0
	global_load_dwordx4 v[148:151], v76, s[8:9]
	s_add_u32 s8, s8, 0x16280
	s_addc_u32 s9, s9, 0
	global_load_dwordx4 v[152:155], v76, s[8:9]
	s_add_u32 s8, s8, 0x16280
	s_addc_u32 s9, s9, 0
	global_load_dwordx4 v[156:159], v76, s[8:9]
	s_add_u32 s8, s8, 0x16280
	s_addc_u32 s9, s9, 0
	global_load_dwordx4 v[160:163], v76, s[8:9]
	s_add_u32 s8, s8, 0x16280
	s_addc_u32 s9, s9, 0
	global_load_dwordx4 v[164:167], v76, s[8:9]
	s_add_u32 s8, s8, 0x16280
	s_addc_u32 s9, s9, 0
	global_load_dwordx4 v[168:171], v76, s[8:9]
	s_add_u32 s8, s8, 0x16280
	s_addc_u32 s9, s9, 0
	global_load_dwordx4 v[172:175], v76, s[8:9]
	s_add_i32 s24, s23, 24
	s_mul_i32 s20, s24, 0x80000
	s_add_u32 s6, s52, s20
	s_addc_u32 s7, s53, 0
	s_cmp_lt_u32 s24, 16
	s_cselect_b32 s20, 1, 0
	s_sub_i32 s21, s24, 16
	s_bitcmp0_b32 s21, 2
	s_cselect_b32 s21, 1, 0
	s_cmp_lt_u32 s24, 40
	s_cselect_b32 s21, s21, 0
	s_or_b32 s20, s20, s21
	s_cmp_lg_u32 s20, 0
	s_cselect_b64 s[20:21], -1, 0
	v_cndmask_b32_e64 v91, v77, v81, s[20:21]
	v_cndmask_b32_e64 v92, v78, v82, s[20:21]
	ds_read_b32 v226, v211
	ds_read_b32 v227, v211 offset:512
	ds_read_b32 v228, v211 offset:1024
	ds_read_b32 v229, v211 offset:1536
	ds_read_b32 v230, v211 offset:2048
	ds_read_b32 v231, v211 offset:2560
	ds_read_b32 v232, v211 offset:3072
	ds_read_b32 v233, v211 offset:3584
	ds_read_b32 v234, v211 offset:4096
	ds_read_b32 v235, v211 offset:4608
	ds_read_b32 v236, v211 offset:5120
	ds_read_b32 v237, v211 offset:5632
	ds_read_b32 v238, v211 offset:6144
	ds_read_b32 v239, v211 offset:6656
	ds_read_b32 v240, v211 offset:7168
	ds_read_b32 v241, v211 offset:7680
	s_waitcnt lgkmcnt(0)
	v_max_f32_e32 v226, v226, v226
	v_max_f32_e32 v227, v227, v227
	v_max_f32_e32 v228, v228, v228
	v_max_f32_e32 v229, v229, v229
	v_max_f32_e32 v230, v230, v230
	v_max_f32_e32 v231, v231, v231
	v_max_f32_e32 v232, v232, v232
	v_max_f32_e32 v233, v233, v233
	v_max_f32_e32 v234, v234, v234
	v_max_f32_e32 v235, v235, v235
	v_max_f32_e32 v236, v236, v236
	v_max_f32_e32 v237, v237, v237
	v_max_f32_e32 v238, v238, v238
	v_max_f32_e32 v239, v239, v239
	v_max_f32_e32 v240, v240, v240
	v_max_f32_e32 v241, v241, v241
	v_med3_f32 v226, v226, s62, v95
	v_med3_f32 v227, v227, s62, v95
	v_med3_f32 v228, v228, s62, v95
	v_med3_f32 v229, v229, s62, v95
	v_med3_f32 v230, v230, s62, v95
	v_med3_f32 v231, v231, s62, v95
	v_med3_f32 v232, v232, s62, v95
	v_med3_f32 v233, v233, s62, v95
	v_med3_f32 v234, v234, s62, v95
	v_med3_f32 v235, v235, s62, v95
	v_med3_f32 v236, v236, s62, v95
	v_med3_f32 v237, v237, s62, v95
	v_med3_f32 v238, v238, s62, v95
	v_med3_f32 v239, v239, s62, v95
	v_med3_f32 v240, v240, s62, v95
	v_med3_f32 v241, v241, s62, v95
	v_mov_b32_e32 v242, 0
	v_mov_b32_e32 v243, 0
	v_mov_b32_e32 v244, 0
	v_mov_b32_e32 v245, 0
	v_cvt_pk_fp8_f32 v242, v226, v227
	v_cvt_pk_fp8_f32 v243, v230, v231
	v_cvt_pk_fp8_f32 v244, v234, v235
	v_cvt_pk_fp8_f32 v245, v238, v239
	v_cvt_pk_fp8_f32 v242, v228, v229 op_sel:[0,0,1]
	v_cvt_pk_fp8_f32 v243, v232, v233 op_sel:[0,0,1]
	v_cvt_pk_fp8_f32 v244, v236, v237 op_sel:[0,0,1]
	v_cvt_pk_fp8_f32 v245, v240, v241 op_sel:[0,0,1]
	s_nop 0
	global_store_dwordx4 v91, v[242:245], s[6:7]
	ds_read_b32 v226, v213
	ds_read_b32 v227, v213 offset:512
	ds_read_b32 v228, v213 offset:1024
	ds_read_b32 v229, v213 offset:1536
	ds_read_b32 v230, v213 offset:2048
	ds_read_b32 v231, v213 offset:2560
	ds_read_b32 v232, v213 offset:3072
	ds_read_b32 v233, v213 offset:3584
	ds_read_b32 v234, v213 offset:4096
	ds_read_b32 v235, v213 offset:4608
	ds_read_b32 v236, v213 offset:5120
	ds_read_b32 v237, v213 offset:5632
	ds_read_b32 v238, v213 offset:6144
	ds_read_b32 v239, v213 offset:6656
	ds_read_b32 v240, v213 offset:7168
	ds_read_b32 v241, v213 offset:7680
	s_waitcnt lgkmcnt(0)
	v_max_f32_e32 v226, v226, v226
	v_max_f32_e32 v227, v227, v227
	v_max_f32_e32 v228, v228, v228
	v_max_f32_e32 v229, v229, v229
	v_max_f32_e32 v230, v230, v230
	v_max_f32_e32 v231, v231, v231
	v_max_f32_e32 v232, v232, v232
	v_max_f32_e32 v233, v233, v233
	v_max_f32_e32 v234, v234, v234
	v_max_f32_e32 v235, v235, v235
	v_max_f32_e32 v236, v236, v236
	v_max_f32_e32 v237, v237, v237
	v_max_f32_e32 v238, v238, v238
	v_max_f32_e32 v239, v239, v239
	v_max_f32_e32 v240, v240, v240
	v_max_f32_e32 v241, v241, v241
	v_med3_f32 v226, v226, s62, v95
	v_med3_f32 v227, v227, s62, v95
	v_med3_f32 v228, v228, s62, v95
	v_med3_f32 v229, v229, s62, v95
	v_med3_f32 v230, v230, s62, v95
	v_med3_f32 v231, v231, s62, v95
	v_med3_f32 v232, v232, s62, v95
	v_med3_f32 v233, v233, s62, v95
	v_med3_f32 v234, v234, s62, v95
	v_med3_f32 v235, v235, s62, v95
	v_med3_f32 v236, v236, s62, v95
	v_med3_f32 v237, v237, s62, v95
	v_med3_f32 v238, v238, s62, v95
	v_med3_f32 v239, v239, s62, v95
	v_med3_f32 v240, v240, s62, v95
	v_med3_f32 v241, v241, s62, v95
	v_mov_b32_e32 v242, 0
	v_mov_b32_e32 v243, 0
	v_mov_b32_e32 v244, 0
	v_mov_b32_e32 v245, 0
	v_cvt_pk_fp8_f32 v242, v226, v227
	v_cvt_pk_fp8_f32 v243, v230, v231
	v_cvt_pk_fp8_f32 v244, v234, v235
	v_cvt_pk_fp8_f32 v245, v238, v239
	v_cvt_pk_fp8_f32 v242, v228, v229 op_sel:[0,0,1]
	v_cvt_pk_fp8_f32 v243, v232, v233 op_sel:[0,0,1]
	v_cvt_pk_fp8_f32 v244, v236, v237 op_sel:[0,0,1]
	v_cvt_pk_fp8_f32 v245, v240, v241 op_sel:[0,0,1]
	s_nop 0
	global_store_dwordx4 v92, v[242:245], s[6:7]
	s_waitcnt vmcnt(12)
	v_mul_f32_e32 v176, v50, v176
	v_mul_f32_e32 v177, v50, v177
	v_mul_f32_e32 v178, v50, v178
	v_mul_f32_e32 v179, v50, v179
	ds_write_b128 v210, v[176:179]
	v_mul_f32_e32 v180, v51, v180
	v_mul_f32_e32 v181, v51, v181
	v_mul_f32_e32 v182, v51, v182
	v_mul_f32_e32 v183, v51, v183
	ds_write_b128 v210, v[180:183] offset:1024
	v_mul_f32_e32 v184, v52, v184
	v_mul_f32_e32 v185, v52, v185
	v_mul_f32_e32 v186, v52, v186
	v_mul_f32_e32 v187, v52, v187
	ds_write_b128 v210, v[184:187] offset:2048
	v_mul_f32_e32 v188, v53, v188
	v_mul_f32_e32 v189, v53, v189
	v_mul_f32_e32 v190, v53, v190
	v_mul_f32_e32 v191, v53, v191
	ds_write_b128 v210, v[188:191] offset:3072
	v_mul_f32_e32 v192, v54, v192
	v_mul_f32_e32 v193, v54, v193
	v_mul_f32_e32 v194, v54, v194
	v_mul_f32_e32 v195, v54, v195
	ds_write_b128 v210, v[192:195] offset:4096
	v_mul_f32_e32 v196, v55, v196
	v_mul_f32_e32 v197, v55, v197
	v_mul_f32_e32 v198, v55, v198
	v_mul_f32_e32 v199, v55, v199
	ds_write_b128 v210, v[196:199] offset:5120
	v_mul_f32_e32 v200, v56, v200
	v_mul_f32_e32 v201, v56, v201
	v_mul_f32_e32 v202, v56, v202
	v_mul_f32_e32 v203, v56, v203
	ds_write_b128 v210, v[200:203] offset:6144
	v_mul_f32_e32 v204, v57, v204
	v_mul_f32_e32 v205, v57, v205
	v_mul_f32_e32 v206, v57, v206
	v_mul_f32_e32 v207, v57, v207
	ds_write_b128 v210, v[204:207] offset:7168
	s_waitcnt lgkmcnt(0)
	s_barrier
; #define GAS __attribute__((address_space(1)))
; #define LAS __attribute__((address_space(3)))
; #define LDS_WAIT() asm volatile("s_waitcnt lgkmcnt(0)" ::: "memory")
; __device__ __forceinline__ int src_col_in(int c) {
;     if (c < 5120) { const int blk = c >> 7, p = c & 127; const bool rope = blk < 16 || ((((blk - 16) >> 2) & 1) == 0); const int d = rope ? (p >> 1) + 64 * (p & 1) : p; return blk * 128 + d; }
;     if (c < OFF_Z) return c + 2096;
;     if (c < OFF_G) return c - 4048;
;     if (c < OFF_DT) return 5120 + (c - OFF_G);
;     if (c < NSRC) return c;
;     return -1;
; }
;     const int pr = item >> 1, kb = 2 * (pr / nblk) + (item & 1), nb = pr % nblk, k0 = 64 * kb, n0 = 32 * nb;
;     const int nr = n0 + (lane & 31); const int sc = MAP == 1 ? src_col_in(nr) : nr;
;     float v[32];
; #pragma unroll
;     for (int i = 0; i < 32; ++i) v[i] = sc >= 0 ? W[(size_t)(k0 + 2 * i + (lane >> 5)) * Nsrc + sc] : 0.f;
; #pragma unroll
;     for (int i = 0; i < 32; ++i) { const int k = k0 + 2 * i + (lane >> 5); float x = v[i] * wscale; if (KS) x *= (k < ksplit ? ksA[k] : ksB[k - ksplit]); scr[(2 * i + (lane >> 5)) * 33 + (lane & 31)] = x; }
;     LDS_WAIT(); asm volatile("" ::: "memory");
;     const int c = lane & 7;
; #pragma unroll
;     for (int j = 0; j < 4; ++j) { const int n = (lane >> 3) + 8 * j; const LAS float* s = scr + (8 * c) * 33 + n;
;         const unsigned long long o = (unsigned long long)pg8::pk4_fp8(s[0 * 33], s[1 * 33], s[2 * 33], s[3 * 33]) | ((unsigned long long)pg8::pk4_fp8(s[4 * 33], s[5 * 33], s[6 * 33], s[7 * 33]) << 32);
;         *(GAS unsigned long long*)(WT + (size_t)(n0 + n) * K + k0 + 8 * c) = o; }
;     LDS_WAIT(); asm volatile("" ::: "memory");
; }
	s_add_i32 s24, s23, 48
	s_lshl_b32 s20, s24, 7
	s_cmp_lt_u32 s24, 40
	s_cselect_b32 s21, 0, 0x830
	s_cmp_lt_u32 s24, 72
	s_cselect_b32 s21, s21, 0xfffff030
	s_add_i32 s20, s20, s21
	s_lshl_b32 s20, s20, 2
	s_add_u32 s8, s50, s20
	s_addc_u32 s9, s51, 0
	global_load_dwordx4 v[176:179], v76, s[8:9]
	s_add_u32 s8, s8, 0x16280
	s_addc_u32 s9, s9, 0
	global_load_dwordx4 v[180:183], v76, s[8:9]
	s_add_u32 s8, s8, 0x16280
	s_addc_u32 s9, s9, 0
	global_load_dwordx4 v[184:187], v76, s[8:9]
	s_add_u32 s8, s8, 0x16280
	s_addc_u32 s9, s9, 0
	global_load_dwordx4 v[188:191], v76, s[8:9]
	s_add_u32 s8, s8, 0x16280
	s_addc_u32 s9, s9, 0
	global_load_dwordx4 v[192:195], v76, s[8:9]
	s_add_u32 s8, s8, 0x16280
	s_addc_u32 s9, s9, 0
	global_load_dwordx4 v[196:199], v76, s[8:9]
	s_add_u32 s8, s8, 0x16280
	s_addc_u32 s9, s9, 0
	global_load_dwordx4 v[200:203], v76, s[8:9]
	s_add_u32 s8, s8, 0x16280
	s_addc_u32 s9, s9, 0
	global_load_dwordx4 v[204:207], v76, s[8:9]
	s_add_i32 s24, s23, 32
	s_mul_i32 s20, s24, 0x80000
	s_add_u32 s6, s52, s20
	s_addc_u32 s7, s53, 0
	s_cmp_lt_u32 s24, 16
	s_cselect_b32 s20, 1, 0
	s_sub_i32 s21, s24, 16
	s_bitcmp0_b32 s21, 2
	s_cselect_b32 s21, 1, 0
	s_cmp_lt_u32 s24, 40
	s_cselect_b32 s21, s21, 0
	s_or_b32 s20, s20, s21
	s_cmp_lg_u32 s20, 0
	s_cselect_b64 s[20:21], -1, 0
	v_cndmask_b32_e64 v91, v77, v81, s[20:21]
	v_cndmask_b32_e64 v92, v78, v82, s[20:21]
	ds_read_b32 v226, v212
	ds_read_b32 v227, v212 offset:512
	ds_read_b32 v228, v212 offset:1024
	ds_read_b32 v229, v212 offset:1536
	ds_read_b32 v230, v212 offset:2048
	ds_read_b32 v231, v212 offset:2560
	ds_read_b32 v232, v212 offset:3072
	ds_read_b32 v233, v212 offset:3584
	ds_read_b32 v234, v212 offset:4096
	ds_read_b32 v235, v212 offset:4608
	ds_read_b32 v236, v212 offset:5120
	ds_read_b32 v237, v212 offset:5632
	ds_read_b32 v238, v212 offset:6144
	ds_read_b32 v239, v212 offset:6656
	ds_read_b32 v240, v212 offset:7168
	ds_read_b32 v241, v212 offset:7680
	s_waitcnt lgkmcnt(0)
	v_max_f32_e32 v226, v226, v226
	v_max_f32_e32 v227, v227, v227
	v_max_f32_e32 v228, v228, v228
	v_max_f32_e32 v229, v229, v229
	v_max_f32_e32 v230, v230, v230
	v_max_f32_e32 v231, v231, v231
	v_max_f32_e32 v232, v232, v232
	v_max_f32_e32 v233, v233, v233
	v_max_f32_e32 v234, v234, v234
	v_max_f32_e32 v235, v235, v235
	v_max_f32_e32 v236, v236, v236
	v_max_f32_e32 v237, v237, v237
	v_max_f32_e32 v238, v238, v238
	v_max_f32_e32 v239, v239, v239
	v_max_f32_e32 v240, v240, v240
	v_max_f32_e32 v241, v241, v241
	v_med3_f32 v226, v226, s62, v95
	v_med3_f32 v227, v227, s62, v95
	v_med3_f32 v228, v228, s62, v95
	v_med3_f32 v229, v229, s62, v95
	v_med3_f32 v230, v230, s62, v95
	v_med3_f32 v231, v231, s62, v95
	v_med3_f32 v232, v232, s62, v95
	v_med3_f32 v233, v233, s62, v95
	v_med3_f32 v234, v234, s62, v95
	v_med3_f32 v235, v235, s62, v95
	v_med3_f32 v236, v236, s62, v95
	v_med3_f32 v237, v237, s62, v95
	v_med3_f32 v238, v238, s62, v95
	v_med3_f32 v239, v239, s62, v95
	v_med3_f32 v240, v240, s62, v95
	v_med3_f32 v241, v241, s62, v95
	v_mov_b32_e32 v242, 0
	v_mov_b32_e32 v243, 0
	v_mov_b32_e32 v244, 0
	v_mov_b32_e32 v245, 0
	v_cvt_pk_fp8_f32 v242, v226, v227
	v_cvt_pk_fp8_f32 v243, v230, v231
	v_cvt_pk_fp8_f32 v244, v234, v235
	v_cvt_pk_fp8_f32 v245, v238, v239
	v_cvt_pk_fp8_f32 v242, v228, v229 op_sel:[0,0,1]
	v_cvt_pk_fp8_f32 v243, v232, v233 op_sel:[0,0,1]
	v_cvt_pk_fp8_f32 v244, v236, v237 op_sel:[0,0,1]
	v_cvt_pk_fp8_f32 v245, v240, v241 op_sel:[0,0,1]
	s_nop 0
	global_store_dwordx4 v91, v[242:245], s[6:7]
	ds_read_b32 v226, v214
	ds_read_b32 v227, v214 offset:512
	ds_read_b32 v228, v214 offset:1024
	ds_read_b32 v229, v214 offset:1536
	ds_read_b32 v230, v214 offset:2048
	ds_read_b32 v231, v214 offset:2560
	ds_read_b32 v232, v214 offset:3072
	ds_read_b32 v233, v214 offset:3584
	ds_read_b32 v234, v214 offset:4096
	ds_read_b32 v235, v214 offset:4608
	ds_read_b32 v236, v214 offset:5120
	ds_read_b32 v237, v214 offset:5632
	ds_read_b32 v238, v214 offset:6144
	ds_read_b32 v239, v214 offset:6656
	ds_read_b32 v240, v214 offset:7168
	ds_read_b32 v241, v214 offset:7680
	s_waitcnt lgkmcnt(0)
	v_max_f32_e32 v226, v226, v226
	v_max_f32_e32 v227, v227, v227
	v_max_f32_e32 v228, v228, v228
	v_max_f32_e32 v229, v229, v229
	v_max_f32_e32 v230, v230, v230
	v_max_f32_e32 v231, v231, v231
	v_max_f32_e32 v232, v232, v232
	v_max_f32_e32 v233, v233, v233
	v_max_f32_e32 v234, v234, v234
	v_max_f32_e32 v235, v235, v235
	v_max_f32_e32 v236, v236, v236
	v_max_f32_e32 v237, v237, v237
	v_max_f32_e32 v238, v238, v238
	v_max_f32_e32 v239, v239, v239
	v_max_f32_e32 v240, v240, v240
	v_max_f32_e32 v241, v241, v241
	v_med3_f32 v226, v226, s62, v95
	v_med3_f32 v227, v227, s62, v95
	v_med3_f32 v228, v228, s62, v95
	v_med3_f32 v229, v229, s62, v95
	v_med3_f32 v230, v230, s62, v95
	v_med3_f32 v231, v231, s62, v95
	v_med3_f32 v232, v232, s62, v95
	v_med3_f32 v233, v233, s62, v95
	v_med3_f32 v234, v234, s62, v95
	v_med3_f32 v235, v235, s62, v95
	v_med3_f32 v236, v236, s62, v95
	v_med3_f32 v237, v237, s62, v95
	v_med3_f32 v238, v238, s62, v95
	v_med3_f32 v239, v239, s62, v95
	v_med3_f32 v240, v240, s62, v95
	v_med3_f32 v241, v241, s62, v95
	v_mov_b32_e32 v242, 0
	v_mov_b32_e32 v243, 0
	v_mov_b32_e32 v244, 0
	v_mov_b32_e32 v245, 0
	v_cvt_pk_fp8_f32 v242, v226, v227
	v_cvt_pk_fp8_f32 v243, v230, v231
	v_cvt_pk_fp8_f32 v244, v234, v235
	v_cvt_pk_fp8_f32 v245, v238, v239
	v_cvt_pk_fp8_f32 v242, v228, v229 op_sel:[0,0,1]
	v_cvt_pk_fp8_f32 v243, v232, v233 op_sel:[0,0,1]
	v_cvt_pk_fp8_f32 v244, v236, v237 op_sel:[0,0,1]
	v_cvt_pk_fp8_f32 v245, v240, v241 op_sel:[0,0,1]
	s_nop 0
	global_store_dwordx4 v92, v[242:245], s[6:7]
	s_waitcnt vmcnt(12)
	v_mul_f32_e32 v144, v50, v144
	v_mul_f32_e32 v145, v50, v145
	v_mul_f32_e32 v146, v50, v146
	v_mul_f32_e32 v147, v50, v147
	ds_write_b128 v209, v[144:147]
	v_mul_f32_e32 v148, v51, v148
	v_mul_f32_e32 v149, v51, v149
	v_mul_f32_e32 v150, v51, v150
	v_mul_f32_e32 v151, v51, v151
	ds_write_b128 v209, v[148:151] offset:1024
	v_mul_f32_e32 v152, v52, v152
	v_mul_f32_e32 v153, v52, v153
	v_mul_f32_e32 v154, v52, v154
	v_mul_f32_e32 v155, v52, v155
	ds_write_b128 v209, v[152:155] offset:2048
	v_mul_f32_e32 v156, v53, v156
	v_mul_f32_e32 v157, v53, v157
	v_mul_f32_e32 v158, v53, v158
	v_mul_f32_e32 v159, v53, v159
	ds_write_b128 v209, v[156:159] offset:3072
	v_mul_f32_e32 v160, v54, v160
	v_mul_f32_e32 v161, v54, v161
	v_mul_f32_e32 v162, v54, v162
	v_mul_f32_e32 v163, v54, v163
	ds_write_b128 v209, v[160:163] offset:4096
	v_mul_f32_e32 v164, v55, v164
	v_mul_f32_e32 v165, v55, v165
	v_mul_f32_e32 v166, v55, v166
	v_mul_f32_e32 v167, v55, v167
	ds_write_b128 v209, v[164:167] offset:5120
	v_mul_f32_e32 v168, v56, v168
	v_mul_f32_e32 v169, v56, v169
	v_mul_f32_e32 v170, v56, v170
	v_mul_f32_e32 v171, v56, v171
	ds_write_b128 v209, v[168:171] offset:6144
	v_mul_f32_e32 v172, v57, v172
	v_mul_f32_e32 v173, v57, v173
	v_mul_f32_e32 v174, v57, v174
	v_mul_f32_e32 v175, v57, v175
	ds_write_b128 v209, v[172:175] offset:7168
	s_waitcnt lgkmcnt(0)
	s_barrier
; #define GAS __attribute__((address_space(1)))
; #define LAS __attribute__((address_space(3)))
; #define LDS_WAIT() asm volatile("s_waitcnt lgkmcnt(0)" ::: "memory")
; __device__ __forceinline__ int src_col_in(int c) {
;     if (c < 5120) { const int blk = c >> 7, p = c & 127; const bool rope = blk < 16 || ((((blk - 16) >> 2) & 1) == 0); const int d = rope ? (p >> 1) + 64 * (p & 1) : p; return blk * 128 + d; }
;     if (c < OFF_Z) return c + 2096;
;     if (c < OFF_G) return c - 4048;
;     if (c < OFF_DT) return 5120 + (c - OFF_G);
;     if (c < NSRC) return c;
;     return -1;
; }
;     const int pr = item >> 1, kb = 2 * (pr / nblk) + (item & 1), nb = pr % nblk, k0 = 64 * kb, n0 = 32 * nb;
;     const int nr = n0 + (lane & 31); const int sc = MAP == 1 ? src_col_in(nr) : nr;
;     float v[32];
; #pragma unroll
;     for (int i = 0; i < 32; ++i) v[i] = sc >= 0 ? W[(size_t)(k0 + 2 * i + (lane >> 5)) * Nsrc + sc] : 0.f;
; #pragma unroll
;     for (int i = 0; i < 32; ++i) { const int k = k0 + 2 * i + (lane >> 5); float x = v[i] * wscale; if (KS) x *= (k < ksplit ? ksA[k] : ksB[k - ksplit]); scr[(2 * i + (lane >> 5)) * 33 + (lane & 31)] = x; }
;     LDS_WAIT(); asm volatile("" ::: "memory");
;     const int c = lane & 7;
; #pragma unroll
;     for (int j = 0; j < 4; ++j) { const int n = (lane >> 3) + 8 * j; const LAS float* s = scr + (8 * c) * 33 + n;
;         const unsigned long long o = (unsigned long long)pg8::pk4_fp8(s[0 * 33], s[1 * 33], s[2 * 33], s[3 * 33]) | ((unsigned long long)pg8::pk4_fp8(s[4 * 33], s[5 * 33], s[6 * 33], s[7 * 33]) << 32);
;         *(GAS unsigned long long*)(WT + (size_t)(n0 + n) * K + k0 + 8 * c) = o; }
;     LDS_WAIT(); asm volatile("" ::: "memory");
; }
	s_add_i32 s24, s23, 56
	s_lshl_b32 s20, s24, 7
	s_cmp_lt_u32 s24, 40
	s_cselect_b32 s21, 0, 0x830
	s_cmp_lt_u32 s24, 72
	s_cselect_b32 s21, s21, 0xfffff030
	s_add_i32 s20, s20, s21
	s_lshl_b32 s20, s20, 2
	s_add_u32 s8, s50, s20
	s_addc_u32 s9, s51, 0
	global_load_dwordx4 v[144:147], v76, s[8:9]
	s_add_u32 s8, s8, 0x16280
	s_addc_u32 s9, s9, 0
	global_load_dwordx4 v[148:151], v76, s[8:9]
	s_add_u32 s8, s8, 0x16280
	s_addc_u32 s9, s9, 0
	global_load_dwordx4 v[152:155], v76, s[8:9]
	s_add_u32 s8, s8, 0x16280
	s_addc_u32 s9, s9, 0
	global_load_dwordx4 v[156:159], v76, s[8:9]
	s_add_u32 s8, s8, 0x16280
	s_addc_u32 s9, s9, 0
	global_load_dwordx4 v[160:163], v76, s[8:9]
	s_add_u32 s8, s8, 0x16280
	s_addc_u32 s9, s9, 0
	global_load_dwordx4 v[164:167], v76, s[8:9]
	s_add_u32 s8, s8, 0x16280
	s_addc_u32 s9, s9, 0
	global_load_dwordx4 v[168:171], v76, s[8:9]
	s_add_u32 s8, s8, 0x16280
	s_addc_u32 s9, s9, 0
	global_load_dwordx4 v[172:175], v76, s[8:9]
	s_add_i32 s24, s23, 40
	s_mul_i32 s20, s24, 0x80000
	s_add_u32 s6, s52, s20
	s_addc_u32 s7, s53, 0
	s_cmp_lt_u32 s24, 16
	s_cselect_b32 s20, 1, 0
	s_sub_i32 s21, s24, 16
	s_bitcmp0_b32 s21, 2
	s_cselect_b32 s21, 1, 0
	s_cmp_lt_u32 s24, 40
	s_cselect_b32 s21, s21, 0
	s_or_b32 s20, s20, s21
	s_cmp_lg_u32 s20, 0
	s_cselect_b64 s[20:21], -1, 0
	v_cndmask_b32_e64 v91, v77, v81, s[20:21]
	v_cndmask_b32_e64 v92, v78, v82, s[20:21]
	ds_read_b32 v226, v211
	ds_read_b32 v227, v211 offset:512
	ds_read_b32 v228, v211 offset:1024
	ds_read_b32 v229, v211 offset:1536
	ds_read_b32 v230, v211 offset:2048
	ds_read_b32 v231, v211 offset:2560
	ds_read_b32 v232, v211 offset:3072
	ds_read_b32 v233, v211 offset:3584
	ds_read_b32 v234, v211 offset:4096
	ds_read_b32 v235, v211 offset:4608
	ds_read_b32 v236, v211 offset:5120
	ds_read_b32 v237, v211 offset:5632
	ds_read_b32 v238, v211 offset:6144
	ds_read_b32 v239, v211 offset:6656
	ds_read_b32 v240, v211 offset:7168
	ds_read_b32 v241, v211 offset:7680
	s_waitcnt lgkmcnt(0)
	v_max_f32_e32 v226, v226, v226
	v_max_f32_e32 v227, v227, v227
	v_max_f32_e32 v228, v228, v228
	v_max_f32_e32 v229, v229, v229
	v_max_f32_e32 v230, v230, v230
	v_max_f32_e32 v231, v231, v231
	v_max_f32_e32 v232, v232, v232
	v_max_f32_e32 v233, v233, v233
	v_max_f32_e32 v234, v234, v234
	v_max_f32_e32 v235, v235, v235
	v_max_f32_e32 v236, v236, v236
	v_max_f32_e32 v237, v237, v237
	v_max_f32_e32 v238, v238, v238
	v_max_f32_e32 v239, v239, v239
	v_max_f32_e32 v240, v240, v240
	v_max_f32_e32 v241, v241, v241
	v_med3_f32 v226, v226, s62, v95
	v_med3_f32 v227, v227, s62, v95
	v_med3_f32 v228, v228, s62, v95
	v_med3_f32 v229, v229, s62, v95
	v_med3_f32 v230, v230, s62, v95
	v_med3_f32 v231, v231, s62, v95
	v_med3_f32 v232, v232, s62, v95
	v_med3_f32 v233, v233, s62, v95
	v_med3_f32 v234, v234, s62, v95
	v_med3_f32 v235, v235, s62, v95
	v_med3_f32 v236, v236, s62, v95
	v_med3_f32 v237, v237, s62, v95
	v_med3_f32 v238, v238, s62, v95
	v_med3_f32 v239, v239, s62, v95
	v_med3_f32 v240, v240, s62, v95
	v_med3_f32 v241, v241, s62, v95
	v_mov_b32_e32 v242, 0
	v_mov_b32_e32 v243, 0
	v_mov_b32_e32 v244, 0
	v_mov_b32_e32 v245, 0
	v_cvt_pk_fp8_f32 v242, v226, v227
	v_cvt_pk_fp8_f32 v243, v230, v231
	v_cvt_pk_fp8_f32 v244, v234, v235
	v_cvt_pk_fp8_f32 v245, v238, v239
	v_cvt_pk_fp8_f32 v242, v228, v229 op_sel:[0,0,1]
	v_cvt_pk_fp8_f32 v243, v232, v233 op_sel:[0,0,1]
	v_cvt_pk_fp8_f32 v244, v236, v237 op_sel:[0,0,1]
	v_cvt_pk_fp8_f32 v245, v240, v241 op_sel:[0,0,1]
	s_nop 0
	global_store_dwordx4 v91, v[242:245], s[6:7]
	ds_read_b32 v226, v213
	ds_read_b32 v227, v213 offset:512
	ds_read_b32 v228, v213 offset:1024
	ds_read_b32 v229, v213 offset:1536
	ds_read_b32 v230, v213 offset:2048
	ds_read_b32 v231, v213 offset:2560
	ds_read_b32 v232, v213 offset:3072
	ds_read_b32 v233, v213 offset:3584
	ds_read_b32 v234, v213 offset:4096
	ds_read_b32 v235, v213 offset:4608
	ds_read_b32 v236, v213 offset:5120
	ds_read_b32 v237, v213 offset:5632
	ds_read_b32 v238, v213 offset:6144
	ds_read_b32 v239, v213 offset:6656
	ds_read_b32 v240, v213 offset:7168
	ds_read_b32 v241, v213 offset:7680
	s_waitcnt lgkmcnt(0)
	v_max_f32_e32 v226, v226, v226
	v_max_f32_e32 v227, v227, v227
	v_max_f32_e32 v228, v228, v228
	v_max_f32_e32 v229, v229, v229
	v_max_f32_e32 v230, v230, v230
	v_max_f32_e32 v231, v231, v231
	v_max_f32_e32 v232, v232, v232
	v_max_f32_e32 v233, v233, v233
	v_max_f32_e32 v234, v234, v234
	v_max_f32_e32 v235, v235, v235
	v_max_f32_e32 v236, v236, v236
	v_max_f32_e32 v237, v237, v237
	v_max_f32_e32 v238, v238, v238
	v_max_f32_e32 v239, v239, v239
	v_max_f32_e32 v240, v240, v240
	v_max_f32_e32 v241, v241, v241
	v_med3_f32 v226, v226, s62, v95
	v_med3_f32 v227, v227, s62, v95
	v_med3_f32 v228, v228, s62, v95
	v_med3_f32 v229, v229, s62, v95
	v_med3_f32 v230, v230, s62, v95
	v_med3_f32 v231, v231, s62, v95
	v_med3_f32 v232, v232, s62, v95
	v_med3_f32 v233, v233, s62, v95
	v_med3_f32 v234, v234, s62, v95
	v_med3_f32 v235, v235, s62, v95
	v_med3_f32 v236, v236, s62, v95
	v_med3_f32 v237, v237, s62, v95
	v_med3_f32 v238, v238, s62, v95
	v_med3_f32 v239, v239, s62, v95
	v_med3_f32 v240, v240, s62, v95
	v_med3_f32 v241, v241, s62, v95
	v_mov_b32_e32 v242, 0
	v_mov_b32_e32 v243, 0
	v_mov_b32_e32 v244, 0
	v_mov_b32_e32 v245, 0
	v_cvt_pk_fp8_f32 v242, v226, v227
	v_cvt_pk_fp8_f32 v243, v230, v231
	v_cvt_pk_fp8_f32 v244, v234, v235
	v_cvt_pk_fp8_f32 v245, v238, v239
	v_cvt_pk_fp8_f32 v242, v228, v229 op_sel:[0,0,1]
	v_cvt_pk_fp8_f32 v243, v232, v233 op_sel:[0,0,1]
	v_cvt_pk_fp8_f32 v244, v236, v237 op_sel:[0,0,1]
	v_cvt_pk_fp8_f32 v245, v240, v241 op_sel:[0,0,1]
	s_nop 0
	global_store_dwordx4 v92, v[242:245], s[6:7]
	s_waitcnt vmcnt(12)
	v_mul_f32_e32 v176, v50, v176
	v_mul_f32_e32 v177, v50, v177
	v_mul_f32_e32 v178, v50, v178
	v_mul_f32_e32 v179, v50, v179
	ds_write_b128 v210, v[176:179]
	v_mul_f32_e32 v180, v51, v180
	v_mul_f32_e32 v181, v51, v181
	v_mul_f32_e32 v182, v51, v182
	v_mul_f32_e32 v183, v51, v183
	ds_write_b128 v210, v[180:183] offset:1024
	v_mul_f32_e32 v184, v52, v184
	v_mul_f32_e32 v185, v52, v185
	v_mul_f32_e32 v186, v52, v186
	v_mul_f32_e32 v187, v52, v187
	ds_write_b128 v210, v[184:187] offset:2048
	v_mul_f32_e32 v188, v53, v188
	v_mul_f32_e32 v189, v53, v189
	v_mul_f32_e32 v190, v53, v190
	v_mul_f32_e32 v191, v53, v191
	ds_write_b128 v210, v[188:191] offset:3072
	v_mul_f32_e32 v192, v54, v192
	v_mul_f32_e32 v193, v54, v193
	v_mul_f32_e32 v194, v54, v194
	v_mul_f32_e32 v195, v54, v195
	ds_write_b128 v210, v[192:195] offset:4096
	v_mul_f32_e32 v196, v55, v196
	v_mul_f32_e32 v197, v55, v197
	v_mul_f32_e32 v198, v55, v198
	v_mul_f32_e32 v199, v55, v199
	ds_write_b128 v210, v[196:199] offset:5120
	v_mul_f32_e32 v200, v56, v200
	v_mul_f32_e32 v201, v56, v201
	v_mul_f32_e32 v202, v56, v202
	v_mul_f32_e32 v203, v56, v203
	ds_write_b128 v210, v[200:203] offset:6144
	v_mul_f32_e32 v204, v57, v204
	v_mul_f32_e32 v205, v57, v205
	v_mul_f32_e32 v206, v57, v206
	v_mul_f32_e32 v207, v57, v207
	ds_write_b128 v210, v[204:207] offset:7168
	s_waitcnt lgkmcnt(0)
	s_barrier
; #define GAS __attribute__((address_space(1)))
; #define LAS __attribute__((address_space(3)))
; #define LDS_WAIT() asm volatile("s_waitcnt lgkmcnt(0)" ::: "memory")
; __device__ __forceinline__ int src_col_in(int c) {
;     if (c < 5120) { const int blk = c >> 7, p = c & 127; const bool rope = blk < 16 || ((((blk - 16) >> 2) & 1) == 0); const int d = rope ? (p >> 1) + 64 * (p & 1) : p; return blk * 128 + d; }
;     if (c < OFF_Z) return c + 2096;
;     if (c < OFF_G) return c - 4048;
;     if (c < OFF_DT) return 5120 + (c - OFF_G);
;     if (c < NSRC) return c;
;     return -1;
; }
;     const int pr = item >> 1, kb = 2 * (pr / nblk) + (item & 1), nb = pr % nblk, k0 = 64 * kb, n0 = 32 * nb;
;     const int nr = n0 + (lane & 31); const int sc = MAP == 1 ? src_col_in(nr) : nr;
;     float v[32];
; #pragma unroll
;     for (int i = 0; i < 32; ++i) v[i] = sc >= 0 ? W[(size_t)(k0 + 2 * i + (lane >> 5)) * Nsrc + sc] : 0.f;
; #pragma unroll
;     for (int i = 0; i < 32; ++i) { const int k = k0 + 2 * i + (lane >> 5); float x = v[i] * wscale; if (KS) x *= (k < ksplit ? ksA[k] : ksB[k - ksplit]); scr[(2 * i + (lane >> 5)) * 33 + (lane & 31)] = x; }
;     LDS_WAIT(); asm volatile("" ::: "memory");
;     const int c = lane & 7;
; #pragma unroll
;     for (int j = 0; j < 4; ++j) { const int n = (lane >> 3) + 8 * j; const LAS float* s = scr + (8 * c) * 33 + n;
;         const unsigned long long o = (unsigned long long)pg8::pk4_fp8(s[0 * 33], s[1 * 33], s[2 * 33], s[3 * 33]) | ((unsigned long long)pg8::pk4_fp8(s[4 * 33], s[5 * 33], s[6 * 33], s[7 * 33]) << 32);
;         *(GAS unsigned long long*)(WT + (size_t)(n0 + n) * K + k0 + 8 * c) = o; }
;     LDS_WAIT(); asm volatile("" ::: "memory");
; }
	s_add_i32 s24, s23, 64
	s_lshl_b32 s20, s24, 7
	s_cmp_lt_u32 s24, 40
	s_cselect_b32 s21, 0, 0x830
	s_cmp_lt_u32 s24, 72
	s_cselect_b32 s21, s21, 0xfffff030
	s_add_i32 s20, s20, s21
	s_lshl_b32 s20, s20, 2
	s_add_u32 s8, s50, s20
	s_addc_u32 s9, s51, 0
	global_load_dwordx4 v[176:179], v76, s[8:9]
	s_add_u32 s8, s8, 0x16280
	s_addc_u32 s9, s9, 0
	global_load_dwordx4 v[180:183], v76, s[8:9]
	s_add_u32 s8, s8, 0x16280
	s_addc_u32 s9, s9, 0
	global_load_dwordx4 v[184:187], v76, s[8:9]
	s_add_u32 s8, s8, 0x16280
	s_addc_u32 s9, s9, 0
	global_load_dwordx4 v[188:191], v76, s[8:9]
	s_add_u32 s8, s8, 0x16280
	s_addc_u32 s9, s9, 0
	global_load_dwordx4 v[192:195], v76, s[8:9]
	s_add_u32 s8, s8, 0x16280
	s_addc_u32 s9, s9, 0
	global_load_dwordx4 v[196:199], v76, s[8:9]
	s_add_u32 s8, s8, 0x16280
	s_addc_u32 s9, s9, 0
	global_load_dwordx4 v[200:203], v76, s[8:9]
	s_add_u32 s8, s8, 0x16280
	s_addc_u32 s9, s9, 0
	global_load_dwordx4 v[204:207], v76, s[8:9]
	s_add_i32 s24, s23, 48
	s_mul_i32 s20, s24, 0x80000
	s_add_u32 s6, s52, s20
	s_addc_u32 s7, s53, 0
	s_cmp_lt_u32 s24, 16
	s_cselect_b32 s20, 1, 0
	s_sub_i32 s21, s24, 16
	s_bitcmp0_b32 s21, 2
	s_cselect_b32 s21, 1, 0
	s_cmp_lt_u32 s24, 40
	s_cselect_b32 s21, s21, 0
	s_or_b32 s20, s20, s21
	s_cmp_lg_u32 s20, 0
	s_cselect_b64 s[20:21], -1, 0
	v_cndmask_b32_e64 v91, v77, v81, s[20:21]
	v_cndmask_b32_e64 v92, v78, v82, s[20:21]
	ds_read_b32 v226, v212
	ds_read_b32 v227, v212 offset:512
	ds_read_b32 v228, v212 offset:1024
	ds_read_b32 v229, v212 offset:1536
	ds_read_b32 v230, v212 offset:2048
	ds_read_b32 v231, v212 offset:2560
	ds_read_b32 v232, v212 offset:3072
	ds_read_b32 v233, v212 offset:3584
	ds_read_b32 v234, v212 offset:4096
	ds_read_b32 v235, v212 offset:4608
	ds_read_b32 v236, v212 offset:5120
	ds_read_b32 v237, v212 offset:5632
	ds_read_b32 v238, v212 offset:6144
	ds_read_b32 v239, v212 offset:6656
	ds_read_b32 v240, v212 offset:7168
	ds_read_b32 v241, v212 offset:7680
	s_waitcnt lgkmcnt(0)
	v_max_f32_e32 v226, v226, v226
	v_max_f32_e32 v227, v227, v227
	v_max_f32_e32 v228, v228, v228
	v_max_f32_e32 v229, v229, v229
	v_max_f32_e32 v230, v230, v230
	v_max_f32_e32 v231, v231, v231
	v_max_f32_e32 v232, v232, v232
	v_max_f32_e32 v233, v233, v233
	v_max_f32_e32 v234, v234, v234
	v_max_f32_e32 v235, v235, v235
	v_max_f32_e32 v236, v236, v236
	v_max_f32_e32 v237, v237, v237
	v_max_f32_e32 v238, v238, v238
	v_max_f32_e32 v239, v239, v239
	v_max_f32_e32 v240, v240, v240
	v_max_f32_e32 v241, v241, v241
	v_med3_f32 v226, v226, s62, v95
	v_med3_f32 v227, v227, s62, v95
	v_med3_f32 v228, v228, s62, v95
	v_med3_f32 v229, v229, s62, v95
	v_med3_f32 v230, v230, s62, v95
	v_med3_f32 v231, v231, s62, v95
	v_med3_f32 v232, v232, s62, v95
	v_med3_f32 v233, v233, s62, v95
	v_med3_f32 v234, v234, s62, v95
	v_med3_f32 v235, v235, s62, v95
	v_med3_f32 v236, v236, s62, v95
	v_med3_f32 v237, v237, s62, v95
	v_med3_f32 v238, v238, s62, v95
	v_med3_f32 v239, v239, s62, v95
	v_med3_f32 v240, v240, s62, v95
	v_med3_f32 v241, v241, s62, v95
	v_mov_b32_e32 v242, 0
	v_mov_b32_e32 v243, 0
	v_mov_b32_e32 v244, 0
	v_mov_b32_e32 v245, 0
	v_cvt_pk_fp8_f32 v242, v226, v227
	v_cvt_pk_fp8_f32 v243, v230, v231
	v_cvt_pk_fp8_f32 v244, v234, v235
	v_cvt_pk_fp8_f32 v245, v238, v239
	v_cvt_pk_fp8_f32 v242, v228, v229 op_sel:[0,0,1]
	v_cvt_pk_fp8_f32 v243, v232, v233 op_sel:[0,0,1]
	v_cvt_pk_fp8_f32 v244, v236, v237 op_sel:[0,0,1]
	v_cvt_pk_fp8_f32 v245, v240, v241 op_sel:[0,0,1]
	s_nop 0
	global_store_dwordx4 v91, v[242:245], s[6:7]
	ds_read_b32 v226, v214
	ds_read_b32 v227, v214 offset:512
	ds_read_b32 v228, v214 offset:1024
	ds_read_b32 v229, v214 offset:1536
	ds_read_b32 v230, v214 offset:2048
	ds_read_b32 v231, v214 offset:2560
	ds_read_b32 v232, v214 offset:3072
	ds_read_b32 v233, v214 offset:3584
	ds_read_b32 v234, v214 offset:4096
	ds_read_b32 v235, v214 offset:4608
	ds_read_b32 v236, v214 offset:5120
	ds_read_b32 v237, v214 offset:5632
	ds_read_b32 v238, v214 offset:6144
	ds_read_b32 v239, v214 offset:6656
	ds_read_b32 v240, v214 offset:7168
	ds_read_b32 v241, v214 offset:7680
	s_waitcnt lgkmcnt(0)
	v_max_f32_e32 v226, v226, v226
	v_max_f32_e32 v227, v227, v227
	v_max_f32_e32 v228, v228, v228
	v_max_f32_e32 v229, v229, v229
	v_max_f32_e32 v230, v230, v230
	v_max_f32_e32 v231, v231, v231
	v_max_f32_e32 v232, v232, v232
	v_max_f32_e32 v233, v233, v233
	v_max_f32_e32 v234, v234, v234
	v_max_f32_e32 v235, v235, v235
	v_max_f32_e32 v236, v236, v236
	v_max_f32_e32 v237, v237, v237
	v_max_f32_e32 v238, v238, v238
	v_max_f32_e32 v239, v239, v239
	v_max_f32_e32 v240, v240, v240
	v_max_f32_e32 v241, v241, v241
	v_med3_f32 v226, v226, s62, v95
	v_med3_f32 v227, v227, s62, v95
	v_med3_f32 v228, v228, s62, v95
	v_med3_f32 v229, v229, s62, v95
	v_med3_f32 v230, v230, s62, v95
	v_med3_f32 v231, v231, s62, v95
	v_med3_f32 v232, v232, s62, v95
	v_med3_f32 v233, v233, s62, v95
	v_med3_f32 v234, v234, s62, v95
	v_med3_f32 v235, v235, s62, v95
	v_med3_f32 v236, v236, s62, v95
	v_med3_f32 v237, v237, s62, v95
	v_med3_f32 v238, v238, s62, v95
	v_med3_f32 v239, v239, s62, v95
	v_med3_f32 v240, v240, s62, v95
	v_med3_f32 v241, v241, s62, v95
	v_mov_b32_e32 v242, 0
	v_mov_b32_e32 v243, 0
	v_mov_b32_e32 v244, 0
	v_mov_b32_e32 v245, 0
	v_cvt_pk_fp8_f32 v242, v226, v227
	v_cvt_pk_fp8_f32 v243, v230, v231
	v_cvt_pk_fp8_f32 v244, v234, v235
	v_cvt_pk_fp8_f32 v245, v238, v239
	v_cvt_pk_fp8_f32 v242, v228, v229 op_sel:[0,0,1]
	v_cvt_pk_fp8_f32 v243, v232, v233 op_sel:[0,0,1]
	v_cvt_pk_fp8_f32 v244, v236, v237 op_sel:[0,0,1]
	v_cvt_pk_fp8_f32 v245, v240, v241 op_sel:[0,0,1]
	s_nop 0
	global_store_dwordx4 v92, v[242:245], s[6:7]
	s_waitcnt vmcnt(12)
	v_mul_f32_e32 v144, v50, v144
	v_mul_f32_e32 v145, v50, v145
	v_mul_f32_e32 v146, v50, v146
	v_mul_f32_e32 v147, v50, v147
	ds_write_b128 v209, v[144:147]
	v_mul_f32_e32 v148, v51, v148
	v_mul_f32_e32 v149, v51, v149
	v_mul_f32_e32 v150, v51, v150
	v_mul_f32_e32 v151, v51, v151
	ds_write_b128 v209, v[148:151] offset:1024
	v_mul_f32_e32 v152, v52, v152
	v_mul_f32_e32 v153, v52, v153
	v_mul_f32_e32 v154, v52, v154
	v_mul_f32_e32 v155, v52, v155
	ds_write_b128 v209, v[152:155] offset:2048
	v_mul_f32_e32 v156, v53, v156
	v_mul_f32_e32 v157, v53, v157
	v_mul_f32_e32 v158, v53, v158
	v_mul_f32_e32 v159, v53, v159
	ds_write_b128 v209, v[156:159] offset:3072
	v_mul_f32_e32 v160, v54, v160
	v_mul_f32_e32 v161, v54, v161
	v_mul_f32_e32 v162, v54, v162
	v_mul_f32_e32 v163, v54, v163
	ds_write_b128 v209, v[160:163] offset:4096
	v_mul_f32_e32 v164, v55, v164
	v_mul_f32_e32 v165, v55, v165
	v_mul_f32_e32 v166, v55, v166
	v_mul_f32_e32 v167, v55, v167
	ds_write_b128 v209, v[164:167] offset:5120
	v_mul_f32_e32 v168, v56, v168
	v_mul_f32_e32 v169, v56, v169
	v_mul_f32_e32 v170, v56, v170
	v_mul_f32_e32 v171, v56, v171
	ds_write_b128 v209, v[168:171] offset:6144
	v_mul_f32_e32 v172, v57, v172
	v_mul_f32_e32 v173, v57, v173
	v_mul_f32_e32 v174, v57, v174
	v_mul_f32_e32 v175, v57, v175
	ds_write_b128 v209, v[172:175] offset:7168
	s_waitcnt lgkmcnt(0)
	s_barrier
; #define GAS __attribute__((address_space(1)))
; #define LAS __attribute__((address_space(3)))
; #define LDS_WAIT() asm volatile("s_waitcnt lgkmcnt(0)" ::: "memory")
; __device__ __forceinline__ int src_col_in(int c) {
;     if (c < 5120) { const int blk = c >> 7, p = c & 127; const bool rope = blk < 16 || ((((blk - 16) >> 2) & 1) == 0); const int d = rope ? (p >> 1) + 64 * (p & 1) : p; return blk * 128 + d; }
;     if (c < OFF_Z) return c + 2096;
;     if (c < OFF_G) return c - 4048;
;     if (c < OFF_DT) return 5120 + (c - OFF_G);
;     if (c < NSRC) return c;
;     return -1;
; }
;     const int pr = item >> 1, kb = 2 * (pr / nblk) + (item & 1), nb = pr % nblk, k0 = 64 * kb, n0 = 32 * nb;
;     const int nr = n0 + (lane & 31); const int sc = MAP == 1 ? src_col_in(nr) : nr;
;     float v[32];
; #pragma unroll
;     for (int i = 0; i < 32; ++i) v[i] = sc >= 0 ? W[(size_t)(k0 + 2 * i + (lane >> 5)) * Nsrc + sc] : 0.f;
; #pragma unroll
;     for (int i = 0; i < 32; ++i) { const int k = k0 + 2 * i + (lane >> 5); float x = v[i] * wscale; if (KS) x *= (k < ksplit ? ksA[k] : ksB[k - ksplit]); scr[(2 * i + (lane >> 5)) * 33 + (lane & 31)] = x; }
;     LDS_WAIT(); asm volatile("" ::: "memory");
;     const int c = lane & 7;
; #pragma unroll
;     for (int j = 0; j < 4; ++j) { const int n = (lane >> 3) + 8 * j; const LAS float* s = scr + (8 * c) * 33 + n;
;         const unsigned long long o = (unsigned long long)pg8::pk4_fp8(s[0 * 33], s[1 * 33], s[2 * 33], s[3 * 33]) | ((unsigned long long)pg8::pk4_fp8(s[4 * 33], s[5 * 33], s[6 * 33], s[7 * 33]) << 32);
;         *(GAS unsigned long long*)(WT + (size_t)(n0 + n) * K + k0 + 8 * c) = o; }
;     LDS_WAIT(); asm volatile("" ::: "memory");
; }
	s_add_i32 s24, s23, 72
	s_lshl_b32 s20, s24, 7
	s_cmp_lt_u32 s24, 40
	s_cselect_b32 s21, 0, 0x830
	s_cmp_lt_u32 s24, 72
	s_cselect_b32 s21, s21, 0xfffff030
	s_add_i32 s20, s20, s21
	s_lshl_b32 s20, s20, 2
	s_add_u32 s8, s50, s20
	s_addc_u32 s9, s51, 0
	global_load_dwordx4 v[144:147], v76, s[8:9]
	s_add_u32 s8, s8, 0x16280
	s_addc_u32 s9, s9, 0
	global_load_dwordx4 v[148:151], v76, s[8:9]
	s_add_u32 s8, s8, 0x16280
	s_addc_u32 s9, s9, 0
	global_load_dwordx4 v[152:155], v76, s[8:9]
	s_add_u32 s8, s8, 0x16280
	s_addc_u32 s9, s9, 0
	global_load_dwordx4 v[156:159], v76, s[8:9]
	s_add_u32 s8, s8, 0x16280
	s_addc_u32 s9, s9, 0
	global_load_dwordx4 v[160:163], v76, s[8:9]
	s_add_u32 s8, s8, 0x16280
	s_addc_u32 s9, s9, 0
	global_load_dwordx4 v[164:167], v76, s[8:9]
	s_add_u32 s8, s8, 0x16280
	s_addc_u32 s9, s9, 0
	global_load_dwordx4 v[168:171], v76, s[8:9]
	s_add_u32 s8, s8, 0x16280
	s_addc_u32 s9, s9, 0
	global_load_dwordx4 v[172:175], v76, s[8:9]
	s_add_i32 s24, s23, 56
	s_mul_i32 s20, s24, 0x80000
	s_add_u32 s6, s52, s20
	s_addc_u32 s7, s53, 0
	s_cmp_lt_u32 s24, 16
	s_cselect_b32 s20, 1, 0
	s_sub_i32 s21, s24, 16
	s_bitcmp0_b32 s21, 2
	s_cselect_b32 s21, 1, 0
	s_cmp_lt_u32 s24, 40
	s_cselect_b32 s21, s21, 0
	s_or_b32 s20, s20, s21
	s_cmp_lg_u32 s20, 0
	s_cselect_b64 s[20:21], -1, 0
	v_cndmask_b32_e64 v91, v77, v81, s[20:21]
	v_cndmask_b32_e64 v92, v78, v82, s[20:21]
	ds_read_b32 v226, v211
	ds_read_b32 v227, v211 offset:512
	ds_read_b32 v228, v211 offset:1024
	ds_read_b32 v229, v211 offset:1536
	ds_read_b32 v230, v211 offset:2048
	ds_read_b32 v231, v211 offset:2560
	ds_read_b32 v232, v211 offset:3072
	ds_read_b32 v233, v211 offset:3584
	ds_read_b32 v234, v211 offset:4096
	ds_read_b32 v235, v211 offset:4608
	ds_read_b32 v236, v211 offset:5120
	ds_read_b32 v237, v211 offset:5632
	ds_read_b32 v238, v211 offset:6144
	ds_read_b32 v239, v211 offset:6656
	ds_read_b32 v240, v211 offset:7168
	ds_read_b32 v241, v211 offset:7680
	s_waitcnt lgkmcnt(0)
	v_max_f32_e32 v226, v226, v226
	v_max_f32_e32 v227, v227, v227
	v_max_f32_e32 v228, v228, v228
	v_max_f32_e32 v229, v229, v229
	v_max_f32_e32 v230, v230, v230
	v_max_f32_e32 v231, v231, v231
	v_max_f32_e32 v232, v232, v232
	v_max_f32_e32 v233, v233, v233
	v_max_f32_e32 v234, v234, v234
	v_max_f32_e32 v235, v235, v235
	v_max_f32_e32 v236, v236, v236
	v_max_f32_e32 v237, v237, v237
	v_max_f32_e32 v238, v238, v238
	v_max_f32_e32 v239, v239, v239
	v_max_f32_e32 v240, v240, v240
	v_max_f32_e32 v241, v241, v241
	v_med3_f32 v226, v226, s62, v95
	v_med3_f32 v227, v227, s62, v95
	v_med3_f32 v228, v228, s62, v95
	v_med3_f32 v229, v229, s62, v95
	v_med3_f32 v230, v230, s62, v95
	v_med3_f32 v231, v231, s62, v95
	v_med3_f32 v232, v232, s62, v95
	v_med3_f32 v233, v233, s62, v95
	v_med3_f32 v234, v234, s62, v95
	v_med3_f32 v235, v235, s62, v95
	v_med3_f32 v236, v236, s62, v95
	v_med3_f32 v237, v237, s62, v95
	v_med3_f32 v238, v238, s62, v95
	v_med3_f32 v239, v239, s62, v95
	v_med3_f32 v240, v240, s62, v95
	v_med3_f32 v241, v241, s62, v95
	v_mov_b32_e32 v242, 0
	v_mov_b32_e32 v243, 0
	v_mov_b32_e32 v244, 0
	v_mov_b32_e32 v245, 0
	v_cvt_pk_fp8_f32 v242, v226, v227
	v_cvt_pk_fp8_f32 v243, v230, v231
	v_cvt_pk_fp8_f32 v244, v234, v235
	v_cvt_pk_fp8_f32 v245, v238, v239
	v_cvt_pk_fp8_f32 v242, v228, v229 op_sel:[0,0,1]
	v_cvt_pk_fp8_f32 v243, v232, v233 op_sel:[0,0,1]
	v_cvt_pk_fp8_f32 v244, v236, v237 op_sel:[0,0,1]
	v_cvt_pk_fp8_f32 v245, v240, v241 op_sel:[0,0,1]
	s_nop 0
	global_store_dwordx4 v91, v[242:245], s[6:7]
	ds_read_b32 v226, v213
	ds_read_b32 v227, v213 offset:512
	ds_read_b32 v228, v213 offset:1024
	ds_read_b32 v229, v213 offset:1536
	ds_read_b32 v230, v213 offset:2048
	ds_read_b32 v231, v213 offset:2560
	ds_read_b32 v232, v213 offset:3072
	ds_read_b32 v233, v213 offset:3584
	ds_read_b32 v234, v213 offset:4096
	ds_read_b32 v235, v213 offset:4608
	ds_read_b32 v236, v213 offset:5120
	ds_read_b32 v237, v213 offset:5632
	ds_read_b32 v238, v213 offset:6144
	ds_read_b32 v239, v213 offset:6656
	ds_read_b32 v240, v213 offset:7168
	ds_read_b32 v241, v213 offset:7680
	s_waitcnt lgkmcnt(0)
	v_max_f32_e32 v226, v226, v226
	v_max_f32_e32 v227, v227, v227
	v_max_f32_e32 v228, v228, v228
	v_max_f32_e32 v229, v229, v229
	v_max_f32_e32 v230, v230, v230
	v_max_f32_e32 v231, v231, v231
	v_max_f32_e32 v232, v232, v232
	v_max_f32_e32 v233, v233, v233
	v_max_f32_e32 v234, v234, v234
	v_max_f32_e32 v235, v235, v235
	v_max_f32_e32 v236, v236, v236
	v_max_f32_e32 v237, v237, v237
	v_max_f32_e32 v238, v238, v238
	v_max_f32_e32 v239, v239, v239
	v_max_f32_e32 v240, v240, v240
	v_max_f32_e32 v241, v241, v241
	v_med3_f32 v226, v226, s62, v95
	v_med3_f32 v227, v227, s62, v95
	v_med3_f32 v228, v228, s62, v95
	v_med3_f32 v229, v229, s62, v95
	v_med3_f32 v230, v230, s62, v95
	v_med3_f32 v231, v231, s62, v95
	v_med3_f32 v232, v232, s62, v95
	v_med3_f32 v233, v233, s62, v95
	v_med3_f32 v234, v234, s62, v95
	v_med3_f32 v235, v235, s62, v95
	v_med3_f32 v236, v236, s62, v95
	v_med3_f32 v237, v237, s62, v95
	v_med3_f32 v238, v238, s62, v95
	v_med3_f32 v239, v239, s62, v95
	v_med3_f32 v240, v240, s62, v95
	v_med3_f32 v241, v241, s62, v95
	v_mov_b32_e32 v242, 0
	v_mov_b32_e32 v243, 0
	v_mov_b32_e32 v244, 0
	v_mov_b32_e32 v245, 0
	v_cvt_pk_fp8_f32 v242, v226, v227
	v_cvt_pk_fp8_f32 v243, v230, v231
	v_cvt_pk_fp8_f32 v244, v234, v235
	v_cvt_pk_fp8_f32 v245, v238, v239
	v_cvt_pk_fp8_f32 v242, v228, v229 op_sel:[0,0,1]
	v_cvt_pk_fp8_f32 v243, v232, v233 op_sel:[0,0,1]
	v_cvt_pk_fp8_f32 v244, v236, v237 op_sel:[0,0,1]
	v_cvt_pk_fp8_f32 v245, v240, v241 op_sel:[0,0,1]
	s_nop 0
	global_store_dwordx4 v92, v[242:245], s[6:7]
	s_waitcnt vmcnt(12)
	v_mul_f32_e32 v176, v50, v176
	v_mul_f32_e32 v177, v50, v177
	v_mul_f32_e32 v178, v50, v178
	v_mul_f32_e32 v179, v50, v179
	ds_write_b128 v210, v[176:179]
	v_mul_f32_e32 v180, v51, v180
	v_mul_f32_e32 v181, v51, v181
	v_mul_f32_e32 v182, v51, v182
	v_mul_f32_e32 v183, v51, v183
	ds_write_b128 v210, v[180:183] offset:1024
	v_mul_f32_e32 v184, v52, v184
	v_mul_f32_e32 v185, v52, v185
	v_mul_f32_e32 v186, v52, v186
	v_mul_f32_e32 v187, v52, v187
	ds_write_b128 v210, v[184:187] offset:2048
	v_mul_f32_e32 v188, v53, v188
	v_mul_f32_e32 v189, v53, v189
	v_mul_f32_e32 v190, v53, v190
	v_mul_f32_e32 v191, v53, v191
	ds_write_b128 v210, v[188:191] offset:3072
	v_mul_f32_e32 v192, v54, v192
	v_mul_f32_e32 v193, v54, v193
	v_mul_f32_e32 v194, v54, v194
	v_mul_f32_e32 v195, v54, v195
	ds_write_b128 v210, v[192:195] offset:4096
	v_mul_f32_e32 v196, v55, v196
	v_mul_f32_e32 v197, v55, v197
	v_mul_f32_e32 v198, v55, v198
	v_mul_f32_e32 v199, v55, v199
	ds_write_b128 v210, v[196:199] offset:5120
	v_mul_f32_e32 v200, v56, v200
	v_mul_f32_e32 v201, v56, v201
	v_mul_f32_e32 v202, v56, v202
	v_mul_f32_e32 v203, v56, v203
	ds_write_b128 v210, v[200:203] offset:6144
	v_mul_f32_e32 v204, v57, v204
	v_mul_f32_e32 v205, v57, v205
	v_mul_f32_e32 v206, v57, v206
	v_mul_f32_e32 v207, v57, v207
	ds_write_b128 v210, v[204:207] offset:7168
	s_waitcnt lgkmcnt(0)
	s_barrier
; #define GAS __attribute__((address_space(1)))
; #define LAS __attribute__((address_space(3)))
; #define LDS_WAIT() asm volatile("s_waitcnt lgkmcnt(0)" ::: "memory")
; __device__ __forceinline__ int src_col_in(int c) {
;     if (c < 5120) { const int blk = c >> 7, p = c & 127; const bool rope = blk < 16 || ((((blk - 16) >> 2) & 1) == 0); const int d = rope ? (p >> 1) + 64 * (p & 1) : p; return blk * 128 + d; }
;     if (c < OFF_Z) return c + 2096;
;     if (c < OFF_G) return c - 4048;
;     if (c < OFF_DT) return 5120 + (c - OFF_G);
;     if (c < NSRC) return c;
;     return -1;
; }
;     const int pr = item >> 1, kb = 2 * (pr / nblk) + (item & 1), nb = pr % nblk, k0 = 64 * kb, n0 = 32 * nb;
;     const int nr = n0 + (lane & 31); const int sc = MAP == 1 ? src_col_in(nr) : nr;
;     float v[32];
; #pragma unroll
;     for (int i = 0; i < 32; ++i) v[i] = sc >= 0 ? W[(size_t)(k0 + 2 * i + (lane >> 5)) * Nsrc + sc] : 0.f;
; #pragma unroll
;     for (int i = 0; i < 32; ++i) { const int k = k0 + 2 * i + (lane >> 5); float x = v[i] * wscale; if (KS) x *= (k < ksplit ? ksA[k] : ksB[k - ksplit]); scr[(2 * i + (lane >> 5)) * 33 + (lane & 31)] = x; }
;     LDS_WAIT(); asm volatile("" ::: "memory");
;     const int c = lane & 7;
; #pragma unroll
;     for (int j = 0; j < 4; ++j) { const int n = (lane >> 3) + 8 * j; const LAS float* s = scr + (8 * c) * 33 + n;
;         const unsigned long long o = (unsigned long long)pg8::pk4_fp8(s[0 * 33], s[1 * 33], s[2 * 33], s[3 * 33]) | ((unsigned long long)pg8::pk4_fp8(s[4 * 33], s[5 * 33], s[6 * 33], s[7 * 33]) << 32);
;         *(GAS unsigned long long*)(WT + (size_t)(n0 + n) * K + k0 + 8 * c) = o; }
;     LDS_WAIT(); asm volatile("" ::: "memory");
; }
	s_add_i32 s24, s23, 80
	s_lshl_b32 s20, s24, 7
	s_cmp_lt_u32 s24, 40
	s_cselect_b32 s21, 0, 0x830
	s_cmp_lt_u32 s24, 72
	s_cselect_b32 s21, s21, 0xfffff030
	s_add_i32 s20, s20, s21
	s_lshl_b32 s20, s20, 2
	s_add_u32 s8, s50, s20
	s_addc_u32 s9, s51, 0
	global_load_dwordx4 v[176:179], v76, s[8:9]
	s_add_u32 s8, s8, 0x16280
	s_addc_u32 s9, s9, 0
	global_load_dwordx4 v[180:183], v76, s[8:9]
	s_add_u32 s8, s8, 0x16280
	s_addc_u32 s9, s9, 0
	global_load_dwordx4 v[184:187], v76, s[8:9]
	s_add_u32 s8, s8, 0x16280
	s_addc_u32 s9, s9, 0
	global_load_dwordx4 v[188:191], v76, s[8:9]
	s_add_u32 s8, s8, 0x16280
	s_addc_u32 s9, s9, 0
	global_load_dwordx4 v[192:195], v76, s[8:9]
	s_add_u32 s8, s8, 0x16280
	s_addc_u32 s9, s9, 0
	global_load_dwordx4 v[196:199], v76, s[8:9]
	s_add_u32 s8, s8, 0x16280
	s_addc_u32 s9, s9, 0
	global_load_dwordx4 v[200:203], v76, s[8:9]
	s_add_u32 s8, s8, 0x16280
	s_addc_u32 s9, s9, 0
	global_load_dwordx4 v[204:207], v76, s[8:9]
	s_add_i32 s24, s23, 64
	s_mul_i32 s20, s24, 0x80000
	s_add_u32 s6, s52, s20
	s_addc_u32 s7, s53, 0
	s_cmp_lt_u32 s24, 16
	s_cselect_b32 s20, 1, 0
	s_sub_i32 s21, s24, 16
	s_bitcmp0_b32 s21, 2
	s_cselect_b32 s21, 1, 0
	s_cmp_lt_u32 s24, 40
	s_cselect_b32 s21, s21, 0
	s_or_b32 s20, s20, s21
	s_cmp_lg_u32 s20, 0
	s_cselect_b64 s[20:21], -1, 0
	v_cndmask_b32_e64 v91, v77, v81, s[20:21]
	v_cndmask_b32_e64 v92, v78, v82, s[20:21]
	ds_read_b32 v226, v212
	ds_read_b32 v227, v212 offset:512
	ds_read_b32 v228, v212 offset:1024
	ds_read_b32 v229, v212 offset:1536
	ds_read_b32 v230, v212 offset:2048
	ds_read_b32 v231, v212 offset:2560
	ds_read_b32 v232, v212 offset:3072
	ds_read_b32 v233, v212 offset:3584
	ds_read_b32 v234, v212 offset:4096
	ds_read_b32 v235, v212 offset:4608
	ds_read_b32 v236, v212 offset:5120
	ds_read_b32 v237, v212 offset:5632
	ds_read_b32 v238, v212 offset:6144
	ds_read_b32 v239, v212 offset:6656
	ds_read_b32 v240, v212 offset:7168
	ds_read_b32 v241, v212 offset:7680
	s_waitcnt lgkmcnt(0)
	v_max_f32_e32 v226, v226, v226
	v_max_f32_e32 v227, v227, v227
	v_max_f32_e32 v228, v228, v228
	v_max_f32_e32 v229, v229, v229
	v_max_f32_e32 v230, v230, v230
	v_max_f32_e32 v231, v231, v231
	v_max_f32_e32 v232, v232, v232
	v_max_f32_e32 v233, v233, v233
	v_max_f32_e32 v234, v234, v234
	v_max_f32_e32 v235, v235, v235
	v_max_f32_e32 v236, v236, v236
	v_max_f32_e32 v237, v237, v237
	v_max_f32_e32 v238, v238, v238
	v_max_f32_e32 v239, v239, v239
	v_max_f32_e32 v240, v240, v240
	v_max_f32_e32 v241, v241, v241
	v_med3_f32 v226, v226, s62, v95
	v_med3_f32 v227, v227, s62, v95
	v_med3_f32 v228, v228, s62, v95
	v_med3_f32 v229, v229, s62, v95
	v_med3_f32 v230, v230, s62, v95
	v_med3_f32 v231, v231, s62, v95
	v_med3_f32 v232, v232, s62, v95
	v_med3_f32 v233, v233, s62, v95
	v_med3_f32 v234, v234, s62, v95
	v_med3_f32 v235, v235, s62, v95
	v_med3_f32 v236, v236, s62, v95
	v_med3_f32 v237, v237, s62, v95
	v_med3_f32 v238, v238, s62, v95
	v_med3_f32 v239, v239, s62, v95
	v_med3_f32 v240, v240, s62, v95
	v_med3_f32 v241, v241, s62, v95
	v_mov_b32_e32 v242, 0
	v_mov_b32_e32 v243, 0
	v_mov_b32_e32 v244, 0
	v_mov_b32_e32 v245, 0
	v_cvt_pk_fp8_f32 v242, v226, v227
	v_cvt_pk_fp8_f32 v243, v230, v231
	v_cvt_pk_fp8_f32 v244, v234, v235
	v_cvt_pk_fp8_f32 v245, v238, v239
	v_cvt_pk_fp8_f32 v242, v228, v229 op_sel:[0,0,1]
	v_cvt_pk_fp8_f32 v243, v232, v233 op_sel:[0,0,1]
	v_cvt_pk_fp8_f32 v244, v236, v237 op_sel:[0,0,1]
	v_cvt_pk_fp8_f32 v245, v240, v241 op_sel:[0,0,1]
	s_nop 0
	global_store_dwordx4 v91, v[242:245], s[6:7]
	ds_read_b32 v226, v214
	ds_read_b32 v227, v214 offset:512
	ds_read_b32 v228, v214 offset:1024
	ds_read_b32 v229, v214 offset:1536
	ds_read_b32 v230, v214 offset:2048
	ds_read_b32 v231, v214 offset:2560
	ds_read_b32 v232, v214 offset:3072
	ds_read_b32 v233, v214 offset:3584
	ds_read_b32 v234, v214 offset:4096
	ds_read_b32 v235, v214 offset:4608
	ds_read_b32 v236, v214 offset:5120
	ds_read_b32 v237, v214 offset:5632
	ds_read_b32 v238, v214 offset:6144
	ds_read_b32 v239, v214 offset:6656
	ds_read_b32 v240, v214 offset:7168
	ds_read_b32 v241, v214 offset:7680
	s_waitcnt lgkmcnt(0)
	v_max_f32_e32 v226, v226, v226
	v_max_f32_e32 v227, v227, v227
	v_max_f32_e32 v228, v228, v228
	v_max_f32_e32 v229, v229, v229
	v_max_f32_e32 v230, v230, v230
	v_max_f32_e32 v231, v231, v231
	v_max_f32_e32 v232, v232, v232
	v_max_f32_e32 v233, v233, v233
	v_max_f32_e32 v234, v234, v234
	v_max_f32_e32 v235, v235, v235
	v_max_f32_e32 v236, v236, v236
	v_max_f32_e32 v237, v237, v237
	v_max_f32_e32 v238, v238, v238
	v_max_f32_e32 v239, v239, v239
	v_max_f32_e32 v240, v240, v240
	v_max_f32_e32 v241, v241, v241
	v_med3_f32 v226, v226, s62, v95
	v_med3_f32 v227, v227, s62, v95
	v_med3_f32 v228, v228, s62, v95
	v_med3_f32 v229, v229, s62, v95
	v_med3_f32 v230, v230, s62, v95
	v_med3_f32 v231, v231, s62, v95
	v_med3_f32 v232, v232, s62, v95
	v_med3_f32 v233, v233, s62, v95
	v_med3_f32 v234, v234, s62, v95
	v_med3_f32 v235, v235, s62, v95
	v_med3_f32 v236, v236, s62, v95
	v_med3_f32 v237, v237, s62, v95
	v_med3_f32 v238, v238, s62, v95
	v_med3_f32 v239, v239, s62, v95
	v_med3_f32 v240, v240, s62, v95
	v_med3_f32 v241, v241, s62, v95
	v_mov_b32_e32 v242, 0
	v_mov_b32_e32 v243, 0
	v_mov_b32_e32 v244, 0
	v_mov_b32_e32 v245, 0
	v_cvt_pk_fp8_f32 v242, v226, v227
	v_cvt_pk_fp8_f32 v243, v230, v231
	v_cvt_pk_fp8_f32 v244, v234, v235
	v_cvt_pk_fp8_f32 v245, v238, v239
	v_cvt_pk_fp8_f32 v242, v228, v229 op_sel:[0,0,1]
	v_cvt_pk_fp8_f32 v243, v232, v233 op_sel:[0,0,1]
	v_cvt_pk_fp8_f32 v244, v236, v237 op_sel:[0,0,1]
	v_cvt_pk_fp8_f32 v245, v240, v241 op_sel:[0,0,1]
	s_nop 0
	global_store_dwordx4 v92, v[242:245], s[6:7]
	s_waitcnt vmcnt(12)
	v_mul_f32_e32 v144, v50, v144
	v_mul_f32_e32 v145, v50, v145
	v_mul_f32_e32 v146, v50, v146
	v_mul_f32_e32 v147, v50, v147
	ds_write_b128 v209, v[144:147]
	v_mul_f32_e32 v148, v51, v148
	v_mul_f32_e32 v149, v51, v149
	v_mul_f32_e32 v150, v51, v150
	v_mul_f32_e32 v151, v51, v151
	ds_write_b128 v209, v[148:151] offset:1024
	v_mul_f32_e32 v152, v52, v152
	v_mul_f32_e32 v153, v52, v153
	v_mul_f32_e32 v154, v52, v154
	v_mul_f32_e32 v155, v52, v155
	ds_write_b128 v209, v[152:155] offset:2048
	v_mul_f32_e32 v156, v53, v156
	v_mul_f32_e32 v157, v53, v157
	v_mul_f32_e32 v158, v53, v158
	v_mul_f32_e32 v159, v53, v159
	ds_write_b128 v209, v[156:159] offset:3072
	v_mul_f32_e32 v160, v54, v160
	v_mul_f32_e32 v161, v54, v161
	v_mul_f32_e32 v162, v54, v162
	v_mul_f32_e32 v163, v54, v163
	ds_write_b128 v209, v[160:163] offset:4096
	v_mul_f32_e32 v164, v55, v164
	v_mul_f32_e32 v165, v55, v165
	v_mul_f32_e32 v166, v55, v166
	v_mul_f32_e32 v167, v55, v167
	ds_write_b128 v209, v[164:167] offset:5120
	v_mul_f32_e32 v168, v56, v168
	v_mul_f32_e32 v169, v56, v169
	v_mul_f32_e32 v170, v56, v170
	v_mul_f32_e32 v171, v56, v171
	ds_write_b128 v209, v[168:171] offset:6144
	v_mul_f32_e32 v172, v57, v172
	v_mul_f32_e32 v173, v57, v173
	v_mul_f32_e32 v174, v57, v174
	v_mul_f32_e32 v175, v57, v175
	ds_write_b128 v209, v[172:175] offset:7168
	s_waitcnt lgkmcnt(0)
	s_barrier
; #define GAS __attribute__((address_space(1)))
; #define LAS __attribute__((address_space(3)))
; #define LDS_WAIT() asm volatile("s_waitcnt lgkmcnt(0)" ::: "memory")
;     const int pr = item >> 1, kb = 2 * (pr / nblk) + (item & 1), nb = pr % nblk, k0 = 64 * kb, n0 = 32 * nb;
;     const int nr = n0 + (lane & 31); const int sc = MAP == 1 ? src_col_in(nr) : nr;
;     float v[32];
; #pragma unroll
;     for (int i = 0; i < 32; ++i) v[i] = sc >= 0 ? W[(size_t)(k0 + 2 * i + (lane >> 5)) * Nsrc + sc] : 0.f;
; #pragma unroll
;     for (int i = 0; i < 32; ++i) { const int k = k0 + 2 * i + (lane >> 5); float x = v[i] * wscale; if (KS) x *= (k < ksplit ? ksA[k] : ksB[k - ksplit]); scr[(2 * i + (lane >> 5)) * 33 + (lane & 31)] = x; }
;     LDS_WAIT(); asm volatile("" ::: "memory");
;     const int c = lane & 7;
; #pragma unroll
;     for (int j = 0; j < 4; ++j) { const int n = (lane >> 3) + 8 * j; const LAS float* s = scr + (8 * c) * 33 + n;
;         const unsigned long long o = (unsigned long long)pg8::pk4_fp8(s[0 * 33], s[1 * 33], s[2 * 33], s[3 * 33]) | ((unsigned long long)pg8::pk4_fp8(s[4 * 33], s[5 * 33], s[6 * 33], s[7 * 33]) << 32);
;         *(GAS unsigned long long*)(WT + (size_t)(n0 + n) * K + k0 + 8 * c) = o; }
;     LDS_WAIT(); asm volatile("" ::: "memory");
; }
; __global__ void __launch_bounds__(NWAVES * 64, 2) hybrid_fwd(Args args) {
;     ...
;             if (r < I_IN) { if (l >= PROJ_F8_FROM) p0_transpose_item_f8<true, 1>(args.in[2] + (size_t)l * DM * NSRC, DM, NSRC, NPROJ / 32, (unsigned char*)(ws + WS_WIN + l * SZ_WIN), WUP8_SCALE, args.in[1] + l * DM, args.in[1] + l * DM, DM, scr, r, lane);
;                 else p0_transpose_item<1, true>(args.in[2] + (size_t)l * DM * NSRC, DM, NSRC, NPROJ / 32, (bf16*)(ws + WS_WIN + l * SZ_WIN), args.in[1] + l * DM, args.in[1] + l * DM, DM, scr, r, lane); continue; } r -= I_IN;
;             if (r < I_O) { if (l >= WO_F8_FROM) p0_transpose_item_f8<true>(args.in[13] + (size_t)l * DM * DM, DM, DM, DM / 32, (unsigned char*)(ws + WS_WO + l * SZ_WO), 64.f, args.in[6] + l * 2048, args.in[12] + l * 2048, 2048, scr, r, lane);
;                 else p0_transpose_item<0, true>(args.in[13] + (size_t)l * DM * DM, DM, DM, DM / 32, (bf16*)(ws + WS_WO + l * SZ_WO), args.in[6] + l * 2048, args.in[12] + l * 2048, 2048, scr, r, lane); continue; } r -= I_O;
	s_mov_b64 s[8:9], s[54:55]
	global_load_dwordx4 v[144:147], v75, s[8:9]
	s_add_u32 s8, s8, 0x8000
	s_addc_u32 s9, s9, 0
	global_load_dwordx4 v[148:151], v75, s[8:9]
	s_add_u32 s8, s8, 0x8000
	s_addc_u32 s9, s9, 0
	global_load_dwordx4 v[152:155], v75, s[8:9]
	s_add_u32 s8, s8, 0x8000
	s_addc_u32 s9, s9, 0
	global_load_dwordx4 v[156:159], v75, s[8:9]
	s_add_u32 s8, s8, 0x8000
	s_addc_u32 s9, s9, 0
	global_load_dwordx4 v[160:163], v75, s[8:9]
	s_add_u32 s8, s8, 0x8000
	s_addc_u32 s9, s9, 0
	global_load_dwordx4 v[164:167], v75, s[8:9]
	s_add_u32 s8, s8, 0x8000
	s_addc_u32 s9, s9, 0
	global_load_dwordx4 v[168:171], v75, s[8:9]
	s_add_u32 s8, s8, 0x8000
	s_addc_u32 s9, s9, 0
	global_load_dwordx4 v[172:175], v75, s[8:9]
	s_add_i32 s24, s23, 72
	s_mul_i32 s20, s24, 0x80000
	s_add_u32 s6, s52, s20
	s_addc_u32 s7, s53, 0
	s_cmp_lt_u32 s24, 16
	s_cselect_b32 s20, 1, 0
	s_sub_i32 s21, s24, 16
	s_bitcmp0_b32 s21, 2
	s_cselect_b32 s21, 1, 0
	s_cmp_lt_u32 s24, 40
	s_cselect_b32 s21, s21, 0
	s_or_b32 s20, s20, s21
	s_cmp_lg_u32 s20, 0
	s_cselect_b64 s[20:21], -1, 0
	v_cndmask_b32_e64 v91, v77, v81, s[20:21]
	v_cndmask_b32_e64 v92, v78, v82, s[20:21]
	ds_read_b32 v226, v211
	ds_read_b32 v227, v211 offset:512
	ds_read_b32 v228, v211 offset:1024
	ds_read_b32 v229, v211 offset:1536
	ds_read_b32 v230, v211 offset:2048
	ds_read_b32 v231, v211 offset:2560
	ds_read_b32 v232, v211 offset:3072
	ds_read_b32 v233, v211 offset:3584
	ds_read_b32 v234, v211 offset:4096
	ds_read_b32 v235, v211 offset:4608
	ds_read_b32 v236, v211 offset:5120
	ds_read_b32 v237, v211 offset:5632
	ds_read_b32 v238, v211 offset:6144
	ds_read_b32 v239, v211 offset:6656
	ds_read_b32 v240, v211 offset:7168
	ds_read_b32 v241, v211 offset:7680
	s_waitcnt lgkmcnt(0)
	v_max_f32_e32 v226, v226, v226
	v_max_f32_e32 v227, v227, v227
	v_max_f32_e32 v228, v228, v228
	v_max_f32_e32 v229, v229, v229
	v_max_f32_e32 v230, v230, v230
	v_max_f32_e32 v231, v231, v231
	v_max_f32_e32 v232, v232, v232
	v_max_f32_e32 v233, v233, v233
	v_max_f32_e32 v234, v234, v234
	v_max_f32_e32 v235, v235, v235
	v_max_f32_e32 v236, v236, v236
	v_max_f32_e32 v237, v237, v237
	v_max_f32_e32 v238, v238, v238
	v_max_f32_e32 v239, v239, v239
	v_max_f32_e32 v240, v240, v240
	v_max_f32_e32 v241, v241, v241
	v_med3_f32 v226, v226, s62, v95
	v_med3_f32 v227, v227, s62, v95
	v_med3_f32 v228, v228, s62, v95
	v_med3_f32 v229, v229, s62, v95
	v_med3_f32 v230, v230, s62, v95
	v_med3_f32 v231, v231, s62, v95
	v_med3_f32 v232, v232, s62, v95
	v_med3_f32 v233, v233, s62, v95
	v_med3_f32 v234, v234, s62, v95
	v_med3_f32 v235, v235, s62, v95
	v_med3_f32 v236, v236, s62, v95
	v_med3_f32 v237, v237, s62, v95
	v_med3_f32 v238, v238, s62, v95
	v_med3_f32 v239, v239, s62, v95
	v_med3_f32 v240, v240, s62, v95
	v_med3_f32 v241, v241, s62, v95
	v_mov_b32_e32 v242, 0
	v_mov_b32_e32 v243, 0
	v_mov_b32_e32 v244, 0
	v_mov_b32_e32 v245, 0
	v_cvt_pk_fp8_f32 v242, v226, v227
	v_cvt_pk_fp8_f32 v243, v230, v231
	v_cvt_pk_fp8_f32 v244, v234, v235
	v_cvt_pk_fp8_f32 v245, v238, v239
	v_cvt_pk_fp8_f32 v242, v228, v229 op_sel:[0,0,1]
	v_cvt_pk_fp8_f32 v243, v232, v233 op_sel:[0,0,1]
	v_cvt_pk_fp8_f32 v244, v236, v237 op_sel:[0,0,1]
	v_cvt_pk_fp8_f32 v245, v240, v241 op_sel:[0,0,1]
	s_nop 0
	global_store_dwordx4 v91, v[242:245], s[6:7]
	ds_read_b32 v226, v213
	ds_read_b32 v227, v213 offset:512
	ds_read_b32 v228, v213 offset:1024
	ds_read_b32 v229, v213 offset:1536
	ds_read_b32 v230, v213 offset:2048
	ds_read_b32 v231, v213 offset:2560
	ds_read_b32 v232, v213 offset:3072
	ds_read_b32 v233, v213 offset:3584
	ds_read_b32 v234, v213 offset:4096
	ds_read_b32 v235, v213 offset:4608
	ds_read_b32 v236, v213 offset:5120
	ds_read_b32 v237, v213 offset:5632
	ds_read_b32 v238, v213 offset:6144
	ds_read_b32 v239, v213 offset:6656
	ds_read_b32 v240, v213 offset:7168
	ds_read_b32 v241, v213 offset:7680
	s_waitcnt lgkmcnt(0)
	v_max_f32_e32 v226, v226, v226
	v_max_f32_e32 v227, v227, v227
	v_max_f32_e32 v228, v228, v228
	v_max_f32_e32 v229, v229, v229
	v_max_f32_e32 v230, v230, v230
	v_max_f32_e32 v231, v231, v231
	v_max_f32_e32 v232, v232, v232
	v_max_f32_e32 v233, v233, v233
	v_max_f32_e32 v234, v234, v234
	v_max_f32_e32 v235, v235, v235
	v_max_f32_e32 v236, v236, v236
	v_max_f32_e32 v237, v237, v237
	v_max_f32_e32 v238, v238, v238
	v_max_f32_e32 v239, v239, v239
	v_max_f32_e32 v240, v240, v240
	v_max_f32_e32 v241, v241, v241
	v_med3_f32 v226, v226, s62, v95
	v_med3_f32 v227, v227, s62, v95
	v_med3_f32 v228, v228, s62, v95
	v_med3_f32 v229, v229, s62, v95
	v_med3_f32 v230, v230, s62, v95
	v_med3_f32 v231, v231, s62, v95
	v_med3_f32 v232, v232, s62, v95
	v_med3_f32 v233, v233, s62, v95
	v_med3_f32 v234, v234, s62, v95
	v_med3_f32 v235, v235, s62, v95
	v_med3_f32 v236, v236, s62, v95
	v_med3_f32 v237, v237, s62, v95
	v_med3_f32 v238, v238, s62, v95
	v_med3_f32 v239, v239, s62, v95
	v_med3_f32 v240, v240, s62, v95
	v_med3_f32 v241, v241, s62, v95
	v_mov_b32_e32 v242, 0
	v_mov_b32_e32 v243, 0
	v_mov_b32_e32 v244, 0
	v_mov_b32_e32 v245, 0
	v_cvt_pk_fp8_f32 v242, v226, v227
	v_cvt_pk_fp8_f32 v243, v230, v231
	v_cvt_pk_fp8_f32 v244, v234, v235
	v_cvt_pk_fp8_f32 v245, v238, v239
	v_cvt_pk_fp8_f32 v242, v228, v229 op_sel:[0,0,1]
	v_cvt_pk_fp8_f32 v243, v232, v233 op_sel:[0,0,1]
	v_cvt_pk_fp8_f32 v244, v236, v237 op_sel:[0,0,1]
	v_cvt_pk_fp8_f32 v245, v240, v241 op_sel:[0,0,1]
	s_nop 0
	global_store_dwordx4 v92, v[242:245], s[6:7]
	s_waitcnt vmcnt(12)
	v_mul_f32_e32 v176, v50, v176
	v_mul_f32_e32 v177, v50, v177
	v_mul_f32_e32 v178, v50, v178
	v_mul_f32_e32 v179, v50, v179
	ds_write_b128 v210, v[176:179]
	v_mul_f32_e32 v180, v51, v180
	v_mul_f32_e32 v181, v51, v181
	v_mul_f32_e32 v182, v51, v182
	v_mul_f32_e32 v183, v51, v183
	ds_write_b128 v210, v[180:183] offset:1024
	v_mul_f32_e32 v184, v52, v184
	v_mul_f32_e32 v185, v52, v185
	v_mul_f32_e32 v186, v52, v186
	v_mul_f32_e32 v187, v52, v187
	ds_write_b128 v210, v[184:187] offset:2048
	v_mul_f32_e32 v188, v53, v188
	v_mul_f32_e32 v189, v53, v189
	v_mul_f32_e32 v190, v53, v190
	v_mul_f32_e32 v191, v53, v191
	ds_write_b128 v210, v[188:191] offset:3072
	v_mul_f32_e32 v192, v54, v192
	v_mul_f32_e32 v193, v54, v193
	v_mul_f32_e32 v194, v54, v194
	v_mul_f32_e32 v195, v54, v195
	ds_write_b128 v210, v[192:195] offset:4096
	v_mul_f32_e32 v196, v55, v196
	v_mul_f32_e32 v197, v55, v197
	v_mul_f32_e32 v198, v55, v198
	v_mul_f32_e32 v199, v55, v199
	ds_write_b128 v210, v[196:199] offset:5120
	v_mul_f32_e32 v200, v56, v200
	v_mul_f32_e32 v201, v56, v201
	v_mul_f32_e32 v202, v56, v202
	v_mul_f32_e32 v203, v56, v203
	ds_write_b128 v210, v[200:203] offset:6144
	v_mul_f32_e32 v204, v57, v204
	v_mul_f32_e32 v205, v57, v205
	v_mul_f32_e32 v206, v57, v206
	v_mul_f32_e32 v207, v57, v207
	ds_write_b128 v210, v[204:207] offset:7168
	s_waitcnt lgkmcnt(0)
	s_barrier
; #define GAS __attribute__((address_space(1)))
; #define LAS __attribute__((address_space(3)))
; #define LDS_WAIT() asm volatile("s_waitcnt lgkmcnt(0)" ::: "memory")
;     const int pr = item >> 1, kb = 2 * (pr / nblk) + (item & 1), nb = pr % nblk, k0 = 64 * kb, n0 = 32 * nb;
;     const int nr = n0 + (lane & 31); const int sc = MAP == 1 ? src_col_in(nr) : nr;
;     float v[32];
; #pragma unroll
;     for (int i = 0; i < 32; ++i) v[i] = sc >= 0 ? W[(size_t)(k0 + 2 * i + (lane >> 5)) * Nsrc + sc] : 0.f;
; #pragma unroll
;     for (int i = 0; i < 32; ++i) { const int k = k0 + 2 * i + (lane >> 5); float x = v[i] * wscale; if (KS) x *= (k < ksplit ? ksA[k] : ksB[k - ksplit]); scr[(2 * i + (lane >> 5)) * 33 + (lane & 31)] = x; }
;     LDS_WAIT(); asm volatile("" ::: "memory");
;     const int c = lane & 7;
; #pragma unroll
;     for (int j = 0; j < 4; ++j) { const int n = (lane >> 3) + 8 * j; const LAS float* s = scr + (8 * c) * 33 + n;
;         const unsigned long long o = (unsigned long long)pg8::pk4_fp8(s[0 * 33], s[1 * 33], s[2 * 33], s[3 * 33]) | ((unsigned long long)pg8::pk4_fp8(s[4 * 33], s[5 * 33], s[6 * 33], s[7 * 33]) << 32);
;         *(GAS unsigned long long*)(WT + (size_t)(n0 + n) * K + k0 + 8 * c) = o; }
;     LDS_WAIT(); asm volatile("" ::: "memory");
; }
; __global__ void __launch_bounds__(NWAVES * 64, 2) hybrid_fwd(Args args) {
;     ...
;             if (r < I_IN) { if (l >= PROJ_F8_FROM) p0_transpose_item_f8<true, 1>(args.in[2] + (size_t)l * DM * NSRC, DM, NSRC, NPROJ / 32, (unsigned char*)(ws + WS_WIN + l * SZ_WIN), WUP8_SCALE, args.in[1] + l * DM, args.in[1] + l * DM, DM, scr, r, lane);
;                 else p0_transpose_item<1, true>(args.in[2] + (size_t)l * DM * NSRC, DM, NSRC, NPROJ / 32, (bf16*)(ws + WS_WIN + l * SZ_WIN), args.in[1] + l * DM, args.in[1] + l * DM, DM, scr, r, lane); continue; } r -= I_IN;
;             if (r < I_O) { if (l >= WO_F8_FROM) p0_transpose_item_f8<true>(args.in[13] + (size_t)l * DM * DM, DM, DM, DM / 32, (unsigned char*)(ws + WS_WO + l * SZ_WO), 64.f, args.in[6] + l * 2048, args.in[12] + l * 2048, 2048, scr, r, lane);
;                 else p0_transpose_item<0, true>(args.in[13] + (size_t)l * DM * DM, DM, DM, DM / 32, (bf16*)(ws + WS_WO + l * SZ_WO), args.in[6] + l * 2048, args.in[12] + l * 2048, 2048, scr, r, lane); continue; } r -= I_O;
	s_add_u32 s8, s54, 0x1000
	s_addc_u32 s9, s55, 0
	global_load_dwordx4 v[176:179], v75, s[8:9]
	s_add_u32 s8, s8, 0x8000
	s_addc_u32 s9, s9, 0
	global_load_dwordx4 v[180:183], v75, s[8:9]
	s_add_u32 s8, s8, 0x8000
	s_addc_u32 s9, s9, 0
	global_load_dwordx4 v[184:187], v75, s[8:9]
	s_add_u32 s8, s8, 0x8000
	s_addc_u32 s9, s9, 0
	global_load_dwordx4 v[188:191], v75, s[8:9]
	s_add_u32 s8, s8, 0x8000
	s_addc_u32 s9, s9, 0
	global_load_dwordx4 v[192:195], v75, s[8:9]
	s_add_u32 s8, s8, 0x8000
	s_addc_u32 s9, s9, 0
	global_load_dwordx4 v[196:199], v75, s[8:9]
	s_add_u32 s8, s8, 0x8000
	s_addc_u32 s9, s9, 0
	global_load_dwordx4 v[200:203], v75, s[8:9]
	s_add_u32 s8, s8, 0x8000
	s_addc_u32 s9, s9, 0
	global_load_dwordx4 v[204:207], v75, s[8:9]
	s_add_i32 s24, s23, 80
	s_mul_i32 s20, s24, 0x80000
	s_add_u32 s6, s52, s20
	s_addc_u32 s7, s53, 0
	s_cmp_lt_u32 s24, 16
	s_cselect_b32 s20, 1, 0
	s_sub_i32 s21, s24, 16
	s_bitcmp0_b32 s21, 2
	s_cselect_b32 s21, 1, 0
	s_cmp_lt_u32 s24, 40
	s_cselect_b32 s21, s21, 0
	s_or_b32 s20, s20, s21
	s_cmp_lg_u32 s20, 0
	s_cselect_b64 s[20:21], -1, 0
	v_cndmask_b32_e64 v91, v77, v81, s[20:21]
	v_cndmask_b32_e64 v92, v78, v82, s[20:21]
	ds_read_b32 v226, v212
	ds_read_b32 v227, v212 offset:512
	ds_read_b32 v228, v212 offset:1024
	ds_read_b32 v229, v212 offset:1536
	ds_read_b32 v230, v212 offset:2048
	ds_read_b32 v231, v212 offset:2560
	ds_read_b32 v232, v212 offset:3072
	ds_read_b32 v233, v212 offset:3584
	ds_read_b32 v234, v212 offset:4096
	ds_read_b32 v235, v212 offset:4608
	ds_read_b32 v236, v212 offset:5120
	ds_read_b32 v237, v212 offset:5632
	ds_read_b32 v238, v212 offset:6144
	ds_read_b32 v239, v212 offset:6656
	ds_read_b32 v240, v212 offset:7168
	ds_read_b32 v241, v212 offset:7680
	s_waitcnt lgkmcnt(0)
	v_max_f32_e32 v226, v226, v226
	v_max_f32_e32 v227, v227, v227
	v_max_f32_e32 v228, v228, v228
	v_max_f32_e32 v229, v229, v229
	v_max_f32_e32 v230, v230, v230
	v_max_f32_e32 v231, v231, v231
	v_max_f32_e32 v232, v232, v232
	v_max_f32_e32 v233, v233, v233
	v_max_f32_e32 v234, v234, v234
	v_max_f32_e32 v235, v235, v235
	v_max_f32_e32 v236, v236, v236
	v_max_f32_e32 v237, v237, v237
	v_max_f32_e32 v238, v238, v238
	v_max_f32_e32 v239, v239, v239
	v_max_f32_e32 v240, v240, v240
	v_max_f32_e32 v241, v241, v241
	v_med3_f32 v226, v226, s62, v95
	v_med3_f32 v227, v227, s62, v95
	v_med3_f32 v228, v228, s62, v95
	v_med3_f32 v229, v229, s62, v95
	v_med3_f32 v230, v230, s62, v95
	v_med3_f32 v231, v231, s62, v95
	v_med3_f32 v232, v232, s62, v95
	v_med3_f32 v233, v233, s62, v95
	v_med3_f32 v234, v234, s62, v95
	v_med3_f32 v235, v235, s62, v95
	v_med3_f32 v236, v236, s62, v95
	v_med3_f32 v237, v237, s62, v95
	v_med3_f32 v238, v238, s62, v95
	v_med3_f32 v239, v239, s62, v95
	v_med3_f32 v240, v240, s62, v95
	v_med3_f32 v241, v241, s62, v95
	v_mov_b32_e32 v242, 0
	v_mov_b32_e32 v243, 0
	v_mov_b32_e32 v244, 0
	v_mov_b32_e32 v245, 0
	v_cvt_pk_fp8_f32 v242, v226, v227
	v_cvt_pk_fp8_f32 v243, v230, v231
	v_cvt_pk_fp8_f32 v244, v234, v235
	v_cvt_pk_fp8_f32 v245, v238, v239
	v_cvt_pk_fp8_f32 v242, v228, v229 op_sel:[0,0,1]
	v_cvt_pk_fp8_f32 v243, v232, v233 op_sel:[0,0,1]
	v_cvt_pk_fp8_f32 v244, v236, v237 op_sel:[0,0,1]
	v_cvt_pk_fp8_f32 v245, v240, v241 op_sel:[0,0,1]
	s_nop 0
	global_store_dwordx4 v91, v[242:245], s[6:7]
	ds_read_b32 v226, v214
	ds_read_b32 v227, v214 offset:512
	ds_read_b32 v228, v214 offset:1024
	ds_read_b32 v229, v214 offset:1536
	ds_read_b32 v230, v214 offset:2048
	ds_read_b32 v231, v214 offset:2560
	ds_read_b32 v232, v214 offset:3072
	ds_read_b32 v233, v214 offset:3584
	ds_read_b32 v234, v214 offset:4096
	ds_read_b32 v235, v214 offset:4608
	ds_read_b32 v236, v214 offset:5120
	ds_read_b32 v237, v214 offset:5632
	ds_read_b32 v238, v214 offset:6144
	ds_read_b32 v239, v214 offset:6656
	ds_read_b32 v240, v214 offset:7168
	ds_read_b32 v241, v214 offset:7680
	s_waitcnt lgkmcnt(0)
	v_max_f32_e32 v226, v226, v226
	v_max_f32_e32 v227, v227, v227
	v_max_f32_e32 v228, v228, v228
	v_max_f32_e32 v229, v229, v229
	v_max_f32_e32 v230, v230, v230
	v_max_f32_e32 v231, v231, v231
	v_max_f32_e32 v232, v232, v232
	v_max_f32_e32 v233, v233, v233
	v_max_f32_e32 v234, v234, v234
	v_max_f32_e32 v235, v235, v235
	v_max_f32_e32 v236, v236, v236
	v_max_f32_e32 v237, v237, v237
	v_max_f32_e32 v238, v238, v238
	v_max_f32_e32 v239, v239, v239
	v_max_f32_e32 v240, v240, v240
	v_max_f32_e32 v241, v241, v241
	v_med3_f32 v226, v226, s62, v95
	v_med3_f32 v227, v227, s62, v95
	v_med3_f32 v228, v228, s62, v95
	v_med3_f32 v229, v229, s62, v95
	v_med3_f32 v230, v230, s62, v95
	v_med3_f32 v231, v231, s62, v95
	v_med3_f32 v232, v232, s62, v95
	v_med3_f32 v233, v233, s62, v95
	v_med3_f32 v234, v234, s62, v95
	v_med3_f32 v235, v235, s62, v95
	v_med3_f32 v236, v236, s62, v95
	v_med3_f32 v237, v237, s62, v95
	v_med3_f32 v238, v238, s62, v95
	v_med3_f32 v239, v239, s62, v95
	v_med3_f32 v240, v240, s62, v95
	v_med3_f32 v241, v241, s62, v95
	v_mov_b32_e32 v242, 0
	v_mov_b32_e32 v243, 0
	v_mov_b32_e32 v244, 0
	v_mov_b32_e32 v245, 0
	v_cvt_pk_fp8_f32 v242, v226, v227
	v_cvt_pk_fp8_f32 v243, v230, v231
	v_cvt_pk_fp8_f32 v244, v234, v235
	v_cvt_pk_fp8_f32 v245, v238, v239
	v_cvt_pk_fp8_f32 v242, v228, v229 op_sel:[0,0,1]
	v_cvt_pk_fp8_f32 v243, v232, v233 op_sel:[0,0,1]
	v_cvt_pk_fp8_f32 v244, v236, v237 op_sel:[0,0,1]
	v_cvt_pk_fp8_f32 v245, v240, v241 op_sel:[0,0,1]
	s_nop 0
	global_store_dwordx4 v92, v[242:245], s[6:7]
	s_waitcnt vmcnt(12)
	v_mul_f32_e32 v144, v58, v144
	v_mul_f32_e32 v145, v58, v145
	v_mul_f32_e32 v146, v58, v146
	v_mul_f32_e32 v147, v58, v147
	ds_write_b128 v209, v[144:147]
	v_mul_f32_e32 v148, v59, v148
	v_mul_f32_e32 v149, v59, v149
	v_mul_f32_e32 v150, v59, v150
	v_mul_f32_e32 v151, v59, v151
	ds_write_b128 v209, v[148:151] offset:1024
	v_mul_f32_e32 v152, v60, v152
	v_mul_f32_e32 v153, v60, v153
	v_mul_f32_e32 v154, v60, v154
	v_mul_f32_e32 v155, v60, v155
	ds_write_b128 v209, v[152:155] offset:2048
	v_mul_f32_e32 v156, v61, v156
	v_mul_f32_e32 v157, v61, v157
	v_mul_f32_e32 v158, v61, v158
	v_mul_f32_e32 v159, v61, v159
	ds_write_b128 v209, v[156:159] offset:3072
	v_mul_f32_e32 v160, v62, v160
	v_mul_f32_e32 v161, v62, v161
	v_mul_f32_e32 v162, v62, v162
	v_mul_f32_e32 v163, v62, v163
	ds_write_b128 v209, v[160:163] offset:4096
	v_mul_f32_e32 v164, v63, v164
	v_mul_f32_e32 v165, v63, v165
	v_mul_f32_e32 v166, v63, v166
	v_mul_f32_e32 v167, v63, v167
	ds_write_b128 v209, v[164:167] offset:5120
	v_mul_f32_e32 v168, v64, v168
	v_mul_f32_e32 v169, v64, v169
	v_mul_f32_e32 v170, v64, v170
	v_mul_f32_e32 v171, v64, v171
	ds_write_b128 v209, v[168:171] offset:6144
	v_mul_f32_e32 v172, v65, v172
	v_mul_f32_e32 v173, v65, v173
	v_mul_f32_e32 v174, v65, v174
	v_mul_f32_e32 v175, v65, v175
	ds_write_b128 v209, v[172:175] offset:7168
	s_waitcnt lgkmcnt(0)
	s_barrier
; #define GAS __attribute__((address_space(1)))
; #define LAS __attribute__((address_space(3)))
; #define LDS_WAIT() asm volatile("s_waitcnt lgkmcnt(0)" ::: "memory")
; __device__ __forceinline__ unsigned pk2(float lo, float hi) { return f2bf(lo) | (f2bf(hi) << 16); }
; __device__ __forceinline__ int nat_dim(int p) { return (p >> 1) + 64 * (p & 1); }
; template <int MAP, bool KS, bool KPERM = false>
; __device__ __forceinline__ void p0_transpose_item(const float* W, int K, int Nsrc, int nblk, bf16* WT, const float* ksA, const float* ksB, int ksplit, LAS float* scr, int item, int lane) {
;     const int kb = item / nblk, nb = item % nblk, k0 = 64 * kb, n0 = 32 * nb;
;     const int nr = n0 + (lane & 31); const int sc = MAP == 1 ? src_col_in(nr) : (MAP == 2 ? nat_dim(nr) : nr);
;     float v[32];
; #pragma unroll
;     for (int i = 0; i < 32; ++i) { const int k = k0 + 2 * i + (lane >> 5); const int ksrc = KPERM ? ((k & ~127) + nat_dim(k & 127)) : k;
;         v[i] = sc >= 0 ? W[(size_t)ksrc * Nsrc + sc] : 0.f; }
; #pragma unroll
;     for (int i = 0; i < 32; ++i) { const int kk = 2 * i + (lane >> 5); const int k = k0 + kk;
;         if (KS) v[i] *= (k < ksplit ? ksA[k] : ksB[k - ksplit]);
;         scr[kk * 33 + (lane & 31)] = v[i]; }
;     LDS_WAIT(); asm volatile("" ::: "memory");
;     const int c = lane & 7;
; #pragma unroll
;     for (int j = 0; j < 4; ++j) { const int n = (lane >> 3) + 8 * j; const LAS float* s = scr + (8 * c) * 33 + n;
;         v4u o; o.x = pk2(s[0 * 33], s[1 * 33]); o.y = pk2(s[2 * 33], s[3 * 33]); o.z = pk2(s[4 * 33], s[5 * 33]); o.w = pk2(s[6 * 33], s[7 * 33]);
;         *(GAS v4u*)(WT + (size_t)(n0 + n) * K + k0 + 8 * c) = o; }
;     LDS_WAIT(); asm volatile("" ::: "memory");
; }
; __global__ void __launch_bounds__(NWAVES * 64, 2) hybrid_fwd(Args args) {
;     ...
;             if (r < I_O) { if (l >= WO_F8_FROM) p0_transpose_item_f8<true>(args.in[13] + (size_t)l * DM * DM, DM, DM, DM / 32, (unsigned char*)(ws + WS_WO + l * SZ_WO), 64.f, args.in[6] + l * 2048, args.in[12] + l * 2048, 2048, scr, r, lane);
;                 else p0_transpose_item<0, true>(args.in[13] + (size_t)l * DM * DM, DM, DM, DM / 32, (bf16*)(ws + WS_WO + l * SZ_WO), args.in[6] + l * 2048, args.in[12] + l * 2048, 2048, scr, r, lane); continue; } r -= I_O;
	s_add_u32 s8, s54, 0x2000
	s_addc_u32 s9, s55, 0
	global_load_dwordx4 v[144:147], v75, s[8:9]
	s_add_u32 s8, s8, 0x8000
	s_addc_u32 s9, s9, 0
	global_load_dwordx4 v[148:151], v75, s[8:9]
	s_add_u32 s8, s8, 0x8000
	s_addc_u32 s9, s9, 0
	global_load_dwordx4 v[152:155], v75, s[8:9]
	s_add_u32 s8, s8, 0x8000
	s_addc_u32 s9, s9, 0
	global_load_dwordx4 v[156:159], v75, s[8:9]
	s_add_u32 s8, s8, 0x8000
	s_addc_u32 s9, s9, 0
	global_load_dwordx4 v[160:163], v75, s[8:9]
	s_add_u32 s8, s8, 0x8000
	s_addc_u32 s9, s9, 0
	global_load_dwordx4 v[164:167], v75, s[8:9]
	s_add_u32 s8, s8, 0x8000
	s_addc_u32 s9, s9, 0
	global_load_dwordx4 v[168:171], v75, s[8:9]
	s_add_u32 s8, s8, 0x8000
	s_addc_u32 s9, s9, 0
	global_load_dwordx4 v[172:175], v75, s[8:9]
	s_mov_b64 s[6:7], s[56:57]
	ds_read_b32 v226, v112
	ds_read_b32 v227, v112 offset:512
	ds_read_b32 v228, v112 offset:1024
	ds_read_b32 v229, v112 offset:1536
	ds_read_b32 v230, v112 offset:2048
	ds_read_b32 v231, v112 offset:2560
	ds_read_b32 v232, v112 offset:3072
	ds_read_b32 v233, v112 offset:3584
	s_waitcnt lgkmcnt(0)
	v_bfe_u32 v120, v226, 16, 1
	v_bfe_u32 v121, v227, 16, 1
	v_bfe_u32 v122, v228, 16, 1
	v_bfe_u32 v123, v229, 16, 1
	v_bfe_u32 v124, v230, 16, 1
	v_bfe_u32 v125, v231, 16, 1
	v_bfe_u32 v126, v232, 16, 1
	v_bfe_u32 v127, v233, 16, 1
	v_add3_u32 v226, v226, v120, s63
	v_add3_u32 v227, v227, v121, s63
	v_add3_u32 v228, v228, v122, s63
	v_add3_u32 v229, v229, v123, s63
	v_add3_u32 v230, v230, v124, s63
	v_add3_u32 v231, v231, v125, s63
	v_add3_u32 v232, v232, v126, s63
	v_add3_u32 v233, v233, v127, s63
	v_perm_b32 v242, v227, v226, s64
	v_perm_b32 v243, v229, v228, s64
	v_perm_b32 v244, v231, v230, s64
	v_perm_b32 v245, v233, v232, s64
	s_nop 0
	global_store_dwordx4 v83, v[242:245], s[6:7]
	ds_read_b32 v226, v114
	ds_read_b32 v227, v114 offset:512
	ds_read_b32 v228, v114 offset:1024
	ds_read_b32 v229, v114 offset:1536
	ds_read_b32 v230, v114 offset:2048
	ds_read_b32 v231, v114 offset:2560
	ds_read_b32 v232, v114 offset:3072
	ds_read_b32 v233, v114 offset:3584
	s_waitcnt lgkmcnt(0)
	v_bfe_u32 v120, v226, 16, 1
	v_bfe_u32 v121, v227, 16, 1
	v_bfe_u32 v122, v228, 16, 1
	v_bfe_u32 v123, v229, 16, 1
	v_bfe_u32 v124, v230, 16, 1
	v_bfe_u32 v125, v231, 16, 1
	v_bfe_u32 v126, v232, 16, 1
	v_bfe_u32 v127, v233, 16, 1
	v_add3_u32 v226, v226, v120, s63
	v_add3_u32 v227, v227, v121, s63
	v_add3_u32 v228, v228, v122, s63
	v_add3_u32 v229, v229, v123, s63
	v_add3_u32 v230, v230, v124, s63
	v_add3_u32 v231, v231, v125, s63
	v_add3_u32 v232, v232, v126, s63
	v_add3_u32 v233, v233, v127, s63
	v_perm_b32 v242, v227, v226, s64
	v_perm_b32 v243, v229, v228, s64
	v_perm_b32 v244, v231, v230, s64
	v_perm_b32 v245, v233, v232, s64
	s_nop 0
	global_store_dwordx4 v84, v[242:245], s[6:7]
	ds_read_b32 v226, v116
	ds_read_b32 v227, v116 offset:512
	ds_read_b32 v228, v116 offset:1024
	ds_read_b32 v229, v116 offset:1536
	ds_read_b32 v230, v116 offset:2048
	ds_read_b32 v231, v116 offset:2560
	ds_read_b32 v232, v116 offset:3072
	ds_read_b32 v233, v116 offset:3584
	s_waitcnt lgkmcnt(0)
	v_bfe_u32 v120, v226, 16, 1
	v_bfe_u32 v121, v227, 16, 1
	v_bfe_u32 v122, v228, 16, 1
	v_bfe_u32 v123, v229, 16, 1
	v_bfe_u32 v124, v230, 16, 1
	v_bfe_u32 v125, v231, 16, 1
	v_bfe_u32 v126, v232, 16, 1
	v_bfe_u32 v127, v233, 16, 1
	v_add3_u32 v226, v226, v120, s63
	v_add3_u32 v227, v227, v121, s63
	v_add3_u32 v228, v228, v122, s63
	v_add3_u32 v229, v229, v123, s63
	v_add3_u32 v230, v230, v124, s63
	v_add3_u32 v231, v231, v125, s63
	v_add3_u32 v232, v232, v126, s63
	v_add3_u32 v233, v233, v127, s63
	v_perm_b32 v242, v227, v226, s64
	v_perm_b32 v243, v229, v228, s64
	v_perm_b32 v244, v231, v230, s64
	v_perm_b32 v245, v233, v232, s64
	s_nop 0
	global_store_dwordx4 v85, v[242:245], s[6:7]
	ds_read_b32 v226, v118
	ds_read_b32 v227, v118 offset:512
	ds_read_b32 v228, v118 offset:1024
	ds_read_b32 v229, v118 offset:1536
	ds_read_b32 v230, v118 offset:2048
	ds_read_b32 v231, v118 offset:2560
	ds_read_b32 v232, v118 offset:3072
	ds_read_b32 v233, v118 offset:3584
	s_waitcnt lgkmcnt(0)
	v_bfe_u32 v120, v226, 16, 1
	v_bfe_u32 v121, v227, 16, 1
	v_bfe_u32 v122, v228, 16, 1
	v_bfe_u32 v123, v229, 16, 1
	v_bfe_u32 v124, v230, 16, 1
	v_bfe_u32 v125, v231, 16, 1
	v_bfe_u32 v126, v232, 16, 1
	v_bfe_u32 v127, v233, 16, 1
	v_add3_u32 v226, v226, v120, s63
	v_add3_u32 v227, v227, v121, s63
	v_add3_u32 v228, v228, v122, s63
	v_add3_u32 v229, v229, v123, s63
	v_add3_u32 v230, v230, v124, s63
	v_add3_u32 v231, v231, v125, s63
	v_add3_u32 v232, v232, v126, s63
	v_add3_u32 v233, v233, v127, s63
	v_perm_b32 v242, v227, v226, s64
	v_perm_b32 v243, v229, v228, s64
	v_perm_b32 v244, v231, v230, s64
	v_perm_b32 v245, v233, v232, s64
	s_nop 0
	global_store_dwordx4 v86, v[242:245], s[6:7]
	s_waitcnt vmcnt(14)
	v_mul_f32_e32 v176, v58, v176
	v_mul_f32_e32 v177, v58, v177
	v_mul_f32_e32 v178, v58, v178
	v_mul_f32_e32 v179, v58, v179
	ds_write_b128 v210, v[176:179]
	v_mul_f32_e32 v180, v59, v180
	v_mul_f32_e32 v181, v59, v181
	v_mul_f32_e32 v182, v59, v182
	v_mul_f32_e32 v183, v59, v183
	ds_write_b128 v210, v[180:183] offset:1024
	v_mul_f32_e32 v184, v60, v184
	v_mul_f32_e32 v185, v60, v185
	v_mul_f32_e32 v186, v60, v186
	v_mul_f32_e32 v187, v60, v187
	ds_write_b128 v210, v[184:187] offset:2048
	v_mul_f32_e32 v188, v61, v188
	v_mul_f32_e32 v189, v61, v189
	v_mul_f32_e32 v190, v61, v190
	v_mul_f32_e32 v191, v61, v191
	ds_write_b128 v210, v[188:191] offset:3072
	v_mul_f32_e32 v192, v62, v192
	v_mul_f32_e32 v193, v62, v193
	v_mul_f32_e32 v194, v62, v194
	v_mul_f32_e32 v195, v62, v195
	ds_write_b128 v210, v[192:195] offset:4096
	v_mul_f32_e32 v196, v63, v196
	v_mul_f32_e32 v197, v63, v197
	v_mul_f32_e32 v198, v63, v198
	v_mul_f32_e32 v199, v63, v199
	ds_write_b128 v210, v[196:199] offset:5120
	v_mul_f32_e32 v200, v64, v200
	v_mul_f32_e32 v201, v64, v201
	v_mul_f32_e32 v202, v64, v202
	v_mul_f32_e32 v203, v64, v203
	ds_write_b128 v210, v[200:203] offset:6144
	v_mul_f32_e32 v204, v65, v204
	v_mul_f32_e32 v205, v65, v205
	v_mul_f32_e32 v206, v65, v206
	v_mul_f32_e32 v207, v65, v207
	ds_write_b128 v210, v[204:207] offset:7168
	s_waitcnt lgkmcnt(0)
	s_barrier
; #define GAS __attribute__((address_space(1)))
; #define LAS __attribute__((address_space(3)))
; #define LDS_WAIT() asm volatile("s_waitcnt lgkmcnt(0)" ::: "memory")
; __device__ __forceinline__ unsigned pk2(float lo, float hi) { return f2bf(lo) | (f2bf(hi) << 16); }
; __device__ __forceinline__ int nat_dim(int p) { return (p >> 1) + 64 * (p & 1); }
; template <int MAP, bool KS, bool KPERM = false>
; __device__ __forceinline__ void p0_transpose_item(const float* W, int K, int Nsrc, int nblk, bf16* WT, const float* ksA, const float* ksB, int ksplit, LAS float* scr, int item, int lane) {
;     const int kb = item / nblk, nb = item % nblk, k0 = 64 * kb, n0 = 32 * nb;
;     const int nr = n0 + (lane & 31); const int sc = MAP == 1 ? src_col_in(nr) : (MAP == 2 ? nat_dim(nr) : nr);
;     float v[32];
; #pragma unroll
;     for (int i = 0; i < 32; ++i) { const int k = k0 + 2 * i + (lane >> 5); const int ksrc = KPERM ? ((k & ~127) + nat_dim(k & 127)) : k;
;         v[i] = sc >= 0 ? W[(size_t)ksrc * Nsrc + sc] : 0.f; }
; #pragma unroll
;     for (int i = 0; i < 32; ++i) { const int kk = 2 * i + (lane >> 5); const int k = k0 + kk;
;         if (KS) v[i] *= (k < ksplit ? ksA[k] : ksB[k - ksplit]);
;         scr[kk * 33 + (lane & 31)] = v[i]; }
;     LDS_WAIT(); asm volatile("" ::: "memory");
;     const int c = lane & 7;
; #pragma unroll
;     for (int j = 0; j < 4; ++j) { const int n = (lane >> 3) + 8 * j; const LAS float* s = scr + (8 * c) * 33 + n;
;         v4u o; o.x = pk2(s[0 * 33], s[1 * 33]); o.y = pk2(s[2 * 33], s[3 * 33]); o.z = pk2(s[4 * 33], s[5 * 33]); o.w = pk2(s[6 * 33], s[7 * 33]);
;         *(GAS v4u*)(WT + (size_t)(n0 + n) * K + k0 + 8 * c) = o; }
;     LDS_WAIT(); asm volatile("" ::: "memory");
; }
; __global__ void __launch_bounds__(NWAVES * 64, 2) hybrid_fwd(Args args) {
;     ...
;             if (r < I_O) { if (l >= WO_F8_FROM) p0_transpose_item_f8<true>(args.in[13] + (size_t)l * DM * DM, DM, DM, DM / 32, (unsigned char*)(ws + WS_WO + l * SZ_WO), 64.f, args.in[6] + l * 2048, args.in[12] + l * 2048, 2048, scr, r, lane);
;                 else p0_transpose_item<0, true>(args.in[13] + (size_t)l * DM * DM, DM, DM, DM / 32, (bf16*)(ws + WS_WO + l * SZ_WO), args.in[6] + l * 2048, args.in[12] + l * 2048, 2048, scr, r, lane); continue; } r -= I_O;
	s_add_u32 s8, s54, 0x3000
	s_addc_u32 s9, s55, 0
	global_load_dwordx4 v[176:179], v75, s[8:9]
	s_add_u32 s8, s8, 0x8000
	s_addc_u32 s9, s9, 0
	global_load_dwordx4 v[180:183], v75, s[8:9]
	s_add_u32 s8, s8, 0x8000
	s_addc_u32 s9, s9, 0
	global_load_dwordx4 v[184:187], v75, s[8:9]
	s_add_u32 s8, s8, 0x8000
	s_addc_u32 s9, s9, 0
	global_load_dwordx4 v[188:191], v75, s[8:9]
	s_add_u32 s8, s8, 0x8000
	s_addc_u32 s9, s9, 0
	global_load_dwordx4 v[192:195], v75, s[8:9]
	s_add_u32 s8, s8, 0x8000
	s_addc_u32 s9, s9, 0
	global_load_dwordx4 v[196:199], v75, s[8:9]
	s_add_u32 s8, s8, 0x8000
	s_addc_u32 s9, s9, 0
	global_load_dwordx4 v[200:203], v75, s[8:9]
	s_add_u32 s8, s8, 0x8000
	s_addc_u32 s9, s9, 0
	global_load_dwordx4 v[204:207], v75, s[8:9]
	s_add_u32 s6, s56, 0x800000
	s_addc_u32 s7, s57, 0
	ds_read_b32 v226, v113
	ds_read_b32 v227, v113 offset:512
	ds_read_b32 v228, v113 offset:1024
	ds_read_b32 v229, v113 offset:1536
	ds_read_b32 v230, v113 offset:2048
	ds_read_b32 v231, v113 offset:2560
	ds_read_b32 v232, v113 offset:3072
	ds_read_b32 v233, v113 offset:3584
	s_waitcnt lgkmcnt(0)
	v_bfe_u32 v120, v226, 16, 1
	v_bfe_u32 v121, v227, 16, 1
	v_bfe_u32 v122, v228, 16, 1
	v_bfe_u32 v123, v229, 16, 1
	v_bfe_u32 v124, v230, 16, 1
	v_bfe_u32 v125, v231, 16, 1
	v_bfe_u32 v126, v232, 16, 1
	v_bfe_u32 v127, v233, 16, 1
	v_add3_u32 v226, v226, v120, s63
	v_add3_u32 v227, v227, v121, s63
	v_add3_u32 v228, v228, v122, s63
	v_add3_u32 v229, v229, v123, s63
	v_add3_u32 v230, v230, v124, s63
	v_add3_u32 v231, v231, v125, s63
	v_add3_u32 v232, v232, v126, s63
	v_add3_u32 v233, v233, v127, s63
	v_perm_b32 v242, v227, v226, s64
	v_perm_b32 v243, v229, v228, s64
	v_perm_b32 v244, v231, v230, s64
	v_perm_b32 v245, v233, v232, s64
	s_nop 0
	global_store_dwordx4 v83, v[242:245], s[6:7]
	ds_read_b32 v226, v115
	ds_read_b32 v227, v115 offset:512
	ds_read_b32 v228, v115 offset:1024
	ds_read_b32 v229, v115 offset:1536
	ds_read_b32 v230, v115 offset:2048
	ds_read_b32 v231, v115 offset:2560
	ds_read_b32 v232, v115 offset:3072
	ds_read_b32 v233, v115 offset:3584
	s_waitcnt lgkmcnt(0)
	v_bfe_u32 v120, v226, 16, 1
	v_bfe_u32 v121, v227, 16, 1
	v_bfe_u32 v122, v228, 16, 1
	v_bfe_u32 v123, v229, 16, 1
	v_bfe_u32 v124, v230, 16, 1
	v_bfe_u32 v125, v231, 16, 1
	v_bfe_u32 v126, v232, 16, 1
	v_bfe_u32 v127, v233, 16, 1
	v_add3_u32 v226, v226, v120, s63
	v_add3_u32 v227, v227, v121, s63
	v_add3_u32 v228, v228, v122, s63
	v_add3_u32 v229, v229, v123, s63
	v_add3_u32 v230, v230, v124, s63
	v_add3_u32 v231, v231, v125, s63
	v_add3_u32 v232, v232, v126, s63
	v_add3_u32 v233, v233, v127, s63
	v_perm_b32 v242, v227, v226, s64
	v_perm_b32 v243, v229, v228, s64
	v_perm_b32 v244, v231, v230, s64
	v_perm_b32 v245, v233, v232, s64
	s_nop 0
	global_store_dwordx4 v84, v[242:245], s[6:7]
	ds_read_b32 v226, v117
	ds_read_b32 v227, v117 offset:512
	ds_read_b32 v228, v117 offset:1024
	ds_read_b32 v229, v117 offset:1536
	ds_read_b32 v230, v117 offset:2048
	ds_read_b32 v231, v117 offset:2560
	ds_read_b32 v232, v117 offset:3072
	ds_read_b32 v233, v117 offset:3584
	s_waitcnt lgkmcnt(0)
	v_bfe_u32 v120, v226, 16, 1
	v_bfe_u32 v121, v227, 16, 1
	v_bfe_u32 v122, v228, 16, 1
	v_bfe_u32 v123, v229, 16, 1
	v_bfe_u32 v124, v230, 16, 1
	v_bfe_u32 v125, v231, 16, 1
	v_bfe_u32 v126, v232, 16, 1
	v_bfe_u32 v127, v233, 16, 1
	v_add3_u32 v226, v226, v120, s63
	v_add3_u32 v227, v227, v121, s63
	v_add3_u32 v228, v228, v122, s63
	v_add3_u32 v229, v229, v123, s63
	v_add3_u32 v230, v230, v124, s63
	v_add3_u32 v231, v231, v125, s63
	v_add3_u32 v232, v232, v126, s63
	v_add3_u32 v233, v233, v127, s63
	v_perm_b32 v242, v227, v226, s64
	v_perm_b32 v243, v229, v228, s64
	v_perm_b32 v244, v231, v230, s64
	v_perm_b32 v245, v233, v232, s64
	s_nop 0
	global_store_dwordx4 v85, v[242:245], s[6:7]
	ds_read_b32 v226, v119
	ds_read_b32 v227, v119 offset:512
	ds_read_b32 v228, v119 offset:1024
	ds_read_b32 v229, v119 offset:1536
	ds_read_b32 v230, v119 offset:2048
	ds_read_b32 v231, v119 offset:2560
	ds_read_b32 v232, v119 offset:3072
	ds_read_b32 v233, v119 offset:3584
	s_waitcnt lgkmcnt(0)
	v_bfe_u32 v120, v226, 16, 1
	v_bfe_u32 v121, v227, 16, 1
	v_bfe_u32 v122, v228, 16, 1
	v_bfe_u32 v123, v229, 16, 1
	v_bfe_u32 v124, v230, 16, 1
	v_bfe_u32 v125, v231, 16, 1
	v_bfe_u32 v126, v232, 16, 1
	v_bfe_u32 v127, v233, 16, 1
	v_add3_u32 v226, v226, v120, s63
	v_add3_u32 v227, v227, v121, s63
	v_add3_u32 v228, v228, v122, s63
	v_add3_u32 v229, v229, v123, s63
	v_add3_u32 v230, v230, v124, s63
	v_add3_u32 v231, v231, v125, s63
	v_add3_u32 v232, v232, v126, s63
	v_add3_u32 v233, v233, v127, s63
	v_perm_b32 v242, v227, v226, s64
	v_perm_b32 v243, v229, v228, s64
	v_perm_b32 v244, v231, v230, s64
	v_perm_b32 v245, v233, v232, s64
	s_nop 0
	global_store_dwordx4 v86, v[242:245], s[6:7]
	s_waitcnt vmcnt(16)
	v_mul_f32_e32 v144, v58, v144
	v_mul_f32_e32 v145, v58, v145
	v_mul_f32_e32 v146, v58, v146
	v_mul_f32_e32 v147, v58, v147
	ds_write_b128 v209, v[144:147]
	v_mul_f32_e32 v148, v59, v148
	v_mul_f32_e32 v149, v59, v149
	v_mul_f32_e32 v150, v59, v150
	v_mul_f32_e32 v151, v59, v151
	ds_write_b128 v209, v[148:151] offset:1024
	v_mul_f32_e32 v152, v60, v152
	v_mul_f32_e32 v153, v60, v153
	v_mul_f32_e32 v154, v60, v154
	v_mul_f32_e32 v155, v60, v155
	ds_write_b128 v209, v[152:155] offset:2048
	v_mul_f32_e32 v156, v61, v156
	v_mul_f32_e32 v157, v61, v157
	v_mul_f32_e32 v158, v61, v158
	v_mul_f32_e32 v159, v61, v159
	ds_write_b128 v209, v[156:159] offset:3072
	v_mul_f32_e32 v160, v62, v160
	v_mul_f32_e32 v161, v62, v161
	v_mul_f32_e32 v162, v62, v162
	v_mul_f32_e32 v163, v62, v163
	ds_write_b128 v209, v[160:163] offset:4096
	v_mul_f32_e32 v164, v63, v164
	v_mul_f32_e32 v165, v63, v165
	v_mul_f32_e32 v166, v63, v166
	v_mul_f32_e32 v167, v63, v167
	ds_write_b128 v209, v[164:167] offset:5120
	v_mul_f32_e32 v168, v64, v168
	v_mul_f32_e32 v169, v64, v169
	v_mul_f32_e32 v170, v64, v170
	v_mul_f32_e32 v171, v64, v171
	ds_write_b128 v209, v[168:171] offset:6144
	v_mul_f32_e32 v172, v65, v172
	v_mul_f32_e32 v173, v65, v173
	v_mul_f32_e32 v174, v65, v174
	v_mul_f32_e32 v175, v65, v175
	ds_write_b128 v209, v[172:175] offset:7168
	s_waitcnt lgkmcnt(0)
	s_barrier
; #define GAS __attribute__((address_space(1)))
; #define LAS __attribute__((address_space(3)))
; #define LDS_WAIT() asm volatile("s_waitcnt lgkmcnt(0)" ::: "memory")
; __device__ __forceinline__ unsigned pk2(float lo, float hi) { return f2bf(lo) | (f2bf(hi) << 16); }
; __device__ __forceinline__ int nat_dim(int p) { return (p >> 1) + 64 * (p & 1); }
; template <int MAP, bool KS, bool KPERM = false>
; __device__ __forceinline__ void p0_transpose_item(const float* W, int K, int Nsrc, int nblk, bf16* WT, const float* ksA, const float* ksB, int ksplit, LAS float* scr, int item, int lane) {
;     const int kb = item / nblk, nb = item % nblk, k0 = 64 * kb, n0 = 32 * nb;
;     const int nr = n0 + (lane & 31); const int sc = MAP == 1 ? src_col_in(nr) : (MAP == 2 ? nat_dim(nr) : nr);
;     float v[32];
; #pragma unroll
;     for (int i = 0; i < 32; ++i) { const int k = k0 + 2 * i + (lane >> 5); const int ksrc = KPERM ? ((k & ~127) + nat_dim(k & 127)) : k;
;         v[i] = sc >= 0 ? W[(size_t)ksrc * Nsrc + sc] : 0.f; }
; #pragma unroll
;     for (int i = 0; i < 32; ++i) { const int kk = 2 * i + (lane >> 5); const int k = k0 + kk;
;         if (KS) v[i] *= (k < ksplit ? ksA[k] : ksB[k - ksplit]);
;         scr[kk * 33 + (lane & 31)] = v[i]; }
;     LDS_WAIT(); asm volatile("" ::: "memory");
;     const int c = lane & 7;
; #pragma unroll
;     for (int j = 0; j < 4; ++j) { const int n = (lane >> 3) + 8 * j; const LAS float* s = scr + (8 * c) * 33 + n;
;         v4u o; o.x = pk2(s[0 * 33], s[1 * 33]); o.y = pk2(s[2 * 33], s[3 * 33]); o.z = pk2(s[4 * 33], s[5 * 33]); o.w = pk2(s[6 * 33], s[7 * 33]);
;         *(GAS v4u*)(WT + (size_t)(n0 + n) * K + k0 + 8 * c) = o; }
;     LDS_WAIT(); asm volatile("" ::: "memory");
; }
; __global__ void __launch_bounds__(NWAVES * 64, 2) hybrid_fwd(Args args) {
;     ...
;             if (r < I_O) { if (l >= WO_F8_FROM) p0_transpose_item_f8<true>(args.in[13] + (size_t)l * DM * DM, DM, DM, DM / 32, (unsigned char*)(ws + WS_WO + l * SZ_WO), 64.f, args.in[6] + l * 2048, args.in[12] + l * 2048, 2048, scr, r, lane);
;                 else p0_transpose_item<0, true>(args.in[13] + (size_t)l * DM * DM, DM, DM, DM / 32, (bf16*)(ws + WS_WO + l * SZ_WO), args.in[6] + l * 2048, args.in[12] + l * 2048, 2048, scr, r, lane); continue; } r -= I_O;
	s_mov_b64 s[8:9], s[58:59]
	global_load_dwordx4 v[144:147], v75, s[8:9]
	s_add_u32 s8, s8, 0x8000
	s_addc_u32 s9, s9, 0
	global_load_dwordx4 v[148:151], v75, s[8:9]
	s_add_u32 s8, s8, 0x8000
	s_addc_u32 s9, s9, 0
	global_load_dwordx4 v[152:155], v75, s[8:9]
	s_add_u32 s8, s8, 0x8000
	s_addc_u32 s9, s9, 0
	global_load_dwordx4 v[156:159], v75, s[8:9]
	s_add_u32 s8, s8, 0x8000
	s_addc_u32 s9, s9, 0
	global_load_dwordx4 v[160:163], v75, s[8:9]
	s_add_u32 s8, s8, 0x8000
	s_addc_u32 s9, s9, 0
	global_load_dwordx4 v[164:167], v75, s[8:9]
	s_add_u32 s8, s8, 0x8000
	s_addc_u32 s9, s9, 0
	global_load_dwordx4 v[168:171], v75, s[8:9]
	s_add_u32 s8, s8, 0x8000
	s_addc_u32 s9, s9, 0
	global_load_dwordx4 v[172:175], v75, s[8:9]
	s_add_u32 s6, s56, 0x1000000
	s_addc_u32 s7, s57, 0
	ds_read_b32 v226, v112
	ds_read_b32 v227, v112 offset:512
	ds_read_b32 v228, v112 offset:1024
	ds_read_b32 v229, v112 offset:1536
	ds_read_b32 v230, v112 offset:2048
	ds_read_b32 v231, v112 offset:2560
	ds_read_b32 v232, v112 offset:3072
	ds_read_b32 v233, v112 offset:3584
	s_waitcnt lgkmcnt(0)
	v_bfe_u32 v120, v226, 16, 1
	v_bfe_u32 v121, v227, 16, 1
	v_bfe_u32 v122, v228, 16, 1
	v_bfe_u32 v123, v229, 16, 1
	v_bfe_u32 v124, v230, 16, 1
	v_bfe_u32 v125, v231, 16, 1
	v_bfe_u32 v126, v232, 16, 1
	v_bfe_u32 v127, v233, 16, 1
	v_add3_u32 v226, v226, v120, s63
	v_add3_u32 v227, v227, v121, s63
	v_add3_u32 v228, v228, v122, s63
	v_add3_u32 v229, v229, v123, s63
	v_add3_u32 v230, v230, v124, s63
	v_add3_u32 v231, v231, v125, s63
	v_add3_u32 v232, v232, v126, s63
	v_add3_u32 v233, v233, v127, s63
	v_perm_b32 v242, v227, v226, s64
	v_perm_b32 v243, v229, v228, s64
	v_perm_b32 v244, v231, v230, s64
	v_perm_b32 v245, v233, v232, s64
	s_nop 0
	global_store_dwordx4 v83, v[242:245], s[6:7]
	ds_read_b32 v226, v114
	ds_read_b32 v227, v114 offset:512
	ds_read_b32 v228, v114 offset:1024
	ds_read_b32 v229, v114 offset:1536
	ds_read_b32 v230, v114 offset:2048
	ds_read_b32 v231, v114 offset:2560
	ds_read_b32 v232, v114 offset:3072
	ds_read_b32 v233, v114 offset:3584
	s_waitcnt lgkmcnt(0)
	v_bfe_u32 v120, v226, 16, 1
	v_bfe_u32 v121, v227, 16, 1
	v_bfe_u32 v122, v228, 16, 1
	v_bfe_u32 v123, v229, 16, 1
	v_bfe_u32 v124, v230, 16, 1
	v_bfe_u32 v125, v231, 16, 1
	v_bfe_u32 v126, v232, 16, 1
	v_bfe_u32 v127, v233, 16, 1
	v_add3_u32 v226, v226, v120, s63
	v_add3_u32 v227, v227, v121, s63
	v_add3_u32 v228, v228, v122, s63
	v_add3_u32 v229, v229, v123, s63
	v_add3_u32 v230, v230, v124, s63
	v_add3_u32 v231, v231, v125, s63
	v_add3_u32 v232, v232, v126, s63
	v_add3_u32 v233, v233, v127, s63
	v_perm_b32 v242, v227, v226, s64
	v_perm_b32 v243, v229, v228, s64
	v_perm_b32 v244, v231, v230, s64
	v_perm_b32 v245, v233, v232, s64
	s_nop 0
	global_store_dwordx4 v84, v[242:245], s[6:7]
	ds_read_b32 v226, v116
	ds_read_b32 v227, v116 offset:512
	ds_read_b32 v228, v116 offset:1024
	ds_read_b32 v229, v116 offset:1536
	ds_read_b32 v230, v116 offset:2048
	ds_read_b32 v231, v116 offset:2560
	ds_read_b32 v232, v116 offset:3072
	ds_read_b32 v233, v116 offset:3584
	s_waitcnt lgkmcnt(0)
	v_bfe_u32 v120, v226, 16, 1
	v_bfe_u32 v121, v227, 16, 1
	v_bfe_u32 v122, v228, 16, 1
	v_bfe_u32 v123, v229, 16, 1
	v_bfe_u32 v124, v230, 16, 1
	v_bfe_u32 v125, v231, 16, 1
	v_bfe_u32 v126, v232, 16, 1
	v_bfe_u32 v127, v233, 16, 1
	v_add3_u32 v226, v226, v120, s63
	v_add3_u32 v227, v227, v121, s63
	v_add3_u32 v228, v228, v122, s63
	v_add3_u32 v229, v229, v123, s63
	v_add3_u32 v230, v230, v124, s63
	v_add3_u32 v231, v231, v125, s63
	v_add3_u32 v232, v232, v126, s63
	v_add3_u32 v233, v233, v127, s63
	v_perm_b32 v242, v227, v226, s64
	v_perm_b32 v243, v229, v228, s64
	v_perm_b32 v244, v231, v230, s64
	v_perm_b32 v245, v233, v232, s64
	s_nop 0
	global_store_dwordx4 v85, v[242:245], s[6:7]
	ds_read_b32 v226, v118
	ds_read_b32 v227, v118 offset:512
	ds_read_b32 v228, v118 offset:1024
	ds_read_b32 v229, v118 offset:1536
	ds_read_b32 v230, v118 offset:2048
	ds_read_b32 v231, v118 offset:2560
	ds_read_b32 v232, v118 offset:3072
	ds_read_b32 v233, v118 offset:3584
	s_waitcnt lgkmcnt(0)
	v_bfe_u32 v120, v226, 16, 1
	v_bfe_u32 v121, v227, 16, 1
	v_bfe_u32 v122, v228, 16, 1
	v_bfe_u32 v123, v229, 16, 1
	v_bfe_u32 v124, v230, 16, 1
	v_bfe_u32 v125, v231, 16, 1
	v_bfe_u32 v126, v232, 16, 1
	v_bfe_u32 v127, v233, 16, 1
	v_add3_u32 v226, v226, v120, s63
	v_add3_u32 v227, v227, v121, s63
	v_add3_u32 v228, v228, v122, s63
	v_add3_u32 v229, v229, v123, s63
	v_add3_u32 v230, v230, v124, s63
	v_add3_u32 v231, v231, v125, s63
	v_add3_u32 v232, v232, v126, s63
	v_add3_u32 v233, v233, v127, s63
	v_perm_b32 v242, v227, v226, s64
	v_perm_b32 v243, v229, v228, s64
	v_perm_b32 v244, v231, v230, s64
	v_perm_b32 v245, v233, v232, s64
	s_nop 0
	global_store_dwordx4 v86, v[242:245], s[6:7]
	s_waitcnt vmcnt(16)
	v_mul_f32_e32 v176, v58, v176
	v_mul_f32_e32 v177, v58, v177
	v_mul_f32_e32 v178, v58, v178
	v_mul_f32_e32 v179, v58, v179
	ds_write_b128 v210, v[176:179]
	v_mul_f32_e32 v180, v59, v180
	v_mul_f32_e32 v181, v59, v181
	v_mul_f32_e32 v182, v59, v182
	v_mul_f32_e32 v183, v59, v183
	ds_write_b128 v210, v[180:183] offset:1024
	v_mul_f32_e32 v184, v60, v184
	v_mul_f32_e32 v185, v60, v185
	v_mul_f32_e32 v186, v60, v186
	v_mul_f32_e32 v187, v60, v187
	ds_write_b128 v210, v[184:187] offset:2048
	v_mul_f32_e32 v188, v61, v188
	v_mul_f32_e32 v189, v61, v189
	v_mul_f32_e32 v190, v61, v190
	v_mul_f32_e32 v191, v61, v191
	ds_write_b128 v210, v[188:191] offset:3072
	v_mul_f32_e32 v192, v62, v192
	v_mul_f32_e32 v193, v62, v193
	v_mul_f32_e32 v194, v62, v194
	v_mul_f32_e32 v195, v62, v195
	ds_write_b128 v210, v[192:195] offset:4096
	v_mul_f32_e32 v196, v63, v196
	v_mul_f32_e32 v197, v63, v197
	v_mul_f32_e32 v198, v63, v198
	v_mul_f32_e32 v199, v63, v199
	ds_write_b128 v210, v[196:199] offset:5120
	v_mul_f32_e32 v200, v64, v200
	v_mul_f32_e32 v201, v64, v201
	v_mul_f32_e32 v202, v64, v202
	v_mul_f32_e32 v203, v64, v203
	ds_write_b128 v210, v[200:203] offset:6144
	v_mul_f32_e32 v204, v65, v204
	v_mul_f32_e32 v205, v65, v205
	v_mul_f32_e32 v206, v65, v206
	v_mul_f32_e32 v207, v65, v207
	ds_write_b128 v210, v[204:207] offset:7168
	s_waitcnt lgkmcnt(0)
	s_barrier
; #define GAS __attribute__((address_space(1)))
; #define LAS __attribute__((address_space(3)))
; #define LDS_WAIT() asm volatile("s_waitcnt lgkmcnt(0)" ::: "memory")
; __device__ __forceinline__ unsigned pk2(float lo, float hi) { return f2bf(lo) | (f2bf(hi) << 16); }
; __device__ __forceinline__ int nat_dim(int p) { return (p >> 1) + 64 * (p & 1); }
; template <int MAP, bool KS, bool KPERM = false>
; __device__ __forceinline__ void p0_transpose_item(const float* W, int K, int Nsrc, int nblk, bf16* WT, const float* ksA, const float* ksB, int ksplit, LAS float* scr, int item, int lane) {
;     const int kb = item / nblk, nb = item % nblk, k0 = 64 * kb, n0 = 32 * nb;
;     const int nr = n0 + (lane & 31); const int sc = MAP == 1 ? src_col_in(nr) : (MAP == 2 ? nat_dim(nr) : nr);
;     float v[32];
; #pragma unroll
;     for (int i = 0; i < 32; ++i) { const int k = k0 + 2 * i + (lane >> 5); const int ksrc = KPERM ? ((k & ~127) + nat_dim(k & 127)) : k;
;         v[i] = sc >= 0 ? W[(size_t)ksrc * Nsrc + sc] : 0.f; }
; #pragma unroll
;     for (int i = 0; i < 32; ++i) { const int kk = 2 * i + (lane >> 5); const int k = k0 + kk;
;         if (KS) v[i] *= (k < ksplit ? ksA[k] : ksB[k - ksplit]);
;         scr[kk * 33 + (lane & 31)] = v[i]; }
;     LDS_WAIT(); asm volatile("" ::: "memory");
;     const int c = lane & 7;
; #pragma unroll
;     for (int j = 0; j < 4; ++j) { const int n = (lane >> 3) + 8 * j; const LAS float* s = scr + (8 * c) * 33 + n;
;         v4u o; o.x = pk2(s[0 * 33], s[1 * 33]); o.y = pk2(s[2 * 33], s[3 * 33]); o.z = pk2(s[4 * 33], s[5 * 33]); o.w = pk2(s[6 * 33], s[7 * 33]);
;         *(GAS v4u*)(WT + (size_t)(n0 + n) * K + k0 + 8 * c) = o; }
;     LDS_WAIT(); asm volatile("" ::: "memory");
; }
; __global__ void __launch_bounds__(NWAVES * 64, 2) hybrid_fwd(Args args) {
;     ...
;             if (r < I_O) { if (l >= WO_F8_FROM) p0_transpose_item_f8<true>(args.in[13] + (size_t)l * DM * DM, DM, DM, DM / 32, (unsigned char*)(ws + WS_WO + l * SZ_WO), 64.f, args.in[6] + l * 2048, args.in[12] + l * 2048, 2048, scr, r, lane);
;                 else p0_transpose_item<0, true>(args.in[13] + (size_t)l * DM * DM, DM, DM, DM / 32, (bf16*)(ws + WS_WO + l * SZ_WO), args.in[6] + l * 2048, args.in[12] + l * 2048, 2048, scr, r, lane); continue; } r -= I_O;
	s_add_u32 s8, s58, 0x1000
	s_addc_u32 s9, s59, 0
	global_load_dwordx4 v[176:179], v75, s[8:9]
	s_add_u32 s8, s8, 0x8000
	s_addc_u32 s9, s9, 0
	global_load_dwordx4 v[180:183], v75, s[8:9]
	s_add_u32 s8, s8, 0x8000
	s_addc_u32 s9, s9, 0
	global_load_dwordx4 v[184:187], v75, s[8:9]
	s_add_u32 s8, s8, 0x8000
	s_addc_u32 s9, s9, 0
	global_load_dwordx4 v[188:191], v75, s[8:9]
	s_add_u32 s8, s8, 0x8000
	s_addc_u32 s9, s9, 0
	global_load_dwordx4 v[192:195], v75, s[8:9]
	s_add_u32 s8, s8, 0x8000
	s_addc_u32 s9, s9, 0
	global_load_dwordx4 v[196:199], v75, s[8:9]
	s_add_u32 s8, s8, 0x8000
	s_addc_u32 s9, s9, 0
	global_load_dwordx4 v[200:203], v75, s[8:9]
	s_add_u32 s8, s8, 0x8000
	s_addc_u32 s9, s9, 0
	global_load_dwordx4 v[204:207], v75, s[8:9]
	s_add_u32 s6, s56, 0x1800000
	s_addc_u32 s7, s57, 0
	ds_read_b32 v226, v113
	ds_read_b32 v227, v113 offset:512
	ds_read_b32 v228, v113 offset:1024
	ds_read_b32 v229, v113 offset:1536
	ds_read_b32 v230, v113 offset:2048
	ds_read_b32 v231, v113 offset:2560
	ds_read_b32 v232, v113 offset:3072
	ds_read_b32 v233, v113 offset:3584
	s_waitcnt lgkmcnt(0)
	v_bfe_u32 v120, v226, 16, 1
	v_bfe_u32 v121, v227, 16, 1
	v_bfe_u32 v122, v228, 16, 1
	v_bfe_u32 v123, v229, 16, 1
	v_bfe_u32 v124, v230, 16, 1
	v_bfe_u32 v125, v231, 16, 1
	v_bfe_u32 v126, v232, 16, 1
	v_bfe_u32 v127, v233, 16, 1
	v_add3_u32 v226, v226, v120, s63
	v_add3_u32 v227, v227, v121, s63
	v_add3_u32 v228, v228, v122, s63
	v_add3_u32 v229, v229, v123, s63
	v_add3_u32 v230, v230, v124, s63
	v_add3_u32 v231, v231, v125, s63
	v_add3_u32 v232, v232, v126, s63
	v_add3_u32 v233, v233, v127, s63
	v_perm_b32 v242, v227, v226, s64
	v_perm_b32 v243, v229, v228, s64
	v_perm_b32 v244, v231, v230, s64
	v_perm_b32 v245, v233, v232, s64
	s_nop 0
	global_store_dwordx4 v83, v[242:245], s[6:7]
	ds_read_b32 v226, v115
	ds_read_b32 v227, v115 offset:512
	ds_read_b32 v228, v115 offset:1024
	ds_read_b32 v229, v115 offset:1536
	ds_read_b32 v230, v115 offset:2048
	ds_read_b32 v231, v115 offset:2560
	ds_read_b32 v232, v115 offset:3072
	ds_read_b32 v233, v115 offset:3584
	s_waitcnt lgkmcnt(0)
	v_bfe_u32 v120, v226, 16, 1
	v_bfe_u32 v121, v227, 16, 1
	v_bfe_u32 v122, v228, 16, 1
	v_bfe_u32 v123, v229, 16, 1
	v_bfe_u32 v124, v230, 16, 1
	v_bfe_u32 v125, v231, 16, 1
	v_bfe_u32 v126, v232, 16, 1
	v_bfe_u32 v127, v233, 16, 1
	v_add3_u32 v226, v226, v120, s63
	v_add3_u32 v227, v227, v121, s63
	v_add3_u32 v228, v228, v122, s63
	v_add3_u32 v229, v229, v123, s63
	v_add3_u32 v230, v230, v124, s63
	v_add3_u32 v231, v231, v125, s63
	v_add3_u32 v232, v232, v126, s63
	v_add3_u32 v233, v233, v127, s63
	v_perm_b32 v242, v227, v226, s64
	v_perm_b32 v243, v229, v228, s64
	v_perm_b32 v244, v231, v230, s64
	v_perm_b32 v245, v233, v232, s64
	s_nop 0
	global_store_dwordx4 v84, v[242:245], s[6:7]
	ds_read_b32 v226, v117
	ds_read_b32 v227, v117 offset:512
	ds_read_b32 v228, v117 offset:1024
	ds_read_b32 v229, v117 offset:1536
	ds_read_b32 v230, v117 offset:2048
	ds_read_b32 v231, v117 offset:2560
	ds_read_b32 v232, v117 offset:3072
	ds_read_b32 v233, v117 offset:3584
	s_waitcnt lgkmcnt(0)
	v_bfe_u32 v120, v226, 16, 1
	v_bfe_u32 v121, v227, 16, 1
	v_bfe_u32 v122, v228, 16, 1
	v_bfe_u32 v123, v229, 16, 1
	v_bfe_u32 v124, v230, 16, 1
	v_bfe_u32 v125, v231, 16, 1
	v_bfe_u32 v126, v232, 16, 1
	v_bfe_u32 v127, v233, 16, 1
	v_add3_u32 v226, v226, v120, s63
	v_add3_u32 v227, v227, v121, s63
	v_add3_u32 v228, v228, v122, s63
	v_add3_u32 v229, v229, v123, s63
	v_add3_u32 v230, v230, v124, s63
	v_add3_u32 v231, v231, v125, s63
	v_add3_u32 v232, v232, v126, s63
	v_add3_u32 v233, v233, v127, s63
	v_perm_b32 v242, v227, v226, s64
	v_perm_b32 v243, v229, v228, s64
	v_perm_b32 v244, v231, v230, s64
	v_perm_b32 v245, v233, v232, s64
	s_nop 0
	global_store_dwordx4 v85, v[242:245], s[6:7]
	ds_read_b32 v226, v119
	ds_read_b32 v227, v119 offset:512
	ds_read_b32 v228, v119 offset:1024
	ds_read_b32 v229, v119 offset:1536
	ds_read_b32 v230, v119 offset:2048
	ds_read_b32 v231, v119 offset:2560
	ds_read_b32 v232, v119 offset:3072
	ds_read_b32 v233, v119 offset:3584
	s_waitcnt lgkmcnt(0)
	v_bfe_u32 v120, v226, 16, 1
	v_bfe_u32 v121, v227, 16, 1
	v_bfe_u32 v122, v228, 16, 1
	v_bfe_u32 v123, v229, 16, 1
	v_bfe_u32 v124, v230, 16, 1
	v_bfe_u32 v125, v231, 16, 1
	v_bfe_u32 v126, v232, 16, 1
	v_bfe_u32 v127, v233, 16, 1
	v_add3_u32 v226, v226, v120, s63
	v_add3_u32 v227, v227, v121, s63
	v_add3_u32 v228, v228, v122, s63
	v_add3_u32 v229, v229, v123, s63
	v_add3_u32 v230, v230, v124, s63
	v_add3_u32 v231, v231, v125, s63
	v_add3_u32 v232, v232, v126, s63
	v_add3_u32 v233, v233, v127, s63
	v_perm_b32 v242, v227, v226, s64
	v_perm_b32 v243, v229, v228, s64
	v_perm_b32 v244, v231, v230, s64
	v_perm_b32 v245, v233, v232, s64
	s_nop 0
	global_store_dwordx4 v86, v[242:245], s[6:7]
	s_waitcnt vmcnt(16)
	v_mul_f32_e32 v144, v66, v144
	v_mul_f32_e32 v145, v66, v145
	v_mul_f32_e32 v146, v66, v146
	v_mul_f32_e32 v147, v66, v147
	ds_write_b128 v209, v[144:147]
	v_mul_f32_e32 v148, v67, v148
	v_mul_f32_e32 v149, v67, v149
	v_mul_f32_e32 v150, v67, v150
	v_mul_f32_e32 v151, v67, v151
	ds_write_b128 v209, v[148:151] offset:1024
	v_mul_f32_e32 v152, v68, v152
	v_mul_f32_e32 v153, v68, v153
	v_mul_f32_e32 v154, v68, v154
	v_mul_f32_e32 v155, v68, v155
	ds_write_b128 v209, v[152:155] offset:2048
	v_mul_f32_e32 v156, v69, v156
	v_mul_f32_e32 v157, v69, v157
	v_mul_f32_e32 v158, v69, v158
	v_mul_f32_e32 v159, v69, v159
	ds_write_b128 v209, v[156:159] offset:3072
	v_mul_f32_e32 v160, v70, v160
	v_mul_f32_e32 v161, v70, v161
	v_mul_f32_e32 v162, v70, v162
	v_mul_f32_e32 v163, v70, v163
	ds_write_b128 v209, v[160:163] offset:4096
	v_mul_f32_e32 v164, v71, v164
	v_mul_f32_e32 v165, v71, v165
	v_mul_f32_e32 v166, v71, v166
	v_mul_f32_e32 v167, v71, v167
	ds_write_b128 v209, v[164:167] offset:5120
	v_mul_f32_e32 v168, v72, v168
	v_mul_f32_e32 v169, v72, v169
	v_mul_f32_e32 v170, v72, v170
	v_mul_f32_e32 v171, v72, v171
	ds_write_b128 v209, v[168:171] offset:6144
	v_mul_f32_e32 v172, v73, v172
	v_mul_f32_e32 v173, v73, v173
	v_mul_f32_e32 v174, v73, v174
	v_mul_f32_e32 v175, v73, v175
	ds_write_b128 v209, v[172:175] offset:7168
	s_waitcnt lgkmcnt(0)
	s_barrier
; #define GAS __attribute__((address_space(1)))
; #define LAS __attribute__((address_space(3)))
; #define LDS_WAIT() asm volatile("s_waitcnt lgkmcnt(0)" ::: "memory")
;     const int pr = item >> 1, kb = 2 * (pr / nblk) + (item & 1), nb = pr % nblk, k0 = 64 * kb, n0 = 32 * nb;
;     const int nr = n0 + (lane & 31); const int sc = MAP == 1 ? src_col_in(nr) : nr;
;     float v[32];
; #pragma unroll
;     for (int i = 0; i < 32; ++i) v[i] = sc >= 0 ? W[(size_t)(k0 + 2 * i + (lane >> 5)) * Nsrc + sc] : 0.f;
; #pragma unroll
;     for (int i = 0; i < 32; ++i) { const int k = k0 + 2 * i + (lane >> 5); float x = v[i] * wscale; if (KS) x *= (k < ksplit ? ksA[k] : ksB[k - ksplit]); scr[(2 * i + (lane >> 5)) * 33 + (lane & 31)] = x; }
;     LDS_WAIT(); asm volatile("" ::: "memory");
;     const int c = lane & 7;
; #pragma unroll
;     for (int j = 0; j < 4; ++j) { const int n = (lane >> 3) + 8 * j; const LAS float* s = scr + (8 * c) * 33 + n;
;         const unsigned long long o = (unsigned long long)pg8::pk4_fp8(s[0 * 33], s[1 * 33], s[2 * 33], s[3 * 33]) | ((unsigned long long)pg8::pk4_fp8(s[4 * 33], s[5 * 33], s[6 * 33], s[7 * 33]) << 32);
;         *(GAS unsigned long long*)(WT + (size_t)(n0 + n) * K + k0 + 8 * c) = o; }
;     LDS_WAIT(); asm volatile("" ::: "memory");
; }
; __global__ void __launch_bounds__(NWAVES * 64, 2) hybrid_fwd(Args args) {
;     ...
;             if (r < I_O) { if (l >= WO_F8_FROM) p0_transpose_item_f8<true>(args.in[13] + (size_t)l * DM * DM, DM, DM, DM / 32, (unsigned char*)(ws + WS_WO + l * SZ_WO), 64.f, args.in[6] + l * 2048, args.in[12] + l * 2048, 2048, scr, r, lane);
	s_add_u32 s8, s58, 0x2000
	s_addc_u32 s9, s59, 0
	global_load_dwordx4 v[144:147], v75, s[8:9]
	s_add_u32 s8, s8, 0x8000
	s_addc_u32 s9, s9, 0
	global_load_dwordx4 v[148:151], v75, s[8:9]
	s_add_u32 s8, s8, 0x8000
	s_addc_u32 s9, s9, 0
	global_load_dwordx4 v[152:155], v75, s[8:9]
	s_add_u32 s8, s8, 0x8000
	s_addc_u32 s9, s9, 0
	global_load_dwordx4 v[156:159], v75, s[8:9]
	s_add_u32 s8, s8, 0x8000
	s_addc_u32 s9, s9, 0
	global_load_dwordx4 v[160:163], v75, s[8:9]
	s_add_u32 s8, s8, 0x8000
	s_addc_u32 s9, s9, 0
	global_load_dwordx4 v[164:167], v75, s[8:9]
	s_add_u32 s8, s8, 0x8000
	s_addc_u32 s9, s9, 0
	global_load_dwordx4 v[168:171], v75, s[8:9]
	s_add_u32 s8, s8, 0x8000
	s_addc_u32 s9, s9, 0
	global_load_dwordx4 v[172:175], v75, s[8:9]
	s_mov_b64 s[6:7], s[60:61]
	ds_read_b32 v226, v211
	ds_read_b32 v227, v211 offset:512
	ds_read_b32 v228, v211 offset:1024
	ds_read_b32 v229, v211 offset:1536
	ds_read_b32 v230, v211 offset:2048
	ds_read_b32 v231, v211 offset:2560
	ds_read_b32 v232, v211 offset:3072
	ds_read_b32 v233, v211 offset:3584
	ds_read_b32 v234, v211 offset:4096
	ds_read_b32 v235, v211 offset:4608
	ds_read_b32 v236, v211 offset:5120
	ds_read_b32 v237, v211 offset:5632
	ds_read_b32 v238, v211 offset:6144
	ds_read_b32 v239, v211 offset:6656
	ds_read_b32 v240, v211 offset:7168
	ds_read_b32 v241, v211 offset:7680
	s_waitcnt lgkmcnt(0)
	v_max_f32_e32 v226, v226, v226
	v_max_f32_e32 v227, v227, v227
	v_max_f32_e32 v228, v228, v228
	v_max_f32_e32 v229, v229, v229
	v_max_f32_e32 v230, v230, v230
	v_max_f32_e32 v231, v231, v231
	v_max_f32_e32 v232, v232, v232
	v_max_f32_e32 v233, v233, v233
	v_max_f32_e32 v234, v234, v234
	v_max_f32_e32 v235, v235, v235
	v_max_f32_e32 v236, v236, v236
	v_max_f32_e32 v237, v237, v237
	v_max_f32_e32 v238, v238, v238
	v_max_f32_e32 v239, v239, v239
	v_max_f32_e32 v240, v240, v240
	v_max_f32_e32 v241, v241, v241
	v_med3_f32 v226, v226, s62, v95
	v_med3_f32 v227, v227, s62, v95
	v_med3_f32 v228, v228, s62, v95
	v_med3_f32 v229, v229, s62, v95
	v_med3_f32 v230, v230, s62, v95
	v_med3_f32 v231, v231, s62, v95
	v_med3_f32 v232, v232, s62, v95
	v_med3_f32 v233, v233, s62, v95
	v_med3_f32 v234, v234, s62, v95
	v_med3_f32 v235, v235, s62, v95
	v_med3_f32 v236, v236, s62, v95
	v_med3_f32 v237, v237, s62, v95
	v_med3_f32 v238, v238, s62, v95
	v_med3_f32 v239, v239, s62, v95
	v_med3_f32 v240, v240, s62, v95
	v_med3_f32 v241, v241, s62, v95
	v_mov_b32_e32 v242, 0
	v_mov_b32_e32 v243, 0
	v_mov_b32_e32 v244, 0
	v_mov_b32_e32 v245, 0
	v_cvt_pk_fp8_f32 v242, v226, v227
	v_cvt_pk_fp8_f32 v243, v230, v231
	v_cvt_pk_fp8_f32 v244, v234, v235
	v_cvt_pk_fp8_f32 v245, v238, v239
	v_cvt_pk_fp8_f32 v242, v228, v229 op_sel:[0,0,1]
	v_cvt_pk_fp8_f32 v243, v232, v233 op_sel:[0,0,1]
	v_cvt_pk_fp8_f32 v244, v236, v237 op_sel:[0,0,1]
	v_cvt_pk_fp8_f32 v245, v240, v241 op_sel:[0,0,1]
	s_nop 0
	global_store_dwordx4 v77, v[242:245], s[6:7]
	ds_read_b32 v226, v213
	ds_read_b32 v227, v213 offset:512
	ds_read_b32 v228, v213 offset:1024
	ds_read_b32 v229, v213 offset:1536
	ds_read_b32 v230, v213 offset:2048
	ds_read_b32 v231, v213 offset:2560
	ds_read_b32 v232, v213 offset:3072
	ds_read_b32 v233, v213 offset:3584
	ds_read_b32 v234, v213 offset:4096
	ds_read_b32 v235, v213 offset:4608
	ds_read_b32 v236, v213 offset:5120
	ds_read_b32 v237, v213 offset:5632
	ds_read_b32 v238, v213 offset:6144
	ds_read_b32 v239, v213 offset:6656
	ds_read_b32 v240, v213 offset:7168
	ds_read_b32 v241, v213 offset:7680
	s_waitcnt lgkmcnt(0)
	v_max_f32_e32 v226, v226, v226
	v_max_f32_e32 v227, v227, v227
	v_max_f32_e32 v228, v228, v228
	v_max_f32_e32 v229, v229, v229
	v_max_f32_e32 v230, v230, v230
	v_max_f32_e32 v231, v231, v231
	v_max_f32_e32 v232, v232, v232
	v_max_f32_e32 v233, v233, v233
	v_max_f32_e32 v234, v234, v234
	v_max_f32_e32 v235, v235, v235
	v_max_f32_e32 v236, v236, v236
	v_max_f32_e32 v237, v237, v237
	v_max_f32_e32 v238, v238, v238
	v_max_f32_e32 v239, v239, v239
	v_max_f32_e32 v240, v240, v240
	v_max_f32_e32 v241, v241, v241
	v_med3_f32 v226, v226, s62, v95
	v_med3_f32 v227, v227, s62, v95
	v_med3_f32 v228, v228, s62, v95
	v_med3_f32 v229, v229, s62, v95
	v_med3_f32 v230, v230, s62, v95
	v_med3_f32 v231, v231, s62, v95
	v_med3_f32 v232, v232, s62, v95
	v_med3_f32 v233, v233, s62, v95
	v_med3_f32 v234, v234, s62, v95
	v_med3_f32 v235, v235, s62, v95
	v_med3_f32 v236, v236, s62, v95
	v_med3_f32 v237, v237, s62, v95
	v_med3_f32 v238, v238, s62, v95
	v_med3_f32 v239, v239, s62, v95
	v_med3_f32 v240, v240, s62, v95
	v_med3_f32 v241, v241, s62, v95
	v_mov_b32_e32 v242, 0
	v_mov_b32_e32 v243, 0
	v_mov_b32_e32 v244, 0
	v_mov_b32_e32 v245, 0
	v_cvt_pk_fp8_f32 v242, v226, v227
	v_cvt_pk_fp8_f32 v243, v230, v231
	v_cvt_pk_fp8_f32 v244, v234, v235
	v_cvt_pk_fp8_f32 v245, v238, v239
	v_cvt_pk_fp8_f32 v242, v228, v229 op_sel:[0,0,1]
	v_cvt_pk_fp8_f32 v243, v232, v233 op_sel:[0,0,1]
	v_cvt_pk_fp8_f32 v244, v236, v237 op_sel:[0,0,1]
	v_cvt_pk_fp8_f32 v245, v240, v241 op_sel:[0,0,1]
	s_nop 0
	global_store_dwordx4 v78, v[242:245], s[6:7]
	s_waitcnt vmcnt(14)
	v_mul_f32_e32 v176, v66, v176
	v_mul_f32_e32 v177, v66, v177
	v_mul_f32_e32 v178, v66, v178
	v_mul_f32_e32 v179, v66, v179
	ds_write_b128 v210, v[176:179]
	v_mul_f32_e32 v180, v67, v180
	v_mul_f32_e32 v181, v67, v181
	v_mul_f32_e32 v182, v67, v182
	v_mul_f32_e32 v183, v67, v183
	ds_write_b128 v210, v[180:183] offset:1024
	v_mul_f32_e32 v184, v68, v184
	v_mul_f32_e32 v185, v68, v185
	v_mul_f32_e32 v186, v68, v186
	v_mul_f32_e32 v187, v68, v187
	ds_write_b128 v210, v[184:187] offset:2048
	v_mul_f32_e32 v188, v69, v188
	v_mul_f32_e32 v189, v69, v189
	v_mul_f32_e32 v190, v69, v190
	v_mul_f32_e32 v191, v69, v191
	ds_write_b128 v210, v[188:191] offset:3072
	v_mul_f32_e32 v192, v70, v192
	v_mul_f32_e32 v193, v70, v193
	v_mul_f32_e32 v194, v70, v194
	v_mul_f32_e32 v195, v70, v195
	ds_write_b128 v210, v[192:195] offset:4096
	v_mul_f32_e32 v196, v71, v196
	v_mul_f32_e32 v197, v71, v197
	v_mul_f32_e32 v198, v71, v198
	v_mul_f32_e32 v199, v71, v199
	ds_write_b128 v210, v[196:199] offset:5120
	v_mul_f32_e32 v200, v72, v200
	v_mul_f32_e32 v201, v72, v201
	v_mul_f32_e32 v202, v72, v202
	v_mul_f32_e32 v203, v72, v203
	ds_write_b128 v210, v[200:203] offset:6144
	v_mul_f32_e32 v204, v73, v204
	v_mul_f32_e32 v205, v73, v205
	v_mul_f32_e32 v206, v73, v206
	v_mul_f32_e32 v207, v73, v207
	ds_write_b128 v210, v[204:207] offset:7168
	s_waitcnt lgkmcnt(0)
	s_barrier
; #define GAS __attribute__((address_space(1)))
; #define LAS __attribute__((address_space(3)))
; #define LDS_WAIT() asm volatile("s_waitcnt lgkmcnt(0)" ::: "memory")
;     const int pr = item >> 1, kb = 2 * (pr / nblk) + (item & 1), nb = pr % nblk, k0 = 64 * kb, n0 = 32 * nb;
;     const int nr = n0 + (lane & 31); const int sc = MAP == 1 ? src_col_in(nr) : nr;
;     float v[32];
; #pragma unroll
;     for (int i = 0; i < 32; ++i) v[i] = sc >= 0 ? W[(size_t)(k0 + 2 * i + (lane >> 5)) * Nsrc + sc] : 0.f;
; #pragma unroll
;     for (int i = 0; i < 32; ++i) { const int k = k0 + 2 * i + (lane >> 5); float x = v[i] * wscale; if (KS) x *= (k < ksplit ? ksA[k] : ksB[k - ksplit]); scr[(2 * i + (lane >> 5)) * 33 + (lane & 31)] = x; }
;     LDS_WAIT(); asm volatile("" ::: "memory");
;     const int c = lane & 7;
; #pragma unroll
;     for (int j = 0; j < 4; ++j) { const int n = (lane >> 3) + 8 * j; const LAS float* s = scr + (8 * c) * 33 + n;
;         const unsigned long long o = (unsigned long long)pg8::pk4_fp8(s[0 * 33], s[1 * 33], s[2 * 33], s[3 * 33]) | ((unsigned long long)pg8::pk4_fp8(s[4 * 33], s[5 * 33], s[6 * 33], s[7 * 33]) << 32);
;         *(GAS unsigned long long*)(WT + (size_t)(n0 + n) * K + k0 + 8 * c) = o; }
;     LDS_WAIT(); asm volatile("" ::: "memory");
; }
; __global__ void __launch_bounds__(NWAVES * 64, 2) hybrid_fwd(Args args) {
;     ...
;             if (r < I_O) { if (l >= WO_F8_FROM) p0_transpose_item_f8<true>(args.in[13] + (size_t)l * DM * DM, DM, DM, DM / 32, (unsigned char*)(ws + WS_WO + l * SZ_WO), 64.f, args.in[6] + l * 2048, args.in[12] + l * 2048, 2048, scr, r, lane);
	s_add_u32 s8, s58, 0x3000
	s_addc_u32 s9, s59, 0
	global_load_dwordx4 v[176:179], v75, s[8:9]
	s_add_u32 s8, s8, 0x8000
	s_addc_u32 s9, s9, 0
	global_load_dwordx4 v[180:183], v75, s[8:9]
	s_add_u32 s8, s8, 0x8000
	s_addc_u32 s9, s9, 0
	global_load_dwordx4 v[184:187], v75, s[8:9]
	s_add_u32 s8, s8, 0x8000
	s_addc_u32 s9, s9, 0
	global_load_dwordx4 v[188:191], v75, s[8:9]
	s_add_u32 s8, s8, 0x8000
	s_addc_u32 s9, s9, 0
	global_load_dwordx4 v[192:195], v75, s[8:9]
	s_add_u32 s8, s8, 0x8000
	s_addc_u32 s9, s9, 0
	global_load_dwordx4 v[196:199], v75, s[8:9]
	s_add_u32 s8, s8, 0x8000
	s_addc_u32 s9, s9, 0
	global_load_dwordx4 v[200:203], v75, s[8:9]
	s_add_u32 s8, s8, 0x8000
	s_addc_u32 s9, s9, 0
	global_load_dwordx4 v[204:207], v75, s[8:9]
	s_add_u32 s6, s60, 0x400000
	s_addc_u32 s7, s61, 0
	ds_read_b32 v226, v212
	ds_read_b32 v227, v212 offset:512
	ds_read_b32 v228, v212 offset:1024
	ds_read_b32 v229, v212 offset:1536
	ds_read_b32 v230, v212 offset:2048
	ds_read_b32 v231, v212 offset:2560
	ds_read_b32 v232, v212 offset:3072
	ds_read_b32 v233, v212 offset:3584
	ds_read_b32 v234, v212 offset:4096
	ds_read_b32 v235, v212 offset:4608
	ds_read_b32 v236, v212 offset:5120
	ds_read_b32 v237, v212 offset:5632
	ds_read_b32 v238, v212 offset:6144
	ds_read_b32 v239, v212 offset:6656
	ds_read_b32 v240, v212 offset:7168
	ds_read_b32 v241, v212 offset:7680
	s_waitcnt lgkmcnt(0)
	v_max_f32_e32 v226, v226, v226
	v_max_f32_e32 v227, v227, v227
	v_max_f32_e32 v228, v228, v228
	v_max_f32_e32 v229, v229, v229
	v_max_f32_e32 v230, v230, v230
	v_max_f32_e32 v231, v231, v231
	v_max_f32_e32 v232, v232, v232
	v_max_f32_e32 v233, v233, v233
	v_max_f32_e32 v234, v234, v234
	v_max_f32_e32 v235, v235, v235
	v_max_f32_e32 v236, v236, v236
	v_max_f32_e32 v237, v237, v237
	v_max_f32_e32 v238, v238, v238
	v_max_f32_e32 v239, v239, v239
	v_max_f32_e32 v240, v240, v240
	v_max_f32_e32 v241, v241, v241
	v_med3_f32 v226, v226, s62, v95
	v_med3_f32 v227, v227, s62, v95
	v_med3_f32 v228, v228, s62, v95
	v_med3_f32 v229, v229, s62, v95
	v_med3_f32 v230, v230, s62, v95
	v_med3_f32 v231, v231, s62, v95
	v_med3_f32 v232, v232, s62, v95
	v_med3_f32 v233, v233, s62, v95
	v_med3_f32 v234, v234, s62, v95
	v_med3_f32 v235, v235, s62, v95
	v_med3_f32 v236, v236, s62, v95
	v_med3_f32 v237, v237, s62, v95
	v_med3_f32 v238, v238, s62, v95
	v_med3_f32 v239, v239, s62, v95
	v_med3_f32 v240, v240, s62, v95
	v_med3_f32 v241, v241, s62, v95
	v_mov_b32_e32 v242, 0
	v_mov_b32_e32 v243, 0
	v_mov_b32_e32 v244, 0
	v_mov_b32_e32 v245, 0
	v_cvt_pk_fp8_f32 v242, v226, v227
	v_cvt_pk_fp8_f32 v243, v230, v231
	v_cvt_pk_fp8_f32 v244, v234, v235
	v_cvt_pk_fp8_f32 v245, v238, v239
	v_cvt_pk_fp8_f32 v242, v228, v229 op_sel:[0,0,1]
	v_cvt_pk_fp8_f32 v243, v232, v233 op_sel:[0,0,1]
	v_cvt_pk_fp8_f32 v244, v236, v237 op_sel:[0,0,1]
	v_cvt_pk_fp8_f32 v245, v240, v241 op_sel:[0,0,1]
	s_nop 0
	global_store_dwordx4 v77, v[242:245], s[6:7]
	ds_read_b32 v226, v214
	ds_read_b32 v227, v214 offset:512
	ds_read_b32 v228, v214 offset:1024
	ds_read_b32 v229, v214 offset:1536
	ds_read_b32 v230, v214 offset:2048
	ds_read_b32 v231, v214 offset:2560
	ds_read_b32 v232, v214 offset:3072
	ds_read_b32 v233, v214 offset:3584
	ds_read_b32 v234, v214 offset:4096
	ds_read_b32 v235, v214 offset:4608
	ds_read_b32 v236, v214 offset:5120
	ds_read_b32 v237, v214 offset:5632
	ds_read_b32 v238, v214 offset:6144
	ds_read_b32 v239, v214 offset:6656
	ds_read_b32 v240, v214 offset:7168
	ds_read_b32 v241, v214 offset:7680
	s_waitcnt lgkmcnt(0)
	v_max_f32_e32 v226, v226, v226
	v_max_f32_e32 v227, v227, v227
	v_max_f32_e32 v228, v228, v228
	v_max_f32_e32 v229, v229, v229
	v_max_f32_e32 v230, v230, v230
	v_max_f32_e32 v231, v231, v231
	v_max_f32_e32 v232, v232, v232
	v_max_f32_e32 v233, v233, v233
	v_max_f32_e32 v234, v234, v234
	v_max_f32_e32 v235, v235, v235
	v_max_f32_e32 v236, v236, v236
	v_max_f32_e32 v237, v237, v237
	v_max_f32_e32 v238, v238, v238
	v_max_f32_e32 v239, v239, v239
	v_max_f32_e32 v240, v240, v240
	v_max_f32_e32 v241, v241, v241
	v_med3_f32 v226, v226, s62, v95
	v_med3_f32 v227, v227, s62, v95
	v_med3_f32 v228, v228, s62, v95
	v_med3_f32 v229, v229, s62, v95
	v_med3_f32 v230, v230, s62, v95
	v_med3_f32 v231, v231, s62, v95
	v_med3_f32 v232, v232, s62, v95
	v_med3_f32 v233, v233, s62, v95
	v_med3_f32 v234, v234, s62, v95
	v_med3_f32 v235, v235, s62, v95
	v_med3_f32 v236, v236, s62, v95
	v_med3_f32 v237, v237, s62, v95
	v_med3_f32 v238, v238, s62, v95
	v_med3_f32 v239, v239, s62, v95
	v_med3_f32 v240, v240, s62, v95
	v_med3_f32 v241, v241, s62, v95
	v_mov_b32_e32 v242, 0
	v_mov_b32_e32 v243, 0
	v_mov_b32_e32 v244, 0
	v_mov_b32_e32 v245, 0
	v_cvt_pk_fp8_f32 v242, v226, v227
	v_cvt_pk_fp8_f32 v243, v230, v231
	v_cvt_pk_fp8_f32 v244, v234, v235
	v_cvt_pk_fp8_f32 v245, v238, v239
	v_cvt_pk_fp8_f32 v242, v228, v229 op_sel:[0,0,1]
	v_cvt_pk_fp8_f32 v243, v232, v233 op_sel:[0,0,1]
	v_cvt_pk_fp8_f32 v244, v236, v237 op_sel:[0,0,1]
	v_cvt_pk_fp8_f32 v245, v240, v241 op_sel:[0,0,1]
	s_nop 0
	global_store_dwordx4 v78, v[242:245], s[6:7]
	s_waitcnt vmcnt(12)
	v_mul_f32_e32 v144, v66, v144
	v_mul_f32_e32 v145, v66, v145
	v_mul_f32_e32 v146, v66, v146
	v_mul_f32_e32 v147, v66, v147
	ds_write_b128 v209, v[144:147]
	v_mul_f32_e32 v148, v67, v148
	v_mul_f32_e32 v149, v67, v149
	v_mul_f32_e32 v150, v67, v150
	v_mul_f32_e32 v151, v67, v151
	ds_write_b128 v209, v[148:151] offset:1024
	v_mul_f32_e32 v152, v68, v152
	v_mul_f32_e32 v153, v68, v153
	v_mul_f32_e32 v154, v68, v154
	v_mul_f32_e32 v155, v68, v155
	ds_write_b128 v209, v[152:155] offset:2048
	v_mul_f32_e32 v156, v69, v156
	v_mul_f32_e32 v157, v69, v157
	v_mul_f32_e32 v158, v69, v158
	v_mul_f32_e32 v159, v69, v159
	ds_write_b128 v209, v[156:159] offset:3072
	v_mul_f32_e32 v160, v70, v160
	v_mul_f32_e32 v161, v70, v161
	v_mul_f32_e32 v162, v70, v162
	v_mul_f32_e32 v163, v70, v163
	ds_write_b128 v209, v[160:163] offset:4096
	v_mul_f32_e32 v164, v71, v164
	v_mul_f32_e32 v165, v71, v165
	v_mul_f32_e32 v166, v71, v166
	v_mul_f32_e32 v167, v71, v167
	ds_write_b128 v209, v[164:167] offset:5120
	v_mul_f32_e32 v168, v72, v168
	v_mul_f32_e32 v169, v72, v169
	v_mul_f32_e32 v170, v72, v170
	v_mul_f32_e32 v171, v72, v171
	ds_write_b128 v209, v[168:171] offset:6144
	v_mul_f32_e32 v172, v73, v172
	v_mul_f32_e32 v173, v73, v173
	v_mul_f32_e32 v174, v73, v174
	v_mul_f32_e32 v175, v73, v175
	ds_write_b128 v209, v[172:175] offset:7168
	s_waitcnt lgkmcnt(0)
	s_barrier
; #define GAS __attribute__((address_space(1)))
; #define LAS __attribute__((address_space(3)))
; #define LDS_WAIT() asm volatile("s_waitcnt lgkmcnt(0)" ::: "memory")
;     const int pr = item >> 1, kb = 2 * (pr / nblk) + (item & 1), nb = pr % nblk, k0 = 64 * kb, n0 = 32 * nb;
;     const int nr = n0 + (lane & 31); const int sc = MAP == 1 ? src_col_in(nr) : nr;
;     float v[32];
; #pragma unroll
;     for (int i = 0; i < 32; ++i) v[i] = sc >= 0 ? W[(size_t)(k0 + 2 * i + (lane >> 5)) * Nsrc + sc] : 0.f;
; #pragma unroll
;     for (int i = 0; i < 32; ++i) { const int k = k0 + 2 * i + (lane >> 5); float x = v[i] * wscale; if (KS) x *= (k < ksplit ? ksA[k] : ksB[k - ksplit]); scr[(2 * i + (lane >> 5)) * 33 + (lane & 31)] = x; }
;     LDS_WAIT(); asm volatile("" ::: "memory");
;     const int c = lane & 7;
; #pragma unroll
;     for (int j = 0; j < 4; ++j) { const int n = (lane >> 3) + 8 * j; const LAS float* s = scr + (8 * c) * 33 + n;
;         const unsigned long long o = (unsigned long long)pg8::pk4_fp8(s[0 * 33], s[1 * 33], s[2 * 33], s[3 * 33]) | ((unsigned long long)pg8::pk4_fp8(s[4 * 33], s[5 * 33], s[6 * 33], s[7 * 33]) << 32);
;         *(GAS unsigned long long*)(WT + (size_t)(n0 + n) * K + k0 + 8 * c) = o; }
;     LDS_WAIT(); asm volatile("" ::: "memory");
; }
; __global__ void __launch_bounds__(NWAVES * 64, 2) hybrid_fwd(Args args) {
;     ...
;             if (r < I_O) { if (l >= WO_F8_FROM) p0_transpose_item_f8<true>(args.in[13] + (size_t)l * DM * DM, DM, DM, DM / 32, (unsigned char*)(ws + WS_WO + l * SZ_WO), 64.f, args.in[6] + l * 2048, args.in[12] + l * 2048, 2048, scr, r, lane);
	s_add_u32 s6, s60, 0x800000
	s_addc_u32 s7, s61, 0
	ds_read_b32 v226, v211
	ds_read_b32 v227, v211 offset:512
	ds_read_b32 v228, v211 offset:1024
	ds_read_b32 v229, v211 offset:1536
	ds_read_b32 v230, v211 offset:2048
	ds_read_b32 v231, v211 offset:2560
	ds_read_b32 v232, v211 offset:3072
	ds_read_b32 v233, v211 offset:3584
	ds_read_b32 v234, v211 offset:4096
	ds_read_b32 v235, v211 offset:4608
	ds_read_b32 v236, v211 offset:5120
	ds_read_b32 v237, v211 offset:5632
	ds_read_b32 v238, v211 offset:6144
	ds_read_b32 v239, v211 offset:6656
	ds_read_b32 v240, v211 offset:7168
	ds_read_b32 v241, v211 offset:7680
	s_waitcnt lgkmcnt(0)
	v_max_f32_e32 v226, v226, v226
	v_max_f32_e32 v227, v227, v227
	v_max_f32_e32 v228, v228, v228
	v_max_f32_e32 v229, v229, v229
	v_max_f32_e32 v230, v230, v230
	v_max_f32_e32 v231, v231, v231
	v_max_f32_e32 v232, v232, v232
	v_max_f32_e32 v233, v233, v233
	v_max_f32_e32 v234, v234, v234
	v_max_f32_e32 v235, v235, v235
	v_max_f32_e32 v236, v236, v236
	v_max_f32_e32 v237, v237, v237
	v_max_f32_e32 v238, v238, v238
	v_max_f32_e32 v239, v239, v239
	v_max_f32_e32 v240, v240, v240
	v_max_f32_e32 v241, v241, v241
	v_med3_f32 v226, v226, s62, v95
	v_med3_f32 v227, v227, s62, v95
	v_med3_f32 v228, v228, s62, v95
	v_med3_f32 v229, v229, s62, v95
	v_med3_f32 v230, v230, s62, v95
	v_med3_f32 v231, v231, s62, v95
	v_med3_f32 v232, v232, s62, v95
	v_med3_f32 v233, v233, s62, v95
	v_med3_f32 v234, v234, s62, v95
	v_med3_f32 v235, v235, s62, v95
	v_med3_f32 v236, v236, s62, v95
	v_med3_f32 v237, v237, s62, v95
	v_med3_f32 v238, v238, s62, v95
	v_med3_f32 v239, v239, s62, v95
	v_med3_f32 v240, v240, s62, v95
	v_med3_f32 v241, v241, s62, v95
	v_mov_b32_e32 v242, 0
	v_mov_b32_e32 v243, 0
	v_mov_b32_e32 v244, 0
	v_mov_b32_e32 v245, 0
	v_cvt_pk_fp8_f32 v242, v226, v227
	v_cvt_pk_fp8_f32 v243, v230, v231
	v_cvt_pk_fp8_f32 v244, v234, v235
	v_cvt_pk_fp8_f32 v245, v238, v239
	v_cvt_pk_fp8_f32 v242, v228, v229 op_sel:[0,0,1]
	v_cvt_pk_fp8_f32 v243, v232, v233 op_sel:[0,0,1]
	v_cvt_pk_fp8_f32 v244, v236, v237 op_sel:[0,0,1]
	v_cvt_pk_fp8_f32 v245, v240, v241 op_sel:[0,0,1]
	s_nop 0
	global_store_dwordx4 v77, v[242:245], s[6:7]
	ds_read_b32 v226, v213
	ds_read_b32 v227, v213 offset:512
	ds_read_b32 v228, v213 offset:1024
	ds_read_b32 v229, v213 offset:1536
	ds_read_b32 v230, v213 offset:2048
	ds_read_b32 v231, v213 offset:2560
	ds_read_b32 v232, v213 offset:3072
	ds_read_b32 v233, v213 offset:3584
	ds_read_b32 v234, v213 offset:4096
	ds_read_b32 v235, v213 offset:4608
	ds_read_b32 v236, v213 offset:5120
	ds_read_b32 v237, v213 offset:5632
	ds_read_b32 v238, v213 offset:6144
	ds_read_b32 v239, v213 offset:6656
	ds_read_b32 v240, v213 offset:7168
	ds_read_b32 v241, v213 offset:7680
	s_waitcnt lgkmcnt(0)
	v_max_f32_e32 v226, v226, v226
	v_max_f32_e32 v227, v227, v227
	v_max_f32_e32 v228, v228, v228
	v_max_f32_e32 v229, v229, v229
	v_max_f32_e32 v230, v230, v230
	v_max_f32_e32 v231, v231, v231
	v_max_f32_e32 v232, v232, v232
	v_max_f32_e32 v233, v233, v233
	v_max_f32_e32 v234, v234, v234
	v_max_f32_e32 v235, v235, v235
	v_max_f32_e32 v236, v236, v236
	v_max_f32_e32 v237, v237, v237
	v_max_f32_e32 v238, v238, v238
	v_max_f32_e32 v239, v239, v239
	v_max_f32_e32 v240, v240, v240
	v_max_f32_e32 v241, v241, v241
	v_med3_f32 v226, v226, s62, v95
	v_med3_f32 v227, v227, s62, v95
	v_med3_f32 v228, v228, s62, v95
	v_med3_f32 v229, v229, s62, v95
	v_med3_f32 v230, v230, s62, v95
	v_med3_f32 v231, v231, s62, v95
	v_med3_f32 v232, v232, s62, v95
	v_med3_f32 v233, v233, s62, v95
	v_med3_f32 v234, v234, s62, v95
	v_med3_f32 v235, v235, s62, v95
	v_med3_f32 v236, v236, s62, v95
	v_med3_f32 v237, v237, s62, v95
	v_med3_f32 v238, v238, s62, v95
	v_med3_f32 v239, v239, s62, v95
	v_med3_f32 v240, v240, s62, v95
	v_med3_f32 v241, v241, s62, v95
	v_mov_b32_e32 v242, 0
	v_mov_b32_e32 v243, 0
	v_mov_b32_e32 v244, 0
	v_mov_b32_e32 v245, 0
	v_cvt_pk_fp8_f32 v242, v226, v227
	v_cvt_pk_fp8_f32 v243, v230, v231
	v_cvt_pk_fp8_f32 v244, v234, v235
	v_cvt_pk_fp8_f32 v245, v238, v239
	v_cvt_pk_fp8_f32 v242, v228, v229 op_sel:[0,0,1]
	v_cvt_pk_fp8_f32 v243, v232, v233 op_sel:[0,0,1]
	v_cvt_pk_fp8_f32 v244, v236, v237 op_sel:[0,0,1]
	v_cvt_pk_fp8_f32 v245, v240, v241 op_sel:[0,0,1]
	s_nop 0
	global_store_dwordx4 v78, v[242:245], s[6:7]
	s_waitcnt vmcnt(4)
	v_mul_f32_e32 v176, v66, v176
	v_mul_f32_e32 v177, v66, v177
	v_mul_f32_e32 v178, v66, v178
	v_mul_f32_e32 v179, v66, v179
	ds_write_b128 v210, v[176:179]
	v_mul_f32_e32 v180, v67, v180
	v_mul_f32_e32 v181, v67, v181
	v_mul_f32_e32 v182, v67, v182
	v_mul_f32_e32 v183, v67, v183
	ds_write_b128 v210, v[180:183] offset:1024
	v_mul_f32_e32 v184, v68, v184
	v_mul_f32_e32 v185, v68, v185
	v_mul_f32_e32 v186, v68, v186
	v_mul_f32_e32 v187, v68, v187
	ds_write_b128 v210, v[184:187] offset:2048
	v_mul_f32_e32 v188, v69, v188
	v_mul_f32_e32 v189, v69, v189
	v_mul_f32_e32 v190, v69, v190
	v_mul_f32_e32 v191, v69, v191
	ds_write_b128 v210, v[188:191] offset:3072
	v_mul_f32_e32 v192, v70, v192
	v_mul_f32_e32 v193, v70, v193
	v_mul_f32_e32 v194, v70, v194
	v_mul_f32_e32 v195, v70, v195
	ds_write_b128 v210, v[192:195] offset:4096
	v_mul_f32_e32 v196, v71, v196
	v_mul_f32_e32 v197, v71, v197
	v_mul_f32_e32 v198, v71, v198
	v_mul_f32_e32 v199, v71, v199
	ds_write_b128 v210, v[196:199] offset:5120
	v_mul_f32_e32 v200, v72, v200
	v_mul_f32_e32 v201, v72, v201
	v_mul_f32_e32 v202, v72, v202
	v_mul_f32_e32 v203, v72, v203
	ds_write_b128 v210, v[200:203] offset:6144
	v_mul_f32_e32 v204, v73, v204
	v_mul_f32_e32 v205, v73, v205
	v_mul_f32_e32 v206, v73, v206
	v_mul_f32_e32 v207, v73, v207
	ds_write_b128 v210, v[204:207] offset:7168
	s_waitcnt lgkmcnt(0)
	s_barrier
; #define GAS __attribute__((address_space(1)))
; #define LAS __attribute__((address_space(3)))
; #define LDS_WAIT() asm volatile("s_waitcnt lgkmcnt(0)" ::: "memory")
; __device__ __forceinline__ unsigned pk4_fp8(float a, float b, float c, float d) {
;     a = fminf(fmaxf(a, -448.f), 448.f); b = fminf(fmaxf(b, -448.f), 448.f); c = fminf(fmaxf(c, -448.f), 448.f); d = fminf(fmaxf(d, -448.f), 448.f);
;     int w = __builtin_amdgcn_cvt_pk_fp8_f32(a, b, 0, false); w = __builtin_amdgcn_cvt_pk_fp8_f32(c, d, w, true); return (unsigned)w; }
;     ...
;     for (int i = 0; i < 32; ++i) { const int k = k0 + 2 * i + (lane >> 5); float x = v[i] * wscale; if (KS) x *= (k < ksplit ? ksA[k] : ksB[k - ksplit]); scr[(2 * i + (lane >> 5)) * 33 + (lane & 31)] = x; }
;     LDS_WAIT(); asm volatile("" ::: "memory");
;     const int c = lane & 7;
; #pragma unroll
;     for (int j = 0; j < 4; ++j) { const int n = (lane >> 3) + 8 * j; const LAS float* s = scr + (8 * c) * 33 + n;
;         const unsigned long long o = (unsigned long long)pg8::pk4_fp8(s[0 * 33], s[1 * 33], s[2 * 33], s[3 * 33]) | ((unsigned long long)pg8::pk4_fp8(s[4 * 33], s[5 * 33], s[6 * 33], s[7 * 33]) << 32);
;         *(GAS unsigned long long*)(WT + (size_t)(n0 + n) * K + k0 + 8 * c) = o; }
	s_add_u32 s6, s60, 0xc00000
	s_addc_u32 s7, s61, 0
	ds_read_b32 v226, v212
	ds_read_b32 v227, v212 offset:512
	ds_read_b32 v228, v212 offset:1024
	ds_read_b32 v229, v212 offset:1536
	ds_read_b32 v230, v212 offset:2048
	ds_read_b32 v231, v212 offset:2560
	ds_read_b32 v232, v212 offset:3072
	ds_read_b32 v233, v212 offset:3584
	ds_read_b32 v234, v212 offset:4096
	ds_read_b32 v235, v212 offset:4608
	ds_read_b32 v236, v212 offset:5120
	ds_read_b32 v237, v212 offset:5632
	ds_read_b32 v238, v212 offset:6144
	ds_read_b32 v239, v212 offset:6656
	ds_read_b32 v240, v212 offset:7168
	ds_read_b32 v241, v212 offset:7680
	s_waitcnt lgkmcnt(0)
	v_max_f32_e32 v226, v226, v226
	v_max_f32_e32 v227, v227, v227
	v_max_f32_e32 v228, v228, v228
	v_max_f32_e32 v229, v229, v229
	v_max_f32_e32 v230, v230, v230
	v_max_f32_e32 v231, v231, v231
	v_max_f32_e32 v232, v232, v232
	v_max_f32_e32 v233, v233, v233
	v_max_f32_e32 v234, v234, v234
	v_max_f32_e32 v235, v235, v235
	v_max_f32_e32 v236, v236, v236
	v_max_f32_e32 v237, v237, v237
	v_max_f32_e32 v238, v238, v238
	v_max_f32_e32 v239, v239, v239
	v_max_f32_e32 v240, v240, v240
	v_max_f32_e32 v241, v241, v241
	v_med3_f32 v226, v226, s62, v95
	v_med3_f32 v227, v227, s62, v95
	v_med3_f32 v228, v228, s62, v95
	v_med3_f32 v229, v229, s62, v95
	v_med3_f32 v230, v230, s62, v95
	v_med3_f32 v231, v231, s62, v95
	v_med3_f32 v232, v232, s62, v95
	v_med3_f32 v233, v233, s62, v95
	v_med3_f32 v234, v234, s62, v95
	v_med3_f32 v235, v235, s62, v95
	v_med3_f32 v236, v236, s62, v95
	v_med3_f32 v237, v237, s62, v95
	v_med3_f32 v238, v238, s62, v95
	v_med3_f32 v239, v239, s62, v95
	v_med3_f32 v240, v240, s62, v95
	v_med3_f32 v241, v241, s62, v95
	v_mov_b32_e32 v242, 0
	v_mov_b32_e32 v243, 0
	v_mov_b32_e32 v244, 0
	v_mov_b32_e32 v245, 0
	v_cvt_pk_fp8_f32 v242, v226, v227
	v_cvt_pk_fp8_f32 v243, v230, v231
	v_cvt_pk_fp8_f32 v244, v234, v235
	v_cvt_pk_fp8_f32 v245, v238, v239
	v_cvt_pk_fp8_f32 v242, v228, v229 op_sel:[0,0,1]
	v_cvt_pk_fp8_f32 v243, v232, v233 op_sel:[0,0,1]
	v_cvt_pk_fp8_f32 v244, v236, v237 op_sel:[0,0,1]
	v_cvt_pk_fp8_f32 v245, v240, v241 op_sel:[0,0,1]
	s_nop 0
	global_store_dwordx4 v77, v[242:245], s[6:7]
	ds_read_b32 v226, v214
	ds_read_b32 v227, v214 offset:512
	ds_read_b32 v228, v214 offset:1024
	ds_read_b32 v229, v214 offset:1536
	ds_read_b32 v230, v214 offset:2048
	ds_read_b32 v231, v214 offset:2560
	ds_read_b32 v232, v214 offset:3072
	ds_read_b32 v233, v214 offset:3584
	ds_read_b32 v234, v214 offset:4096
	ds_read_b32 v235, v214 offset:4608
	ds_read_b32 v236, v214 offset:5120
	ds_read_b32 v237, v214 offset:5632
	ds_read_b32 v238, v214 offset:6144
	ds_read_b32 v239, v214 offset:6656
	ds_read_b32 v240, v214 offset:7168
	ds_read_b32 v241, v214 offset:7680
	s_waitcnt lgkmcnt(0)
	v_max_f32_e32 v226, v226, v226
	v_max_f32_e32 v227, v227, v227
	v_max_f32_e32 v228, v228, v228
	v_max_f32_e32 v229, v229, v229
	v_max_f32_e32 v230, v230, v230
	v_max_f32_e32 v231, v231, v231
	v_max_f32_e32 v232, v232, v232
	v_max_f32_e32 v233, v233, v233
	v_max_f32_e32 v234, v234, v234
	v_max_f32_e32 v235, v235, v235
	v_max_f32_e32 v236, v236, v236
	v_max_f32_e32 v237, v237, v237
	v_max_f32_e32 v238, v238, v238
	v_max_f32_e32 v239, v239, v239
	v_max_f32_e32 v240, v240, v240
	v_max_f32_e32 v241, v241, v241
	v_med3_f32 v226, v226, s62, v95
	v_med3_f32 v227, v227, s62, v95
	v_med3_f32 v228, v228, s62, v95
	v_med3_f32 v229, v229, s62, v95
	v_med3_f32 v230, v230, s62, v95
	v_med3_f32 v231, v231, s62, v95
	v_med3_f32 v232, v232, s62, v95
	v_med3_f32 v233, v233, s62, v95
	v_med3_f32 v234, v234, s62, v95
	v_med3_f32 v235, v235, s62, v95
	v_med3_f32 v236, v236, s62, v95
	v_med3_f32 v237, v237, s62, v95
	v_med3_f32 v238, v238, s62, v95
	v_med3_f32 v239, v239, s62, v95
	v_med3_f32 v240, v240, s62, v95
	v_med3_f32 v241, v241, s62, v95
	v_mov_b32_e32 v242, 0
	v_mov_b32_e32 v243, 0
	v_mov_b32_e32 v244, 0
	v_mov_b32_e32 v245, 0
	v_cvt_pk_fp8_f32 v242, v226, v227
	v_cvt_pk_fp8_f32 v243, v230, v231
	v_cvt_pk_fp8_f32 v244, v234, v235
	v_cvt_pk_fp8_f32 v245, v238, v239
	v_cvt_pk_fp8_f32 v242, v228, v229 op_sel:[0,0,1]
	v_cvt_pk_fp8_f32 v243, v232, v233 op_sel:[0,0,1]
	v_cvt_pk_fp8_f32 v244, v236, v237 op_sel:[0,0,1]
	v_cvt_pk_fp8_f32 v245, v240, v241 op_sel:[0,0,1]
	s_nop 0
	global_store_dwordx4 v78, v[242:245], s[6:7]
	s_waitcnt lgkmcnt(0)
	s_barrier
; __device__ __forceinline__ int src_col_in(int c) {
;     if (c < 5120) { const int blk = c >> 7, p = c & 127; const bool rope = blk < 16 || ((((blk - 16) >> 2) & 1) == 0); const int d = rope ? (p >> 1) + 64 * (p & 1) : p; return blk * 128 + d; }
;     if (c < OFF_Z) return c + 2096;
;     if (c < OFF_G) return c - 4048;
;     if (c < OFF_DT) return 5120 + (c - OFF_G);
;     if (c < NSRC) return c;
;     return -1;
; }
; __global__ void __launch_bounds__(NWAVES * 64, 2) hybrid_fwd(Args args) {
;     ...
;         for (int rep = 0; rep < REP_PRO; ++rep)
;         for (int it = gw; it < DEPTH * I_L; it += NGW) {
;             const int l = it / I_L; int r = it % I_L;
;             if (r < I_IN) { if (l >= PROJ_F8_FROM) p0_transpose_item_f8<true, 1>(args.in[2] + (size_t)l * DM * NSRC, DM, NSRC, NPROJ / 32, (unsigned char*)(ws + WS_WIN + l * SZ_WIN), WUP8_SCALE, args.in[1] + l * DM, args.in[1] + l * DM, DM, scr, r, lane);
;                 else p0_transpose_item<1, true>(args.in[2] + (size_t)l * DM * NSRC, DM, NSRC, NPROJ / 32, (bf16*)(ws + WS_WIN + l * SZ_WIN), args.in[1] + l * DM, args.in[1] + l * DM, DM, scr, r, lane); continue; } r -= I_IN;
;             if (r < I_O) { if (l >= WO_F8_FROM) p0_transpose_item_f8<true>(args.in[13] + (size_t)l * DM * DM, DM, DM, DM / 32, (unsigned char*)(ws + WS_WO + l * SZ_WO), 64.f, args.in[6] + l * 2048, args.in[12] + l * 2048, 2048, scr, r, lane);
;                 else p0_transpose_item<0, true>(args.in[13] + (size_t)l * DM * DM, DM, DM, DM / 32, (bf16*)(ws + WS_WO + l * SZ_WO), args.in[6] + l * 2048, args.in[12] + l * 2048, 2048, scr, r, lane); continue; } r -= I_O;
;             if (r < I_UP) { p0_transpose_item_f8<true>(args.in[15] + (size_t)l * DM * FF, DM, FF, FF / 32, (unsigned char*)(ws + WS_WUP + l * SZ_WUP), WUP8_SCALE, args.in[14] + l * DM, args.in[14] + l * DM, DM, scr, r, lane); continue; } r -= I_UP;
;             p0_transpose_item_f8<false>(args.in[16] + (size_t)l * FF * DM, FF, DM, DM / 32, (unsigned char*)(ws + WS_WDN + l * SZ_WDN), 128.f, args.in[16], args.in[16], 0, scr, r, lane);
	v_readlane_b32 s12, v253, 35
	v_readlane_b32 s18, v253, 41
	v_readlane_b32 s19, v253, 42
	s_add_u32 s81, s18, 0x1f600000
	s_addc_u32 s94, s19, 0
	s_add_u32 s24, s18, 0xf600000
	v_or_b32_e32 v2, 2, v6
	v_mov_b32_e32 v3, 0x630
	v_readlane_b32 s13, v253, 36
	v_readlane_b32 s14, v253, 37
	v_readlane_b32 s15, v253, 38
	s_addc_u32 s25, s19, 0
	v_mad_u32_u24 v58, v2, s0, v3
	v_mov_b32_e32 v3, 0xc60
	s_add_u32 s26, s18, 0xb600000
	v_mad_u32_u24 v59, v2, s0, v3
	v_readlane_b32 s0, v253, 19
	s_addc_u32 s27, s19, 0
	v_readlane_b32 s2, v253, 21
	v_readlane_b32 s10, v253, 29
	v_readlane_b32 s3, v253, 22
	v_readlane_b32 s11, v253, 30
	s_add_u32 s2, s10, 0x4000000
	v_readlane_b32 s40, v253, 3
	s_addc_u32 s3, s11, 0
	v_readlane_b32 s52, v253, 15
	v_readlane_b32 s53, v253, 16
	s_add_u32 s22, s52, 0x2000
	v_readlane_b32 s8, v253, 27
	s_addc_u32 s23, s53, 0
	v_readlane_b32 s9, v253, 28
	s_add_u32 s84, s8, 0x2000
	s_addc_u32 s85, s9, 0
	s_add_u32 s33, s18, 0x200000
	v_readlane_b32 s44, v253, 7
	s_addc_u32 s38, s19, 0
	v_mov_b32_e32 v9, v11
	v_readlane_b32 s1, v253, 20
	v_readlane_b32 s45, v253, 8
	s_add_u32 s86, s44, 0xb140000
	v_mul_u32_u24_e32 v57, 0x84, v2
	v_readlane_b32 s42, v253, 5
	v_lshl_add_u64 v[2:3], s[18:19], 0, v[8:9]
	s_mov_b64 s[0:1], 0xd600000
	s_addc_u32 s87, s45, 0
	v_readlane_b32 s12, v253, 31
	v_readlane_b32 s13, v253, 32
	v_readlane_b32 s14, v253, 33
	v_readlane_b32 s15, v253, 34
	v_readlane_b32 s43, v253, 6
	v_readlane_b32 s54, v253, 17
	v_readlane_b32 s55, v253, 18
	v_lshl_add_u64 v[12:13], v[2:3], 0, s[0:1]
	s_add_u32 s88, s42, 0x4000
	s_mov_b64 s[0:1], 0x5c00000
	v_readlane_b32 s41, v253, 4
	v_readlane_b32 s46, v253, 9
	v_readlane_b32 s47, v253, 10
	v_readlane_b32 s48, v253, 11
	v_readlane_b32 s49, v253, 12
	v_readlane_b32 s50, v253, 13
	s_addc_u32 s89, s43, 0
	v_lshlrev_b32_e32 v4, 6, v18
	v_lshl_add_u64 v[14:15], v[2:3], 0, s[0:1]
	s_lshl_b32 s0, s80, 5
	s_movk_i32 s12, 0xe000
	s_movk_i32 s14, 0xe008
	s_movk_i32 s18, 0xe010
	s_movk_i32 s78, 0xe018
	s_movk_i32 s92, 0xe0d0
	s_movk_i32 s28, 0xe0d8
	s_movk_i32 s34, 0xe0e0
	s_movk_i32 s52, 0xe0e8
	s_movk_i32 s54, 0xe0f0
	s_movk_i32 s56, 0xe0f8
	v_or_b32_e32 v26, 0x2000, v18
	v_or_b32_e32 v27, 0x4000, v18
	v_or_b32_e32 v28, 0x6000, v18
	v_or_b32_e32 v29, 0x8000, v18
	v_or_b32_e32 v30, 0xa000, v18
	v_or_b32_e32 v31, 0xc000, v18
	v_or_b32_e32 v32, 0xe000, v18
	v_or_b32_e32 v33, 0x10000, v18
	v_or_b32_e32 v34, 0x12000, v18
	v_or_b32_e32 v35, 0x14000, v18
	v_or_b32_e32 v36, 0x16000, v18
	v_or_b32_e32 v37, 0x18000, v18
	v_or_b32_e32 v38, 0x1a000, v18
	v_or_b32_e32 v39, 0x1c000, v18
	v_or_b32_e32 v40, 0x1e000, v18
	v_or_b32_e32 v41, 0x20000, v18
	v_or_b32_e32 v42, 0x22000, v18
	v_or_b32_e32 v43, 0x24000, v18
	v_or_b32_e32 v44, 0x26000, v18
	v_or_b32_e32 v45, 0x28000, v18
	v_or_b32_e32 v46, 0x2a000, v18
	v_or_b32_e32 v47, 0x2c000, v18
	v_or_b32_e32 v48, 0x2e000, v18
	v_or_b32_e32 v49, 0x30000, v18
	v_or_b32_e32 v50, 0x32000, v18
	v_or_b32_e32 v51, 0x34000, v18
	v_or_b32_e32 v52, 0x36000, v18
	v_or_b32_e32 v53, 0x38000, v18
	v_or_b32_e32 v54, 0x3a000, v18
	v_or_b32_e32 v55, 0x3c000, v18
	v_or_b32_e32 v56, 0x3e000, v18
	v_and_b32_e32 v60, 64, v4
	v_mov_b32_e32 v7, v11
	s_lshl_b32 s39, s80, 6
	s_add_i32 s40, s0, 0xfff4c000
	s_lshl_b32 s41, s83, 8
	s_lshl_b32 s42, s80, 4
	s_lshl_b32 s43, s83, 7
	s_mov_b32 s91, 0
	s_mov_b32 s44, 0xc3e00000
	s_movk_i32 s45, 0x7fff
	s_mov_b32 s46, 0xffff0000
	s_movk_i32 s47, 0x2c2f
	s_movk_i32 s48, 0x2c50
	s_mov_b32 s49, 0xb140
	v_add_u32_e32 v61, 0x400, v19
	v_add_u32_e32 v62, 0x800, v19
	v_add_u32_e32 v63, 0xc00, v19
	v_mov_b32_e32 v64, 0x43e00000
	s_mov_b32 s50, s80
	s_mov_b32 s13, -1
	s_mov_b32 s15, -1
	s_mov_b32 s19, -1
	s_mov_b32 s79, -1
	s_mov_b32 s93, -1
	s_mov_b32 s29, -1
	s_mov_b32 s35, -1
	s_mov_b32 s53, -1
	s_mov_b32 s55, -1
	s_mov_b32 s57, -1
	v_readlane_b32 s16, v253, 39
	v_readlane_b32 s17, v253, 40
	v_readlane_b32 s4, v253, 23
	v_readlane_b32 s5, v253, 24
	v_readlane_b32 s6, v253, 25
	v_readlane_b32 s7, v253, 26
	v_readlane_b32 s51, v253, 14
	s_branch .LBB0_15

; #define LAS __attribute__((address_space(3)))
; __device__ __forceinline__ int nat_dim(int p) { return (p >> 1) + 64 * (p & 1); }
; template <int MAP, bool KS, bool KPERM = false>
; __device__ __forceinline__ void p0_transpose_item(const float* W, int K, int Nsrc, int nblk, bf16* WT, const float* ksA, const float* ksB, int ksplit, LAS float* scr, int item, int lane) {
;     const int kb = item / nblk, nb = item % nblk, k0 = 64 * kb, n0 = 32 * nb;
;     const int nr = n0 + (lane & 31); const int sc = MAP == 1 ? src_col_in(nr) : (MAP == 2 ? nat_dim(nr) : nr);
;     float v[32];
; #pragma unroll
;     for (int i = 0; i < 32; ++i) { const int k = k0 + 2 * i + (lane >> 5); const int ksrc = KPERM ? ((k & ~127) + nat_dim(k & 127)) : k;
;         v[i] = sc >= 0 ? W[(size_t)ksrc * Nsrc + sc] : 0.f; }
; #pragma unroll
;     for (int i = 0; i < 32; ++i) { const int kk = 2 * i + (lane >> 5); const int k = k0 + kk;
;         if (KS) v[i] *= (k < ksplit ? ksA[k] : ksB[k - ksplit]);
;         scr[kk * 33 + (lane & 31)] = v[i]; }
; __global__ void __launch_bounds__(NWAVES * 64, 2) hybrid_fwd(Args args) {
;     ...
;             if (r < I_O) { if (l >= WO_F8_FROM) p0_transpose_item_f8<true>(args.in[13] + (size_t)l * DM * DM, DM, DM, DM / 32, (unsigned char*)(ws + WS_WO + l * SZ_WO), 64.f, args.in[6] + l * 2048, args.in[12] + l * 2048, 2048, scr, r, lane);
;                 else p0_transpose_item<0, true>(args.in[13] + (size_t)l * DM * DM, DM, DM, DM / 32, (bf16*)(ws + WS_WO + l * SZ_WO), args.in[6] + l * 2048, args.in[12] + l * 2048, 2048, scr, r, lane); continue; } r -= I_O;
.LBB0_22:
	s_andn2_b64 vcc, exec, s[0:1]
	s_cbranch_vccnz .LBB0_27
	s_branch .LBB0_14
	s_add_i32 s82, s51, 0xffffa600
	s_cmp_lt_i32 s50, 0x17a00
	s_mov_b64 s[0:1], -1
	s_cbranch_scc0 .LBB0_25
	s_ashr_i32 s59, s58, 31
	v_readlane_b32 s4, v253, 19
	s_lshl_b64 s[0:1], s[58:59], 26
	v_readlane_b32 s14, v253, 29
	v_readlane_b32 s15, v253, 30
	s_add_u32 s30, s14, s0
	s_addc_u32 s31, s15, s1
	s_lshl_b64 s[0:1], s[58:59], 25
	s_add_u32 s21, s26, s0
	s_addc_u32 s59, s27, s1
	s_lshl_b32 s0, s58, 11
	s_ashr_i32 s1, s0, 31
	v_readlane_b32 s60, v253, 3
	s_lshl_b64 s[36:37], s[0:1], 2
	v_readlane_b32 s72, v253, 15
	v_readlane_b32 s73, v253, 16
	s_add_u32 s0, s72, s36
	v_readlane_b32 s12, v253, 27
	s_addc_u32 s1, s73, s37
	v_readlane_b32 s13, v253, 28
	s_add_u32 s36, s12, s36
	s_addc_u32 s37, s13, s37
	s_lshr_b32 s20, s82, 1
	s_and_b32 s60, s20, 0xfc0
	v_or_b32_e32 v2, s60, v6
	s_and_b32 s20, s40, 0xfe0
	v_lshlrev_b32_e32 v3, 12, v2
	v_or3_b32 v4, s20, v18, v3
	v_lshlrev_b32_e32 v4, 2, v4
	global_load_dword v84, v4, s[30:31]
	v_or3_b32 v4, s20, v26, v3
	v_lshlrev_b32_e32 v4, 2, v4
	global_load_dword v86, v4, s[30:31]
	v_or3_b32 v4, s20, v27, v3
	v_lshlrev_b32_e32 v4, 2, v4
	global_load_dword v87, v4, s[30:31]
	v_or3_b32 v4, s20, v28, v3
	v_lshlrev_b32_e32 v4, 2, v4
	global_load_dword v88, v4, s[30:31]
	v_or3_b32 v4, s20, v29, v3
	v_lshlrev_b32_e32 v4, 2, v4
	global_load_dword v89, v4, s[30:31]
	v_or3_b32 v4, s20, v30, v3
	v_lshlrev_b32_e32 v4, 2, v4
	global_load_dword v90, v4, s[30:31]
	v_or3_b32 v4, s20, v31, v3
	v_lshlrev_b32_e32 v4, 2, v4
	global_load_dword v91, v4, s[30:31]
	v_or3_b32 v4, s20, v32, v3
	v_lshlrev_b32_e32 v4, 2, v4
	global_load_dword v92, v4, s[30:31]
	v_or3_b32 v4, s20, v33, v3
	v_lshlrev_b32_e32 v4, 2, v4
	global_load_dword v93, v4, s[30:31]
	v_or3_b32 v4, s20, v34, v3
	v_lshlrev_b32_e32 v4, 2, v4
	global_load_dword v94, v4, s[30:31]
	v_or3_b32 v4, s20, v35, v3
	v_lshlrev_b32_e32 v4, 2, v4
	global_load_dword v95, v4, s[30:31]
	v_or3_b32 v4, s20, v36, v3
	v_lshlrev_b32_e32 v4, 2, v4
	global_load_dword v96, v4, s[30:31]
	v_or3_b32 v4, s20, v37, v3
	v_lshlrev_b32_e32 v4, 2, v4
	global_load_dword v97, v4, s[30:31]
	v_or3_b32 v4, s20, v38, v3
	v_lshlrev_b32_e32 v4, 2, v4
	global_load_dword v81, v4, s[30:31]
	v_or3_b32 v4, s20, v39, v3
	v_lshlrev_b32_e32 v4, 2, v4
	global_load_dword v79, v4, s[30:31]
	v_or3_b32 v4, s20, v40, v3
	v_lshlrev_b32_e32 v4, 2, v4
	global_load_dword v80, v4, s[30:31]
	v_or3_b32 v4, s20, v41, v3
	v_lshlrev_b32_e32 v4, 2, v4
	global_load_dword v78, v4, s[30:31]
	v_or3_b32 v4, s20, v42, v3
	v_lshlrev_b32_e32 v4, 2, v4
	global_load_dword v77, v4, s[30:31]
	v_or3_b32 v4, s20, v43, v3
	v_lshlrev_b32_e32 v4, 2, v4
	global_load_dword v76, v4, s[30:31]
	v_or3_b32 v4, s20, v44, v3
	v_lshlrev_b32_e32 v4, 2, v4
	global_load_dword v75, v4, s[30:31]
	v_or3_b32 v4, s20, v45, v3
	v_lshlrev_b32_e32 v4, 2, v4
	global_load_dword v74, v4, s[30:31]
	v_or3_b32 v4, s20, v46, v3
	v_lshlrev_b32_e32 v4, 2, v4
	global_load_dword v73, v4, s[30:31]
	v_or3_b32 v4, s20, v47, v3
	v_lshlrev_b32_e32 v4, 2, v4
	global_load_dword v72, v4, s[30:31]
	v_or3_b32 v4, s20, v48, v3
	v_lshlrev_b32_e32 v4, 2, v4
	global_load_dword v71, v4, s[30:31]
	v_or3_b32 v4, s20, v49, v3
	v_lshlrev_b32_e32 v4, 2, v4
	global_load_dword v70, v4, s[30:31]
	v_or3_b32 v4, s20, v50, v3
	v_lshlrev_b32_e32 v4, 2, v4
	global_load_dword v69, v4, s[30:31]
	v_or3_b32 v4, s20, v51, v3
	v_lshlrev_b32_e32 v4, 2, v4
	global_load_dword v68, v4, s[30:31]
	v_or3_b32 v4, s20, v52, v3
	v_lshlrev_b32_e32 v4, 2, v4
	global_load_dword v67, v4, s[30:31]
	v_or3_b32 v4, s20, v53, v3
	v_lshlrev_b32_e32 v4, 2, v4
	global_load_dword v66, v4, s[30:31]
	v_or3_b32 v4, s20, v54, v3
	v_lshlrev_b32_e32 v4, 2, v4
	global_load_dword v65, v4, s[30:31]
	v_or3_b32 v4, s20, v55, v3
	v_or3_b32 v3, s20, v56, v3
	s_movk_i32 s12, 0xe000
	v_lshlrev_b32_e32 v4, 2, v4
	v_lshlrev_b32_e32 v3, 2, v3
	v_lshlrev_b32_e32 v10, 2, v2
	s_mov_b32 s13, -1
	global_load_dword v17, v4, s[30:31]
	global_load_dword v16, v3, s[30:31]
	s_cmpk_lt_u32 s82, 0x1000
	v_lshl_add_u64 v[2:3], s[36:37], 0, v[10:11]
	s_cselect_b64 vcc, -1, 0
	v_lshl_add_u64 v[82:83], v[2:3], 0, s[12:13]
	v_lshl_add_u64 v[4:5], s[0:1], 0, v[10:11]
	v_cndmask_b32_e32 v83, v83, v5, vcc
	v_cndmask_b32_e32 v82, v82, v4, vcc
	global_load_dword v10, v[82:83], off
	s_movk_i32 s14, 0xe008
	v_readlane_b32 s18, v253, 33
	v_readlane_b32 s19, v253, 34
	s_mov_b32 s15, -1
	s_movk_i32 s18, 0xe010
	v_lshl_add_u64 v[82:83], v[4:5], 0, 8
	s_mov_b32 s19, -1
	s_movk_i32 s0, 0xe020
	s_mov_b32 s1, -1
	v_readlane_b32 s5, v253, 20
	v_readlane_b32 s6, v253, 21
	v_readlane_b32 s7, v253, 22
	v_readlane_b32 s8, v253, 23
	v_readlane_b32 s9, v253, 24
	v_readlane_b32 s10, v253, 25
	v_readlane_b32 s11, v253, 26
	v_readlane_b32 s16, v253, 31
	v_readlane_b32 s17, v253, 32
	v_readlane_b32 s61, v253, 4
	v_readlane_b32 s62, v253, 5
	v_readlane_b32 s63, v253, 6
	v_readlane_b32 s64, v253, 7
	v_readlane_b32 s65, v253, 8
	v_readlane_b32 s66, v253, 9
	v_readlane_b32 s67, v253, 10
	v_readlane_b32 s68, v253, 11
	v_readlane_b32 s69, v253, 12
	v_readlane_b32 s70, v253, 13
	v_readlane_b32 s71, v253, 14
	v_readlane_b32 s74, v253, 17
	v_readlane_b32 s75, v253, 18
	s_waitcnt vmcnt(0)
	v_mul_f32_e32 v10, v84, v10
	v_lshl_add_u64 v[84:85], v[2:3], 0, s[14:15]
	v_cndmask_b32_e32 v83, v85, v83, vcc
	v_cndmask_b32_e32 v82, v84, v82, vcc
	ds_write_b32 v19, v10
	global_load_dword v10, v[82:83], off
	v_lshl_add_u64 v[82:83], v[4:5], 0, 16
	v_lshl_add_u64 v[84:85], v[2:3], 0, s[18:19]
	v_cndmask_b32_e32 v83, v85, v83, vcc
	v_cndmask_b32_e32 v82, v84, v82, vcc
	global_load_dword v82, v[82:83], off
	v_lshl_add_u64 v[84:85], v[2:3], 0, s[78:79]
	s_waitcnt vmcnt(1)
; __device__ __forceinline__ int nat_dim(int p) { return (p >> 1) + 64 * (p & 1); }
; template <int MAP, bool KS, bool KPERM = false>
; __device__ __forceinline__ void p0_transpose_item(const float* W, int K, int Nsrc, int nblk, bf16* WT, const float* ksA, const float* ksB, int ksplit, LAS float* scr, int item, int lane) {
;     ...
;     for (int i = 0; i < 32; ++i) { const int k = k0 + 2 * i + (lane >> 5); const int ksrc = KPERM ? ((k & ~127) + nat_dim(k & 127)) : k;
;         v[i] = sc >= 0 ? W[(size_t)ksrc * Nsrc + sc] : 0.f; }
; #pragma unroll
;     for (int i = 0; i < 32; ++i) { const int kk = 2 * i + (lane >> 5); const int k = k0 + kk;
;         if (KS) v[i] *= (k < ksplit ? ksA[k] : ksB[k - ksplit]);
;         scr[kk * 33 + (lane & 31)] = v[i]; }
	v_mul_f32_e32 v10, v86, v10
	v_add_u32_e32 v86, v25, v57
	s_waitcnt vmcnt(0)
	v_mul_f32_e32 v82, v87, v82
	ds_write2_b32 v86, v10, v82 offset1:66
	v_lshl_add_u64 v[82:83], v[4:5], 0, 24
	v_cndmask_b32_e32 v83, v85, v83, vcc
	v_cndmask_b32_e32 v82, v84, v82, vcc
	global_load_dword v10, v[82:83], off
	v_lshl_add_u64 v[82:83], v[4:5], 0, 32
	v_lshl_add_u64 v[84:85], v[2:3], 0, s[0:1]
	v_cndmask_b32_e32 v83, v85, v83, vcc
	v_cndmask_b32_e32 v82, v84, v82, vcc
	global_load_dword v82, v[82:83], off
	s_movk_i32 s0, 0xe028
	s_mov_b32 s1, -1
	v_lshl_add_u64 v[84:85], v[2:3], 0, s[0:1]
	s_movk_i32 s0, 0xe030
	s_mov_b32 s1, -1
	s_waitcnt vmcnt(1)
	v_mul_f32_e32 v10, v88, v10
	s_waitcnt vmcnt(0)
	v_mul_f32_e32 v82, v89, v82
	ds_write2_b32 v86, v10, v82 offset0:132 offset1:198
	v_lshl_add_u64 v[82:83], v[4:5], 0, 40
	v_cndmask_b32_e32 v83, v85, v83, vcc
	v_cndmask_b32_e32 v82, v84, v82, vcc
	global_load_dword v10, v[82:83], off
	v_lshl_add_u64 v[82:83], v[4:5], 0, 48
	v_lshl_add_u64 v[84:85], v[2:3], 0, s[0:1]
	v_cndmask_b32_e32 v83, v85, v83, vcc
	v_cndmask_b32_e32 v82, v84, v82, vcc
	global_load_dword v82, v[82:83], off
	s_movk_i32 s0, 0xe038
	v_add_u32_e32 v83, 0x400, v86
	s_mov_b32 s1, -1
	v_lshl_add_u64 v[84:85], v[2:3], 0, s[0:1]
	s_movk_i32 s0, 0xe040
	s_mov_b32 s1, -1
	v_add_u32_e32 v86, v25, v58
	s_waitcnt vmcnt(1)
	v_mul_f32_e32 v10, v90, v10
	s_waitcnt vmcnt(0)
	v_mul_f32_e32 v82, v91, v82
	ds_write2_b32 v83, v10, v82 offset0:8 offset1:74
	v_lshl_add_u64 v[82:83], v[4:5], 0, 56
	v_cndmask_b32_e32 v83, v85, v83, vcc
	v_cndmask_b32_e32 v82, v84, v82, vcc
	global_load_dword v10, v[82:83], off
	v_lshl_add_u64 v[82:83], v[4:5], 0, 64
	v_lshl_add_u64 v[84:85], v[2:3], 0, s[0:1]
	v_cndmask_b32_e32 v83, v85, v83, vcc
	v_cndmask_b32_e32 v82, v84, v82, vcc
	global_load_dword v82, v[82:83], off
	s_mov_b64 s[0:1], 0x48
	s_waitcnt vmcnt(1)
	v_mul_f32_e32 v10, v92, v10
	s_waitcnt vmcnt(0)
	v_mul_f32_e32 v82, v93, v82
	ds_write2_b32 v86, v10, v82 offset1:66
	v_lshl_add_u64 v[82:83], v[4:5], 0, s[0:1]
	s_movk_i32 s0, 0xe048
	s_mov_b32 s1, -1
	v_lshl_add_u64 v[84:85], v[2:3], 0, s[0:1]
	v_cndmask_b32_e32 v83, v85, v83, vcc
	v_cndmask_b32_e32 v82, v84, v82, vcc
	s_mov_b64 s[0:1], 0x50
	global_load_dword v10, v[82:83], off
	v_lshl_add_u64 v[82:83], v[4:5], 0, s[0:1]
	s_movk_i32 s0, 0xe050
	s_mov_b32 s1, -1
	v_lshl_add_u64 v[84:85], v[2:3], 0, s[0:1]
	v_cndmask_b32_e32 v83, v85, v83, vcc
	v_cndmask_b32_e32 v82, v84, v82, vcc
	global_load_dword v82, v[82:83], off
	s_mov_b64 s[0:1], 0x58
	s_waitcnt vmcnt(1)
	v_mul_f32_e32 v10, v94, v10
	s_waitcnt vmcnt(0)
	v_mul_f32_e32 v82, v95, v82
	ds_write2_b32 v86, v10, v82 offset0:132 offset1:198
	v_lshl_add_u64 v[82:83], v[4:5], 0, s[0:1]
	s_movk_i32 s0, 0xe058
	s_mov_b32 s1, -1
	v_lshl_add_u64 v[84:85], v[2:3], 0, s[0:1]
	v_cndmask_b32_e32 v83, v85, v83, vcc
	v_cndmask_b32_e32 v82, v84, v82, vcc
	s_mov_b64 s[0:1], 0x60
	global_load_dword v10, v[82:83], off
	v_lshl_add_u64 v[82:83], v[4:5], 0, s[0:1]
	s_movk_i32 s0, 0xe060
	s_mov_b32 s1, -1
	v_lshl_add_u64 v[84:85], v[2:3], 0, s[0:1]
	v_cndmask_b32_e32 v83, v85, v83, vcc
	v_cndmask_b32_e32 v82, v84, v82, vcc
	global_load_dword v82, v[82:83], off
	v_add_u32_e32 v83, 0x400, v86
	s_mov_b64 s[0:1], 0x68
	s_waitcnt vmcnt(1)
	v_mul_f32_e32 v10, v96, v10
	s_waitcnt vmcnt(0)
	v_mul_f32_e32 v82, v97, v82
	ds_write2_b32 v83, v10, v82 offset0:8 offset1:74
	v_lshl_add_u64 v[82:83], v[4:5], 0, s[0:1]
	s_movk_i32 s0, 0xe068
	s_mov_b32 s1, -1
	v_lshl_add_u64 v[84:85], v[2:3], 0, s[0:1]
	v_cndmask_b32_e32 v83, v85, v83, vcc
	v_cndmask_b32_e32 v82, v84, v82, vcc
	s_mov_b64 s[0:1], 0x70
	global_load_dword v10, v[82:83], off
	v_lshl_add_u64 v[82:83], v[4:5], 0, s[0:1]
	s_movk_i32 s0, 0xe070
	s_mov_b32 s1, -1
	v_lshl_add_u64 v[84:85], v[2:3], 0, s[0:1]
	v_cndmask_b32_e32 v83, v85, v83, vcc
	v_cndmask_b32_e32 v82, v84, v82, vcc
	global_load_dword v82, v[82:83], off
	s_mov_b64 s[0:1], 0x78
	s_waitcnt vmcnt(1)
	v_mul_f32_e32 v81, v81, v10
	v_add_u32_e32 v10, v25, v59
	s_waitcnt vmcnt(0)
	v_mul_f32_e32 v79, v79, v82
	v_lshl_add_u64 v[82:83], v[4:5], 0, s[0:1]
	s_movk_i32 s0, 0xe078
	s_mov_b32 s1, -1
	v_lshl_add_u64 v[84:85], v[2:3], 0, s[0:1]
	v_cndmask_b32_e32 v83, v85, v83, vcc
	v_cndmask_b32_e32 v82, v84, v82, vcc
	ds_write2_b32 v10, v81, v79 offset1:66
	global_load_dword v79, v[82:83], off
	s_mov_b64 s[0:1], 0x80
	s_waitcnt vmcnt(0)
	v_mul_f32_e32 v79, v80, v79
	v_lshl_add_u64 v[80:81], v[4:5], 0, s[0:1]
	s_movk_i32 s0, 0xe080
	s_mov_b32 s1, -1
	v_lshl_add_u64 v[82:83], v[2:3], 0, s[0:1]
	v_cndmask_b32_e32 v81, v83, v81, vcc
	v_cndmask_b32_e32 v80, v82, v80, vcc
	global_load_dword v80, v[80:81], off
	s_mov_b64 s[0:1], 0x88
	s_waitcnt vmcnt(0)
	v_mul_f32_e32 v78, v78, v80
	ds_write2_b32 v10, v79, v78 offset0:132 offset1:198
	v_lshl_add_u64 v[78:79], v[4:5], 0, s[0:1]
	s_movk_i32 s0, 0xe088
	s_mov_b32 s1, -1
	v_lshl_add_u64 v[80:81], v[2:3], 0, s[0:1]
	v_cndmask_b32_e32 v79, v81, v79, vcc
	v_cndmask_b32_e32 v78, v80, v78, vcc
	global_load_dword v78, v[78:79], off
	s_mov_b64 s[0:1], 0x90
	s_waitcnt vmcnt(0)
	v_mul_f32_e32 v77, v77, v78
	v_lshl_add_u64 v[78:79], v[4:5], 0, s[0:1]
	s_movk_i32 s0, 0xe090
	s_mov_b32 s1, -1
	v_lshl_add_u64 v[80:81], v[2:3], 0, s[0:1]
	v_cndmask_b32_e32 v79, v81, v79, vcc
	v_cndmask_b32_e32 v78, v80, v78, vcc
	global_load_dword v78, v[78:79], off
	v_add_u32_e32 v80, 0x400, v10
	s_mov_b64 s[0:1], 0x98
	s_waitcnt vmcnt(0)
	v_mul_f32_e32 v76, v76, v78
	ds_write2_b32 v80, v77, v76 offset0:8 offset1:74
	v_lshl_add_u64 v[76:77], v[4:5], 0, s[0:1]
	s_movk_i32 s0, 0xe098
	s_mov_b32 s1, -1
	v_lshl_add_u64 v[78:79], v[2:3], 0, s[0:1]
	v_cndmask_b32_e32 v77, v79, v77, vcc
	v_cndmask_b32_e32 v76, v78, v76, vcc
	global_load_dword v76, v[76:77], off
	s_mov_b64 s[0:1], 0xa0
	s_waitcnt vmcnt(0)
; #define LAS __attribute__((address_space(3)))
; #define LDS_WAIT() asm volatile("s_waitcnt lgkmcnt(0)" ::: "memory")
; __device__ __forceinline__ unsigned pk2(float lo, float hi) { return f2bf(lo) | (f2bf(hi) << 16); }
; template <int MAP, bool KS, bool KPERM = false>
; __device__ __forceinline__ void p0_transpose_item(const float* W, int K, int Nsrc, int nblk, bf16* WT, const float* ksA, const float* ksB, int ksplit, LAS float* scr, int item, int lane) {
;     ...
;     for (int i = 0; i < 32; ++i) { const int kk = 2 * i + (lane >> 5); const int k = k0 + kk;
;         if (KS) v[i] *= (k < ksplit ? ksA[k] : ksB[k - ksplit]);
;         scr[kk * 33 + (lane & 31)] = v[i]; }
;     LDS_WAIT(); asm volatile("" ::: "memory");
;     const int c = lane & 7;
; #pragma unroll
;     for (int j = 0; j < 4; ++j) { const int n = (lane >> 3) + 8 * j; const LAS float* s = scr + (8 * c) * 33 + n;
;         v4u o; o.x = pk2(s[0 * 33], s[1 * 33]); o.y = pk2(s[2 * 33], s[3 * 33]); o.z = pk2(s[4 * 33], s[5 * 33]); o.w = pk2(s[6 * 33], s[7 * 33]);
	v_mul_f32_e32 v75, v75, v76
	v_lshl_add_u64 v[76:77], v[4:5], 0, s[0:1]
	s_movk_i32 s0, 0xe0a0
	s_mov_b32 s1, -1
	v_lshl_add_u64 v[78:79], v[2:3], 0, s[0:1]
	v_cndmask_b32_e32 v77, v79, v77, vcc
	v_cndmask_b32_e32 v76, v78, v76, vcc
	global_load_dword v76, v[76:77], off
	s_mov_b64 s[0:1], 0xa8
	s_waitcnt vmcnt(0)
	v_mul_f32_e32 v74, v74, v76
	ds_write2_b32 v80, v75, v74 offset0:140 offset1:206
	v_lshl_add_u64 v[74:75], v[4:5], 0, s[0:1]
	s_movk_i32 s0, 0xe0a8
	s_mov_b32 s1, -1
	v_lshl_add_u64 v[76:77], v[2:3], 0, s[0:1]
	v_cndmask_b32_e32 v75, v77, v75, vcc
	v_cndmask_b32_e32 v74, v76, v74, vcc
	global_load_dword v74, v[74:75], off
	s_mov_b64 s[0:1], 0xb0
	s_waitcnt vmcnt(0)
	v_mul_f32_e32 v73, v73, v74
	v_lshl_add_u64 v[74:75], v[4:5], 0, s[0:1]
	s_movk_i32 s0, 0xe0b0
	s_mov_b32 s1, -1
	v_lshl_add_u64 v[76:77], v[2:3], 0, s[0:1]
	v_cndmask_b32_e32 v75, v77, v75, vcc
	v_cndmask_b32_e32 v74, v76, v74, vcc
	global_load_dword v74, v[74:75], off
	v_add_u32_e32 v76, 0x800, v10
	s_mov_b64 s[0:1], 0xb8
	s_waitcnt vmcnt(0)
	v_mul_f32_e32 v72, v72, v74
	ds_write2_b32 v76, v73, v72 offset0:16 offset1:82
	v_lshl_add_u64 v[72:73], v[4:5], 0, s[0:1]
	s_movk_i32 s0, 0xe0b8
	s_mov_b32 s1, -1
	v_lshl_add_u64 v[74:75], v[2:3], 0, s[0:1]
	v_cndmask_b32_e32 v73, v75, v73, vcc
	v_cndmask_b32_e32 v72, v74, v72, vcc
	global_load_dword v72, v[72:73], off
	s_mov_b64 s[0:1], 0xc0
	s_waitcnt vmcnt(0)
	v_mul_f32_e32 v71, v71, v72
	v_lshl_add_u64 v[72:73], v[4:5], 0, s[0:1]
	s_movk_i32 s0, 0xe0c0
	s_mov_b32 s1, -1
	v_lshl_add_u64 v[74:75], v[2:3], 0, s[0:1]
	v_cndmask_b32_e32 v73, v75, v73, vcc
	v_cndmask_b32_e32 v72, v74, v72, vcc
	global_load_dword v72, v[72:73], off
	s_mov_b64 s[0:1], 0xc8
	s_waitcnt vmcnt(0)
	v_mul_f32_e32 v70, v70, v72
	ds_write2_b32 v76, v71, v70 offset0:148 offset1:214
	v_lshl_add_u64 v[70:71], v[4:5], 0, s[0:1]
	s_movk_i32 s0, 0xe0c8
	s_mov_b32 s1, -1
	v_lshl_add_u64 v[72:73], v[2:3], 0, s[0:1]
	v_cndmask_b32_e32 v71, v73, v71, vcc
	v_cndmask_b32_e32 v70, v72, v70, vcc
	global_load_dword v70, v[70:71], off
	s_mov_b64 s[0:1], 0xd0
	v_lshl_add_u64 v[72:73], v[2:3], 0, s[92:93]
	s_waitcnt vmcnt(0)
	v_mul_f32_e32 v69, v69, v70
	v_lshl_add_u64 v[70:71], v[4:5], 0, s[0:1]
	v_cndmask_b32_e32 v71, v73, v71, vcc
	v_cndmask_b32_e32 v70, v72, v70, vcc
	global_load_dword v70, v[70:71], off
	v_add_u32_e32 v72, 0xc00, v10
	s_mov_b64 s[0:1], 0xd8
	s_waitcnt vmcnt(0)
	v_mul_f32_e32 v68, v68, v70
	ds_write2_b32 v72, v69, v68 offset0:24 offset1:90
	v_lshl_add_u64 v[68:69], v[4:5], 0, s[0:1]
	v_lshl_add_u64 v[70:71], v[2:3], 0, s[28:29]
	v_cndmask_b32_e32 v69, v71, v69, vcc
	v_cndmask_b32_e32 v68, v70, v68, vcc
	global_load_dword v68, v[68:69], off
	s_mov_b64 s[0:1], 0xe0
	v_lshl_add_u64 v[70:71], v[2:3], 0, s[34:35]
	s_waitcnt vmcnt(0)
	v_mul_f32_e32 v67, v67, v68
	v_lshl_add_u64 v[68:69], v[4:5], 0, s[0:1]
	v_cndmask_b32_e32 v69, v71, v69, vcc
	v_cndmask_b32_e32 v68, v70, v68, vcc
	global_load_dword v68, v[68:69], off
	s_mov_b64 s[0:1], 0xe8
	s_waitcnt vmcnt(0)
	v_mul_f32_e32 v66, v66, v68
	ds_write2_b32 v72, v67, v66 offset0:156 offset1:222
	v_lshl_add_u64 v[66:67], v[4:5], 0, s[0:1]
	v_lshl_add_u64 v[68:69], v[2:3], 0, s[52:53]
	v_cndmask_b32_e32 v67, v69, v67, vcc
	v_cndmask_b32_e32 v66, v68, v66, vcc
	global_load_dword v66, v[66:67], off
	s_mov_b64 s[0:1], 0xf0
	v_lshl_add_u64 v[68:69], v[2:3], 0, s[54:55]
	v_lshl_add_u64 v[2:3], v[2:3], 0, s[56:57]
	s_waitcnt vmcnt(0)
	v_mul_f32_e32 v65, v65, v66
	v_lshl_add_u64 v[66:67], v[4:5], 0, s[0:1]
	s_mov_b64 s[0:1], 0xf8
	v_lshl_add_u64 v[4:5], v[4:5], 0, s[0:1]
	v_cndmask_b32_e32 v67, v69, v67, vcc
	v_cndmask_b32_e32 v66, v68, v66, vcc
	v_cndmask_b32_e32 v3, v3, v5, vcc
	v_cndmask_b32_e32 v2, v2, v4, vcc
	global_load_dword v66, v[66:67], off
	s_lshl_b32 s0, s60, 1
	global_load_dword v2, v[2:3], off
	s_add_u32 s0, s21, s0
	s_addc_u32 s1, s59, 0
	s_waitcnt vmcnt(1)
	v_mul_f32_e32 v17, v17, v66
	v_add_u32_e32 v66, 0x1000, v10
	s_waitcnt vmcnt(0)
	v_mul_f32_e32 v2, v16, v2
	ds_write2_b32 v66, v65, v17 offset0:32 offset1:98
	ds_write_b32 v10, v2 offset:4752
	s_waitcnt lgkmcnt(0)
	ds_read2_b32 v[66:67], v21 offset0:33 offset1:41
	ds_read2_b32 v[68:69], v21 offset1:8
	ds_read2_b32 v[70:71], v21 offset0:66 offset1:74
	ds_read2_b32 v[72:73], v21 offset0:99 offset1:107
	ds_read2_b32 v[74:75], v21 offset0:132 offset1:140
	ds_read2_b32 v[76:77], v21 offset0:165 offset1:173
	ds_read2_b32 v[78:79], v21 offset0:198 offset1:206
	ds_read2_b32 v[80:81], v21 offset0:231 offset1:239
	s_waitcnt lgkmcnt(7)
; #define GAS __attribute__((address_space(1)))
; #define LAS __attribute__((address_space(3)))
; #define LDS_WAIT() asm volatile("s_waitcnt lgkmcnt(0)" ::: "memory")
; __device__ __forceinline__ unsigned f2bf(float f) { unsigned u = __builtin_bit_cast(unsigned, f); return (u + 0x7fffu + ((u >> 16) & 1u)) >> 16; }
; __device__ __forceinline__ unsigned pk2(float lo, float hi) { return f2bf(lo) | (f2bf(hi) << 16); }
; template <int MAP, bool KS, bool KPERM = false>
; __device__ __forceinline__ void p0_transpose_item(const float* W, int K, int Nsrc, int nblk, bf16* WT, const float* ksA, const float* ksB, int ksplit, LAS float* scr, int item, int lane) {
;     ...
;     const int c = lane & 7;
; #pragma unroll
;     for (int j = 0; j < 4; ++j) { const int n = (lane >> 3) + 8 * j; const LAS float* s = scr + (8 * c) * 33 + n;
;         v4u o; o.x = pk2(s[0 * 33], s[1 * 33]); o.y = pk2(s[2 * 33], s[3 * 33]); o.z = pk2(s[4 * 33], s[5 * 33]); o.w = pk2(s[6 * 33], s[7 * 33]);
;         *(GAS v4u*)(WT + (size_t)(n0 + n) * K + k0 + 8 * c) = o; }
;     LDS_WAIT(); asm volatile("" ::: "memory");
	v_bfe_u32 v3, v66, 16, 1
	s_waitcnt lgkmcnt(6)
	v_bfe_u32 v2, v68, 16, 1
	v_add3_u32 v2, v68, v2, s45
	v_lshrrev_b32_e32 v2, 16, v2
	v_add3_u32 v3, v66, v3, s45
	v_and_or_b32 v2, v3, s46, v2
	s_waitcnt lgkmcnt(5)
	v_bfe_u32 v3, v70, 16, 1
	v_add3_u32 v3, v70, v3, s45
	s_waitcnt lgkmcnt(4)
	v_bfe_u32 v4, v72, 16, 1
	v_lshrrev_b32_e32 v3, 16, v3
	v_add3_u32 v4, v72, v4, s45
	v_and_or_b32 v3, v4, s46, v3
	s_waitcnt lgkmcnt(3)
	v_bfe_u32 v4, v74, 16, 1
	v_add3_u32 v4, v74, v4, s45
	s_waitcnt lgkmcnt(2)
	v_bfe_u32 v5, v76, 16, 1
	v_lshrrev_b32_e32 v4, 16, v4
	v_add3_u32 v5, v76, v5, s45
	v_lshlrev_b32_e32 v10, 1, v8
	v_and_or_b32 v4, v5, s46, v4
	s_waitcnt lgkmcnt(1)
	v_bfe_u32 v5, v78, 16, 1
	v_lshl_add_u64 v[16:17], s[0:1], 0, v[10:11]
	v_add3_u32 v5, v78, v5, s45
	s_waitcnt lgkmcnt(0)
	v_bfe_u32 v10, v80, 16, 1
	v_lshrrev_b32_e32 v5, 16, v5
	v_add3_u32 v10, v80, v10, s45
	v_and_or_b32 v5, v10, s46, v5
	v_or_b32_e32 v10, s20, v20
	v_lshlrev_b32_e32 v10, 13, v10
	v_lshl_add_u64 v[82:83], v[16:17], 0, v[10:11]
	global_store_dwordx4 v[82:83], v[2:5], off
	v_bfe_u32 v10, v81, 16, 1
	v_add3_u32 v10, v81, v10, s45
	v_bfe_u32 v2, v69, 16, 1
	v_add3_u32 v2, v69, v2, s45
	v_bfe_u32 v3, v67, 16, 1
	v_lshrrev_b32_e32 v2, 16, v2
	v_add3_u32 v3, v67, v3, s45
	v_and_or_b32 v2, v3, s46, v2
	v_bfe_u32 v3, v71, 16, 1
	v_add3_u32 v3, v71, v3, s45
	v_bfe_u32 v4, v73, 16, 1
	v_lshrrev_b32_e32 v3, 16, v3
	v_add3_u32 v4, v73, v4, s45
	v_and_or_b32 v3, v4, s46, v3
	v_bfe_u32 v4, v75, 16, 1
	v_add3_u32 v4, v75, v4, s45
	v_bfe_u32 v5, v77, 16, 1
	v_lshrrev_b32_e32 v4, 16, v4
	v_add3_u32 v5, v77, v5, s45
	v_and_or_b32 v4, v5, s46, v4
	v_bfe_u32 v5, v79, 16, 1
	v_add3_u32 v5, v79, v5, s45
	v_lshrrev_b32_e32 v5, 16, v5
	v_and_or_b32 v5, v10, s46, v5
	v_or_b32_e32 v10, s20, v22
	v_lshlrev_b32_e32 v10, 13, v10
	v_lshl_add_u64 v[66:67], v[16:17], 0, v[10:11]
	global_store_dwordx4 v[66:67], v[2:5], off
	ds_read2_b32 v[66:67], v21 offset0:49 offset1:57
	ds_read2_b32 v[68:69], v21 offset0:16 offset1:24
	ds_read2_b32 v[70:71], v21 offset0:82 offset1:90
	ds_read2_b32 v[72:73], v21 offset0:115 offset1:123
	ds_read2_b32 v[74:75], v21 offset0:148 offset1:156
	ds_read2_b32 v[76:77], v21 offset0:181 offset1:189
	ds_read2_b32 v[78:79], v21 offset0:214 offset1:222
	ds_read2_b32 v[80:81], v21 offset0:247 offset1:255
	s_waitcnt lgkmcnt(7)
	v_bfe_u32 v3, v66, 16, 1
	s_waitcnt lgkmcnt(6)
	v_bfe_u32 v2, v68, 16, 1
	v_add3_u32 v2, v68, v2, s45
	v_lshrrev_b32_e32 v2, 16, v2
	v_add3_u32 v3, v66, v3, s45
	v_and_or_b32 v2, v3, s46, v2
	s_waitcnt lgkmcnt(5)
	v_bfe_u32 v3, v70, 16, 1
	v_add3_u32 v3, v70, v3, s45
	s_waitcnt lgkmcnt(4)
	v_bfe_u32 v4, v72, 16, 1
	v_lshrrev_b32_e32 v3, 16, v3
	v_add3_u32 v4, v72, v4, s45
	v_and_or_b32 v3, v4, s46, v3
	s_waitcnt lgkmcnt(3)
	v_bfe_u32 v4, v74, 16, 1
	v_add3_u32 v4, v74, v4, s45
	s_waitcnt lgkmcnt(2)
	v_bfe_u32 v5, v76, 16, 1
	v_lshrrev_b32_e32 v4, 16, v4
	v_add3_u32 v5, v76, v5, s45
	v_and_or_b32 v4, v5, s46, v4
	s_waitcnt lgkmcnt(1)
	v_bfe_u32 v5, v78, 16, 1
	v_add3_u32 v5, v78, v5, s45
	s_waitcnt lgkmcnt(0)
	v_bfe_u32 v10, v80, 16, 1
	v_lshrrev_b32_e32 v5, 16, v5
	v_add3_u32 v10, v80, v10, s45
	v_and_or_b32 v5, v10, s46, v5
	v_or_b32_e32 v10, s20, v23
	v_lshlrev_b32_e32 v10, 13, v10
	v_lshl_add_u64 v[82:83], v[16:17], 0, v[10:11]
	global_store_dwordx4 v[82:83], v[2:5], off
	v_bfe_u32 v10, v81, 16, 1
	v_add3_u32 v10, v81, v10, s45
	v_bfe_u32 v2, v69, 16, 1
	v_add3_u32 v2, v69, v2, s45
	v_bfe_u32 v3, v67, 16, 1
	v_lshrrev_b32_e32 v2, 16, v2
	v_add3_u32 v3, v67, v3, s45
	v_and_or_b32 v2, v3, s46, v2
	v_bfe_u32 v3, v71, 16, 1
	v_add3_u32 v3, v71, v3, s45
	v_bfe_u32 v4, v73, 16, 1
	v_lshrrev_b32_e32 v3, 16, v3
	v_add3_u32 v4, v73, v4, s45
	v_and_or_b32 v3, v4, s46, v3
	v_bfe_u32 v4, v75, 16, 1
	v_add3_u32 v4, v75, v4, s45
	v_bfe_u32 v5, v77, 16, 1
	v_lshrrev_b32_e32 v4, 16, v4
	v_add3_u32 v5, v77, v5, s45
	v_and_or_b32 v4, v5, s46, v4
	v_bfe_u32 v5, v79, 16, 1
	v_add3_u32 v5, v79, v5, s45
	v_lshrrev_b32_e32 v5, 16, v5
	v_and_or_b32 v5, v10, s46, v5
	v_or_b32_e32 v10, s20, v24
	v_lshlrev_b32_e32 v10, 13, v10
	v_lshl_add_u64 v[16:17], v[16:17], 0, v[10:11]
	global_store_dwordx4 v[16:17], v[2:5], off
	s_waitcnt lgkmcnt(0)
	s_mov_b64 s[0:1], 0
